# whole kernel: every 8-byte or longer instruction on an 8-byte boundary (e32 to e64 promotions and s_nop padding)
# speedup vs baseline: 1.0059x; 1.0059x over previous
_Z6mk_fwd4Args:
	s_mov_b32 s10, s2
	s_nop 0
	s_load_dwordx2 s[2:3], s[0:1], 0xd0
	s_load_dwordx4 s[4:7], s[0:1], 0xc0
	s_load_dword s61, s[0:1], 0xe0
	s_mov_b32 s93, s10
	s_waitcnt lgkmcnt(0)
	v_writelane_b32 v253, s2, 0
	s_nop 1
	s_nop 0
	v_writelane_b32 v253, s3, 1
	v_writelane_b32 v253, s4, 2
	s_add_u32 s2, s0, 0xe0
	s_addc_u32 s3, s1, 0
	s_nop 0
	v_writelane_b32 v253, s5, 3
	v_writelane_b32 v253, s6, 4
	v_writelane_b32 v253, s7, 5
	v_writelane_b32 v253, s2, 6
	v_readfirstlane_b32 s6, v0
	s_nop 0
	v_writelane_b32 v253, s3, 7
	s_and_b32 s3, s61, 7
	s_mov_b32 s2, 0
	s_cmp_lg_u32 s3, 0
	s_nop 0
	v_writelane_b32 v253, s93, 8
	s_cbranch_scc1 .LBB0_2
	s_ashr_i32 s4, s10, 31
	s_lshr_b32 s4, s4, 29
	s_add_i32 s4, s10, s4
	s_ashr_i32 s5, s4, 3
	s_and_b32 s4, s4, -8
	s_ashr_i32 s3, s61, 3
	s_sub_i32 s4, s10, s4
	s_mul_i32 s3, s3, s4
	s_add_i32 s3, s3, s5
	v_writelane_b32 v253, s3, 8
.LBB0_2:
	s_load_dwordx2 s[36:37], s[0:1], 0xd8
	s_lshr_b32 s3, s6, 6
	s_nop 0
	v_mbcnt_lo_u32_b32 v0, -1, s2
	s_and_b32 s64, s6, 0xffffffc0
	v_mbcnt_hi_u32_b32 v1, -1, v0
	v_writelane_b32 v253, s3, 9
	v_add_u32_e32 v0, s64, v1
	s_movk_i32 s2, 0x1000
	v_writelane_b32 v253, s6, 11
	v_cmp_gt_i32_e32 vcc, s2, v0
	s_and_saveexec_b64 s[2:3], vcc
	s_cbranch_execz .LBB0_5
	s_nop 0
	v_readlane_b32 s4, v253, 9
	s_lshl_b32 s4, s4, 8
	s_add_i32 s4, s4, 0
	v_lshl_add_u32 v1, v1, 2, s4
	v_add_u32_e32 v0, 0xfffffe00, v0
	v_add_u32_e32 v1, 0x20000, v1
	s_mov_b64 s[4:5], 0
	v_mov_b32_e32 v2, 0
	s_movk_i32 s6, 0xdff
.LBB0_4:
	s_nop 0
	v_add_u32_e32 v0, 0x200, v0
	v_cmp_lt_i32_e32 vcc, s6, v0
	s_nop 0
	ds_write_b32 v1, v2
	s_or_b64 s[4:5], vcc, s[4:5]
	s_nop 0
	v_add_u32_e32 v1, 0x800, v1
	s_andn2_b64 exec, exec, s[4:5]
	s_cbranch_execnz .LBB0_4
.LBB0_5:
	s_or_b64 exec, exec, s[2:3]
	s_nop 0
	s_load_dwordx16 s[12:27], s[0:1], 0x0
	s_waitcnt lgkmcnt(0)
	s_barrier
	v_writelane_b32 v253, s12, 18
	s_nop 1
	s_nop 0
	v_writelane_b32 v253, s13, 19
	v_writelane_b32 v253, s14, 20
	v_writelane_b32 v253, s15, 21
	v_writelane_b32 v253, s16, 22
	v_writelane_b32 v253, s17, 23
	v_writelane_b32 v253, s18, 24
	v_writelane_b32 v253, s19, 25
	v_writelane_b32 v253, s20, 26
	v_writelane_b32 v253, s21, 27
	v_writelane_b32 v253, s22, 28
	v_writelane_b32 v253, s23, 29
	v_writelane_b32 v253, s24, 30
	v_writelane_b32 v253, s25, 31
	v_writelane_b32 v253, s26, 32
	v_writelane_b32 v253, s27, 33
	s_load_dwordx16 s[12:27], s[0:1], 0x40
	s_waitcnt lgkmcnt(0)
	s_nop 0
	v_writelane_b32 v253, s12, 34
	s_nop 1
	s_nop 0
	v_writelane_b32 v253, s13, 35
	v_writelane_b32 v253, s14, 36
	v_writelane_b32 v253, s15, 37
	v_writelane_b32 v253, s16, 38
	v_writelane_b32 v253, s17, 39
	v_writelane_b32 v253, s18, 40
	v_writelane_b32 v253, s19, 41
	v_writelane_b32 v253, s20, 42
	v_writelane_b32 v253, s21, 43
	v_writelane_b32 v253, s22, 44
	v_writelane_b32 v253, s23, 45
	v_writelane_b32 v253, s24, 46
	v_writelane_b32 v253, s25, 47
	v_writelane_b32 v253, s26, 48
	v_writelane_b32 v253, s27, 49
	s_load_dwordx16 s[12:27], s[0:1], 0x80
	s_sub_i32 s0, s37, s36
	s_cmp_gt_i32 s0, 1
	s_cselect_b64 s[2:3], -1, 0
	s_waitcnt lgkmcnt(0)
	v_writelane_b32 v253, s12, 50
	s_nop 1
	s_nop 0
	v_writelane_b32 v253, s13, 51
	v_writelane_b32 v253, s14, 52
	v_writelane_b32 v253, s15, 53
	v_writelane_b32 v253, s16, 54
	v_writelane_b32 v253, s17, 55
	v_writelane_b32 v253, s18, 56
	v_writelane_b32 v253, s19, 57
	v_writelane_b32 v253, s20, 58
	v_writelane_b32 v253, s21, 59
	v_writelane_b32 v253, s22, 60
	v_writelane_b32 v253, s23, 61
	v_writelane_b32 v253, s24, 62
	v_writelane_b32 v253, s25, 63
	v_writelane_b32 v254, s26, 0
	v_readlane_b32 s0, v253, 0
	v_readlane_b32 s1, v253, 1
	s_add_u32 s0, s0, 0x4000
	s_addc_u32 s1, s1, 0
	s_nop 0
	v_writelane_b32 v253, s0, 12
	v_writelane_b32 v254, s27, 1
	s_nop 0
	s_nop 0
	v_writelane_b32 v253, s1, 13
	s_mov_b32 s0, 0
	s_nop 0
	v_writelane_b32 v253, s0, 14
	v_writelane_b32 v253, s2, 15
	s_and_b64 vcc, exec, s[2:3]
	s_nop 0
	v_writelane_b32 v253, s3, 16
	v_writelane_b32 v253, s0, 17
	s_cbranch_vccz .LBB0_14
	s_getreg_b32 s0, hwreg(HW_REG_XCC_ID, 0, 4)
	s_and_b32 s0, s0, 15
	s_nop 0
	v_writelane_b32 v253, s0, 17
	s_mov_b32 s0, 0
	s_nop 0
	v_readlane_b32 s1, v253, 9
	s_lshl_b32 s1, s1, 6
	s_nop 0
	v_mbcnt_lo_u32_b32 v0, -1, s0
	s_sub_i32 s1, 0, s1
	s_nop 0
	v_mbcnt_hi_u32_b32 v0, -1, v0
	s_mov_b32 s4, 0
	v_cmp_eq_u32_e32 vcc, s1, v0
	s_and_saveexec_b64 s[0:1], vcc
	s_cbranch_execz .LBB0_9
	s_mov_b64 s[2:3], exec
	s_nop 0
	v_mbcnt_lo_u32_b32 v0, s2, 0
	v_mbcnt_hi_u32_b32 v0, s3, v0
	v_cmp_eq_u32_e32 vcc, 0, v0
	s_and_b64 s[6:7], exec, vcc
	s_mov_b64 exec, s[6:7]
	s_cbranch_execz .LBB0_9
	v_readlane_b32 s5, v253, 17
	s_bcnt1_i32_b64 s2, s[2:3]
	s_lshl_b32 s5, s5, 8
	v_mov_b32_e64 v1, s2
	v_readlane_b32 s2, v253, 12
	v_mov_b32_e64 v0, s5
	v_readlane_b32 s3, v253, 13
	s_nop 4
	s_nop 0
	global_atomic_add v0, v1, s[2:3] offset:1024
.LBB0_9:
	s_or_b64 exec, exec, s[0:1]
	s_sub_i32 s0, 0, s64
	v_mbcnt_lo_u32_b32 v0, -1, s4
	v_mbcnt_hi_u32_b32 v0, -1, v0
	v_cmp_eq_u32_e32 vcc, s0, v0
	s_and_saveexec_b64 s[0:1], vcc
	s_cbranch_execz .LBB0_13
	s_getreg_b32 s4, hwreg(HW_REG_XCC_ID, 0, 4)
	s_and_b32 s6, s4, 15
	s_nop 0
	s_add_i32 s4, 0, 0x20190
	s_mov_b64 s[2:3], exec
	v_mov_b32_e32 v0, s4
	v_mov_b32_e64 v1, s6
	ds_write_b32 v0, v1
	v_mbcnt_lo_u32_b32 v0, s2, 0
	v_mbcnt_hi_u32_b32 v0, s3, v0
	v_cmp_eq_u32_e32 vcc, 0, v0
	s_and_saveexec_b64 s[4:5], vcc
	s_cbranch_execz .LBB0_12
	s_lshl_b32 s6, s6, 8
	v_readlane_b32 s8, v253, 0
	v_readlane_b32 s9, v253, 1
	s_add_u32 s6, s8, s6
	s_addc_u32 s7, s9, 0
	s_bcnt1_i32_b64 s2, s[2:3]
	s_nop 0
	v_mov_b32_e32 v1, 0xc000
	v_mov_b32_e64 v2, s2
	global_atomic_add v1, v1, v2, s[6:7] sc0
.LBB0_12:
	s_or_b64 exec, exec, s[4:5]
	s_waitcnt vmcnt(0)
	v_readfirstlane_b32 s2, v1
	s_nop 1
	v_add_u32_e64 v0, s2, v0
	s_add_i32 s2, 0, 0x20194
	v_mov_b32_e64 v1, s2
	ds_write_b32 v1, v0
.LBB0_13:
	s_or_b64 exec, exec, s[0:1]
	s_nop 0
	s_add_i32 s0, 0, 0x20160
	v_writelane_b32 v253, s0, 14
.LBB0_14:
	s_cmp_gt_i32 s36, 0
	s_nop 0
	v_writelane_b32 v254, s10, 2
	s_cselect_b64 s[2:3], -1, 0
	s_cmp_lt_i32 s37, 1
	v_writelane_b32 v254, s61, 3
	s_cselect_b64 s[4:5], -1, 0
	s_nop 0
	v_writelane_b32 v254, s64, 4
	s_or_b64 s[2:3], s[2:3], s[4:5]
	s_nop 0
	v_writelane_b32 v254, s36, 5
	s_mov_b32 s0, 0
	s_and_b64 vcc, exec, s[2:3]
	v_writelane_b32 v254, s37, 6
	s_cbranch_vccnz .LBB0_247
	s_nop 0
	v_readlane_b32 s12, v253, 18
	v_mbcnt_lo_u32_b32 v2, -1, s0
	v_mbcnt_hi_u32_b32 v51, -1, v2
	v_readlane_b32 s14, v253, 20
	v_readlane_b32 s15, v253, 21
	v_add_u32_e32 v48, s64, v51
	v_mov_b32_e32 v0, s14
	v_mov_b32_e32 v1, s15
	v_ashrrev_i32_e32 v49, 31, v48
	v_lshl_add_u64 v[0:1], v[48:49], 2, v[0:1]
	global_load_dword v26, v[0:1], off
	global_load_dword v28, v[0:1], off offset:2048
	s_movk_i32 s0, 0x1000
	v_add_co_u32_e32 v2, vcc, s0, v0
	s_movk_i32 s0, 0x2000
	s_nop 0
	v_addc_co_u32_e32 v3, vcc, 0, v1, vcc
	v_add_co_u32_e32 v6, vcc, s0, v0
	s_movk_i32 s1, 0x3000
	s_nop 0
	v_addc_co_u32_e32 v7, vcc, 0, v1, vcc
	s_nop 0
	global_load_dword v41, v[6:7], off offset:-4096
	v_add_co_u32_e32 v4, vcc, s1, v0
	s_movk_i32 s1, 0x4000
	s_nop 0
	v_addc_co_u32_e32 v5, vcc, 0, v1, vcc
	v_add_co_u32_e32 v8, vcc, s1, v0
	s_movk_i32 s1, 0x5000
	s_nop 0
	v_addc_co_u32_e32 v9, vcc, 0, v1, vcc
	v_add_co_u32_e32 v14, vcc, s1, v0
	s_movk_i32 s1, 0x6000
	s_nop 0
	v_addc_co_u32_e32 v15, vcc, 0, v1, vcc
	v_add_co_u32_e32 v10, vcc, s1, v0
	s_movk_i32 s1, 0x7000
	s_nop 0
	v_addc_co_u32_e32 v11, vcc, 0, v1, vcc
	v_add_co_u32_e32 v16, vcc, s1, v0
	s_nop 0
	s_mov_b32 s1, 0x8000
	s_nop 0
	v_addc_co_u32_e32 v17, vcc, 0, v1, vcc
	v_add_co_u32_e32 v12, vcc, s1, v0
	s_nop 0
	s_mov_b32 s1, 0x9000
	s_nop 0
	v_addc_co_u32_e32 v13, vcc, 0, v1, vcc
	v_add_co_u32_e32 v20, vcc, s1, v0
	s_nop 0
	s_mov_b32 s1, 0xa000
	s_nop 0
	v_addc_co_u32_e32 v21, vcc, 0, v1, vcc
	v_add_co_u32_e32 v34, vcc, s1, v0
	s_nop 0
	s_mov_b32 s1, 0xb000
	s_nop 0
	v_addc_co_u32_e32 v35, vcc, 0, v1, vcc
	v_add_co_u32_e32 v24, vcc, s1, v0
	s_nop 0
	global_load_dword v54, v[8:9], off offset:2048
	global_load_dword v55, v[10:11], off offset:-4096
	global_load_dword v56, v[10:11], off
	global_load_dword v57, v[10:11], off offset:2048
	global_load_dword v58, v[12:13], off offset:-4096
	global_load_dword v29, v[12:13], off
	global_load_dword v27, v[12:13], off offset:2048
	global_load_dword v18, v[34:35], off offset:-4096
	v_addc_co_u32_e32 v25, vcc, 0, v1, vcc
	s_nop 0
	global_load_dword v11, v[2:3], off offset:2048
	global_load_dword v59, v[4:5], off offset:2048
	global_load_dword v60, v[14:15], off offset:2048
	global_load_dword v61, v[16:17], off offset:2048
	s_nop 0
	s_nop 0
	global_load_dword v20, v[20:21], off offset:2048
	s_nop 0
	s_nop 0
	global_load_dword v5, v[24:25], off offset:2048
	s_mov_b32 s1, 0xc000
	v_add_co_u32_e32 v36, vcc, s1, v0
	s_nop 0
	s_mov_b32 s1, 0xd000
	s_nop 0
	v_addc_co_u32_e32 v37, vcc, 0, v1, vcc
	v_add_co_u32_e32 v2, vcc, s1, v0
	s_nop 0
	s_mov_b32 s1, 0xe000
	s_nop 0
	v_addc_co_u32_e32 v3, vcc, 0, v1, vcc
	v_add_co_u32_e32 v38, vcc, s1, v0
	s_nop 0
	s_mov_b32 s1, 0xf000
	s_nop 0
	v_addc_co_u32_e32 v39, vcc, 0, v1, vcc
	v_add_co_u32_e32 v0, vcc, s1, v0
	s_nop 0
	v_add_u32_e32 v23, 0x200, v48
	s_nop 0
	v_addc_co_u32_e32 v1, vcc, 0, v1, vcc
	s_waitcnt vmcnt(16)
	s_nop 0
	v_mul_f32_e32 v4, 0xbfb8aa3b, v26
	v_exp_f32_e64 v4, v4
	v_add_u32_e32 v40, 0x400, v48
	v_add_u32_e32 v42, 0x600, v48
	v_add_u32_e32 v43, 0x800, v48
	v_add_f32_e64 v12, 1.0, v4
	global_load_dword v16, v[6:7], off
	global_load_dword v62, v[6:7], off offset:2048
	global_load_dword v63, v[8:9], off offset:-4096
	global_load_dword v64, v[8:9], off
	global_load_dword v4, v[2:3], off offset:2048
	s_nop 0
	s_nop 0
	global_load_dword v2, v[0:1], off
	s_nop 0
	s_nop 0
	global_load_dword v1, v[0:1], off offset:2048
	v_div_scale_f32 v14, s[2:3], v12, v12, v26
	v_rcp_f32_e32 v15, v14
	v_ashrrev_i32_e32 v6, 10, v48
	v_add_u32_e32 v44, 0xa00, v48
	v_add_u32_e32 v45, 0xc00, v48
	v_fma_f32 v0, -v14, v15, 1.0
	v_fmac_f32_e32 v15, v0, v15
	s_nop 0
	v_div_scale_f32 v0, vcc, v26, v12, v26
	v_mul_f32_e64 v3, v0, v15
	v_fma_f32 v7, -v14, v3, v0
	v_fmac_f32_e32 v3, v7, v15
	s_nop 0
	v_fma_f32 v0, -v14, v3, v0
	v_div_fmas_f32 v0, v0, v15, v3
	s_waitcnt vmcnt(22)
	s_nop 0
	v_mul_f32_e32 v3, 0xbfb8aa3b, v28
	v_exp_f32_e64 v3, v3
	v_div_fixup_f32 v7, v0, v12, v26
	v_lshlrev_b32_e32 v0, 6, v48
	s_nop 0
	v_and_b32_e32 v8, 0xffc0, v0
	v_add_f32_e64 v9, 1.0, v3
	v_div_scale_f32 v12, s[2:3], v9, v9, v28
	v_rcp_f32_e32 v14, v12
	v_add_u32_e32 v3, 0, v8
	v_lshl_add_u32 v6, v6, 2, v3
	ds_write_b32 v6, v7
	v_fma_f32 v6, -v12, v14, 1.0
	v_fmac_f32_e32 v14, v6, v14
	s_nop 0
	v_div_scale_f32 v6, vcc, v28, v9, v28
	v_mul_f32_e64 v7, v6, v14
	v_fma_f32 v8, -v12, v7, v6
	v_fmac_f32_e32 v7, v8, v14
	s_waitcnt vmcnt(21)
	v_mul_f32_e32 v8, 0xbfb8aa3b, v41
	v_exp_f32_e64 v8, v8
	v_fma_f32 v6, -v12, v7, v6
	v_div_fmas_f32 v6, v6, v14, v7
	v_ashrrev_i32_e32 v7, 10, v23
	v_add_f32_e32 v8, 1.0, v8
	v_div_scale_f32 v12, s[2:3], v8, v8, v41
	v_rcp_f32_e32 v14, v12
	s_nop 0
	v_div_fixup_f32 v6, v6, v9, v28
	v_lshlrev_b32_e32 v9, 6, v23
	s_nop 0
	v_and_b32_e32 v9, 0xffc0, v9
	v_lshlrev_b32_e32 v7, 2, v7
	s_nop 0
	v_add3_u32 v7, 0, v9, v7
	ds_write_b32 v7, v6
	v_fma_f32 v6, -v12, v14, 1.0
	v_fmac_f32_e32 v14, v6, v14
	s_nop 0
	v_div_scale_f32 v6, vcc, v41, v8, v41
	v_mul_f32_e64 v7, v6, v14
	v_fma_f32 v9, -v12, v7, v6
	v_fmac_f32_e32 v7, v9, v14
	s_waitcnt vmcnt(12)
	v_mul_f32_e32 v9, 0xbfb8aa3b, v11
	v_exp_f32_e64 v9, v9
	v_fma_f32 v6, -v12, v7, v6
	v_div_fmas_f32 v6, v6, v14, v7
	v_div_fixup_f32 v6, v6, v8, v41
	v_add_f32_e64 v7, 1.0, v9
	v_div_scale_f32 v8, s[2:3], v7, v7, v11
	v_rcp_f32_e32 v9, v8
	v_ashrrev_i32_e32 v12, 10, v40
	v_lshl_add_u32 v12, v12, 2, v3
	ds_write_b32 v12, v6
	v_fma_f32 v6, -v8, v9, 1.0
	v_fmac_f32_e32 v9, v6, v9
	s_nop 0
	v_div_scale_f32 v6, vcc, v11, v7, v11
	v_mul_f32_e64 v15, v6, v9
	v_fma_f32 v12, -v8, v15, v6
	v_fmac_f32_e32 v15, v12, v9
	s_nop 0
	v_fma_f32 v6, -v8, v15, v6
	v_div_fmas_f32 v6, v6, v9, v15
	s_waitcnt vmcnt(6)
	s_nop 0
	v_mul_f32_e32 v9, 0xbfb8aa3b, v16
	v_exp_f32_e64 v9, v9
	v_div_fixup_f32 v6, v6, v7, v11
	v_ashrrev_i32_e32 v8, 10, v42
	v_lshlrev_b32_e32 v7, 6, v42
	v_add_f32_e64 v9, 1.0, v9
	v_div_scale_f32 v11, s[2:3], v9, v9, v16
	v_rcp_f32_e32 v15, v11
	s_nop 0
	v_and_b32_e32 v7, 0xffc0, v7
	v_lshlrev_b32_e32 v8, 2, v8
	s_nop 0
	v_add3_u32 v7, 0, v7, v8
	ds_write_b32 v7, v6
	v_fma_f32 v6, -v11, v15, 1.0
	v_fmac_f32_e32 v15, v6, v15
	s_nop 0
	v_div_scale_f32 v6, vcc, v16, v9, v16
	v_mul_f32_e64 v7, v6, v15
	v_fma_f32 v8, -v11, v7, v6
	v_fmac_f32_e32 v7, v8, v15
	s_nop 0
	v_fma_f32 v6, -v11, v7, v6
	v_div_fmas_f32 v8, v6, v15, v7
	s_waitcnt vmcnt(5)
	s_nop 0
	v_mul_f32_e32 v6, 0xbfb8aa3b, v62
	v_exp_f32_e64 v11, v6
	v_div_fixup_f32 v8, v8, v9, v16
	global_load_dword v40, v[34:35], off
	s_nop 0
	s_nop 0
	global_load_dword v35, v[34:35], off offset:2048
	s_nop 0
	s_nop 0
	global_load_dword v34, v[36:37], off offset:-4096
	global_load_dword v28, v[36:37], off
	global_load_dword v26, v[36:37], off offset:2048
	global_load_dword v17, v[38:39], off offset:-4096
	global_load_dword v7, v[38:39], off
	global_load_dword v6, v[38:39], off offset:2048
	v_ashrrev_i32_e32 v15, 10, v43
	v_add_f32_e32 v9, 1.0, v11
	v_div_scale_f32 v11, s[2:3], v9, v9, v62
	v_rcp_f32_e32 v36, v11
	s_nop 0
	v_lshl_add_u32 v15, v15, 2, v3
	ds_write_b32 v15, v8
	v_ashrrev_i32_e32 v39, 10, v45
	s_nop 0
	v_fma_f32 v8, -v11, v36, 1.0
	v_fmac_f32_e32 v36, v8, v36
	s_nop 0
	v_div_scale_f32 v8, vcc, v62, v9, v62
	v_mul_f32_e64 v37, v8, v36
	v_fma_f32 v15, -v11, v37, v8
	v_fmac_f32_e32 v37, v15, v36
	s_nop 0
	v_fma_f32 v8, -v11, v37, v8
	v_div_fmas_f32 v8, v8, v36, v37
	s_waitcnt vmcnt(12)
	s_nop 0
	v_mul_f32_e32 v36, 0xbfb8aa3b, v63
	v_exp_f32_e32 v36, v36
	v_ashrrev_i32_e32 v11, 10, v44
	v_div_fixup_f32 v8, v8, v9, v62
	v_lshlrev_b32_e32 v9, 6, v44
	v_add_f32_e32 v36, 1.0, v36
	v_div_scale_f32 v37, s[2:3], v36, v36, v63
	v_rcp_f32_e32 v38, v37
	s_nop 0
	v_and_b32_e32 v9, 0xffc0, v9
	v_lshlrev_b32_e32 v11, 2, v11
	s_nop 0
	v_add3_u32 v9, 0, v9, v11
	ds_write_b32 v9, v8
	v_fma_f32 v8, -v37, v38, 1.0
	v_fmac_f32_e32 v38, v8, v38
	s_nop 0
	v_div_scale_f32 v8, vcc, v63, v36, v63
	v_mul_f32_e64 v11, v8, v38
	v_fma_f32 v9, -v37, v11, v8
	v_fmac_f32_e32 v11, v9, v38
	s_nop 0
	v_fma_f32 v8, -v37, v11, v8
	v_mul_f32_e32 v37, 0xbfb8aa3b, v59
	v_exp_f32_e64 v37, v37
	v_div_fmas_f32 v8, v8, v38, v11
	v_div_fixup_f32 v8, v8, v36, v63
	v_lshl_add_u32 v39, v39, 2, v3
	v_add_f32_e64 v36, 1.0, v37
	v_div_scale_f32 v37, s[2:3], v36, v36, v59
	v_rcp_f32_e32 v38, v37
	s_nop 0
	ds_write_b32 v39, v8
	v_div_scale_f32 v39, vcc, v59, v36, v59
	v_fma_f32 v8, -v37, v38, 1.0
	v_fmac_f32_e32 v38, v8, v38
	v_mul_f32_e32 v41, v39, v38
	v_fma_f32 v8, -v37, v41, v39
	v_fmac_f32_e32 v41, v8, v38
	s_nop 0
	v_fma_f32 v37, -v37, v41, v39
	v_div_fmas_f32 v37, v37, v38, v41
	v_div_fixup_f32 v36, v37, v36, v59
	s_waitcnt vmcnt(11)
	s_nop 0
	v_mul_f32_e32 v37, 0xbfb8aa3b, v64
	v_exp_f32_e64 v37, v37
	v_add_u32_e32 v46, 0xe00, v48
	v_ashrrev_i32_e32 v39, 10, v46
	v_lshlrev_b32_e32 v38, 6, v46
	v_add_f32_e64 v37, 1.0, v37
	v_div_scale_f32 v41, s[2:3], v37, v37, v64
	v_rcp_f32_e32 v42, v41
	s_nop 0
	v_and_b32_e32 v38, 0xffc0, v38
	v_lshlrev_b32_e32 v39, 2, v39
	s_nop 0
	v_add3_u32 v38, 0, v38, v39
	ds_write_b32 v38, v36
	v_fma_f32 v38, -v41, v42, 1.0
	v_fmac_f32_e32 v42, v38, v42
	s_nop 0
	v_div_scale_f32 v38, vcc, v64, v37, v64
	v_mul_f32_e64 v39, v38, v42
	v_fma_f32 v43, -v41, v39, v38
	v_fmac_f32_e32 v39, v43, v42
	s_nop 0
	v_fma_f32 v38, -v41, v39, v38
	v_mul_f32_e32 v41, 0xbfb8aa3b, v54
	v_exp_f32_e64 v41, v41
	v_div_fmas_f32 v38, v38, v42, v39
	v_div_fixup_f32 v37, v38, v37, v64
	v_add_u32_e32 v47, 0x1000, v48
	v_add_f32_e64 v38, 1.0, v41
	v_div_scale_f32 v39, s[2:3], v38, v38, v54
	v_rcp_f32_e32 v41, v39
	v_ashrrev_i32_e32 v36, 10, v47
	v_lshl_add_u32 v36, v36, 2, v3
	ds_write_b32 v36, v37
	v_fma_f32 v37, -v39, v41, 1.0
	v_fmac_f32_e32 v41, v37, v41
	s_nop 0
	v_div_scale_f32 v37, vcc, v54, v38, v54
	v_mul_f32_e64 v42, v37, v41
	v_fma_f32 v43, -v39, v42, v37
	v_fmac_f32_e32 v42, v43, v41
	s_nop 0
	v_fma_f32 v37, -v39, v42, v37
	v_div_fmas_f32 v37, v37, v41, v42
	v_div_fixup_f32 v37, v37, v38, v54
	v_mul_f32_e32 v38, 0xbfb8aa3b, v55
	v_exp_f32_e64 v38, v38
	v_add_u32_e32 v49, 0x1200, v48
	v_ashrrev_i32_e32 v36, 10, v49
	v_lshlrev_b32_e32 v39, 6, v49
	v_add_f32_e64 v38, 1.0, v38
	v_div_scale_f32 v41, s[2:3], v38, v38, v55
	v_rcp_f32_e32 v42, v41
	s_nop 0
	v_and_b32_e32 v39, 0xffc0, v39
	v_lshlrev_b32_e32 v36, 2, v36
	s_nop 0
	v_add3_u32 v36, 0, v39, v36
	ds_write_b32 v36, v37
	v_fma_f32 v37, -v41, v42, 1.0
	v_fmac_f32_e32 v42, v37, v42
	s_nop 0
	v_div_scale_f32 v37, vcc, v55, v38, v55
	v_mul_f32_e64 v39, v37, v42
	v_fma_f32 v43, -v41, v39, v37
	v_fmac_f32_e32 v39, v43, v42
	s_nop 0
	v_fma_f32 v37, -v41, v39, v37
	v_mul_f32_e32 v41, 0xbfb8aa3b, v60
	v_exp_f32_e64 v41, v41
	v_div_fmas_f32 v37, v37, v42, v39
	v_div_fixup_f32 v37, v37, v38, v55
	v_add_u32_e32 v50, 0x1400, v48
	v_add_f32_e64 v38, 1.0, v41
	v_div_scale_f32 v39, s[2:3], v38, v38, v60
	v_rcp_f32_e32 v41, v39
	v_ashrrev_i32_e32 v36, 10, v50
	v_lshl_add_u32 v36, v36, 2, v3
	ds_write_b32 v36, v37
	v_fma_f32 v37, -v39, v41, 1.0
	v_fmac_f32_e32 v41, v37, v41
	s_nop 0
	v_div_scale_f32 v37, vcc, v60, v38, v60
	v_mul_f32_e64 v42, v37, v41
	v_fma_f32 v43, -v39, v42, v37
	v_fmac_f32_e32 v42, v43, v41
	s_nop 0
	v_fma_f32 v37, -v39, v42, v37
	v_div_fmas_f32 v37, v37, v41, v42
	v_div_fixup_f32 v37, v37, v38, v60
	v_mul_f32_e32 v38, 0xbfb8aa3b, v56
	v_exp_f32_e64 v38, v38
	v_add_u32_e32 v52, 0x1600, v48
	v_ashrrev_i32_e32 v36, 10, v52
	v_lshlrev_b32_e32 v39, 6, v52
	v_add_f32_e64 v38, 1.0, v38
	v_div_scale_f32 v41, s[2:3], v38, v38, v56
	v_rcp_f32_e32 v42, v41
	s_nop 0
	v_and_b32_e32 v39, 0xffc0, v39
	v_lshlrev_b32_e32 v36, 2, v36
	s_nop 0
	v_add3_u32 v36, 0, v39, v36
	ds_write_b32 v36, v37
	v_fma_f32 v37, -v41, v42, 1.0
	v_fmac_f32_e32 v42, v37, v42
	s_nop 0
	v_div_scale_f32 v37, vcc, v56, v38, v56
	v_mul_f32_e64 v39, v37, v42
	v_fma_f32 v43, -v41, v39, v37
	v_fmac_f32_e32 v39, v43, v42
	s_nop 0
	v_fma_f32 v37, -v41, v39, v37
	v_mul_f32_e32 v41, 0xbfb8aa3b, v57
	v_exp_f32_e64 v41, v41
	v_div_fmas_f32 v37, v37, v42, v39
	v_div_fixup_f32 v37, v37, v38, v56
	v_add_u32_e32 v53, 0x1800, v48
	v_add_f32_e64 v38, 1.0, v41
	v_div_scale_f32 v39, s[2:3], v38, v38, v57
	v_rcp_f32_e32 v41, v39
	v_ashrrev_i32_e32 v36, 10, v53
	v_lshl_add_u32 v36, v36, 2, v3
	ds_write_b32 v36, v37
	v_fma_f32 v37, -v39, v41, 1.0
	v_fmac_f32_e32 v41, v37, v41
	s_nop 0
	v_div_scale_f32 v37, vcc, v57, v38, v57
	v_mul_f32_e64 v42, v37, v41
	v_fma_f32 v43, -v39, v42, v37
	v_fmac_f32_e32 v42, v43, v41
	s_nop 0
	v_fma_f32 v37, -v39, v42, v37
	v_div_fmas_f32 v37, v37, v41, v42
	v_div_fixup_f32 v37, v37, v38, v57
	v_mul_f32_e32 v38, 0xbfb8aa3b, v58
	v_exp_f32_e64 v38, v38
	v_add_u32_e32 v33, 0x1a00, v48
	v_ashrrev_i32_e32 v36, 10, v33
	v_lshlrev_b32_e32 v33, 6, v33
	v_add_f32_e64 v38, 1.0, v38
	v_div_scale_f32 v39, s[2:3], v38, v38, v58
	v_rcp_f32_e32 v41, v39
	s_nop 0
	v_and_b32_e32 v33, 0xffc0, v33
	v_lshlrev_b32_e32 v36, 2, v36
	s_nop 0
	v_add3_u32 v33, 0, v33, v36
	ds_write_b32 v33, v37
	v_fma_f32 v33, -v39, v41, 1.0
	v_fmac_f32_e32 v41, v33, v41
	s_nop 0
	v_div_scale_f32 v33, vcc, v58, v38, v58
	v_mul_f32_e64 v36, v33, v41
	v_fma_f32 v37, -v39, v36, v33
	v_fmac_f32_e32 v36, v37, v41
	s_nop 0
	v_mul_f32_e32 v37, 0xbfb8aa3b, v61
	v_exp_f32_e64 v37, v37
	v_fma_f32 v33, -v39, v36, v33
	v_div_fmas_f32 v33, v33, v41, v36
	v_div_fixup_f32 v33, v33, v38, v58
	v_add_f32_e64 v36, 1.0, v37
	v_div_scale_f32 v37, s[2:3], v36, v36, v61
	v_rcp_f32_e32 v38, v37
	s_nop 0
	v_add_u32_e32 v32, 0x1c00, v48
	v_ashrrev_i32_e32 v32, 10, v32
	s_nop 0
	v_lshl_add_u32 v32, v32, 2, v3
	ds_write_b32 v32, v33
	v_fma_f32 v33, -v37, v38, 1.0
	v_fmac_f32_e32 v38, v33, v38
	s_nop 0
	v_div_scale_f32 v33, vcc, v61, v36, v61
	v_mul_f32_e64 v39, v33, v38
	v_fma_f32 v41, -v37, v39, v33
	v_fmac_f32_e32 v39, v41, v38
	s_nop 0
	v_fma_f32 v33, -v37, v39, v33
	v_div_fmas_f32 v33, v33, v38, v39
	v_div_fixup_f32 v33, v33, v36, v61
	v_mul_f32_e32 v36, 0xbfb8aa3b, v29
	v_exp_f32_e64 v36, v36
	v_add_u32_e32 v31, 0x1e00, v48
	v_ashrrev_i32_e32 v32, 10, v31
	v_lshlrev_b32_e32 v31, 6, v31
	v_add_f32_e64 v36, 1.0, v36
	v_div_scale_f32 v37, s[2:3], v36, v36, v29
	v_rcp_f32_e32 v38, v37
	s_nop 0
	v_and_b32_e32 v31, 0xffc0, v31
	v_lshlrev_b32_e32 v32, 2, v32
	s_nop 0
	v_add3_u32 v31, 0, v31, v32
	ds_write_b32 v31, v33
	v_fma_f32 v31, -v37, v38, 1.0
	v_fmac_f32_e32 v38, v31, v38
	s_nop 0
	v_div_scale_f32 v31, vcc, v29, v36, v29
	v_mul_f32_e64 v32, v31, v38
	v_fma_f32 v33, -v37, v32, v31
	v_fmac_f32_e32 v32, v33, v38
	s_nop 0
	v_mul_f32_e32 v33, 0xbfb8aa3b, v27
	v_exp_f32_e64 v33, v33
	v_fma_f32 v31, -v37, v32, v31
	v_div_fmas_f32 v31, v31, v38, v32
	v_div_fixup_f32 v29, v31, v36, v29
	v_add_f32_e64 v31, 1.0, v33
	v_div_scale_f32 v32, s[2:3], v31, v31, v27
	v_rcp_f32_e32 v33, v32
	s_nop 0
	v_add_u32_e32 v30, 0x2000, v48
	v_ashrrev_i32_e32 v30, 10, v30
	s_nop 0
	v_lshl_add_u32 v30, v30, 2, v3
	ds_write_b32 v30, v29
	v_fma_f32 v30, -v32, v33, 1.0
	v_fmac_f32_e32 v33, v30, v33
	s_nop 0
	v_div_scale_f32 v30, vcc, v27, v31, v27
	v_mul_f32_e64 v36, v30, v33
	v_fma_f32 v37, -v32, v36, v30
	v_fmac_f32_e32 v36, v37, v33
	s_nop 0
	v_fma_f32 v30, -v32, v36, v30
	v_div_fmas_f32 v30, v30, v33, v36
	v_div_fixup_f32 v27, v30, v31, v27
	v_mul_f32_e32 v30, 0xbfb8aa3b, v18
	v_exp_f32_e64 v30, v30
	v_add_u32_e32 v22, 0x2200, v48
	v_ashrrev_i32_e32 v29, 10, v22
	v_lshlrev_b32_e32 v22, 6, v22
	v_add_f32_e64 v30, 1.0, v30
	v_div_scale_f32 v31, s[2:3], v30, v30, v18
	v_rcp_f32_e32 v32, v31
	s_nop 0
	v_and_b32_e32 v22, 0xffc0, v22
	v_lshlrev_b32_e32 v29, 2, v29
	s_nop 0
	v_add3_u32 v22, 0, v22, v29
	ds_write_b32 v22, v27
	v_fma_f32 v22, -v31, v32, 1.0
	v_fmac_f32_e32 v32, v22, v32
	s_nop 0
	v_div_scale_f32 v22, vcc, v18, v30, v18
	v_mul_f32_e64 v27, v22, v32
	v_fma_f32 v29, -v31, v27, v22
	v_fmac_f32_e32 v27, v29, v32
	s_nop 0
	v_mul_f32_e32 v29, 0xbfb8aa3b, v20
	v_exp_f32_e64 v29, v29
	v_fma_f32 v22, -v31, v27, v22
	v_div_fmas_f32 v22, v22, v32, v27
	v_div_fixup_f32 v18, v22, v30, v18
	v_add_f32_e64 v22, 1.0, v29
	v_div_scale_f32 v27, s[2:3], v22, v22, v20
	v_rcp_f32_e32 v29, v27
	s_nop 0
	v_add_u32_e32 v19, 0x2400, v48
	v_ashrrev_i32_e32 v19, 10, v19
	s_nop 0
	v_lshl_add_u32 v19, v19, 2, v3
	ds_write_b32 v19, v18
	v_fma_f32 v19, -v27, v29, 1.0
	v_fmac_f32_e32 v29, v19, v29
	s_nop 0
	v_div_scale_f32 v19, vcc, v20, v22, v20
	v_mul_f32_e64 v30, v19, v29
	v_fma_f32 v31, -v27, v30, v19
	v_fmac_f32_e32 v30, v31, v29
	s_nop 0
	v_fma_f32 v19, -v27, v30, v19
	v_div_fmas_f32 v19, v19, v29, v30
	v_div_fixup_f32 v19, v19, v22, v20
	s_waitcnt vmcnt(7)
	s_nop 0
	v_mul_f32_e32 v20, 0xbfb8aa3b, v40
	v_exp_f32_e64 v20, v20
	v_add_u32_e32 v13, 0x2600, v48
	v_ashrrev_i32_e32 v18, 10, v13
	v_lshlrev_b32_e32 v13, 6, v13
	v_add_f32_e64 v20, 1.0, v20
	v_div_scale_f32 v22, s[2:3], v20, v20, v40
	v_rcp_f32_e32 v27, v22
	s_nop 0
	v_and_b32_e32 v13, 0xffc0, v13
	v_lshlrev_b32_e32 v18, 2, v18
	s_nop 0
	v_add3_u32 v13, 0, v13, v18
	ds_write_b32 v13, v19
	v_fma_f32 v13, -v22, v27, 1.0
	v_fmac_f32_e32 v27, v13, v27
	s_nop 0
	v_div_scale_f32 v13, vcc, v40, v20, v40
	v_mul_f32_e64 v18, v13, v27
	v_fma_f32 v19, -v22, v18, v13
	v_fmac_f32_e32 v18, v19, v27
	s_waitcnt vmcnt(6)
	v_mul_f32_e32 v19, 0xbfb8aa3b, v35
	v_exp_f32_e64 v19, v19
	v_fma_f32 v13, -v22, v18, v13
	v_div_fmas_f32 v13, v13, v27, v18
	v_div_fixup_f32 v13, v13, v20, v40
	v_add_f32_e64 v18, 1.0, v19
	v_div_scale_f32 v19, s[2:3], v18, v18, v35
	v_rcp_f32_e32 v20, v19
	s_nop 0
	v_add_u32_e32 v10, 0x2800, v48
	v_ashrrev_i32_e32 v10, 10, v10
	s_nop 0
	v_lshl_add_u32 v10, v10, 2, v3
	ds_write_b32 v10, v13
	v_fma_f32 v13, -v19, v20, 1.0
	v_fmac_f32_e32 v20, v13, v20
	s_nop 0
	v_div_scale_f32 v13, vcc, v35, v18, v35
	v_mul_f32_e64 v22, v13, v20
	v_fma_f32 v27, -v19, v22, v13
	v_fmac_f32_e32 v22, v27, v20
	s_nop 0
	v_fma_f32 v13, -v19, v22, v13
	v_div_fmas_f32 v13, v13, v20, v22
	v_div_fixup_f32 v13, v13, v18, v35
	s_waitcnt vmcnt(5)
	s_nop 0
	v_mul_f32_e32 v18, 0xbfb8aa3b, v34
	v_exp_f32_e64 v18, v18
	v_add_u32_e32 v25, 0x2a00, v48
	v_ashrrev_i32_e32 v10, 10, v25
	v_lshlrev_b32_e32 v19, 6, v25
	v_add_f32_e64 v18, 1.0, v18
	v_div_scale_f32 v20, s[2:3], v18, v18, v34
	v_rcp_f32_e32 v22, v20
	s_nop 0
	v_and_b32_e32 v19, 0xffc0, v19
	v_lshlrev_b32_e32 v10, 2, v10
	s_nop 0
	v_add3_u32 v10, 0, v19, v10
	ds_write_b32 v10, v13
	v_fma_f32 v13, -v20, v22, 1.0
	v_fmac_f32_e32 v22, v13, v22
	s_nop 0
	v_div_scale_f32 v13, vcc, v34, v18, v34
	v_add_u32_e32 v24, 0x2c00, v48
	v_mul_f32_e32 v19, v13, v22
	v_ashrrev_i32_e32 v10, 10, v24
	v_fma_f32 v24, -v20, v19, v13
	v_fmac_f32_e32 v19, v24, v22
	s_nop 0
	v_fma_f32 v13, -v20, v19, v13
	v_mul_f32_e32 v20, 0xbfb8aa3b, v5
	v_exp_f32_e64 v20, v20
	v_div_fmas_f32 v13, v13, v22, v19
	v_div_fixup_f32 v13, v13, v18, v34
	v_lshl_add_u32 v10, v10, 2, v3
	v_add_f32_e64 v18, 1.0, v20
	v_div_scale_f32 v19, s[2:3], v18, v18, v5
	v_rcp_f32_e32 v20, v19
	s_nop 0
	ds_write_b32 v10, v13
	v_add_u32_e32 v21, 0x2e00, v48
	v_ashrrev_i32_e32 v10, 10, v21
	s_nop 0
	v_fma_f32 v13, -v19, v20, 1.0
	v_fmac_f32_e32 v20, v13, v20
	s_nop 0
	v_div_scale_f32 v13, vcc, v5, v18, v5
	v_mul_f32_e64 v22, v13, v20
	v_fma_f32 v24, -v19, v22, v13
	v_fmac_f32_e32 v22, v24, v20
	s_nop 0
	v_fma_f32 v13, -v19, v22, v13
	v_div_fmas_f32 v13, v13, v20, v22
	v_div_fixup_f32 v5, v13, v18, v5
	s_waitcnt vmcnt(4)
	s_nop 0
	v_mul_f32_e32 v13, 0xbfb8aa3b, v28
	v_exp_f32_e32 v13, v13
	v_lshlrev_b32_e32 v18, 6, v21
	v_and_b32_e32 v18, 0xffc0, v18
	v_lshlrev_b32_e32 v10, 2, v10
	v_add_f32_e32 v13, 1.0, v13
	v_div_scale_f32 v19, s[2:3], v13, v13, v28
	v_rcp_f32_e32 v20, v19
	s_nop 0
	v_add3_u32 v10, 0, v18, v10
	ds_write_b32 v10, v5
	v_add_u32_e32 v23, 0x3000, v48
	v_fma_f32 v10, -v19, v20, 1.0
	v_fmac_f32_e32 v20, v10, v20
	s_nop 0
	v_div_scale_f32 v10, vcc, v28, v13, v28
	v_mul_f32_e64 v18, v10, v20
	v_fma_f32 v21, -v19, v18, v10
	v_fmac_f32_e32 v18, v21, v20
	s_nop 0
	v_fma_f32 v10, -v19, v18, v10
	s_waitcnt vmcnt(3)
	s_nop 0
	v_mul_f32_e32 v19, 0xbfb8aa3b, v26
	v_exp_f32_e64 v19, v19
	v_div_fmas_f32 v10, v10, v20, v18
	v_div_fixup_f32 v10, v10, v13, v28
	v_ashrrev_i32_e32 v5, 10, v23
	v_add_f32_e32 v13, 1.0, v19
	v_div_scale_f32 v18, s[2:3], v13, v13, v26
	v_rcp_f32_e32 v19, v18
	s_nop 0
	v_lshl_add_u32 v5, v5, 2, v3
	ds_write_b32 v5, v10
	v_add_u32_e32 v14, 0x3200, v48
	v_fma_f32 v10, -v18, v19, 1.0
	v_fmac_f32_e32 v19, v10, v19
	s_nop 0
	v_div_scale_f32 v10, vcc, v26, v13, v26
	v_mul_f32_e64 v20, v10, v19
	v_fma_f32 v21, -v18, v20, v10
	v_fmac_f32_e32 v20, v21, v19
	s_nop 0
	v_fma_f32 v10, -v18, v20, v10
	v_div_fmas_f32 v10, v10, v19, v20
	v_div_fixup_f32 v10, v10, v13, v26
	s_waitcnt vmcnt(2)
	s_nop 0
	v_mul_f32_e32 v13, 0xbfb8aa3b, v17
	v_exp_f32_e64 v13, v13
	v_ashrrev_i32_e32 v5, 10, v14
	v_lshlrev_b32_e32 v14, 6, v14
	v_and_b32_e32 v14, 0xffc0, v14
	v_add_f32_e64 v13, 1.0, v13
	v_div_scale_f32 v18, s[2:3], v13, v13, v17
	v_rcp_f32_e32 v19, v18
	v_lshlrev_b32_e32 v5, 2, v5
	v_add3_u32 v5, 0, v14, v5
	ds_write_b32 v5, v10
	v_fma_f32 v10, -v18, v19, 1.0
	v_add_u32_e32 v12, 0x3400, v48
	v_fmac_f32_e32 v19, v10, v19
	s_nop 0
	v_div_scale_f32 v10, vcc, v17, v13, v17
	v_ashrrev_i32_e32 v5, 10, v12
	v_mul_f32_e32 v12, v10, v19
	v_fma_f32 v14, -v18, v12, v10
	v_fmac_f32_e32 v12, v14, v19
	s_nop 0
	v_mul_f32_e32 v14, 0xbfb8aa3b, v4
	v_exp_f32_e64 v14, v14
	v_fma_f32 v10, -v18, v12, v10
	v_div_fmas_f32 v10, v10, v19, v12
	v_div_fixup_f32 v10, v10, v13, v17
	v_add_f32_e64 v12, 1.0, v14
	v_div_scale_f32 v13, s[2:3], v12, v12, v4
	v_rcp_f32_e32 v14, v13
	s_nop 0
	v_lshl_add_u32 v5, v5, 2, v3
	ds_write_b32 v5, v10
	v_add_u32_e32 v16, 0x3600, v48
	v_fma_f32 v10, -v13, v14, 1.0
	v_fmac_f32_e32 v14, v10, v14
	s_nop 0
	v_div_scale_f32 v10, vcc, v4, v12, v4
	v_mul_f32_e64 v17, v10, v14
	v_fma_f32 v18, -v13, v17, v10
	v_fmac_f32_e32 v17, v18, v14
	s_nop 0
	v_fma_f32 v10, -v13, v17, v10
	v_div_fmas_f32 v10, v10, v14, v17
	v_div_fixup_f32 v4, v10, v12, v4
	s_waitcnt vmcnt(1)
	s_nop 0
	v_mul_f32_e32 v10, 0xbfb8aa3b, v7
	v_exp_f32_e64 v10, v10
	v_ashrrev_i32_e32 v5, 10, v16
	v_lshlrev_b32_e32 v12, 6, v16
	v_and_b32_e32 v12, 0xffc0, v12
	v_add_f32_e64 v10, 1.0, v10
	v_div_scale_f32 v13, s[2:3], v10, v10, v7
	v_rcp_f32_e32 v14, v13
	v_lshlrev_b32_e32 v5, 2, v5
	v_add3_u32 v5, 0, v12, v5
	ds_write_b32 v5, v4
	v_fma_f32 v5, -v13, v14, 1.0
	v_fmac_f32_e32 v14, v5, v14
	s_nop 0
	v_div_scale_f32 v5, vcc, v7, v10, v7
	v_add_u32_e32 v15, 0x3800, v48
	v_mul_f32_e32 v12, v5, v14
	v_ashrrev_i32_e32 v4, 10, v15
	v_fma_f32 v15, -v13, v12, v5
	v_fmac_f32_e32 v12, v15, v14
	s_nop 0
	v_fma_f32 v5, -v13, v12, v5
	s_waitcnt vmcnt(0)
	s_nop 0
	v_mul_f32_e32 v13, 0xbfb8aa3b, v6
	v_exp_f32_e64 v13, v13
	v_div_fmas_f32 v5, v5, v14, v12
	v_div_fixup_f32 v5, v5, v10, v7
	v_lshl_add_u32 v4, v4, 2, v3
	v_add_f32_e64 v7, 1.0, v13
	v_div_scale_f32 v10, s[2:3], v7, v7, v6
	v_rcp_f32_e32 v12, v10
	s_nop 0
	ds_write_b32 v4, v5
	v_add_u32_e32 v9, 0x3a00, v48
	v_ashrrev_i32_e32 v4, 10, v9
	s_nop 0
	v_fma_f32 v5, -v10, v12, 1.0
	v_fmac_f32_e32 v12, v5, v12
	s_nop 0
	v_div_scale_f32 v5, vcc, v6, v7, v6
	v_mul_f32_e64 v13, v5, v12
	v_fma_f32 v14, -v10, v13, v5
	v_fmac_f32_e32 v13, v14, v12
	s_nop 0
	v_fma_f32 v5, -v10, v13, v5
	v_div_fmas_f32 v5, v5, v12, v13
	v_div_fixup_f32 v5, v5, v7, v6
	v_mul_f32_e32 v6, 0xbfb8aa3b, v2
	v_exp_f32_e32 v6, v6
	v_lshlrev_b32_e32 v7, 6, v9
	v_and_b32_e32 v7, 0xffc0, v7
	v_lshlrev_b32_e32 v4, 2, v4
	v_add_f32_e32 v6, 1.0, v6
	v_div_scale_f32 v9, s[2:3], v6, v6, v2
	v_rcp_f32_e32 v10, v9
	s_nop 0
	v_add3_u32 v4, 0, v7, v4
	ds_write_b32 v4, v5
	v_add_u32_e32 v11, 0x3c00, v48
	v_fma_f32 v5, -v9, v10, 1.0
	v_fmac_f32_e32 v10, v5, v10
	s_nop 0
	v_div_scale_f32 v5, vcc, v2, v6, v2
	v_mul_f32_e32 v7, v5, v10
	v_ashrrev_i32_e32 v4, 10, v11
	v_fma_f32 v11, -v9, v7, v5
	v_fmac_f32_e32 v7, v11, v10
	s_nop 0
	v_fma_f32 v5, -v9, v7, v5
	v_mul_f32_e32 v9, 0xbfb8aa3b, v1
	v_exp_f32_e64 v9, v9
	v_div_fmas_f32 v5, v5, v10, v7
	v_div_fixup_f32 v2, v5, v6, v2
	v_lshl_add_u32 v3, v4, 2, v3
	v_add_f32_e64 v5, 1.0, v9
	v_div_scale_f32 v6, s[2:3], v5, v5, v1
	v_rcp_f32_e32 v7, v6
	s_nop 0
	ds_write_b32 v3, v2
	v_add_u32_e32 v8, 0x3e00, v48
	v_ashrrev_i32_e32 v2, 10, v8
	s_nop 0
	v_fma_f32 v3, -v6, v7, 1.0
	v_fmac_f32_e32 v7, v3, v7
	s_nop 0
	v_div_scale_f32 v3, vcc, v1, v5, v1
	v_mul_f32_e64 v4, v3, v7
	v_fma_f32 v9, -v6, v4, v3
	v_fmac_f32_e32 v4, v9, v7
	s_nop 0
	v_fma_f32 v3, -v6, v4, v3
	v_div_fmas_f32 v3, v3, v7, v4
	v_div_fixup_f32 v1, v3, v5, v1
	v_lshlrev_b32_e32 v3, 6, v8
	s_nop 0
	v_and_b32_e32 v3, 0xffc0, v3
	v_lshlrev_b32_e32 v2, 2, v2
	s_movk_i32 s0, 0x800
	v_add3_u32 v2, 0, v3, v2
	s_cmpk_gt_i32 s10, 0xdf
	s_nop 0
	v_writelane_b32 v254, s93, 7
	v_readlane_b32 s13, v253, 19
	v_readlane_b32 s16, v253, 22
	v_readlane_b32 s17, v253, 23
	v_readlane_b32 s18, v253, 24
	v_readlane_b32 s19, v253, 25
	v_readlane_b32 s20, v253, 26
	v_readlane_b32 s21, v253, 27
	v_readlane_b32 s22, v253, 28
	v_readlane_b32 s23, v253, 29
	v_readlane_b32 s24, v253, 30
	v_readlane_b32 s25, v253, 31
	v_readlane_b32 s26, v253, 32
	v_readlane_b32 s27, v253, 33
	ds_write_b32 v2, v1
	s_waitcnt lgkmcnt(0)
	s_barrier
	s_cbranch_scc1 .LBB0_35
	s_nop 0
	v_readlane_b32 s2, v253, 0
	v_readlane_b32 s3, v253, 1
	s_add_u32 s4, s2, 0x2a0000
	s_addc_u32 s5, s3, 0
	s_nop 0
	v_writelane_b32 v254, s4, 8
	v_and_b32_e32 v2, 0x7f, v48
	v_lshlrev_b32_e32 v1, 1, v48
	s_nop 0
	v_writelane_b32 v254, s5, 9
	s_add_u32 s4, s2, 0x280000
	s_addc_u32 s5, s3, 0
	s_nop 0
	v_writelane_b32 v254, s4, 10
	s_add_u32 s1, s2, 0x100000
	v_add_u32_e64 v0, 0, v0
	v_writelane_b32 v254, s5, 11
	v_writelane_b32 v254, s1, 12
	s_addc_u32 s1, s3, 0
	s_nop 0
	v_writelane_b32 v254, s1, 13
	s_add_u32 s1, s2, 0x300000
	v_writelane_b32 v254, s1, 15
	s_addc_u32 s1, s3, 0
	s_nop 0
	v_writelane_b32 v254, s1, 16
	v_cmp_gt_i32_e64 s[0:1], s0, v48
	v_and_b32_e32 v50, 0xffffff00, v1
	v_mov_b32_e64 v53, 0
	v_writelane_b32 v254, s0, 17
	v_lshlrev_b32_e32 v54, 2, v2
	s_nop 0
	v_add_u32_e32 v49, 0x10000, v0
	v_writelane_b32 v254, s1, 18
	s_mov_b32 s5, s93
	s_branch .LBB0_18
.LBB0_17:
	s_or_b64 exec, exec, s[0:1]
	s_nop 0
	v_readlane_b32 s5, v254, 19
	s_add_i32 s5, s5, s61
	s_cmpk_gt_i32 s5, 0xdf
	s_barrier
	s_cbranch_scc1 .LBB0_35
.LBB0_18:
	s_cmpk_gt_i32 s5, 0xbf
	s_mov_b64 s[2:3], -1
	s_cbranch_scc0 .LBB0_25
	s_lshl_b32 s4, s5, 7
	s_cmpk_gt_u32 s5, 0xcf
	s_cbranch_scc0 .LBB0_21
	v_readlane_b32 s8, v253, 50
	v_readlane_b32 s9, v253, 51
	v_readlane_b32 s10, v253, 52
	v_readlane_b32 s11, v253, 53
	v_readlane_b32 s8, v253, 2
	v_readlane_b32 s22, v254, 0
	v_readlane_b32 s23, v254, 1
	v_readlane_b32 s9, v253, 3
	s_add_i32 s24, s4, 0xffff9800
	s_mov_b64 s[2:3], 0
	s_nop 0
	v_readlane_b32 s12, v253, 54
	v_readlane_b32 s13, v253, 55
	v_readlane_b32 s14, v253, 56
	v_readlane_b32 s15, v253, 57
	v_readlane_b32 s16, v253, 58
	v_readlane_b32 s17, v253, 59
	v_readlane_b32 s18, v253, 60
	v_readlane_b32 s19, v253, 61
	v_readlane_b32 s20, v253, 62
	v_readlane_b32 s21, v253, 63
	s_mov_b64 s[0:1], s[22:23]
	s_nop 0
	v_readlane_b32 s10, v253, 4
	v_readlane_b32 s11, v253, 5
	s_mov_b64 s[6:7], s[8:9]
	s_branch .LBB0_22
.LBB0_21:
	v_readlane_b32 s8, v253, 18
	v_readlane_b32 s9, v253, 19
	v_readlane_b32 s10, v253, 20
	v_readlane_b32 s11, v253, 21
	v_readlane_b32 s12, v253, 22
	v_readlane_b32 s13, v253, 23
	v_readlane_b32 s14, v253, 24
	v_readlane_b32 s15, v253, 25
	v_readlane_b32 s16, v253, 26
	v_readlane_b32 s17, v253, 27
	v_readlane_b32 s18, v253, 28
	v_readlane_b32 s19, v253, 29
	v_readlane_b32 s20, v253, 30
	v_readlane_b32 s21, v253, 31
	v_readlane_b32 s22, v253, 32
	v_readlane_b32 s23, v253, 33
	s_mov_b64 s[0:1], s[22:23]
	s_nop 0
	v_readlane_b32 s8, v253, 34
	v_readlane_b32 s9, v253, 35
	s_mov_b64 s[6:7], s[8:9]
	s_nop 0
	v_readlane_b32 s10, v253, 36
	v_readlane_b32 s11, v253, 37
	v_readlane_b32 s12, v253, 38
	v_readlane_b32 s13, v253, 39
	v_readlane_b32 s14, v253, 40
	v_readlane_b32 s15, v253, 41
	v_readlane_b32 s16, v253, 42
	v_readlane_b32 s17, v253, 43
	v_readlane_b32 s18, v253, 44
	v_readlane_b32 s19, v253, 45
	v_readlane_b32 s20, v253, 46
	v_readlane_b32 s21, v253, 47
	v_readlane_b32 s22, v253, 48
	v_readlane_b32 s23, v253, 49
.LBB0_22:
	s_andn2_b64 vcc, exec, s[2:3]
	s_nop 0
	v_readlane_b32 s2, v254, 8
	v_readlane_b32 s3, v254, 9
	s_cbranch_vccnz .LBB0_24
	s_nop 0
	v_readlane_b32 s2, v254, 10
	s_add_i32 s24, s4, 0xffffa000
	v_readlane_b32 s3, v254, 11
.LBB0_24:
	v_writelane_b32 v254, s2, 24
	s_nop 1
	s_nop 0
	v_writelane_b32 v254, s3, 25
	s_mov_b64 s[2:3], 0
.LBB0_25:
	s_andn2_b64 vcc, exec, s[2:3]
	v_writelane_b32 v254, s5, 19
	s_cbranch_vccnz .LBB0_27
	s_nop 0
	s_mul_hi_i32 s0, s5, 0x2aaaaaab
	s_lshr_b32 s1, s0, 31
	s_ashr_i32 s0, s0, 3
	s_add_i32 s4, s0, s1
	s_mul_i32 s0, s4, 48
	s_sub_i32 s0, s5, s0
	s_nop 0
	v_readlane_b32 s8, v253, 34
	s_lshl_b32 s24, s0, 7
	s_nop 0
	s_mul_i32 s0, s4, 0x1800000
	v_readlane_b32 s22, v253, 48
	s_mul_hi_i32 s1, s4, 0x1800000
	v_readlane_b32 s23, v253, 49
	s_add_u32 s0, s22, s0
	s_nop 0
	s_mul_i32 s2, s4, 0x1800
	v_readlane_b32 s9, v253, 35
	v_readlane_b32 s10, v253, 36
	v_readlane_b32 s11, v253, 37
	v_readlane_b32 s12, v253, 38
	v_readlane_b32 s13, v253, 39
	v_readlane_b32 s14, v253, 40
	v_readlane_b32 s15, v253, 41
	v_readlane_b32 s16, v253, 42
	v_readlane_b32 s17, v253, 43
	v_readlane_b32 s18, v253, 44
	v_readlane_b32 s19, v253, 45
	v_readlane_b32 s20, v253, 46
	v_readlane_b32 s21, v253, 47
	s_addc_u32 s1, s23, s1
	s_ashr_i32 s3, s2, 31
	s_lshl_b64 s[2:3], s[2:3], 2
	s_nop 0
	v_readlane_b32 s8, v253, 50
	v_readlane_b32 s9, v253, 51
	s_add_u32 s2, s8, s2
	s_addc_u32 s3, s9, s3
	v_readlane_b32 s22, v254, 0
	v_readlane_b32 s23, v254, 1
	v_writelane_b32 v254, s2, 20
	v_readlane_b32 s10, v253, 52
	v_readlane_b32 s11, v253, 53
	v_writelane_b32 v254, s3, 21
	s_mul_hi_i32 s3, s4, 0x18000
	s_mul_i32 s2, s4, 0x18000
	s_lshl_b64 s[4:5], s[2:3], 2
	s_nop 0
	v_readlane_b32 s6, v254, 12
	s_add_u32 s6, s6, s4
	s_nop 0
	v_readlane_b32 s4, v254, 13
	s_addc_u32 s7, s4, s5
	s_nop 0
	v_writelane_b32 v254, s6, 24
	s_lshl_b64 s[2:3], s[2:3], 1
	s_nop 0
	s_mov_b64 s[10:11], 0x1800
	v_writelane_b32 v254, s7, 25
	v_readlane_b32 s12, v253, 54
	v_readlane_b32 s4, v254, 15
	s_add_u32 s4, s4, s2
	s_nop 0
	v_readlane_b32 s2, v254, 16
	s_addc_u32 s5, s2, s3
	s_nop 0
	v_writelane_b32 v254, s4, 22
	v_readlane_b32 s13, v253, 55
	v_readlane_b32 s14, v253, 56
	v_writelane_b32 v254, s5, 23
	v_readlane_b32 s15, v253, 57
	v_readlane_b32 s16, v253, 58
	v_readlane_b32 s17, v253, 59
	v_readlane_b32 s18, v253, 60
	v_readlane_b32 s19, v253, 61
	v_readlane_b32 s20, v253, 62
	v_readlane_b32 s21, v253, 63
	s_branch .LBB0_28
.LBB0_27:
	s_nop 0
	v_writelane_b32 v254, s6, 20
	s_mov_b64 s[2:3], 0
	s_nop 0
	s_mov_b64 s[10:11], 0x800
	v_writelane_b32 v254, s7, 21
	v_writelane_b32 v254, s2, 22
	s_nop 1
	s_nop 0
	v_writelane_b32 v254, s3, 23
.LBB0_28:
	v_mad_i64_i32 v[0:1], s[2:3], s10, v50, 0
	v_lshl_add_u64 v[0:1], v[0:1], 2, s[0:1]
	s_ashr_i32 s25, s24, 31
	s_nop 0
	v_writelane_b32 v254, s24, 26
	v_mov_b32_e32 v55, v53
	v_mov_b32_e32 v2, 0
	v_lshl_add_u64 v[0:1], s[24:25], 2, v[0:1]
	v_writelane_b32 v254, s25, 27
	v_lshl_add_u64 v[56:57], v[0:1], 0, v[54:55]
	s_mov_b32 s11, 0
	v_mov_b32_e32 v3, v2
	v_mov_b32_e32 v0, v2
	v_mov_b32_e32 v1, v2
	v_mov_b32_e32 v6, v2
	v_mov_b32_e32 v7, v2
	v_mov_b32_e32 v4, v2
	v_mov_b32_e32 v5, v2
	v_mov_b32_e32 v10, v2
	v_mov_b32_e32 v11, v2
	v_mov_b32_e32 v8, v2
	v_mov_b32_e32 v9, v2
	v_mov_b32_e32 v14, v2
	v_mov_b32_e32 v15, v2
	v_mov_b32_e32 v12, v2
	v_mov_b32_e32 v13, v2
.LBB0_29:
	s_mul_hi_u32 s1, s10, s11
	s_mul_i32 s0, s10, s11
	v_lshl_add_u64 v[16:17], s[0:1], 2, v[56:57]
	global_load_dword v84, v[16:17], off
	s_or_b32 s2, s11, 1
	s_or_b32 s64, s11, 2
	s_or_b32 s68, s11, 3
	s_or_b32 s65, s11, 4
	s_or_b32 s75, s11, 5
	s_or_b32 s74, s11, 6
	s_or_b32 s79, s11, 7
	v_add_u32_e32 v20, s11, v50
	s_mul_hi_u32 s49, s10, s2
	s_mul_i32 s48, s10, s2
	s_mul_hi_u32 s47, s10, s64
	s_mul_i32 s46, s10, s64
	s_mul_hi_u32 s45, s10, s68
	s_mul_i32 s44, s10, s68
	s_mul_hi_u32 s57, s10, s65
	s_mul_i32 s56, s10, s65
	s_mul_hi_u32 s55, s10, s75
	s_mul_i32 s54, s10, s75
	s_mul_hi_u32 s53, s10, s74
	s_mul_i32 s52, s10, s74
	s_mul_hi_u32 s51, s10, s79
	s_mul_i32 s50, s10, s79
	v_lshl_add_u64 v[18:19], s[48:49], 2, v[56:57]
	v_lshl_add_u64 v[30:31], s[46:47], 2, v[56:57]
	v_lshl_add_u32 v29, v20, 6, 0
	v_lshl_add_u64 v[44:45], s[44:45], 2, v[56:57]
	v_lshl_add_u64 v[62:63], s[56:57], 2, v[56:57]
	v_lshl_add_u64 v[72:73], s[54:55], 2, v[56:57]
	v_lshl_add_u64 v[80:81], s[52:53], 2, v[56:57]
	v_lshl_add_u64 v[82:83], s[50:51], 2, v[56:57]
	ds_read_b128 v[68:71], v29
	ds_read_b128 v[76:79], v29 offset:16
	global_load_dword v86, v[18:19], off
	s_nop 0
	s_nop 0
	global_load_dword v30, v[30:31], off
	s_nop 0
	s_nop 0
	global_load_dword v88, v[44:45], off
	global_load_dword v20, v[62:63], off
	global_load_dword v22, v[72:73], off
	global_load_dword v18, v[80:81], off
	global_load_dword v16, v[82:83], off
	v_add_u32_e64 v28, s2, v50
	v_lshl_add_u32 v17, v28, 6, 0
	v_add_u32_e32 v27, s64, v50
	v_add_u32_e32 v25, s68, v50
	v_add_u32_e32 v24, s65, v50
	v_add_u32_e32 v21, s75, v50
	v_add_u32_e64 v23, s74, v50
	v_add_u32_e32 v26, s79, v50
	s_or_b32 s78, s11, 8
	s_or_b32 s39, s11, 9
	s_or_b32 s12, s11, 10
	s_mul_hi_u32 s43, s10, s78
	s_mul_i32 s42, s10, s78
	s_mul_hi_u32 s41, s10, s39
	s_mul_i32 s40, s10, s39
	s_mul_hi_u32 s35, s10, s12
	s_mul_i32 s34, s10, s12
	v_add_u32_e32 v64, s78, v50
	s_or_b32 s3, s11, 56
	v_writelane_b32 v254, s3, 28
	s_or_b32 s3, s11, 57
	s_nop 0
	v_writelane_b32 v254, s3, 30
	s_or_b32 s3, s11, 58
	s_nop 0
	v_writelane_b32 v254, s3, 31
	s_or_b32 s3, s11, 59
	s_nop 0
	v_writelane_b32 v254, s3, 32
	s_or_b32 s3, s11, 60
	s_nop 0
	v_writelane_b32 v254, s3, 34
	s_or_b32 s3, s11, 61
	s_or_b32 s36, s11, 11
	v_writelane_b32 v254, s3, 36
	s_or_b32 s3, s11, 62
	s_or_b32 s13, s11, 12
	s_or_b32 s37, s11, 13
	s_or_b32 s16, s11, 14
	s_or_b32 s38, s11, 15
	s_nop 0
	v_writelane_b32 v254, s3, 38
	s_or_b32 s3, s11, 63
	s_mul_hi_u32 s31, s10, s36
	s_mul_i32 s30, s10, s36
	s_nop 0
	v_writelane_b32 v254, s3, 39
	s_mul_hi_u32 s29, s10, s13
	s_mul_i32 s28, s10, s13
	s_mul_hi_u32 s23, s10, s37
	s_mul_i32 s22, s10, s37
	s_mul_hi_u32 s5, s10, s16
	s_mul_i32 s4, s10, s16
	s_waitcnt vmcnt(7) lgkmcnt(1)
	s_nop 0
	v_pk_fma_f32 v[44:45], v[84:85], v[68:69], v[12:13] op_sel_hi:[0,1,1]
	v_pk_fma_f32 v[70:71], v[84:85], v[70:71], v[14:15] op_sel_hi:[0,1,1]
	s_waitcnt lgkmcnt(0)
	s_nop 0
	v_pk_fma_f32 v[76:77], v[84:85], v[76:77], v[8:9] op_sel_hi:[0,1,1]
	v_pk_fma_f32 v[78:79], v[84:85], v[78:79], v[10:11] op_sel_hi:[0,1,1]
	ds_read_b128 v[8:11], v29 offset:32
	ds_read_b128 v[12:15], v29 offset:48
	s_mul_hi_u32 s3, s10, s38
	s_mul_i32 s2, s10, s38
	v_add_u32_e32 v65, s39, v50
	s_waitcnt lgkmcnt(1)
	v_pk_fma_f32 v[8:9], v[84:85], v[8:9], v[4:5] op_sel_hi:[0,1,1]
	v_pk_fma_f32 v[10:11], v[84:85], v[10:11], v[6:7] op_sel_hi:[0,1,1]
	s_waitcnt lgkmcnt(0)
	s_nop 0
	v_pk_fma_f32 v[12:13], v[84:85], v[12:13], v[0:1] op_sel_hi:[0,1,1]
	v_pk_fma_f32 v[14:15], v[84:85], v[14:15], v[2:3] op_sel_hi:[0,1,1]
	ds_read_b128 v[0:3], v17
	ds_read_b128 v[4:7], v17 offset:16
	v_add_u32_e32 v37, s12, v50
	v_add_u32_e32 v36, s36, v50
	v_add_u32_e32 v35, s13, v50
	v_add_u32_e32 v34, s37, v50
	v_add_u32_e32 v33, s16, v50
	v_add_u32_e32 v32, s38, v50
	s_or_b32 s17, s11, 16
	s_or_b32 s76, s11, 17
	s_or_b32 s71, s11, 18
	s_or_b32 s77, s11, 19
	s_mul_hi_u32 s69, s10, s17
	s_mul_i32 s68, s10, s17
	s_mul_hi_u32 s65, s10, s76
	s_waitcnt vmcnt(6) lgkmcnt(1)
	v_pk_fma_f32 v[28:29], v[86:87], v[0:1], v[44:45] op_sel_hi:[0,1,1]
	v_pk_fma_f32 v[70:71], v[86:87], v[2:3], v[70:71] op_sel_hi:[0,1,1]
	s_waitcnt lgkmcnt(0)
	s_nop 0
	v_pk_fma_f32 v[76:77], v[86:87], v[4:5], v[76:77] op_sel_hi:[0,1,1]
	v_pk_fma_f32 v[78:79], v[86:87], v[6:7], v[78:79] op_sel_hi:[0,1,1]
	ds_read_b128 v[0:3], v17 offset:32
	ds_read_b128 v[4:7], v17 offset:48
	v_lshl_add_u32 v17, v27, 6, 0
	s_mul_i32 s64, s10, s76
	s_mul_hi_u32 s75, s10, s71
	s_waitcnt lgkmcnt(1)
	s_nop 0
	v_pk_fma_f32 v[8:9], v[86:87], v[0:1], v[8:9] op_sel_hi:[0,1,1]
	v_pk_fma_f32 v[10:11], v[86:87], v[2:3], v[10:11] op_sel_hi:[0,1,1]
	s_waitcnt lgkmcnt(0)
	s_nop 0
	v_pk_fma_f32 v[12:13], v[86:87], v[4:5], v[12:13] op_sel_hi:[0,1,1]
	v_pk_fma_f32 v[14:15], v[86:87], v[6:7], v[14:15] op_sel_hi:[0,1,1]
	ds_read_b128 v[0:3], v17
	ds_read_b128 v[4:7], v17 offset:16
	s_mul_i32 s74, s10, s71
	s_mul_hi_u32 s83, s10, s77
	s_mul_i32 s82, s10, s77
	s_waitcnt vmcnt(5) lgkmcnt(1)
	v_pk_fma_f32 v[28:29], v[30:31], v[0:1], v[28:29] op_sel_hi:[0,1,1]
	v_pk_fma_f32 v[70:71], v[30:31], v[2:3], v[70:71] op_sel_hi:[0,1,1]
	s_waitcnt lgkmcnt(0)
	s_nop 0
	v_pk_fma_f32 v[76:77], v[30:31], v[4:5], v[76:77] op_sel_hi:[0,1,1]
	v_pk_fma_f32 v[78:79], v[30:31], v[6:7], v[78:79] op_sel_hi:[0,1,1]
	ds_read_b128 v[0:3], v17 offset:32
	ds_read_b128 v[4:7], v17 offset:48
	v_lshl_add_u32 v17, v25, 6, 0
	s_or_b32 s19, s11, 20
	s_or_b32 s18, s11, 21
	s_waitcnt lgkmcnt(1)
	s_nop 0
	v_pk_fma_f32 v[80:81], v[30:31], v[0:1], v[8:9] op_sel_hi:[0,1,1]
	v_pk_fma_f32 v[10:11], v[30:31], v[2:3], v[10:11] op_sel_hi:[0,1,1]
	s_waitcnt lgkmcnt(0)
	s_nop 0
	v_pk_fma_f32 v[12:13], v[30:31], v[4:5], v[12:13] op_sel_hi:[0,1,1]
	v_pk_fma_f32 v[14:15], v[30:31], v[6:7], v[14:15] op_sel_hi:[0,1,1]
	ds_read_b128 v[2:5], v17
	ds_read_b128 v[6:9], v17 offset:16
	v_lshl_add_u64 v[0:1], s[42:43], 2, v[56:57]
	s_or_b32 s20, s11, 22
	s_or_b32 s21, s11, 23
	s_waitcnt vmcnt(4) lgkmcnt(1)
	s_nop 0
	v_pk_fma_f32 v[28:29], v[88:89], v[2:3], v[28:29] op_sel_hi:[0,1,1]
	v_pk_fma_f32 v[30:31], v[88:89], v[4:5], v[70:71] op_sel_hi:[0,1,1]
	ds_read_b128 v[2:5], v17 offset:32
	s_waitcnt lgkmcnt(1)
	s_nop 0
	v_pk_fma_f32 v[70:71], v[88:89], v[6:7], v[76:77] op_sel_hi:[0,1,1]
	v_pk_fma_f32 v[76:77], v[88:89], v[8:9], v[78:79] op_sel_hi:[0,1,1]
	ds_read_b128 v[6:9], v17 offset:48
	v_lshl_add_u32 v17, v24, 6, 0
	s_waitcnt lgkmcnt(1)
	s_nop 0
	v_pk_fma_f32 v[78:79], v[88:89], v[2:3], v[80:81] op_sel_hi:[0,1,1]
	v_pk_fma_f32 v[80:81], v[88:89], v[4:5], v[10:11] op_sel_hi:[0,1,1]
	v_lshl_add_u64 v[2:3], s[40:41], 2, v[56:57]
	s_waitcnt lgkmcnt(0)
	s_nop 0
	v_pk_fma_f32 v[24:25], v[88:89], v[6:7], v[12:13] op_sel_hi:[0,1,1]
	v_pk_fma_f32 v[82:83], v[88:89], v[8:9], v[14:15] op_sel_hi:[0,1,1]
	ds_read_b128 v[4:7], v17
	ds_read_b128 v[8:11], v17 offset:16
	v_lshl_add_u64 v[14:15], s[30:31], 2, v[56:57]
	s_mul_hi_u32 s1, s10, s19
	s_mul_i32 s0, s10, s19
	s_waitcnt vmcnt(3) lgkmcnt(1)
	s_nop 0
	v_pk_fma_f32 v[30:31], v[20:21], v[6:7], v[30:31] op_sel_hi:[0,1,1]
	s_waitcnt lgkmcnt(0)
	s_nop 0
	v_pk_fma_f32 v[70:71], v[20:21], v[8:9], v[70:71] op_sel_hi:[0,1,1]
	v_pk_fma_f32 v[76:77], v[20:21], v[10:11], v[76:77] op_sel_hi:[0,1,1]
	ds_read_b128 v[6:9], v17 offset:32
	ds_read_b128 v[10:13], v17 offset:48
	v_lshl_add_u32 v17, v21, 6, 0
	v_pk_fma_f32 v[28:29], v[20:21], v[4:5], v[28:29] op_sel_hi:[0,1,1]
	v_lshl_add_u64 v[4:5], s[34:35], 2, v[56:57]
	s_waitcnt lgkmcnt(1)
	s_nop 0
	v_pk_fma_f32 v[78:79], v[20:21], v[6:7], v[78:79] op_sel_hi:[0,1,1]
	v_pk_fma_f32 v[80:81], v[20:21], v[8:9], v[80:81] op_sel_hi:[0,1,1]
	s_waitcnt lgkmcnt(0)
	s_nop 0
	v_pk_fma_f32 v[24:25], v[20:21], v[10:11], v[24:25] op_sel_hi:[0,1,1]
	v_pk_fma_f32 v[82:83], v[20:21], v[12:13], v[82:83] op_sel_hi:[0,1,1]
	ds_read_b128 v[6:9], v17
	ds_read_b128 v[10:13], v17 offset:16
	v_lshl_add_u64 v[20:21], s[28:29], 2, v[56:57]
	v_add_u32_e64 v66, s17, v50
	s_mul_hi_u32 s13, s10, s18
	s_waitcnt vmcnt(2) lgkmcnt(1)
	v_pk_fma_f32 v[28:29], v[22:23], v[6:7], v[28:29] op_sel_hi:[0,1,1]
	v_pk_fma_f32 v[30:31], v[22:23], v[8:9], v[30:31] op_sel_hi:[0,1,1]
	ds_read_b128 v[6:9], v17 offset:32
	s_waitcnt lgkmcnt(1)
	s_nop 0
	v_pk_fma_f32 v[70:71], v[22:23], v[10:11], v[70:71] op_sel_hi:[0,1,1]
	v_pk_fma_f32 v[76:77], v[22:23], v[12:13], v[76:77] op_sel_hi:[0,1,1]
	ds_read_b128 v[10:13], v17 offset:48
	v_lshl_add_u32 v17, v23, 6, 0
	s_waitcnt lgkmcnt(1)
	s_nop 0
	v_pk_fma_f32 v[78:79], v[22:23], v[6:7], v[78:79] op_sel_hi:[0,1,1]
	v_pk_fma_f32 v[80:81], v[22:23], v[8:9], v[80:81] op_sel_hi:[0,1,1]
	s_mul_i32 s12, s10, s18
	s_waitcnt lgkmcnt(0)
	v_pk_fma_f32 v[84:85], v[22:23], v[10:11], v[24:25] op_sel_hi:[0,1,1]
	v_pk_fma_f32 v[82:83], v[22:23], v[12:13], v[82:83] op_sel_hi:[0,1,1]
	ds_read_b128 v[6:9], v17
	ds_read_b128 v[10:13], v17 offset:16
	v_lshl_add_u64 v[22:23], s[22:23], 2, v[56:57]
	v_lshl_add_u64 v[24:25], s[4:5], 2, v[56:57]
	s_mul_hi_u32 s39, s10, s20
	s_waitcnt vmcnt(1) lgkmcnt(1)
	v_pk_fma_f32 v[86:87], v[18:19], v[6:7], v[28:29] op_sel_hi:[0,1,1]
	v_pk_fma_f32 v[88:89], v[18:19], v[8:9], v[30:31] op_sel_hi:[0,1,1]
	s_waitcnt lgkmcnt(0)
	s_nop 0
	v_pk_fma_f32 v[70:71], v[18:19], v[10:11], v[70:71] op_sel_hi:[0,1,1]
	v_pk_fma_f32 v[76:77], v[18:19], v[12:13], v[76:77] op_sel_hi:[0,1,1]
	ds_read_b128 v[6:9], v17 offset:32
	ds_read_b128 v[10:13], v17 offset:48
	v_lshl_add_u32 v17, v26, 6, 0
	s_mul_i32 s38, s10, s20
	s_mul_hi_u32 s37, s10, s21
	s_waitcnt lgkmcnt(1)
	s_nop 0
	v_pk_fma_f32 v[90:91], v[18:19], v[6:7], v[78:79] op_sel_hi:[0,1,1]
	v_pk_fma_f32 v[80:81], v[18:19], v[8:9], v[80:81] op_sel_hi:[0,1,1]
	s_waitcnt lgkmcnt(0)
	s_nop 0
	v_pk_fma_f32 v[28:29], v[18:19], v[10:11], v[84:85] op_sel_hi:[0,1,1]
	v_pk_fma_f32 v[30:31], v[18:19], v[12:13], v[82:83] op_sel_hi:[0,1,1]
	ds_read_b128 v[6:9], v17
	ds_read_b128 v[10:13], v17 offset:16
	s_mul_i32 s36, s10, s21
	v_add_u32_e32 v58, s76, v50
	v_add_u32_e32 v43, s71, v50
	s_waitcnt vmcnt(0) lgkmcnt(1)
	v_pk_fma_f32 v[18:19], v[16:17], v[6:7], v[86:87] op_sel_hi:[0,1,1]
	v_pk_fma_f32 v[26:27], v[16:17], v[8:9], v[88:89] op_sel_hi:[0,1,1]
	ds_read_b128 v[6:9], v17 offset:32
	s_waitcnt lgkmcnt(1)
	s_nop 0
	v_pk_fma_f32 v[10:11], v[16:17], v[10:11], v[70:71] op_sel_hi:[0,1,1]
	v_pk_fma_f32 v[12:13], v[16:17], v[12:13], v[76:77] op_sel_hi:[0,1,1]
	ds_read_b128 v[76:79], v17 offset:48
	v_lshl_add_u64 v[70:71], s[2:3], 2, v[56:57]
	s_waitcnt lgkmcnt(1)
	s_nop 0
	v_pk_fma_f32 v[6:7], v[16:17], v[6:7], v[90:91] op_sel_hi:[0,1,1]
	v_pk_fma_f32 v[8:9], v[16:17], v[8:9], v[80:81] op_sel_hi:[0,1,1]
	v_lshl_add_u32 v17, v64, 6, 0
	global_load_dword v64, v[0:1], off
	global_load_dword v80, v[2:3], off
	global_load_dword v82, v[4:5], off
	s_waitcnt lgkmcnt(0)
	s_nop 0
	v_pk_fma_f32 v[84:85], v[16:17], v[76:77], v[28:29] op_sel_hi:[0,1,1]
	v_pk_fma_f32 v[30:31], v[16:17], v[78:79], v[30:31] op_sel_hi:[0,1,1]
	ds_read_b128 v[76:79], v17
	global_load_dword v28, v[14:15], off
	s_nop 0
	s_nop 0
	global_load_dword v14, v[20:21], off
	global_load_dword v2, v[22:23], off
	global_load_dword v0, v[24:25], off
	global_load_dword v4, v[70:71], off
	ds_read_b128 v[20:23], v17 offset:16
	v_lshl_add_u32 v1, v65, 6, 0
	v_lshl_add_u32 v5, v32, 6, 0
	s_or_b32 s7, s11, 48
	v_add_u32_e32 v42, s77, v50
	v_add_u32_e32 v59, s19, v50
	v_add_u32_e32 v60, s18, v50
	v_add_u32_e32 v52, s20, v50
	v_add_u32_e32 v47, s21, v50
	s_or_b32 s24, s11, 24
	s_or_b32 s25, s11, 25
	s_or_b32 s26, s11, 26
	s_or_b32 s27, s11, 27
	s_mul_hi_u32 s17, s10, s24
	s_mul_i32 s16, s10, s24
	s_mul_hi_u32 s19, s10, s25
	s_mul_i32 s18, s10, s25
	s_mul_hi_u32 s21, s10, s26
	s_mul_i32 s20, s10, s26
	v_add_u32_e32 v46, s24, v50
	v_add_u32_e32 v41, s25, v50
	s_mul_hi_u32 s25, s10, s27
	s_mul_i32 s24, s10, s27
	s_or_b32 s70, s11, 28
	s_or_b32 s62, s11, 31
	s_or_b32 s73, s11, 29
	s_or_b32 s72, s11, 30
	v_add_u32_e32 v40, s26, v50
	v_add_u32_e32 v39, s27, v50
	s_mul_hi_u32 s27, s10, s70
	s_mul_i32 s26, s10, s70
	s_mul_hi_u32 s45, s10, s62
	s_mul_i32 s44, s10, s62
	s_mul_hi_u32 s49, s10, s73
	s_mul_i32 s48, s10, s73
	s_mul_hi_u32 s47, s10, s72
	s_mul_i32 s46, s10, s72
	v_lshl_add_u64 v[90:91], s[48:49], 2, v[56:57]
	v_lshl_add_u64 v[96:97], s[46:47], 2, v[56:57]
	v_add_u32_e32 v38, s70, v50
	v_add_u32_e32 v74, s73, v50
	v_add_u32_e64 v73, s72, v50
	v_add_u32_e32 v72, s62, v50
	s_or_b32 s63, s11, 32
	s_or_b32 s67, s11, 34
	s_or_b32 s66, s11, 33
	s_or_b32 s61, s11, 35
	s_add_i32 s70, s11, 64
	s_mul_hi_u32 s91, s10, s63
	s_mul_i32 s90, s10, s63
	s_mul_hi_u32 s79, s10, s67
	s_mul_i32 s78, s10, s67
	v_writelane_b32 v254, s70, 40
	s_mul_hi_u32 s87, s10, s66
	s_mul_i32 s86, s10, s66
	s_mul_hi_u32 s71, s10, s61
	s_mul_i32 s70, s10, s61
	s_or_b32 s59, s11, 36
	s_or_b32 s95, s11, 39
	s_or_b32 s60, s11, 37
	s_or_b32 s58, s11, 38
	s_mul_hi_u32 s81, s10, s59
	s_mul_i32 s80, s10, s59
	v_add_u32_e32 v69, s63, v50
	s_mul_hi_u32 s77, s10, s95
	s_mul_i32 s76, s10, s95
	s_mul_hi_u32 s73, s10, s60
	s_mul_i32 s72, s10, s60
	v_add_u32_e32 v63, s66, v50
	v_add_u32_e64 v62, s67, v50
	s_mul_hi_u32 s67, s10, s58
	s_mul_i32 s66, s10, s58
	v_add_u32_e32 v61, s61, v50
	s_waitcnt vmcnt(7) lgkmcnt(1)
	v_pk_fma_f32 v[24:25], v[64:65], v[76:77], v[18:19] op_sel_hi:[0,1,1]
	s_waitcnt lgkmcnt(0)
	s_nop 0
	v_pk_fma_f32 v[20:21], v[64:65], v[20:21], v[10:11] op_sel_hi:[0,1,1]
	v_pk_fma_f32 v[22:23], v[64:65], v[22:23], v[12:13] op_sel_hi:[0,1,1]
	ds_read_b128 v[10:13], v17 offset:32
	ds_read_b128 v[16:19], v17 offset:48
	v_pk_fma_f32 v[26:27], v[64:65], v[78:79], v[26:27] op_sel_hi:[0,1,1]
	v_readlane_b32 s42, v254, 30
	v_add_u32_e32 v55, s59, v50
	s_waitcnt lgkmcnt(1)
	v_pk_fma_f32 v[78:79], v[64:65], v[10:11], v[6:7] op_sel_hi:[0,1,1]
	v_pk_fma_f32 v[86:87], v[64:65], v[12:13], v[8:9] op_sel_hi:[0,1,1]
	ds_read_b128 v[6:9], v1
	ds_read_b128 v[10:13], v1 offset:16
	s_waitcnt lgkmcnt(2)
	s_nop 0
	v_pk_fma_f32 v[16:17], v[64:65], v[16:17], v[84:85] op_sel_hi:[0,1,1]
	v_pk_fma_f32 v[18:19], v[64:65], v[18:19], v[30:31] op_sel_hi:[0,1,1]
	v_add_u32_e32 v45, s60, v50
	s_waitcnt vmcnt(6) lgkmcnt(1)
	v_pk_fma_f32 v[24:25], v[80:81], v[6:7], v[24:25] op_sel_hi:[0,1,1]
	v_pk_fma_f32 v[26:27], v[80:81], v[8:9], v[26:27] op_sel_hi:[0,1,1]
	s_waitcnt lgkmcnt(0)
	s_nop 0
	v_pk_fma_f32 v[20:21], v[80:81], v[10:11], v[20:21] op_sel_hi:[0,1,1]
	v_pk_fma_f32 v[22:23], v[80:81], v[12:13], v[22:23] op_sel_hi:[0,1,1]
	ds_read_b128 v[6:9], v1 offset:32
	ds_read_b128 v[10:13], v1 offset:48
	v_lshl_add_u32 v1, v37, 6, 0
	v_add_u32_e64 v44, s58, v50
	v_add_u32_e32 v75, s95, v50
	s_waitcnt lgkmcnt(1)
	v_pk_fma_f32 v[30:31], v[80:81], v[6:7], v[78:79] op_sel_hi:[0,1,1]
	v_pk_fma_f32 v[78:79], v[80:81], v[8:9], v[86:87] op_sel_hi:[0,1,1]
	s_waitcnt lgkmcnt(0)
	s_nop 0
	v_pk_fma_f32 v[16:17], v[80:81], v[10:11], v[16:17] op_sel_hi:[0,1,1]
	v_pk_fma_f32 v[18:19], v[80:81], v[12:13], v[18:19] op_sel_hi:[0,1,1]
	ds_read_b128 v[6:9], v1
	ds_read_b128 v[10:13], v1 offset:16
	s_or_b32 s94, s11, 40
	s_or_b32 s96, s11, 41
	s_or_b32 s97, s11, 42
	s_waitcnt vmcnt(5) lgkmcnt(1)
	v_pk_fma_f32 v[24:25], v[82:83], v[6:7], v[24:25] op_sel_hi:[0,1,1]
	v_pk_fma_f32 v[26:27], v[82:83], v[8:9], v[26:27] op_sel_hi:[0,1,1]
	s_waitcnt lgkmcnt(0)
	s_nop 0
	v_pk_fma_f32 v[20:21], v[82:83], v[10:11], v[20:21] op_sel_hi:[0,1,1]
	v_pk_fma_f32 v[22:23], v[82:83], v[12:13], v[22:23] op_sel_hi:[0,1,1]
	ds_read_b128 v[6:9], v1 offset:32
	ds_read_b128 v[10:13], v1 offset:48
	v_lshl_add_u32 v1, v36, 6, 0
	s_or_b32 s89, s11, 43
	s_mul_hi_u32 s61, s10, s94
	s_waitcnt lgkmcnt(1)
	s_nop 0
	v_pk_fma_f32 v[78:79], v[82:83], v[8:9], v[78:79] op_sel_hi:[0,1,1]
	s_waitcnt lgkmcnt(0)
	s_nop 0
	v_pk_fma_f32 v[36:37], v[82:83], v[10:11], v[16:17] op_sel_hi:[0,1,1]
	v_pk_fma_f32 v[12:13], v[82:83], v[12:13], v[18:19] op_sel_hi:[0,1,1]
	ds_read_b128 v[8:11], v1
	ds_read_b128 v[16:19], v1 offset:16
	v_pk_fma_f32 v[30:31], v[82:83], v[6:7], v[30:31] op_sel_hi:[0,1,1]
	v_lshl_add_u64 v[6:7], s[68:69], 2, v[56:57]
	s_mul_i32 s60, s10, s94
	s_waitcnt vmcnt(4) lgkmcnt(1)
	v_pk_fma_f32 v[24:25], v[28:29], v[8:9], v[24:25] op_sel_hi:[0,1,1]
	v_pk_fma_f32 v[26:27], v[28:29], v[10:11], v[26:27] op_sel_hi:[0,1,1]
	ds_read_b128 v[8:11], v1 offset:32
	s_waitcnt lgkmcnt(1)
	s_nop 0
	v_pk_fma_f32 v[80:81], v[28:29], v[16:17], v[20:21] op_sel_hi:[0,1,1]
	v_pk_fma_f32 v[82:83], v[28:29], v[18:19], v[22:23] op_sel_hi:[0,1,1]
	ds_read_b128 v[18:21], v1 offset:48
	v_lshl_add_u32 v1, v35, 6, 0
	s_waitcnt lgkmcnt(1)
	s_nop 0
	v_pk_fma_f32 v[30:31], v[28:29], v[8:9], v[30:31] op_sel_hi:[0,1,1]
	v_pk_fma_f32 v[78:79], v[28:29], v[10:11], v[78:79] op_sel_hi:[0,1,1]
	v_lshl_add_u64 v[16:17], s[64:65], 2, v[56:57]
	s_waitcnt lgkmcnt(0)
	s_nop 0
	v_pk_fma_f32 v[12:13], v[28:29], v[20:21], v[12:13] op_sel_hi:[0,1,1]
	ds_read_b128 v[8:11], v1
	ds_read_b128 v[20:23], v1 offset:16
	v_pk_fma_f32 v[36:37], v[28:29], v[18:19], v[36:37] op_sel_hi:[0,1,1]
	v_lshl_add_u64 v[18:19], s[74:75], 2, v[56:57]
	s_mul_hi_u32 s59, s10, s96
	s_waitcnt vmcnt(3) lgkmcnt(1)
	v_pk_fma_f32 v[28:29], v[14:15], v[8:9], v[24:25] op_sel_hi:[0,1,1]
	v_pk_fma_f32 v[26:27], v[14:15], v[10:11], v[26:27] op_sel_hi:[0,1,1]
	s_waitcnt lgkmcnt(0)
	s_nop 0
	v_pk_fma_f32 v[82:83], v[14:15], v[22:23], v[82:83] op_sel_hi:[0,1,1]
	ds_read_b128 v[8:11], v1 offset:32
	ds_read_b128 v[22:25], v1 offset:48
	v_lshl_add_u32 v1, v34, 6, 0
	v_pk_fma_f32 v[80:81], v[14:15], v[20:21], v[80:81] op_sel_hi:[0,1,1]
	v_lshl_add_u64 v[20:21], s[82:83], 2, v[56:57]
	s_waitcnt lgkmcnt(1)
	s_nop 0
	v_pk_fma_f32 v[30:31], v[14:15], v[8:9], v[30:31] op_sel_hi:[0,1,1]
	v_pk_fma_f32 v[78:79], v[14:15], v[10:11], v[78:79] op_sel_hi:[0,1,1]
	s_waitcnt lgkmcnt(0)
	s_nop 0
	v_pk_fma_f32 v[34:35], v[14:15], v[22:23], v[36:37] op_sel_hi:[0,1,1]
	v_pk_fma_f32 v[24:25], v[14:15], v[24:25], v[12:13] op_sel_hi:[0,1,1]
	ds_read_b128 v[8:11], v1
	ds_read_b128 v[12:15], v1 offset:16
	v_lshl_add_u64 v[22:23], s[0:1], 2, v[56:57]
	s_mul_i32 s58, s10, s96
	s_mul_hi_u32 s63, s10, s97
	s_waitcnt vmcnt(2) lgkmcnt(1)
	s_nop 0
	v_pk_fma_f32 v[28:29], v[2:3], v[8:9], v[28:29] op_sel_hi:[0,1,1]
	v_pk_fma_f32 v[26:27], v[2:3], v[10:11], v[26:27] op_sel_hi:[0,1,1]
	ds_read_b128 v[8:11], v1 offset:32
	s_waitcnt lgkmcnt(1)
	s_nop 0
	v_pk_fma_f32 v[36:37], v[2:3], v[12:13], v[80:81] op_sel_hi:[0,1,1]
	v_pk_fma_f32 v[80:81], v[2:3], v[14:15], v[82:83] op_sel_hi:[0,1,1]
	ds_read_b128 v[12:15], v1 offset:48
	v_lshl_add_u32 v1, v33, 6, 0
	s_waitcnt lgkmcnt(1)
	s_nop 0
	v_pk_fma_f32 v[30:31], v[2:3], v[8:9], v[30:31] op_sel_hi:[0,1,1]
	v_pk_fma_f32 v[78:79], v[2:3], v[10:11], v[78:79] op_sel_hi:[0,1,1]
	s_mul_i32 s62, s10, s97
	s_waitcnt lgkmcnt(0)
	v_pk_fma_f32 v[34:35], v[2:3], v[12:13], v[34:35] op_sel_hi:[0,1,1]
	v_pk_fma_f32 v[2:3], v[2:3], v[14:15], v[24:25] op_sel_hi:[0,1,1]
	ds_read_b128 v[8:11], v1
	ds_read_b128 v[12:15], v1 offset:16
	v_lshl_add_u64 v[24:25], s[12:13], 2, v[56:57]
	s_mul_hi_u32 s57, s10, s89
	s_mul_i32 s56, s10, s89
	s_waitcnt vmcnt(1) lgkmcnt(1)
	s_nop 0
	v_pk_fma_f32 v[28:29], v[0:1], v[8:9], v[28:29] op_sel_hi:[0,1,1]
	v_pk_fma_f32 v[82:83], v[0:1], v[10:11], v[26:27] op_sel_hi:[0,1,1]
	s_waitcnt lgkmcnt(0)
	s_nop 0
	v_pk_fma_f32 v[36:37], v[0:1], v[12:13], v[36:37] op_sel_hi:[0,1,1]
	v_pk_fma_f32 v[84:85], v[0:1], v[14:15], v[80:81] op_sel_hi:[0,1,1]
	ds_read_b128 v[8:11], v1 offset:32
	ds_read_b128 v[12:15], v1 offset:48
	v_lshl_add_u64 v[26:27], s[38:39], 2, v[56:57]
	s_or_b32 s88, s11, 44
	s_or_b32 s85, s11, 45
	s_waitcnt lgkmcnt(1)
	s_nop 0
	v_pk_fma_f32 v[86:87], v[0:1], v[8:9], v[30:31] op_sel_hi:[0,1,1]
	v_pk_fma_f32 v[88:89], v[0:1], v[10:11], v[78:79] op_sel_hi:[0,1,1]
	s_waitcnt lgkmcnt(0)
	s_nop 0
	v_pk_fma_f32 v[32:33], v[0:1], v[12:13], v[34:35] op_sel_hi:[0,1,1]
	v_pk_fma_f32 v[34:35], v[0:1], v[14:15], v[2:3] op_sel_hi:[0,1,1]
	ds_read_b128 v[0:3], v5
	ds_read_b128 v[8:11], v5 offset:16
	ds_read_b128 v[78:81], v5 offset:32
	s_or_b32 s84, s11, 46
	s_or_b32 s6, s11, 47
	s_waitcnt vmcnt(0) lgkmcnt(2)
	s_nop 0
	v_pk_fma_f32 v[28:29], v[4:5], v[0:1], v[28:29] op_sel_hi:[0,1,1]
	v_pk_fma_f32 v[30:31], v[4:5], v[2:3], v[82:83] op_sel_hi:[0,1,1]
	s_waitcnt lgkmcnt(1)
	s_nop 0
	v_pk_fma_f32 v[14:15], v[4:5], v[10:11], v[84:85] op_sel_hi:[0,1,1]
	ds_read_b128 v[0:3], v5 offset:48
	s_waitcnt lgkmcnt(1)
	s_nop 0
	v_pk_fma_f32 v[10:11], v[4:5], v[80:81], v[88:89] op_sel_hi:[0,1,1]
	global_load_dword v80, v[6:7], off
	global_load_dword v82, v[16:17], off
	s_nop 0
	s_nop 0
	global_load_dword v18, v[18:19], off
	s_nop 0
	s_nop 0
	global_load_dword v16, v[20:21], off
	v_pk_fma_f32 v[12:13], v[4:5], v[8:9], v[36:37] op_sel_hi:[0,1,1]
	v_pk_fma_f32 v[8:9], v[4:5], v[78:79], v[86:87] op_sel_hi:[0,1,1]
	v_lshl_add_u32 v5, v66, 6, 0
	v_lshl_add_u64 v[36:37], s[36:37], 2, v[56:57]
	s_waitcnt lgkmcnt(0)
	s_nop 0
	v_pk_fma_f32 v[84:85], v[4:5], v[0:1], v[32:33] op_sel_hi:[0,1,1]
	v_pk_fma_f32 v[86:87], v[4:5], v[2:3], v[34:35] op_sel_hi:[0,1,1]
	ds_read_b128 v[32:35], v5
	global_load_dword v6, v[22:23], off
	global_load_dword v4, v[24:25], off
	global_load_dword v2, v[26:27], off
	global_load_dword v0, v[36:37], off
	ds_read_b128 v[20:23], v5 offset:16
	v_lshl_add_u32 v1, v58, 6, 0
	v_add_u32_e64 v19, s7, v50
	v_lshl_add_u64 v[36:37], s[16:17], 2, v[56:57]
	s_mul_hi_u32 s55, s10, s88
	s_mul_i32 s54, s10, s88
	v_add_u32_e32 v76, s94, v50
	s_mul_hi_u32 s53, s10, s85
	s_mul_i32 s52, s10, s85
	s_mul_hi_u32 s35, s10, s84
	s_mul_i32 s34, s10, s84
	s_mul_hi_u32 s31, s10, s6
	s_mul_i32 s30, s10, s6
	v_add_u32_e32 v71, s96, v50
	v_add_u32_e32 v70, s97, v50
	v_add_u32_e32 v68, s89, v50
	v_add_u32_e32 v67, s88, v50
	v_add_u32_e32 v65, s85, v50
	v_add_u32_e64 v64, s84, v50
	v_add_u32_e32 v77, s6, v50
	s_or_b32 s8, s11, 49
	s_or_b32 s9, s11, 50
	s_or_b32 s14, s11, 51
	s_or_b32 s15, s11, 52
	s_or_b32 s33, s11, 53
	s_mul_hi_u32 s29, s10, s7
	s_mul_i32 s28, s10, s7
	s_mul_hi_u32 s95, s10, s8
	s_mul_i32 s94, s10, s8
	s_mul_hi_u32 vcc_hi, s10, s9
	s_mul_i32 vcc_lo, s10, s9
	v_readlane_b32 s43, v254, 28
	v_readlane_b32 s40, v254, 32
	s_mul_hi_u32 s3, s10, s14
	s_mul_i32 s2, s10, s14
	s_mul_hi_u32 s5, s10, s15
	s_mul_i32 s4, s10, s15
	s_mul_hi_u32 s23, s10, s33
	s_mul_i32 s22, s10, s33
	s_or_b32 s92, s11, 54
	s_or_b32 s93, s11, 55
	s_mul_hi_u32 s97, s10, s92
	s_mul_i32 s96, s10, s92
	s_mul_hi_u32 s89, s10, s93
	s_mul_i32 s88, s10, s93
	v_readlane_b32 s7, v254, 38
	v_readlane_b32 s41, v254, 31
	v_add_u32_e32 v78, s9, v50
	v_add_u32_e32 v79, s14, v50
	s_mul_hi_u32 s85, s10, s43
	s_mul_i32 s84, s10, s43
	v_readlane_b32 s39, v254, 34
	v_readlane_b32 s38, v254, 36
	v_add_u32_e64 v66, s8, v50
	v_readlane_b32 s6, v254, 39
	s_mul_hi_u32 s83, s10, s42
	s_mul_i32 s82, s10, s42
	s_mul_hi_u32 s75, s10, s41
	s_mul_i32 s74, s10, s41
	s_mul_hi_u32 s69, s10, s40
	s_mul_i32 s68, s10, s40
	s_mul_hi_u32 s65, s10, s39
	s_mul_i32 s64, s10, s39
	s_mul_hi_u32 s1, s10, s38
	s_mul_i32 s0, s10, s38
	s_mul_hi_u32 s13, s10, s7
	s_mul_i32 s12, s10, s7
	s_mul_hi_u32 s37, s10, s6
	s_waitcnt vmcnt(7) lgkmcnt(1)
	v_pk_fma_f32 v[24:25], v[80:81], v[32:33], v[28:29] op_sel_hi:[0,1,1]
	v_pk_fma_f32 v[26:27], v[80:81], v[34:35], v[30:31] op_sel_hi:[0,1,1]
	s_waitcnt lgkmcnt(0)
	s_nop 0
	v_pk_fma_f32 v[28:29], v[80:81], v[20:21], v[12:13] op_sel_hi:[0,1,1]
	v_pk_fma_f32 v[30:31], v[80:81], v[22:23], v[14:15] op_sel_hi:[0,1,1]
	ds_read_b128 v[12:15], v5 offset:32
	ds_read_b128 v[20:23], v5 offset:48
	s_mul_i32 s36, s10, s6
	s_cmpk_lt_u32 s11, 0xc0
	v_readlane_b32 s11, v254, 40
	s_waitcnt lgkmcnt(1)
	s_nop 0
	v_pk_fma_f32 v[32:33], v[80:81], v[12:13], v[8:9] op_sel_hi:[0,1,1]
	v_pk_fma_f32 v[34:35], v[80:81], v[14:15], v[10:11] op_sel_hi:[0,1,1]
	ds_read_b128 v[8:11], v1
	ds_read_b128 v[12:15], v1 offset:16
	s_waitcnt lgkmcnt(2)
	s_nop 0
	v_pk_fma_f32 v[20:21], v[80:81], v[20:21], v[84:85] op_sel_hi:[0,1,1]
	v_pk_fma_f32 v[22:23], v[80:81], v[22:23], v[86:87] op_sel_hi:[0,1,1]
	v_lshl_add_u64 v[84:85], s[18:19], 2, v[56:57]
	s_waitcnt vmcnt(6) lgkmcnt(1)
	s_nop 0
	v_pk_fma_f32 v[24:25], v[82:83], v[8:9], v[24:25] op_sel_hi:[0,1,1]
	v_pk_fma_f32 v[26:27], v[82:83], v[10:11], v[26:27] op_sel_hi:[0,1,1]
	s_waitcnt lgkmcnt(0)
	s_nop 0
	v_pk_fma_f32 v[28:29], v[82:83], v[12:13], v[28:29] op_sel_hi:[0,1,1]
	v_pk_fma_f32 v[30:31], v[82:83], v[14:15], v[30:31] op_sel_hi:[0,1,1]
	ds_read_b128 v[8:11], v1 offset:32
	ds_read_b128 v[12:15], v1 offset:48
	v_lshl_add_u32 v1, v43, 6, 0
	v_lshl_add_u64 v[86:87], s[26:27], 2, v[56:57]
	v_add_u32_e32 v43, s92, v50
	s_waitcnt lgkmcnt(1)
	v_pk_fma_f32 v[32:33], v[82:83], v[8:9], v[32:33] op_sel_hi:[0,1,1]
	v_pk_fma_f32 v[34:35], v[82:83], v[10:11], v[34:35] op_sel_hi:[0,1,1]
	s_waitcnt lgkmcnt(0)
	s_nop 0
	v_pk_fma_f32 v[20:21], v[82:83], v[12:13], v[20:21] op_sel_hi:[0,1,1]
	v_pk_fma_f32 v[22:23], v[82:83], v[14:15], v[22:23] op_sel_hi:[0,1,1]
	ds_read_b128 v[8:11], v1
	ds_read_b128 v[12:15], v1 offset:16
	v_add_u32_e32 v80, s15, v50
	v_add_u32_e32 v81, s33, v50
	v_add_u32_e32 v82, s93, v50
	s_waitcnt vmcnt(5) lgkmcnt(1)
	v_pk_fma_f32 v[24:25], v[18:19], v[8:9], v[24:25] op_sel_hi:[0,1,1]
	v_pk_fma_f32 v[26:27], v[18:19], v[10:11], v[26:27] op_sel_hi:[0,1,1]
	s_waitcnt lgkmcnt(0)
	s_nop 0
	v_pk_fma_f32 v[28:29], v[18:19], v[12:13], v[28:29] op_sel_hi:[0,1,1]
	v_pk_fma_f32 v[30:31], v[18:19], v[14:15], v[30:31] op_sel_hi:[0,1,1]
	ds_read_b128 v[8:11], v1 offset:32
	ds_read_b128 v[12:15], v1 offset:48
	v_lshl_add_u32 v1, v42, 6, 0
	v_add_u32_e64 v42, s43, v50
	v_add_u32_e32 v83, s41, v50
	s_waitcnt lgkmcnt(1)
	v_pk_fma_f32 v[32:33], v[18:19], v[8:9], v[32:33] op_sel_hi:[0,1,1]
	v_pk_fma_f32 v[34:35], v[18:19], v[10:11], v[34:35] op_sel_hi:[0,1,1]
	s_waitcnt lgkmcnt(0)
	s_nop 0
	v_pk_fma_f32 v[20:21], v[18:19], v[12:13], v[20:21] op_sel_hi:[0,1,1]
	v_pk_fma_f32 v[22:23], v[18:19], v[14:15], v[22:23] op_sel_hi:[0,1,1]
	ds_read_b128 v[8:11], v1
	ds_read_b128 v[12:15], v1 offset:16
	s_waitcnt vmcnt(4) lgkmcnt(1)
	s_nop 0
	v_pk_fma_f32 v[24:25], v[16:17], v[8:9], v[24:25] op_sel_hi:[0,1,1]
	v_pk_fma_f32 v[26:27], v[16:17], v[10:11], v[26:27] op_sel_hi:[0,1,1]
	s_waitcnt lgkmcnt(0)
	s_nop 0
	v_pk_fma_f32 v[28:29], v[16:17], v[12:13], v[28:29] op_sel_hi:[0,1,1]
	v_pk_fma_f32 v[30:31], v[16:17], v[14:15], v[30:31] op_sel_hi:[0,1,1]
	ds_read_b128 v[8:11], v1 offset:32
	ds_read_b128 v[12:15], v1 offset:48
	v_lshl_add_u32 v1, v59, 6, 0
	v_lshl_add_u64 v[58:59], s[20:21], 2, v[56:57]
	s_waitcnt lgkmcnt(1)
	s_nop 0
	v_pk_fma_f32 v[32:33], v[16:17], v[8:9], v[32:33] op_sel_hi:[0,1,1]
	v_pk_fma_f32 v[34:35], v[16:17], v[10:11], v[34:35] op_sel_hi:[0,1,1]
	s_waitcnt lgkmcnt(0)
	s_nop 0
	v_pk_fma_f32 v[20:21], v[16:17], v[12:13], v[20:21] op_sel_hi:[0,1,1]
	v_pk_fma_f32 v[16:17], v[16:17], v[14:15], v[22:23] op_sel_hi:[0,1,1]
	ds_read_b128 v[8:11], v1
	ds_read_b128 v[12:15], v1 offset:16
	s_waitcnt vmcnt(3) lgkmcnt(1)
	s_nop 0
	v_pk_fma_f32 v[22:23], v[6:7], v[8:9], v[24:25] op_sel_hi:[0,1,1]
	v_pk_fma_f32 v[24:25], v[6:7], v[10:11], v[26:27] op_sel_hi:[0,1,1]
	ds_read_b128 v[8:11], v1 offset:32
	s_waitcnt lgkmcnt(1)
	s_nop 0
	v_pk_fma_f32 v[26:27], v[6:7], v[12:13], v[28:29] op_sel_hi:[0,1,1]
	v_pk_fma_f32 v[28:29], v[6:7], v[14:15], v[30:31] op_sel_hi:[0,1,1]
	ds_read_b128 v[12:15], v1 offset:48
	v_lshl_add_u32 v1, v60, 6, 0
	s_waitcnt lgkmcnt(1)
	s_nop 0
	v_pk_fma_f32 v[30:31], v[6:7], v[8:9], v[32:33] op_sel_hi:[0,1,1]
	v_pk_fma_f32 v[32:33], v[6:7], v[10:11], v[34:35] op_sel_hi:[0,1,1]
	s_waitcnt lgkmcnt(0)
	s_nop 0
	v_pk_fma_f32 v[20:21], v[6:7], v[12:13], v[20:21] op_sel_hi:[0,1,1]
	v_pk_fma_f32 v[14:15], v[6:7], v[14:15], v[16:17] op_sel_hi:[0,1,1]
	ds_read_b128 v[6:9], v1
	ds_read_b128 v[10:13], v1 offset:16
	s_waitcnt vmcnt(2) lgkmcnt(1)
	s_nop 0
	v_pk_fma_f32 v[16:17], v[4:5], v[6:7], v[22:23] op_sel_hi:[0,1,1]
	v_pk_fma_f32 v[22:23], v[4:5], v[8:9], v[24:25] op_sel_hi:[0,1,1]
	s_waitcnt lgkmcnt(0)
	s_nop 0
	v_pk_fma_f32 v[26:27], v[4:5], v[10:11], v[26:27] op_sel_hi:[0,1,1]
	v_pk_fma_f32 v[28:29], v[4:5], v[12:13], v[28:29] op_sel_hi:[0,1,1]
	ds_read_b128 v[6:9], v1 offset:32
	ds_read_b128 v[10:13], v1 offset:48
	v_lshl_add_u32 v1, v52, 6, 0
	v_lshl_add_u64 v[24:25], s[24:25], 2, v[56:57]
	s_waitcnt lgkmcnt(1)
	s_nop 0
	v_pk_fma_f32 v[30:31], v[4:5], v[6:7], v[30:31] op_sel_hi:[0,1,1]
	v_pk_fma_f32 v[32:33], v[4:5], v[8:9], v[32:33] op_sel_hi:[0,1,1]
	s_waitcnt lgkmcnt(0)
	s_nop 0
	v_pk_fma_f32 v[20:21], v[4:5], v[10:11], v[20:21] op_sel_hi:[0,1,1]
	v_pk_fma_f32 v[12:13], v[4:5], v[12:13], v[14:15] op_sel_hi:[0,1,1]
	ds_read_b128 v[4:7], v1
	ds_read_b128 v[8:11], v1 offset:16
	s_waitcnt vmcnt(1) lgkmcnt(1)
	s_nop 0
	v_pk_fma_f32 v[14:15], v[2:3], v[4:5], v[16:17] op_sel_hi:[0,1,1]
	v_pk_fma_f32 v[16:17], v[2:3], v[6:7], v[22:23] op_sel_hi:[0,1,1]
	ds_read_b128 v[4:7], v1 offset:32
	s_waitcnt lgkmcnt(1)
	s_nop 0
	v_pk_fma_f32 v[22:23], v[2:3], v[8:9], v[26:27] op_sel_hi:[0,1,1]
	v_pk_fma_f32 v[26:27], v[2:3], v[10:11], v[28:29] op_sel_hi:[0,1,1]
	ds_read_b128 v[8:11], v1 offset:48
	v_lshl_add_u32 v1, v47, 6, 0
	s_waitcnt lgkmcnt(1)
	s_nop 0
	v_pk_fma_f32 v[34:35], v[2:3], v[4:5], v[30:31] op_sel_hi:[0,1,1]
	v_pk_fma_f32 v[88:89], v[2:3], v[6:7], v[32:33] op_sel_hi:[0,1,1]
	v_add_u32_e32 v47, s42, v50
	s_waitcnt lgkmcnt(0)
	v_pk_fma_f32 v[20:21], v[2:3], v[8:9], v[20:21] op_sel_hi:[0,1,1]
	v_pk_fma_f32 v[10:11], v[2:3], v[10:11], v[12:13] op_sel_hi:[0,1,1]
	ds_read_b128 v[2:5], v1
	ds_read_b128 v[6:9], v1 offset:16
	v_lshl_add_u32 v13, v46, 6, 0
	s_waitcnt vmcnt(0) lgkmcnt(1)
	s_nop 0
	v_pk_fma_f32 v[92:93], v[0:1], v[2:3], v[14:15] op_sel_hi:[0,1,1]
	v_pk_fma_f32 v[94:95], v[0:1], v[4:5], v[16:17] op_sel_hi:[0,1,1]
	s_waitcnt lgkmcnt(0)
	s_nop 0
	v_pk_fma_f32 v[28:29], v[0:1], v[6:7], v[22:23] op_sel_hi:[0,1,1]
	v_pk_fma_f32 v[30:31], v[0:1], v[8:9], v[26:27] op_sel_hi:[0,1,1]
	ds_read_b128 v[2:5], v1 offset:32
	ds_read_b128 v[6:9], v1 offset:48
	global_load_dword v18, v[36:37], off
	global_load_dword v16, v[84:85], off
	global_load_dword v14, v[58:59], off
	global_load_dword v12, v[24:25], off
	v_add_u32_e64 v85, s7, v50
	v_add_u32_e32 v84, s38, v50
	s_waitcnt lgkmcnt(1)
	v_pk_fma_f32 v[32:33], v[0:1], v[2:3], v[34:35] op_sel_hi:[0,1,1]
	v_pk_fma_f32 v[34:35], v[0:1], v[4:5], v[88:89] op_sel_hi:[0,1,1]
	v_lshl_add_u64 v[4:5], s[44:45], 2, v[56:57]
	s_waitcnt lgkmcnt(0)
	s_nop 0
	v_pk_fma_f32 v[20:21], v[0:1], v[6:7], v[20:21] op_sel_hi:[0,1,1]
	v_pk_fma_f32 v[22:23], v[0:1], v[8:9], v[10:11] op_sel_hi:[0,1,1]
	ds_read_b128 v[24:27], v13
	ds_read_b128 v[0:3], v13 offset:16
	global_load_dword v10, v[86:87], off
	global_load_dword v8, v[90:91], off
	global_load_dword v6, v[96:97], off
	s_nop 0
	s_nop 0
	global_load_dword v4, v[4:5], off
	v_lshl_add_u32 v5, v41, 6, 0
	v_lshl_add_u64 v[88:89], s[30:31], 2, v[56:57]
	s_waitcnt vmcnt(7) lgkmcnt(0)
	s_nop 0
	v_pk_fma_f32 v[36:37], v[18:19], v[0:1], v[28:29] op_sel_hi:[0,1,1]
	v_pk_fma_f32 v[58:59], v[18:19], v[2:3], v[30:31] op_sel_hi:[0,1,1]
	ds_read_b128 v[0:3], v13 offset:32
	ds_read_b128 v[28:31], v13 offset:48
	v_pk_fma_f32 v[24:25], v[18:19], v[24:25], v[92:93] op_sel_hi:[0,1,1]
	v_pk_fma_f32 v[26:27], v[18:19], v[26:27], v[94:95] op_sel_hi:[0,1,1]
	s_waitcnt lgkmcnt(1)
	s_nop 0
	v_pk_fma_f32 v[32:33], v[18:19], v[0:1], v[32:33] op_sel_hi:[0,1,1]
	v_pk_fma_f32 v[34:35], v[18:19], v[2:3], v[34:35] op_sel_hi:[0,1,1]
	s_waitcnt lgkmcnt(0)
	s_nop 0
	v_pk_fma_f32 v[28:29], v[18:19], v[28:29], v[20:21] op_sel_hi:[0,1,1]
	v_pk_fma_f32 v[30:31], v[18:19], v[30:31], v[22:23] op_sel_hi:[0,1,1]
	ds_read_b128 v[0:3], v5
	ds_read_b128 v[20:23], v5 offset:16
	s_waitcnt vmcnt(6) lgkmcnt(1)
	s_nop 0
	v_pk_fma_f32 v[86:87], v[16:17], v[0:1], v[24:25] op_sel_hi:[0,1,1]
	v_pk_fma_f32 v[26:27], v[16:17], v[2:3], v[26:27] op_sel_hi:[0,1,1]
	s_waitcnt lgkmcnt(0)
	s_nop 0
	v_pk_fma_f32 v[36:37], v[16:17], v[20:21], v[36:37] op_sel_hi:[0,1,1]
	v_pk_fma_f32 v[58:59], v[16:17], v[22:23], v[58:59] op_sel_hi:[0,1,1]
	ds_read_b128 v[0:3], v5 offset:32
	ds_read_b128 v[20:23], v5 offset:48
	v_lshl_add_u32 v5, v40, 6, 0
	v_add_u32_e64 v24, s40, v50
	v_add_u32_e32 v25, s39, v50
	s_waitcnt lgkmcnt(1)
	v_pk_fma_f32 v[32:33], v[16:17], v[0:1], v[32:33] op_sel_hi:[0,1,1]
	v_pk_fma_f32 v[34:35], v[16:17], v[2:3], v[34:35] op_sel_hi:[0,1,1]
	s_waitcnt lgkmcnt(0)
	s_nop 0
	v_pk_fma_f32 v[28:29], v[16:17], v[20:21], v[28:29] op_sel_hi:[0,1,1]
	v_pk_fma_f32 v[16:17], v[16:17], v[22:23], v[30:31] op_sel_hi:[0,1,1]
	ds_read_b128 v[0:3], v5
	ds_read_b128 v[20:23], v5 offset:16
	v_lshl_add_u32 v25, v25, 6, 0
	s_waitcnt vmcnt(5) lgkmcnt(1)
	s_nop 0
	v_pk_fma_f32 v[30:31], v[14:15], v[0:1], v[86:87] op_sel_hi:[0,1,1]
	v_pk_fma_f32 v[26:27], v[14:15], v[2:3], v[26:27] op_sel_hi:[0,1,1]
	s_waitcnt lgkmcnt(0)
	s_nop 0
	v_pk_fma_f32 v[36:37], v[14:15], v[20:21], v[36:37] op_sel_hi:[0,1,1]
	v_pk_fma_f32 v[40:41], v[14:15], v[22:23], v[58:59] op_sel_hi:[0,1,1]
	ds_read_b128 v[0:3], v5 offset:32
	ds_read_b128 v[20:23], v5 offset:48
	v_lshl_add_u32 v5, v39, 6, 0
	v_lshl_add_u64 v[58:59], s[86:87], 2, v[56:57]
	v_add_u32_e32 v86, s6, v50
	s_waitcnt lgkmcnt(1)
	v_pk_fma_f32 v[32:33], v[14:15], v[0:1], v[32:33] op_sel_hi:[0,1,1]
	v_pk_fma_f32 v[34:35], v[14:15], v[2:3], v[34:35] op_sel_hi:[0,1,1]
	s_waitcnt lgkmcnt(0)
	s_nop 0
	v_pk_fma_f32 v[20:21], v[14:15], v[20:21], v[28:29] op_sel_hi:[0,1,1]
	v_pk_fma_f32 v[22:23], v[14:15], v[22:23], v[16:17] op_sel_hi:[0,1,1]
	ds_read_b128 v[0:3], v5
	ds_read_b128 v[14:17], v5 offset:16
	s_waitcnt vmcnt(4) lgkmcnt(1)
	s_nop 0
	v_pk_fma_f32 v[28:29], v[12:13], v[0:1], v[30:31] op_sel_hi:[0,1,1]
	v_pk_fma_f32 v[26:27], v[12:13], v[2:3], v[26:27] op_sel_hi:[0,1,1]
	s_waitcnt lgkmcnt(0)
	s_nop 0
	v_pk_fma_f32 v[36:37], v[12:13], v[14:15], v[36:37] op_sel_hi:[0,1,1]
	v_pk_fma_f32 v[40:41], v[12:13], v[16:17], v[40:41] op_sel_hi:[0,1,1]
	ds_read_b128 v[0:3], v5 offset:32
	ds_read_b128 v[14:17], v5 offset:48
	v_lshl_add_u32 v5, v38, 6, 0
	v_lshl_add_u64 v[30:31], s[90:91], 2, v[56:57]
	v_lshl_add_u64 v[38:39], s[78:79], 2, v[56:57]
	s_waitcnt lgkmcnt(1)
	s_nop 0
	v_pk_fma_f32 v[32:33], v[12:13], v[0:1], v[32:33] op_sel_hi:[0,1,1]
	v_pk_fma_f32 v[34:35], v[12:13], v[2:3], v[34:35] op_sel_hi:[0,1,1]
	s_waitcnt lgkmcnt(0)
	s_nop 0
	v_pk_fma_f32 v[20:21], v[12:13], v[14:15], v[20:21] op_sel_hi:[0,1,1]
	v_pk_fma_f32 v[16:17], v[12:13], v[16:17], v[22:23] op_sel_hi:[0,1,1]
	ds_read_b128 v[0:3], v5
	ds_read_b128 v[12:15], v5 offset:16
	s_waitcnt vmcnt(3) lgkmcnt(1)
	s_nop 0
	v_pk_fma_f32 v[22:23], v[10:11], v[0:1], v[28:29] op_sel_hi:[0,1,1]
	v_pk_fma_f32 v[26:27], v[10:11], v[2:3], v[26:27] op_sel_hi:[0,1,1]
	ds_read_b128 v[0:3], v5 offset:32
	s_waitcnt lgkmcnt(1)
	s_nop 0
	v_pk_fma_f32 v[28:29], v[10:11], v[12:13], v[36:37] op_sel_hi:[0,1,1]
	v_pk_fma_f32 v[36:37], v[10:11], v[14:15], v[40:41] op_sel_hi:[0,1,1]
	ds_read_b128 v[12:15], v5 offset:48
	v_lshl_add_u32 v5, v74, 6, 0
	s_waitcnt lgkmcnt(1)
	s_nop 0
	v_pk_fma_f32 v[32:33], v[10:11], v[0:1], v[32:33] op_sel_hi:[0,1,1]
	v_pk_fma_f32 v[34:35], v[10:11], v[2:3], v[34:35] op_sel_hi:[0,1,1]
	v_lshl_add_u64 v[40:41], s[80:81], 2, v[56:57]
	s_waitcnt lgkmcnt(0)
	s_nop 0
	v_pk_fma_f32 v[20:21], v[10:11], v[12:13], v[20:21] op_sel_hi:[0,1,1]
	v_pk_fma_f32 v[14:15], v[10:11], v[14:15], v[16:17] op_sel_hi:[0,1,1]
	ds_read_b128 v[0:3], v5
	ds_read_b128 v[10:13], v5 offset:16
	s_waitcnt vmcnt(2) lgkmcnt(1)
	s_nop 0
	v_pk_fma_f32 v[16:17], v[8:9], v[0:1], v[22:23] op_sel_hi:[0,1,1]
	v_pk_fma_f32 v[22:23], v[8:9], v[2:3], v[26:27] op_sel_hi:[0,1,1]
	s_waitcnt lgkmcnt(0)
	s_nop 0
	v_pk_fma_f32 v[28:29], v[8:9], v[10:11], v[28:29] op_sel_hi:[0,1,1]
	v_pk_fma_f32 v[36:37], v[8:9], v[12:13], v[36:37] op_sel_hi:[0,1,1]
	ds_read_b128 v[0:3], v5 offset:32
	ds_read_b128 v[10:13], v5 offset:48
	v_lshl_add_u32 v5, v73, 6, 0
	v_lshl_add_u64 v[26:27], s[70:71], 2, v[56:57]
	s_waitcnt lgkmcnt(1)
	s_nop 0
	v_pk_fma_f32 v[32:33], v[8:9], v[0:1], v[32:33] op_sel_hi:[0,1,1]
	v_pk_fma_f32 v[34:35], v[8:9], v[2:3], v[34:35] op_sel_hi:[0,1,1]
	s_waitcnt lgkmcnt(0)
	s_nop 0
	v_pk_fma_f32 v[20:21], v[8:9], v[10:11], v[20:21] op_sel_hi:[0,1,1]
	v_pk_fma_f32 v[12:13], v[8:9], v[12:13], v[14:15] op_sel_hi:[0,1,1]
	ds_read_b128 v[0:3], v5
	ds_read_b128 v[8:11], v5 offset:16
	s_waitcnt vmcnt(1) lgkmcnt(1)
	s_nop 0
	v_pk_fma_f32 v[14:15], v[6:7], v[0:1], v[16:17] op_sel_hi:[0,1,1]
	v_pk_fma_f32 v[16:17], v[6:7], v[2:3], v[22:23] op_sel_hi:[0,1,1]
	ds_read_b128 v[0:3], v5 offset:32
	s_waitcnt lgkmcnt(1)
	s_nop 0
	v_pk_fma_f32 v[22:23], v[6:7], v[8:9], v[28:29] op_sel_hi:[0,1,1]
	v_pk_fma_f32 v[28:29], v[6:7], v[10:11], v[36:37] op_sel_hi:[0,1,1]
	ds_read_b128 v[8:11], v5 offset:48
	v_lshl_add_u32 v5, v72, 6, 0
	s_waitcnt lgkmcnt(1)
	s_nop 0
	v_pk_fma_f32 v[32:33], v[6:7], v[0:1], v[32:33] op_sel_hi:[0,1,1]
	v_pk_fma_f32 v[34:35], v[6:7], v[2:3], v[34:35] op_sel_hi:[0,1,1]
	v_lshl_add_u64 v[36:37], s[72:73], 2, v[56:57]
	s_waitcnt lgkmcnt(0)
	s_nop 0
	v_pk_fma_f32 v[20:21], v[6:7], v[8:9], v[20:21] op_sel_hi:[0,1,1]
	v_pk_fma_f32 v[10:11], v[6:7], v[10:11], v[12:13] op_sel_hi:[0,1,1]
	ds_read_b128 v[0:3], v5
	ds_read_b128 v[6:9], v5 offset:16
	v_lshl_add_u64 v[12:13], s[66:67], 2, v[56:57]
	s_waitcnt vmcnt(0) lgkmcnt(1)
	s_nop 0
	v_pk_fma_f32 v[72:73], v[4:5], v[0:1], v[14:15] op_sel_hi:[0,1,1]
	v_pk_fma_f32 v[16:17], v[4:5], v[2:3], v[16:17] op_sel_hi:[0,1,1]
	s_waitcnt lgkmcnt(0)
	s_nop 0
	v_pk_fma_f32 v[22:23], v[4:5], v[6:7], v[22:23] op_sel_hi:[0,1,1]
	v_pk_fma_f32 v[28:29], v[4:5], v[8:9], v[28:29] op_sel_hi:[0,1,1]
	ds_read_b128 v[0:3], v5 offset:32
	ds_read_b128 v[6:9], v5 offset:48
	global_load_dword v18, v[30:31], off
	s_nop 0
	s_nop 0
	global_load_dword v30, v[58:59], off
	s_nop 0
	s_nop 0
	global_load_dword v38, v[38:39], off
	s_nop 0
	s_nop 0
	global_load_dword v46, v[26:27], off
	s_waitcnt lgkmcnt(1)
	s_nop 0
	v_pk_fma_f32 v[32:33], v[4:5], v[0:1], v[32:33] op_sel_hi:[0,1,1]
	v_pk_fma_f32 v[34:35], v[4:5], v[2:3], v[34:35] op_sel_hi:[0,1,1]
	v_lshl_add_u64 v[2:3], s[76:77], 2, v[56:57]
	v_lshl_add_u32 v1, v69, 6, 0
	s_waitcnt lgkmcnt(0)
	s_nop 0
	v_pk_fma_f32 v[20:21], v[4:5], v[6:7], v[20:21] op_sel_hi:[0,1,1]
	v_pk_fma_f32 v[26:27], v[4:5], v[8:9], v[10:11] op_sel_hi:[0,1,1]
	ds_read_b128 v[8:11], v1
	global_load_dword v0, v[40:41], off
	global_load_dword v4, v[36:37], off
	global_load_dword v6, v[12:13], off
	s_nop 0
	s_nop 0
	global_load_dword v2, v[2:3], off
	ds_read_b128 v[12:15], v1 offset:16
	v_lshl_add_u32 v3, v44, 6, 0
	s_waitcnt vmcnt(7) lgkmcnt(1)
	s_nop 0
	v_pk_fma_f32 v[36:37], v[18:19], v[8:9], v[72:73] op_sel_hi:[0,1,1]
	v_pk_fma_f32 v[40:41], v[18:19], v[10:11], v[16:17] op_sel_hi:[0,1,1]
	ds_read_b128 v[8:11], v1 offset:32
	s_waitcnt lgkmcnt(1)
	s_nop 0
	v_pk_fma_f32 v[22:23], v[18:19], v[12:13], v[22:23] op_sel_hi:[0,1,1]
	v_pk_fma_f32 v[28:29], v[18:19], v[14:15], v[28:29] op_sel_hi:[0,1,1]
	ds_read_b128 v[12:15], v1 offset:48
	v_lshl_add_u32 v1, v63, 6, 0
	s_waitcnt lgkmcnt(1)
	s_nop 0
	v_pk_fma_f32 v[34:35], v[18:19], v[10:11], v[34:35] op_sel_hi:[0,1,1]
	v_pk_fma_f32 v[32:33], v[18:19], v[8:9], v[32:33] op_sel_hi:[0,1,1]
	v_lshl_add_u64 v[8:9], s[60:61], 2, v[56:57]
	s_waitcnt lgkmcnt(0)
	s_nop 0
	v_pk_fma_f32 v[58:59], v[18:19], v[12:13], v[20:21] op_sel_hi:[0,1,1]
	v_pk_fma_f32 v[26:27], v[18:19], v[14:15], v[26:27] op_sel_hi:[0,1,1]
	ds_read_b128 v[10:13], v1
	ds_read_b128 v[14:17], v1 offset:16
	s_waitcnt vmcnt(6) lgkmcnt(1)
	s_nop 0
	v_pk_fma_f32 v[40:41], v[30:31], v[12:13], v[40:41] op_sel_hi:[0,1,1]
	s_waitcnt lgkmcnt(0)
	s_nop 0
	v_pk_fma_f32 v[72:73], v[30:31], v[14:15], v[22:23] op_sel_hi:[0,1,1]
	ds_read_b128 v[12:15], v1 offset:32
	ds_read_b128 v[20:23], v1 offset:48
	v_lshl_add_u32 v1, v62, 6, 0
	v_pk_fma_f32 v[36:37], v[30:31], v[10:11], v[36:37] op_sel_hi:[0,1,1]
	v_pk_fma_f32 v[16:17], v[30:31], v[16:17], v[28:29] op_sel_hi:[0,1,1]
	s_waitcnt lgkmcnt(1)
	s_nop 0
	v_pk_fma_f32 v[12:13], v[30:31], v[12:13], v[32:33] op_sel_hi:[0,1,1]
	v_pk_fma_f32 v[32:33], v[30:31], v[14:15], v[34:35] op_sel_hi:[0,1,1]
	s_waitcnt lgkmcnt(0)
	s_nop 0
	v_pk_fma_f32 v[34:35], v[30:31], v[20:21], v[58:59] op_sel_hi:[0,1,1]
	v_pk_fma_f32 v[30:31], v[30:31], v[22:23], v[26:27] op_sel_hi:[0,1,1]
	ds_read_b128 v[20:23], v1
	ds_read_b128 v[26:29], v1 offset:16
	v_lshl_add_u64 v[10:11], s[58:59], 2, v[56:57]
	v_lshl_add_u64 v[14:15], s[62:63], 2, v[56:57]
	s_waitcnt vmcnt(5) lgkmcnt(1)
	s_nop 0
	v_pk_fma_f32 v[36:37], v[38:39], v[20:21], v[36:37] op_sel_hi:[0,1,1]
	v_pk_fma_f32 v[40:41], v[38:39], v[22:23], v[40:41] op_sel_hi:[0,1,1]
	ds_read_b128 v[20:23], v1 offset:32
	s_waitcnt lgkmcnt(1)
	s_nop 0
	v_pk_fma_f32 v[58:59], v[38:39], v[26:27], v[72:73] op_sel_hi:[0,1,1]
	v_pk_fma_f32 v[62:63], v[38:39], v[28:29], v[16:17] op_sel_hi:[0,1,1]
	ds_read_b128 v[26:29], v1 offset:48
	v_lshl_add_u32 v1, v61, 6, 0
	s_waitcnt lgkmcnt(1)
	s_nop 0
	v_pk_fma_f32 v[12:13], v[38:39], v[20:21], v[12:13] op_sel_hi:[0,1,1]
	v_pk_fma_f32 v[32:33], v[38:39], v[22:23], v[32:33] op_sel_hi:[0,1,1]
	v_lshl_add_u64 v[16:17], s[56:57], 2, v[56:57]
	s_waitcnt lgkmcnt(0)
	s_nop 0
	v_pk_fma_f32 v[34:35], v[38:39], v[26:27], v[34:35] op_sel_hi:[0,1,1]
	v_pk_fma_f32 v[30:31], v[38:39], v[28:29], v[30:31] op_sel_hi:[0,1,1]
	ds_read_b128 v[20:23], v1
	ds_read_b128 v[26:29], v1 offset:16
	v_lshl_add_u64 v[72:73], s[34:35], 2, v[56:57]
	s_waitcnt vmcnt(4) lgkmcnt(1)
	s_nop 0
	v_pk_fma_f32 v[36:37], v[46:47], v[20:21], v[36:37] op_sel_hi:[0,1,1]
	v_pk_fma_f32 v[38:39], v[46:47], v[22:23], v[40:41] op_sel_hi:[0,1,1]
	s_waitcnt lgkmcnt(0)
	s_nop 0
	v_pk_fma_f32 v[58:59], v[46:47], v[26:27], v[58:59] op_sel_hi:[0,1,1]
	v_pk_fma_f32 v[60:61], v[46:47], v[28:29], v[62:63] op_sel_hi:[0,1,1]
	ds_read_b128 v[20:23], v1 offset:32
	ds_read_b128 v[26:29], v1 offset:48
	v_lshl_add_u32 v1, v55, 6, 0
	v_lshl_add_u64 v[40:41], s[54:55], 2, v[56:57]
	v_lshl_add_u64 v[62:63], s[52:53], 2, v[56:57]
	s_waitcnt lgkmcnt(1)
	s_nop 0
	v_pk_fma_f32 v[12:13], v[46:47], v[20:21], v[12:13] op_sel_hi:[0,1,1]
	v_pk_fma_f32 v[32:33], v[46:47], v[22:23], v[32:33] op_sel_hi:[0,1,1]
	s_waitcnt lgkmcnt(0)
	s_nop 0
	v_pk_fma_f32 v[34:35], v[46:47], v[26:27], v[34:35] op_sel_hi:[0,1,1]
	v_pk_fma_f32 v[30:31], v[46:47], v[28:29], v[30:31] op_sel_hi:[0,1,1]
	ds_read_b128 v[20:23], v1
	ds_read_b128 v[26:29], v1 offset:16
	v_lshl_add_u32 v55, v86, 6, 0
	s_waitcnt vmcnt(3) lgkmcnt(1)
	s_nop 0
	v_pk_fma_f32 v[36:37], v[0:1], v[20:21], v[36:37] op_sel_hi:[0,1,1]
	v_pk_fma_f32 v[38:39], v[0:1], v[22:23], v[38:39] op_sel_hi:[0,1,1]
	ds_read_b128 v[20:23], v1 offset:32
	s_waitcnt lgkmcnt(1)
	s_nop 0
	v_pk_fma_f32 v[58:59], v[0:1], v[26:27], v[58:59] op_sel_hi:[0,1,1]
	v_pk_fma_f32 v[60:61], v[0:1], v[28:29], v[60:61] op_sel_hi:[0,1,1]
	ds_read_b128 v[26:29], v1 offset:48
	s_waitcnt lgkmcnt(1)
	s_nop 0
	v_pk_fma_f32 v[12:13], v[0:1], v[20:21], v[12:13] op_sel_hi:[0,1,1]
	v_pk_fma_f32 v[32:33], v[0:1], v[22:23], v[32:33] op_sel_hi:[0,1,1]
	v_lshl_add_u32 v1, v45, 6, 0
	s_waitcnt lgkmcnt(0)
	s_nop 0
	v_pk_fma_f32 v[34:35], v[0:1], v[26:27], v[34:35] op_sel_hi:[0,1,1]
	v_pk_fma_f32 v[30:31], v[0:1], v[28:29], v[30:31] op_sel_hi:[0,1,1]
	ds_read_b128 v[20:23], v1
	ds_read_b128 v[26:29], v1 offset:16
	s_waitcnt vmcnt(2) lgkmcnt(1)
	s_nop 0
	v_pk_fma_f32 v[36:37], v[4:5], v[20:21], v[36:37] op_sel_hi:[0,1,1]
	v_pk_fma_f32 v[38:39], v[4:5], v[22:23], v[38:39] op_sel_hi:[0,1,1]
	s_waitcnt lgkmcnt(0)
	s_nop 0
	v_pk_fma_f32 v[58:59], v[4:5], v[26:27], v[58:59] op_sel_hi:[0,1,1]
	v_pk_fma_f32 v[60:61], v[4:5], v[28:29], v[60:61] op_sel_hi:[0,1,1]
	ds_read_b128 v[20:23], v1 offset:32
	ds_read_b128 v[26:29], v1 offset:48
	v_lshl_add_u64 v[0:1], s[28:29], 2, v[56:57]
	s_waitcnt lgkmcnt(1)
	s_nop 0
	v_pk_fma_f32 v[12:13], v[4:5], v[20:21], v[12:13] op_sel_hi:[0,1,1]
	v_pk_fma_f32 v[32:33], v[4:5], v[22:23], v[32:33] op_sel_hi:[0,1,1]
	s_waitcnt lgkmcnt(0)
	s_nop 0
	v_pk_fma_f32 v[34:35], v[4:5], v[26:27], v[34:35] op_sel_hi:[0,1,1]
	v_pk_fma_f32 v[30:31], v[4:5], v[28:29], v[30:31] op_sel_hi:[0,1,1]
	ds_read_b128 v[20:23], v3
	ds_read_b128 v[26:29], v3 offset:16
	v_lshl_add_u64 v[4:5], s[94:95], 2, v[56:57]
	s_waitcnt vmcnt(1) lgkmcnt(1)
	s_nop 0
	v_pk_fma_f32 v[36:37], v[6:7], v[20:21], v[36:37] op_sel_hi:[0,1,1]
	v_pk_fma_f32 v[38:39], v[6:7], v[22:23], v[38:39] op_sel_hi:[0,1,1]
	ds_read_b128 v[20:23], v3 offset:32
	s_waitcnt lgkmcnt(1)
	s_nop 0
	v_pk_fma_f32 v[44:45], v[6:7], v[26:27], v[58:59] op_sel_hi:[0,1,1]
	v_pk_fma_f32 v[58:59], v[6:7], v[28:29], v[60:61] op_sel_hi:[0,1,1]
	ds_read_b128 v[26:29], v3 offset:48
	v_lshl_add_u32 v3, v75, 6, 0
	s_waitcnt lgkmcnt(1)
	s_nop 0
	v_pk_fma_f32 v[60:61], v[6:7], v[20:21], v[12:13] op_sel_hi:[0,1,1]
	v_pk_fma_f32 v[32:33], v[6:7], v[22:23], v[32:33] op_sel_hi:[0,1,1]
	v_lshl_add_u64 v[12:13], vcc, 2, v[56:57]
	s_waitcnt lgkmcnt(0)
	s_nop 0
	v_pk_fma_f32 v[34:35], v[6:7], v[26:27], v[34:35] op_sel_hi:[0,1,1]
	v_pk_fma_f32 v[6:7], v[6:7], v[28:29], v[30:31] op_sel_hi:[0,1,1]
	ds_read_b128 v[20:23], v3
	ds_read_b128 v[26:29], v3 offset:16
	s_waitcnt vmcnt(0) lgkmcnt(1)
	s_nop 0
	v_pk_fma_f32 v[30:31], v[2:3], v[20:21], v[36:37] op_sel_hi:[0,1,1]
	v_pk_fma_f32 v[36:37], v[2:3], v[22:23], v[38:39] op_sel_hi:[0,1,1]
	s_waitcnt lgkmcnt(0)
	s_nop 0
	v_pk_fma_f32 v[38:39], v[2:3], v[26:27], v[44:45] op_sel_hi:[0,1,1]
	v_pk_fma_f32 v[58:59], v[2:3], v[28:29], v[58:59] op_sel_hi:[0,1,1]
	ds_read_b128 v[20:23], v3 offset:32
	ds_read_b128 v[26:29], v3 offset:48
	global_load_dword v52, v[8:9], off
	s_nop 0
	s_nop 0
	global_load_dword v10, v[10:11], off
	s_nop 0
	s_nop 0
	global_load_dword v14, v[14:15], off
	s_nop 0
	s_nop 0
	global_load_dword v74, v[16:17], off
	v_lshl_add_u32 v11, v71, 6, 0
	v_lshl_add_u32 v17, v68, 6, 0
	s_waitcnt lgkmcnt(1)
	s_nop 0
	v_pk_fma_f32 v[32:33], v[2:3], v[22:23], v[32:33] op_sel_hi:[0,1,1]
	v_lshl_add_u32 v23, v76, 6, 0
	v_pk_fma_f32 v[20:21], v[2:3], v[20:21], v[60:61] op_sel_hi:[0,1,1]
	s_waitcnt lgkmcnt(0)
	s_nop 0
	v_pk_fma_f32 v[34:35], v[2:3], v[26:27], v[34:35] op_sel_hi:[0,1,1]
	v_pk_fma_f32 v[2:3], v[2:3], v[28:29], v[6:7] op_sel_hi:[0,1,1]
	ds_read_b128 v[6:9], v23
	global_load_dword v16, v[40:41], off
	global_load_dword v22, v[62:63], off
	global_load_dword v18, v[72:73], off
	global_load_dword v46, v[88:89], off
	ds_read_b128 v[26:29], v23 offset:16
	v_lshl_add_u64 v[44:45], s[2:3], 2, v[56:57]
	v_lshl_add_u64 v[60:61], s[22:23], 2, v[56:57]
	s_waitcnt vmcnt(7) lgkmcnt(1)
	s_nop 0
	v_pk_fma_f32 v[30:31], v[52:53], v[6:7], v[30:31] op_sel_hi:[0,1,1]
	v_pk_fma_f32 v[36:37], v[52:53], v[8:9], v[36:37] op_sel_hi:[0,1,1]
	ds_read_b128 v[6:9], v23 offset:32
	s_waitcnt lgkmcnt(1)
	s_nop 0
	v_pk_fma_f32 v[38:39], v[52:53], v[26:27], v[38:39] op_sel_hi:[0,1,1]
	v_pk_fma_f32 v[40:41], v[52:53], v[28:29], v[58:59] op_sel_hi:[0,1,1]
	ds_read_b128 v[26:29], v23 offset:48
	v_lshl_add_u32 v23, v65, 6, 0
	s_waitcnt lgkmcnt(1)
	s_nop 0
	v_pk_fma_f32 v[20:21], v[52:53], v[6:7], v[20:21] op_sel_hi:[0,1,1]
	v_pk_fma_f32 v[32:33], v[52:53], v[8:9], v[32:33] op_sel_hi:[0,1,1]
	v_lshl_add_u64 v[58:59], s[4:5], 2, v[56:57]
	s_waitcnt lgkmcnt(0)
	s_nop 0
	v_pk_fma_f32 v[34:35], v[52:53], v[26:27], v[34:35] op_sel_hi:[0,1,1]
	v_pk_fma_f32 v[62:63], v[52:53], v[28:29], v[2:3] op_sel_hi:[0,1,1]
	ds_read_b128 v[6:9], v11
	ds_read_b128 v[26:29], v11 offset:16
	v_lshl_add_u32 v52, v77, 6, 0
	v_lshl_add_u64 v[2:3], s[96:97], 2, v[56:57]
	s_waitcnt vmcnt(6) lgkmcnt(1)
	s_nop 0
	v_pk_fma_f32 v[30:31], v[10:11], v[6:7], v[30:31] op_sel_hi:[0,1,1]
	v_pk_fma_f32 v[36:37], v[10:11], v[8:9], v[36:37] op_sel_hi:[0,1,1]
	s_waitcnt lgkmcnt(0)
	s_nop 0
	v_pk_fma_f32 v[38:39], v[10:11], v[26:27], v[38:39] op_sel_hi:[0,1,1]
	v_pk_fma_f32 v[40:41], v[10:11], v[28:29], v[40:41] op_sel_hi:[0,1,1]
	ds_read_b128 v[6:9], v11 offset:32
	ds_read_b128 v[26:29], v11 offset:48
	s_waitcnt lgkmcnt(1)
	s_nop 0
	v_pk_fma_f32 v[20:21], v[10:11], v[6:7], v[20:21] op_sel_hi:[0,1,1]
	v_pk_fma_f32 v[32:33], v[10:11], v[8:9], v[32:33] op_sel_hi:[0,1,1]
	v_lshl_add_u32 v11, v70, 6, 0
	s_waitcnt lgkmcnt(0)
	s_nop 0
	v_pk_fma_f32 v[34:35], v[10:11], v[26:27], v[34:35] op_sel_hi:[0,1,1]
	v_pk_fma_f32 v[62:63], v[10:11], v[28:29], v[62:63] op_sel_hi:[0,1,1]
	ds_read_b128 v[6:9], v11
	ds_read_b128 v[26:29], v11 offset:16
	s_waitcnt vmcnt(5) lgkmcnt(1)
	s_nop 0
	v_pk_fma_f32 v[30:31], v[14:15], v[6:7], v[30:31] op_sel_hi:[0,1,1]
	v_pk_fma_f32 v[36:37], v[14:15], v[8:9], v[36:37] op_sel_hi:[0,1,1]
	ds_read_b128 v[6:9], v11 offset:32
	s_waitcnt lgkmcnt(1)
	s_nop 0
	v_pk_fma_f32 v[38:39], v[14:15], v[26:27], v[38:39] op_sel_hi:[0,1,1]
	v_pk_fma_f32 v[40:41], v[14:15], v[28:29], v[40:41] op_sel_hi:[0,1,1]
	ds_read_b128 v[26:29], v11 offset:48
	v_lshl_add_u64 v[10:11], s[88:89], 2, v[56:57]
	s_waitcnt lgkmcnt(1)
	s_nop 0
	v_pk_fma_f32 v[20:21], v[14:15], v[6:7], v[20:21] op_sel_hi:[0,1,1]
	v_pk_fma_f32 v[70:71], v[14:15], v[8:9], v[32:33] op_sel_hi:[0,1,1]
	s_waitcnt lgkmcnt(0)
	s_nop 0
	v_pk_fma_f32 v[34:35], v[14:15], v[26:27], v[34:35] op_sel_hi:[0,1,1]
	v_pk_fma_f32 v[14:15], v[14:15], v[28:29], v[62:63] op_sel_hi:[0,1,1]
	ds_read_b128 v[6:9], v17
	ds_read_b128 v[26:29], v17 offset:16
	s_waitcnt vmcnt(4) lgkmcnt(1)
	s_nop 0
	v_pk_fma_f32 v[62:63], v[74:75], v[6:7], v[30:31] op_sel_hi:[0,1,1]
	s_waitcnt lgkmcnt(0)
	s_nop 0
	v_pk_fma_f32 v[38:39], v[74:75], v[26:27], v[38:39] op_sel_hi:[0,1,1]
	v_pk_fma_f32 v[40:41], v[74:75], v[28:29], v[40:41] op_sel_hi:[0,1,1]
	ds_read_b128 v[26:29], v17 offset:32
	ds_read_b128 v[30:33], v17 offset:48
	v_lshl_add_u32 v17, v67, 6, 0
	v_pk_fma_f32 v[36:37], v[74:75], v[8:9], v[36:37] op_sel_hi:[0,1,1]
	v_lshl_add_u32 v67, v42, 6, 0
	s_waitcnt lgkmcnt(1)
	s_nop 0
	v_pk_fma_f32 v[20:21], v[74:75], v[26:27], v[20:21] op_sel_hi:[0,1,1]
	v_pk_fma_f32 v[68:69], v[74:75], v[28:29], v[70:71] op_sel_hi:[0,1,1]
	s_waitcnt lgkmcnt(0)
	s_nop 0
	v_pk_fma_f32 v[34:35], v[74:75], v[30:31], v[34:35] op_sel_hi:[0,1,1]
	v_pk_fma_f32 v[70:71], v[74:75], v[32:33], v[14:15] op_sel_hi:[0,1,1]
	ds_read_b128 v[26:29], v17
	ds_read_b128 v[30:33], v17 offset:16
	v_lshl_add_u64 v[6:7], s[84:85], 2, v[56:57]
	v_lshl_add_u32 v74, v66, 6, 0
	v_lshl_add_u64 v[8:9], s[82:83], 2, v[56:57]
	s_waitcnt vmcnt(3) lgkmcnt(1)
	s_nop 0
	v_pk_fma_f32 v[62:63], v[16:17], v[26:27], v[62:63] op_sel_hi:[0,1,1]
	v_pk_fma_f32 v[36:37], v[16:17], v[28:29], v[36:37] op_sel_hi:[0,1,1]
	ds_read_b128 v[26:29], v17 offset:32
	s_waitcnt lgkmcnt(1)
	s_nop 0
	v_pk_fma_f32 v[38:39], v[16:17], v[30:31], v[38:39] op_sel_hi:[0,1,1]
	v_pk_fma_f32 v[40:41], v[16:17], v[32:33], v[40:41] op_sel_hi:[0,1,1]
	ds_read_b128 v[30:33], v17 offset:48
	v_lshl_add_u64 v[14:15], s[74:75], 2, v[56:57]
	s_waitcnt lgkmcnt(1)
	s_nop 0
	v_pk_fma_f32 v[20:21], v[16:17], v[26:27], v[20:21] op_sel_hi:[0,1,1]
	v_pk_fma_f32 v[68:69], v[16:17], v[28:29], v[68:69] op_sel_hi:[0,1,1]
	v_lshl_add_u32 v66, v47, 6, 0
	s_waitcnt lgkmcnt(0)
	s_nop 0
	v_pk_fma_f32 v[34:35], v[16:17], v[30:31], v[34:35] op_sel_hi:[0,1,1]
	v_pk_fma_f32 v[70:71], v[16:17], v[32:33], v[70:71] op_sel_hi:[0,1,1]
	ds_read_b128 v[26:29], v23
	ds_read_b128 v[30:33], v23 offset:16
	v_lshl_add_u64 v[16:17], s[68:69], 2, v[56:57]
	s_waitcnt vmcnt(2) lgkmcnt(1)
	s_nop 0
	v_pk_fma_f32 v[62:63], v[22:23], v[26:27], v[62:63] op_sel_hi:[0,1,1]
	v_pk_fma_f32 v[36:37], v[22:23], v[28:29], v[36:37] op_sel_hi:[0,1,1]
	s_waitcnt lgkmcnt(0)
	s_nop 0
	v_pk_fma_f32 v[38:39], v[22:23], v[30:31], v[38:39] op_sel_hi:[0,1,1]
	v_pk_fma_f32 v[40:41], v[22:23], v[32:33], v[40:41] op_sel_hi:[0,1,1]
	ds_read_b128 v[26:29], v23 offset:32
	ds_read_b128 v[30:33], v23 offset:48
	s_waitcnt lgkmcnt(1)
	s_nop 0
	v_pk_fma_f32 v[72:73], v[22:23], v[26:27], v[20:21] op_sel_hi:[0,1,1]
	v_pk_fma_f32 v[68:69], v[22:23], v[28:29], v[68:69] op_sel_hi:[0,1,1]
	v_lshl_add_u32 v23, v64, 6, 0
	s_waitcnt lgkmcnt(0)
	s_nop 0
	v_pk_fma_f32 v[34:35], v[22:23], v[30:31], v[34:35] op_sel_hi:[0,1,1]
	v_pk_fma_f32 v[64:65], v[22:23], v[32:33], v[70:71] op_sel_hi:[0,1,1]
	ds_read_b128 v[26:29], v23
	ds_read_b128 v[30:33], v23 offset:16
	v_lshl_add_u64 v[20:21], s[64:65], 2, v[56:57]
	s_waitcnt vmcnt(1) lgkmcnt(1)
	s_nop 0
	v_pk_fma_f32 v[62:63], v[18:19], v[26:27], v[62:63] op_sel_hi:[0,1,1]
	v_pk_fma_f32 v[36:37], v[18:19], v[28:29], v[36:37] op_sel_hi:[0,1,1]
	ds_read_b128 v[26:29], v23 offset:32
	s_waitcnt lgkmcnt(1)
	s_nop 0
	v_pk_fma_f32 v[38:39], v[18:19], v[30:31], v[38:39] op_sel_hi:[0,1,1]
	v_pk_fma_f32 v[40:41], v[18:19], v[32:33], v[40:41] op_sel_hi:[0,1,1]
	ds_read_b128 v[30:33], v23 offset:48
	v_lshl_add_u64 v[22:23], s[0:1], 2, v[56:57]
	s_waitcnt lgkmcnt(1)
	s_nop 0
	v_pk_fma_f32 v[70:71], v[18:19], v[26:27], v[72:73] op_sel_hi:[0,1,1]
	v_pk_fma_f32 v[68:69], v[18:19], v[28:29], v[68:69] op_sel_hi:[0,1,1]
	v_lshl_add_u32 v73, v78, 6, 0
	s_waitcnt lgkmcnt(0)
	s_nop 0
	v_pk_fma_f32 v[76:77], v[18:19], v[30:31], v[34:35] op_sel_hi:[0,1,1]
	v_pk_fma_f32 v[92:93], v[18:19], v[32:33], v[64:65] op_sel_hi:[0,1,1]
	ds_read_b128 v[26:29], v52
	ds_read_b128 v[30:33], v52 offset:16
	v_lshl_add_u32 v72, v79, 6, 0
	v_lshl_add_u32 v65, v83, 6, 0
	s_waitcnt vmcnt(0) lgkmcnt(1)
	s_nop 0
	v_pk_fma_f32 v[34:35], v[46:47], v[26:27], v[62:63] op_sel_hi:[0,1,1]
	s_waitcnt lgkmcnt(0)
	s_nop 0
	v_pk_fma_f32 v[38:39], v[46:47], v[30:31], v[38:39] op_sel_hi:[0,1,1]
	v_pk_fma_f32 v[40:41], v[46:47], v[32:33], v[40:41] op_sel_hi:[0,1,1]
	ds_read_b128 v[30:33], v52 offset:32
	ds_read_b128 v[88:91], v52 offset:48
	v_lshl_add_u32 v63, v24, 6, 0
	global_load_dword v42, v[0:1], off
	global_load_dword v24, v[4:5], off
	global_load_dword v18, v[12:13], off
	s_nop 0
	s_nop 0
	global_load_dword v12, v[44:45], off
	global_load_dword v4, v[58:59], off
	global_load_dword v0, v[60:61], off
	v_lshl_add_u32 v52, v19, 6, 0
	ds_read_b128 v[58:61], v52
	global_load_dword v64, v[2:3], off
	global_load_dword v62, v[10:11], off
	v_pk_fma_f32 v[36:37], v[46:47], v[28:29], v[36:37] op_sel_hi:[0,1,1]
	s_waitcnt lgkmcnt(2)
	s_nop 0
	v_pk_fma_f32 v[32:33], v[46:47], v[32:33], v[68:69] op_sel_hi:[0,1,1]
	v_lshl_add_u32 v69, v43, 6, 0
	v_lshl_add_u32 v43, v85, 6, 0
	v_pk_fma_f32 v[30:31], v[46:47], v[30:31], v[70:71] op_sel_hi:[0,1,1]
	v_lshl_add_u32 v71, v80, 6, 0
	v_lshl_add_u32 v70, v81, 6, 0
	v_lshl_add_u32 v68, v82, 6, 0
	s_waitcnt lgkmcnt(1)
	s_nop 0
	v_pk_fma_f32 v[44:45], v[46:47], v[88:89], v[76:77] op_sel_hi:[0,1,1]
	ds_read_b128 v[76:79], v52 offset:16
	v_lshl_add_u64 v[26:27], s[12:13], 2, v[56:57]
	v_lshl_add_u64 v[28:29], s[36:37], 2, v[56:57]
	v_lshl_add_u32 v19, v84, 6, 0
	v_pk_fma_f32 v[46:47], v[46:47], v[90:91], v[92:93] op_sel_hi:[0,1,1]
	s_waitcnt vmcnt(7) lgkmcnt(1)
	s_nop 0
	v_pk_fma_f32 v[80:81], v[42:43], v[58:59], v[34:35] op_sel_hi:[0,1,1]
	v_pk_fma_f32 v[82:83], v[42:43], v[60:61], v[36:37] op_sel_hi:[0,1,1]
	ds_read_b128 v[34:37], v52 offset:32
	s_waitcnt lgkmcnt(1)
	s_nop 0
	v_pk_fma_f32 v[38:39], v[42:43], v[76:77], v[38:39] op_sel_hi:[0,1,1]
	v_pk_fma_f32 v[84:85], v[42:43], v[78:79], v[40:41] op_sel_hi:[0,1,1]
	ds_read_b128 v[76:79], v52 offset:48
	s_waitcnt lgkmcnt(1)
	s_nop 0
	v_pk_fma_f32 v[86:87], v[42:43], v[34:35], v[30:31] op_sel_hi:[0,1,1]
	v_pk_fma_f32 v[36:37], v[42:43], v[36:37], v[32:33] op_sel_hi:[0,1,1]
	ds_read_b128 v[32:35], v74
	global_load_dword v10, v[6:7], off
	global_load_dword v2, v[8:9], off
	s_nop 0
	s_nop 0
	global_load_dword v6, v[14:15], off
	global_load_dword v30, v[16:17], off
	global_load_dword v40, v[20:21], off
	global_load_dword v60, v[22:23], off
	global_load_dword v58, v[26:27], off
	global_load_dword v52, v[28:29], off
	ds_read_b128 v[14:17], v74 offset:16
	ds_read_b128 v[20:23], v74 offset:32
	ds_read_b128 v[26:29], v74 offset:48
	s_waitcnt lgkmcnt(4)
	s_nop 0
	v_pk_fma_f32 v[8:9], v[42:43], v[76:77], v[44:45] op_sel_hi:[0,1,1]
	v_pk_fma_f32 v[44:45], v[42:43], v[78:79], v[46:47] op_sel_hi:[0,1,1]
	s_waitcnt vmcnt(14) lgkmcnt(3)
	s_nop 0
	v_pk_fma_f32 v[32:33], v[24:25], v[32:33], v[80:81] op_sel_hi:[0,1,1]
	s_waitcnt lgkmcnt(2)
	s_nop 0
	v_pk_fma_f32 v[38:39], v[24:25], v[14:15], v[38:39] op_sel_hi:[0,1,1]
	v_pk_fma_f32 v[46:47], v[24:25], v[16:17], v[84:85] op_sel_hi:[0,1,1]
	ds_read_b128 v[14:17], v73
	s_waitcnt lgkmcnt(2)
	s_nop 0
	v_pk_fma_f32 v[74:75], v[24:25], v[20:21], v[86:87] op_sel_hi:[0,1,1]
	v_pk_fma_f32 v[36:37], v[24:25], v[22:23], v[36:37] op_sel_hi:[0,1,1]
	ds_read_b128 v[20:23], v73 offset:16
	s_waitcnt lgkmcnt(2)
	s_nop 0
	v_pk_fma_f32 v[8:9], v[24:25], v[26:27], v[8:9] op_sel_hi:[0,1,1]
	v_pk_fma_f32 v[44:45], v[24:25], v[28:29], v[44:45] op_sel_hi:[0,1,1]
	ds_read_b128 v[26:29], v73 offset:32
	v_pk_fma_f32 v[34:35], v[24:25], v[34:35], v[82:83] op_sel_hi:[0,1,1]
	s_waitcnt vmcnt(13) lgkmcnt(2)
	s_nop 0
	v_pk_fma_f32 v[76:77], v[18:19], v[14:15], v[32:33] op_sel_hi:[0,1,1]
	v_pk_fma_f32 v[78:79], v[18:19], v[16:17], v[34:35] op_sel_hi:[0,1,1]
	ds_read_b128 v[14:17], v73 offset:48
	s_waitcnt lgkmcnt(2)
	s_nop 0
	v_pk_fma_f32 v[38:39], v[18:19], v[20:21], v[38:39] op_sel_hi:[0,1,1]
	v_pk_fma_f32 v[46:47], v[18:19], v[22:23], v[46:47] op_sel_hi:[0,1,1]
	ds_read_b128 v[20:23], v72
	s_waitcnt lgkmcnt(2)
	s_nop 0
	v_pk_fma_f32 v[74:75], v[18:19], v[26:27], v[74:75] op_sel_hi:[0,1,1]
	v_pk_fma_f32 v[36:37], v[18:19], v[28:29], v[36:37] op_sel_hi:[0,1,1]
	ds_read_b128 v[26:29], v72 offset:16
	s_waitcnt lgkmcnt(2)
	s_nop 0
	v_pk_fma_f32 v[8:9], v[18:19], v[14:15], v[8:9] op_sel_hi:[0,1,1]
	v_pk_fma_f32 v[44:45], v[18:19], v[16:17], v[44:45] op_sel_hi:[0,1,1]
	ds_read_b128 v[14:17], v72 offset:32
	ds_read_b128 v[32:35], v72 offset:48
	s_waitcnt vmcnt(12) lgkmcnt(3)
	s_nop 0
	v_pk_fma_f32 v[72:73], v[12:13], v[20:21], v[76:77] op_sel_hi:[0,1,1]
	v_pk_fma_f32 v[76:77], v[12:13], v[22:23], v[78:79] op_sel_hi:[0,1,1]
	ds_read_b128 v[20:23], v71
	s_waitcnt lgkmcnt(3)
	s_nop 0
	v_pk_fma_f32 v[78:79], v[12:13], v[26:27], v[38:39] op_sel_hi:[0,1,1]
	v_pk_fma_f32 v[46:47], v[12:13], v[28:29], v[46:47] op_sel_hi:[0,1,1]
	ds_read_b128 v[26:29], v71 offset:16
	s_waitcnt lgkmcnt(3)
	s_nop 0
	v_pk_fma_f32 v[74:75], v[12:13], v[14:15], v[74:75] op_sel_hi:[0,1,1]
	v_pk_fma_f32 v[80:81], v[12:13], v[16:17], v[36:37] op_sel_hi:[0,1,1]
	ds_read_b128 v[14:17], v71 offset:32
	s_waitcnt lgkmcnt(3)
	s_nop 0
	v_pk_fma_f32 v[8:9], v[12:13], v[32:33], v[8:9] op_sel_hi:[0,1,1]
	v_pk_fma_f32 v[44:45], v[12:13], v[34:35], v[44:45] op_sel_hi:[0,1,1]
	ds_read_b128 v[32:35], v71 offset:48
	ds_read_b128 v[36:39], v70
	s_waitcnt vmcnt(11) lgkmcnt(4)
	s_nop 0
	v_pk_fma_f32 v[72:73], v[4:5], v[20:21], v[72:73] op_sel_hi:[0,1,1]
	v_pk_fma_f32 v[76:77], v[4:5], v[22:23], v[76:77] op_sel_hi:[0,1,1]
	ds_read_b128 v[20:23], v70 offset:16
	s_waitcnt lgkmcnt(4)
	s_nop 0
	v_pk_fma_f32 v[78:79], v[4:5], v[26:27], v[78:79] op_sel_hi:[0,1,1]
	v_pk_fma_f32 v[82:83], v[4:5], v[28:29], v[46:47] op_sel_hi:[0,1,1]
	ds_read_b128 v[26:29], v70 offset:32
	s_waitcnt lgkmcnt(4)
	s_nop 0
	v_pk_fma_f32 v[74:75], v[4:5], v[14:15], v[74:75] op_sel_hi:[0,1,1]
	ds_read_b128 v[12:15], v70 offset:48
	v_pk_fma_f32 v[16:17], v[4:5], v[16:17], v[80:81] op_sel_hi:[0,1,1]
	s_waitcnt lgkmcnt(4)
	s_nop 0
	v_pk_fma_f32 v[8:9], v[4:5], v[32:33], v[8:9] op_sel_hi:[0,1,1]
	v_pk_fma_f32 v[4:5], v[4:5], v[34:35], v[44:45] op_sel_hi:[0,1,1]
	ds_read_b128 v[32:35], v69
	ds_read_b128 v[44:47], v69 offset:16
	s_waitcnt vmcnt(10) lgkmcnt(5)
	s_nop 0
	v_pk_fma_f32 v[70:71], v[0:1], v[36:37], v[72:73] op_sel_hi:[0,1,1]
	v_pk_fma_f32 v[72:73], v[0:1], v[38:39], v[76:77] op_sel_hi:[0,1,1]
	ds_read_b128 v[36:39], v69 offset:32
	s_waitcnt lgkmcnt(5)
	s_nop 0
	v_pk_fma_f32 v[76:77], v[0:1], v[20:21], v[78:79] op_sel_hi:[0,1,1]
	v_pk_fma_f32 v[78:79], v[0:1], v[22:23], v[82:83] op_sel_hi:[0,1,1]
	ds_read_b128 v[20:23], v69 offset:48
	s_waitcnt lgkmcnt(5)
	s_nop 0
	v_pk_fma_f32 v[74:75], v[0:1], v[26:27], v[74:75] op_sel_hi:[0,1,1]
	v_pk_fma_f32 v[16:17], v[0:1], v[28:29], v[16:17] op_sel_hi:[0,1,1]
	ds_read_b128 v[26:29], v68
	s_waitcnt lgkmcnt(5)
	s_nop 0
	v_pk_fma_f32 v[8:9], v[0:1], v[12:13], v[8:9] op_sel_hi:[0,1,1]
	v_pk_fma_f32 v[0:1], v[0:1], v[14:15], v[4:5] op_sel_hi:[0,1,1]
	ds_read_b128 v[12:15], v68 offset:16
	s_waitcnt vmcnt(9) lgkmcnt(5)
	s_nop 0
	v_pk_fma_f32 v[4:5], v[64:65], v[32:33], v[70:71] op_sel_hi:[0,1,1]
	v_pk_fma_f32 v[72:73], v[64:65], v[34:35], v[72:73] op_sel_hi:[0,1,1]
	ds_read_b128 v[32:35], v68 offset:32
	ds_read_b128 v[68:71], v68 offset:48
	s_waitcnt lgkmcnt(6)
	s_nop 0
	v_pk_fma_f32 v[76:77], v[64:65], v[44:45], v[76:77] op_sel_hi:[0,1,1]
	v_pk_fma_f32 v[78:79], v[64:65], v[46:47], v[78:79] op_sel_hi:[0,1,1]
	ds_read_b128 v[44:47], v67
	s_waitcnt lgkmcnt(6)
	s_nop 0
	v_pk_fma_f32 v[74:75], v[64:65], v[36:37], v[74:75] op_sel_hi:[0,1,1]
	v_pk_fma_f32 v[16:17], v[64:65], v[38:39], v[16:17] op_sel_hi:[0,1,1]
	ds_read_b128 v[36:39], v67 offset:16
	s_waitcnt lgkmcnt(6)
	s_nop 0
	v_pk_fma_f32 v[8:9], v[64:65], v[20:21], v[8:9] op_sel_hi:[0,1,1]
	v_pk_fma_f32 v[0:1], v[64:65], v[22:23], v[0:1] op_sel_hi:[0,1,1]
	ds_read_b128 v[20:23], v67 offset:32
	s_waitcnt vmcnt(8) lgkmcnt(6)
	s_nop 0
	v_pk_fma_f32 v[4:5], v[62:63], v[26:27], v[4:5] op_sel_hi:[0,1,1]
	v_pk_fma_f32 v[80:81], v[62:63], v[28:29], v[72:73] op_sel_hi:[0,1,1]
	ds_read_b128 v[26:29], v67 offset:48
	s_waitcnt lgkmcnt(6)
	s_nop 0
	v_pk_fma_f32 v[76:77], v[62:63], v[12:13], v[76:77] op_sel_hi:[0,1,1]
	v_pk_fma_f32 v[78:79], v[62:63], v[14:15], v[78:79] op_sel_hi:[0,1,1]
	ds_read_b128 v[12:15], v66
	s_waitcnt lgkmcnt(6)
	s_nop 0
	v_pk_fma_f32 v[82:83], v[62:63], v[32:33], v[74:75] op_sel_hi:[0,1,1]
	v_pk_fma_f32 v[16:17], v[62:63], v[34:35], v[16:17] op_sel_hi:[0,1,1]
	ds_read_b128 v[32:35], v66 offset:16
	s_waitcnt lgkmcnt(6)
	s_nop 0
	v_pk_fma_f32 v[8:9], v[62:63], v[68:69], v[8:9] op_sel_hi:[0,1,1]
	v_pk_fma_f32 v[0:1], v[62:63], v[70:71], v[0:1] op_sel_hi:[0,1,1]
	ds_read_b128 v[68:71], v66 offset:32
	ds_read_b128 v[72:75], v66 offset:48
	s_waitcnt vmcnt(7) lgkmcnt(7)
	s_nop 0
	v_pk_fma_f32 v[4:5], v[10:11], v[44:45], v[4:5] op_sel_hi:[0,1,1]
	v_pk_fma_f32 v[66:67], v[10:11], v[46:47], v[80:81] op_sel_hi:[0,1,1]
	ds_read_b128 v[44:47], v65
	s_waitcnt lgkmcnt(7)
	s_nop 0
	v_pk_fma_f32 v[76:77], v[10:11], v[36:37], v[76:77] op_sel_hi:[0,1,1]
	v_pk_fma_f32 v[78:79], v[10:11], v[38:39], v[78:79] op_sel_hi:[0,1,1]
	ds_read_b128 v[36:39], v65 offset:16
	s_waitcnt lgkmcnt(7)
	s_nop 0
	v_pk_fma_f32 v[80:81], v[10:11], v[20:21], v[82:83] op_sel_hi:[0,1,1]
	v_pk_fma_f32 v[16:17], v[10:11], v[22:23], v[16:17] op_sel_hi:[0,1,1]
	ds_read_b128 v[20:23], v65 offset:32
	s_waitcnt lgkmcnt(7)
	s_nop 0
	v_pk_fma_f32 v[82:83], v[10:11], v[26:27], v[8:9] op_sel_hi:[0,1,1]
	v_pk_fma_f32 v[0:1], v[10:11], v[28:29], v[0:1] op_sel_hi:[0,1,1]
	ds_read_b128 v[8:11], v65 offset:48
	ds_read_b128 v[26:29], v63
	s_waitcnt vmcnt(6) lgkmcnt(8)
	s_nop 0
	v_pk_fma_f32 v[4:5], v[2:3], v[12:13], v[4:5] op_sel_hi:[0,1,1]
	v_pk_fma_f32 v[12:13], v[2:3], v[14:15], v[66:67] op_sel_hi:[0,1,1]
	ds_read_b128 v[64:67], v63 offset:16
	s_waitcnt lgkmcnt(8)
	s_nop 0
	v_pk_fma_f32 v[14:15], v[2:3], v[32:33], v[76:77] op_sel_hi:[0,1,1]
	v_pk_fma_f32 v[84:85], v[2:3], v[34:35], v[78:79] op_sel_hi:[0,1,1]
	ds_read_b128 v[32:35], v63 offset:32
	s_waitcnt lgkmcnt(8)
	s_nop 0
	v_pk_fma_f32 v[86:87], v[2:3], v[68:69], v[80:81] op_sel_hi:[0,1,1]
	v_pk_fma_f32 v[16:17], v[2:3], v[70:71], v[16:17] op_sel_hi:[0,1,1]
	ds_read_b128 v[68:71], v63 offset:48
	s_waitcnt lgkmcnt(8)
	s_nop 0
	v_pk_fma_f32 v[62:63], v[2:3], v[72:73], v[82:83] op_sel_hi:[0,1,1]
	v_pk_fma_f32 v[88:89], v[2:3], v[74:75], v[0:1] op_sel_hi:[0,1,1]
	ds_read_b128 v[72:75], v25
	ds_read_b128 v[76:79], v25 offset:16
	s_waitcnt vmcnt(5) lgkmcnt(9)
	s_nop 0
	v_pk_fma_f32 v[90:91], v[6:7], v[44:45], v[4:5] op_sel_hi:[0,1,1]
	v_pk_fma_f32 v[12:13], v[6:7], v[46:47], v[12:13] op_sel_hi:[0,1,1]
	ds_read_b128 v[44:47], v25 offset:32
	ds_read_b128 v[80:83], v25 offset:48
	s_waitcnt lgkmcnt(10)
	s_nop 0
	v_pk_fma_f32 v[36:37], v[6:7], v[36:37], v[14:15] op_sel_hi:[0,1,1]
	v_pk_fma_f32 v[38:39], v[6:7], v[38:39], v[84:85] op_sel_hi:[0,1,1]
	s_waitcnt lgkmcnt(9)
	s_nop 0
	v_pk_fma_f32 v[20:21], v[6:7], v[20:21], v[86:87] op_sel_hi:[0,1,1]
	v_pk_fma_f32 v[22:23], v[6:7], v[22:23], v[16:17] op_sel_hi:[0,1,1]
	ds_read_b128 v[0:3], v19
	s_waitcnt lgkmcnt(9)
	s_nop 0
	v_pk_fma_f32 v[24:25], v[6:7], v[8:9], v[62:63] op_sel_hi:[0,1,1]
	v_pk_fma_f32 v[62:63], v[6:7], v[10:11], v[88:89] op_sel_hi:[0,1,1]
	ds_read_b128 v[4:7], v19 offset:16
	s_waitcnt vmcnt(4) lgkmcnt(9)
	s_nop 0
	v_pk_fma_f32 v[28:29], v[30:31], v[28:29], v[12:13] op_sel_hi:[0,1,1]
	ds_read_b128 v[8:11], v19 offset:32
	ds_read_b128 v[12:15], v19 offset:48
	v_pk_fma_f32 v[84:85], v[30:31], v[26:27], v[90:91] op_sel_hi:[0,1,1]
	s_waitcnt lgkmcnt(10)
	s_nop 0
	v_pk_fma_f32 v[36:37], v[30:31], v[64:65], v[36:37] op_sel_hi:[0,1,1]
	v_pk_fma_f32 v[38:39], v[30:31], v[66:67], v[38:39] op_sel_hi:[0,1,1]
	ds_read_b128 v[16:19], v43
	s_waitcnt lgkmcnt(10)
	s_nop 0
	v_pk_fma_f32 v[86:87], v[30:31], v[32:33], v[20:21] op_sel_hi:[0,1,1]
	v_pk_fma_f32 v[88:89], v[30:31], v[34:35], v[22:23] op_sel_hi:[0,1,1]
	ds_read_b128 v[20:23], v43 offset:16
	s_waitcnt lgkmcnt(10)
	s_nop 0
	v_pk_fma_f32 v[90:91], v[30:31], v[68:69], v[24:25] op_sel_hi:[0,1,1]
	v_pk_fma_f32 v[92:93], v[30:31], v[70:71], v[62:63] op_sel_hi:[0,1,1]
	ds_read_b128 v[24:27], v43 offset:32
	s_waitcnt vmcnt(3) lgkmcnt(10)
	s_nop 0
	v_pk_fma_f32 v[64:65], v[40:41], v[74:75], v[28:29] op_sel_hi:[0,1,1]
	ds_read_b128 v[28:31], v43 offset:48
	v_pk_fma_f32 v[62:63], v[40:41], v[72:73], v[84:85] op_sel_hi:[0,1,1]
	s_waitcnt lgkmcnt(10)
	s_nop 0
	v_pk_fma_f32 v[66:67], v[40:41], v[76:77], v[36:37] op_sel_hi:[0,1,1]
	v_pk_fma_f32 v[68:69], v[40:41], v[78:79], v[38:39] op_sel_hi:[0,1,1]
	ds_read_b128 v[32:35], v55
	ds_read_b128 v[36:39], v55 offset:16
	s_waitcnt lgkmcnt(11)
	s_nop 0
	v_pk_fma_f32 v[70:71], v[40:41], v[44:45], v[86:87] op_sel_hi:[0,1,1]
	v_pk_fma_f32 v[72:73], v[40:41], v[46:47], v[88:89] op_sel_hi:[0,1,1]
	s_waitcnt lgkmcnt(10)
	s_nop 0
	v_pk_fma_f32 v[74:75], v[40:41], v[80:81], v[90:91] op_sel_hi:[0,1,1]
	v_pk_fma_f32 v[76:77], v[40:41], v[82:83], v[92:93] op_sel_hi:[0,1,1]
	ds_read_b128 v[40:43], v55 offset:32
	ds_read_b128 v[44:47], v55 offset:48
	s_waitcnt vmcnt(2) lgkmcnt(11)
	s_nop 0
	v_pk_fma_f32 v[0:1], v[60:61], v[0:1], v[62:63] op_sel_hi:[0,1,1]
	v_pk_fma_f32 v[2:3], v[60:61], v[2:3], v[64:65] op_sel_hi:[0,1,1]
	s_waitcnt lgkmcnt(10)
	s_nop 0
	v_pk_fma_f32 v[4:5], v[60:61], v[4:5], v[66:67] op_sel_hi:[0,1,1]
	v_pk_fma_f32 v[6:7], v[60:61], v[6:7], v[68:69] op_sel_hi:[0,1,1]
	s_waitcnt lgkmcnt(9)
	s_nop 0
	v_pk_fma_f32 v[8:9], v[60:61], v[8:9], v[70:71] op_sel_hi:[0,1,1]
	v_pk_fma_f32 v[10:11], v[60:61], v[10:11], v[72:73] op_sel_hi:[0,1,1]
	s_waitcnt lgkmcnt(8)
	s_nop 0
	v_pk_fma_f32 v[12:13], v[60:61], v[12:13], v[74:75] op_sel_hi:[0,1,1]
	v_pk_fma_f32 v[14:15], v[60:61], v[14:15], v[76:77] op_sel_hi:[0,1,1]
	s_waitcnt vmcnt(1) lgkmcnt(7)
	s_nop 0
	v_pk_fma_f32 v[0:1], v[58:59], v[16:17], v[0:1] op_sel_hi:[0,1,1]
	v_pk_fma_f32 v[2:3], v[58:59], v[18:19], v[2:3] op_sel_hi:[0,1,1]
	s_waitcnt lgkmcnt(6)
	s_nop 0
	v_pk_fma_f32 v[4:5], v[58:59], v[20:21], v[4:5] op_sel_hi:[0,1,1]
	v_pk_fma_f32 v[6:7], v[58:59], v[22:23], v[6:7] op_sel_hi:[0,1,1]
	s_waitcnt lgkmcnt(5)
	s_nop 0
	v_pk_fma_f32 v[16:17], v[58:59], v[24:25], v[8:9] op_sel_hi:[0,1,1]
	v_pk_fma_f32 v[18:19], v[58:59], v[26:27], v[10:11] op_sel_hi:[0,1,1]
	s_waitcnt lgkmcnt(4)
	s_nop 0
	v_pk_fma_f32 v[20:21], v[58:59], v[28:29], v[12:13] op_sel_hi:[0,1,1]
	v_pk_fma_f32 v[22:23], v[58:59], v[30:31], v[14:15] op_sel_hi:[0,1,1]
	s_waitcnt vmcnt(0) lgkmcnt(3)
	s_nop 0
	v_pk_fma_f32 v[12:13], v[52:53], v[32:33], v[0:1] op_sel_hi:[0,1,1]
	v_pk_fma_f32 v[14:15], v[52:53], v[34:35], v[2:3] op_sel_hi:[0,1,1]
	s_waitcnt lgkmcnt(2)
	s_nop 0
	v_pk_fma_f32 v[8:9], v[52:53], v[36:37], v[4:5] op_sel_hi:[0,1,1]
	v_pk_fma_f32 v[10:11], v[52:53], v[38:39], v[6:7] op_sel_hi:[0,1,1]
	s_waitcnt lgkmcnt(1)
	s_nop 0
	v_pk_fma_f32 v[4:5], v[52:53], v[40:41], v[16:17] op_sel_hi:[0,1,1]
	v_pk_fma_f32 v[6:7], v[52:53], v[42:43], v[18:19] op_sel_hi:[0,1,1]
	s_waitcnt lgkmcnt(0)
	s_nop 0
	v_pk_fma_f32 v[0:1], v[52:53], v[44:45], v[20:21] op_sel_hi:[0,1,1]
	v_pk_fma_f32 v[2:3], v[52:53], v[46:47], v[22:23] op_sel_hi:[0,1,1]
	s_cbranch_scc1 .LBB0_29
	s_nop 0
	ds_write_b128 v49, v[12:15]
	ds_write_b128 v49, v[8:11] offset:16
	ds_write_b128 v49, v[4:7] offset:32
	ds_write_b128 v49, v[0:3] offset:48
	s_waitcnt lgkmcnt(0)
	s_barrier
	s_mov_b64 s[0:1], exec
	s_nop 0
	v_readlane_b32 s2, v254, 17
	v_readlane_b32 s3, v254, 18
	v_readlane_b32 s36, v254, 5
	v_readlane_b32 s16, v254, 26
	v_readlane_b32 s18, v254, 20
	s_and_b64 s[2:3], s[0:1], s[2:3]
	s_nop 0
	v_readlane_b32 s61, v254, 3
	v_readlane_b32 s64, v254, 4
	v_readlane_b32 s93, v254, 7
	v_readlane_b32 s37, v254, 6
	s_movk_i32 s9, 0x3000
	s_nop 0
	v_readlane_b32 s17, v254, 27
	v_readlane_b32 s19, v254, 21
	s_mov_b64 exec, s[2:3]
	s_cbranch_execz .LBB0_17
	s_lshl_b64 s[2:3], s[16:17], 2
	s_nop 0
	v_readlane_b32 s4, v254, 24
	v_readlane_b32 s5, v254, 25
	s_add_u32 s2, s4, s2
	s_addc_u32 s3, s5, s3
	s_lshl_b64 s[4:5], s[16:17], 1
	s_nop 0
	v_readlane_b32 s6, v254, 22
	v_readlane_b32 s7, v254, 23
	s_add_u32 s4, s6, s4
	s_addc_u32 s5, s7, s5
	s_cmp_lg_u64 s[6:7], 0
	s_mov_b64 s[12:13], 0
	s_cselect_b64 s[14:15], -1, 0
	v_mov_b32_e32 v0, v48
	s_branch .LBB0_33
.LBB0_32:
	s_movk_i32 s6, 0x5ff
	v_add_u32_e32 v1, 0x200, v0
	v_cmp_lt_i32_e32 vcc, s6, v0
	s_or_b64 s[12:13], vcc, s[12:13]
	v_mov_b32_e64 v0, v1
	s_andn2_b64 exec, exec, s[12:13]
	s_cbranch_execz .LBB0_17
.LBB0_33:
	v_and_b32_e32 v1, 0x7f, v0
	v_add_u32_e32 v2, s16, v1
	v_ashrrev_i32_e32 v3, 31, v2
	v_lshl_add_u64 v[2:3], v[2:3], 2, s[18:19]
	global_load_dword v3, v[2:3], off
	v_ashrrev_i32_e32 v2, 7, v0
	s_nop 0
	s_add_i32 s8, 0, 0x10000
	v_lshlrev_b32_e32 v6, 6, v1
	v_lshlrev_b32_e32 v7, 2, v2
	v_add3_u32 v8, s8, v6, v7
	ds_read2st64_b32 v[6:7], v8 offset1:32
	ds_read2st64_b32 v[8:9], v8 offset0:64 offset1:96
	v_mad_i64_i32 v[4:5], s[6:7], s10, v2, 0
	v_lshlrev_b32_e32 v52, 2, v1
	s_waitcnt lgkmcnt(1)
	v_add_f32_e32 v6, v6, v7
	s_waitcnt lgkmcnt(0)
	v_add_f32_e64 v6, v6, v8
	v_lshl_add_u64 v[4:5], v[4:5], 2, s[2:3]
	v_add_f32_e64 v6, v6, v9
	v_lshl_add_u64 v[4:5], v[4:5], 0, v[52:53]
	s_andn2_b64 vcc, exec, s[14:15]
	s_waitcnt vmcnt(0)
	v_add_f32_e64 v3, v6, v3
	global_store_dword v[4:5], v3, off
	s_cbranch_vccnz .LBB0_32
	s_nop 0
	v_bfe_u32 v4, v3, 16, 1
	s_movk_i32 s6, 0x7fff
	s_nop 0
	v_add3_u32 v6, v3, v4, s6
	v_mov_b64_e32 v[4:5], s[4:5]
	s_nop 0
	v_mad_i64_i32 v[2:3], s[6:7], v2, s9, v[4:5]
	v_lshlrev_b32_e32 v52, 1, v1
	s_nop 0
	v_lshl_add_u64 v[2:3], v[2:3], 0, v[52:53]
	global_store_short_d16_hi v[2:3], v6, off
	s_branch .LBB0_32
.LBB0_35:
	s_nop 0
	v_readlane_b32 s0, v253, 8
	s_lshl_b32 s0, s0, 3
	s_nop 0
	v_readlane_b32 s1, v253, 9
	s_add_i32 s19, s0, s1
	s_nop 0
	s_cmp_lt_i32 s19, 0xdc00
	v_and_b32_e32 v34, 63, v51
	s_cselect_b64 s[0:1], -1, 0
	s_cmp_gt_i32 s19, 0xdbff
	s_barrier
	s_cbranch_scc1 .LBB0_43
	s_cmpk_gt_i32 s19, 0xbff
	s_cbranch_scc0 .LBB0_150
	s_cmpk_gt_u32 s19, 0xfff
	s_cbranch_scc0 .LBB0_151
	s_cmpk_gt_u32 s19, 0x13ff
	s_cbranch_scc0 .LBB0_152
	s_cmpk_gt_u32 s19, 0x17ff
	s_cbranch_scc0 .LBB0_153
	s_cmpk_gt_u32 s19, 0x1bff
	s_cbranch_scc0 .LBB0_154
	s_cmpk_gt_u32 s19, 0x9bff
	s_cbranch_scc0 .LBB0_155
	v_readlane_b32 s36, v253, 50
	s_add_i32 s2, s19, 0xffff6400
	v_readlane_b32 s40, v253, 54
	v_readlane_b32 s41, v253, 55
	s_lshr_b32 s2, s2, 8
	s_mov_b32 s3, 0
	v_readlane_b32 s42, v253, 56
	v_readlane_b32 s43, v253, 57
	v_readlane_b32 s44, v253, 58
	v_readlane_b32 s45, v253, 59
	v_readlane_b32 s46, v253, 60
	v_readlane_b32 s47, v253, 61
	v_readlane_b32 s48, v253, 62
	v_readlane_b32 s49, v253, 63
	s_mov_b64 s[8:9], s[40:41]
	s_lshl_b64 s[2:3], s[2:3], 21
	s_mov_b64 s[14:15], s[46:47]
	s_add_u32 s2, s14, s2
	v_readlane_b32 s37, v253, 51
	s_addc_u32 s3, s15, s3
	s_lshl_b32 s4, s19, 1
	v_readlane_b32 s36, v254, 5
	s_and_b32 s5, s4, 0x1c0
	s_lshl_b32 s4, s19, 5
	s_nop 0
	v_readlane_b32 s38, v253, 52
	v_readlane_b32 s39, v253, 53
	v_readlane_b32 s50, v254, 0
	v_readlane_b32 s51, v254, 1
	v_readlane_b32 s37, v254, 6
	s_mov_b64 s[10:11], s[42:43]
	s_mov_b64 s[12:13], s[44:45]
	s_mov_b64 s[16:17], s[48:49]
	s_nop 0
	s_and_b32 s4, s4, 0x3e0
	s_mov_b64 s[6:7], 0
	s_branch .LBB0_156

.LBB0_45:
	s_nop 0
	v_readlane_b32 s0, v253, 9
	s_lshl_b32 s0, s0, 14
	s_add_i32 s0, s0, 0
	s_lshl_b32 s20, s61, 4
	s_nop 0
	v_readlane_b32 s4, v253, 0
	v_readlane_b32 s5, v253, 1
	s_add_u32 s21, s4, 0xae00000
	s_addc_u32 s22, s5, 0
	s_nop 0
	s_add_u32 s23, s4, 0x2e00000
	s_addc_u32 s24, s5, 0
	s_nop 0
	s_add_u32 s25, s4, 0x2a00000
	s_addc_u32 s26, s5, 0
	s_nop 0
	s_add_u32 s27, s4, 0x2600000
	s_addc_u32 s28, s5, 0
	s_nop 0
	s_add_u32 s2, s4, 0x2200000
	s_addc_u32 s3, s5, 0
	s_nop 0
	s_add_u32 s29, s4, 0x1e00000
	v_lshlrev_b32_e32 v36, 3, v34
	s_addc_u32 s30, s5, 0
	v_lshrrev_b32_e32 v33, 5, v34
	v_and_b32_e32 v32, 31, v51
	v_and_b32_e32 v36, 56, v36
	v_lshrrev_b32_e32 v40, 3, v34
	s_add_u32 s31, s4, 0x1200000
	v_lshl_add_u32 v45, v32, 2, s0
	v_mul_u32_u24_e32 v46, 0x84, v33
	v_mov_b32_e64 v35, 0
	v_mul_u32_u24_e32 v41, 0x84, v36
	v_lshlrev_b32_e32 v34, 2, v40
	s_mov_b32 s49, s93
	s_mov_b32 s1, 0
	s_addc_u32 s33, s5, 0
	v_mov_b32_e64 v37, v35
	v_add3_u32 v41, s0, v41, v34
	v_or_b32_e32 v42, 8, v40
	v_or_b32_e32 v43, 16, v40
	v_or_b32_e32 v44, 24, v40
	s_lshl_b32 s34, s19, 1
	s_lshl_b32 s35, s61, 5
	s_lshl_b32 s36, s19, 5
	s_lshl_b32 s37, s61, 9
	s_lshl_b32 s38, s19, 6
	s_lshl_b32 s39, s61, 10
	s_mul_i32 s40, s61, 24
	s_mul_i32 s41, s61, 0x300
	s_mul_i32 s42, s61, 48
	s_lshl_b32 s43, s61, 8
	s_movk_i32 s44, 0xa400
	s_nop 0
	s_mov_b32 s45, 0xc3e00000
	v_add_u32_e64 v45, v45, v46
	v_mov_b32_e32 v46, 0x43e00000
	s_branch .LBB0_49
.LBB0_46:
	s_ashr_i32 s15, s14, 31
	s_lshl_b64 s[14:15], s[14:15], 2
	s_add_u32 s12, s12, s14
	v_add_u32_e64 v88, s0, v33
	s_addc_u32 s13, s13, s15
	v_lshlrev_b32_e32 v34, 2, v32
	v_lshl_add_u64 v[38:39], s[12:13], 0, v[34:35]
	v_ashrrev_i32_e32 v34, 31, v88
	s_nop 0
	v_mul_lo_u32 v34, s10, v34
	v_mul_lo_u32 v47, s11, v88
	v_mad_u64_u32 v[48:49], s[12:13], s10, v88, 0
	v_add3_u32 v49, v49, v34, v47
	v_add_u32_e32 v34, 2, v88
	v_ashrrev_i32_e32 v47, 31, v34
	v_mul_lo_u32 v47, s10, v47
	v_mul_lo_u32 v52, s11, v34
	v_mad_u64_u32 v[50:51], s[12:13], s10, v34, 0
	v_add_u32_e64 v34, 4, v88
	v_add3_u32 v51, v51, v47, v52
	v_ashrrev_i32_e32 v47, 31, v34
	s_nop 0
	v_mul_lo_u32 v47, s10, v47
	v_mul_lo_u32 v54, s11, v34
	v_mad_u64_u32 v[52:53], s[12:13], s10, v34, 0
	v_add_u32_e64 v34, 6, v88
	v_add3_u32 v53, v53, v47, v54
	v_ashrrev_i32_e32 v47, 31, v34
	s_nop 0
	v_mul_lo_u32 v47, s10, v47
	v_mul_lo_u32 v56, s11, v34
	v_mad_u64_u32 v[54:55], s[12:13], s10, v34, 0
	v_add_u32_e64 v34, 8, v88
	v_add3_u32 v55, v55, v47, v56
	v_ashrrev_i32_e32 v47, 31, v34
	s_nop 0
	v_mul_lo_u32 v47, s10, v47
	v_mul_lo_u32 v58, s11, v34
	v_mad_u64_u32 v[56:57], s[12:13], s10, v34, 0
	v_add_u32_e64 v34, 10, v88
	v_add3_u32 v57, v57, v47, v58
	v_ashrrev_i32_e32 v47, 31, v34
	s_nop 0
	v_mul_lo_u32 v47, s10, v47
	v_mul_lo_u32 v60, s11, v34
	v_mad_u64_u32 v[58:59], s[12:13], s10, v34, 0
	v_add_u32_e64 v34, 12, v88
	v_add3_u32 v59, v59, v47, v60
	v_ashrrev_i32_e32 v47, 31, v34
	s_nop 0
	v_mul_lo_u32 v47, s10, v47
	v_mul_lo_u32 v62, s11, v34
	v_mad_u64_u32 v[60:61], s[12:13], s10, v34, 0
	v_add_u32_e64 v34, 14, v88
	v_add3_u32 v61, v61, v47, v62
	v_ashrrev_i32_e32 v47, 31, v34
	s_nop 0
	v_mul_lo_u32 v47, s10, v47
	v_mul_lo_u32 v64, s11, v34
	v_mad_u64_u32 v[62:63], s[12:13], s10, v34, 0
	v_lshl_add_u64 v[48:49], v[48:49], 2, v[38:39]
	v_lshl_add_u64 v[50:51], v[50:51], 2, v[38:39]
	v_lshl_add_u64 v[52:53], v[52:53], 2, v[38:39]
	v_lshl_add_u64 v[54:55], v[54:55], 2, v[38:39]
	v_add3_u32 v63, v63, v47, v64
	v_add_u32_e64 v34, 16, v88
	v_lshl_add_u64 v[56:57], v[56:57], 2, v[38:39]
	v_lshl_add_u64 v[58:59], v[58:59], 2, v[38:39]
	v_lshl_add_u64 v[60:61], v[60:61], 2, v[38:39]
	v_lshl_add_u64 v[62:63], v[62:63], 2, v[38:39]
	global_load_dword v47, v[48:49], off
	s_nop 0
	s_nop 0
	global_load_dword v48, v[50:51], off
	global_load_dword v49, v[52:53], off
	s_nop 0
	s_nop 0
	global_load_dword v50, v[54:55], off
	global_load_dword v52, v[56:57], off
	global_load_dword v53, v[58:59], off
	s_nop 0
	s_nop 0
	global_load_dword v54, v[60:61], off
	global_load_dword v55, v[62:63], off
	v_ashrrev_i32_e32 v51, 31, v34
	s_nop 0
	v_mul_lo_u32 v51, s10, v51
	v_mul_lo_u32 v58, s11, v34
	v_mad_u64_u32 v[56:57], s[12:13], s10, v34, 0
	v_add_u32_e64 v34, 18, v88
	v_add3_u32 v57, v57, v51, v58
	v_ashrrev_i32_e32 v51, 31, v34
	s_nop 0
	v_mul_lo_u32 v51, s10, v51
	v_mul_lo_u32 v60, s11, v34
	v_mad_u64_u32 v[58:59], s[12:13], s10, v34, 0
	v_add_u32_e64 v34, 20, v88
	v_add3_u32 v59, v59, v51, v60
	v_ashrrev_i32_e32 v51, 31, v34
	s_nop 0
	v_mul_lo_u32 v51, s10, v51
	v_mul_lo_u32 v62, s11, v34
	v_mad_u64_u32 v[60:61], s[12:13], s10, v34, 0
	v_add_u32_e64 v34, 22, v88
	v_add3_u32 v61, v61, v51, v62
	v_ashrrev_i32_e32 v51, 31, v34
	s_nop 0
	v_mul_lo_u32 v51, s10, v51
	v_mul_lo_u32 v64, s11, v34
	v_mad_u64_u32 v[62:63], s[12:13], s10, v34, 0
	v_add_u32_e64 v34, 24, v88
	v_add3_u32 v63, v63, v51, v64
	v_ashrrev_i32_e32 v51, 31, v34
	s_nop 0
	v_mul_lo_u32 v51, s10, v51
	v_mul_lo_u32 v66, s11, v34
	v_mad_u64_u32 v[64:65], s[12:13], s10, v34, 0
	v_add_u32_e64 v34, 26, v88
	v_add3_u32 v65, v65, v51, v66
	v_ashrrev_i32_e32 v51, 31, v34
	s_nop 0
	v_mul_lo_u32 v51, s10, v51
	v_mul_lo_u32 v68, s11, v34
	v_mad_u64_u32 v[66:67], s[12:13], s10, v34, 0
	v_add_u32_e64 v34, 28, v88
	v_add3_u32 v67, v67, v51, v68
	v_ashrrev_i32_e32 v51, 31, v34
	s_nop 0
	v_mul_lo_u32 v51, s10, v51
	v_mul_lo_u32 v70, s11, v34
	v_mad_u64_u32 v[68:69], s[12:13], s10, v34, 0
	v_add_u32_e64 v34, 30, v88
	v_add3_u32 v69, v69, v51, v70
	v_ashrrev_i32_e32 v51, 31, v34
	s_nop 0
	v_mul_lo_u32 v51, s10, v51
	v_mul_lo_u32 v72, s11, v34
	v_mad_u64_u32 v[70:71], s[12:13], s10, v34, 0
	v_add_u32_e64 v34, 32, v88
	v_lshl_add_u64 v[56:57], v[56:57], 2, v[38:39]
	v_lshl_add_u64 v[58:59], v[58:59], 2, v[38:39]
	v_lshl_add_u64 v[60:61], v[60:61], 2, v[38:39]
	v_lshl_add_u64 v[62:63], v[62:63], 2, v[38:39]
	v_lshl_add_u64 v[64:65], v[64:65], 2, v[38:39]
	v_lshl_add_u64 v[66:67], v[66:67], 2, v[38:39]
	v_add3_u32 v71, v71, v51, v72
	v_ashrrev_i32_e32 v51, 31, v34
	s_nop 0
	v_lshl_add_u64 v[68:69], v[68:69], 2, v[38:39]
	v_lshl_add_u64 v[70:71], v[70:71], 2, v[38:39]
	global_load_dword v56, v[56:57], off
	s_nop 0
	s_nop 0
	global_load_dword v57, v[58:59], off
	s_nop 0
	s_nop 0
	global_load_dword v58, v[60:61], off
	global_load_dword v59, v[62:63], off
	s_nop 0
	s_nop 0
	global_load_dword v60, v[64:65], off
	global_load_dword v61, v[66:67], off
	global_load_dword v62, v[68:69], off
	global_load_dword v63, v[70:71], off
	v_mul_lo_u32 v51, s10, v51
	v_mul_lo_u32 v66, s11, v34
	v_mad_u64_u32 v[64:65], s[12:13], s10, v34, 0
	v_add_u32_e64 v34, 34, v88
	v_add3_u32 v65, v65, v51, v66
	v_ashrrev_i32_e32 v51, 31, v34
	s_nop 0
	v_mul_lo_u32 v51, s10, v51
	v_mul_lo_u32 v68, s11, v34
	v_mad_u64_u32 v[66:67], s[12:13], s10, v34, 0
	v_add_u32_e64 v34, 36, v88
	v_add3_u32 v67, v67, v51, v68
	v_ashrrev_i32_e32 v51, 31, v34
	s_nop 0
	v_mul_lo_u32 v51, s10, v51
	v_mul_lo_u32 v70, s11, v34
	v_mad_u64_u32 v[68:69], s[12:13], s10, v34, 0
	v_add_u32_e64 v34, 38, v88
	v_add3_u32 v69, v69, v51, v70
	v_ashrrev_i32_e32 v51, 31, v34
	s_nop 0
	v_mul_lo_u32 v51, s10, v51
	v_mul_lo_u32 v72, s11, v34
	v_mad_u64_u32 v[70:71], s[12:13], s10, v34, 0
	v_add_u32_e64 v34, 40, v88
	v_add3_u32 v71, v71, v51, v72
	v_ashrrev_i32_e32 v51, 31, v34
	s_nop 0
	v_mul_lo_u32 v51, s10, v51
	v_mul_lo_u32 v74, s11, v34
	v_mad_u64_u32 v[72:73], s[12:13], s10, v34, 0
	v_add_u32_e64 v34, 42, v88
	v_add3_u32 v73, v73, v51, v74
	v_ashrrev_i32_e32 v51, 31, v34
	s_nop 0
	v_mul_lo_u32 v51, s10, v51
	v_mul_lo_u32 v76, s11, v34
	v_mad_u64_u32 v[74:75], s[12:13], s10, v34, 0
	v_add_u32_e64 v34, 44, v88
	v_add3_u32 v75, v75, v51, v76
	v_ashrrev_i32_e32 v51, 31, v34
	s_nop 0
	v_mul_lo_u32 v51, s10, v51
	v_mul_lo_u32 v78, s11, v34
	v_mad_u64_u32 v[76:77], s[12:13], s10, v34, 0
	v_add_u32_e64 v34, 46, v88
	v_add3_u32 v77, v77, v51, v78
	v_ashrrev_i32_e32 v51, 31, v34
	s_nop 0
	v_mul_lo_u32 v51, s10, v51
	v_mul_lo_u32 v80, s11, v34
	v_mad_u64_u32 v[78:79], s[12:13], s10, v34, 0
	v_add_u32_e64 v34, 48, v88
	v_lshl_add_u64 v[64:65], v[64:65], 2, v[38:39]
	v_lshl_add_u64 v[66:67], v[66:67], 2, v[38:39]
	v_lshl_add_u64 v[68:69], v[68:69], 2, v[38:39]
	v_lshl_add_u64 v[70:71], v[70:71], 2, v[38:39]
	v_lshl_add_u64 v[72:73], v[72:73], 2, v[38:39]
	v_lshl_add_u64 v[74:75], v[74:75], 2, v[38:39]
	v_add3_u32 v79, v79, v51, v80
	v_ashrrev_i32_e32 v51, 31, v34
	s_nop 0
	v_lshl_add_u64 v[76:77], v[76:77], 2, v[38:39]
	v_lshl_add_u64 v[78:79], v[78:79], 2, v[38:39]
	global_load_dword v64, v[64:65], off
	s_nop 0
	s_nop 0
	global_load_dword v65, v[66:67], off
	s_nop 0
	s_nop 0
	global_load_dword v66, v[68:69], off
	global_load_dword v67, v[70:71], off
	s_nop 0
	s_nop 0
	global_load_dword v68, v[72:73], off
	global_load_dword v69, v[74:75], off
	global_load_dword v70, v[76:77], off
	global_load_dword v71, v[78:79], off
	v_mul_lo_u32 v51, s10, v51
	v_mul_lo_u32 v74, s11, v34
	v_mad_u64_u32 v[72:73], s[12:13], s10, v34, 0
	v_add_u32_e64 v34, 50, v88
	v_add3_u32 v73, v73, v51, v74
	v_ashrrev_i32_e32 v51, 31, v34
	s_nop 0
	v_mul_lo_u32 v51, s10, v51
	v_mul_lo_u32 v76, s11, v34
	v_mad_u64_u32 v[74:75], s[12:13], s10, v34, 0
	v_add_u32_e64 v34, 52, v88
	v_add3_u32 v75, v75, v51, v76
	v_ashrrev_i32_e32 v51, 31, v34
	s_nop 0
	v_lshl_add_u64 v[76:77], v[74:75], 2, v[38:39]
	v_mul_lo_u32 v51, s10, v51
	v_mul_lo_u32 v78, s11, v34
	v_mad_u64_u32 v[74:75], s[12:13], s10, v34, 0
	v_add_u32_e64 v34, 54, v88
	v_add3_u32 v75, v75, v51, v78
	v_ashrrev_i32_e32 v51, 31, v34
	s_nop 0
	v_lshl_add_u64 v[78:79], v[74:75], 2, v[38:39]
	v_mul_lo_u32 v51, s10, v51
	v_mul_lo_u32 v80, s11, v34
	v_mad_u64_u32 v[74:75], s[12:13], s10, v34, 0
	v_add_u32_e64 v34, 56, v88
	v_add3_u32 v75, v75, v51, v80
	v_ashrrev_i32_e32 v51, 31, v34
	s_nop 0
	v_lshl_add_u64 v[80:81], v[74:75], 2, v[38:39]
	v_mul_lo_u32 v51, s10, v51
	v_mul_lo_u32 v82, s11, v34
	v_mad_u64_u32 v[74:75], s[12:13], s10, v34, 0
	v_add_u32_e64 v34, 58, v88
	v_add3_u32 v75, v75, v51, v82
	v_ashrrev_i32_e32 v51, 31, v34
	s_nop 0
	v_lshl_add_u64 v[82:83], v[74:75], 2, v[38:39]
	v_mul_lo_u32 v51, s10, v51
	v_mul_lo_u32 v84, s11, v34
	v_mad_u64_u32 v[74:75], s[12:13], s10, v34, 0
	v_add_u32_e64 v34, 60, v88
	v_add3_u32 v75, v75, v51, v84
	v_ashrrev_i32_e32 v51, 31, v34
	s_nop 0
	v_lshl_add_u64 v[84:85], v[74:75], 2, v[38:39]
	v_mul_lo_u32 v51, s10, v51
	v_mul_lo_u32 v86, s11, v34
	v_mad_u64_u32 v[74:75], s[12:13], s10, v34, 0
	v_add_u32_e64 v34, 62, v88
	v_add3_u32 v75, v75, v51, v86
	v_ashrrev_i32_e32 v51, 31, v34
	s_nop 0
	v_lshl_add_u64 v[86:87], v[74:75], 2, v[38:39]
	v_mul_lo_u32 v51, s10, v51
	v_mul_lo_u32 v88, s11, v34
	v_mad_u64_u32 v[74:75], s[10:11], s10, v34, 0
	v_lshl_add_u64 v[72:73], v[72:73], 2, v[38:39]
	v_add3_u32 v75, v75, v51, v88
	v_lshl_add_u64 v[88:89], v[74:75], 2, v[38:39]
	global_load_dword v74, v[72:73], off
	global_load_dword v75, v[76:77], off
	s_nop 0
	s_nop 0
	global_load_dword v76, v[78:79], off
	global_load_dword v77, v[80:81], off
	global_load_dword v38, v[82:83], off
	global_load_dword v39, v[84:85], off
	global_load_dword v72, v[86:87], off
	global_load_dword v73, v[88:89], off
.LBB0_47:
	s_waitcnt lgkmcnt(0)
	s_nop 0
	ds_read2_b32 v[78:79], v41 offset1:33
	ds_read2_b32 v[82:83], v41 offset0:66 offset1:99
	v_mov_b32_e32 v84, v35
	v_mov_b32_e32 v85, v35
	s_ashr_i32 s0, s48, 31
	s_waitcnt lgkmcnt(1)
	v_med3_f32 v34, v78, s45, v46
	v_med3_f32 v51, v79, s45, v46
	ds_read2_b32 v[78:79], v41 offset0:132 offset1:165
	v_cvt_pk_fp8_f32 v84, v34, v51
	s_waitcnt lgkmcnt(1)
	s_nop 0
	v_med3_f32 v34, v82, s45, v46
	v_med3_f32 v51, v83, s45, v46
	ds_read2_b32 v[82:83], v41 offset0:198 offset1:231
	s_waitcnt lgkmcnt(1)
	s_nop 0
	v_med3_f32 v78, v78, s45, v46
	v_med3_f32 v79, v79, s45, v46
	v_cvt_pk_fp8_f32 v85, v78, v79
	s_add_u32 s8, s8, s48
	s_nop 0
	v_cvt_pk_fp8_f32 v84, v34, v51 op_sel:[0,0,1]
	s_waitcnt lgkmcnt(0)
	s_nop 0
	v_med3_f32 v34, v82, s45, v46
	v_med3_f32 v51, v83, s45, v46
	s_addc_u32 s9, s9, s0
	s_nop 0
	v_cvt_pk_fp8_f32 v85, v34, v51 op_sel:[0,0,1]
	v_add_u32_e64 v34, s47, v40
	v_lshl_add_u64 v[80:81], s[8:9], 0, v[36:37]
	v_ashrrev_i32_e32 v51, 31, v34
	s_nop 0
	v_mul_lo_u32 v51, s6, v51
	v_mad_u64_u32 v[78:79], s[8:9], s6, v34, v[80:81]
	v_mul_lo_u32 v34, s7, v34
	v_add3_u32 v79, v34, v79, v51
	global_store_dwordx2 v[78:79], v[84:85], off
	ds_read2_b32 v[78:79], v41 offset0:8 offset1:41
	ds_read2_b32 v[82:83], v41 offset0:74 offset1:107
	v_mov_b32_e64 v84, v35
	v_mov_b32_e32 v85, v35
	s_waitcnt lgkmcnt(1)
	v_med3_f32 v34, v78, s45, v46
	v_med3_f32 v51, v79, s45, v46
	ds_read2_b32 v[78:79], v41 offset0:140 offset1:173
	v_cvt_pk_fp8_f32 v84, v34, v51
	s_waitcnt lgkmcnt(1)
	s_nop 0
	v_med3_f32 v34, v82, s45, v46
	v_med3_f32 v51, v83, s45, v46
	ds_read2_b32 v[82:83], v41 offset0:206 offset1:239
	s_waitcnt lgkmcnt(1)
	s_nop 0
	v_med3_f32 v78, v78, s45, v46
	v_med3_f32 v79, v79, s45, v46
	v_cvt_pk_fp8_f32 v85, v78, v79
	v_cvt_pk_fp8_f32 v84, v34, v51 op_sel:[0,0,1]
	s_waitcnt lgkmcnt(0)
	s_nop 0
	v_med3_f32 v34, v82, s45, v46
	v_med3_f32 v51, v83, s45, v46
	v_cvt_pk_fp8_f32 v85, v34, v51 op_sel:[0,0,1]
	v_add_u32_e32 v34, s47, v42
	v_ashrrev_i32_e32 v51, 31, v34
	v_mul_lo_u32 v51, s6, v51
	v_mad_u64_u32 v[78:79], s[8:9], s6, v34, v[80:81]
	v_mul_lo_u32 v34, s7, v34
	v_add3_u32 v79, v34, v79, v51
	global_store_dwordx2 v[78:79], v[84:85], off
	ds_read2_b32 v[78:79], v41 offset0:16 offset1:49
	ds_read2_b32 v[82:83], v41 offset0:82 offset1:115
	v_mov_b32_e64 v84, v35
	v_mov_b32_e32 v85, v35
	s_waitcnt lgkmcnt(1)
	v_med3_f32 v34, v78, s45, v46
	v_med3_f32 v51, v79, s45, v46
	ds_read2_b32 v[78:79], v41 offset0:148 offset1:181
	v_cvt_pk_fp8_f32 v84, v34, v51
	s_waitcnt lgkmcnt(1)
	s_nop 0
	v_med3_f32 v34, v82, s45, v46
	v_med3_f32 v51, v83, s45, v46
	ds_read2_b32 v[82:83], v41 offset0:214 offset1:247
	s_waitcnt lgkmcnt(1)
	s_nop 0
	v_med3_f32 v78, v78, s45, v46
	v_med3_f32 v79, v79, s45, v46
	v_cvt_pk_fp8_f32 v85, v78, v79
	v_cvt_pk_fp8_f32 v84, v34, v51 op_sel:[0,0,1]
	s_waitcnt lgkmcnt(0)
	s_nop 0
	v_med3_f32 v34, v82, s45, v46
	v_med3_f32 v51, v83, s45, v46
	v_cvt_pk_fp8_f32 v85, v34, v51 op_sel:[0,0,1]
	v_add_u32_e32 v34, s47, v43
	v_ashrrev_i32_e32 v51, 31, v34
	v_mul_lo_u32 v51, s6, v51
	v_mad_u64_u32 v[78:79], s[8:9], s6, v34, v[80:81]
	v_mul_lo_u32 v34, s7, v34
	v_add3_u32 v79, v34, v79, v51
	global_store_dwordx2 v[78:79], v[84:85], off
	ds_read2_b32 v[78:79], v41 offset0:24 offset1:57
	ds_read2_b32 v[82:83], v41 offset0:90 offset1:123
	v_mov_b32_e64 v84, v35
	v_mov_b32_e32 v85, v35
	s_waitcnt lgkmcnt(1)
	v_med3_f32 v34, v78, s45, v46
	v_med3_f32 v51, v79, s45, v46
	ds_read2_b32 v[78:79], v41 offset0:156 offset1:189
	v_cvt_pk_fp8_f32 v84, v34, v51
	s_waitcnt lgkmcnt(1)
	s_nop 0
	v_med3_f32 v34, v82, s45, v46
	v_med3_f32 v51, v83, s45, v46
	ds_read2_b32 v[82:83], v41 offset0:222 offset1:255
	s_waitcnt lgkmcnt(1)
	s_nop 0
	v_med3_f32 v78, v78, s45, v46
	v_med3_f32 v79, v79, s45, v46
	v_cvt_pk_fp8_f32 v85, v78, v79
	v_cvt_pk_fp8_f32 v84, v34, v51 op_sel:[0,0,1]
	s_waitcnt lgkmcnt(0)
	s_nop 0
	v_med3_f32 v34, v82, s45, v46
	v_med3_f32 v51, v83, s45, v46
	v_cvt_pk_fp8_f32 v85, v34, v51 op_sel:[0,0,1]
	v_add_u32_e32 v34, s47, v44
	v_ashrrev_i32_e32 v51, 31, v34
	v_mul_lo_u32 v51, s6, v51
	v_mad_u64_u32 v[78:79], s[8:9], s6, v34, v[80:81]
	v_mul_lo_u32 v34, s7, v34
	v_add3_u32 v79, v34, v79, v51
	global_store_dwordx2 v[78:79], v[84:85], off
	s_waitcnt lgkmcnt(0)

.LBB0_49:
	s_cmpk_gt_i32 s19, 0xbff
	s_mov_b64 s[4:5], -1
	s_cbranch_scc0 .LBB0_71
	s_cmpk_gt_u32 s19, 0xfff
	s_cbranch_scc0 .LBB0_68
	s_cmpk_gt_u32 s19, 0x13ff
	s_cbranch_scc0 .LBB0_65
	s_cmpk_gt_u32 s19, 0x17ff
	s_cbranch_scc0 .LBB0_62
	s_cmpk_gt_u32 s19, 0x1bff
	s_cbranch_scc0 .LBB0_59
	s_cmpk_gt_u32 s19, 0x9bff
	s_cbranch_scc0 .LBB0_56
	s_add_i32 s0, s19, 0xffff6400
	s_lshr_b32 s0, s0, 8
	s_nop 0
	s_and_b32 s48, s34, 0x1c0
	s_and_b32 s47, s36, 0x3e0
	s_lshl_b64 s[4:5], s[0:1], 19
	s_add_u32 s8, s21, s4
	s_addc_u32 s9, s22, s5
	s_mov_b64 s[4:5], 0
.LBB0_56:
	s_andn2_b64 vcc, exec, s[4:5]
	s_nop 0
	s_mov_b64 s[6:7], 0x200
	s_cbranch_vccnz .LBB0_58
	s_cmpk_gt_u32 s19, 0x5bff
	s_cselect_b32 s0, s44, 0xffffe400
	s_cselect_b32 s6, 0x80, 0
	s_add_i32 s4, s0, s19
	s_lshr_b32 s0, s4, 8
	s_lshl_b32 s7, s4, 5
	s_lshl_b32 s4, s4, 2
	s_and_b32 s48, s4, 0x3c0
	s_lshl_b64 s[4:5], s[0:1], 20
	s_add_u32 s8, s23, s4
	s_addc_u32 s9, s24, s5
	s_nop 0
	s_and_b32 s0, s38, 0x300
	s_and_b32 s4, s7, 0x60
	s_or_b32 s0, s0, s6
	s_or_b32 s47, s0, s4
	s_mov_b64 s[6:7], 0x400

.LBB0_59:
	s_andn2_b64 vcc, exec, s[4:5]
	s_cbranch_vccnz .LBB0_61
	s_nop 0
	s_add_i32 s0, s19, 0xffffe800
	s_lshr_b32 s0, s0, 9
	s_lshl_b64 s[4:5], s[0:1], 20
	s_and_b32 s48, s34, 0x3c0
	s_and_b32 s47, s36, 0x3e0
	s_add_u32 s8, s25, s4
	s_addc_u32 s9, s26, s5
	s_mov_b64 s[6:7], 0x400

.LBB0_62:
	s_andn2_b64 vcc, exec, s[4:5]
	s_cbranch_vccnz .LBB0_64
	s_nop 0
	s_add_i32 s0, s19, 0xffffec00
	s_lshr_b32 s0, s0, 9
	s_lshl_b64 s[4:5], s[0:1], 20
	s_and_b32 s48, s34, 0x3c0
	s_and_b32 s47, s36, 0x3e0
	s_add_u32 s8, s27, s4
	s_addc_u32 s9, s28, s5
	s_mov_b64 s[6:7], 0x400

.LBB0_65:
	s_andn2_b64 vcc, exec, s[4:5]
	s_cbranch_vccnz .LBB0_67
	s_nop 0
	s_and_b32 s0, s19, 0x1fc0
	s_add_i32 s48, s0, 0xfffff000
	s_and_b32 s47, s36, 0x7e0
	s_mov_b64 s[6:7], 0x400
	s_mov_b64 s[8:9], s[2:3]

.LBB0_71:
	s_andn2_b64 vcc, exec, s[4:5]
	s_cbranch_vccnz .LBB0_73
	s_nop 0
	s_mul_hi_i32 s0, s19, 0x2aaaaaab
	s_lshr_b32 s4, s0, 31
	s_ashr_i32 s0, s0, 8
	s_add_i32 s0, s0, s4
	s_nop 0
	s_mul_i32 s4, s0, 0xfffffa00
	s_add_i32 s4, s19, s4
	s_nop 0
	s_mul_i32 s5, s4, 0x2aab
	s_lshr_b32 s6, s5, 31
	s_ashr_i32 s5, s5, 20
	s_add_i32 s5, s5, s6
	s_nop 0
	s_mul_i32 s6, s5, 0x60
	s_sub_i32 s4, s4, s6
	s_sext_i32_i16 s4, s4
	s_lshl_b32 s48, s5, 6
	s_lshl_b32 s47, s4, 5
	s_mul_hi_i32 s4, s0, 0x300000
	s_mul_i32 s0, s0, 0x300000
	s_add_u32 s8, s31, s0
	s_addc_u32 s9, s33, s4
	s_mov_b64 s[6:7], 0x400
.LBB0_73:
	s_waitcnt vmcnt(31)
	s_nop 0
	v_mul_f32_e32 v34, 0x42000000, v0
	s_waitcnt vmcnt(30)
	s_nop 0
	v_mul_f32_e32 v51, 0x42000000, v1
	ds_write2_b32 v45, v34, v51 offset1:66
	s_waitcnt vmcnt(29)
	s_nop 0
	v_mul_f32_e32 v34, 0x42000000, v2
	s_waitcnt vmcnt(28)
	s_nop 0
	v_mul_f32_e32 v51, 0x42000000, v3
	ds_write2_b32 v45, v34, v51 offset0:132 offset1:198
	s_waitcnt vmcnt(27)
	s_nop 0
	v_mul_f32_e32 v34, 0x42000000, v4
	s_waitcnt vmcnt(26)
	s_nop 0
	v_mul_f32_e32 v78, 0x42000000, v5
	v_add_u32_e32 v51, 0x400, v45
	ds_write2_b32 v51, v34, v78 offset0:8 offset1:74
	s_waitcnt vmcnt(25)
	s_nop 0
	v_mul_f32_e32 v34, 0x42000000, v6
	s_waitcnt vmcnt(24)
	s_nop 0
	v_mul_f32_e32 v78, 0x42000000, v7
	ds_write2_b32 v51, v34, v78 offset0:140 offset1:206
	s_waitcnt vmcnt(23)
	s_nop 0
	v_mul_f32_e32 v34, 0x42000000, v8
	s_waitcnt vmcnt(22)
	s_nop 0
	v_mul_f32_e32 v79, 0x42000000, v9
	v_add_u32_e32 v78, 0x800, v45
	ds_write2_b32 v78, v34, v79 offset0:16 offset1:82
	s_waitcnt vmcnt(21)
	s_nop 0
	v_mul_f32_e32 v34, 0x42000000, v10
	s_waitcnt vmcnt(20)
	s_nop 0
	v_mul_f32_e32 v79, 0x42000000, v11
	ds_write2_b32 v78, v34, v79 offset0:148 offset1:214
	s_waitcnt vmcnt(19)
	s_nop 0
	v_mul_f32_e32 v34, 0x42000000, v12
	s_waitcnt vmcnt(18)
	s_nop 0
	v_mul_f32_e32 v80, 0x42000000, v13
	v_add_u32_e32 v79, 0xc00, v45
	ds_write2_b32 v79, v34, v80 offset0:24 offset1:90
	s_waitcnt vmcnt(17)
	s_nop 0
	v_mul_f32_e32 v34, 0x42000000, v14
	s_waitcnt vmcnt(16)
	s_nop 0
	v_mul_f32_e32 v80, 0x42000000, v15
	ds_write2_b32 v79, v34, v80 offset0:156 offset1:222
	s_waitcnt vmcnt(15)
	s_nop 0
	v_mul_f32_e32 v34, 0x42000000, v16
	s_waitcnt vmcnt(14)
	s_nop 0
	v_mul_f32_e32 v81, 0x42000000, v17
	v_add_u32_e32 v80, 0x1000, v45
	ds_write2_b32 v80, v34, v81 offset0:32 offset1:98
	s_waitcnt vmcnt(13)
	s_nop 0
	v_mul_f32_e32 v34, 0x42000000, v18
	s_waitcnt vmcnt(12)
	s_nop 0
	v_mul_f32_e32 v81, 0x42000000, v19
	ds_write2_b32 v80, v34, v81 offset0:164 offset1:230
	s_waitcnt vmcnt(11)
	s_nop 0
	v_mul_f32_e32 v34, 0x42000000, v20
	s_waitcnt vmcnt(10)
	s_nop 0
	v_mul_f32_e32 v82, 0x42000000, v21
	v_add_u32_e32 v81, 0x1400, v45
	ds_write2_b32 v81, v34, v82 offset0:40 offset1:106
	s_waitcnt vmcnt(9)
	s_nop 0
	v_mul_f32_e32 v34, 0x42000000, v22
	s_waitcnt vmcnt(8)
	s_nop 0
	v_mul_f32_e32 v82, 0x42000000, v23
	ds_write2_b32 v81, v34, v82 offset0:172 offset1:238
	s_waitcnt vmcnt(7)
	s_nop 0
	v_mul_f32_e32 v34, 0x42000000, v24
	s_waitcnt vmcnt(6)
	s_nop 0
	v_mul_f32_e32 v82, 0x42000000, v25
	v_add_u32_e32 v83, 0x1800, v45
	s_add_i32 s46, s19, s20
	s_nop 0
	ds_write2_b32 v83, v34, v82 offset0:48 offset1:114
	s_waitcnt vmcnt(5)
	s_nop 0
	v_mul_f32_e32 v34, 0x42000000, v26
	s_waitcnt vmcnt(4)
	s_nop 0
	v_mul_f32_e32 v82, 0x42000000, v27
	s_cmp_gt_i32 s46, 0xdbff
	ds_write2_b32 v83, v34, v82 offset0:180 offset1:246
	s_waitcnt vmcnt(3)
	s_nop 0
	v_mul_f32_e32 v34, 0x42000000, v28
	s_waitcnt vmcnt(2)
	s_nop 0
	v_mul_f32_e32 v84, 0x42000000, v29
	v_add_u32_e32 v82, 0x1c00, v45
	s_cselect_b64 s[4:5], -1, 0
	s_nop 0
	ds_write2_b32 v82, v34, v84 offset0:56 offset1:122
	s_waitcnt vmcnt(1)
	s_nop 0
	v_mul_f32_e32 v34, 0x42000000, v30
	s_waitcnt vmcnt(0)
	s_nop 0
	v_mul_f32_e32 v84, 0x42000000, v31
	s_and_b64 vcc, exec, s[4:5]
	s_nop 0
	ds_write2_b32 v82, v34, v84 offset0:188 offset1:254
	s_cbranch_vccnz .LBB0_99
	s_cmpk_gt_i32 s46, 0xbff
	s_mov_b64 s[16:17], -1
	s_cbranch_scc0 .LBB0_96
	s_cmpk_gt_u32 s46, 0xfff
	s_cbranch_scc0 .LBB0_93
	s_cmpk_gt_u32 s46, 0x13ff
	s_cbranch_scc0 .LBB0_90
	s_cmpk_gt_u32 s46, 0x17ff
	s_cbranch_scc0 .LBB0_87
	s_cmpk_gt_u32 s46, 0x1bff
	s_cbranch_scc0 .LBB0_84
	s_cmpk_gt_u32 s46, 0x9bff
	s_mov_b64 s[10:11], -1
	s_cbranch_scc0 .LBB0_81
	s_nop 0
	v_readlane_b32 s64, v253, 50
	s_add_i32 s0, s46, 0xffff6400
	v_readlane_b32 s65, v253, 51
	v_readlane_b32 s66, v253, 52
	v_readlane_b32 s67, v253, 53
	v_readlane_b32 s68, v253, 54
	v_readlane_b32 s69, v253, 55
	v_readlane_b32 s70, v253, 56
	v_readlane_b32 s71, v253, 57
	v_readlane_b32 s72, v253, 58
	v_readlane_b32 s73, v253, 59
	s_lshr_b32 s0, s0, 8
	s_nop 0
	v_readlane_b32 s74, v253, 60
	v_readlane_b32 s75, v253, 61
	v_readlane_b32 s76, v253, 62
	v_readlane_b32 s77, v253, 63
	s_mov_b64 s[64:65], s[68:69]
	s_lshl_b64 s[10:11], s[0:1], 21
	s_mov_b64 s[66:67], s[70:71]
	s_mov_b64 s[68:69], s[72:73]
	s_mov_b64 s[70:71], s[74:75]
	s_add_u32 s12, s70, s10
	s_addc_u32 s13, s71, s11
	s_add_i32 s0, s35, s34
	s_add_i32 s10, s37, s36
	s_nop 0
	v_readlane_b32 s78, v254, 0
	v_readlane_b32 s79, v254, 1
	s_mov_b64 s[72:73], s[76:77]
	s_nop 0
	v_readlane_b32 s64, v254, 4
	s_and_b32 s0, s0, 0x1c0
	s_and_b32 s14, s10, 0x3e0
	s_mov_b64 s[10:11], 0
.LBB0_81:
	s_andn2_b64 vcc, exec, s[10:11]
	s_mov_b64 s[10:11], 0x400
	s_cbranch_vccnz .LBB0_83
	s_cmpk_gt_u32 s46, 0x5bff
	s_cselect_b64 s[10:11], -1, 0
	s_and_b64 s[12:13], s[10:11], exec
	s_cselect_b32 s0, s44, 0xffffe400
	s_add_i32 s0, s20, s0
	s_add_i32 s15, s0, s19
	v_readlane_b32 s64, v253, 50
	s_lshl_b32 s12, s15, 5
	s_nop 0
	v_readlane_b32 s65, v253, 51
	v_readlane_b32 s66, v253, 52
	v_readlane_b32 s67, v253, 53
	v_readlane_b32 s68, v253, 54
	v_readlane_b32 s69, v253, 55
	v_readlane_b32 s70, v253, 56
	v_readlane_b32 s71, v253, 57
	v_readlane_b32 s72, v253, 58
	v_readlane_b32 s73, v253, 59
	s_lshr_b32 s0, s15, 8
	s_nop 0
	s_and_b32 s14, s12, 0x1e0
	v_readlane_b32 s74, v253, 60
	v_readlane_b32 s75, v253, 61
	v_readlane_b32 s76, v253, 62
	v_readlane_b32 s77, v253, 63
	s_mov_b64 s[64:65], s[68:69]
	s_and_b64 s[10:11], s[10:11], exec
	s_mov_b64 s[66:67], s[70:71]
	s_mov_b64 s[68:69], s[72:73]
	s_cselect_b32 s13, s69, s67
	s_cselect_b32 s12, s68, s66
	s_lshl_b64 s[10:11], s[0:1], 21
	s_add_u32 s12, s12, s10
	s_addc_u32 s13, s13, s11
	s_lshl_b32 s0, s15, 2
	v_readlane_b32 s64, v254, 4
	s_and_b32 s0, s0, 0x3c0
	s_mov_b64 s[10:11], 0x200
	v_readlane_b32 s78, v254, 0
	v_readlane_b32 s79, v254, 1
	s_mov_b64 s[70:71], s[74:75]
	s_mov_b64 s[72:73], s[76:77]

.LBB0_84:
	s_andn2_b64 vcc, exec, s[16:17]
	s_cbranch_vccnz .LBB0_86
	s_nop 0
	v_readlane_b32 s68, v253, 34
	s_add_i32 s0, s46, 0xffffe800
	v_readlane_b32 s69, v253, 35
	v_readlane_b32 s70, v253, 36
	v_readlane_b32 s71, v253, 37
	v_readlane_b32 s72, v253, 38
	v_readlane_b32 s73, v253, 39
	v_readlane_b32 s74, v253, 40
	v_readlane_b32 s75, v253, 41
	v_readlane_b32 s76, v253, 42
	v_readlane_b32 s77, v253, 43
	s_lshr_b32 s0, s0, 9
	s_nop 0
	v_readlane_b32 s78, v253, 44
	v_readlane_b32 s79, v253, 45
	v_readlane_b32 s80, v253, 46
	v_readlane_b32 s81, v253, 47
	s_mov_b64 s[68:69], s[72:73]
	s_lshl_b64 s[10:11], s[0:1], 22
	s_mov_b64 s[70:71], s[74:75]
	s_mov_b64 s[72:73], s[76:77]
	s_add_u32 s12, s72, s10
	s_addc_u32 s13, s73, s11
	s_add_i32 s0, s35, s34
	s_add_i32 s10, s37, s36
	s_and_b32 s0, s0, 0x3c0
	s_and_b32 s14, s10, 0x3e0
	s_mov_b64 s[10:11], 0x400
	v_readlane_b32 s82, v253, 48
	v_readlane_b32 s83, v253, 49
	s_mov_b64 s[74:75], s[78:79]
	s_mov_b64 s[76:77], s[80:81]

.LBB0_87:
	s_andn2_b64 vcc, exec, s[16:17]
	s_cbranch_vccnz .LBB0_89
	s_nop 0
	v_readlane_b32 s68, v253, 34
	s_add_i32 s0, s46, 0xffffec00
	v_readlane_b32 s69, v253, 35
	v_readlane_b32 s70, v253, 36
	v_readlane_b32 s71, v253, 37
	v_readlane_b32 s72, v253, 38
	v_readlane_b32 s73, v253, 39
	v_readlane_b32 s74, v253, 40
	v_readlane_b32 s75, v253, 41
	v_readlane_b32 s76, v253, 42
	v_readlane_b32 s77, v253, 43
	s_lshr_b32 s0, s0, 9
	s_nop 0
	v_readlane_b32 s78, v253, 44
	v_readlane_b32 s79, v253, 45
	v_readlane_b32 s80, v253, 46
	v_readlane_b32 s81, v253, 47
	s_mov_b64 s[68:69], s[72:73]
	s_lshl_b64 s[10:11], s[0:1], 22
	s_mov_b64 s[70:71], s[74:75]
	s_add_u32 s12, s70, s10
	s_addc_u32 s13, s71, s11
	s_add_i32 s0, s35, s34
	s_add_i32 s10, s37, s36
	s_nop 0
	s_and_b32 s0, s0, 0x3c0
	s_and_b32 s14, s10, 0x3e0
	s_mov_b64 s[10:11], 0x400
	v_readlane_b32 s82, v253, 48
	v_readlane_b32 s83, v253, 49
	s_mov_b64 s[72:73], s[76:77]
	s_mov_b64 s[74:75], s[78:79]
	s_mov_b64 s[76:77], s[80:81]

.LBB0_90:
	s_nop 0
	v_readlane_b32 s68, v253, 34
	v_readlane_b32 s70, v253, 36
	v_readlane_b32 s71, v253, 37
	s_mov_b64 s[12:13], s[70:71]
	s_nop 0
	v_readlane_b32 s69, v253, 35
	v_readlane_b32 s72, v253, 38
	v_readlane_b32 s73, v253, 39
	v_readlane_b32 s74, v253, 40
	v_readlane_b32 s75, v253, 41
	v_readlane_b32 s76, v253, 42
	v_readlane_b32 s77, v253, 43
	v_readlane_b32 s78, v253, 44
	v_readlane_b32 s79, v253, 45
	v_readlane_b32 s80, v253, 46
	v_readlane_b32 s81, v253, 47
	v_readlane_b32 s82, v253, 48
	v_readlane_b32 s83, v253, 49
	s_andn2_b64 vcc, exec, s[16:17]
	s_cbranch_vccnz .LBB0_92

.LBB0_93:
	s_andn2_b64 vcc, exec, s[16:17]
	s_cbranch_vccnz .LBB0_95
	s_nop 0
	s_add_i32 s0, s46, 0xfffff400
	s_lshr_b32 s0, s0, 9
	s_nop 0
	v_readlane_b32 s68, v253, 18
	s_lshl_b64 s[10:11], s[0:1], 22
	s_nop 0
	v_readlane_b32 s78, v253, 28
	v_readlane_b32 s79, v253, 29
	s_add_u32 s12, s78, s10
	s_addc_u32 s13, s79, s11
	s_add_i32 s0, s35, s34
	s_add_i32 s10, s37, s36
	s_and_b32 s0, s0, 0x3c0
	s_and_b32 s14, s10, 0x3e0
	s_mov_b64 s[10:11], 0x400
	v_readlane_b32 s69, v253, 19
	v_readlane_b32 s70, v253, 20
	v_readlane_b32 s71, v253, 21
	v_readlane_b32 s72, v253, 22
	v_readlane_b32 s73, v253, 23
	v_readlane_b32 s74, v253, 24
	v_readlane_b32 s75, v253, 25
	v_readlane_b32 s76, v253, 26
	v_readlane_b32 s77, v253, 27
	v_readlane_b32 s80, v253, 30
	v_readlane_b32 s81, v253, 31
	v_readlane_b32 s82, v253, 32
	v_readlane_b32 s83, v253, 33

.LBB0_96:
	s_andn2_b64 vcc, exec, s[16:17]
	s_cbranch_vccnz .LBB0_98
	s_nop 0
	s_mul_hi_i32 s0, s46, 0x2aaaaaab
	s_lshr_b32 s10, s0, 31
	s_ashr_i32 s0, s0, 8
	s_add_i32 s0, s0, s10
	s_nop 0
	s_mul_i32 s10, s0, 0xfffffa00
	s_add_i32 s10, s46, s10
	s_nop 0
	s_mul_i32 s11, s10, 0x2aab
	s_lshr_b32 s12, s11, 31
	s_ashr_i32 s11, s11, 20
	s_add_i32 s11, s11, s12
	s_nop 0
	s_mul_i32 s12, s11, 0x60
	v_readlane_b32 s68, v253, 18
	s_sub_i32 s10, s10, s12
	s_nop 0
	s_mul_hi_i32 s13, s0, 0xc10000
	s_mul_i32 s0, s0, 0xc10000
	v_readlane_b32 s72, v253, 22
	s_sext_i32_i16 s10, s10
	s_nop 0
	v_readlane_b32 s73, v253, 23
	s_add_u32 s12, s72, s0
	s_addc_u32 s13, s73, s13
	s_lshl_b32 s0, s11, 6
	s_lshl_b32 s14, s10, 5
	s_mov_b64 s[10:11], 0xc10
	v_readlane_b32 s69, v253, 19
	v_readlane_b32 s70, v253, 20
	v_readlane_b32 s71, v253, 21
	v_readlane_b32 s74, v253, 24
	v_readlane_b32 s75, v253, 25
	v_readlane_b32 s76, v253, 26
	v_readlane_b32 s77, v253, 27
	v_readlane_b32 s78, v253, 28
	v_readlane_b32 s79, v253, 29
	v_readlane_b32 s80, v253, 30
	v_readlane_b32 s81, v253, 31
	v_readlane_b32 s82, v253, 32
	v_readlane_b32 s83, v253, 33
.LBB0_98:
	s_ashr_i32 s15, s14, 31
	s_lshl_b64 s[14:15], s[14:15], 2
	v_add_u32_e64 v116, s0, v33
	s_add_u32 s12, s12, s14
	s_addc_u32 s13, s13, s15
	v_lshlrev_b32_e32 v34, 2, v32
	v_ashrrev_i32_e32 v2, 31, v116
	v_lshl_add_u64 v[0:1], s[12:13], 0, v[34:35]
	v_mul_lo_u32 v4, s10, v2
	v_mul_lo_u32 v5, s11, v116
	v_mad_u64_u32 v[2:3], s[12:13], s10, v116, 0
	v_add3_u32 v3, v3, v4, v5
	v_add_u32_e32 v4, 2, v116
	v_ashrrev_i32_e32 v5, 31, v4
	v_mul_lo_u32 v6, s10, v5
	v_mul_lo_u32 v7, s11, v4
	v_mad_u64_u32 v[4:5], s[12:13], s10, v4, 0
	v_add3_u32 v5, v5, v6, v7
	v_add_u32_e32 v6, 4, v116
	v_ashrrev_i32_e32 v7, 31, v6
	v_mul_lo_u32 v8, s10, v7
	v_mul_lo_u32 v9, s11, v6
	v_mad_u64_u32 v[6:7], s[12:13], s10, v6, 0
	v_add3_u32 v7, v7, v8, v9
	v_add_u32_e32 v8, 6, v116
	v_ashrrev_i32_e32 v9, 31, v8
	v_mul_lo_u32 v10, s10, v9
	v_mul_lo_u32 v11, s11, v8
	v_mad_u64_u32 v[8:9], s[12:13], s10, v8, 0
	v_add3_u32 v9, v9, v10, v11
	v_add_u32_e32 v10, 8, v116
	v_ashrrev_i32_e32 v11, 31, v10
	v_mul_lo_u32 v12, s10, v11
	v_mul_lo_u32 v13, s11, v10
	v_mad_u64_u32 v[10:11], s[12:13], s10, v10, 0
	v_add3_u32 v11, v11, v12, v13
	v_add_u32_e32 v12, 10, v116
	v_ashrrev_i32_e32 v13, 31, v12
	v_mul_lo_u32 v14, s10, v13
	v_mul_lo_u32 v15, s11, v12
	v_mad_u64_u32 v[12:13], s[12:13], s10, v12, 0
	v_add3_u32 v13, v13, v14, v15
	v_add_u32_e32 v14, 12, v116
	v_ashrrev_i32_e32 v15, 31, v14
	v_mul_lo_u32 v16, s10, v15
	v_mul_lo_u32 v17, s11, v14
	v_mad_u64_u32 v[14:15], s[12:13], s10, v14, 0
	v_add3_u32 v15, v15, v16, v17
	v_add_u32_e32 v16, 14, v116
	v_ashrrev_i32_e32 v17, 31, v16
	v_mul_lo_u32 v18, s10, v17
	v_mul_lo_u32 v19, s11, v16
	v_mad_u64_u32 v[16:17], s[12:13], s10, v16, 0
	v_add3_u32 v17, v17, v18, v19
	v_add_u32_e32 v18, 16, v116
	v_ashrrev_i32_e32 v19, 31, v18
	v_mul_lo_u32 v20, s10, v19
	v_mul_lo_u32 v21, s11, v18
	v_mad_u64_u32 v[18:19], s[12:13], s10, v18, 0
	v_add3_u32 v19, v19, v20, v21
	v_add_u32_e32 v20, 18, v116
	v_ashrrev_i32_e32 v21, 31, v20
	v_mul_lo_u32 v22, s10, v21
	v_mul_lo_u32 v23, s11, v20
	v_mad_u64_u32 v[20:21], s[12:13], s10, v20, 0
	v_add3_u32 v21, v21, v22, v23
	v_add_u32_e32 v22, 20, v116
	v_ashrrev_i32_e32 v23, 31, v22
	v_mul_lo_u32 v24, s10, v23
	v_mul_lo_u32 v25, s11, v22
	v_mad_u64_u32 v[22:23], s[12:13], s10, v22, 0
	v_add3_u32 v23, v23, v24, v25
	v_add_u32_e32 v24, 22, v116
	v_ashrrev_i32_e32 v25, 31, v24
	v_mul_lo_u32 v26, s10, v25
	v_mul_lo_u32 v27, s11, v24
	v_mad_u64_u32 v[24:25], s[12:13], s10, v24, 0
	v_add3_u32 v25, v25, v26, v27
	v_add_u32_e32 v26, 24, v116
	v_ashrrev_i32_e32 v27, 31, v26
	v_mul_lo_u32 v28, s10, v27
	v_mul_lo_u32 v29, s11, v26
	v_mad_u64_u32 v[26:27], s[12:13], s10, v26, 0
	v_add3_u32 v27, v27, v28, v29
	v_add_u32_e32 v28, 26, v116
	v_ashrrev_i32_e32 v29, 31, v28
	v_mul_lo_u32 v30, s10, v29
	v_mul_lo_u32 v31, s11, v28
	v_mad_u64_u32 v[28:29], s[12:13], s10, v28, 0
	v_add3_u32 v29, v29, v30, v31
	v_add_u32_e32 v30, 28, v116
	v_ashrrev_i32_e32 v31, 31, v30
	v_mul_lo_u32 v34, s10, v31
	v_mul_lo_u32 v84, s11, v30
	v_mad_u64_u32 v[30:31], s[12:13], s10, v30, 0
	v_add3_u32 v31, v31, v34, v84
	v_add_u32_e32 v34, 30, v116
	v_ashrrev_i32_e32 v84, 31, v34
	v_mul_lo_u32 v86, s10, v84
	v_mul_lo_u32 v87, s11, v34
	v_mad_u64_u32 v[84:85], s[12:13], s10, v34, 0
	v_add_u32_e64 v34, 32, v116
	v_add3_u32 v85, v85, v86, v87
	v_ashrrev_i32_e32 v86, 31, v34
	s_nop 0
	v_mul_lo_u32 v88, s10, v86
	v_mul_lo_u32 v89, s11, v34
	v_mad_u64_u32 v[86:87], s[12:13], s10, v34, 0
	v_add_u32_e64 v34, 34, v116
	v_add3_u32 v87, v87, v88, v89
	v_ashrrev_i32_e32 v88, 31, v34
	s_nop 0
	v_mul_lo_u32 v90, s10, v88
	v_mul_lo_u32 v91, s11, v34
	v_mad_u64_u32 v[88:89], s[12:13], s10, v34, 0
	v_add_u32_e64 v34, 36, v116
	v_add3_u32 v89, v89, v90, v91
	v_ashrrev_i32_e32 v90, 31, v34
	s_nop 0
	v_mul_lo_u32 v92, s10, v90
	v_mul_lo_u32 v93, s11, v34
	v_mad_u64_u32 v[90:91], s[12:13], s10, v34, 0
	v_add_u32_e64 v34, 38, v116
	v_add3_u32 v91, v91, v92, v93
	v_ashrrev_i32_e32 v92, 31, v34
	s_nop 0
	v_mul_lo_u32 v94, s10, v92
	v_mul_lo_u32 v95, s11, v34
	v_mad_u64_u32 v[92:93], s[12:13], s10, v34, 0
	v_add_u32_e64 v34, 40, v116
	v_add3_u32 v93, v93, v94, v95
	v_ashrrev_i32_e32 v94, 31, v34
	s_nop 0
	v_mul_lo_u32 v96, s10, v94
	v_mul_lo_u32 v97, s11, v34
	v_mad_u64_u32 v[94:95], s[12:13], s10, v34, 0
	v_add_u32_e64 v34, 42, v116
	v_add3_u32 v95, v95, v96, v97
	v_ashrrev_i32_e32 v96, 31, v34
	s_nop 0
	v_mul_lo_u32 v98, s10, v96
	v_mul_lo_u32 v99, s11, v34
	v_mad_u64_u32 v[96:97], s[12:13], s10, v34, 0
	v_add_u32_e64 v34, 44, v116
	v_add3_u32 v97, v97, v98, v99
	v_ashrrev_i32_e32 v98, 31, v34
	s_nop 0
	v_mul_lo_u32 v100, s10, v98
	v_mul_lo_u32 v101, s11, v34
	v_mad_u64_u32 v[98:99], s[12:13], s10, v34, 0
	v_add_u32_e64 v34, 46, v116
	v_add3_u32 v99, v99, v100, v101
	v_ashrrev_i32_e32 v100, 31, v34
	s_nop 0
	v_mul_lo_u32 v102, s10, v100
	v_mul_lo_u32 v103, s11, v34
	v_mad_u64_u32 v[100:101], s[12:13], s10, v34, 0
	v_add_u32_e64 v34, 48, v116
	v_add3_u32 v101, v101, v102, v103
	v_ashrrev_i32_e32 v102, 31, v34
	s_nop 0
	v_mul_lo_u32 v104, s10, v102
	v_mul_lo_u32 v105, s11, v34
	v_mad_u64_u32 v[102:103], s[12:13], s10, v34, 0
	v_add_u32_e64 v34, 50, v116
	v_add3_u32 v103, v103, v104, v105
	v_ashrrev_i32_e32 v104, 31, v34
	s_nop 0
	v_mul_lo_u32 v106, s10, v104
	v_mul_lo_u32 v107, s11, v34
	v_mad_u64_u32 v[104:105], s[12:13], s10, v34, 0
	v_add_u32_e64 v34, 52, v116
	v_add3_u32 v105, v105, v106, v107
	v_ashrrev_i32_e32 v106, 31, v34
	s_nop 0
	v_mul_lo_u32 v108, s10, v106
	v_mul_lo_u32 v109, s11, v34
	v_mad_u64_u32 v[106:107], s[12:13], s10, v34, 0
	v_add_u32_e64 v34, 54, v116
	v_add3_u32 v107, v107, v108, v109
	v_ashrrev_i32_e32 v108, 31, v34
	s_nop 0
	v_mul_lo_u32 v110, s10, v108
	v_mul_lo_u32 v111, s11, v34
	v_mad_u64_u32 v[108:109], s[12:13], s10, v34, 0
	v_add_u32_e64 v34, 56, v116
	v_add3_u32 v109, v109, v110, v111
	v_ashrrev_i32_e32 v110, 31, v34
	s_nop 0
	v_mul_lo_u32 v112, s10, v110
	v_mul_lo_u32 v113, s11, v34
	v_mad_u64_u32 v[110:111], s[12:13], s10, v34, 0
	v_add_u32_e64 v34, 58, v116
	v_add3_u32 v111, v111, v112, v113
	v_ashrrev_i32_e32 v112, 31, v34
	s_nop 0
	v_mul_lo_u32 v114, s10, v112
	v_mul_lo_u32 v115, s11, v34
	v_mad_u64_u32 v[112:113], s[12:13], s10, v34, 0
	v_add_u32_e64 v34, 60, v116
	v_add3_u32 v113, v113, v114, v115
	v_ashrrev_i32_e32 v114, 31, v34
	s_nop 0
	v_mul_lo_u32 v117, s10, v114
	v_mul_lo_u32 v118, s11, v34
	v_mad_u64_u32 v[114:115], s[12:13], s10, v34, 0
	v_add_u32_e32 v34, 62, v116
	v_ashrrev_i32_e32 v116, 31, v34
	v_add3_u32 v115, v115, v117, v118
	v_mul_lo_u32 v118, s10, v116
	v_mul_lo_u32 v119, s11, v34
	v_mad_u64_u32 v[116:117], s[10:11], s10, v34, 0
	v_lshl_add_u64 v[2:3], v[2:3], 2, v[0:1]
	v_lshl_add_u64 v[4:5], v[4:5], 2, v[0:1]
	v_lshl_add_u64 v[6:7], v[6:7], 2, v[0:1]
	v_lshl_add_u64 v[8:9], v[8:9], 2, v[0:1]
	v_lshl_add_u64 v[10:11], v[10:11], 2, v[0:1]
	v_lshl_add_u64 v[12:13], v[12:13], 2, v[0:1]
	v_lshl_add_u64 v[14:15], v[14:15], 2, v[0:1]
	v_lshl_add_u64 v[16:17], v[16:17], 2, v[0:1]
	v_lshl_add_u64 v[18:19], v[18:19], 2, v[0:1]
	v_lshl_add_u64 v[20:21], v[20:21], 2, v[0:1]
	v_lshl_add_u64 v[22:23], v[22:23], 2, v[0:1]
	v_lshl_add_u64 v[24:25], v[24:25], 2, v[0:1]
	v_lshl_add_u64 v[26:27], v[26:27], 2, v[0:1]
	v_lshl_add_u64 v[28:29], v[28:29], 2, v[0:1]
	v_lshl_add_u64 v[30:31], v[30:31], 2, v[0:1]
	v_add3_u32 v117, v117, v118, v119
	v_lshl_add_u64 v[84:85], v[84:85], 2, v[0:1]
	v_lshl_add_u64 v[86:87], v[86:87], 2, v[0:1]
	v_lshl_add_u64 v[88:89], v[88:89], 2, v[0:1]
	v_lshl_add_u64 v[90:91], v[90:91], 2, v[0:1]
	v_lshl_add_u64 v[92:93], v[92:93], 2, v[0:1]
	v_lshl_add_u64 v[94:95], v[94:95], 2, v[0:1]
	v_lshl_add_u64 v[96:97], v[96:97], 2, v[0:1]
	v_lshl_add_u64 v[98:99], v[98:99], 2, v[0:1]
	v_lshl_add_u64 v[100:101], v[100:101], 2, v[0:1]
	v_lshl_add_u64 v[102:103], v[102:103], 2, v[0:1]
	v_lshl_add_u64 v[104:105], v[104:105], 2, v[0:1]
	v_lshl_add_u64 v[106:107], v[106:107], 2, v[0:1]
	v_lshl_add_u64 v[108:109], v[108:109], 2, v[0:1]
	v_lshl_add_u64 v[110:111], v[110:111], 2, v[0:1]
	v_lshl_add_u64 v[112:113], v[112:113], 2, v[0:1]
	v_lshl_add_u64 v[114:115], v[114:115], 2, v[0:1]
	v_lshl_add_u64 v[116:117], v[116:117], 2, v[0:1]
	global_load_dword v0, v[2:3], off
	global_load_dword v1, v[4:5], off
	s_nop 0
	s_nop 0
	global_load_dword v2, v[6:7], off
	global_load_dword v3, v[8:9], off
	global_load_dword v4, v[10:11], off
	global_load_dword v5, v[12:13], off
	s_nop 0
	s_nop 0
	global_load_dword v6, v[14:15], off
	global_load_dword v7, v[16:17], off
	global_load_dword v8, v[18:19], off
	global_load_dword v9, v[20:21], off
	global_load_dword v10, v[22:23], off
	global_load_dword v11, v[24:25], off
	global_load_dword v12, v[26:27], off
	global_load_dword v13, v[28:29], off
	global_load_dword v14, v[30:31], off
	global_load_dword v15, v[84:85], off
	global_load_dword v16, v[86:87], off
	global_load_dword v17, v[88:89], off
	global_load_dword v18, v[90:91], off
	global_load_dword v19, v[92:93], off
	global_load_dword v20, v[94:95], off
	global_load_dword v21, v[96:97], off
	global_load_dword v22, v[98:99], off
	global_load_dword v23, v[100:101], off
	global_load_dword v24, v[102:103], off
	global_load_dword v25, v[104:105], off
	global_load_dword v26, v[106:107], off
	global_load_dword v27, v[108:109], off
	global_load_dword v28, v[110:111], off
	global_load_dword v29, v[112:113], off
	global_load_dword v30, v[114:115], off
	global_load_dword v31, v[116:117], off
.LBB0_99:
	s_waitcnt lgkmcnt(0)
	s_nop 0
	ds_read2_b32 v[84:85], v41 offset1:33
	ds_read2_b32 v[88:89], v41 offset0:66 offset1:99
	v_mov_b32_e32 v90, v35
	s_ashr_i32 s0, s48, 31
	s_add_u32 s8, s8, s48
	s_waitcnt lgkmcnt(1)
	v_med3_f32 v34, v84, s45, v46
	v_med3_f32 v91, v85, s45, v46
	ds_read2_b32 v[84:85], v41 offset0:132 offset1:165
	v_cvt_pk_fp8_f32 v90, v34, v91
	s_waitcnt lgkmcnt(1)
	s_nop 0
	v_med3_f32 v34, v88, s45, v46
	v_med3_f32 v92, v89, s45, v46
	ds_read2_b32 v[88:89], v41 offset0:198 offset1:231
	s_waitcnt lgkmcnt(1)
	s_nop 0
	v_med3_f32 v84, v84, s45, v46
	v_med3_f32 v85, v85, s45, v46
	v_mov_b32_e64 v91, v35
	v_cvt_pk_fp8_f32 v91, v84, v85
	v_cvt_pk_fp8_f32 v90, v34, v92 op_sel:[0,0,1]
	s_waitcnt lgkmcnt(0)
	s_nop 0
	v_med3_f32 v34, v88, s45, v46
	v_med3_f32 v84, v89, s45, v46
	s_addc_u32 s9, s9, s0
	s_nop 0
	v_cvt_pk_fp8_f32 v91, v34, v84 op_sel:[0,0,1]
	v_add_u32_e64 v34, s47, v40
	v_lshl_add_u64 v[86:87], s[8:9], 0, v[36:37]
	v_ashrrev_i32_e32 v84, 31, v34
	s_nop 0
	v_mul_lo_u32 v88, s6, v84
	v_mad_u64_u32 v[84:85], s[8:9], s6, v34, v[86:87]
	v_mul_lo_u32 v34, s7, v34
	v_add3_u32 v85, v34, v85, v88
	global_store_dwordx2 v[84:85], v[90:91], off
	ds_read2_b32 v[84:85], v41 offset0:8 offset1:41
	ds_read2_b32 v[88:89], v41 offset0:74 offset1:107
	v_mov_b32_e32 v90, v35
	s_add_i32 s12, s18, s19
	s_cmp_gt_i32 s12, 0xdbff
	s_waitcnt lgkmcnt(1)
	s_nop 0
	v_med3_f32 v34, v84, s45, v46
	v_med3_f32 v91, v85, s45, v46
	ds_read2_b32 v[84:85], v41 offset0:140 offset1:173
	v_cvt_pk_fp8_f32 v90, v34, v91
	s_waitcnt lgkmcnt(1)
	s_nop 0
	v_med3_f32 v34, v88, s45, v46
	v_med3_f32 v92, v89, s45, v46
	ds_read2_b32 v[88:89], v41 offset0:206 offset1:239
	s_waitcnt lgkmcnt(1)
	s_nop 0
	v_med3_f32 v84, v84, s45, v46
	v_med3_f32 v85, v85, s45, v46
	v_mov_b32_e64 v91, v35
	v_cvt_pk_fp8_f32 v91, v84, v85
	v_cvt_pk_fp8_f32 v90, v34, v92 op_sel:[0,0,1]
	s_waitcnt lgkmcnt(0)
	s_nop 0
	v_med3_f32 v34, v88, s45, v46
	v_med3_f32 v84, v89, s45, v46
	v_cvt_pk_fp8_f32 v91, v34, v84 op_sel:[0,0,1]
	v_add_u32_e32 v34, s47, v42
	v_ashrrev_i32_e32 v84, 31, v34
	v_mul_lo_u32 v88, s6, v84
	v_mad_u64_u32 v[84:85], s[8:9], s6, v34, v[86:87]
	v_mul_lo_u32 v34, s7, v34
	v_add3_u32 v85, v34, v85, v88
	global_store_dwordx2 v[84:85], v[90:91], off
	ds_read2_b32 v[84:85], v41 offset0:16 offset1:49
	ds_read2_b32 v[88:89], v41 offset0:82 offset1:115
	v_mov_b32_e32 v90, v35
	s_waitcnt lgkmcnt(1)
	v_med3_f32 v34, v84, s45, v46
	v_med3_f32 v91, v85, s45, v46
	ds_read2_b32 v[84:85], v41 offset0:148 offset1:181
	v_cvt_pk_fp8_f32 v90, v34, v91
	s_waitcnt lgkmcnt(1)
	s_nop 0
	v_med3_f32 v34, v88, s45, v46
	v_med3_f32 v92, v89, s45, v46
	ds_read2_b32 v[88:89], v41 offset0:214 offset1:247
	s_waitcnt lgkmcnt(1)
	s_nop 0
	v_med3_f32 v84, v84, s45, v46
	v_med3_f32 v85, v85, s45, v46
	v_mov_b32_e64 v91, v35
	v_cvt_pk_fp8_f32 v91, v84, v85
	v_cvt_pk_fp8_f32 v90, v34, v92 op_sel:[0,0,1]
	s_waitcnt lgkmcnt(0)
	s_nop 0
	v_med3_f32 v34, v88, s45, v46
	v_med3_f32 v84, v89, s45, v46
	v_cvt_pk_fp8_f32 v91, v34, v84 op_sel:[0,0,1]
	v_add_u32_e32 v34, s47, v43
	v_ashrrev_i32_e32 v84, 31, v34
	v_mul_lo_u32 v88, s6, v84
	v_mad_u64_u32 v[84:85], s[8:9], s6, v34, v[86:87]
	v_mul_lo_u32 v34, s7, v34
	v_add3_u32 v85, v34, v85, v88
	global_store_dwordx2 v[84:85], v[90:91], off
	ds_read2_b32 v[84:85], v41 offset0:24 offset1:57
	ds_read2_b32 v[88:89], v41 offset0:90 offset1:123
	v_mov_b32_e32 v90, v35
	s_waitcnt lgkmcnt(1)
	v_med3_f32 v34, v84, s45, v46
	v_med3_f32 v91, v85, s45, v46
	ds_read2_b32 v[84:85], v41 offset0:156 offset1:189
	v_cvt_pk_fp8_f32 v90, v34, v91
	s_waitcnt lgkmcnt(1)
	s_nop 0
	v_med3_f32 v34, v88, s45, v46
	v_med3_f32 v92, v89, s45, v46
	ds_read2_b32 v[88:89], v41 offset0:222 offset1:255
	s_waitcnt lgkmcnt(1)
	s_nop 0
	v_med3_f32 v84, v84, s45, v46
	v_med3_f32 v85, v85, s45, v46
	v_mov_b32_e64 v91, v35
	v_cvt_pk_fp8_f32 v91, v84, v85
	v_cvt_pk_fp8_f32 v90, v34, v92 op_sel:[0,0,1]
	s_waitcnt lgkmcnt(0)
	s_nop 0
	v_med3_f32 v34, v88, s45, v46
	v_med3_f32 v84, v89, s45, v46
	v_cvt_pk_fp8_f32 v91, v34, v84 op_sel:[0,0,1]
	v_add_u32_e32 v34, s47, v44
	v_ashrrev_i32_e32 v84, 31, v34
	v_mul_lo_u32 v88, s6, v84
	v_mad_u64_u32 v[84:85], s[8:9], s6, v34, v[86:87]
	v_mul_lo_u32 v34, s7, v34
	v_add3_u32 v85, v34, v85, v88
	global_store_dwordx2 v[84:85], v[90:91], off
	s_waitcnt lgkmcnt(0)
	s_cbranch_scc1 .LBB0_48
	s_cmpk_gt_i32 s12, 0xbff
	s_mov_b64 s[10:11], -1
	s_cbranch_scc0 .LBB0_122
	s_cmpk_gt_u32 s12, 0xfff
	s_cbranch_scc0 .LBB0_119
	s_cmpk_gt_u32 s12, 0x13ff
	s_cbranch_scc0 .LBB0_116
	s_cmpk_gt_u32 s12, 0x17ff
	s_cbranch_scc0 .LBB0_113
	s_cmpk_gt_u32 s12, 0x1bff
	s_cbranch_scc0 .LBB0_110
	s_cmpk_gt_u32 s12, 0x9bff
	s_mov_b64 s[6:7], -1
	s_cbranch_scc0 .LBB0_107
	s_add_i32 s0, s12, 0xffff6400
	s_add_i32 s6, s20, s34
	s_lshr_b32 s0, s0, 8
	s_and_b32 s48, s6, 0x1c0
	s_add_i32 s6, s43, s36
	s_nop 0
	s_and_b32 s47, s6, 0x3e0
	s_lshl_b64 s[6:7], s[0:1], 19
	s_add_u32 s8, s21, s6
	s_addc_u32 s9, s22, s7
	s_mov_b64 s[6:7], 0
.LBB0_107:
	s_andn2_b64 vcc, exec, s[6:7]
	s_nop 0
	s_mov_b64 s[6:7], 0x200
	s_cbranch_vccnz .LBB0_109
	s_cmpk_gt_u32 s12, 0x5bff
	s_cselect_b32 s0, s44, 0xffffe400
	s_cselect_b32 s10, 0x80, 0
	s_add_i32 s0, s18, s0
	s_add_i32 s6, s0, s19
	s_lshr_b32 s0, s6, 8
	s_lshl_b32 s11, s6, 5
	s_lshl_b32 s6, s6, 2
	s_nop 0
	s_and_b32 s48, s6, 0x3c0
	s_lshl_b64 s[6:7], s[0:1], 20
	s_add_u32 s8, s23, s6
	s_addc_u32 s9, s24, s7
	s_add_i32 s0, s37, s38
	s_and_b32 s0, s0, 0x300
	s_and_b32 s6, s11, 0x60
	s_or_b32 s0, s0, s10
	s_or_b32 s47, s0, s6
	s_mov_b64 s[6:7], 0x400

.LBB0_110:
	s_andn2_b64 vcc, exec, s[10:11]
	s_cbranch_vccnz .LBB0_112
	s_nop 0
	s_add_i32 s0, s12, 0xffffe800
	s_lshr_b32 s0, s0, 9
	s_lshl_b64 s[6:7], s[0:1], 20
	s_add_i32 s0, s20, s34
	s_nop 0
	s_and_b32 s48, s0, 0x3c0
	s_add_i32 s0, s43, s36
	s_nop 0
	s_and_b32 s47, s0, 0x3e0
	s_add_u32 s8, s25, s6
	s_addc_u32 s9, s26, s7
	s_mov_b64 s[6:7], 0x400

.LBB0_113:
	s_andn2_b64 vcc, exec, s[10:11]
	s_cbranch_vccnz .LBB0_115
	s_nop 0
	s_add_i32 s0, s12, 0xffffec00
	s_lshr_b32 s0, s0, 9
	s_lshl_b64 s[6:7], s[0:1], 20
	s_add_i32 s0, s20, s34
	s_nop 0
	s_and_b32 s48, s0, 0x3c0
	s_add_i32 s0, s43, s36
	s_nop 0
	s_and_b32 s47, s0, 0x3e0
	s_add_u32 s8, s27, s6
	s_addc_u32 s9, s28, s7
	s_mov_b64 s[6:7], 0x400

.LBB0_116:
	s_andn2_b64 vcc, exec, s[10:11]
	s_cbranch_vccnz .LBB0_118
	s_nop 0
	s_and_b32 s0, s12, 0x1fc0
	s_add_i32 s48, s0, 0xfffff000
	s_add_i32 s0, s43, s36
	s_nop 0
	s_and_b32 s47, s0, 0x7e0
	s_mov_b64 s[6:7], 0x400
	s_mov_b64 s[8:9], s[2:3]

.LBB0_119:
	s_andn2_b64 vcc, exec, s[10:11]
	s_cbranch_vccnz .LBB0_121
	s_add_i32 s0, s12, 0xfffff400
	s_lshr_b32 s0, s0, 9
	s_lshl_b64 s[6:7], s[0:1], 20
	s_add_i32 s0, s20, s34
	s_nop 0
	s_and_b32 s48, s0, 0x3c0
	s_add_i32 s0, s43, s36
	s_nop 0
	s_and_b32 s47, s0, 0x3e0
	s_add_u32 s8, s29, s6
	s_addc_u32 s9, s30, s7
	s_mov_b64 s[6:7], 0x400

.LBB0_122:
	s_andn2_b64 vcc, exec, s[10:11]
	s_cbranch_vccnz .LBB0_124
	s_nop 0
	s_mul_hi_i32 s0, s12, 0x2aaaaaab
	s_lshr_b32 s6, s0, 31
	s_ashr_i32 s0, s0, 8
	s_add_i32 s0, s0, s6
	s_nop 0
	s_mul_i32 s6, s0, 0x600
	s_sub_i32 s6, s12, s6
	s_nop 0
	s_mul_i32 s7, s6, 0x2aab
	s_lshr_b32 s8, s7, 31
	s_ashr_i32 s7, s7, 20
	s_add_i32 s7, s7, s8
	s_nop 0
	s_mul_i32 s8, s7, 0x60
	s_sub_i32 s6, s6, s8
	s_sext_i32_i16 s6, s6
	s_lshl_b32 s48, s7, 6
	s_lshl_b32 s47, s6, 5
	s_mul_hi_i32 s6, s0, 0x300000
	s_mul_i32 s0, s0, 0x300000
	s_add_u32 s8, s31, s0
	s_addc_u32 s9, s33, s6
	s_mov_b64 s[6:7], 0x400
.LBB0_124:
	v_mul_f32_e32 v34, 0x42000000, v47
	v_mul_f32_e32 v84, 0x42000000, v48
	ds_write2_b32 v45, v34, v84 offset1:66
	v_mul_f32_e32 v34, 0x42000000, v49
	v_mul_f32_e32 v84, 0x42000000, v50
	ds_write2_b32 v45, v34, v84 offset0:132 offset1:198
	v_mul_f32_e32 v34, 0x42000000, v52
	v_mul_f32_e32 v84, 0x42000000, v53
	ds_write2_b32 v51, v34, v84 offset0:8 offset1:74
	v_mul_f32_e32 v34, 0x42000000, v54
	v_mul_f32_e32 v84, 0x42000000, v55
	ds_write2_b32 v51, v34, v84 offset0:140 offset1:206
	v_mul_f32_e32 v34, 0x42000000, v56
	v_mul_f32_e32 v51, 0x42000000, v57
	ds_write2_b32 v78, v34, v51 offset0:16 offset1:82
	v_mul_f32_e32 v34, 0x42000000, v58
	v_mul_f32_e32 v51, 0x42000000, v59
	ds_write2_b32 v78, v34, v51 offset0:148 offset1:214
	v_mul_f32_e32 v34, 0x42000000, v60
	v_mul_f32_e32 v51, 0x42000000, v61
	ds_write2_b32 v79, v34, v51 offset0:24 offset1:90
	v_mul_f32_e32 v34, 0x42000000, v62
	v_mul_f32_e32 v51, 0x42000000, v63
	ds_write2_b32 v79, v34, v51 offset0:156 offset1:222
	v_mul_f32_e32 v34, 0x42000000, v64
	v_mul_f32_e32 v51, 0x42000000, v65
	ds_write2_b32 v80, v34, v51 offset0:32 offset1:98
	v_mul_f32_e32 v34, 0x42000000, v66
	v_mul_f32_e32 v51, 0x42000000, v67
	ds_write2_b32 v80, v34, v51 offset0:164 offset1:230
	v_mul_f32_e32 v34, 0x42000000, v68
	v_mul_f32_e32 v51, 0x42000000, v69
	ds_write2_b32 v81, v34, v51 offset0:40 offset1:106
	v_mul_f32_e32 v34, 0x42000000, v70
	v_mul_f32_e32 v51, 0x42000000, v71
	ds_write2_b32 v81, v34, v51 offset0:172 offset1:238
	v_mul_f32_e32 v34, 0x42000000, v74
	v_mul_f32_e32 v51, 0x42000000, v75
	ds_write2_b32 v83, v34, v51 offset0:48 offset1:114
	v_mul_f32_e32 v34, 0x42000000, v76
	v_mul_f32_e32 v51, 0x42000000, v77
	s_add_i32 s15, s40, s19
	s_nop 0
	ds_write2_b32 v83, v34, v51 offset0:180 offset1:246
	v_mul_f32_e32 v34, 0x42000000, v38
	v_mul_f32_e32 v51, 0x42000000, v39
	ds_write2_b32 v82, v34, v51 offset0:56 offset1:122
	v_mul_f32_e32 v34, 0x42000000, v72
	v_mul_f32_e32 v51, 0x42000000, v73
	s_cmp_gt_i32 s15, 0xdbff
	ds_write2_b32 v82, v34, v51 offset0:188 offset1:254
	s_cbranch_scc1 .LBB0_47
	s_cmpk_gt_i32 s15, 0xbff
	s_mov_b64 s[16:17], -1
	s_cbranch_scc0 .LBB0_147
	s_cmpk_gt_u32 s15, 0xfff
	s_cbranch_scc0 .LBB0_144
	s_cmpk_gt_u32 s15, 0x13ff
	s_cbranch_scc0 .LBB0_141
	s_cmpk_gt_u32 s15, 0x17ff
	s_cbranch_scc0 .LBB0_138
	s_cmpk_gt_u32 s15, 0x1bff
	s_cbranch_scc0 .LBB0_135
	s_cmpk_gt_u32 s15, 0x9bff
	s_mov_b64 s[10:11], -1
	s_cbranch_scc0 .LBB0_132
	s_nop 0
	v_readlane_b32 s64, v253, 50
	s_add_i32 s0, s15, 0xffff6400
	v_readlane_b32 s65, v253, 51
	v_readlane_b32 s66, v253, 52
	v_readlane_b32 s67, v253, 53
	v_readlane_b32 s68, v253, 54
	v_readlane_b32 s69, v253, 55
	v_readlane_b32 s70, v253, 56
	v_readlane_b32 s71, v253, 57
	v_readlane_b32 s72, v253, 58
	v_readlane_b32 s73, v253, 59
	s_lshr_b32 s0, s0, 8
	s_nop 0
	v_readlane_b32 s74, v253, 60
	v_readlane_b32 s75, v253, 61
	v_readlane_b32 s76, v253, 62
	v_readlane_b32 s77, v253, 63
	s_mov_b64 s[64:65], s[68:69]
	s_lshl_b64 s[10:11], s[0:1], 21
	s_mov_b64 s[66:67], s[70:71]
	s_mov_b64 s[68:69], s[72:73]
	s_mov_b64 s[70:71], s[74:75]
	s_add_u32 s12, s70, s10
	s_addc_u32 s13, s71, s11
	s_add_i32 s0, s42, s34
	s_add_i32 s10, s41, s36
	s_nop 0
	v_readlane_b32 s78, v254, 0
	v_readlane_b32 s79, v254, 1
	s_mov_b64 s[72:73], s[76:77]
	s_nop 0
	v_readlane_b32 s64, v254, 4
	s_and_b32 s0, s0, 0x1c0
	s_and_b32 s14, s10, 0x3e0
	s_mov_b64 s[10:11], 0
.LBB0_132:
	s_andn2_b64 vcc, exec, s[10:11]
	s_mov_b64 s[10:11], 0x400
	s_cbranch_vccnz .LBB0_134
	s_cmpk_gt_u32 s15, 0x5bff
	s_cselect_b64 s[10:11], -1, 0
	s_and_b64 s[12:13], s[10:11], exec
	s_cselect_b32 s0, s44, 0xffffe400
	s_add_i32 s0, s40, s0
	s_add_i32 s16, s0, s19
	v_readlane_b32 s64, v253, 50
	s_lshl_b32 s12, s16, 5
	s_nop 0
	v_readlane_b32 s65, v253, 51
	v_readlane_b32 s66, v253, 52
	v_readlane_b32 s67, v253, 53
	v_readlane_b32 s68, v253, 54
	v_readlane_b32 s69, v253, 55
	v_readlane_b32 s70, v253, 56
	v_readlane_b32 s71, v253, 57
	v_readlane_b32 s72, v253, 58
	v_readlane_b32 s73, v253, 59
	s_lshr_b32 s0, s16, 8
	s_nop 0
	s_and_b32 s14, s12, 0x1e0
	v_readlane_b32 s74, v253, 60
	v_readlane_b32 s75, v253, 61
	v_readlane_b32 s76, v253, 62
	v_readlane_b32 s77, v253, 63
	s_mov_b64 s[64:65], s[68:69]
	s_and_b64 s[10:11], s[10:11], exec
	s_mov_b64 s[66:67], s[70:71]
	s_mov_b64 s[68:69], s[72:73]
	s_cselect_b32 s13, s69, s67
	s_cselect_b32 s12, s68, s66
	s_lshl_b64 s[10:11], s[0:1], 21
	s_add_u32 s12, s12, s10
	s_addc_u32 s13, s13, s11
	s_lshl_b32 s0, s16, 2
	v_readlane_b32 s64, v254, 4
	s_and_b32 s0, s0, 0x3c0
	s_mov_b64 s[10:11], 0x200
	v_readlane_b32 s78, v254, 0
	v_readlane_b32 s79, v254, 1
	s_mov_b64 s[70:71], s[74:75]
	s_mov_b64 s[72:73], s[76:77]

.LBB0_135:
	s_andn2_b64 vcc, exec, s[16:17]
	s_cbranch_vccnz .LBB0_137
	s_nop 0
	v_readlane_b32 s68, v253, 34
	s_add_i32 s0, s15, 0xffffe800
	v_readlane_b32 s69, v253, 35
	v_readlane_b32 s70, v253, 36
	v_readlane_b32 s71, v253, 37
	v_readlane_b32 s72, v253, 38
	v_readlane_b32 s73, v253, 39
	v_readlane_b32 s74, v253, 40
	v_readlane_b32 s75, v253, 41
	v_readlane_b32 s76, v253, 42
	v_readlane_b32 s77, v253, 43
	s_lshr_b32 s0, s0, 9
	s_nop 0
	v_readlane_b32 s78, v253, 44
	v_readlane_b32 s79, v253, 45
	v_readlane_b32 s80, v253, 46
	v_readlane_b32 s81, v253, 47
	s_mov_b64 s[68:69], s[72:73]
	s_lshl_b64 s[10:11], s[0:1], 22
	s_mov_b64 s[70:71], s[74:75]
	s_mov_b64 s[72:73], s[76:77]
	s_add_u32 s12, s72, s10
	s_addc_u32 s13, s73, s11
	s_add_i32 s0, s42, s34
	s_add_i32 s10, s41, s36
	s_and_b32 s0, s0, 0x3c0
	s_and_b32 s14, s10, 0x3e0
	s_mov_b64 s[10:11], 0x400
	v_readlane_b32 s82, v253, 48
	v_readlane_b32 s83, v253, 49
	s_mov_b64 s[74:75], s[78:79]
	s_mov_b64 s[76:77], s[80:81]

.LBB0_138:
	s_andn2_b64 vcc, exec, s[16:17]
	s_cbranch_vccnz .LBB0_140
	s_nop 0
	v_readlane_b32 s68, v253, 34
	s_add_i32 s0, s15, 0xffffec00
	v_readlane_b32 s69, v253, 35
	v_readlane_b32 s70, v253, 36
	v_readlane_b32 s71, v253, 37
	v_readlane_b32 s72, v253, 38
	v_readlane_b32 s73, v253, 39
	v_readlane_b32 s74, v253, 40
	v_readlane_b32 s75, v253, 41
	v_readlane_b32 s76, v253, 42
	v_readlane_b32 s77, v253, 43
	s_lshr_b32 s0, s0, 9
	s_nop 0
	v_readlane_b32 s78, v253, 44
	v_readlane_b32 s79, v253, 45
	v_readlane_b32 s80, v253, 46
	v_readlane_b32 s81, v253, 47
	s_mov_b64 s[68:69], s[72:73]
	s_lshl_b64 s[10:11], s[0:1], 22
	s_mov_b64 s[70:71], s[74:75]
	s_add_u32 s12, s70, s10
	s_addc_u32 s13, s71, s11
	s_add_i32 s0, s42, s34
	s_add_i32 s10, s41, s36
	s_nop 0
	s_and_b32 s0, s0, 0x3c0
	s_and_b32 s14, s10, 0x3e0
	s_mov_b64 s[10:11], 0x400
	v_readlane_b32 s82, v253, 48
	v_readlane_b32 s83, v253, 49
	s_mov_b64 s[72:73], s[76:77]
	s_mov_b64 s[74:75], s[78:79]
	s_mov_b64 s[76:77], s[80:81]

.LBB0_144:
	s_andn2_b64 vcc, exec, s[16:17]
	s_cbranch_vccnz .LBB0_146
	s_nop 0
	s_add_i32 s0, s15, 0xfffff400
	s_lshr_b32 s0, s0, 9
	s_nop 0
	v_readlane_b32 s68, v253, 18
	s_lshl_b64 s[10:11], s[0:1], 22
	s_nop 0
	v_readlane_b32 s78, v253, 28
	v_readlane_b32 s79, v253, 29
	s_add_u32 s12, s78, s10
	s_addc_u32 s13, s79, s11
	s_add_i32 s0, s42, s34
	s_add_i32 s10, s41, s36
	s_and_b32 s0, s0, 0x3c0
	s_and_b32 s14, s10, 0x3e0
	s_mov_b64 s[10:11], 0x400
	v_readlane_b32 s69, v253, 19
	v_readlane_b32 s70, v253, 20
	v_readlane_b32 s71, v253, 21
	v_readlane_b32 s72, v253, 22
	v_readlane_b32 s73, v253, 23
	v_readlane_b32 s74, v253, 24
	v_readlane_b32 s75, v253, 25
	v_readlane_b32 s76, v253, 26
	v_readlane_b32 s77, v253, 27
	v_readlane_b32 s80, v253, 30
	v_readlane_b32 s81, v253, 31
	v_readlane_b32 s82, v253, 32
	v_readlane_b32 s83, v253, 33

.LBB0_147:
	s_andn2_b64 vcc, exec, s[16:17]
	s_cbranch_vccnz .LBB0_46
	s_nop 0
	s_mul_hi_i32 s0, s15, 0x2aaaaaab
	s_lshr_b32 s10, s0, 31
	s_ashr_i32 s0, s0, 8
	s_add_i32 s0, s0, s10
	s_nop 0
	s_mul_i32 s10, s0, 0x600
	s_sub_i32 s10, s15, s10
	s_nop 0
	s_mul_i32 s11, s10, 0x2aab
	s_lshr_b32 s12, s11, 31
	s_ashr_i32 s11, s11, 20
	s_add_i32 s11, s11, s12
	s_nop 0
	s_mul_i32 s12, s11, 0x60
	v_readlane_b32 s68, v253, 18
	s_sub_i32 s10, s10, s12
	s_nop 0
	s_mul_hi_i32 s13, s0, 0xc10000
	s_mul_i32 s0, s0, 0xc10000
	v_readlane_b32 s72, v253, 22
	s_sext_i32_i16 s10, s10
	s_nop 0
	v_readlane_b32 s73, v253, 23
	s_add_u32 s12, s72, s0
	s_addc_u32 s13, s73, s13
	s_lshl_b32 s0, s11, 6
	s_lshl_b32 s14, s10, 5
	s_mov_b64 s[10:11], 0xc10
	v_readlane_b32 s69, v253, 19
	v_readlane_b32 s70, v253, 20
	v_readlane_b32 s71, v253, 21
	v_readlane_b32 s74, v253, 24
	v_readlane_b32 s75, v253, 25
	v_readlane_b32 s76, v253, 26
	v_readlane_b32 s77, v253, 27
	v_readlane_b32 s78, v253, 28
	v_readlane_b32 s79, v253, 29
	v_readlane_b32 s80, v253, 30
	v_readlane_b32 s81, v253, 31
	v_readlane_b32 s82, v253, 32
	v_readlane_b32 s83, v253, 33
	s_branch .LBB0_46
.LBB0_149:
	s_nop 0
	v_readlane_b32 s36, v254, 5
	v_readlane_b32 s37, v254, 6
	s_mov_b32 s93, s49
	s_cmp_lt_i32 s37, 2
	s_cbranch_scc1 .LBB0_247
	s_branch .LBB0_202

.LBB0_156:
	s_andn2_b64 vcc, exec, s[6:7]
	s_nop 0
	s_mov_b64 s[6:7], 0x400
	s_cbranch_vccnz .LBB0_158
	s_cmpk_gt_u32 s19, 0x5bff
	s_cselect_b64 s[2:3], -1, 0
	s_movk_i32 s6, 0xa400
	s_and_b64 s[4:5], s[2:3], exec
	s_nop 0
	s_cselect_b32 s4, s6, 0xffffe400
	s_add_i32 s5, s4, s19
	s_lshl_b32 s4, s5, 5
	s_lshr_b32 s6, s5, 8
	s_nop 0
	s_and_b32 s4, s4, 0x1e0
	v_readlane_b32 s36, v253, 50
	s_and_b64 s[2:3], s[2:3], exec
	s_nop 0
	v_readlane_b32 s42, v253, 56
	v_readlane_b32 s43, v253, 57
	v_readlane_b32 s44, v253, 58
	v_readlane_b32 s45, v253, 59
	s_mov_b32 s7, 0
	s_cselect_b32 s8, s45, s43
	s_cselect_b32 s9, s44, s42
	s_lshl_b64 s[2:3], s[6:7], 21
	v_readlane_b32 s37, v253, 51
	s_add_u32 s2, s9, s2
	s_nop 0
	v_readlane_b32 s36, v254, 5
	s_addc_u32 s3, s8, s3
	s_lshl_b32 s5, s5, 2
	v_readlane_b32 s37, v254, 6
	s_and_b32 s5, s5, 0x3c0
	s_mov_b64 s[6:7], 0x200
	v_readlane_b32 s38, v253, 52
	v_readlane_b32 s39, v253, 53
	v_readlane_b32 s40, v253, 54
	v_readlane_b32 s41, v253, 55
	v_readlane_b32 s46, v253, 60
	v_readlane_b32 s47, v253, 61
	v_readlane_b32 s48, v253, 62
	v_readlane_b32 s49, v253, 63
	v_readlane_b32 s50, v254, 0
	v_readlane_b32 s51, v254, 1
.LBB0_158:
	s_mov_b64 s[8:9], 0
	s_nop 0
	v_readlane_b32 s93, v254, 7
.LBB0_159:
	s_andn2_b64 vcc, exec, s[8:9]
	s_cbranch_vccnz .LBB0_161
	v_readlane_b32 s40, v253, 34
	s_add_i32 s2, s19, 0xffffe800
	v_readlane_b32 s44, v253, 38
	v_readlane_b32 s45, v253, 39
	s_lshr_b32 s2, s2, 9
	s_mov_b32 s3, 0
	v_readlane_b32 s46, v253, 40
	v_readlane_b32 s47, v253, 41
	v_readlane_b32 s48, v253, 42
	v_readlane_b32 s49, v253, 43
	v_readlane_b32 s50, v253, 44
	v_readlane_b32 s51, v253, 45
	v_readlane_b32 s52, v253, 46
	v_readlane_b32 s53, v253, 47
	s_mov_b64 s[8:9], s[44:45]
	s_lshl_b64 s[2:3], s[2:3], 22
	s_mov_b64 s[12:13], s[48:49]
	s_add_u32 s2, s12, s2
	s_addc_u32 s3, s13, s3
	s_lshl_b32 s4, s19, 1
	s_and_b32 s5, s4, 0x3c0
	s_lshl_b32 s4, s19, 5
	s_nop 0
	s_and_b32 s4, s4, 0x3e0
	s_mov_b64 s[6:7], 0x400
	v_readlane_b32 s41, v253, 35
	v_readlane_b32 s42, v253, 36
	v_readlane_b32 s43, v253, 37
	v_readlane_b32 s54, v253, 48
	v_readlane_b32 s55, v253, 49
	s_mov_b64 s[10:11], s[46:47]
	s_mov_b64 s[14:15], s[50:51]
	s_mov_b64 s[16:17], s[52:53]

.LBB0_162:
	s_andn2_b64 vcc, exec, s[8:9]
	s_cbranch_vccnz .LBB0_164
	v_readlane_b32 s40, v253, 34
	s_add_i32 s2, s19, 0xffffec00
	v_readlane_b32 s44, v253, 38
	v_readlane_b32 s45, v253, 39
	s_lshr_b32 s2, s2, 9
	s_mov_b32 s3, 0
	v_readlane_b32 s46, v253, 40
	v_readlane_b32 s47, v253, 41
	v_readlane_b32 s48, v253, 42
	v_readlane_b32 s49, v253, 43
	v_readlane_b32 s50, v253, 44
	v_readlane_b32 s51, v253, 45
	v_readlane_b32 s52, v253, 46
	v_readlane_b32 s53, v253, 47
	s_mov_b64 s[8:9], s[44:45]
	s_lshl_b64 s[2:3], s[2:3], 22
	s_mov_b64 s[10:11], s[46:47]
	s_add_u32 s2, s10, s2
	s_addc_u32 s3, s11, s3
	s_lshl_b32 s4, s19, 1
	s_and_b32 s5, s4, 0x3c0
	s_lshl_b32 s4, s19, 5
	s_nop 0
	s_and_b32 s4, s4, 0x3e0
	s_mov_b64 s[6:7], 0x400
	v_readlane_b32 s41, v253, 35
	v_readlane_b32 s42, v253, 36
	v_readlane_b32 s43, v253, 37
	v_readlane_b32 s54, v253, 48
	v_readlane_b32 s55, v253, 49
	s_mov_b64 s[12:13], s[48:49]
	s_mov_b64 s[14:15], s[50:51]
	s_mov_b64 s[16:17], s[52:53]

.LBB0_165:
	s_andn2_b64 vcc, exec, s[8:9]
	s_cbranch_vccnz .LBB0_167
	s_and_b32 s4, s19, 0x1fc0
	s_add_i32 s5, s4, 0xfffff000
	s_lshl_b32 s4, s19, 5
	s_nop 0
	s_and_b32 s4, s4, 0x7e0
	s_mov_b64 s[6:7], 0x810

.LBB0_168:
	s_nop 0
	v_readlane_b32 s68, v253, 18
	s_add_i32 s2, s19, 0xfffff400
	v_readlane_b32 s72, v253, 22
	v_readlane_b32 s73, v253, 23
	s_lshr_b32 s2, s2, 9
	s_mov_b32 s3, 0
	v_readlane_b32 s74, v253, 24
	v_readlane_b32 s75, v253, 25
	v_readlane_b32 s76, v253, 26
	v_readlane_b32 s77, v253, 27
	v_readlane_b32 s78, v253, 28
	v_readlane_b32 s79, v253, 29
	v_readlane_b32 s80, v253, 30
	v_readlane_b32 s81, v253, 31
	s_mov_b64 s[8:9], s[72:73]
	s_lshl_b64 s[2:3], s[2:3], 22
	s_mov_b64 s[14:15], s[78:79]
	s_add_u32 s2, s14, s2
	s_addc_u32 s3, s15, s3
	s_lshl_b32 s4, s19, 1
	s_and_b32 s5, s4, 0x3c0
	s_lshl_b32 s4, s19, 5
	s_nop 0
	s_and_b32 s4, s4, 0x3e0
	s_mov_b64 s[6:7], 0x400
	v_readlane_b32 s69, v253, 19
	v_readlane_b32 s70, v253, 20
	v_readlane_b32 s71, v253, 21
	v_readlane_b32 s82, v253, 32
	v_readlane_b32 s83, v253, 33
	s_mov_b64 s[10:11], s[74:75]
	s_mov_b64 s[12:13], s[76:77]
	s_mov_b64 s[16:17], s[80:81]

.LBB0_170:
	s_mul_hi_i32 s2, s19, 0x2aaaaaab
	s_lshr_b32 s3, s2, 31
	s_ashr_i32 s2, s2, 8
	s_add_i32 s2, s2, s3
	s_nop 0
	s_mul_i32 s3, s2, 0x600
	s_sub_i32 s3, s19, s3
	s_nop 0
	s_mul_i32 s4, s3, 0x2aab
	s_lshr_b32 s5, s4, 31
	s_ashr_i32 s4, s4, 20
	s_add_i32 s4, s4, s5
	s_nop 0
	s_mul_i32 s5, s4, 0x60
	v_readlane_b32 s68, v253, 18
	s_sub_i32 s3, s3, s5
	s_nop 0
	v_readlane_b32 s72, v253, 22
	v_readlane_b32 s73, v253, 23
	s_sext_i32_i16 s6, s3
	s_nop 0
	s_mul_hi_i32 s3, s2, 0xc10000
	s_mul_i32 s2, s2, 0xc10000
	v_readlane_b32 s74, v253, 24
	v_readlane_b32 s75, v253, 25
	v_readlane_b32 s76, v253, 26
	v_readlane_b32 s77, v253, 27
	v_readlane_b32 s78, v253, 28
	v_readlane_b32 s79, v253, 29
	v_readlane_b32 s80, v253, 30
	v_readlane_b32 s81, v253, 31
	s_mov_b64 s[20:21], s[72:73]
	s_add_u32 s2, s20, s2
	s_addc_u32 s3, s21, s3
	s_lshl_b32 s5, s4, 6
	s_lshl_b32 s4, s6, 5
	s_nop 0
	s_mov_b64 s[6:7], 0xc10
	v_readlane_b32 s69, v253, 19
	v_readlane_b32 s70, v253, 20
	v_readlane_b32 s71, v253, 21
	v_readlane_b32 s82, v253, 32
	v_readlane_b32 s83, v253, 33
	s_mov_b64 s[22:23], s[74:75]
	s_mov_b64 s[24:25], s[76:77]
	s_mov_b64 s[26:27], s[78:79]
	s_mov_b64 s[28:29], s[80:81]
.LBB0_171:
	v_lshrrev_b32_e32 v0, 5, v34
	v_add_u32_e32 v35, s5, v0
	v_ashrrev_i32_e32 v0, 31, v35
	s_nop 0
	v_mul_lo_u32 v2, s6, v0
	v_mul_lo_u32 v3, s7, v35
	v_mad_u64_u32 v[0:1], s[8:9], s6, v35, 0
	v_add3_u32 v1, v1, v2, v3
	v_add_u32_e32 v2, 2, v35
	v_ashrrev_i32_e32 v3, 31, v2
	v_mul_lo_u32 v4, s6, v3
	v_mul_lo_u32 v5, s7, v2
	v_mad_u64_u32 v[2:3], s[8:9], s6, v2, 0
	v_add3_u32 v3, v3, v4, v5
	v_add_u32_e32 v4, 4, v35
	v_ashrrev_i32_e32 v5, 31, v4
	v_mul_lo_u32 v6, s6, v5
	v_mul_lo_u32 v7, s7, v4
	v_mad_u64_u32 v[4:5], s[8:9], s6, v4, 0
	v_add3_u32 v5, v5, v6, v7
	v_add_u32_e32 v6, 6, v35
	v_ashrrev_i32_e32 v7, 31, v6
	v_mul_lo_u32 v8, s6, v7
	v_mul_lo_u32 v9, s7, v6
	v_mad_u64_u32 v[6:7], s[8:9], s6, v6, 0
	v_add3_u32 v7, v7, v8, v9
	v_add_u32_e32 v8, 8, v35
	v_ashrrev_i32_e32 v9, 31, v8
	v_mul_lo_u32 v10, s6, v9
	v_mul_lo_u32 v11, s7, v8
	v_mad_u64_u32 v[8:9], s[8:9], s6, v8, 0
	v_add3_u32 v9, v9, v10, v11
	v_add_u32_e32 v10, 10, v35
	v_ashrrev_i32_e32 v11, 31, v10
	v_mul_lo_u32 v12, s6, v11
	v_mul_lo_u32 v13, s7, v10
	v_mad_u64_u32 v[10:11], s[8:9], s6, v10, 0
	v_add3_u32 v11, v11, v12, v13
	v_add_u32_e32 v12, 12, v35
	v_ashrrev_i32_e32 v13, 31, v12
	v_mul_lo_u32 v14, s6, v13
	v_mul_lo_u32 v15, s7, v12
	v_mad_u64_u32 v[12:13], s[8:9], s6, v12, 0
	v_add3_u32 v13, v13, v14, v15
	v_add_u32_e32 v14, 14, v35
	v_ashrrev_i32_e32 v15, 31, v14
	v_mul_lo_u32 v16, s6, v15
	v_mul_lo_u32 v17, s7, v14
	v_mad_u64_u32 v[14:15], s[8:9], s6, v14, 0
	v_add3_u32 v15, v15, v16, v17
	v_add_u32_e32 v16, 16, v35
	v_ashrrev_i32_e32 v17, 31, v16
	v_mul_lo_u32 v18, s6, v17
	v_mul_lo_u32 v19, s7, v16
	v_mad_u64_u32 v[16:17], s[8:9], s6, v16, 0
	v_add3_u32 v17, v17, v18, v19
	v_add_u32_e32 v18, 18, v35
	v_ashrrev_i32_e32 v19, 31, v18
	v_mul_lo_u32 v20, s6, v19
	v_mul_lo_u32 v21, s7, v18
	v_mad_u64_u32 v[18:19], s[8:9], s6, v18, 0
	v_add3_u32 v19, v19, v20, v21
	v_add_u32_e32 v20, 20, v35
	v_ashrrev_i32_e32 v21, 31, v20
	v_mul_lo_u32 v22, s6, v21
	v_mul_lo_u32 v23, s7, v20
	v_mad_u64_u32 v[20:21], s[8:9], s6, v20, 0
	v_add3_u32 v21, v21, v22, v23
	v_add_u32_e32 v22, 22, v35
	v_ashrrev_i32_e32 v23, 31, v22
	v_mul_lo_u32 v24, s6, v23
	v_mul_lo_u32 v25, s7, v22
	v_mad_u64_u32 v[22:23], s[8:9], s6, v22, 0
	v_add3_u32 v23, v23, v24, v25
	v_add_u32_e32 v24, 24, v35
	v_ashrrev_i32_e32 v25, 31, v24
	v_mul_lo_u32 v26, s6, v25
	v_mul_lo_u32 v27, s7, v24
	v_mad_u64_u32 v[24:25], s[8:9], s6, v24, 0
	v_add3_u32 v25, v25, v26, v27
	v_add_u32_e32 v26, 26, v35
	v_ashrrev_i32_e32 v27, 31, v26
	v_mul_lo_u32 v28, s6, v27
	v_mul_lo_u32 v29, s7, v26
	v_mad_u64_u32 v[26:27], s[8:9], s6, v26, 0
	v_add3_u32 v27, v27, v28, v29
	v_add_u32_e32 v28, 28, v35
	v_ashrrev_i32_e32 v29, 31, v28
	v_mul_lo_u32 v30, s6, v29
	v_mul_lo_u32 v31, s7, v28
	v_mad_u64_u32 v[28:29], s[8:9], s6, v28, 0
	v_add3_u32 v29, v29, v30, v31
	v_add_u32_e32 v30, 30, v35
	v_ashrrev_i32_e32 v31, 31, v30
	v_mul_lo_u32 v32, s6, v31
	v_mul_lo_u32 v33, s7, v30
	v_mad_u64_u32 v[30:31], s[8:9], s6, v30, 0
	v_add3_u32 v31, v31, v32, v33
	v_add_u32_e32 v32, 32, v35
	v_ashrrev_i32_e32 v33, 31, v32
	v_mul_lo_u32 v36, s6, v33
	v_mul_lo_u32 v37, s7, v32
	v_mad_u64_u32 v[32:33], s[8:9], s6, v32, 0
	v_add3_u32 v33, v33, v36, v37
	v_add_u32_e32 v36, 34, v35
	v_ashrrev_i32_e32 v37, 31, v36
	v_mul_lo_u32 v38, s6, v37
	v_mul_lo_u32 v39, s7, v36
	v_mad_u64_u32 v[36:37], s[8:9], s6, v36, 0
	v_add3_u32 v37, v37, v38, v39
	v_add_u32_e32 v38, 36, v35
	v_ashrrev_i32_e32 v39, 31, v38
	v_mul_lo_u32 v40, s6, v39
	v_mul_lo_u32 v41, s7, v38
	v_mad_u64_u32 v[38:39], s[8:9], s6, v38, 0
	v_add3_u32 v39, v39, v40, v41
	v_add_u32_e32 v40, 38, v35
	v_ashrrev_i32_e32 v41, 31, v40
	v_mul_lo_u32 v42, s6, v41
	v_mul_lo_u32 v43, s7, v40
	v_mad_u64_u32 v[40:41], s[8:9], s6, v40, 0
	v_add3_u32 v41, v41, v42, v43
	v_add_u32_e32 v42, 40, v35
	v_ashrrev_i32_e32 v43, 31, v42
	v_mul_lo_u32 v44, s6, v43
	v_mul_lo_u32 v45, s7, v42
	v_mad_u64_u32 v[42:43], s[8:9], s6, v42, 0
	v_add3_u32 v43, v43, v44, v45
	v_add_u32_e32 v44, 42, v35
	v_ashrrev_i32_e32 v45, 31, v44
	v_mul_lo_u32 v46, s6, v45
	v_mul_lo_u32 v47, s7, v44
	v_mad_u64_u32 v[44:45], s[8:9], s6, v44, 0
	v_add3_u32 v45, v45, v46, v47
	v_add_u32_e32 v46, 44, v35
	v_ashrrev_i32_e32 v47, 31, v46
	v_mul_lo_u32 v48, s6, v47
	v_mul_lo_u32 v49, s7, v46
	v_mad_u64_u32 v[46:47], s[8:9], s6, v46, 0
	v_add3_u32 v47, v47, v48, v49
	v_add_u32_e32 v48, 46, v35
	v_ashrrev_i32_e32 v49, 31, v48
	v_mul_lo_u32 v50, s6, v49
	v_mul_lo_u32 v52, s7, v48
	v_mad_u64_u32 v[48:49], s[8:9], s6, v48, 0
	v_add3_u32 v49, v49, v50, v52
	v_add_u32_e32 v50, 48, v35
	v_ashrrev_i32_e32 v52, 31, v50
	v_mul_lo_u32 v54, s6, v52
	v_mul_lo_u32 v55, s7, v50
	v_mad_u64_u32 v[52:53], s[8:9], s6, v50, 0
	v_add_u32_e64 v50, 50, v35
	v_add3_u32 v53, v53, v54, v55
	v_ashrrev_i32_e32 v54, 31, v50
	s_nop 0
	v_mul_lo_u32 v56, s6, v54
	v_mul_lo_u32 v57, s7, v50
	v_mad_u64_u32 v[54:55], s[8:9], s6, v50, 0
	v_add_u32_e64 v50, 52, v35
	v_add3_u32 v55, v55, v56, v57
	v_ashrrev_i32_e32 v56, 31, v50
	s_nop 0
	v_mul_lo_u32 v58, s6, v56
	v_mul_lo_u32 v59, s7, v50
	v_mad_u64_u32 v[56:57], s[8:9], s6, v50, 0
	v_add_u32_e64 v50, 54, v35
	v_add3_u32 v57, v57, v58, v59
	v_ashrrev_i32_e32 v58, 31, v50
	s_nop 0
	v_mul_lo_u32 v60, s6, v58
	v_mul_lo_u32 v61, s7, v50
	v_mad_u64_u32 v[58:59], s[8:9], s6, v50, 0
	v_add_u32_e64 v50, 56, v35
	v_add3_u32 v59, v59, v60, v61
	v_ashrrev_i32_e32 v60, 31, v50
	s_nop 0
	v_mul_lo_u32 v62, s6, v60
	v_mul_lo_u32 v63, s7, v50
	v_mad_u64_u32 v[60:61], s[8:9], s6, v50, 0
	v_add_u32_e64 v50, 58, v35
	v_add3_u32 v61, v61, v62, v63
	v_ashrrev_i32_e32 v62, 31, v50
	s_nop 0
	v_mul_lo_u32 v64, s6, v62
	v_mul_lo_u32 v65, s7, v50
	v_mad_u64_u32 v[62:63], s[8:9], s6, v50, 0
	v_add_u32_e64 v50, 60, v35
	v_add3_u32 v63, v63, v64, v65
	v_ashrrev_i32_e32 v64, 31, v50
	v_add_u32_e32 v35, 62, v35
	s_ashr_i32 s5, s4, 31
	s_nop 0
	v_mul_lo_u32 v66, s6, v64
	v_mul_lo_u32 v67, s7, v50
	v_mad_u64_u32 v[64:65], s[8:9], s6, v50, 0
	v_ashrrev_i32_e32 v50, 31, v35
	s_lshl_b64 s[4:5], s[4:5], 2
	v_add3_u32 v65, v65, v66, v67
	v_mul_lo_u32 v50, s6, v50
	v_mul_lo_u32 v68, s7, v35
	v_mad_u64_u32 v[66:67], s[6:7], s6, v35, 0
	s_add_u32 s2, s2, s4
	v_and_b32_e32 v35, 31, v51
	v_add3_u32 v67, v67, v50, v68
	s_addc_u32 s3, s3, s5
	v_lshlrev_b32_e32 v68, 2, v35
	v_mov_b32_e64 v69, 0
	v_lshl_add_u64 v[68:69], s[2:3], 0, v[68:69]
	v_lshl_add_u64 v[0:1], v[0:1], 2, v[68:69]
	v_lshl_add_u64 v[2:3], v[2:3], 2, v[68:69]
	v_lshl_add_u64 v[4:5], v[4:5], 2, v[68:69]
	v_lshl_add_u64 v[6:7], v[6:7], 2, v[68:69]
	v_lshl_add_u64 v[8:9], v[8:9], 2, v[68:69]
	v_lshl_add_u64 v[10:11], v[10:11], 2, v[68:69]
	v_lshl_add_u64 v[12:13], v[12:13], 2, v[68:69]
	v_lshl_add_u64 v[14:15], v[14:15], 2, v[68:69]
	v_lshl_add_u64 v[16:17], v[16:17], 2, v[68:69]
	v_lshl_add_u64 v[18:19], v[18:19], 2, v[68:69]
	v_lshl_add_u64 v[20:21], v[20:21], 2, v[68:69]
	v_lshl_add_u64 v[22:23], v[22:23], 2, v[68:69]
	v_lshl_add_u64 v[24:25], v[24:25], 2, v[68:69]
	v_lshl_add_u64 v[26:27], v[26:27], 2, v[68:69]
	v_lshl_add_u64 v[28:29], v[28:29], 2, v[68:69]
	v_lshl_add_u64 v[30:31], v[30:31], 2, v[68:69]
	v_lshl_add_u64 v[32:33], v[32:33], 2, v[68:69]
	v_lshl_add_u64 v[36:37], v[36:37], 2, v[68:69]
	v_lshl_add_u64 v[38:39], v[38:39], 2, v[68:69]
	v_lshl_add_u64 v[40:41], v[40:41], 2, v[68:69]
	v_lshl_add_u64 v[42:43], v[42:43], 2, v[68:69]
	v_lshl_add_u64 v[44:45], v[44:45], 2, v[68:69]
	v_lshl_add_u64 v[46:47], v[46:47], 2, v[68:69]
	v_lshl_add_u64 v[48:49], v[48:49], 2, v[68:69]
	v_lshl_add_u64 v[52:53], v[52:53], 2, v[68:69]
	v_lshl_add_u64 v[54:55], v[54:55], 2, v[68:69]
	v_lshl_add_u64 v[56:57], v[56:57], 2, v[68:69]
	v_lshl_add_u64 v[58:59], v[58:59], 2, v[68:69]
	v_lshl_add_u64 v[60:61], v[60:61], 2, v[68:69]
	v_lshl_add_u64 v[62:63], v[62:63], 2, v[68:69]
	v_lshl_add_u64 v[64:65], v[64:65], 2, v[68:69]
	v_lshl_add_u64 v[66:67], v[66:67], 2, v[68:69]
	global_load_dword v0, v[0:1], off
	s_nop 0
	s_nop 0
	global_load_dword v1, v[2:3], off
	s_nop 0
	s_nop 0
	global_load_dword v2, v[4:5], off
	global_load_dword v3, v[6:7], off
	s_nop 0
	s_nop 0
	global_load_dword v4, v[8:9], off
	global_load_dword v5, v[10:11], off
	global_load_dword v6, v[12:13], off
	global_load_dword v7, v[14:15], off
	s_nop 0
	s_nop 0
	global_load_dword v8, v[16:17], off
	global_load_dword v9, v[18:19], off
	global_load_dword v10, v[20:21], off
	global_load_dword v11, v[22:23], off
	global_load_dword v12, v[24:25], off
	global_load_dword v13, v[26:27], off
	global_load_dword v14, v[28:29], off
	global_load_dword v15, v[30:31], off
	global_load_dword v16, v[32:33], off
	global_load_dword v17, v[36:37], off
	global_load_dword v18, v[38:39], off
	global_load_dword v19, v[40:41], off
	global_load_dword v20, v[42:43], off
	global_load_dword v21, v[44:45], off
	global_load_dword v22, v[46:47], off
	global_load_dword v23, v[48:49], off
	global_load_dword v24, v[52:53], off
	global_load_dword v25, v[54:55], off
	global_load_dword v26, v[56:57], off
	global_load_dword v27, v[58:59], off
	global_load_dword v28, v[60:61], off
	global_load_dword v29, v[62:63], off
	global_load_dword v30, v[64:65], off
	global_load_dword v31, v[66:67], off
	s_lshl_b32 s18, s61, 3
	s_add_i32 s7, s19, s18
	s_cmp_gt_i32 s7, 0xdbff
	s_cbranch_scc1 .LBB0_44
.LBB0_172:
	s_cmpk_gt_i32 s7, 0xbff
	s_cbranch_scc0 .LBB0_179
	s_cmpk_gt_u32 s7, 0xfff
	s_cbranch_scc0 .LBB0_180
	s_cmpk_gt_u32 s7, 0x13ff
	s_cbranch_scc0 .LBB0_181
	s_cmpk_gt_u32 s7, 0x17ff
	s_cbranch_scc0 .LBB0_182
	s_cmpk_gt_u32 s7, 0x1bff
	s_cbranch_scc0 .LBB0_183
	s_cmpk_gt_u32 s7, 0x9bff
	s_cbranch_scc0 .LBB0_184
	s_nop 0
	s_add_i32 s2, s7, 0xffff6400
	s_lshr_b32 s2, s2, 8
	s_mov_b32 s3, 0
	v_readlane_b32 s36, v253, 50
	s_lshl_b64 s[2:3], s[2:3], 21
	s_nop 0
	v_readlane_b32 s46, v253, 60
	v_readlane_b32 s47, v253, 61
	s_add_u32 s4, s46, s2
	s_nop 0
	v_readlane_b32 s37, v253, 51
	s_addc_u32 s5, s47, s3
	s_lshl_b32 s2, s7, 1
	v_readlane_b32 s36, v254, 5
	s_and_b32 s10, s2, 0x1c0
	s_lshl_b32 s2, s7, 5
	s_nop 0
	v_readlane_b32 s38, v253, 52
	v_readlane_b32 s39, v253, 53
	v_readlane_b32 s40, v253, 54
	v_readlane_b32 s41, v253, 55
	v_readlane_b32 s42, v253, 56
	v_readlane_b32 s43, v253, 57
	v_readlane_b32 s44, v253, 58
	v_readlane_b32 s45, v253, 59
	v_readlane_b32 s48, v253, 62
	v_readlane_b32 s49, v253, 63
	v_readlane_b32 s50, v254, 0
	v_readlane_b32 s51, v254, 1
	v_readlane_b32 s37, v254, 6
	s_and_b32 s6, s2, 0x3e0
	s_mov_b64 s[2:3], 0
	s_branch .LBB0_185

.LBB0_185:
	s_andn2_b64 vcc, exec, s[2:3]
	s_nop 0
	s_mov_b64 s[2:3], 0x400
	s_cbranch_vccnz .LBB0_187
	s_cmpk_gt_u32 s7, 0x5bff
	s_cselect_b64 s[2:3], -1, 0
	s_movk_i32 s6, 0xa400
	s_and_b64 s[4:5], s[2:3], exec
	s_nop 0
	s_cselect_b32 s4, s6, 0xffffe400
	s_add_i32 s8, s4, s7
	s_lshl_b32 s5, s8, 5
	s_lshr_b32 s4, s8, 8
	s_nop 0
	s_and_b32 s6, s5, 0x1e0
	v_readlane_b32 s36, v253, 50
	s_and_b64 s[2:3], s[2:3], exec
	s_nop 0
	v_readlane_b32 s42, v253, 56
	v_readlane_b32 s43, v253, 57
	v_readlane_b32 s44, v253, 58
	v_readlane_b32 s45, v253, 59
	s_mov_b32 s5, 0
	s_cselect_b32 s9, s45, s43
	s_cselect_b32 s10, s44, s42
	s_lshl_b64 s[2:3], s[4:5], 21
	v_readlane_b32 s37, v253, 51
	s_add_u32 s4, s10, s2
	s_nop 0
	v_readlane_b32 s36, v254, 5
	s_addc_u32 s5, s9, s3
	s_lshl_b32 s2, s8, 2
	v_readlane_b32 s37, v254, 6
	s_and_b32 s10, s2, 0x3c0
	s_mov_b64 s[2:3], 0x200
	v_readlane_b32 s38, v253, 52
	v_readlane_b32 s39, v253, 53
	v_readlane_b32 s40, v253, 54
	v_readlane_b32 s41, v253, 55
	v_readlane_b32 s46, v253, 60
	v_readlane_b32 s47, v253, 61
	v_readlane_b32 s48, v253, 62
	v_readlane_b32 s49, v253, 63
	v_readlane_b32 s50, v254, 0
	v_readlane_b32 s51, v254, 1

.LBB0_188:
	s_andn2_b64 vcc, exec, s[8:9]
	s_cbranch_vccnz .LBB0_190
	v_readlane_b32 s40, v253, 34
	s_add_i32 s2, s7, 0xffffe800
	v_readlane_b32 s41, v253, 35
	v_readlane_b32 s42, v253, 36
	v_readlane_b32 s43, v253, 37
	v_readlane_b32 s44, v253, 38
	v_readlane_b32 s45, v253, 39
	v_readlane_b32 s46, v253, 40
	v_readlane_b32 s47, v253, 41
	v_readlane_b32 s48, v253, 42
	v_readlane_b32 s49, v253, 43
	s_lshr_b32 s2, s2, 9
	s_mov_b32 s3, 0
	v_readlane_b32 s50, v253, 44
	v_readlane_b32 s51, v253, 45
	v_readlane_b32 s52, v253, 46
	v_readlane_b32 s53, v253, 47
	s_mov_b64 s[40:41], s[44:45]
	s_lshl_b64 s[2:3], s[2:3], 22
	s_mov_b64 s[42:43], s[46:47]
	s_mov_b64 s[44:45], s[48:49]
	s_add_u32 s4, s44, s2
	s_addc_u32 s5, s45, s3
	s_lshl_b32 s2, s7, 1
	s_nop 0
	s_and_b32 s10, s2, 0x3c0
	s_lshl_b32 s2, s7, 5
	s_nop 0
	s_and_b32 s6, s2, 0x3e0
	s_mov_b64 s[2:3], 0x400
	v_readlane_b32 s54, v253, 48
	v_readlane_b32 s55, v253, 49
	s_mov_b64 s[46:47], s[50:51]
	s_mov_b64 s[48:49], s[52:53]

.LBB0_191:
	s_andn2_b64 vcc, exec, s[8:9]
	s_cbranch_vccnz .LBB0_193
	s_nop 0
	v_readlane_b32 s40, v253, 34
	s_add_i32 s2, s7, 0xffffec00
	v_readlane_b32 s41, v253, 35
	v_readlane_b32 s42, v253, 36
	v_readlane_b32 s43, v253, 37
	v_readlane_b32 s44, v253, 38
	v_readlane_b32 s45, v253, 39
	v_readlane_b32 s46, v253, 40
	v_readlane_b32 s47, v253, 41
	v_readlane_b32 s48, v253, 42
	v_readlane_b32 s49, v253, 43
	s_lshr_b32 s2, s2, 9
	s_mov_b32 s3, 0
	v_readlane_b32 s50, v253, 44
	v_readlane_b32 s51, v253, 45
	v_readlane_b32 s52, v253, 46
	v_readlane_b32 s53, v253, 47
	s_mov_b64 s[40:41], s[44:45]
	s_lshl_b64 s[2:3], s[2:3], 22
	s_mov_b64 s[42:43], s[46:47]
	s_add_u32 s4, s42, s2
	s_addc_u32 s5, s43, s3
	s_lshl_b32 s2, s7, 1
	s_and_b32 s10, s2, 0x3c0
	s_lshl_b32 s2, s7, 5
	s_nop 0
	s_and_b32 s6, s2, 0x3e0
	s_mov_b64 s[2:3], 0x400
	v_readlane_b32 s54, v253, 48
	v_readlane_b32 s55, v253, 49
	s_mov_b64 s[44:45], s[48:49]
	s_mov_b64 s[46:47], s[50:51]
	s_mov_b64 s[48:49], s[52:53]

.LBB0_194:
	s_andn2_b64 vcc, exec, s[8:9]
	s_cbranch_vccnz .LBB0_196
	s_and_b32 s2, s7, 0x1fc0
	s_add_i32 s10, s2, 0xfffff000
	s_lshl_b32 s2, s7, 5
	s_nop 0
	s_and_b32 s6, s2, 0x7e0
	s_mov_b64 s[2:3], 0x810

.LBB0_197:
	s_nop 0
	v_readlane_b32 s68, v253, 18
	s_add_i32 s2, s7, 0xfffff400
	v_readlane_b32 s72, v253, 22
	v_readlane_b32 s73, v253, 23
	s_lshr_b32 s2, s2, 9
	s_mov_b32 s3, 0
	v_readlane_b32 s74, v253, 24
	v_readlane_b32 s75, v253, 25
	v_readlane_b32 s76, v253, 26
	v_readlane_b32 s77, v253, 27
	v_readlane_b32 s78, v253, 28
	v_readlane_b32 s79, v253, 29
	v_readlane_b32 s80, v253, 30
	v_readlane_b32 s81, v253, 31
	s_mov_b64 s[8:9], s[72:73]
	s_lshl_b64 s[2:3], s[2:3], 22
	s_mov_b64 s[14:15], s[78:79]
	s_add_u32 s4, s14, s2
	s_mov_b64 s[10:11], s[74:75]
	s_addc_u32 s5, s15, s3
	s_lshl_b32 s2, s7, 1
	s_nop 0
	s_and_b32 s10, s2, 0x3c0
	s_lshl_b32 s2, s7, 5
	s_nop 0
	s_and_b32 s6, s2, 0x3e0
	s_mov_b64 s[2:3], 0x400
	v_readlane_b32 s69, v253, 19
	v_readlane_b32 s70, v253, 20
	v_readlane_b32 s71, v253, 21
	v_readlane_b32 s82, v253, 32
	v_readlane_b32 s83, v253, 33
	s_mov_b64 s[12:13], s[76:77]
	s_mov_b64 s[16:17], s[80:81]

.LBB0_199:
	s_nop 0
	s_mul_hi_i32 s2, s7, 0x2aaaaaab
	s_lshr_b32 s3, s2, 31
	s_ashr_i32 s2, s2, 8
	s_add_i32 s2, s2, s3
	s_nop 0
	s_mul_i32 s3, s2, 0x600
	s_sub_i32 s3, s7, s3
	s_nop 0
	s_mul_i32 s4, s3, 0x2aab
	s_lshr_b32 s5, s4, 31
	s_ashr_i32 s4, s4, 20
	s_add_i32 s6, s4, s5
	s_nop 0
	v_readlane_b32 s68, v253, 18
	s_mul_i32 s4, s6, 0x60
	v_readlane_b32 s72, v253, 22
	v_readlane_b32 s73, v253, 23
	s_sub_i32 s3, s3, s4
	s_nop 0
	s_mul_hi_i32 s5, s2, 0xc10000
	s_mul_i32 s2, s2, 0xc10000
	v_readlane_b32 s74, v253, 24
	v_readlane_b32 s75, v253, 25
	v_readlane_b32 s76, v253, 26
	v_readlane_b32 s77, v253, 27
	v_readlane_b32 s78, v253, 28
	v_readlane_b32 s79, v253, 29
	v_readlane_b32 s80, v253, 30
	v_readlane_b32 s81, v253, 31
	s_mov_b64 s[20:21], s[72:73]
	s_sext_i32_i16 s3, s3
	s_add_u32 s4, s20, s2
	s_addc_u32 s5, s21, s5
	s_lshl_b32 s10, s6, 6
	s_lshl_b32 s6, s3, 5
	s_mov_b64 s[2:3], 0xc10
	v_readlane_b32 s69, v253, 19
	v_readlane_b32 s70, v253, 20
	v_readlane_b32 s71, v253, 21
	v_readlane_b32 s82, v253, 32
	v_readlane_b32 s83, v253, 33
	s_mov_b64 s[22:23], s[74:75]
	s_mov_b64 s[24:25], s[76:77]
	s_mov_b64 s[26:27], s[78:79]
	s_mov_b64 s[28:29], s[80:81]
.LBB0_200:
	s_ashr_i32 s7, s6, 31
	v_lshrrev_b32_e32 v32, 5, v34
	s_lshl_b64 s[6:7], s[6:7], 2
	v_add_u32_e32 v35, s10, v32
	v_and_b32_e32 v32, 31, v51
	s_add_u32 s4, s4, s6
	s_addc_u32 s5, s5, s7
	v_lshlrev_b32_e32 v32, 2, v32
	v_mov_b32_e32 v33, 0
	v_ashrrev_i32_e32 v36, 31, v35
	v_lshl_add_u64 v[32:33], s[4:5], 0, v[32:33]
	v_mul_lo_u32 v38, s2, v36
	v_mul_lo_u32 v39, s3, v35
	v_mad_u64_u32 v[36:37], s[4:5], s2, v35, 0
	v_add3_u32 v37, v37, v38, v39
	v_add_u32_e32 v38, 2, v35
	v_ashrrev_i32_e32 v39, 31, v38
	v_mul_lo_u32 v40, s2, v39
	v_mul_lo_u32 v41, s3, v38
	v_mad_u64_u32 v[38:39], s[4:5], s2, v38, 0
	v_add3_u32 v39, v39, v40, v41
	v_add_u32_e32 v40, 4, v35
	v_ashrrev_i32_e32 v41, 31, v40
	v_mul_lo_u32 v42, s2, v41
	v_mul_lo_u32 v43, s3, v40
	v_mad_u64_u32 v[40:41], s[4:5], s2, v40, 0
	v_add3_u32 v41, v41, v42, v43
	v_add_u32_e32 v42, 6, v35
	v_ashrrev_i32_e32 v43, 31, v42
	v_mul_lo_u32 v44, s2, v43
	v_mul_lo_u32 v45, s3, v42
	v_mad_u64_u32 v[42:43], s[4:5], s2, v42, 0
	v_add3_u32 v43, v43, v44, v45
	v_add_u32_e32 v44, 8, v35
	v_ashrrev_i32_e32 v45, 31, v44
	v_mul_lo_u32 v46, s2, v45
	v_mul_lo_u32 v47, s3, v44
	v_mad_u64_u32 v[44:45], s[4:5], s2, v44, 0
	v_add3_u32 v45, v45, v46, v47
	v_add_u32_e32 v46, 10, v35
	v_ashrrev_i32_e32 v47, 31, v46
	v_mul_lo_u32 v48, s2, v47
	v_mul_lo_u32 v49, s3, v46
	v_mad_u64_u32 v[46:47], s[4:5], s2, v46, 0
	v_add3_u32 v47, v47, v48, v49
	v_lshl_add_u64 v[54:55], v[46:47], 2, v[32:33]
	v_add_u32_e32 v46, 12, v35
	v_ashrrev_i32_e32 v47, 31, v46
	v_mul_lo_u32 v48, s2, v47
	v_mul_lo_u32 v49, s3, v46
	v_mad_u64_u32 v[46:47], s[4:5], s2, v46, 0
	v_add3_u32 v47, v47, v48, v49
	v_lshl_add_u64 v[56:57], v[46:47], 2, v[32:33]
	v_add_u32_e32 v46, 14, v35
	v_ashrrev_i32_e32 v47, 31, v46
	v_mul_lo_u32 v48, s2, v47
	v_mul_lo_u32 v49, s3, v46
	v_mad_u64_u32 v[46:47], s[4:5], s2, v46, 0
	v_lshl_add_u64 v[36:37], v[36:37], 2, v[32:33]
	v_add3_u32 v47, v47, v48, v49
	v_lshl_add_u64 v[38:39], v[38:39], 2, v[32:33]
	v_lshl_add_u64 v[40:41], v[40:41], 2, v[32:33]
	v_lshl_add_u64 v[42:43], v[42:43], 2, v[32:33]
	v_lshl_add_u64 v[44:45], v[44:45], 2, v[32:33]
	v_lshl_add_u64 v[58:59], v[46:47], 2, v[32:33]
	global_load_dword v47, v[36:37], off
	global_load_dword v48, v[38:39], off
	global_load_dword v49, v[40:41], off
	global_load_dword v50, v[42:43], off
	global_load_dword v52, v[44:45], off
	global_load_dword v53, v[54:55], off
	s_nop 0
	s_nop 0
	global_load_dword v54, v[56:57], off
	global_load_dword v55, v[58:59], off
	v_add_u32_e32 v36, 16, v35
	v_ashrrev_i32_e32 v37, 31, v36
	v_mul_lo_u32 v38, s2, v37
	v_mul_lo_u32 v39, s3, v36
	v_mad_u64_u32 v[36:37], s[4:5], s2, v36, 0
	v_add3_u32 v37, v37, v38, v39
	v_add_u32_e32 v38, 18, v35
	v_ashrrev_i32_e32 v39, 31, v38
	v_mul_lo_u32 v40, s2, v39
	v_mul_lo_u32 v41, s3, v38
	v_mad_u64_u32 v[38:39], s[4:5], s2, v38, 0
	v_add3_u32 v39, v39, v40, v41
	v_add_u32_e32 v40, 20, v35
	v_ashrrev_i32_e32 v41, 31, v40
	v_mul_lo_u32 v42, s2, v41
	v_mul_lo_u32 v43, s3, v40
	v_mad_u64_u32 v[40:41], s[4:5], s2, v40, 0
	v_add3_u32 v41, v41, v42, v43
	v_add_u32_e32 v42, 22, v35
	v_ashrrev_i32_e32 v43, 31, v42
	v_mul_lo_u32 v44, s2, v43
	v_mul_lo_u32 v45, s3, v42
	v_mad_u64_u32 v[42:43], s[4:5], s2, v42, 0
	v_add3_u32 v43, v43, v44, v45
	v_add_u32_e32 v44, 24, v35
	v_ashrrev_i32_e32 v45, 31, v44
	v_mul_lo_u32 v46, s2, v45
	v_mul_lo_u32 v56, s3, v44
	v_mad_u64_u32 v[44:45], s[4:5], s2, v44, 0
	v_add3_u32 v45, v45, v46, v56
	v_add_u32_e32 v46, 26, v35
	v_ashrrev_i32_e32 v56, 31, v46
	v_mul_lo_u32 v58, s2, v56
	v_mul_lo_u32 v59, s3, v46
	v_mad_u64_u32 v[56:57], s[4:5], s2, v46, 0
	v_add3_u32 v57, v57, v58, v59
	v_add_u32_e64 v46, 28, v35
	v_lshl_add_u64 v[62:63], v[56:57], 2, v[32:33]
	v_ashrrev_i32_e32 v56, 31, v46
	s_nop 0
	v_mul_lo_u32 v58, s2, v56
	v_mul_lo_u32 v59, s3, v46
	v_mad_u64_u32 v[56:57], s[4:5], s2, v46, 0
	v_add3_u32 v57, v57, v58, v59
	v_add_u32_e64 v46, 30, v35
	v_lshl_add_u64 v[64:65], v[56:57], 2, v[32:33]
	v_ashrrev_i32_e32 v56, 31, v46
	s_nop 0
	v_mul_lo_u32 v58, s2, v56
	v_mul_lo_u32 v59, s3, v46
	v_mad_u64_u32 v[56:57], s[4:5], s2, v46, 0
	v_lshl_add_u64 v[36:37], v[36:37], 2, v[32:33]
	v_add3_u32 v57, v57, v58, v59
	v_lshl_add_u64 v[38:39], v[38:39], 2, v[32:33]
	v_lshl_add_u64 v[40:41], v[40:41], 2, v[32:33]
	v_lshl_add_u64 v[42:43], v[42:43], 2, v[32:33]
	v_lshl_add_u64 v[44:45], v[44:45], 2, v[32:33]
	v_lshl_add_u64 v[66:67], v[56:57], 2, v[32:33]
	global_load_dword v56, v[36:37], off
	global_load_dword v57, v[38:39], off
	global_load_dword v58, v[40:41], off
	global_load_dword v59, v[42:43], off
	global_load_dword v60, v[44:45], off
	global_load_dword v61, v[62:63], off
	s_nop 0
	s_nop 0
	global_load_dword v62, v[64:65], off
	global_load_dword v63, v[66:67], off
	v_add_u32_e32 v36, 32, v35
	v_ashrrev_i32_e32 v37, 31, v36
	v_mul_lo_u32 v38, s2, v37
	v_mul_lo_u32 v39, s3, v36
	v_mad_u64_u32 v[36:37], s[4:5], s2, v36, 0
	v_add3_u32 v37, v37, v38, v39
	v_add_u32_e32 v38, 34, v35
	v_ashrrev_i32_e32 v39, 31, v38
	v_mul_lo_u32 v40, s2, v39
	v_mul_lo_u32 v41, s3, v38
	v_mad_u64_u32 v[38:39], s[4:5], s2, v38, 0
	v_add3_u32 v39, v39, v40, v41
	v_add_u32_e32 v40, 36, v35
	v_ashrrev_i32_e32 v41, 31, v40
	v_mul_lo_u32 v42, s2, v41
	v_mul_lo_u32 v43, s3, v40
	v_mad_u64_u32 v[40:41], s[4:5], s2, v40, 0
	v_add3_u32 v41, v41, v42, v43
	v_add_u32_e32 v42, 38, v35
	v_ashrrev_i32_e32 v43, 31, v42
	v_mul_lo_u32 v44, s2, v43
	v_mul_lo_u32 v45, s3, v42
	v_mad_u64_u32 v[42:43], s[4:5], s2, v42, 0
	v_add3_u32 v43, v43, v44, v45
	v_add_u32_e32 v44, 40, v35
	v_ashrrev_i32_e32 v45, 31, v44
	v_mul_lo_u32 v46, s2, v45
	v_mul_lo_u32 v64, s3, v44
	v_mad_u64_u32 v[44:45], s[4:5], s2, v44, 0
	v_add3_u32 v45, v45, v46, v64
	v_add_u32_e32 v46, 42, v35
	v_ashrrev_i32_e32 v64, 31, v46
	v_mul_lo_u32 v66, s2, v64
	v_mul_lo_u32 v67, s3, v46
	v_mad_u64_u32 v[64:65], s[4:5], s2, v46, 0
	v_add3_u32 v65, v65, v66, v67
	v_add_u32_e64 v46, 44, v35
	v_lshl_add_u64 v[70:71], v[64:65], 2, v[32:33]
	v_ashrrev_i32_e32 v64, 31, v46
	s_nop 0
	v_mul_lo_u32 v66, s2, v64
	v_mul_lo_u32 v67, s3, v46
	v_mad_u64_u32 v[64:65], s[4:5], s2, v46, 0
	v_add3_u32 v65, v65, v66, v67
	v_add_u32_e64 v46, 46, v35
	v_lshl_add_u64 v[72:73], v[64:65], 2, v[32:33]
	v_ashrrev_i32_e32 v64, 31, v46
	s_nop 0
	v_mul_lo_u32 v66, s2, v64
	v_mul_lo_u32 v67, s3, v46
	v_mad_u64_u32 v[64:65], s[4:5], s2, v46, 0
	v_lshl_add_u64 v[36:37], v[36:37], 2, v[32:33]
	v_add3_u32 v65, v65, v66, v67
	v_lshl_add_u64 v[38:39], v[38:39], 2, v[32:33]
	v_lshl_add_u64 v[40:41], v[40:41], 2, v[32:33]
	v_lshl_add_u64 v[42:43], v[42:43], 2, v[32:33]
	v_lshl_add_u64 v[44:45], v[44:45], 2, v[32:33]
	v_lshl_add_u64 v[74:75], v[64:65], 2, v[32:33]
	global_load_dword v64, v[36:37], off
	global_load_dword v65, v[38:39], off
	global_load_dword v66, v[40:41], off
	global_load_dword v67, v[42:43], off
	global_load_dword v68, v[44:45], off
	global_load_dword v69, v[70:71], off
	s_nop 0
	s_nop 0
	global_load_dword v70, v[72:73], off
	global_load_dword v71, v[74:75], off
	v_add_u32_e32 v36, 48, v35
	v_ashrrev_i32_e32 v37, 31, v36
	v_mul_lo_u32 v38, s2, v37
	v_mul_lo_u32 v39, s3, v36
	v_mad_u64_u32 v[36:37], s[4:5], s2, v36, 0
	v_add3_u32 v37, v37, v38, v39
	v_add_u32_e32 v38, 50, v35
	v_ashrrev_i32_e32 v39, 31, v38
	v_mul_lo_u32 v40, s2, v39
	v_mul_lo_u32 v41, s3, v38
	v_mad_u64_u32 v[38:39], s[4:5], s2, v38, 0
	v_add3_u32 v39, v39, v40, v41
	v_add_u32_e32 v40, 52, v35
	v_ashrrev_i32_e32 v41, 31, v40
	v_mul_lo_u32 v42, s2, v41
	v_mul_lo_u32 v43, s3, v40
	v_mad_u64_u32 v[40:41], s[4:5], s2, v40, 0
	v_add3_u32 v41, v41, v42, v43
	v_add_u32_e32 v42, 54, v35
	v_ashrrev_i32_e32 v43, 31, v42
	v_mul_lo_u32 v44, s2, v43
	v_mul_lo_u32 v45, s3, v42
	v_mad_u64_u32 v[42:43], s[4:5], s2, v42, 0
	v_add3_u32 v43, v43, v44, v45
	v_add_u32_e32 v44, 56, v35
	v_ashrrev_i32_e32 v45, 31, v44
	v_mul_lo_u32 v46, s2, v45
	v_mul_lo_u32 v72, s3, v44
	v_mad_u64_u32 v[44:45], s[4:5], s2, v44, 0
	v_add3_u32 v45, v45, v46, v72
	v_add_u32_e32 v46, 58, v35
	v_ashrrev_i32_e32 v72, 31, v46
	v_mul_lo_u32 v74, s2, v72
	v_mul_lo_u32 v75, s3, v46
	v_mad_u64_u32 v[72:73], s[4:5], s2, v46, 0
	v_add_u32_e64 v46, 60, v35
	v_add3_u32 v73, v73, v74, v75
	v_ashrrev_i32_e32 v74, 31, v46
	s_nop 0
	v_mul_lo_u32 v76, s2, v74
	v_mul_lo_u32 v77, s3, v46
	v_mad_u64_u32 v[74:75], s[4:5], s2, v46, 0
	v_add_u32_e64 v35, 62, v35
	v_add3_u32 v75, v75, v76, v77
	v_ashrrev_i32_e32 v46, 31, v35
	s_nop 0
	v_lshl_add_u64 v[78:79], v[74:75], 2, v[32:33]
	v_mul_lo_u32 v46, s2, v46
	v_mul_lo_u32 v76, s3, v35
	v_mad_u64_u32 v[74:75], s[2:3], s2, v35, 0
	v_lshl_add_u64 v[36:37], v[36:37], 2, v[32:33]
	v_lshl_add_u64 v[38:39], v[38:39], 2, v[32:33]
	v_lshl_add_u64 v[72:73], v[72:73], 2, v[32:33]
	v_add3_u32 v75, v75, v46, v76
	v_lshl_add_u64 v[40:41], v[40:41], 2, v[32:33]
	v_lshl_add_u64 v[42:43], v[42:43], 2, v[32:33]
	v_lshl_add_u64 v[44:45], v[44:45], 2, v[32:33]
	v_lshl_add_u64 v[32:33], v[74:75], 2, v[32:33]
	global_load_dword v74, v[36:37], off
	global_load_dword v75, v[38:39], off
	global_load_dword v76, v[40:41], off
	global_load_dword v77, v[42:43], off
	s_nop 0
	s_nop 0
	global_load_dword v38, v[44:45], off
	global_load_dword v39, v[72:73], off
	s_nop 0
	s_nop 0
	global_load_dword v72, v[78:79], off
	global_load_dword v73, v[32:33], off
	s_andn2_b64 vcc, exec, s[0:1]
	s_cbranch_vccz .LBB0_45

.LBB0_202:
	s_mov_b32 s0, 0
	s_nop 0
	v_readlane_b32 s1, v253, 9
	s_waitcnt vmcnt(0)
	s_waitcnt vmcnt(63) expcnt(7) lgkmcnt(15)
	s_barrier
	s_lshl_b32 s1, s1, 6
	s_waitcnt vmcnt(31)
	s_nop 0
	v_mbcnt_lo_u32_b32 v0, -1, s0
	s_sub_i32 s1, 0, s1
	s_nop 0
	v_mbcnt_hi_u32_b32 v0, -1, v0
	v_cmp_eq_u32_e32 vcc, s1, v0
	s_and_saveexec_b64 s[22:23], vcc
	s_cbranch_execz .LBB0_246
	s_nop 0
	v_readlane_b32 s34, v253, 12
	v_readlane_b32 s0, v253, 14
	v_readlane_b32 s35, v253, 13
	v_readlane_b32 s33, v253, 17
	v_mov_b32_e32 v0, s0
	s_waitcnt vmcnt(0) expcnt(0) lgkmcnt(0)
	ds_read_b32 v2, v0
	ds_read_b32 v0, v0 offset:4
	s_waitcnt lgkmcnt(1)
	v_cmp_ne_u32_e32 vcc, 0, v2
	s_cbranch_vccnz .LBB0_217
	s_nop 0
	v_readlane_b32 s2, v253, 6
	v_readlane_b32 s3, v253, 7
	s_load_dwordx2 s[0:1], s[2:3], 0x4
	s_add_u32 s2, s34, 0x1000
	s_addc_u32 s3, s35, 0
	s_nop 0
	s_add_u32 s4, s34, 0x1100
	s_addc_u32 s5, s35, 0
	s_nop 0
	s_add_u32 s6, s34, 0x1200
	s_addc_u32 s7, s35, 0
	s_nop 0
	s_add_u32 s8, s34, 0x1300
	s_waitcnt lgkmcnt(0)
	s_mul_i32 s18, s0, s61
	s_addc_u32 s9, s35, 0
	s_mul_i32 s18, s18, s1
	s_mov_b32 s19, 1
	s_mov_b64 s[0:1], 0
	v_mov_b64_e32 v[0:1], s[34:35]
	v_mov_b64_e32 v[2:3], s[2:3]
	v_mov_b64_e32 v[4:5], s[4:5]
	v_mov_b64_e32 v[6:7], s[6:7]
	v_mov_b64_e32 v[8:9], s[8:9]
	s_branch .LBB0_207

.LBB0_207:
	s_nop 0
	flat_load_dword v25, v[0:1] offset:1024 sc1
	flat_load_dword v10, v[0:1] offset:1280 sc1
	flat_load_dword v11, v[0:1] offset:1536 sc1
	flat_load_dword v12, v[0:1] offset:1792 sc1
	flat_load_dword v13, v[0:1] offset:2048 sc1
	flat_load_dword v14, v[0:1] offset:2304 sc1
	flat_load_dword v15, v[0:1] offset:2560 sc1
	flat_load_dword v16, v[0:1] offset:2816 sc1
	flat_load_dword v17, v[0:1] offset:3072 sc1
	flat_load_dword v18, v[0:1] offset:3328 sc1
	flat_load_dword v19, v[0:1] offset:3584 sc1
	flat_load_dword v20, v[0:1] offset:3840 sc1
	flat_load_dword v21, v[2:3] sc1
	flat_load_dword v22, v[4:5] sc1
	flat_load_dword v23, v[6:7] sc1
	flat_load_dword v24, v[8:9] sc1
	s_or_b64 s[6:7], s[6:7], exec
	s_or_b64 s[4:5], s[4:5], exec
	s_waitcnt vmcnt(0) lgkmcnt(0)
	v_add_u32_e32 v26, v10, v25
	v_add_u32_e32 v26, v26, v11
	v_add_u32_e32 v26, v26, v12
	v_add_u32_e32 v26, v26, v13
	v_add_u32_e32 v26, v26, v14
	v_add_u32_e32 v26, v26, v15
	v_add_u32_e32 v26, v26, v16
	v_add_u32_e32 v26, v26, v17
	v_add_u32_e32 v26, v26, v18
	v_add_u32_e32 v26, v26, v19
	v_add_u32_e32 v26, v26, v20
	v_add_u32_e32 v26, v26, v21
	v_add_u32_e32 v26, v26, v22
	v_add_u32_e64 v26, v26, v23
	v_add_u32_e32 v26, v26, v24
	v_cmp_ne_u32_e32 vcc, s18, v26
	s_and_saveexec_b64 s[8:9], vcc
	s_cbranch_execz .LBB0_206
	s_and_b32 s12, s19, 0xff
	s_mov_b64 s[10:11], -1
	s_cmp_eq_u32 s12, 0
	s_mov_b64 s[14:15], -1
	s_mov_b64 s[12:13], -1
	s_sleep 1
	s_cbranch_scc1 .LBB0_210
	s_and_saveexec_b64 s[16:17], s[14:15]
	s_cbranch_execz .LBB0_205
	s_branch .LBB0_213
.LBB0_210:
	s_nop 0
	flat_load_dword v26, v[0:1] offset:512 sc1
	s_mov_b64 s[14:15], 0
	s_waitcnt vmcnt(0) lgkmcnt(0)
	v_cmp_eq_u32_e32 vcc, 0, v26
	s_and_saveexec_b64 s[16:17], vcc
	s_cmp_lt_u32 s19, 0x400001
	s_cselect_b64 s[14:15], -1, 0
	s_xor_b64 s[12:13], exec, -1
	s_and_b64 s[14:15], s[14:15], exec
	s_or_b64 exec, exec, s[16:17]
	s_and_saveexec_b64 s[16:17], s[14:15]
	s_cbranch_execz .LBB0_205

.LBB0_216:
	s_or_b64 exec, exec, s[0:1]
	s_cmp_eq_u32 s33, 15
	s_cselect_b64 vcc, -1, 0
	s_cmp_eq_u32 s33, 14
	s_cselect_b64 s[0:1], -1, 0
	s_cmp_eq_u32 s33, 13
	s_cselect_b64 s[2:3], -1, 0
	s_cmp_eq_u32 s33, 12
	s_cselect_b64 s[4:5], -1, 0
	s_cmp_eq_u32 s33, 11
	s_cselect_b64 s[6:7], -1, 0
	s_cmp_eq_u32 s33, 10
	s_cselect_b64 s[8:9], -1, 0
	s_cmp_eq_u32 s33, 9
	s_cselect_b64 s[10:11], -1, 0
	s_cmp_eq_u32 s33, 8
	s_cselect_b64 s[12:13], -1, 0
	s_cmp_eq_u32 s33, 7
	s_cselect_b64 s[14:15], -1, 0
	s_cmp_eq_u32 s33, 6
	s_cselect_b64 s[16:17], -1, 0
	s_cmp_eq_u32 s33, 5
	s_cselect_b64 s[18:19], -1, 0
	s_cmp_eq_u32 s33, 4
	s_cselect_b64 s[20:21], -1, 0
	s_cmp_eq_u32 s33, 3
	s_cselect_b64 s[24:25], -1, 0
	s_cmp_eq_u32 s33, 2
	s_cselect_b64 s[26:27], -1, 0
	s_cmp_eq_u32 s33, 1
	s_cselect_b64 s[28:29], -1, 0
	s_cmp_eq_u32 s33, 0
	s_cselect_b64 s[30:31], -1, 0
	s_nop 0
	v_cndmask_b32_e64 v0, 0, v25, s[30:31]
	v_cndmask_b32_e64 v0, v0, v10, s[28:29]
	v_cndmask_b32_e64 v0, v0, v11, s[26:27]
	v_cndmask_b32_e64 v0, v0, v12, s[24:25]
	v_cndmask_b32_e64 v0, v0, v13, s[20:21]
	v_cndmask_b32_e64 v0, v0, v14, s[18:19]
	v_cndmask_b32_e64 v0, v0, v15, s[16:17]
	v_cndmask_b32_e64 v0, v0, v16, s[14:15]
	v_cndmask_b32_e64 v0, v0, v17, s[12:13]
	v_cndmask_b32_e64 v0, v0, v18, s[10:11]
	v_cndmask_b32_e64 v0, v0, v19, s[8:9]
	v_cndmask_b32_e64 v0, v0, v20, s[6:7]
	v_cndmask_b32_e64 v0, v0, v21, s[4:5]
	v_cndmask_b32_e64 v0, v0, v22, s[2:3]
	v_cndmask_b32_e64 v0, v0, v23, s[0:1]
	v_cndmask_b32_e32 v0, v0, v24, vcc
	v_cmp_ne_u32_e32 vcc, 0, v25
	v_readlane_b32 s0, v253, 14
	s_nop 0
	s_nop 0
	v_cndmask_b32_e64 v1, 0, 1, vcc
	v_cmp_ne_u32_e32 vcc, 0, v10
	s_nop 1
	v_addc_co_u32_e32 v1, vcc, 0, v1, vcc
	v_cmp_ne_u32_e32 vcc, 0, v11
	s_nop 1
	s_nop 0
	v_cndmask_b32_e64 v2, 0, 1, vcc
	v_cmp_ne_u32_e32 vcc, 0, v12
	s_nop 1
	v_addc_co_u32_e32 v1, vcc, v1, v2, vcc
	v_cmp_ne_u32_e32 vcc, 0, v13
	s_nop 1
	s_nop 0
	v_cndmask_b32_e64 v2, 0, 1, vcc
	v_cmp_ne_u32_e32 vcc, 0, v14
	s_nop 1
	v_addc_co_u32_e32 v1, vcc, v1, v2, vcc
	v_cmp_ne_u32_e32 vcc, 0, v15
	s_nop 1
	s_nop 0
	v_cndmask_b32_e64 v2, 0, 1, vcc
	v_cmp_ne_u32_e32 vcc, 0, v16
	s_nop 1
	v_addc_co_u32_e32 v1, vcc, v1, v2, vcc
	v_cmp_ne_u32_e32 vcc, 0, v17
	s_nop 1
	s_nop 0
	v_cndmask_b32_e64 v2, 0, 1, vcc
	v_cmp_ne_u32_e32 vcc, 0, v18
	s_nop 1
	v_addc_co_u32_e32 v1, vcc, v1, v2, vcc
	v_cmp_ne_u32_e32 vcc, 0, v19
	s_nop 1
	s_nop 0
	v_cndmask_b32_e64 v2, 0, 1, vcc
	v_cmp_ne_u32_e32 vcc, 0, v20
	s_nop 1
	v_addc_co_u32_e32 v1, vcc, v1, v2, vcc
	v_cmp_ne_u32_e32 vcc, 0, v21
	s_nop 1
	s_nop 0
	v_cndmask_b32_e64 v2, 0, 1, vcc
	v_cmp_ne_u32_e32 vcc, 0, v22
	s_nop 1
	v_addc_co_u32_e32 v1, vcc, v1, v2, vcc
	v_cmp_ne_u32_e32 vcc, 0, v23
	s_nop 1
	s_nop 0
	v_cndmask_b32_e64 v2, 0, 1, vcc
	v_cmp_ne_u32_e32 vcc, 0, v24
	s_nop 1
	v_addc_co_u32_e32 v1, vcc, v1, v2, vcc
	v_max_u32_e32 v2, 1, v0
	v_max_u32_e32 v0, 1, v1
	v_mov_b32_e32 v1, s0
	ds_write_b32 v1, v2
	ds_write_b32 v1, v0 offset:4
.LBB0_217:
	s_lshl_b32 s20, s33, 6
	s_nop 0
	s_add_i32 s2, s20, 0x500
	s_mov_b32 s3, 0
	s_lshl_b64 s[0:1], s[2:3], 2
	s_add_u32 s0, s34, s0
	s_addc_u32 s1, s35, s1
	v_mov_b32_e32 v1, 1
	v_mov_b64_e32 v[4:5], s[0:1]
	flat_atomic_add v1, v[4:5], v1 sc0
	v_cvt_f32_u32_e32 v3, v2
	v_sub_u32_e32 v4, 0, v2
	v_rcp_iflag_f32_e32 v3, v3
	s_nop 0
	v_mul_f32_e32 v3, 0x4f7ffffe, v3
	v_cvt_u32_f32_e32 v3, v3
	s_nop 0
	v_mul_lo_u32 v4, v4, v3
	v_mul_hi_u32 v4, v3, v4
	v_add_u32_e32 v3, v3, v4
	s_waitcnt vmcnt(0) lgkmcnt(0)
	v_mul_hi_u32 v3, v1, v3
	v_mul_lo_u32 v5, v3, v2
	v_add_u32_e32 v4, 1, v1
	v_sub_u32_e32 v1, v1, v5
	v_add_u32_e32 v6, 1, v3
	v_cmp_ge_u32_e32 vcc, v1, v2
	v_sub_u32_e32 v5, v1, v2
	s_nop 0
	v_cndmask_b32_e32 v3, v3, v6, vcc
	v_cndmask_b32_e32 v1, v1, v5, vcc
	v_add_u32_e32 v5, 1, v3
	v_cmp_ge_u32_e32 vcc, v1, v2
	s_nop 1
	v_cndmask_b32_e32 v1, v3, v5, vcc
	v_mad_u64_u32 v[2:3], s[0:1], v2, v1, v[2:3]
	v_cmp_ne_u32_e32 vcc, v4, v2
	s_and_saveexec_b64 s[0:1], vcc
	s_xor_b64 s[0:1], exec, s[0:1]
	s_cbranch_execz .LBB0_230
	s_add_i32 s2, s20, 0x900
	s_lshl_b64 s[2:3], s[2:3], 2
	s_add_u32 s4, s34, s2
	s_addc_u32 s5, s35, s3
	v_mov_b64_e32 v[2:3], s[4:5]
	flat_load_dword v0, v[2:3] sc1
	s_waitcnt vmcnt(0) lgkmcnt(0)
	v_cmp_eq_u32_e32 vcc, v0, v1
	s_and_saveexec_b64 s[2:3], vcc
	s_cbranch_execz .LBB0_229
	s_mov_b32 s21, 1
	s_mov_b64 s[6:7], 0
	s_branch .LBB0_221

.LBB0_221:
	s_nop 0
	s_and_b32 s14, s21, 0xff
	s_mov_b64 s[12:13], -1
	s_cmp_lg_u32 s14, 0
	s_mov_b64 s[14:15], -1
	s_sleep 1
	s_cbranch_scc1 .LBB0_225
	v_mov_b64_e32 v[2:3], s[34:35]
	flat_load_dword v0, v[2:3] offset:512 sc1
	s_mov_b64 s[14:15], 0
	s_mov_b64 s[16:17], -1
	s_waitcnt vmcnt(0) lgkmcnt(0)
	v_cmp_eq_u32_e32 vcc, 0, v0
	s_and_saveexec_b64 s[18:19], vcc
	s_nop 0
	s_cmp_lt_u32 s21, 0x400001
	s_cselect_b64 s[14:15], -1, 0
	s_xor_b64 s[16:17], exec, -1
	s_and_b64 s[14:15], s[14:15], exec
	s_or_b64 exec, exec, s[18:19]

.LBB0_227:
	s_or_b64 exec, exec, s[6:7]
	s_xor_b64 s[4:5], s[8:9], -1
	s_and_saveexec_b64 s[6:7], s[4:5]
	s_xor_b64 s[6:7], exec, s[6:7]
	s_cbranch_execz .LBB0_229
	v_mov_b32_e32 v2, 1
	v_mov_b64_e32 v[0:1], s[34:35]
	s_nop 0
	flat_atomic_add v[0:1], v2 offset:512

.LBB0_230:
	s_andn2_saveexec_b64 s[0:1], s[0:1]
	s_cbranch_execz .LBB0_246
	v_mov_b32_e32 v1, s34
	v_add_co_u32_e32 v2, vcc, 0x3000, v1
	v_mov_b32_e64 v1, s35
	buffer_wbl2 sc1
	s_waitcnt vmcnt(0)
	v_addc_co_u32_e32 v3, vcc, 0, v1, vcc
	v_mov_b32_e64 v1, 1
	flat_atomic_add v1, v[2:3], v1 offset:1024 sc0
	v_cvt_f32_u32_e32 v2, v0
	v_sub_u32_e32 v3, 0, v0
	s_add_u32 s0, s34, 0x3500
	s_addc_u32 s1, s35, 0
	v_rcp_iflag_f32_e32 v2, v2
	s_mov_b64 s[4:5], -1
	s_nop 0
	v_mul_f32_e32 v2, 0x4f7ffffe, v2
	v_cvt_u32_f32_e32 v2, v2
	s_nop 0
	v_mul_lo_u32 v3, v3, v2
	v_mul_hi_u32 v3, v2, v3
	v_add_u32_e32 v2, v2, v3
	s_waitcnt vmcnt(0) lgkmcnt(0)
	v_mul_hi_u32 v2, v1, v2
	v_mul_lo_u32 v4, v2, v0
	v_add_u32_e32 v3, 1, v1
	v_sub_u32_e32 v1, v1, v4
	v_add_u32_e32 v5, 1, v2
	v_cmp_ge_u32_e32 vcc, v1, v0
	v_sub_u32_e32 v4, v1, v0
	s_nop 0
	v_cndmask_b32_e32 v2, v2, v5, vcc
	v_cndmask_b32_e32 v1, v1, v4, vcc
	v_add_u32_e32 v4, 1, v2
	v_cmp_ge_u32_e32 vcc, v1, v0
	s_nop 1
	v_cndmask_b32_e32 v2, v2, v4, vcc
	v_mad_u64_u32 v[0:1], s[2:3], v0, v2, v[0:1]
	v_cmp_ne_u32_e32 vcc, v3, v0
	v_mov_b64_e32 v[0:1], s[0:1]
	s_and_saveexec_b64 s[2:3], vcc
	s_cbranch_execz .LBB0_243
	v_mov_b64_e32 v[0:1], s[0:1]
	s_nop 0
	flat_load_dword v0, v[0:1] sc1
	s_mov_b64 s[8:9], 0
	s_waitcnt vmcnt(0) lgkmcnt(0)
	v_cmp_eq_u32_e32 vcc, v0, v2
	s_and_saveexec_b64 s[6:7], vcc
	s_cbranch_execz .LBB0_242
	s_nop 0
	s_add_u32 s4, s34, 0x200
	s_addc_u32 s5, s35, 0
	s_mov_b32 s21, 1
	s_branch .LBB0_235

.LBB0_237:
	v_mov_b64_e32 v[0:1], s[4:5]
	s_nop 0
	flat_load_dword v0, v[0:1] sc1
	s_mov_b64 s[14:15], 0
	s_mov_b64 s[12:13], -1
	s_waitcnt vmcnt(0) lgkmcnt(0)
	v_cmp_eq_u32_e32 vcc, 0, v0
	s_and_saveexec_b64 s[16:17], vcc
	s_nop 0
	s_cmp_lt_u32 s21, 0x400001
	s_cselect_b64 s[14:15], -1, 0
	s_xor_b64 s[12:13], exec, -1
	s_and_b64 s[14:15], s[14:15], exec
	s_or_b64 exec, exec, s[16:17]
	s_mov_b64 s[16:17], -1
	s_and_saveexec_b64 s[18:19], s[14:15]
	s_cbranch_execz .LBB0_234

.LBB0_243:
	s_or_b64 exec, exec, s[2:3]
	s_and_saveexec_b64 s[0:1], s[4:5]
	s_cbranch_execz .LBB0_245
	v_mov_b32_e64 v2, 1
	flat_atomic_add v[0:1], v2
.LBB0_245:
	s_or_b64 exec, exec, s[0:1]
	s_nop 0
	s_add_i32 s0, s20, 0x900
	s_mov_b32 s1, 0
	s_lshl_b64 s[0:1], s[0:1], 2
	s_add_u32 s0, s34, s0
	s_addc_u32 s1, s35, s1
	v_mov_b32_e64 v2, 1
	v_mov_b64_e32 v[0:1], s[0:1]
	s_waitcnt vmcnt(0) lgkmcnt(0)
	buffer_inv sc1
	flat_atomic_add v[0:1], v2
	s_waitcnt vmcnt(0)

.LBB0_247:
	s_cmpk_eq_i32 s61, 0x100
	s_cselect_b64 s[2:3], -1, 0
	s_cmpk_lg_i32 s61, 0x100
	s_cselect_b64 s[42:43], -1, 0
	s_cmp_eq_u32 s36, 0
	s_nop 0
	v_readlane_b32 s4, v253, 15
	s_cselect_b64 s[0:1], -1, 0
	s_nop 0
	v_readlane_b32 s5, v253, 16
	s_and_b64 s[0:1], s[0:1], s[4:5]
	s_nop 0
	v_writelane_b32 v254, s2, 42
	s_and_b64 s[0:1], s[0:1], s[2:3]
	s_andn2_b64 vcc, exec, s[0:1]
	v_writelane_b32 v254, s3, 43
	s_mov_b64 s[14:15], 0
	s_cbranch_vccnz .LBB0_251
	v_readlane_b32 s0, v253, 0
	s_waitcnt vmcnt(0)
	s_nop 0
	v_mov_b32_e32 v0, 0xc000
	v_readlane_b32 s1, v253, 1
	s_nop 4
	s_nop 0
	global_load_dword v1, v0, s[0:1] sc1
	global_load_dword v2, v0, s[0:1] offset:256 sc1
	global_load_dword v3, v0, s[0:1] offset:512 sc1
	global_load_dword v4, v0, s[0:1] offset:768 sc1
	global_load_dword v5, v0, s[0:1] offset:1024 sc1
	global_load_dword v6, v0, s[0:1] offset:1280 sc1
	global_load_dword v7, v0, s[0:1] offset:1536 sc1
	global_load_dword v8, v0, s[0:1] offset:1792 sc1
	s_waitcnt vmcnt(7)
	v_cmp_ne_u32_e32 vcc, 32, v1
	s_waitcnt vmcnt(6)
	s_nop 0
	v_cmp_ne_u32_e64 s[0:1], 32, v2
	s_waitcnt vmcnt(5)
	s_nop 0
	v_cmp_ne_u32_e64 s[2:3], 32, v3
	s_or_b64 s[0:1], vcc, s[0:1]
	s_waitcnt vmcnt(4)
	v_cmp_ne_u32_e64 s[4:5], 32, v4
	s_or_b64 s[0:1], s[0:1], s[2:3]
	s_waitcnt vmcnt(3)
	v_cmp_ne_u32_e64 s[6:7], 32, v5
	s_or_b64 s[0:1], s[0:1], s[4:5]
	s_waitcnt vmcnt(2)
	v_cmp_ne_u32_e64 s[8:9], 32, v6
	s_or_b64 s[0:1], s[0:1], s[6:7]
	s_waitcnt vmcnt(1)
	v_cmp_ne_u32_e64 s[10:11], 32, v7
	s_or_b64 s[0:1], s[0:1], s[8:9]
	s_waitcnt vmcnt(0)
	v_cmp_ne_u32_e64 s[12:13], 32, v8
	s_or_b64 s[0:1], s[0:1], s[10:11]
	s_or_b64 s[0:1], s[0:1], s[12:13]
	s_and_b64 vcc, exec, s[0:1]
	s_mov_b32 s0, s93
	s_cbranch_vccnz .LBB0_250
	s_nop 0
	s_add_i32 s0, 0, 0x20190
	v_mov_b32_e64 v0, s0
	s_add_i32 s0, 0, 0x20194
	ds_read_b32 v0, v0
	v_mov_b32_e64 v1, s0
	ds_read_b32 v1, v1
	s_mov_b64 s[14:15], -1
	s_waitcnt lgkmcnt(1)
	v_lshlrev_b32_e32 v2, 5, v0
	s_waitcnt lgkmcnt(0)
	v_lshlrev_b32_e32 v3, 3, v1
	v_add_u32_e32 v1, v2, v1
	v_add_u32_e32 v0, v3, v0
	v_readfirstlane_b32 s0, v1
	v_readfirstlane_b32 s93, v0
	s_nop 0
	v_writelane_b32 v253, s0, 8

.LBB0_252:
	v_readlane_b32 s0, v253, 0
	v_readlane_b32 s1, v253, 1
	s_add_u32 s0, s0, 0x37a00000
	s_addc_u32 s1, s1, 0
	s_nop 0
	v_writelane_b32 v254, s0, 32
	s_mov_b32 s97, 0
	s_mov_b32 s92, 1
	v_writelane_b32 v254, s1, 33
	v_readlane_b32 s0, v253, 15
	v_readlane_b32 s1, v253, 16
	v_readlane_b32 s16, v254, 42
	s_and_b64 s[18:19], s[0:1], s[14:15]
	s_nop 0
	v_readlane_b32 s17, v254, 43
	s_and_b64 s[0:1], s[16:17], s[18:19]
	s_xor_b64 s[0:1], s[0:1], -1
	v_writelane_b32 v254, s0, 44
	s_movk_i32 s68, 0x1800
	v_mov_b32_e32 v97, 0
	v_writelane_b32 v254, s1, 45
	v_readlane_b32 s0, v253, 34
	v_readlane_b32 s2, v253, 36
	v_readlane_b32 s1, v253, 35
	v_readlane_b32 s3, v253, 37
	s_add_u32 s0, s2, 0x2000
	s_addc_u32 s1, s3, 0
	s_nop 0
	v_writelane_b32 v254, s0, 46
	v_readlane_b32 s7, v253, 41
	s_ashr_i32 s7, s50, 31
	s_nop 0
	v_writelane_b32 v254, s1, 47
	v_readlane_b32 s0, v253, 9
	s_lshl_b32 s0, s0, 6
	s_sub_i32 s65, 0, s0
	s_lshr_b32 s0, s7, 29
	s_nop 0
	v_readlane_b32 s8, v253, 42
	s_add_i32 s0, s50, s0
	s_nop 0
	v_readlane_b32 s9, v253, 43
	v_readlane_b32 s10, v253, 44
	s_ashr_i32 s8, s0, 3
	s_and_b32 s0, s0, -8
	s_sub_i32 s9, s50, s0
	s_ashr_i32 s10, s61, 31
	s_and_b64 s[0:1], s[16:17], exec
	s_cselect_b32 s0, 1, s61
	v_readlane_b32 s2, v253, 8
	v_writelane_b32 v254, s0, 48
	s_and_b32 s0, s2, 0xffffffe0
	s_bfe_u32 s1, s2, 0x20003
	v_readlane_b32 s4, v253, 38
	s_or_b32 s0, s1, s0
	s_nop 0
	v_readlane_b32 s5, v253, 39
	s_sub_i32 s4, s61, s2
	s_nop 0
	v_writelane_b32 v254, s0, 49
	s_and_b32 s0, s2, 7
	s_nop 0
	v_readlane_b32 s6, v253, 40
	v_readlane_b32 s11, v253, 45
	v_readlane_b32 s12, v253, 46
	v_readlane_b32 s13, v253, 47
	v_readlane_b32 s14, v253, 48
	v_readlane_b32 s15, v253, 49
	s_add_i32 s5, s4, 0xff
	v_writelane_b32 v253, s0, 15
	s_xor_b32 s0, s0, 15
	s_cmpk_gt_i32 s50, 0x3ff
	v_writelane_b32 v254, s0, 10
	s_cselect_b64 s[0:1], -1, 0
	s_and_b32 s2, s50, 7
	v_writelane_b32 v254, s2, 50
	s_ashr_i32 s11, s50, 3
	s_lshr_b32 s2, s7, 26
	s_add_i32 s2, s11, s2
	s_ashr_i32 s3, s2, 6
	s_andn2_b32 s2, s2, 63
	s_lshl_b32 s6, s9, 7
	s_lshl_b32 s3, s3, 3
	s_sub_i32 s12, s11, s2
	v_writelane_b32 v254, s3, 51
	s_and_b64 s[2:3], s[18:19], exec
	s_cselect_b32 s69, 64, 0
	s_sub_i32 s2, 0, s64
	s_nop 0
	v_writelane_b32 v254, s2, 52
	v_writelane_b32 v254, s18, 28
	s_xor_b64 s[2:3], s[18:19], -1
	s_movk_i32 s75, 0x1000
	v_writelane_b32 v254, s19, 29
	v_writelane_b32 v254, s2, 40
	s_movk_i32 s66, 0x2000
	s_movk_i32 s67, 0x7fff
	v_writelane_b32 v254, s3, 41
	s_lshr_b32 s2, s7, 27
	s_add_i32 s2, s11, s2
	s_ashr_i32 s3, s2, 5
	s_lshl_b32 s3, s3, 3
	v_writelane_b32 v254, s3, 53
	s_andn2_b32 s2, s2, 31
	s_nop 0
	v_writelane_b32 v254, s11, 19
	s_sub_i32 s11, s11, s2
	s_nop 0
	v_readlane_b32 s2, v253, 11
	s_cmp_lt_u32 s2, 64
	s_cselect_b64 s[2:3], -1, 0
	v_writelane_b32 v254, s2, 54
	s_or_b64 s[0:1], s[16:17], s[0:1]
	s_nop 0
	v_mov_b32_e32 v220, 0x358637bd
	v_writelane_b32 v254, s3, 55
	s_and_b32 s2, s7, s61
	s_nop 0
	v_writelane_b32 v254, s7, 39
	s_add_i32 s2, s2, s50
	s_nop 0
	v_writelane_b32 v254, s2, 56
	s_ashr_i32 s2, s2, 1
	s_nop 0
	v_writelane_b32 v254, s2, 57
	s_ashr_i32 s2, s2, 31
	s_nop 0
	v_writelane_b32 v254, s2, 58
	s_lshr_b32 s2, s9, 31
	s_nop 0
	v_writelane_b32 v254, s2, 59
	s_cmp_lt_i32 s9, 0
	s_nop 0
	s_mul_i32 s2, s9, 0x81
	s_cselect_b32 s2, s2, s6
	s_add_i32 s2, s2, s8
	s_ashr_i32 s3, s2, 31
	s_lshr_b32 s3, s3, 27
	s_add_i32 s3, s2, s3
	s_ashr_i32 s6, s3, 5
	s_and_b32 s3, s3, 0xffe0
	s_sub_i32 s2, s2, s3
	s_nop 0
	s_bfe_i32 s3, s2, 0x80000
	s_bfe_u32 s3, s3, 0x3000c
	s_add_i32 s3, s2, s3
	s_nop 0
	s_bfe_i32 s7, s3, 0x80000
	s_and_b32 s3, s3, 0xf8
	s_sub_i32 s2, s2, s3
	s_lshl_b32 s6, s6, 3
	s_sext_i32_i16 s7, s7
	s_sext_i32_i8 s2, s2
	s_add_i32 s6, s6, s2
	s_ashr_i32 s7, s7, 3
	v_writelane_b32 v254, s9, 60
	s_and_b64 s[2:3], s[0:1], exec
	s_nop 0
	v_writelane_b32 v254, s8, 61
	s_cselect_b32 s8, 0, s7
	s_and_b64 s[2:3], s[16:17], exec
	s_cselect_b32 s2, s93, s6
	s_abs_i32 s6, s61
	s_waitcnt vmcnt(0)
	v_cvt_f32_u32_e32 v0, s6
	s_xor_b64 s[0:1], s[0:1], -1
	s_or_b64 s[0:1], s[16:17], s[0:1]
	v_writelane_b32 v254, s0, 62
	v_rcp_iflag_f32_e32 v0, v0
	s_nop 0
	v_writelane_b32 v255, s2, 0
	v_writelane_b32 v254, s1, 63
	s_lshl_b32 s0, s2, 8
	s_nop 0
	v_mul_f32_e32 v0, 0x4f7ffffe, v0
	v_cvt_u32_f32_e32 v0, v0
	s_nop 0
	v_writelane_b32 v255, s0, 1
	s_mov_b32 s0, s8
	s_ashr_i32 s9, s8, 31
	v_writelane_b32 v255, s0, 2
	s_sub_i32 s2, 0, s6
	v_readfirstlane_b32 s3, v0
	v_writelane_b32 v255, s1, 3
	s_lshl_b64 s[0:1], s[8:9], 18
	s_nop 0
	v_writelane_b32 v255, s0, 4
	s_mul_i32 s2, s2, s3
	s_mul_hi_u32 s2, s3, s2
	v_writelane_b32 v255, s1, 5
	s_sub_i32 s1, 0xffffff01, s4
	s_max_i32 s1, s5, s1
	s_add_i32 s2, s3, s2
	v_writelane_b32 v255, s2, 6
	s_mul_hi_u32 s2, s1, s2
	s_mul_i32 s3, s2, s6
	s_ashr_i32 s0, s5, 31
	s_sub_i32 s1, s1, s3
	s_xor_b32 s0, s0, s10
	s_add_i32 s3, s2, 1
	s_sub_i32 s4, s1, s6
	s_cmp_ge_u32 s1, s6
	s_cselect_b32 s2, s3, s2
	s_cselect_b32 s1, s4, s1
	s_add_i32 s3, s2, 1
	s_cmp_ge_u32 s1, s6
	s_cselect_b32 s1, s3, s2
	s_xor_b32 s1, s1, s0
	s_sub_i32 s0, s1, s0
	s_nop 0
	v_writelane_b32 v255, s6, 7
	s_lshl_b32 s0, s0, 4
	s_nop 0
	v_writelane_b32 v255, s0, 8
	s_ashr_i32 s0, s12, 31
	s_nop 0
	v_writelane_b32 v255, s0, 9
	v_writelane_b32 v255, s12, 10
	s_abs_i32 s0, s12
	s_nop 0
	v_writelane_b32 v255, s0, 11
	s_ashr_i32 s0, s11, 31
	s_nop 0
	v_writelane_b32 v255, s0, 12
	s_abs_i32 s0, s11
	s_nop 0
	v_writelane_b32 v255, s11, 13
	s_bitcmp1_b32 s61, 0
	s_nop 0
	v_writelane_b32 v254, s10, 38
	v_writelane_b32 v255, s0, 14
	s_cselect_b64 s[0:1], -1, 0
	s_nop 0
	v_writelane_b32 v254, s0, 13
	s_mov_b32 s95, 0xf800000
	v_mbcnt_lo_u32_b32 v0, -1, 0
	v_writelane_b32 v254, s1, 14
	s_add_i32 s0, 0, 0x15200
	v_writelane_b32 v253, s0, 11
	s_add_i32 s0, 0, 0x12200
	v_writelane_b32 v255, s0, 15
	s_add_i32 s0, 0, 0x16300
	v_writelane_b32 v255, s0, 16
	s_add_i32 s0, 0, 0x16700
	v_writelane_b32 v255, s0, 17
	s_add_i32 s0, 0, 0x16280
	v_writelane_b32 v255, s0, 18
	s_add_i32 s0, 0, 0x201c0
	v_writelane_b32 v254, s0, 30
	s_add_i32 s0, 0, 0x20250
	v_writelane_b32 v255, s0, 19
	s_add_i32 s0, 0, 0x201d0
	v_writelane_b32 v255, s0, 20
	s_add_i32 s0, 0, 0x20260
	v_writelane_b32 v255, s0, 21
	s_add_i32 s0, 0, 0x201e0
	v_writelane_b32 v255, s0, 22
	s_add_i32 s0, 0, 0x20270
	v_writelane_b32 v255, s0, 23
	s_add_i32 s0, 0, 0x201f0
	v_writelane_b32 v255, s0, 24
	s_add_i32 s0, 0, 0x20280
	v_writelane_b32 v255, s0, 25
	s_add_i32 s0, 0, 0x20200
	v_writelane_b32 v255, s0, 26
	s_add_i32 s0, 0, 0x20290
	v_writelane_b32 v255, s0, 27
	s_add_i32 s0, 0, 0x20210
	v_writelane_b32 v255, s0, 28
	s_add_i32 s0, 0, 0x20220
	v_writelane_b32 v254, s0, 15
	s_add_i32 s0, 0, 0x201c4
	v_writelane_b32 v255, s0, 29
	s_add_i32 s0, 0, 0x201c8
	v_writelane_b32 v255, s0, 30
	s_add_i32 s0, 0, 0x201cc
	v_writelane_b32 v255, s0, 31
	s_add_i32 s0, 0, 0x201d4
	v_writelane_b32 v255, s0, 32
	s_add_i32 s0, 0, 0x201d8
	v_writelane_b32 v255, s0, 33
	s_add_i32 s0, 0, 0x201dc
	v_writelane_b32 v255, s0, 34
	s_add_i32 s0, 0, 0x201e4
	v_writelane_b32 v255, s0, 35
	s_add_i32 s0, 0, 0x201e8
	v_writelane_b32 v255, s0, 36
	s_add_i32 s0, 0, 0x201ec
	v_writelane_b32 v255, s0, 37
	s_add_i32 s0, 0, 0x201f4
	v_writelane_b32 v255, s0, 38
	s_add_i32 s0, 0, 0x201f8
	v_writelane_b32 v255, s0, 39
	s_add_i32 s0, 0, 0x201fc
	v_writelane_b32 v255, s0, 40
	s_add_i32 s0, 0, 0x20204
	v_writelane_b32 v255, s0, 41
	s_add_i32 s0, 0, 0x20208
	v_writelane_b32 v255, s0, 42
	s_add_i32 s0, 0, 0x2020c
	v_writelane_b32 v255, s0, 43
	s_add_i32 s0, 0, 0x20214
	v_writelane_b32 v255, s0, 44
	s_add_i32 s0, 0, 0x20218
	v_writelane_b32 v255, s0, 45
	s_add_i32 s0, 0, 0x2021c
	v_writelane_b32 v255, s0, 46
	s_add_i32 s0, 0, 0x201a0
	v_writelane_b32 v254, s0, 8
	v_writelane_b32 v254, s42, 34
	v_mov_b32_e32 v221, 0x260
	s_mov_b32 s82, 0xc3e00000
	v_writelane_b32 v254, s43, 35
	v_writelane_b32 v254, s50, 31
	v_mov_b32_e32 v222, 0x3ca908c9
	s_mov_b32 s83, 0x3f2aaaab
	v_mov_b32_e32 v223, 0x3ecc95a3
	v_mov_b32_e32 v225, 0x7f7f7f7f
	v_mov_b32_e32 v226, 0x7a7a7a7a
	v_mov_b32_e32 v228, 0x7d7d7d7d
	v_mbcnt_hi_u32_b32 v227, -1, v0
	v_mov_b32_e32 v229, 0x43e00000
	v_mov_b32_e32 v230, 0x7f800000
	v_mov_b32_e32 v198, 0x3f317218
	v_mov_b32_e32 v231, 0x7fc00000
	v_mov_b32_e32 v232, 0xff800000
	v_mov_b32_e32 v233, 0x300
	v_mov_b32_e32 v234, 0x1800
	v_mov_b64_e32 v[200:201], 0x1e8481
	s_add_i32 s76, 0, 0x10800
	s_add_i32 s77, 0, 0x14800
	s_add_i32 s94, 0, 0x18800
	s_add_i32 s33, 0, 0x1c800
	s_mov_b32 s84, 0x5040100
	s_mov_b32 s85, 0xffff
	s_mov_b64 s[86:87], 0x1000
	s_mov_b32 s74, 0xbfb8aa3b
	s_mov_b64 s[62:63], 0x40000
	s_mov_b32 s4, s97
	s_nop 0
	s_mov_b32 s88, 0x3f803f80
	v_writelane_b32 v255, s65, 47
	v_writelane_b32 v254, s93, 7
	s_branch .LBB0_255
.LBB0_253:
	s_nop 0
	v_readlane_b32 s4, v254, 22
	v_readlane_b32 s36, v254, 5
	s_mov_b32 s92, s89
	s_nop 0
	v_readlane_b32 s5, v254, 23
	v_readlane_b32 s37, v254, 6

.LBB0_255:
	s_nop 0
	v_readlane_b32 s70, v253, 0
	v_readlane_b32 s71, v253, 1
	s_add_u32 s78, s70, 0xee00000
	s_addc_u32 s79, s71, 0
	s_nop 0
	s_add_u32 s0, s70, 0x400000
	s_addc_u32 s1, s71, 0
	s_cmp_lt_u32 s4, 2
	v_writelane_b32 v254, s0, 36
	s_cselect_b64 s[8:9], -1, 0
	s_cmp_lg_u32 s4, 2
	v_writelane_b32 v254, s1, 37
	s_cselect_b64 s[0:1], -1, 0
	s_add_i32 s2, s4, -1
	s_cmp_eq_u32 s4, 2
	s_nop 0
	v_writelane_b32 v254, s0, 24
	s_cselect_b64 s[56:57], -1, 0
	s_waitcnt vmcnt(0)
	v_cndmask_b32_e64 v0, 0, 1, s[8:9]
	v_writelane_b32 v254, s1, 25
	s_and_b64 s[0:1], s[56:57], exec
	s_cselect_b32 s2, 2, s2
	s_cmp_gt_u32 s4, 1
	s_cselect_b64 s[0:1], -1, 0
	v_writelane_b32 v253, s0, 9
	v_writelane_b32 v255, s2, 48
	s_nop 0
	s_nop 0
	v_writelane_b32 v253, s1, 10
	s_and_b64 s[0:1], s[0:1], exec
	s_mov_b32 s0, s4
	s_cselect_b32 s4, s2, s4
	s_cmp_eq_u32 s4, 0
	v_writelane_b32 v254, s0, 22
	s_cselect_b64 s[80:81], -1, 0
	s_nop 0
	v_readlane_b32 s12, v253, 18
	v_writelane_b32 v254, s1, 23
	s_and_b64 s[0:1], s[80:81], exec
	s_nop 0
	v_readlane_b32 s0, v254, 32
	v_readlane_b32 s13, v253, 19
	v_readlane_b32 s1, v254, 33
	s_cselect_b32 s1, s13, s1
	s_cselect_b32 s0, s12, s0
	v_writelane_b32 v254, s0, 20
	s_cmp_lg_u32 s4, 0
	s_cselect_b64 s[2:3], -1, 0
	v_writelane_b32 v254, s1, 21
	s_ashr_i32 s5, s4, 31
	s_nop 0
	s_mul_hi_i32 s1, s4, 0x18000
	v_writelane_b32 v254, s4, 17
	s_mul_i32 s0, s4, 0x18000
	v_writelane_b32 v255, s0, 49
	v_writelane_b32 v254, s5, 18
	v_readlane_b32 s14, v253, 20
	v_writelane_b32 v255, s1, 50
	s_lshl_b64 s[0:1], s[0:1], 2
	s_add_u32 s0, s70, s0
	s_addc_u32 s1, s71, s1
	s_nop 0
	s_add_u32 s60, s0, 0x100000
	s_addc_u32 s72, s1, 0
	s_nop 0
	v_readlane_b32 s4, v254, 5
	v_readlane_b32 s5, v254, 6
	s_cmp_le_i32 s4, s92
	s_cselect_b64 s[0:1], -1, 0
	s_cmp_lt_i32 s92, s5
	s_cselect_b64 s[4:5], -1, 0
	s_and_b64 s[10:11], s[0:1], s[4:5]
	s_andn2_b64 vcc, exec, s[10:11]
	v_cmp_ne_u32_e64 s[0:1], 1, v0
	v_readlane_b32 s15, v253, 21
	v_readlane_b32 s16, v253, 22
	v_readlane_b32 s17, v253, 23
	v_readlane_b32 s18, v253, 24
	v_readlane_b32 s19, v253, 25
	v_readlane_b32 s20, v253, 26
	v_readlane_b32 s21, v253, 27
	v_readlane_b32 s22, v253, 28
	v_readlane_b32 s23, v253, 29
	v_readlane_b32 s24, v253, 30
	v_readlane_b32 s25, v253, 31
	v_readlane_b32 s26, v253, 32
	v_readlane_b32 s27, v253, 33
	s_cbranch_vccnz .LBB0_357
	s_nop 0
	v_readlane_b32 s24, v254, 46
	s_mov_b32 s38, s93
	s_nop 0
	s_mov_b64 s[20:21], 0x810
	s_and_b64 vcc, exec, s[0:1]
	s_nop 0
	v_readlane_b32 s25, v254, 47
	s_cbranch_vccnz .LBB0_258
	s_nop 0
	v_readlane_b32 s6, v254, 17
	v_readlane_b32 s12, v253, 18
	s_mul_i32 s5, s6, 0xc10000
	v_readlane_b32 s16, v253, 22
	s_mul_hi_i32 s4, s6, 0xc10000
	v_readlane_b32 s17, v253, 23
	s_add_u32 s5, s16, s5
	s_nop 0
	v_readlane_b32 s24, v253, 30
	s_addc_u32 s4, s17, s4
	s_nop 0
	v_readlane_b32 s20, v253, 26
	v_readlane_b32 s21, v253, 27
	v_readlane_b32 s25, v253, 31
	s_add_u32 s24, s5, 0x3000
	s_addc_u32 s25, s4, 0
	s_nop 0
	s_mov_b64 s[20:21], 0xc10
	v_readlane_b32 s7, v254, 18
	v_readlane_b32 s13, v253, 19
	v_readlane_b32 s14, v253, 20
	v_readlane_b32 s15, v253, 21
	v_readlane_b32 s18, v253, 24
	v_readlane_b32 s19, v253, 25
	v_readlane_b32 s22, v253, 28
	v_readlane_b32 s23, v253, 29
	v_readlane_b32 s26, v253, 32
	v_readlane_b32 s27, v253, 33
.LBB0_258:
	v_readlane_b32 s4, v254, 17
	v_readlane_b32 s5, v254, 18
	s_lshl_b32 s4, s4, 10
	s_nop 0
	v_readlane_b32 s40, v253, 34
	s_ashr_i32 s5, s4, 31
	s_nop 0
	v_readlane_b32 s46, v253, 40
	v_readlane_b32 s47, v253, 41
	v_readlane_b32 s50, v253, 44
	v_readlane_b32 s51, v253, 45
	s_lshl_b64 s[4:5], s[4:5], 2
	s_mov_b64 s[46:47], s[50:51]
	s_add_u32 s6, s46, s4
	s_nop 0
	v_readlane_b32 s41, v253, 35
	v_readlane_b32 s42, v253, 36
	v_readlane_b32 s43, v253, 37
	v_readlane_b32 s44, v253, 38
	v_readlane_b32 s45, v253, 39
	v_readlane_b32 s48, v253, 42
	v_readlane_b32 s49, v253, 43
	v_readlane_b32 s52, v253, 46
	v_readlane_b32 s53, v253, 47
	v_readlane_b32 s54, v253, 48
	v_readlane_b32 s55, v253, 49
	s_addc_u32 s7, s47, s5
	s_and_b64 s[4:5], s[56:57], exec
	v_readlane_b32 s40, v253, 18
	s_movk_i32 s4, 0x800
	s_nop 0
	v_readlane_b32 s52, v253, 30
	v_readlane_b32 s53, v253, 31
	s_cselect_b32 s26, s4, 0x1800
	s_cselect_b32 s5, s53, s7
	s_cselect_b32 s4, s52, s6
	s_add_u32 s12, s70, 0x280000
	s_addc_u32 s13, s71, 0
	s_and_b64 s[6:7], s[56:57], exec
	s_mov_b32 s6, s97
	s_cselect_b32 s12, s12, s60
	s_cselect_b32 s13, s13, s72
	s_nop 0
	v_mbcnt_lo_u32_b32 v0, -1, s6
	s_add_u32 s14, s12, 0x1000
	v_mbcnt_hi_u32_b32 v0, -1, v0
	s_addc_u32 s15, s13, 0
	v_add_u32_e32 v142, s64, v0
	s_mov_b32 s27, s38
	s_cmpk_lt_i32 s27, 0x100
	s_cselect_b64 s[6:7], -1, 0
	s_and_b64 s[16:17], s[2:3], s[6:7]
	v_cndmask_b32_e64 v0, 0, 1, s[16:17]
	s_mov_b32 s93, s38
	v_readfirstlane_b32 s21, v142
	v_mov_b32_e64 v170, 0
	v_cmp_ne_u32_e64 s[2:3], 1, v0
	s_andn2_b64 vcc, exec, s[16:17]
	v_ashrrev_i32_e32 v143, 31, v142
	v_mov_b32_e32 v171, 0
	v_mov_b32_e32 v172, 0
	v_mov_b32_e32 v173, 0
	v_mov_b32_e32 v168, 0
	v_mov_b32_e64 v169, 0
	v_readlane_b32 s41, v253, 19
	v_readlane_b32 s42, v253, 20
	v_readlane_b32 s43, v253, 21
	v_readlane_b32 s44, v253, 22
	v_readlane_b32 s45, v253, 23
	v_readlane_b32 s46, v253, 24
	v_readlane_b32 s47, v253, 25
	v_readlane_b32 s48, v253, 26
	v_readlane_b32 s49, v253, 27
	v_readlane_b32 s50, v253, 28
	v_readlane_b32 s51, v253, 29
	v_readlane_b32 s54, v253, 32
	v_readlane_b32 s55, v253, 33
	s_cbranch_vccnz .LBB0_260
	s_ashr_i32 s18, s27, 4
	v_lshl_add_u64 v[0:1], v[142:143], 2, s[4:5]
	global_load_dword v169, v[0:1], off
	global_load_dword v168, v[0:1], off offset:2048
	v_mov_b32_e64 v0, s18
	v_mad_i64_i32 v[0:1], s[18:19], s26, v0, v[142:143]
	v_lshlrev_b64 v[0:1], 2, v[0:1]
	v_lshl_add_u64 v[2:3], s[14:15], 0, v[0:1]
	v_lshl_add_u64 v[0:1], s[12:13], 0, v[0:1]
	global_load_dword v173, v[2:3], off
	global_load_dword v172, v[2:3], off offset:2048
	global_load_dword v171, v[0:1], off
	global_load_dword v170, v[0:1], off offset:2048
.LBB0_260:
	v_readlane_b32 s18, v254, 22
	v_readlane_b32 s19, v254, 23
	s_mov_b32 s22, s18
	s_cmp_lt_u32 s18, 3
	v_and_b32_e32 v174, 15, v142
	s_nop 0
	v_add_u32_e32 v0, 0x200, v142
	v_add_u32_e32 v1, 0x400, v142
	v_add_u32_e32 v2, 0x600, v142
	v_add_u32_e32 v3, 0x800, v142
	v_add_u32_e32 v4, 0xa00, v142
	v_add_u32_e32 v5, 0xc00, v142
	v_add_u32_e32 v6, 0xe00, v142
	v_add_u32_e32 v7, 0x1000, v142
	v_add_u32_e32 v8, 0x1200, v142
	v_add_u32_e32 v9, 0x1400, v142
	v_add_u32_e32 v10, 0x1600, v142
	v_add_u32_e32 v11, 0x1800, v142
	v_add_u32_e32 v12, 0x1a00, v142
	v_add_u32_e32 v13, 0x1c00, v142
	v_add_u32_e32 v14, 0x1e00, v142
	v_add_u32_e32 v15, 0x2000, v142
	v_add_u32_e32 v16, 0x2200, v142
	v_add_u32_e32 v17, 0x2400, v142
	v_add_u32_e32 v18, 0x2600, v142
	v_add_u32_e32 v19, 0x2800, v142
	v_add_u32_e32 v20, 0x2a00, v142
	v_add_u32_e32 v21, 0x2c00, v142
	v_add_u32_e32 v22, 0x2e00, v142
	v_add_u32_e32 v23, 0x3000, v142
	v_add_u32_e32 v24, 0x3200, v142
	v_add_u32_e32 v25, 0x3400, v142
	v_add_u32_e32 v26, 0x3600, v142
	v_add_u32_e32 v27, 0x3800, v142
	v_add_u32_e32 v28, 0x3a00, v142
	v_add_u32_e32 v29, 0x3c00, v142
	v_add_u32_e32 v30, 0x3e00, v142
	s_cselect_b64 s[18:19], -1, 0
	s_cmp_gt_u32 s22, 2
	v_lshlrev_b32_e32 v96, 2, v174
	v_ashrrev_i32_e32 v178, 4, v142
	v_ashrrev_i32_e32 v186, 4, v0
	v_ashrrev_i32_e32 v184, 4, v1
	v_ashrrev_i32_e32 v181, 4, v2
	v_ashrrev_i32_e32 v177, 4, v3
	v_ashrrev_i32_e32 v167, 4, v4
	v_ashrrev_i32_e32 v164, 4, v5
	v_ashrrev_i32_e32 v162, 4, v6
	v_ashrrev_i32_e32 v160, 4, v7
	v_ashrrev_i32_e32 v158, 4, v8
	v_ashrrev_i32_e32 v157, 4, v9
	v_ashrrev_i32_e32 v154, 4, v10
	v_ashrrev_i32_e32 v153, 4, v11
	v_ashrrev_i32_e32 v152, 4, v12
	v_ashrrev_i32_e32 v151, 4, v13
	v_ashrrev_i32_e32 v150, 4, v14
	v_ashrrev_i32_e32 v149, 4, v15
	v_ashrrev_i32_e32 v148, 4, v16
	v_ashrrev_i32_e32 v147, 4, v17
	v_ashrrev_i32_e32 v146, 4, v18
	v_ashrrev_i32_e32 v145, 4, v19
	v_ashrrev_i32_e32 v144, 4, v20
	v_ashrrev_i32_e32 v141, 4, v21
	v_ashrrev_i32_e32 v140, 4, v22
	v_ashrrev_i32_e32 v139, 4, v23
	v_ashrrev_i32_e32 v138, 4, v24
	v_ashrrev_i32_e32 v137, 4, v25
	v_ashrrev_i32_e32 v136, 4, v26
	v_ashrrev_i32_e32 v135, 4, v27
	v_ashrrev_i32_e32 v134, 4, v28
	v_ashrrev_i32_e32 v133, 4, v29
	v_ashrrev_i32_e32 v132, 4, v30
	s_cbranch_scc1 .LBB0_262
	v_lshl_add_u64 v[0:1], s[24:25], 0, v[96:97]
	v_mad_i64_i32 v[2:3], s[22:23], s20, v178, 0
	v_lshl_add_u64 v[2:3], v[2:3], 2, v[0:1]
	v_mad_i64_i32 v[4:5], s[22:23], s20, v186, 0
	v_mad_i64_i32 v[6:7], s[22:23], s20, v184, 0
	v_mad_i64_i32 v[8:9], s[22:23], s20, v181, 0
	v_mad_i64_i32 v[10:11], s[22:23], s20, v177, 0
	v_mad_i64_i32 v[12:13], s[22:23], s20, v167, 0
	v_mad_i64_i32 v[14:15], s[22:23], s20, v164, 0
	v_mad_i64_i32 v[16:17], s[22:23], s20, v162, 0
	v_lshl_add_u64 v[4:5], v[4:5], 2, v[0:1]
	v_lshl_add_u64 v[6:7], v[6:7], 2, v[0:1]
	v_lshl_add_u64 v[8:9], v[8:9], 2, v[0:1]
	v_lshl_add_u64 v[10:11], v[10:11], 2, v[0:1]
	v_lshl_add_u64 v[12:13], v[12:13], 2, v[0:1]
	v_lshl_add_u64 v[14:15], v[14:15], 2, v[0:1]
	v_lshl_add_u64 v[16:17], v[16:17], 2, v[0:1]
	global_load_dword v208, v[2:3], off
	global_load_dword v207, v[4:5], off
	global_load_dword v206, v[6:7], off
	global_load_dword v205, v[8:9], off
	global_load_dword v204, v[10:11], off
	global_load_dword v202, v[12:13], off
	global_load_dword v197, v[14:15], off
	global_load_dword v195, v[16:17], off
	v_mad_i64_i32 v[2:3], s[22:23], s20, v160, 0
	v_lshl_add_u64 v[2:3], v[2:3], 2, v[0:1]
	v_mad_i64_i32 v[4:5], s[22:23], s20, v158, 0
	v_mad_i64_i32 v[6:7], s[22:23], s20, v157, 0
	v_mad_i64_i32 v[8:9], s[22:23], s20, v154, 0
	v_mad_i64_i32 v[10:11], s[22:23], s20, v153, 0
	v_mad_i64_i32 v[12:13], s[22:23], s20, v152, 0
	v_mad_i64_i32 v[14:15], s[22:23], s20, v151, 0
	v_mad_i64_i32 v[16:17], s[22:23], s20, v150, 0
	v_lshl_add_u64 v[4:5], v[4:5], 2, v[0:1]
	v_lshl_add_u64 v[6:7], v[6:7], 2, v[0:1]
	v_lshl_add_u64 v[8:9], v[8:9], 2, v[0:1]
	v_lshl_add_u64 v[10:11], v[10:11], 2, v[0:1]
	v_lshl_add_u64 v[12:13], v[12:13], 2, v[0:1]
	v_lshl_add_u64 v[14:15], v[14:15], 2, v[0:1]
	v_lshl_add_u64 v[16:17], v[16:17], 2, v[0:1]
	global_load_dword v203, v[2:3], off
	global_load_dword v199, v[4:5], off
	global_load_dword v196, v[6:7], off
	global_load_dword v194, v[8:9], off
	global_load_dword v193, v[10:11], off
	global_load_dword v191, v[12:13], off
	global_load_dword v189, v[14:15], off
	global_load_dword v187, v[16:17], off
	v_mad_i64_i32 v[2:3], s[22:23], s20, v149, 0
	v_lshl_add_u64 v[2:3], v[2:3], 2, v[0:1]
	v_mad_i64_i32 v[4:5], s[22:23], s20, v148, 0
	v_mad_i64_i32 v[6:7], s[22:23], s20, v147, 0
	v_mad_i64_i32 v[8:9], s[22:23], s20, v146, 0
	v_mad_i64_i32 v[10:11], s[22:23], s20, v145, 0
	v_mad_i64_i32 v[12:13], s[22:23], s20, v144, 0
	v_mad_i64_i32 v[14:15], s[22:23], s20, v141, 0
	v_mad_i64_i32 v[16:17], s[22:23], s20, v140, 0
	v_lshl_add_u64 v[4:5], v[4:5], 2, v[0:1]
	v_lshl_add_u64 v[6:7], v[6:7], 2, v[0:1]
	v_lshl_add_u64 v[8:9], v[8:9], 2, v[0:1]
	v_lshl_add_u64 v[10:11], v[10:11], 2, v[0:1]
	v_lshl_add_u64 v[12:13], v[12:13], 2, v[0:1]
	v_lshl_add_u64 v[14:15], v[14:15], 2, v[0:1]
	v_lshl_add_u64 v[16:17], v[16:17], 2, v[0:1]
	global_load_dword v192, v[2:3], off
	global_load_dword v190, v[4:5], off
	global_load_dword v188, v[6:7], off
	global_load_dword v185, v[8:9], off
	global_load_dword v183, v[10:11], off
	global_load_dword v180, v[12:13], off
	global_load_dword v176, v[14:15], off
	global_load_dword v166, v[16:17], off
	v_mad_i64_i32 v[2:3], s[22:23], s20, v139, 0
	v_lshl_add_u64 v[2:3], v[2:3], 2, v[0:1]
	v_mad_i64_i32 v[4:5], s[22:23], s20, v138, 0
	v_mad_i64_i32 v[6:7], s[22:23], s20, v137, 0
	v_mad_i64_i32 v[8:9], s[22:23], s20, v136, 0
	v_mad_i64_i32 v[10:11], s[22:23], s20, v135, 0
	v_mad_i64_i32 v[12:13], s[22:23], s20, v134, 0
	v_mad_i64_i32 v[14:15], s[22:23], s20, v133, 0
	v_mad_i64_i32 v[16:17], s[22:23], s20, v132, 0
	v_lshl_add_u64 v[4:5], v[4:5], 2, v[0:1]
	v_lshl_add_u64 v[6:7], v[6:7], 2, v[0:1]
	v_lshl_add_u64 v[8:9], v[8:9], 2, v[0:1]
	v_lshl_add_u64 v[10:11], v[10:11], 2, v[0:1]
	v_lshl_add_u64 v[12:13], v[12:13], 2, v[0:1]
	v_lshl_add_u64 v[14:15], v[14:15], 2, v[0:1]
	v_lshl_add_u64 v[0:1], v[16:17], 2, v[0:1]
	global_load_dword v182, v[2:3], off
	global_load_dword v179, v[4:5], off
	global_load_dword v175, v[6:7], off
	global_load_dword v165, v[8:9], off
	global_load_dword v163, v[10:11], off
	global_load_dword v161, v[12:13], off
	global_load_dword v159, v[14:15], off
	global_load_dword v156, v[0:1], off
.LBB0_262:
	v_bfe_u32 v155, v142, 4, 2
	v_readlane_b32 s42, v254, 34
	s_ashr_i32 s20, s21, 6
	s_and_b64 vcc, exec, s[2:3]
	v_lshlrev_b32_e32 v98, 5, v155
	s_nop 0
	v_readlane_b32 s43, v254, 35
	v_readlane_b32 s50, v254, 31
	s_cbranch_vccnz .LBB0_266
	s_lshl_b32 s2, s27, 8
	s_lshl_b32 s3, s20, 5
	s_add_i32 s3, s3, s2
	v_or_b32_e32 v0, s3, v174
	v_ashrrev_i32_e32 v1, 31, v0
	v_readlane_b32 s2, v254, 32
	v_lshlrev_b64 v[0:1], 11, v[0:1]
	v_readlane_b32 s3, v254, 33
	v_mov_b32_e32 v99, v97
	s_nop 0
	v_lshl_add_u64 v[0:1], s[2:3], 0, v[0:1]
	v_lshl_add_u64 v[124:125], v[0:1], 0, v[98:99]
	global_load_dwordx4 v[4:7], v[124:125], off offset:16
	global_load_dwordx4 v[0:3], v[124:125], off
	global_load_dwordx4 v[12:15], v[124:125], off offset:144
	global_load_dwordx4 v[8:11], v[124:125], off offset:128
	global_load_dwordx4 v[20:23], v[124:125], off offset:272
	global_load_dwordx4 v[16:19], v[124:125], off offset:256
	global_load_dwordx4 v[28:31], v[124:125], off offset:400
	global_load_dwordx4 v[24:27], v[124:125], off offset:384
	global_load_dwordx4 v[36:39], v[124:125], off offset:528
	global_load_dwordx4 v[32:35], v[124:125], off offset:512
	global_load_dwordx4 v[44:47], v[124:125], off offset:656
	global_load_dwordx4 v[40:43], v[124:125], off offset:640
	global_load_dwordx4 v[52:55], v[124:125], off offset:784
	global_load_dwordx4 v[48:51], v[124:125], off offset:768
	global_load_dwordx4 v[60:63], v[124:125], off offset:912
	global_load_dwordx4 v[56:59], v[124:125], off offset:896
	global_load_dwordx4 v[68:71], v[124:125], off offset:1040
	global_load_dwordx4 v[64:67], v[124:125], off offset:1024
	global_load_dwordx4 v[76:79], v[124:125], off offset:1168
	global_load_dwordx4 v[72:75], v[124:125], off offset:1152
	global_load_dwordx4 v[84:87], v[124:125], off offset:1296
	global_load_dwordx4 v[80:83], v[124:125], off offset:1280
	global_load_dwordx4 v[92:95], v[124:125], off offset:1424
	global_load_dwordx4 v[88:91], v[124:125], off offset:1408
	global_load_dwordx4 v[104:107], v[124:125], off offset:1552
	global_load_dwordx4 v[100:103], v[124:125], off offset:1536
	global_load_dwordx4 v[112:115], v[124:125], off offset:1680
	global_load_dwordx4 v[108:111], v[124:125], off offset:1664
	global_load_dwordx4 v[120:123], v[124:125], off offset:1808
	global_load_dwordx4 v[116:119], v[124:125], off offset:1792
	global_load_dwordx4 v[128:131], v[124:125], off offset:1936
	s_nop 0
	s_nop 0
	global_load_dwordx4 v[124:127], v[124:125], off offset:1920
	v_cndmask_b32_e64 v99, 0, 1, s[18:19]
	v_cmp_ne_u32_e64 s[2:3], 1, v99
	s_andn2_b64 vcc, exec, s[18:19]
	s_cbranch_vccz .LBB0_267

.LBB0_267:
	s_movk_i32 s18, 0x408
	s_waitcnt vmcnt(31)
	v_bfe_u32 v99, v208, 16, 1
	v_mad_u32_u24 v178, v174, s18, v178
	v_add3_u32 v99, v208, v99, s67
	v_lshl_add_u32 v178, v178, 1, 0
	ds_write_b16_d16_hi v178, v99 offset:8192
	v_and_b32_e32 v99, 0xffff0000, v99
	v_sub_f32_e64 v99, v208, v99
	v_bfe_u32 v208, v99, 16, 1
	v_add3_u32 v99, v99, v208, s67
	ds_write_b16_d16_hi v178, v99 offset:41216
	s_waitcnt vmcnt(30)
	s_nop 0
	v_bfe_u32 v99, v207, 16, 1
	v_mad_u32_u24 v178, v174, s18, v186
	v_add3_u32 v99, v207, v99, s67
	v_lshl_add_u32 v178, v178, 1, 0
	ds_write_b16_d16_hi v178, v99 offset:8192
	v_and_b32_e32 v99, 0xffff0000, v99
	v_sub_f32_e64 v99, v207, v99
	v_bfe_u32 v186, v99, 16, 1
	v_add3_u32 v99, v99, v186, s67
	ds_write_b16_d16_hi v178, v99 offset:41216
	s_waitcnt vmcnt(29)
	s_nop 0
	v_bfe_u32 v99, v206, 16, 1
	v_mad_u32_u24 v178, v174, s18, v184
	v_add3_u32 v99, v206, v99, s67
	v_lshl_add_u32 v178, v178, 1, 0
	ds_write_b16_d16_hi v178, v99 offset:8192
	v_and_b32_e32 v99, 0xffff0000, v99
	v_sub_f32_e64 v99, v206, v99
	v_bfe_u32 v184, v99, 16, 1
	v_add3_u32 v99, v99, v184, s67
	ds_write_b16_d16_hi v178, v99 offset:41216
	s_waitcnt vmcnt(28)
	s_nop 0
	v_bfe_u32 v99, v205, 16, 1
	v_mad_u32_u24 v178, v174, s18, v181
	v_add3_u32 v99, v205, v99, s67
	v_lshl_add_u32 v178, v178, 1, 0
	ds_write_b16_d16_hi v178, v99 offset:8192
	v_and_b32_e32 v99, 0xffff0000, v99
	v_sub_f32_e64 v99, v205, v99
	v_bfe_u32 v181, v99, 16, 1
	v_add3_u32 v99, v99, v181, s67
	ds_write_b16_d16_hi v178, v99 offset:41216
	s_waitcnt vmcnt(27)
	s_nop 0
	v_bfe_u32 v99, v204, 16, 1
	v_mad_u32_u24 v177, v174, s18, v177
	v_add3_u32 v99, v204, v99, s67
	v_lshl_add_u32 v177, v177, 1, 0
	ds_write_b16_d16_hi v177, v99 offset:8192
	v_and_b32_e32 v99, 0xffff0000, v99
	v_sub_f32_e64 v99, v204, v99
	v_bfe_u32 v178, v99, 16, 1
	v_add3_u32 v99, v99, v178, s67
	ds_write_b16_d16_hi v177, v99 offset:41216
	s_waitcnt vmcnt(26)
	s_nop 0
	v_bfe_u32 v99, v202, 16, 1
	v_mad_u32_u24 v167, v174, s18, v167
	v_add3_u32 v99, v202, v99, s67
	v_lshl_add_u32 v167, v167, 1, 0
	ds_write_b16_d16_hi v167, v99 offset:8192
	v_and_b32_e32 v99, 0xffff0000, v99
	v_sub_f32_e64 v99, v202, v99
	v_bfe_u32 v177, v99, 16, 1
	v_add3_u32 v99, v99, v177, s67
	ds_write_b16_d16_hi v167, v99 offset:41216
	s_waitcnt vmcnt(25)
	s_nop 0
	v_bfe_u32 v99, v197, 16, 1
	v_mad_u32_u24 v164, v174, s18, v164
	v_add3_u32 v99, v197, v99, s67
	v_lshl_add_u32 v164, v164, 1, 0
	ds_write_b16_d16_hi v164, v99 offset:8192
	v_and_b32_e32 v99, 0xffff0000, v99
	v_sub_f32_e64 v99, v197, v99
	v_bfe_u32 v167, v99, 16, 1
	v_add3_u32 v99, v99, v167, s67
	ds_write_b16_d16_hi v164, v99 offset:41216
	s_waitcnt vmcnt(24)
	s_nop 0
	v_bfe_u32 v99, v195, 16, 1
	v_mad_u32_u24 v162, v174, s18, v162
	v_add3_u32 v99, v195, v99, s67
	v_lshl_add_u32 v162, v162, 1, 0
	ds_write_b16_d16_hi v162, v99 offset:8192
	v_and_b32_e32 v99, 0xffff0000, v99
	v_sub_f32_e64 v99, v195, v99
	v_bfe_u32 v164, v99, 16, 1
	v_add3_u32 v99, v99, v164, s67
	ds_write_b16_d16_hi v162, v99 offset:41216
	s_waitcnt vmcnt(23)
	s_nop 0
	v_bfe_u32 v99, v203, 16, 1
	v_mad_u32_u24 v160, v174, s18, v160
	v_add3_u32 v99, v203, v99, s67
	v_lshl_add_u32 v160, v160, 1, 0
	ds_write_b16_d16_hi v160, v99 offset:8192
	v_and_b32_e32 v99, 0xffff0000, v99
	v_sub_f32_e64 v99, v203, v99
	v_bfe_u32 v162, v99, 16, 1
	v_add3_u32 v99, v99, v162, s67
	ds_write_b16_d16_hi v160, v99 offset:41216
	s_waitcnt vmcnt(22)
	s_nop 0
	v_bfe_u32 v99, v199, 16, 1
	v_mad_u32_u24 v158, v174, s18, v158
	v_add3_u32 v99, v199, v99, s67
	v_lshl_add_u32 v158, v158, 1, 0
	ds_write_b16_d16_hi v158, v99 offset:8192
	v_and_b32_e32 v99, 0xffff0000, v99
	v_sub_f32_e64 v99, v199, v99
	v_bfe_u32 v160, v99, 16, 1
	v_add3_u32 v99, v99, v160, s67
	ds_write_b16_d16_hi v158, v99 offset:41216
	s_waitcnt vmcnt(21)
	s_nop 0
	v_bfe_u32 v99, v196, 16, 1
	v_mad_u32_u24 v157, v174, s18, v157
	v_add3_u32 v99, v196, v99, s67
	v_lshl_add_u32 v157, v157, 1, 0
	ds_write_b16_d16_hi v157, v99 offset:8192
	v_and_b32_e32 v99, 0xffff0000, v99
	v_sub_f32_e64 v99, v196, v99
	v_bfe_u32 v158, v99, 16, 1
	v_add3_u32 v99, v99, v158, s67
	ds_write_b16_d16_hi v157, v99 offset:41216
	s_waitcnt vmcnt(20)
	s_nop 0
	v_bfe_u32 v99, v194, 16, 1
	v_mad_u32_u24 v154, v174, s18, v154
	v_add3_u32 v99, v194, v99, s67
	v_lshl_add_u32 v154, v154, 1, 0
	ds_write_b16_d16_hi v154, v99 offset:8192
	v_and_b32_e32 v99, 0xffff0000, v99
	v_sub_f32_e64 v99, v194, v99
	v_bfe_u32 v157, v99, 16, 1
	v_add3_u32 v99, v99, v157, s67
	ds_write_b16_d16_hi v154, v99 offset:41216
	s_waitcnt vmcnt(19)
	s_nop 0
	v_bfe_u32 v99, v193, 16, 1
	v_mad_u32_u24 v153, v174, s18, v153
	v_add3_u32 v99, v193, v99, s67
	v_lshl_add_u32 v153, v153, 1, 0
	ds_write_b16_d16_hi v153, v99 offset:8192
	v_and_b32_e32 v99, 0xffff0000, v99
	v_sub_f32_e64 v99, v193, v99
	v_bfe_u32 v154, v99, 16, 1
	v_add3_u32 v99, v99, v154, s67
	ds_write_b16_d16_hi v153, v99 offset:41216
	s_waitcnt vmcnt(18)
	s_nop 0
	v_bfe_u32 v99, v191, 16, 1
	v_mad_u32_u24 v152, v174, s18, v152
	v_add3_u32 v99, v191, v99, s67
	v_lshl_add_u32 v152, v152, 1, 0
	ds_write_b16_d16_hi v152, v99 offset:8192
	v_and_b32_e32 v99, 0xffff0000, v99
	v_sub_f32_e64 v99, v191, v99
	v_bfe_u32 v153, v99, 16, 1
	v_add3_u32 v99, v99, v153, s67
	ds_write_b16_d16_hi v152, v99 offset:41216
	s_waitcnt vmcnt(17)
	s_nop 0
	v_bfe_u32 v99, v189, 16, 1
	v_mad_u32_u24 v151, v174, s18, v151
	v_add3_u32 v99, v189, v99, s67
	v_lshl_add_u32 v151, v151, 1, 0
	ds_write_b16_d16_hi v151, v99 offset:8192
	v_and_b32_e32 v99, 0xffff0000, v99
	v_sub_f32_e64 v99, v189, v99
	v_bfe_u32 v152, v99, 16, 1
	v_add3_u32 v99, v99, v152, s67
	ds_write_b16_d16_hi v151, v99 offset:41216
	s_waitcnt vmcnt(16)
	s_nop 0
	v_bfe_u32 v99, v187, 16, 1
	v_mad_u32_u24 v150, v174, s18, v150
	v_add3_u32 v99, v187, v99, s67
	v_lshl_add_u32 v150, v150, 1, 0
	ds_write_b16_d16_hi v150, v99 offset:8192
	v_and_b32_e32 v99, 0xffff0000, v99
	v_sub_f32_e64 v99, v187, v99
	v_bfe_u32 v151, v99, 16, 1
	v_add3_u32 v99, v99, v151, s67
	ds_write_b16_d16_hi v150, v99 offset:41216
	s_waitcnt vmcnt(15)
	s_nop 0
	v_bfe_u32 v99, v192, 16, 1
	v_mad_u32_u24 v149, v174, s18, v149
	v_add3_u32 v99, v192, v99, s67
	v_lshl_add_u32 v149, v149, 1, 0
	ds_write_b16_d16_hi v149, v99 offset:8192
	v_and_b32_e32 v99, 0xffff0000, v99
	v_sub_f32_e64 v99, v192, v99
	v_bfe_u32 v150, v99, 16, 1
	v_add3_u32 v99, v99, v150, s67
	ds_write_b16_d16_hi v149, v99 offset:41216
	s_waitcnt vmcnt(14)
	s_nop 0
	v_bfe_u32 v99, v190, 16, 1
	v_mad_u32_u24 v148, v174, s18, v148
	v_add3_u32 v99, v190, v99, s67
	v_lshl_add_u32 v148, v148, 1, 0
	ds_write_b16_d16_hi v148, v99 offset:8192
	v_and_b32_e32 v99, 0xffff0000, v99
	v_sub_f32_e64 v99, v190, v99
	v_bfe_u32 v149, v99, 16, 1
	v_add3_u32 v99, v99, v149, s67
	ds_write_b16_d16_hi v148, v99 offset:41216
	s_waitcnt vmcnt(13)
	s_nop 0
	v_bfe_u32 v99, v188, 16, 1
	v_mad_u32_u24 v147, v174, s18, v147
	v_add3_u32 v99, v188, v99, s67
	v_lshl_add_u32 v147, v147, 1, 0
	ds_write_b16_d16_hi v147, v99 offset:8192
	v_and_b32_e32 v99, 0xffff0000, v99
	v_sub_f32_e64 v99, v188, v99
	v_bfe_u32 v148, v99, 16, 1
	v_add3_u32 v99, v99, v148, s67
	ds_write_b16_d16_hi v147, v99 offset:41216
	s_waitcnt vmcnt(12)
	s_nop 0
	v_bfe_u32 v99, v185, 16, 1
	v_mad_u32_u24 v146, v174, s18, v146
	v_add3_u32 v99, v185, v99, s67
	v_lshl_add_u32 v146, v146, 1, 0
	ds_write_b16_d16_hi v146, v99 offset:8192
	v_and_b32_e32 v99, 0xffff0000, v99
	v_sub_f32_e64 v99, v185, v99
	v_bfe_u32 v147, v99, 16, 1
	v_add3_u32 v99, v99, v147, s67
	ds_write_b16_d16_hi v146, v99 offset:41216
	s_waitcnt vmcnt(11)
	s_nop 0
	v_bfe_u32 v99, v183, 16, 1
	v_mad_u32_u24 v145, v174, s18, v145
	v_add3_u32 v99, v183, v99, s67
	v_lshl_add_u32 v145, v145, 1, 0
	ds_write_b16_d16_hi v145, v99 offset:8192
	v_and_b32_e32 v99, 0xffff0000, v99
	v_sub_f32_e64 v99, v183, v99
	v_bfe_u32 v146, v99, 16, 1
	v_add3_u32 v99, v99, v146, s67
	ds_write_b16_d16_hi v145, v99 offset:41216
	s_waitcnt vmcnt(10)
	s_nop 0
	v_bfe_u32 v99, v180, 16, 1
	v_mad_u32_u24 v144, v174, s18, v144
	v_add3_u32 v99, v180, v99, s67
	v_lshl_add_u32 v144, v144, 1, 0
	ds_write_b16_d16_hi v144, v99 offset:8192
	v_and_b32_e32 v99, 0xffff0000, v99
	v_sub_f32_e64 v99, v180, v99
	v_bfe_u32 v145, v99, 16, 1
	v_add3_u32 v99, v99, v145, s67
	ds_write_b16_d16_hi v144, v99 offset:41216
	s_waitcnt vmcnt(9)
	s_nop 0
	v_bfe_u32 v99, v176, 16, 1
	v_mad_u32_u24 v141, v174, s18, v141
	v_add3_u32 v99, v176, v99, s67
	v_lshl_add_u32 v141, v141, 1, 0
	ds_write_b16_d16_hi v141, v99 offset:8192
	v_and_b32_e32 v99, 0xffff0000, v99
	v_sub_f32_e64 v99, v176, v99
	v_bfe_u32 v144, v99, 16, 1
	v_add3_u32 v99, v99, v144, s67
	ds_write_b16_d16_hi v141, v99 offset:41216
	s_waitcnt vmcnt(8)
	s_nop 0
	v_bfe_u32 v99, v166, 16, 1
	v_mad_u32_u24 v140, v174, s18, v140
	v_add3_u32 v99, v166, v99, s67
	v_lshl_add_u32 v140, v140, 1, 0
	ds_write_b16_d16_hi v140, v99 offset:8192
	v_and_b32_e32 v99, 0xffff0000, v99
	v_sub_f32_e64 v99, v166, v99
	v_bfe_u32 v141, v99, 16, 1
	v_add3_u32 v99, v99, v141, s67
	ds_write_b16_d16_hi v140, v99 offset:41216
	s_waitcnt vmcnt(7)
	s_nop 0
	v_bfe_u32 v99, v182, 16, 1
	v_mad_u32_u24 v139, v174, s18, v139
	v_add3_u32 v99, v182, v99, s67
	v_lshl_add_u32 v139, v139, 1, 0
	ds_write_b16_d16_hi v139, v99 offset:8192
	v_and_b32_e32 v99, 0xffff0000, v99
	v_sub_f32_e64 v99, v182, v99
	v_bfe_u32 v140, v99, 16, 1
	v_add3_u32 v99, v99, v140, s67
	ds_write_b16_d16_hi v139, v99 offset:41216
	s_waitcnt vmcnt(6)
	s_nop 0
	v_bfe_u32 v99, v179, 16, 1
	v_mad_u32_u24 v138, v174, s18, v138
	v_add3_u32 v99, v179, v99, s67
	v_lshl_add_u32 v138, v138, 1, 0
	ds_write_b16_d16_hi v138, v99 offset:8192
	v_and_b32_e32 v99, 0xffff0000, v99
	v_sub_f32_e64 v99, v179, v99
	v_bfe_u32 v139, v99, 16, 1
	v_add3_u32 v99, v99, v139, s67
	ds_write_b16_d16_hi v138, v99 offset:41216
	s_waitcnt vmcnt(5)
	s_nop 0
	v_bfe_u32 v99, v175, 16, 1
	v_mad_u32_u24 v137, v174, s18, v137
	v_add3_u32 v99, v175, v99, s67
	v_lshl_add_u32 v137, v137, 1, 0
	ds_write_b16_d16_hi v137, v99 offset:8192
	v_and_b32_e32 v99, 0xffff0000, v99
	v_sub_f32_e64 v99, v175, v99
	v_bfe_u32 v138, v99, 16, 1
	v_add3_u32 v99, v99, v138, s67
	ds_write_b16_d16_hi v137, v99 offset:41216
	s_waitcnt vmcnt(4)
	s_nop 0
	v_bfe_u32 v99, v165, 16, 1
	v_mad_u32_u24 v136, v174, s18, v136
	v_add3_u32 v99, v165, v99, s67
	v_lshl_add_u32 v136, v136, 1, 0
	ds_write_b16_d16_hi v136, v99 offset:8192
	v_and_b32_e32 v99, 0xffff0000, v99
	v_sub_f32_e64 v99, v165, v99
	v_bfe_u32 v137, v99, 16, 1
	v_add3_u32 v99, v99, v137, s67
	ds_write_b16_d16_hi v136, v99 offset:41216
	s_waitcnt vmcnt(3)
	s_nop 0
	v_bfe_u32 v99, v163, 16, 1
	v_mad_u32_u24 v135, v174, s18, v135
	v_add3_u32 v99, v163, v99, s67
	v_lshl_add_u32 v135, v135, 1, 0
	ds_write_b16_d16_hi v135, v99 offset:8192
	v_and_b32_e32 v99, 0xffff0000, v99
	v_sub_f32_e64 v99, v163, v99
	v_bfe_u32 v136, v99, 16, 1
	v_add3_u32 v99, v99, v136, s67
	ds_write_b16_d16_hi v135, v99 offset:41216
	s_waitcnt vmcnt(2)
	s_nop 0
	v_bfe_u32 v99, v161, 16, 1
	v_mad_u32_u24 v134, v174, s18, v134
	v_add3_u32 v99, v161, v99, s67
	v_lshl_add_u32 v134, v134, 1, 0
	ds_write_b16_d16_hi v134, v99 offset:8192
	v_and_b32_e32 v99, 0xffff0000, v99
	v_sub_f32_e64 v99, v161, v99
	v_bfe_u32 v135, v99, 16, 1
	v_add3_u32 v99, v99, v135, s67
	ds_write_b16_d16_hi v134, v99 offset:41216
	s_waitcnt vmcnt(1)
	s_nop 0
	v_bfe_u32 v99, v159, 16, 1
	v_mad_u32_u24 v133, v174, s18, v133
	v_add3_u32 v99, v159, v99, s67
	v_lshl_add_u32 v133, v133, 1, 0
	ds_write_b16_d16_hi v133, v99 offset:8192
	v_and_b32_e32 v99, 0xffff0000, v99
	v_sub_f32_e64 v99, v159, v99
	v_bfe_u32 v134, v99, 16, 1
	v_add3_u32 v99, v99, v134, s67
	ds_write_b16_d16_hi v133, v99 offset:41216
	s_waitcnt vmcnt(0)
	s_nop 0
	v_bfe_u32 v99, v156, 16, 1
	v_mad_u32_u24 v132, v174, s18, v132
	v_add3_u32 v99, v156, v99, s67
	v_lshl_add_u32 v132, v132, 1, 0
	ds_write_b16_d16_hi v132, v99 offset:8192
	v_and_b32_e32 v99, 0xffff0000, v99
	v_sub_f32_e64 v99, v156, v99
	v_bfe_u32 v133, v99, 16, 1
	v_add3_u32 v99, v99, v133, s67
	ds_write_b16_d16_hi v132, v99 offset:41216
	v_cmp_gt_i32_e32 vcc, 32, v142
	s_nop 0
	v_lshl_add_u32 v175, v142, 2, 0
	s_and_saveexec_b64 s[18:19], vcc
	s_cbranch_execnz .LBB0_265

.LBB0_269:
	s_nop 0
	v_readlane_b32 s6, v254, 17
	v_readlane_b32 s7, v254, 18
	s_lshl_b32 s6, s6, 4
	s_ashr_i32 s7, s6, 31
	v_readlane_b32 s40, v253, 18
	s_lshl_b64 s[6:7], s[6:7], 2
	s_nop 0
	v_readlane_b32 s46, v253, 24
	v_readlane_b32 s41, v253, 19
	v_readlane_b32 s42, v253, 20
	v_readlane_b32 s43, v253, 21
	v_readlane_b32 s44, v253, 22
	v_readlane_b32 s45, v253, 23
	v_readlane_b32 s47, v253, 25
	v_readlane_b32 s48, v253, 26
	v_readlane_b32 s49, v253, 27
	v_readlane_b32 s50, v253, 28
	v_readlane_b32 s51, v253, 29
	v_readlane_b32 s52, v253, 30
	v_readlane_b32 s53, v253, 31
	v_readlane_b32 s54, v253, 32
	v_readlane_b32 s55, v253, 33
	s_add_u32 s18, s46, s6
	s_nop 0
	v_lshl_add_u64 v[144:145], v[142:143], 2, s[4:5]
	v_readlane_b32 s4, v254, 20
	s_addc_u32 s19, s47, s7
	s_nop 0
	v_readlane_b32 s6, v253, 9
	v_readlane_b32 s40, v253, 34
	v_lshlrev_b32_e32 v134, 6, v155
	v_mov_b32_e32 v135, v97
	v_readlane_b32 s5, v254, 21
	v_sub_co_u32_e32 v136, vcc, 0, v98
	s_nop 0
	v_readlane_b32 s7, v253, 10
	v_readlane_b32 s41, v253, 35
	v_readlane_b32 s44, v253, 38
	v_readlane_b32 s45, v253, 39
	v_lshl_add_u64 v[146:147], s[4:5], 0, v[134:135]
	v_subb_co_u32_e64 v137, s[4:5], 0, 0, vcc
	s_and_b64 s[6:7], s[6:7], exec
	s_mov_b64 s[40:41], s[44:45]
	v_readlane_b32 s4, v254, 36
	v_readlane_b32 s42, v253, 36
	v_readlane_b32 s43, v253, 37
	v_readlane_b32 s46, v253, 40
	s_cselect_b32 s7, s41, s19
	s_cselect_b32 s6, s40, s18
	v_lshlrev_b32_e32 v132, 4, v155
	v_mov_b32_e32 v133, v97
	v_mul_u32_u24_e32 v99, 0x810, v174
	v_readlane_b32 s5, v254, 37
	s_lshl_b32 s24, s20, 5
	s_nop 0
	v_lshl_add_u64 v[148:149], v[146:147], 0, v[136:137]
	v_lshl_add_u64 v[150:151], s[6:7], 0, v[96:97]
	v_lshlrev_b32_e32 v176, 2, v155
	s_nop 0
	v_lshl_add_u64 v[152:153], s[4:5], 0, v[96:97]
	v_cmp_lt_u32_e64 s[4:5], 7, v174
	v_add_u32_e64 v177, 0, v134
	v_add3_u32 v178, 0, v99, v98
	v_lshl_add_u64 v[154:155], s[78:79], 0, v[132:133]
	s_mov_b32 s28, -1
	s_mov_b32 s25, s27
	s_mov_b32 s39, 0x3fb8aa3b
	s_mov_b32 s40, 0xc2ce8ed0
	s_mov_b32 s41, 0x42b17218
	s_mov_b32 s42, 0x7f800000
	s_brev_b32 s43, -2
	s_nop 0
	s_mov_b32 s44, 0x33800000
	s_mov_b32 s45, 0x3f200000
	s_mov_b32 s46, 0x3f317218
	v_readlane_b32 s47, v253, 41
	v_readlane_b32 s48, v253, 42
	v_readlane_b32 s49, v253, 43
	v_readlane_b32 s50, v253, 44
	v_readlane_b32 s51, v253, 45
	v_readlane_b32 s52, v253, 46
	v_readlane_b32 s53, v253, 47
	v_readlane_b32 s54, v253, 48
	v_readlane_b32 s55, v253, 49
	s_branch .LBB0_271

.LBB0_274:
	s_waitcnt vmcnt(3)
	v_add_f32_e32 v132, 1.0, v132
	s_waitcnt vmcnt(2)
	v_add_f32_e32 v99, 1.0, v99
	v_mul_f32_e64 v98, v132, v98
	v_mul_f32_e32 v96, v99, v96
	s_mov_b32 s28, s6
	ds_write2st64_b32 v175, v98, v96 offset1:8
	s_waitcnt vmcnt(0)
	s_nop 0
	ds_write2st64_b32 v175, v134, v133 offset0:16 offset1:24

.LBB0_276:
	v_or_b32_e32 v132, 3, v98
	v_ashrrev_i32_e32 v133, 31, v132
	s_nop 0
	v_lshlrev_b64 v[132:133], 6, v[132:133]
	v_lshl_add_u64 v[132:133], v[152:153], 0, v[132:133]
	global_store_dword v[132:133], v99, off

.LBB0_278:
	s_or_b32 s30, s6, s29
	s_and_b64 s[6:7], s[18:19], s[20:21]
	v_or_b32_e32 v98, s30, v174
	s_and_b64 s[6:7], s[16:17], s[6:7]
	v_ashrrev_i32_e32 v99, 31, v98
	s_and_b64 vcc, exec, s[6:7]
	s_cbranch_vccnz .LBB0_283
	s_mov_b64 s[6:7], -1
	s_and_b64 vcc, s[80:81], exec
	s_cbranch_vccz .LBB0_281
	s_nop 0
	v_lshlrev_b64 v[0:1], 12, v[98:99]
	s_waitcnt vmcnt(0)
	s_nop 0
	v_lshl_add_u64 v[124:125], v[146:147], 0, v[0:1]
	global_load_dwordx4 v[6:9], v[124:125], off offset:48
	global_load_dwordx4 v[10:13], v[124:125], off offset:32
	global_load_dwordx4 v[2:5], v[124:125], off offset:16
	global_load_dwordx4 v[14:17], v[124:125], off
	s_mov_b64 s[6:7], 0
	s_waitcnt vmcnt(3)
	v_cvt_pk_bf16_f32 v6, v6, v7
	v_cvt_pk_bf16_f32 v7, v8, v9
	s_waitcnt vmcnt(1)
	s_nop 0
	v_cvt_pk_bf16_f32 v2, v2, v3
	s_waitcnt vmcnt(0)
	s_nop 0
	v_cvt_pk_bf16_f32 v0, v14, v15
	v_cvt_pk_bf16_f32 v1, v16, v17
	v_cvt_pk_bf16_f32 v3, v4, v5
	v_cvt_pk_bf16_f32 v4, v10, v11
	v_cvt_pk_bf16_f32 v5, v12, v13
	global_load_dwordx4 v[14:17], v[124:125], off offset:304
	global_load_dwordx4 v[18:21], v[124:125], off offset:288
	global_load_dwordx4 v[10:13], v[124:125], off offset:272
	global_load_dwordx4 v[22:25], v[124:125], off offset:256
	s_waitcnt vmcnt(3)
	s_nop 0
	v_cvt_pk_bf16_f32 v14, v14, v15
	v_cvt_pk_bf16_f32 v15, v16, v17
	s_waitcnt vmcnt(1)
	s_nop 0
	v_cvt_pk_bf16_f32 v10, v10, v11
	s_waitcnt vmcnt(0)
	s_nop 0
	v_cvt_pk_bf16_f32 v8, v22, v23
	v_cvt_pk_bf16_f32 v9, v24, v25
	v_cvt_pk_bf16_f32 v11, v12, v13
	v_cvt_pk_bf16_f32 v12, v18, v19
	v_cvt_pk_bf16_f32 v13, v20, v21
	global_load_dwordx4 v[22:25], v[124:125], off offset:560
	global_load_dwordx4 v[26:29], v[124:125], off offset:544
	global_load_dwordx4 v[18:21], v[124:125], off offset:528
	global_load_dwordx4 v[30:33], v[124:125], off offset:512
	s_waitcnt vmcnt(3)
	s_nop 0
	v_cvt_pk_bf16_f32 v22, v22, v23
	v_cvt_pk_bf16_f32 v23, v24, v25
	s_waitcnt vmcnt(1)
	s_nop 0
	v_cvt_pk_bf16_f32 v18, v18, v19
	s_waitcnt vmcnt(0)
	s_nop 0
	v_cvt_pk_bf16_f32 v16, v30, v31
	v_cvt_pk_bf16_f32 v17, v32, v33
	v_cvt_pk_bf16_f32 v19, v20, v21
	v_cvt_pk_bf16_f32 v20, v26, v27
	v_cvt_pk_bf16_f32 v21, v28, v29
	global_load_dwordx4 v[30:33], v[124:125], off offset:816
	global_load_dwordx4 v[34:37], v[124:125], off offset:800
	global_load_dwordx4 v[26:29], v[124:125], off offset:784
	global_load_dwordx4 v[38:41], v[124:125], off offset:768
	s_waitcnt vmcnt(3)
	s_nop 0
	v_cvt_pk_bf16_f32 v30, v30, v31
	v_cvt_pk_bf16_f32 v31, v32, v33
	s_waitcnt vmcnt(1)
	s_nop 0
	v_cvt_pk_bf16_f32 v26, v26, v27
	s_waitcnt vmcnt(0)
	s_nop 0
	v_cvt_pk_bf16_f32 v24, v38, v39
	v_cvt_pk_bf16_f32 v25, v40, v41
	v_cvt_pk_bf16_f32 v27, v28, v29
	v_cvt_pk_bf16_f32 v28, v34, v35
	v_cvt_pk_bf16_f32 v29, v36, v37
	global_load_dwordx4 v[38:41], v[124:125], off offset:1072
	global_load_dwordx4 v[42:45], v[124:125], off offset:1056
	global_load_dwordx4 v[34:37], v[124:125], off offset:1040
	global_load_dwordx4 v[46:49], v[124:125], off offset:1024
	s_waitcnt vmcnt(3)
	s_nop 0
	v_cvt_pk_bf16_f32 v38, v38, v39
	v_cvt_pk_bf16_f32 v39, v40, v41
	s_waitcnt vmcnt(1)
	s_nop 0
	v_cvt_pk_bf16_f32 v34, v34, v35
	s_waitcnt vmcnt(0)
	s_nop 0
	v_cvt_pk_bf16_f32 v32, v46, v47
	v_cvt_pk_bf16_f32 v33, v48, v49
	v_cvt_pk_bf16_f32 v35, v36, v37
	v_cvt_pk_bf16_f32 v36, v42, v43
	v_cvt_pk_bf16_f32 v37, v44, v45
	global_load_dwordx4 v[46:49], v[124:125], off offset:1328
	global_load_dwordx4 v[50:53], v[124:125], off offset:1312
	global_load_dwordx4 v[42:45], v[124:125], off offset:1296
	global_load_dwordx4 v[54:57], v[124:125], off offset:1280
	s_waitcnt vmcnt(3)
	s_nop 0
	v_cvt_pk_bf16_f32 v46, v46, v47
	v_cvt_pk_bf16_f32 v47, v48, v49
	s_waitcnt vmcnt(1)
	s_nop 0
	v_cvt_pk_bf16_f32 v42, v42, v43
	s_waitcnt vmcnt(0)
	s_nop 0
	v_cvt_pk_bf16_f32 v40, v54, v55
	v_cvt_pk_bf16_f32 v41, v56, v57
	v_cvt_pk_bf16_f32 v43, v44, v45
	v_cvt_pk_bf16_f32 v44, v50, v51
	v_cvt_pk_bf16_f32 v45, v52, v53
	global_load_dwordx4 v[54:57], v[124:125], off offset:1584
	global_load_dwordx4 v[58:61], v[124:125], off offset:1568
	global_load_dwordx4 v[50:53], v[124:125], off offset:1552
	global_load_dwordx4 v[62:65], v[124:125], off offset:1536
	s_waitcnt vmcnt(3)
	s_nop 0
	v_cvt_pk_bf16_f32 v54, v54, v55
	v_cvt_pk_bf16_f32 v55, v56, v57
	s_waitcnt vmcnt(1)
	s_nop 0
	v_cvt_pk_bf16_f32 v50, v50, v51
	s_waitcnt vmcnt(0)
	s_nop 0
	v_cvt_pk_bf16_f32 v48, v62, v63
	v_cvt_pk_bf16_f32 v49, v64, v65
	v_cvt_pk_bf16_f32 v51, v52, v53
	v_cvt_pk_bf16_f32 v52, v58, v59
	v_cvt_pk_bf16_f32 v53, v60, v61
	global_load_dwordx4 v[62:65], v[124:125], off offset:1840
	global_load_dwordx4 v[66:69], v[124:125], off offset:1824
	global_load_dwordx4 v[58:61], v[124:125], off offset:1808
	global_load_dwordx4 v[70:73], v[124:125], off offset:1792
	s_waitcnt vmcnt(3)
	s_nop 0
	v_cvt_pk_bf16_f32 v62, v62, v63
	v_cvt_pk_bf16_f32 v63, v64, v65
	s_waitcnt vmcnt(1)
	s_nop 0
	v_cvt_pk_bf16_f32 v58, v58, v59
	s_waitcnt vmcnt(0)
	s_nop 0
	v_cvt_pk_bf16_f32 v56, v70, v71
	v_cvt_pk_bf16_f32 v57, v72, v73
	v_cvt_pk_bf16_f32 v59, v60, v61
	v_cvt_pk_bf16_f32 v60, v66, v67
	v_cvt_pk_bf16_f32 v61, v68, v69
	global_load_dwordx4 v[70:73], v[124:125], off offset:2096
	global_load_dwordx4 v[74:77], v[124:125], off offset:2080
	global_load_dwordx4 v[66:69], v[124:125], off offset:2064
	global_load_dwordx4 v[78:81], v[124:125], off offset:2048
	s_waitcnt vmcnt(3)
	s_nop 0
	v_cvt_pk_bf16_f32 v70, v70, v71
	v_cvt_pk_bf16_f32 v71, v72, v73
	s_waitcnt vmcnt(1)
	s_nop 0
	v_cvt_pk_bf16_f32 v66, v66, v67
	s_waitcnt vmcnt(0)
	s_nop 0
	v_cvt_pk_bf16_f32 v64, v78, v79
	v_cvt_pk_bf16_f32 v65, v80, v81
	v_cvt_pk_bf16_f32 v67, v68, v69
	v_cvt_pk_bf16_f32 v68, v74, v75
	v_cvt_pk_bf16_f32 v69, v76, v77
	global_load_dwordx4 v[78:81], v[124:125], off offset:2352
	global_load_dwordx4 v[82:85], v[124:125], off offset:2336
	global_load_dwordx4 v[74:77], v[124:125], off offset:2320
	global_load_dwordx4 v[86:89], v[124:125], off offset:2304
	s_waitcnt vmcnt(3)
	s_nop 0
	v_cvt_pk_bf16_f32 v78, v78, v79
	v_cvt_pk_bf16_f32 v79, v80, v81
	s_waitcnt vmcnt(1)
	s_nop 0
	v_cvt_pk_bf16_f32 v74, v74, v75
	s_waitcnt vmcnt(0)
	s_nop 0
	v_cvt_pk_bf16_f32 v72, v86, v87
	v_cvt_pk_bf16_f32 v73, v88, v89
	v_cvt_pk_bf16_f32 v75, v76, v77
	v_cvt_pk_bf16_f32 v76, v82, v83
	v_cvt_pk_bf16_f32 v77, v84, v85
	global_load_dwordx4 v[86:89], v[124:125], off offset:2608
	global_load_dwordx4 v[90:93], v[124:125], off offset:2592
	global_load_dwordx4 v[82:85], v[124:125], off offset:2576
	global_load_dwordx4 v[100:103], v[124:125], off offset:2560
	s_waitcnt vmcnt(3)
	s_nop 0
	v_cvt_pk_bf16_f32 v86, v86, v87
	v_cvt_pk_bf16_f32 v87, v88, v89
	s_waitcnt vmcnt(1)
	s_nop 0
	v_cvt_pk_bf16_f32 v82, v82, v83
	s_waitcnt vmcnt(0)
	s_nop 0
	v_cvt_pk_bf16_f32 v80, v100, v101
	v_cvt_pk_bf16_f32 v81, v102, v103
	v_cvt_pk_bf16_f32 v83, v84, v85
	v_cvt_pk_bf16_f32 v84, v90, v91
	v_cvt_pk_bf16_f32 v85, v92, v93
	global_load_dwordx4 v[100:103], v[124:125], off offset:2864
	global_load_dwordx4 v[92:95], v[124:125], off offset:2848
	global_load_dwordx4 v[104:107], v[124:125], off offset:2832
	global_load_dwordx4 v[88:91], v[124:125], off offset:2816
	s_waitcnt vmcnt(2)
	s_nop 0
	v_cvt_pk_bf16_f32 v92, v92, v93
	v_cvt_pk_bf16_f32 v93, v94, v95
	s_waitcnt vmcnt(0)
	s_nop 0
	v_cvt_pk_bf16_f32 v88, v88, v89
	v_cvt_pk_bf16_f32 v89, v90, v91
	v_cvt_pk_bf16_f32 v90, v104, v105
	v_cvt_pk_bf16_f32 v91, v106, v107
	v_cvt_pk_bf16_f32 v95, v102, v103
	global_load_dwordx4 v[106:109], v[124:125], off offset:3120
	global_load_dwordx4 v[110:113], v[124:125], off offset:3104
	global_load_dwordx4 v[102:105], v[124:125], off offset:3088
	global_load_dwordx4 v[114:117], v[124:125], off offset:3072
	v_cvt_pk_bf16_f32 v94, v100, v101
	s_waitcnt vmcnt(3)
	s_nop 0
	v_cvt_pk_bf16_f32 v106, v106, v107
	v_cvt_pk_bf16_f32 v107, v108, v109
	s_waitcnt vmcnt(1)
	s_nop 0
	v_cvt_pk_bf16_f32 v102, v102, v103
	s_waitcnt vmcnt(0)
	s_nop 0
	v_cvt_pk_bf16_f32 v100, v114, v115
	v_cvt_pk_bf16_f32 v101, v116, v117
	v_cvt_pk_bf16_f32 v103, v104, v105
	v_cvt_pk_bf16_f32 v104, v110, v111
	v_cvt_pk_bf16_f32 v105, v112, v113
	global_load_dwordx4 v[114:117], v[124:125], off offset:3376
	global_load_dwordx4 v[118:121], v[124:125], off offset:3360
	global_load_dwordx4 v[110:113], v[124:125], off offset:3344
	global_load_dwordx4 v[126:129], v[124:125], off offset:3328
	s_waitcnt vmcnt(3)
	s_nop 0
	v_cvt_pk_bf16_f32 v114, v114, v115
	v_cvt_pk_bf16_f32 v115, v116, v117
	s_waitcnt vmcnt(1)
	s_nop 0
	v_cvt_pk_bf16_f32 v110, v110, v111
	s_waitcnt vmcnt(0)
	s_nop 0
	v_cvt_pk_bf16_f32 v108, v126, v127
	v_cvt_pk_bf16_f32 v109, v128, v129
	v_cvt_pk_bf16_f32 v111, v112, v113
	v_cvt_pk_bf16_f32 v112, v118, v119
	v_cvt_pk_bf16_f32 v113, v120, v121
	global_load_dwordx4 v[126:129], v[124:125], off offset:3632
	global_load_dwordx4 v[120:123], v[124:125], off offset:3616
	global_load_dwordx4 v[130:133], v[124:125], off offset:3600
	global_load_dwordx4 v[116:119], v[124:125], off offset:3584
	s_waitcnt vmcnt(2)
	s_nop 0
	v_cvt_pk_bf16_f32 v120, v120, v121
	v_cvt_pk_bf16_f32 v121, v122, v123
	s_waitcnt vmcnt(0)
	s_nop 0
	v_cvt_pk_bf16_f32 v116, v116, v117
	v_cvt_pk_bf16_f32 v117, v118, v119
	v_cvt_pk_bf16_f32 v118, v130, v131
	v_cvt_pk_bf16_f32 v119, v132, v133
	v_cvt_pk_bf16_f32 v122, v126, v127
	v_cvt_pk_bf16_f32 v123, v128, v129
	global_load_dwordx4 v[130:133], v[124:125], off offset:3888
	global_load_dwordx4 v[134:137], v[124:125], off offset:3872
	global_load_dwordx4 v[126:129], v[124:125], off offset:3856
	global_load_dwordx4 v[138:141], v[124:125], off offset:3840
	s_waitcnt vmcnt(3)
	s_nop 0
	v_cvt_pk_bf16_f32 v130, v130, v131
	v_cvt_pk_bf16_f32 v131, v132, v133
	s_waitcnt vmcnt(1)
	s_nop 0
	v_cvt_pk_bf16_f32 v126, v126, v127
	s_waitcnt vmcnt(0)
	s_nop 0
	v_cvt_pk_bf16_f32 v124, v138, v139
	v_cvt_pk_bf16_f32 v125, v140, v141
	v_cvt_pk_bf16_f32 v127, v128, v129
	v_cvt_pk_bf16_f32 v128, v134, v135
	v_cvt_pk_bf16_f32 v129, v136, v137
.LBB0_281:
	s_andn2_b64 vcc, exec, s[6:7]
	s_cbranch_vccnz .LBB0_283
	v_lshlrev_b64 v[0:1], 11, v[98:99]
	s_waitcnt vmcnt(0)
	s_nop 0
	v_lshl_add_u64 v[124:125], v[148:149], 0, v[0:1]
	global_load_dwordx4 v[4:7], v[124:125], off offset:16
	global_load_dwordx4 v[0:3], v[124:125], off
	global_load_dwordx4 v[12:15], v[124:125], off offset:144
	global_load_dwordx4 v[8:11], v[124:125], off offset:128
	global_load_dwordx4 v[20:23], v[124:125], off offset:272
	global_load_dwordx4 v[16:19], v[124:125], off offset:256
	global_load_dwordx4 v[28:31], v[124:125], off offset:400
	global_load_dwordx4 v[24:27], v[124:125], off offset:384
	global_load_dwordx4 v[36:39], v[124:125], off offset:528
	global_load_dwordx4 v[32:35], v[124:125], off offset:512
	global_load_dwordx4 v[44:47], v[124:125], off offset:656
	global_load_dwordx4 v[40:43], v[124:125], off offset:640
	global_load_dwordx4 v[52:55], v[124:125], off offset:784
	global_load_dwordx4 v[48:51], v[124:125], off offset:768
	global_load_dwordx4 v[60:63], v[124:125], off offset:912
	global_load_dwordx4 v[56:59], v[124:125], off offset:896
	global_load_dwordx4 v[68:71], v[124:125], off offset:1040
	global_load_dwordx4 v[64:67], v[124:125], off offset:1024
	global_load_dwordx4 v[76:79], v[124:125], off offset:1168
	global_load_dwordx4 v[72:75], v[124:125], off offset:1152
	global_load_dwordx4 v[84:87], v[124:125], off offset:1296
	global_load_dwordx4 v[80:83], v[124:125], off offset:1280
	global_load_dwordx4 v[92:95], v[124:125], off offset:1424
	global_load_dwordx4 v[88:91], v[124:125], off offset:1408
	global_load_dwordx4 v[104:107], v[124:125], off offset:1552
	global_load_dwordx4 v[100:103], v[124:125], off offset:1536
	global_load_dwordx4 v[112:115], v[124:125], off offset:1680
	global_load_dwordx4 v[108:111], v[124:125], off offset:1664
	global_load_dwordx4 v[120:123], v[124:125], off offset:1808
	global_load_dwordx4 v[116:119], v[124:125], off offset:1792
	global_load_dwordx4 v[128:131], v[124:125], off offset:1936
	s_nop 0
	s_nop 0
	global_load_dwordx4 v[124:127], v[124:125], off offset:1920
.LBB0_283:
	s_waitcnt vmcnt(30)
	s_nop 0
	v_and_b32_e32 v132, 0xffff0000, v0
	v_lshlrev_b32_e32 v96, 16, v0
	v_mul_f32_e32 v132, v132, v132
	v_and_b32_e32 v133, 0xffff0000, v1
	v_fmac_f32_e32 v132, v96, v96
	v_lshlrev_b32_e32 v96, 16, v1
	v_mul_f32_e32 v133, v133, v133
	v_fmac_f32_e32 v133, v96, v96
	v_add_f32_e64 v96, v132, v133
	v_and_b32_e32 v133, 0xffff0000, v2
	v_lshlrev_b32_e32 v132, 16, v2
	v_mul_f32_e32 v133, v133, v133
	v_fmac_f32_e32 v133, v132, v132
	v_add_f32_e32 v96, v133, v96
	v_and_b32_e32 v133, 0xffff0000, v3
	v_lshlrev_b32_e32 v132, 16, v3
	v_mul_f32_e32 v133, v133, v133
	v_fmac_f32_e32 v133, v132, v132
	v_add_f32_e32 v96, v133, v96
	v_and_b32_e32 v133, 0xffff0000, v4
	v_lshlrev_b32_e32 v132, 16, v4
	v_mul_f32_e32 v133, v133, v133
	v_fmac_f32_e32 v133, v132, v132
	v_add_f32_e32 v96, v133, v96
	v_and_b32_e32 v133, 0xffff0000, v5
	v_lshlrev_b32_e32 v132, 16, v5
	v_mul_f32_e32 v133, v133, v133
	v_fmac_f32_e32 v133, v132, v132
	v_add_f32_e32 v96, v133, v96
	v_and_b32_e32 v133, 0xffff0000, v6
	v_lshlrev_b32_e32 v132, 16, v6
	v_mul_f32_e32 v133, v133, v133
	v_fmac_f32_e32 v133, v132, v132
	v_add_f32_e32 v96, v133, v96
	v_and_b32_e32 v133, 0xffff0000, v7
	v_lshlrev_b32_e32 v132, 16, v7
	v_mul_f32_e32 v133, v133, v133
	v_fmac_f32_e32 v133, v132, v132
	v_add_f32_e32 v96, v133, v96
	s_waitcnt vmcnt(28)
	s_nop 0
	v_and_b32_e32 v133, 0xffff0000, v8
	v_lshlrev_b32_e32 v132, 16, v8
	v_mul_f32_e32 v133, v133, v133
	v_fmac_f32_e32 v133, v132, v132
	v_add_f32_e32 v96, v133, v96
	v_and_b32_e32 v133, 0xffff0000, v9
	v_lshlrev_b32_e32 v132, 16, v9
	v_mul_f32_e32 v133, v133, v133
	v_fmac_f32_e32 v133, v132, v132
	v_add_f32_e32 v96, v133, v96
	v_and_b32_e32 v133, 0xffff0000, v10
	v_lshlrev_b32_e32 v132, 16, v10
	v_mul_f32_e32 v133, v133, v133
	v_fmac_f32_e32 v133, v132, v132
	v_add_f32_e32 v96, v133, v96
	v_and_b32_e32 v133, 0xffff0000, v11
	v_lshlrev_b32_e32 v132, 16, v11
	v_mul_f32_e32 v133, v133, v133
	v_fmac_f32_e32 v133, v132, v132
	v_add_f32_e32 v96, v133, v96
	v_and_b32_e32 v133, 0xffff0000, v12
	v_lshlrev_b32_e32 v132, 16, v12
	v_mul_f32_e32 v133, v133, v133
	v_fmac_f32_e32 v133, v132, v132
	v_add_f32_e32 v96, v133, v96
	v_and_b32_e32 v133, 0xffff0000, v13
	v_lshlrev_b32_e32 v132, 16, v13
	v_mul_f32_e32 v133, v133, v133
	v_fmac_f32_e32 v133, v132, v132
	v_add_f32_e32 v96, v133, v96
	v_and_b32_e32 v133, 0xffff0000, v14
	v_lshlrev_b32_e32 v132, 16, v14
	v_mul_f32_e32 v133, v133, v133
	v_fmac_f32_e32 v133, v132, v132
	v_add_f32_e32 v96, v133, v96
	v_and_b32_e32 v133, 0xffff0000, v15
	v_lshlrev_b32_e32 v132, 16, v15
	v_mul_f32_e32 v133, v133, v133
	v_fmac_f32_e32 v133, v132, v132
	v_add_f32_e32 v96, v133, v96
	s_waitcnt vmcnt(26)
	s_nop 0
	v_and_b32_e32 v133, 0xffff0000, v16
	v_lshlrev_b32_e32 v132, 16, v16
	v_mul_f32_e32 v133, v133, v133
	v_fmac_f32_e32 v133, v132, v132
	v_add_f32_e32 v96, v133, v96
	v_and_b32_e32 v133, 0xffff0000, v17
	v_lshlrev_b32_e32 v132, 16, v17
	v_mul_f32_e32 v133, v133, v133
	v_fmac_f32_e32 v133, v132, v132
	v_add_f32_e32 v96, v133, v96
	v_and_b32_e32 v133, 0xffff0000, v18
	v_lshlrev_b32_e32 v132, 16, v18
	v_mul_f32_e32 v133, v133, v133
	v_fmac_f32_e32 v133, v132, v132
	v_add_f32_e32 v96, v133, v96
	v_and_b32_e32 v133, 0xffff0000, v19
	v_lshlrev_b32_e32 v132, 16, v19
	v_mul_f32_e32 v133, v133, v133
	v_fmac_f32_e32 v133, v132, v132
	v_add_f32_e32 v96, v133, v96
	v_and_b32_e32 v133, 0xffff0000, v20
	v_lshlrev_b32_e32 v132, 16, v20
	v_mul_f32_e32 v133, v133, v133
	v_fmac_f32_e32 v133, v132, v132
	v_add_f32_e32 v96, v133, v96
	v_and_b32_e32 v133, 0xffff0000, v21
	v_lshlrev_b32_e32 v132, 16, v21
	v_mul_f32_e32 v133, v133, v133
	v_fmac_f32_e32 v133, v132, v132
	v_add_f32_e32 v96, v133, v96
	v_and_b32_e32 v133, 0xffff0000, v22
	v_lshlrev_b32_e32 v132, 16, v22
	v_mul_f32_e32 v133, v133, v133
	v_fmac_f32_e32 v133, v132, v132
	v_add_f32_e32 v96, v133, v96
	v_and_b32_e32 v133, 0xffff0000, v23
	v_lshlrev_b32_e32 v132, 16, v23
	v_mul_f32_e32 v133, v133, v133
	v_fmac_f32_e32 v133, v132, v132
	v_add_f32_e32 v96, v133, v96
	s_waitcnt vmcnt(24)
	s_nop 0
	v_and_b32_e32 v133, 0xffff0000, v24
	v_lshlrev_b32_e32 v132, 16, v24
	v_mul_f32_e32 v133, v133, v133
	v_fmac_f32_e32 v133, v132, v132
	v_add_f32_e32 v96, v133, v96
	v_and_b32_e32 v133, 0xffff0000, v25
	v_lshlrev_b32_e32 v132, 16, v25
	v_mul_f32_e32 v133, v133, v133
	v_fmac_f32_e32 v133, v132, v132
	v_add_f32_e32 v96, v133, v96
	v_and_b32_e32 v133, 0xffff0000, v26
	v_lshlrev_b32_e32 v132, 16, v26
	v_mul_f32_e32 v133, v133, v133
	v_fmac_f32_e32 v133, v132, v132
	v_add_f32_e32 v96, v133, v96
	v_and_b32_e32 v133, 0xffff0000, v27
	v_lshlrev_b32_e32 v132, 16, v27
	v_mul_f32_e32 v133, v133, v133
	v_fmac_f32_e32 v133, v132, v132
	v_add_f32_e32 v96, v133, v96
	v_and_b32_e32 v133, 0xffff0000, v28
	v_lshlrev_b32_e32 v132, 16, v28
	v_mul_f32_e32 v133, v133, v133
	v_fmac_f32_e32 v133, v132, v132
	v_add_f32_e32 v96, v133, v96
	v_and_b32_e32 v133, 0xffff0000, v29
	v_lshlrev_b32_e32 v132, 16, v29
	v_mul_f32_e32 v133, v133, v133
	v_fmac_f32_e32 v133, v132, v132
	v_add_f32_e32 v96, v133, v96
	v_and_b32_e32 v133, 0xffff0000, v30
	v_lshlrev_b32_e32 v132, 16, v30
	v_mul_f32_e32 v133, v133, v133
	v_fmac_f32_e32 v133, v132, v132
	v_add_f32_e32 v96, v133, v96
	v_and_b32_e32 v133, 0xffff0000, v31
	v_lshlrev_b32_e32 v132, 16, v31
	v_mul_f32_e32 v133, v133, v133
	v_fmac_f32_e32 v133, v132, v132
	v_add_f32_e32 v96, v133, v96
	s_waitcnt vmcnt(22)
	s_nop 0
	v_and_b32_e32 v133, 0xffff0000, v32
	v_lshlrev_b32_e32 v132, 16, v32
	v_mul_f32_e32 v133, v133, v133
	v_fmac_f32_e32 v133, v132, v132
	v_add_f32_e32 v96, v133, v96
	v_and_b32_e32 v133, 0xffff0000, v33
	v_lshlrev_b32_e32 v132, 16, v33
	v_mul_f32_e32 v133, v133, v133
	v_fmac_f32_e32 v133, v132, v132
	v_add_f32_e32 v96, v133, v96
	v_and_b32_e32 v133, 0xffff0000, v34
	v_lshlrev_b32_e32 v132, 16, v34
	v_mul_f32_e32 v133, v133, v133
	v_fmac_f32_e32 v133, v132, v132
	v_add_f32_e32 v96, v133, v96
	v_and_b32_e32 v133, 0xffff0000, v35
	v_lshlrev_b32_e32 v132, 16, v35
	v_mul_f32_e32 v133, v133, v133
	v_fmac_f32_e32 v133, v132, v132
	v_add_f32_e32 v96, v133, v96
	v_and_b32_e32 v133, 0xffff0000, v36
	v_lshlrev_b32_e32 v132, 16, v36
	v_mul_f32_e32 v133, v133, v133
	v_fmac_f32_e32 v133, v132, v132
	v_add_f32_e32 v96, v133, v96
	v_and_b32_e32 v133, 0xffff0000, v37
	v_lshlrev_b32_e32 v132, 16, v37
	v_mul_f32_e32 v133, v133, v133
	v_fmac_f32_e32 v133, v132, v132
	v_add_f32_e32 v96, v133, v96
	v_and_b32_e32 v133, 0xffff0000, v38
	v_lshlrev_b32_e32 v132, 16, v38
	v_mul_f32_e32 v133, v133, v133
	v_fmac_f32_e32 v133, v132, v132
	v_add_f32_e32 v96, v133, v96
	v_and_b32_e32 v133, 0xffff0000, v39
	v_lshlrev_b32_e32 v132, 16, v39
	v_mul_f32_e32 v133, v133, v133
	v_fmac_f32_e32 v133, v132, v132
	v_add_f32_e32 v96, v133, v96
	s_waitcnt vmcnt(20)
	s_nop 0
	v_and_b32_e32 v133, 0xffff0000, v40
	v_lshlrev_b32_e32 v132, 16, v40
	v_mul_f32_e32 v133, v133, v133
	v_fmac_f32_e32 v133, v132, v132
	v_add_f32_e32 v96, v133, v96
	v_and_b32_e32 v133, 0xffff0000, v41
	v_lshlrev_b32_e32 v132, 16, v41
	v_mul_f32_e32 v133, v133, v133
	v_fmac_f32_e32 v133, v132, v132
	v_add_f32_e32 v96, v133, v96
	v_and_b32_e32 v133, 0xffff0000, v42
	v_lshlrev_b32_e32 v132, 16, v42
	v_mul_f32_e32 v133, v133, v133
	v_fmac_f32_e32 v133, v132, v132
	v_add_f32_e32 v96, v133, v96
	v_and_b32_e32 v133, 0xffff0000, v43
	v_lshlrev_b32_e32 v132, 16, v43
	v_mul_f32_e32 v133, v133, v133
	v_fmac_f32_e32 v133, v132, v132
	v_add_f32_e32 v96, v133, v96
	v_and_b32_e32 v133, 0xffff0000, v44
	v_lshlrev_b32_e32 v132, 16, v44
	v_mul_f32_e32 v133, v133, v133
	v_fmac_f32_e32 v133, v132, v132
	v_add_f32_e32 v96, v133, v96
	v_and_b32_e32 v133, 0xffff0000, v45
	v_lshlrev_b32_e32 v132, 16, v45
	v_mul_f32_e32 v133, v133, v133
	v_fmac_f32_e32 v133, v132, v132
	v_add_f32_e32 v96, v133, v96
	v_and_b32_e32 v133, 0xffff0000, v46
	v_lshlrev_b32_e32 v132, 16, v46
	v_mul_f32_e32 v133, v133, v133
	v_fmac_f32_e32 v133, v132, v132
	v_add_f32_e32 v96, v133, v96
	v_and_b32_e32 v133, 0xffff0000, v47
	v_lshlrev_b32_e32 v132, 16, v47
	v_mul_f32_e32 v133, v133, v133
	v_fmac_f32_e32 v133, v132, v132
	v_add_f32_e32 v96, v133, v96
	s_waitcnt vmcnt(18)
	s_nop 0
	v_and_b32_e32 v133, 0xffff0000, v48
	v_lshlrev_b32_e32 v132, 16, v48
	v_mul_f32_e32 v133, v133, v133
	v_fmac_f32_e32 v133, v132, v132
	v_add_f32_e32 v96, v133, v96
	v_and_b32_e32 v133, 0xffff0000, v49
	v_lshlrev_b32_e32 v132, 16, v49
	v_mul_f32_e32 v133, v133, v133
	v_fmac_f32_e32 v133, v132, v132
	v_add_f32_e32 v96, v133, v96
	v_and_b32_e32 v133, 0xffff0000, v50
	v_lshlrev_b32_e32 v132, 16, v50
	v_mul_f32_e32 v133, v133, v133
	v_fmac_f32_e32 v133, v132, v132
	v_add_f32_e32 v96, v133, v96
	v_and_b32_e32 v133, 0xffff0000, v51
	v_lshlrev_b32_e32 v132, 16, v51
	v_mul_f32_e32 v133, v133, v133
	v_fmac_f32_e32 v133, v132, v132
	v_add_f32_e32 v96, v133, v96
	v_and_b32_e32 v133, 0xffff0000, v52
	v_lshlrev_b32_e32 v132, 16, v52
	v_mul_f32_e32 v133, v133, v133
	v_fmac_f32_e32 v133, v132, v132
	v_add_f32_e32 v96, v133, v96
	v_and_b32_e32 v133, 0xffff0000, v53
	v_lshlrev_b32_e32 v132, 16, v53
	v_mul_f32_e32 v133, v133, v133
	v_fmac_f32_e32 v133, v132, v132
	v_add_f32_e32 v96, v133, v96
	v_and_b32_e32 v133, 0xffff0000, v54
	v_lshlrev_b32_e32 v132, 16, v54
	v_mul_f32_e32 v133, v133, v133
	v_fmac_f32_e32 v133, v132, v132
	v_add_f32_e32 v96, v133, v96
	v_and_b32_e32 v133, 0xffff0000, v55
	v_lshlrev_b32_e32 v132, 16, v55
	v_mul_f32_e32 v133, v133, v133
	v_fmac_f32_e32 v133, v132, v132
	v_add_f32_e32 v96, v133, v96
	s_waitcnt vmcnt(16)
	s_nop 0
	v_and_b32_e32 v133, 0xffff0000, v56
	v_lshlrev_b32_e32 v132, 16, v56
	v_mul_f32_e32 v133, v133, v133
	v_fmac_f32_e32 v133, v132, v132
	v_add_f32_e32 v96, v133, v96
	v_and_b32_e32 v133, 0xffff0000, v57
	v_lshlrev_b32_e32 v132, 16, v57
	v_mul_f32_e32 v133, v133, v133
	v_fmac_f32_e32 v133, v132, v132
	v_add_f32_e32 v96, v133, v96
	v_and_b32_e32 v133, 0xffff0000, v58
	v_lshlrev_b32_e32 v132, 16, v58
	v_mul_f32_e32 v133, v133, v133
	v_fmac_f32_e32 v133, v132, v132
	v_add_f32_e32 v96, v133, v96
	v_and_b32_e32 v133, 0xffff0000, v59
	v_lshlrev_b32_e32 v132, 16, v59
	v_mul_f32_e32 v133, v133, v133
	v_fmac_f32_e32 v133, v132, v132
	v_add_f32_e32 v96, v133, v96
	v_and_b32_e32 v133, 0xffff0000, v60
	v_lshlrev_b32_e32 v132, 16, v60
	v_mul_f32_e32 v133, v133, v133
	v_fmac_f32_e32 v133, v132, v132
	v_add_f32_e32 v96, v133, v96
	v_and_b32_e32 v133, 0xffff0000, v61
	v_lshlrev_b32_e32 v132, 16, v61
	v_mul_f32_e32 v133, v133, v133
	v_fmac_f32_e32 v133, v132, v132
	v_add_f32_e32 v96, v133, v96
	v_and_b32_e32 v133, 0xffff0000, v62
	v_lshlrev_b32_e32 v132, 16, v62
	v_mul_f32_e32 v133, v133, v133
	v_fmac_f32_e32 v133, v132, v132
	v_add_f32_e32 v96, v133, v96
	v_and_b32_e32 v133, 0xffff0000, v63
	v_lshlrev_b32_e32 v132, 16, v63
	v_mul_f32_e32 v133, v133, v133
	v_fmac_f32_e32 v133, v132, v132
	v_add_f32_e32 v96, v133, v96
	s_waitcnt vmcnt(14)
	s_nop 0
	v_and_b32_e32 v133, 0xffff0000, v64
	v_lshlrev_b32_e32 v132, 16, v64
	v_mul_f32_e32 v133, v133, v133
	v_fmac_f32_e32 v133, v132, v132
	v_add_f32_e32 v96, v133, v96
	v_and_b32_e32 v133, 0xffff0000, v65
	v_lshlrev_b32_e32 v132, 16, v65
	v_mul_f32_e32 v133, v133, v133
	v_fmac_f32_e32 v133, v132, v132
	v_add_f32_e32 v96, v133, v96
	v_and_b32_e32 v133, 0xffff0000, v66
	v_lshlrev_b32_e32 v132, 16, v66
	v_mul_f32_e32 v133, v133, v133
	v_fmac_f32_e32 v133, v132, v132
	v_add_f32_e32 v96, v133, v96
	v_and_b32_e32 v133, 0xffff0000, v67
	v_lshlrev_b32_e32 v132, 16, v67
	v_mul_f32_e32 v133, v133, v133
	v_fmac_f32_e32 v133, v132, v132
	v_add_f32_e32 v96, v133, v96
	v_and_b32_e32 v133, 0xffff0000, v68
	v_lshlrev_b32_e32 v132, 16, v68
	v_mul_f32_e32 v133, v133, v133
	v_fmac_f32_e32 v133, v132, v132
	v_add_f32_e32 v96, v133, v96
	v_and_b32_e32 v133, 0xffff0000, v69
	v_lshlrev_b32_e32 v132, 16, v69
	v_mul_f32_e32 v133, v133, v133
	v_fmac_f32_e32 v133, v132, v132
	v_add_f32_e32 v96, v133, v96
	v_and_b32_e32 v133, 0xffff0000, v70
	v_lshlrev_b32_e32 v132, 16, v70
	v_mul_f32_e32 v133, v133, v133
	v_fmac_f32_e32 v133, v132, v132
	v_add_f32_e32 v96, v133, v96
	v_and_b32_e32 v133, 0xffff0000, v71
	v_lshlrev_b32_e32 v132, 16, v71
	v_mul_f32_e32 v133, v133, v133
	v_fmac_f32_e32 v133, v132, v132
	v_add_f32_e32 v96, v133, v96
	s_waitcnt vmcnt(12)
	s_nop 0
	v_and_b32_e32 v133, 0xffff0000, v72
	v_lshlrev_b32_e32 v132, 16, v72
	v_mul_f32_e32 v133, v133, v133
	v_fmac_f32_e32 v133, v132, v132
	v_add_f32_e32 v96, v133, v96
	v_and_b32_e32 v133, 0xffff0000, v73
	v_lshlrev_b32_e32 v132, 16, v73
	v_mul_f32_e32 v133, v133, v133
	v_fmac_f32_e32 v133, v132, v132
	v_add_f32_e32 v96, v133, v96
	v_and_b32_e32 v133, 0xffff0000, v74
	v_lshlrev_b32_e32 v132, 16, v74
	v_mul_f32_e32 v133, v133, v133
	v_fmac_f32_e32 v133, v132, v132
	v_add_f32_e32 v96, v133, v96
	v_and_b32_e32 v133, 0xffff0000, v75
	v_lshlrev_b32_e32 v132, 16, v75
	v_mul_f32_e32 v133, v133, v133
	v_fmac_f32_e32 v133, v132, v132
	v_add_f32_e32 v96, v133, v96
	v_and_b32_e32 v133, 0xffff0000, v76
	v_lshlrev_b32_e32 v132, 16, v76
	v_mul_f32_e32 v133, v133, v133
	v_fmac_f32_e32 v133, v132, v132
	v_add_f32_e32 v96, v133, v96
	v_and_b32_e32 v133, 0xffff0000, v77
	v_lshlrev_b32_e32 v132, 16, v77
	v_mul_f32_e32 v133, v133, v133
	v_fmac_f32_e32 v133, v132, v132
	v_add_f32_e32 v96, v133, v96
	v_and_b32_e32 v133, 0xffff0000, v78
	v_lshlrev_b32_e32 v132, 16, v78
	v_mul_f32_e32 v133, v133, v133
	v_fmac_f32_e32 v133, v132, v132
	v_add_f32_e32 v96, v133, v96
	v_and_b32_e32 v133, 0xffff0000, v79
	v_lshlrev_b32_e32 v132, 16, v79
	v_mul_f32_e32 v133, v133, v133
	v_fmac_f32_e32 v133, v132, v132
	v_add_f32_e32 v96, v133, v96
	s_waitcnt vmcnt(10)
	s_nop 0
	v_and_b32_e32 v133, 0xffff0000, v80
	v_lshlrev_b32_e32 v132, 16, v80
	v_mul_f32_e32 v133, v133, v133
	v_fmac_f32_e32 v133, v132, v132
	v_add_f32_e32 v96, v133, v96
	v_and_b32_e32 v133, 0xffff0000, v81
	v_lshlrev_b32_e32 v132, 16, v81
	v_mul_f32_e32 v133, v133, v133
	v_fmac_f32_e32 v133, v132, v132
	v_add_f32_e32 v96, v133, v96
	v_and_b32_e32 v133, 0xffff0000, v82
	v_lshlrev_b32_e32 v132, 16, v82
	v_mul_f32_e32 v133, v133, v133
	v_fmac_f32_e32 v133, v132, v132
	v_add_f32_e32 v96, v133, v96
	v_and_b32_e32 v133, 0xffff0000, v83
	v_lshlrev_b32_e32 v132, 16, v83
	v_mul_f32_e32 v133, v133, v133
	v_fmac_f32_e32 v133, v132, v132
	v_add_f32_e32 v96, v133, v96
	v_and_b32_e32 v133, 0xffff0000, v84
	v_lshlrev_b32_e32 v132, 16, v84
	v_mul_f32_e32 v133, v133, v133
	v_fmac_f32_e32 v133, v132, v132
	v_add_f32_e32 v96, v133, v96
	v_and_b32_e32 v133, 0xffff0000, v85
	v_lshlrev_b32_e32 v132, 16, v85
	v_mul_f32_e32 v133, v133, v133
	v_fmac_f32_e32 v133, v132, v132
	v_add_f32_e32 v96, v133, v96
	v_and_b32_e32 v133, 0xffff0000, v86
	v_lshlrev_b32_e32 v132, 16, v86
	v_mul_f32_e32 v133, v133, v133
	v_fmac_f32_e32 v133, v132, v132
	v_add_f32_e32 v96, v133, v96
	v_and_b32_e32 v133, 0xffff0000, v87
	v_lshlrev_b32_e32 v132, 16, v87
	v_mul_f32_e32 v133, v133, v133
	v_fmac_f32_e32 v133, v132, v132
	v_add_f32_e32 v96, v133, v96
	s_waitcnt vmcnt(8)
	s_nop 0
	v_and_b32_e32 v133, 0xffff0000, v88
	v_lshlrev_b32_e32 v132, 16, v88
	v_mul_f32_e32 v133, v133, v133
	v_fmac_f32_e32 v133, v132, v132
	v_add_f32_e32 v96, v133, v96
	v_and_b32_e32 v133, 0xffff0000, v89
	v_lshlrev_b32_e32 v132, 16, v89
	v_mul_f32_e32 v133, v133, v133
	v_fmac_f32_e32 v133, v132, v132
	v_add_f32_e32 v96, v133, v96
	v_and_b32_e32 v133, 0xffff0000, v90
	v_lshlrev_b32_e32 v132, 16, v90
	v_mul_f32_e32 v133, v133, v133
	v_fmac_f32_e32 v133, v132, v132
	v_add_f32_e32 v96, v133, v96
	v_and_b32_e32 v133, 0xffff0000, v91
	v_lshlrev_b32_e32 v132, 16, v91
	v_mul_f32_e32 v133, v133, v133
	v_fmac_f32_e32 v133, v132, v132
	v_add_f32_e32 v96, v133, v96
	v_and_b32_e32 v133, 0xffff0000, v92
	v_lshlrev_b32_e32 v132, 16, v92
	v_mul_f32_e32 v133, v133, v133
	v_fmac_f32_e32 v133, v132, v132
	v_add_f32_e32 v96, v133, v96
	v_and_b32_e32 v133, 0xffff0000, v93
	v_lshlrev_b32_e32 v132, 16, v93
	v_mul_f32_e32 v133, v133, v133
	v_fmac_f32_e32 v133, v132, v132
	v_add_f32_e32 v96, v133, v96
	v_and_b32_e32 v133, 0xffff0000, v94
	v_lshlrev_b32_e32 v132, 16, v94
	v_mul_f32_e32 v133, v133, v133
	v_fmac_f32_e32 v133, v132, v132
	v_add_f32_e32 v96, v133, v96
	v_and_b32_e32 v133, 0xffff0000, v95
	v_lshlrev_b32_e32 v132, 16, v95
	v_mul_f32_e32 v133, v133, v133
	v_fmac_f32_e32 v133, v132, v132
	v_add_f32_e32 v96, v133, v96
	s_waitcnt vmcnt(6)
	s_nop 0
	v_and_b32_e32 v133, 0xffff0000, v100
	v_lshlrev_b32_e32 v132, 16, v100
	v_mul_f32_e32 v133, v133, v133
	v_fmac_f32_e32 v133, v132, v132
	v_add_f32_e32 v96, v133, v96
	v_and_b32_e32 v133, 0xffff0000, v101
	v_lshlrev_b32_e32 v132, 16, v101
	v_mul_f32_e32 v133, v133, v133
	v_fmac_f32_e32 v133, v132, v132
	v_add_f32_e32 v96, v133, v96
	v_and_b32_e32 v133, 0xffff0000, v102
	v_lshlrev_b32_e32 v132, 16, v102
	v_mul_f32_e32 v133, v133, v133
	v_fmac_f32_e32 v133, v132, v132
	v_add_f32_e32 v96, v133, v96
	v_and_b32_e32 v133, 0xffff0000, v103
	v_lshlrev_b32_e32 v132, 16, v103
	v_mul_f32_e32 v133, v133, v133
	v_fmac_f32_e32 v133, v132, v132
	v_add_f32_e32 v96, v133, v96
	v_and_b32_e32 v133, 0xffff0000, v104
	v_lshlrev_b32_e32 v132, 16, v104
	v_mul_f32_e32 v133, v133, v133
	v_fmac_f32_e32 v133, v132, v132
	v_add_f32_e32 v96, v133, v96
	v_and_b32_e32 v133, 0xffff0000, v105
	v_lshlrev_b32_e32 v132, 16, v105
	v_mul_f32_e32 v133, v133, v133
	v_fmac_f32_e32 v133, v132, v132
	v_add_f32_e32 v96, v133, v96
	v_and_b32_e32 v133, 0xffff0000, v106
	v_lshlrev_b32_e32 v132, 16, v106
	v_mul_f32_e32 v133, v133, v133
	v_fmac_f32_e32 v133, v132, v132
	v_add_f32_e32 v96, v133, v96
	v_and_b32_e32 v133, 0xffff0000, v107
	v_lshlrev_b32_e32 v132, 16, v107
	v_mul_f32_e32 v133, v133, v133
	v_fmac_f32_e32 v133, v132, v132
	v_add_f32_e32 v96, v133, v96
	s_waitcnt vmcnt(4)
	s_nop 0
	v_and_b32_e32 v133, 0xffff0000, v108
	v_lshlrev_b32_e32 v132, 16, v108
	v_mul_f32_e32 v133, v133, v133
	v_fmac_f32_e32 v133, v132, v132
	v_add_f32_e32 v96, v133, v96
	v_and_b32_e32 v133, 0xffff0000, v109
	v_lshlrev_b32_e32 v132, 16, v109
	v_mul_f32_e32 v133, v133, v133
	v_fmac_f32_e32 v133, v132, v132
	v_add_f32_e32 v96, v133, v96
	v_and_b32_e32 v133, 0xffff0000, v110
	v_lshlrev_b32_e32 v132, 16, v110
	v_mul_f32_e32 v133, v133, v133
	v_fmac_f32_e32 v133, v132, v132
	v_add_f32_e32 v96, v133, v96
	v_and_b32_e32 v133, 0xffff0000, v111
	v_lshlrev_b32_e32 v132, 16, v111
	v_mul_f32_e32 v133, v133, v133
	v_fmac_f32_e32 v133, v132, v132
	v_add_f32_e32 v96, v133, v96
	v_and_b32_e32 v133, 0xffff0000, v112
	v_lshlrev_b32_e32 v132, 16, v112
	v_mul_f32_e32 v133, v133, v133
	v_fmac_f32_e32 v133, v132, v132
	v_add_f32_e32 v96, v133, v96
	v_and_b32_e32 v133, 0xffff0000, v113
	v_lshlrev_b32_e32 v132, 16, v113
	v_mul_f32_e32 v133, v133, v133
	v_fmac_f32_e32 v133, v132, v132
	v_add_f32_e32 v96, v133, v96
	v_and_b32_e32 v133, 0xffff0000, v114
	v_lshlrev_b32_e32 v132, 16, v114
	v_mul_f32_e32 v133, v133, v133
	v_fmac_f32_e32 v133, v132, v132
	v_add_f32_e32 v96, v133, v96
	v_and_b32_e32 v133, 0xffff0000, v115
	v_lshlrev_b32_e32 v132, 16, v115
	v_mul_f32_e32 v133, v133, v133
	v_fmac_f32_e32 v133, v132, v132
	v_add_f32_e32 v96, v133, v96
	s_waitcnt vmcnt(2)
	s_nop 0
	v_and_b32_e32 v133, 0xffff0000, v116
	v_lshlrev_b32_e32 v132, 16, v116
	v_mul_f32_e32 v133, v133, v133
	v_fmac_f32_e32 v133, v132, v132
	v_add_f32_e32 v96, v133, v96
	v_and_b32_e32 v133, 0xffff0000, v117
	v_lshlrev_b32_e32 v132, 16, v117
	v_mul_f32_e32 v133, v133, v133
	v_fmac_f32_e32 v133, v132, v132
	v_add_f32_e32 v96, v133, v96
	v_and_b32_e32 v133, 0xffff0000, v118
	v_lshlrev_b32_e32 v132, 16, v118
	v_mul_f32_e32 v133, v133, v133
	v_fmac_f32_e32 v133, v132, v132
	v_add_f32_e32 v96, v133, v96
	v_and_b32_e32 v133, 0xffff0000, v119
	v_lshlrev_b32_e32 v132, 16, v119
	v_mul_f32_e32 v133, v133, v133
	v_fmac_f32_e32 v133, v132, v132
	v_add_f32_e32 v96, v133, v96
	v_and_b32_e32 v133, 0xffff0000, v120
	v_lshlrev_b32_e32 v132, 16, v120
	v_mul_f32_e32 v133, v133, v133
	v_fmac_f32_e32 v133, v132, v132
	v_add_f32_e32 v96, v133, v96
	v_and_b32_e32 v133, 0xffff0000, v121
	v_lshlrev_b32_e32 v132, 16, v121
	v_mul_f32_e32 v133, v133, v133
	v_fmac_f32_e32 v133, v132, v132
	v_add_f32_e32 v96, v133, v96
	v_and_b32_e32 v133, 0xffff0000, v122
	v_lshlrev_b32_e32 v132, 16, v122
	v_mul_f32_e32 v133, v133, v133
	v_fmac_f32_e32 v133, v132, v132
	v_add_f32_e32 v96, v133, v96
	v_and_b32_e32 v133, 0xffff0000, v123
	v_lshlrev_b32_e32 v132, 16, v123
	v_mul_f32_e32 v133, v133, v133
	v_fmac_f32_e32 v133, v132, v132
	v_add_f32_e32 v96, v133, v96
	s_waitcnt vmcnt(0)
	s_nop 0
	v_and_b32_e32 v133, 0xffff0000, v124
	v_lshlrev_b32_e32 v132, 16, v124
	v_mul_f32_e32 v133, v133, v133
	v_fmac_f32_e32 v133, v132, v132
	v_add_f32_e32 v96, v133, v96
	v_and_b32_e32 v133, 0xffff0000, v125
	v_lshlrev_b32_e32 v132, 16, v125
	v_mul_f32_e32 v133, v133, v133
	v_fmac_f32_e32 v133, v132, v132
	s_nop 0
	v_and_b32_e32 v135, 0xffff0000, v127
	v_and_b32_e32 v134, 0xffff0000, v126
	v_add_f32_e64 v96, v133, v96
	v_lshlrev_b32_e32 v133, 16, v127
	v_lshlrev_b32_e32 v132, 16, v126
	v_pk_mul_f32 v[134:135], v[134:135], v[134:135]
	s_nop 0
	s_nop 0
	v_pk_fma_f32 v[132:133], v[132:133], v[132:133], v[134:135]
	v_and_b32_e32 v135, 0xffff0000, v129
	v_add_f32_e64 v96, v132, v96
	v_and_b32_e32 v134, 0xffff0000, v128
	v_add_f32_e64 v96, v133, v96
	v_lshlrev_b32_e32 v133, 16, v129
	v_lshlrev_b32_e32 v132, 16, v128
	v_pk_mul_f32 v[134:135], v[134:135], v[134:135]
	s_nop 0
	s_nop 0
	v_pk_fma_f32 v[132:133], v[132:133], v[132:133], v[134:135]
	v_and_b32_e32 v135, 0xffff0000, v131
	v_add_f32_e64 v96, v132, v96
	v_and_b32_e32 v134, 0xffff0000, v130
	v_add_f32_e64 v96, v133, v96
	v_lshlrev_b32_e32 v133, 16, v131
	v_lshlrev_b32_e32 v132, 16, v130
	v_pk_mul_f32 v[134:135], v[134:135], v[134:135]
	s_nop 0
	s_nop 0
	v_pk_fma_f32 v[132:133], v[132:133], v[132:133], v[134:135]
	v_lshlrev_b32_e32 v184, 16, v0
	v_add_f32_e32 v96, v132, v96
	v_add_f32_e64 v96, v133, v96
	v_and_b32_e32 v133, 64, v227
	v_xor_b32_e32 v132, 16, v227
	v_add_u32_e32 v133, 64, v133
	v_cmp_lt_i32_e32 vcc, v132, v133
	v_and_b32_e32 v185, 0xffff0000, v0
	v_lshlrev_b64 v[98:99], 10, v[98:99]
	v_cndmask_b32_e32 v132, v227, v132, vcc
	v_lshlrev_b32_e32 v132, 2, v132
	ds_bpermute_b32 v132, v132, v96
	s_waitcnt lgkmcnt(0)
	v_add_f32_e32 v96, v96, v132
	v_xor_b32_e32 v132, 32, v227
	v_cmp_lt_i32_e32 vcc, v132, v133
	s_nop 1
	v_cndmask_b32_e32 v132, v227, v132, vcc
	v_lshlrev_b32_e32 v132, 2, v132
	s_nop 0
	ds_bpermute_b32 v132, v132, v96
	s_waitcnt lgkmcnt(0)
	v_add_f32_e32 v96, v96, v132
	v_fmamk_f32 v96, v96, 0x3a800000, v220
	v_mul_f32_e32 v132, 0x4f800000, v96
	v_cmp_gt_f32_e32 vcc, s95, v96
	s_nop 1
	v_cndmask_b32_e32 v96, v96, v132, vcc
	v_sqrt_f32_e32 v132, v96
	s_nop 0
	v_add_u32_e32 v133, -1, v132
	v_fma_f32 v134, -v133, v132, v96
	v_cmp_ge_f32_e64 s[6:7], 0, v134
	v_add_u32_e32 v134, 1, v132
	s_nop 0
	v_cndmask_b32_e64 v133, v132, v133, s[6:7]
	v_fma_f32 v132, -v134, v132, v96
	v_cmp_lt_f32_e64 s[6:7], 0, v132
	s_nop 1
	s_nop 0
	v_cndmask_b32_e64 v132, v133, v134, s[6:7]
	v_mul_f32_e32 v133, 0x37800000, v132
	v_cndmask_b32_e32 v132, v132, v133, vcc
	v_cmp_class_f32_e32 vcc, v96, v221
	s_nop 1
	v_cndmask_b32_e32 v96, v132, v96, vcc
	v_div_scale_f32 v132, s[6:7], v96, v96, 1.0
	v_rcp_f32_e32 v133, v132
	s_nop 0
	v_fma_f32 v134, -v132, v133, 1.0
	v_fmac_f32_e32 v133, v134, v133
	s_nop 0
	v_div_scale_f32 v134, vcc, 1.0, v96, 1.0
	v_mul_f32_e64 v135, v134, v133
	v_fma_f32 v136, -v132, v135, v134
	v_fmac_f32_e32 v135, v136, v133
	s_nop 0
	v_fma_f32 v132, -v132, v135, v134
	v_div_fmas_f32 v132, v132, v133, v135
	v_div_fixup_f32 v136, v132, v96, 1.0
	ds_read_b128 v[132:135], v177
	ds_read_b128 v[156:159], v177 offset:16
	ds_read_b128 v[160:163], v177 offset:32
	ds_read_b128 v[164:167], v177 offset:48
	ds_read_b128 v[138:141], v177 offset:4096
	ds_read_b128 v[180:183], v177 offset:4112
	v_pk_mul_f32 v[184:185], v[136:137], v[184:185] op_sel_hi:[0,1]
	s_and_b64 vcc, exec, s[2:3]
	s_waitcnt lgkmcnt(1)
	v_pk_fma_f32 v[132:133], v[132:133], v[184:185], v[138:139]
	v_lshlrev_b32_e32 v138, 16, v1
	s_nop 0
	v_and_b32_e32 v139, 0xffff0000, v1
	v_pk_mul_f32 v[138:139], v[136:137], v[138:139] op_sel_hi:[0,1]
	v_pk_fma_f32 v[134:135], v[134:135], v[138:139], v[140:141]
	v_lshlrev_b32_e32 v138, 16, v2
	s_nop 0
	v_and_b32_e32 v139, 0xffff0000, v2
	v_pk_mul_f32 v[138:139], v[136:137], v[138:139] op_sel_hi:[0,1]
	s_waitcnt lgkmcnt(0)
	s_nop 0
	v_pk_fma_f32 v[140:141], v[156:157], v[138:139], v[180:181]
	v_lshlrev_b32_e32 v138, 16, v3
	s_nop 0
	v_and_b32_e32 v139, 0xffff0000, v3
	v_pk_mul_f32 v[138:139], v[136:137], v[138:139] op_sel_hi:[0,1]
	v_med3_f32 v96, v132, s82, v229
	v_med3_f32 v137, v133, s82, v229
	v_mov_b32_e64 v180, v97
	v_cvt_pk_fp8_f32 v180, v96, v137
	v_pk_fma_f32 v[156:157], v[158:159], v[138:139], v[182:183]
	ds_read_b128 v[182:185], v177 offset:4128
	ds_read_b128 v[186:189], v177 offset:4144
	v_med3_f32 v96, v134, s82, v229
	v_med3_f32 v137, v135, s82, v229
	v_med3_f32 v138, v140, s82, v229
	v_med3_f32 v139, v141, s82, v229
	v_mov_b32_e64 v181, v97
	v_cvt_pk_fp8_f32 v181, v138, v139
	v_cvt_pk_fp8_f32 v180, v96, v137 op_sel:[0,0,1]
	v_med3_f32 v137, v157, s82, v229
	v_lshlrev_b32_e32 v138, 16, v4
	s_nop 0
	v_and_b32_e32 v139, 0xffff0000, v4
	v_pk_mul_f32 v[138:139], v[136:137], v[138:139] op_sel_hi:[0,1]
	s_waitcnt lgkmcnt(1)
	s_nop 0
	v_pk_fma_f32 v[158:159], v[160:161], v[138:139], v[182:183]
	v_lshlrev_b32_e32 v138, 16, v5
	s_nop 0
	v_and_b32_e32 v139, 0xffff0000, v5
	v_pk_mul_f32 v[138:139], v[136:137], v[138:139] op_sel_hi:[0,1]
	v_pk_fma_f32 v[160:161], v[162:163], v[138:139], v[184:185]
	v_lshlrev_b32_e32 v138, 16, v6
	s_nop 0
	v_and_b32_e32 v139, 0xffff0000, v6
	v_pk_mul_f32 v[138:139], v[136:137], v[138:139] op_sel_hi:[0,1]
	v_med3_f32 v96, v156, s82, v229
	s_waitcnt lgkmcnt(0)
	s_nop 0
	v_pk_fma_f32 v[162:163], v[164:165], v[138:139], v[186:187]
	v_lshlrev_b32_e32 v138, 16, v7
	s_nop 0
	v_and_b32_e32 v139, 0xffff0000, v7
	v_cvt_pk_fp8_f32 v181, v96, v137 op_sel:[0,0,1]
	v_pk_mul_f32 v[138:139], v[136:137], v[138:139] op_sel_hi:[0,1]
	v_med3_f32 v96, v158, s82, v229
	v_med3_f32 v137, v159, s82, v229
	v_mov_b32_e64 v182, v97
	v_pk_fma_f32 v[164:165], v[166:167], v[138:139], v[188:189]
	v_cvt_pk_fp8_f32 v182, v96, v137
	v_med3_f32 v138, v162, s82, v229
	v_med3_f32 v139, v163, s82, v229
	v_mov_b32_e64 v183, v97
	v_cvt_pk_fp8_f32 v183, v138, v139
	v_med3_f32 v96, v160, s82, v229
	v_med3_f32 v137, v161, s82, v229
	v_cvt_pk_fp8_f32 v182, v96, v137 op_sel:[0,0,1]
	v_med3_f32 v96, v164, s82, v229
	v_med3_f32 v137, v165, s82, v229
	v_cvt_pk_fp8_f32 v183, v96, v137 op_sel:[0,0,1]
	v_lshl_add_u64 v[138:139], v[154:155], 0, v[98:99]
	global_store_dwordx4 v[138:139], v[180:183], off
	s_cbranch_vccnz .LBB0_285
	s_nop 0
	v_cvt_pk_bf16_f32 v132, v132, v133
	v_cvt_pk_bf16_f32 v133, v134, v135
	v_cvt_pk_bf16_f32 v134, v140, v141
	v_cvt_pk_bf16_f32 v135, v156, v157
	ds_read_b128 v[180:183], v178 offset:8192
	v_cvt_pk_bf16_f32 v156, v158, v159
	v_cvt_pk_bf16_f32 v157, v160, v161
	v_cvt_pk_bf16_f32 v158, v162, v163
	v_cvt_pk_bf16_f32 v159, v164, v165
	ds_read_b128 v[160:163], v178 offset:8208
	s_waitcnt lgkmcnt(1)
	s_nop 0
	v_mfma_f32_16x16x32_bf16 v[132:135], v[132:135], v[180:183], 0
	s_waitcnt lgkmcnt(0)
	s_nop 0
	v_mfma_f32_16x16x32_bf16 v[132:135], v[156:159], v[160:163], v[132:135]
	s_branch .LBB0_286

.LBB0_286:
	ds_read_b128 v[156:159], v177 offset:256
	ds_read_b128 v[160:163], v177 offset:272
	ds_read_b128 v[164:167], v177 offset:288
	ds_read_b128 v[180:183], v177 offset:304
	ds_read_b128 v[184:187], v177 offset:4352
	ds_read_b128 v[188:191], v177 offset:4368
	v_mov_b32_e32 v137, v136
	v_lshlrev_b32_e32 v98, 16, v8
	v_and_b32_e32 v99, 0xffff0000, v8
	v_pk_mul_f32 v[98:99], v[136:137], v[98:99]
	v_lshlrev_b32_e32 v140, 16, v9
	s_nop 0
	v_and_b32_e32 v141, 0xffff0000, v9
	s_waitcnt lgkmcnt(1)
	s_nop 0
	v_pk_fma_f32 v[98:99], v[98:99], v[156:157], v[184:185]
	v_pk_mul_f32 v[140:141], v[136:137], v[140:141]
	v_lshlrev_b32_e32 v156, 16, v10
	s_nop 0
	v_and_b32_e32 v157, 0xffff0000, v10
	v_pk_fma_f32 v[140:141], v[140:141], v[158:159], v[186:187]
	v_pk_mul_f32 v[156:157], v[136:137], v[156:157]
	v_lshlrev_b32_e32 v158, 16, v11
	s_nop 0
	v_and_b32_e32 v159, 0xffff0000, v11
	s_waitcnt lgkmcnt(0)
	s_nop 0
	v_pk_fma_f32 v[156:157], v[156:157], v[160:161], v[188:189]
	v_pk_mul_f32 v[158:159], v[136:137], v[158:159]
	v_med3_f32 v96, v98, s82, v229
	v_med3_f32 v160, v99, s82, v229
	v_mov_b32_e64 v184, v97
	v_pk_fma_f32 v[158:159], v[158:159], v[162:163], v[190:191]
	v_cvt_pk_fp8_f32 v184, v96, v160
	v_med3_f32 v161, v156, s82, v229
	v_med3_f32 v162, v157, s82, v229
	v_mov_b32_e64 v185, v97
	v_cvt_pk_fp8_f32 v185, v161, v162
	v_med3_f32 v96, v140, s82, v229
	v_med3_f32 v160, v141, s82, v229
	v_cvt_pk_fp8_f32 v184, v96, v160 op_sel:[0,0,1]
	v_med3_f32 v96, v158, s82, v229
	v_med3_f32 v160, v159, s82, v229
	v_cvt_pk_fp8_f32 v185, v96, v160 op_sel:[0,0,1]
	ds_read_b128 v[160:163], v177 offset:4384
	ds_read_b128 v[186:189], v177 offset:4400
	v_lshlrev_b32_e32 v190, 16, v12
	s_nop 0
	v_and_b32_e32 v191, 0xffff0000, v12
	v_pk_mul_f32 v[190:191], v[136:137], v[190:191]
	s_and_b64 vcc, exec, s[2:3]
	s_waitcnt lgkmcnt(1)
	v_pk_fma_f32 v[160:161], v[190:191], v[164:165], v[160:161]
	v_lshlrev_b32_e32 v164, 16, v13
	s_nop 0
	v_and_b32_e32 v165, 0xffff0000, v13
	v_pk_mul_f32 v[164:165], v[136:137], v[164:165]
	v_med3_f32 v96, v160, s82, v229
	v_pk_fma_f32 v[162:163], v[164:165], v[166:167], v[162:163]
	v_lshlrev_b32_e32 v164, 16, v14
	s_nop 0
	v_and_b32_e32 v165, 0xffff0000, v14
	v_pk_mul_f32 v[164:165], v[136:137], v[164:165]
	v_med3_f32 v179, v161, s82, v229
	s_waitcnt lgkmcnt(0)
	s_nop 0
	v_pk_fma_f32 v[164:165], v[164:165], v[180:181], v[186:187]
	v_mov_b32_e64 v186, v97
	v_cvt_pk_fp8_f32 v186, v96, v179
	v_med3_f32 v180, v164, s82, v229
	v_med3_f32 v181, v165, s82, v229
	v_mov_b32_e32 v187, v97
	v_lshlrev_b32_e32 v166, 16, v15
	v_and_b32_e32 v167, 0xffff0000, v15
	v_cvt_pk_fp8_f32 v187, v180, v181
	v_pk_mul_f32 v[166:167], v[136:137], v[166:167]
	v_med3_f32 v96, v162, s82, v229
	v_pk_fma_f32 v[166:167], v[166:167], v[182:183], v[188:189]
	v_med3_f32 v179, v163, s82, v229
	v_cvt_pk_fp8_f32 v186, v96, v179 op_sel:[0,0,1]
	v_med3_f32 v96, v166, s82, v229
	v_med3_f32 v179, v167, s82, v229
	v_cvt_pk_fp8_f32 v187, v96, v179 op_sel:[0,0,1]
	global_store_dwordx4 v[138:139], v[184:187], off offset:64
	s_cbranch_vccnz .LBB0_288
	s_nop 0
	v_cvt_pk_bf16_f32 v180, v98, v99
	v_cvt_pk_bf16_f32 v181, v140, v141
	v_cvt_pk_bf16_f32 v182, v156, v157
	v_cvt_pk_bf16_f32 v183, v158, v159
	ds_read_b128 v[156:159], v178 offset:8320
	v_cvt_pk_bf16_f32 v160, v160, v161
	v_cvt_pk_bf16_f32 v161, v162, v163
	v_cvt_pk_bf16_f32 v162, v164, v165
	v_cvt_pk_bf16_f32 v163, v166, v167
	s_waitcnt lgkmcnt(0)
	s_nop 0
	v_mfma_f32_16x16x32_bf16 v[132:135], v[180:183], v[156:159], v[132:135]
	ds_read_b128 v[156:159], v178 offset:8336
	s_waitcnt lgkmcnt(0)
	s_nop 0
	v_mfma_f32_16x16x32_bf16 v[132:135], v[160:163], v[156:159], v[132:135]
.LBB0_288:
	ds_read_b128 v[156:159], v177 offset:512
	ds_read_b128 v[160:163], v177 offset:528
	ds_read_b128 v[164:167], v177 offset:544
	ds_read_b128 v[180:183], v177 offset:560
	ds_read_b128 v[184:187], v177 offset:4608
	ds_read_b128 v[188:191], v177 offset:4624
	v_lshlrev_b32_e32 v98, 16, v16
	s_nop 0
	v_and_b32_e32 v99, 0xffff0000, v16
	v_pk_mul_f32 v[98:99], v[136:137], v[98:99]
	v_lshlrev_b32_e32 v140, 16, v17
	s_nop 0
	v_and_b32_e32 v141, 0xffff0000, v17
	s_waitcnt lgkmcnt(1)
	s_nop 0
	v_pk_fma_f32 v[98:99], v[98:99], v[156:157], v[184:185]
	v_pk_mul_f32 v[140:141], v[136:137], v[140:141]
	v_lshlrev_b32_e32 v156, 16, v18
	s_nop 0
	v_and_b32_e32 v157, 0xffff0000, v18
	v_pk_fma_f32 v[140:141], v[140:141], v[158:159], v[186:187]
	v_pk_mul_f32 v[156:157], v[136:137], v[156:157]
	v_lshlrev_b32_e32 v158, 16, v19
	s_nop 0
	v_and_b32_e32 v159, 0xffff0000, v19
	s_waitcnt lgkmcnt(0)
	s_nop 0
	v_pk_fma_f32 v[156:157], v[156:157], v[160:161], v[188:189]
	v_pk_mul_f32 v[158:159], v[136:137], v[158:159]
	v_med3_f32 v96, v98, s82, v229
	v_med3_f32 v160, v99, s82, v229
	v_mov_b32_e64 v184, v97
	v_pk_fma_f32 v[158:159], v[158:159], v[162:163], v[190:191]
	v_cvt_pk_fp8_f32 v184, v96, v160
	v_med3_f32 v161, v156, s82, v229
	v_med3_f32 v162, v157, s82, v229
	v_mov_b32_e64 v185, v97
	v_cvt_pk_fp8_f32 v185, v161, v162
	v_med3_f32 v96, v140, s82, v229
	v_med3_f32 v160, v141, s82, v229
	v_cvt_pk_fp8_f32 v184, v96, v160 op_sel:[0,0,1]
	v_med3_f32 v96, v158, s82, v229
	v_med3_f32 v160, v159, s82, v229
	v_cvt_pk_fp8_f32 v185, v96, v160 op_sel:[0,0,1]
	ds_read_b128 v[160:163], v177 offset:4640
	ds_read_b128 v[186:189], v177 offset:4656
	v_lshlrev_b32_e32 v190, 16, v20
	s_nop 0
	v_and_b32_e32 v191, 0xffff0000, v20
	v_pk_mul_f32 v[190:191], v[136:137], v[190:191]
	s_and_b64 vcc, exec, s[2:3]
	s_waitcnt lgkmcnt(1)
	v_pk_fma_f32 v[160:161], v[190:191], v[164:165], v[160:161]
	v_lshlrev_b32_e32 v164, 16, v21
	s_nop 0
	v_and_b32_e32 v165, 0xffff0000, v21
	v_pk_mul_f32 v[164:165], v[136:137], v[164:165]
	v_med3_f32 v96, v160, s82, v229
	v_pk_fma_f32 v[162:163], v[164:165], v[166:167], v[162:163]
	v_lshlrev_b32_e32 v164, 16, v22
	s_nop 0
	v_and_b32_e32 v165, 0xffff0000, v22
	v_pk_mul_f32 v[164:165], v[136:137], v[164:165]
	v_med3_f32 v179, v161, s82, v229
	s_waitcnt lgkmcnt(0)
	s_nop 0
	v_pk_fma_f32 v[164:165], v[164:165], v[180:181], v[186:187]
	v_mov_b32_e64 v186, v97
	v_cvt_pk_fp8_f32 v186, v96, v179
	v_med3_f32 v180, v164, s82, v229
	v_med3_f32 v181, v165, s82, v229
	v_mov_b32_e32 v187, v97
	v_lshlrev_b32_e32 v166, 16, v23
	v_and_b32_e32 v167, 0xffff0000, v23
	v_cvt_pk_fp8_f32 v187, v180, v181
	v_pk_mul_f32 v[166:167], v[136:137], v[166:167]
	v_med3_f32 v96, v162, s82, v229
	v_pk_fma_f32 v[166:167], v[166:167], v[182:183], v[188:189]
	v_med3_f32 v179, v163, s82, v229
	v_cvt_pk_fp8_f32 v186, v96, v179 op_sel:[0,0,1]
	v_med3_f32 v96, v166, s82, v229
	v_med3_f32 v179, v167, s82, v229
	v_cvt_pk_fp8_f32 v187, v96, v179 op_sel:[0,0,1]
	global_store_dwordx4 v[138:139], v[184:187], off offset:128
	s_cbranch_vccnz .LBB0_290
	s_nop 0
	v_cvt_pk_bf16_f32 v180, v98, v99
	v_cvt_pk_bf16_f32 v181, v140, v141
	v_cvt_pk_bf16_f32 v182, v156, v157
	v_cvt_pk_bf16_f32 v183, v158, v159
	ds_read_b128 v[156:159], v178 offset:8448
	v_cvt_pk_bf16_f32 v160, v160, v161
	v_cvt_pk_bf16_f32 v161, v162, v163
	v_cvt_pk_bf16_f32 v162, v164, v165
	v_cvt_pk_bf16_f32 v163, v166, v167
	s_waitcnt lgkmcnt(0)
	s_nop 0
	v_mfma_f32_16x16x32_bf16 v[132:135], v[180:183], v[156:159], v[132:135]
	ds_read_b128 v[156:159], v178 offset:8464
	s_waitcnt lgkmcnt(0)
	s_nop 0
	v_mfma_f32_16x16x32_bf16 v[132:135], v[160:163], v[156:159], v[132:135]
.LBB0_290:
	ds_read_b128 v[156:159], v177 offset:768
	ds_read_b128 v[160:163], v177 offset:784
	ds_read_b128 v[164:167], v177 offset:800
	ds_read_b128 v[180:183], v177 offset:816
	ds_read_b128 v[184:187], v177 offset:4864
	ds_read_b128 v[188:191], v177 offset:4880
	v_lshlrev_b32_e32 v98, 16, v24
	s_nop 0
	v_and_b32_e32 v99, 0xffff0000, v24
	v_pk_mul_f32 v[98:99], v[136:137], v[98:99]
	v_lshlrev_b32_e32 v140, 16, v25
	s_nop 0
	v_and_b32_e32 v141, 0xffff0000, v25
	s_waitcnt lgkmcnt(1)
	s_nop 0
	v_pk_fma_f32 v[98:99], v[98:99], v[156:157], v[184:185]
	v_pk_mul_f32 v[140:141], v[136:137], v[140:141]
	v_lshlrev_b32_e32 v156, 16, v26
	s_nop 0
	v_and_b32_e32 v157, 0xffff0000, v26
	v_pk_fma_f32 v[140:141], v[140:141], v[158:159], v[186:187]
	v_pk_mul_f32 v[156:157], v[136:137], v[156:157]
	v_lshlrev_b32_e32 v158, 16, v27
	s_nop 0
	v_and_b32_e32 v159, 0xffff0000, v27
	s_waitcnt lgkmcnt(0)
	s_nop 0
	v_pk_fma_f32 v[156:157], v[156:157], v[160:161], v[188:189]
	v_pk_mul_f32 v[158:159], v[136:137], v[158:159]
	v_med3_f32 v96, v98, s82, v229
	v_med3_f32 v160, v99, s82, v229
	v_mov_b32_e64 v184, v97
	v_pk_fma_f32 v[158:159], v[158:159], v[162:163], v[190:191]
	v_cvt_pk_fp8_f32 v184, v96, v160
	v_med3_f32 v161, v156, s82, v229
	v_med3_f32 v162, v157, s82, v229
	v_mov_b32_e64 v185, v97
	v_cvt_pk_fp8_f32 v185, v161, v162
	v_med3_f32 v96, v140, s82, v229
	v_med3_f32 v160, v141, s82, v229
	v_cvt_pk_fp8_f32 v184, v96, v160 op_sel:[0,0,1]
	v_med3_f32 v96, v158, s82, v229
	v_med3_f32 v160, v159, s82, v229
	v_cvt_pk_fp8_f32 v185, v96, v160 op_sel:[0,0,1]
	ds_read_b128 v[160:163], v177 offset:4896
	ds_read_b128 v[186:189], v177 offset:4912
	v_lshlrev_b32_e32 v190, 16, v28
	s_nop 0
	v_and_b32_e32 v191, 0xffff0000, v28
	v_pk_mul_f32 v[190:191], v[136:137], v[190:191]
	s_and_b64 vcc, exec, s[2:3]
	s_waitcnt lgkmcnt(1)
	v_pk_fma_f32 v[160:161], v[190:191], v[164:165], v[160:161]
	v_lshlrev_b32_e32 v164, 16, v29
	s_nop 0
	v_and_b32_e32 v165, 0xffff0000, v29
	v_pk_mul_f32 v[164:165], v[136:137], v[164:165]
	v_med3_f32 v96, v160, s82, v229
	v_pk_fma_f32 v[162:163], v[164:165], v[166:167], v[162:163]
	v_lshlrev_b32_e32 v164, 16, v30
	s_nop 0
	v_and_b32_e32 v165, 0xffff0000, v30
	v_pk_mul_f32 v[164:165], v[136:137], v[164:165]
	v_med3_f32 v179, v161, s82, v229
	s_waitcnt lgkmcnt(0)
	s_nop 0
	v_pk_fma_f32 v[164:165], v[164:165], v[180:181], v[186:187]
	v_mov_b32_e64 v186, v97
	v_cvt_pk_fp8_f32 v186, v96, v179
	v_med3_f32 v180, v164, s82, v229
	v_med3_f32 v181, v165, s82, v229
	v_mov_b32_e32 v187, v97
	v_lshlrev_b32_e32 v166, 16, v31
	v_and_b32_e32 v167, 0xffff0000, v31
	v_cvt_pk_fp8_f32 v187, v180, v181
	v_pk_mul_f32 v[166:167], v[136:137], v[166:167]
	v_med3_f32 v96, v162, s82, v229
	v_pk_fma_f32 v[166:167], v[166:167], v[182:183], v[188:189]
	v_med3_f32 v179, v163, s82, v229
	v_cvt_pk_fp8_f32 v186, v96, v179 op_sel:[0,0,1]
	v_med3_f32 v96, v166, s82, v229
	v_med3_f32 v179, v167, s82, v229
	v_cvt_pk_fp8_f32 v187, v96, v179 op_sel:[0,0,1]
	global_store_dwordx4 v[138:139], v[184:187], off offset:192
	s_cbranch_vccnz .LBB0_292
	s_nop 0
	v_cvt_pk_bf16_f32 v180, v98, v99
	v_cvt_pk_bf16_f32 v181, v140, v141
	v_cvt_pk_bf16_f32 v182, v156, v157
	v_cvt_pk_bf16_f32 v183, v158, v159
	ds_read_b128 v[156:159], v178 offset:8576
	v_cvt_pk_bf16_f32 v160, v160, v161
	v_cvt_pk_bf16_f32 v161, v162, v163
	v_cvt_pk_bf16_f32 v162, v164, v165
	v_cvt_pk_bf16_f32 v163, v166, v167
	s_waitcnt lgkmcnt(0)
	s_nop 0
	v_mfma_f32_16x16x32_bf16 v[132:135], v[180:183], v[156:159], v[132:135]
	ds_read_b128 v[156:159], v178 offset:8592
	s_waitcnt lgkmcnt(0)
	s_nop 0
	v_mfma_f32_16x16x32_bf16 v[132:135], v[160:163], v[156:159], v[132:135]
.LBB0_292:
	ds_read_b128 v[156:159], v177 offset:1024
	ds_read_b128 v[160:163], v177 offset:1040
	ds_read_b128 v[164:167], v177 offset:1056
	ds_read_b128 v[180:183], v177 offset:1072
	ds_read_b128 v[184:187], v177 offset:5120
	ds_read_b128 v[188:191], v177 offset:5136
	v_lshlrev_b32_e32 v98, 16, v32
	s_nop 0
	v_and_b32_e32 v99, 0xffff0000, v32
	v_pk_mul_f32 v[98:99], v[136:137], v[98:99]
	v_lshlrev_b32_e32 v140, 16, v33
	s_nop 0
	v_and_b32_e32 v141, 0xffff0000, v33
	s_waitcnt lgkmcnt(1)
	s_nop 0
	v_pk_fma_f32 v[98:99], v[98:99], v[156:157], v[184:185]
	v_pk_mul_f32 v[140:141], v[136:137], v[140:141]
	v_lshlrev_b32_e32 v156, 16, v34
	s_nop 0
	v_and_b32_e32 v157, 0xffff0000, v34
	v_pk_fma_f32 v[140:141], v[140:141], v[158:159], v[186:187]
	v_pk_mul_f32 v[156:157], v[136:137], v[156:157]
	v_lshlrev_b32_e32 v158, 16, v35
	s_nop 0
	v_and_b32_e32 v159, 0xffff0000, v35
	s_waitcnt lgkmcnt(0)
	s_nop 0
	v_pk_fma_f32 v[156:157], v[156:157], v[160:161], v[188:189]
	v_pk_mul_f32 v[158:159], v[136:137], v[158:159]
	v_med3_f32 v96, v98, s82, v229
	v_med3_f32 v160, v99, s82, v229
	v_mov_b32_e64 v184, v97
	v_pk_fma_f32 v[158:159], v[158:159], v[162:163], v[190:191]
	v_cvt_pk_fp8_f32 v184, v96, v160
	v_med3_f32 v161, v156, s82, v229
	v_med3_f32 v162, v157, s82, v229
	v_mov_b32_e64 v185, v97
	v_cvt_pk_fp8_f32 v185, v161, v162
	v_med3_f32 v96, v140, s82, v229
	v_med3_f32 v160, v141, s82, v229
	v_cvt_pk_fp8_f32 v184, v96, v160 op_sel:[0,0,1]
	v_med3_f32 v96, v158, s82, v229
	v_med3_f32 v160, v159, s82, v229
	v_cvt_pk_fp8_f32 v185, v96, v160 op_sel:[0,0,1]
	ds_read_b128 v[160:163], v177 offset:5152
	ds_read_b128 v[186:189], v177 offset:5168
	v_lshlrev_b32_e32 v190, 16, v36
	s_nop 0
	v_and_b32_e32 v191, 0xffff0000, v36
	v_pk_mul_f32 v[190:191], v[136:137], v[190:191]
	s_and_b64 vcc, exec, s[2:3]
	s_waitcnt lgkmcnt(1)
	v_pk_fma_f32 v[160:161], v[190:191], v[164:165], v[160:161]
	v_lshlrev_b32_e32 v164, 16, v37
	s_nop 0
	v_and_b32_e32 v165, 0xffff0000, v37
	v_pk_mul_f32 v[164:165], v[136:137], v[164:165]
	v_med3_f32 v96, v160, s82, v229
	v_pk_fma_f32 v[162:163], v[164:165], v[166:167], v[162:163]
	v_lshlrev_b32_e32 v164, 16, v38
	s_nop 0
	v_and_b32_e32 v165, 0xffff0000, v38
	v_pk_mul_f32 v[164:165], v[136:137], v[164:165]
	v_med3_f32 v179, v161, s82, v229
	s_waitcnt lgkmcnt(0)
	s_nop 0
	v_pk_fma_f32 v[164:165], v[164:165], v[180:181], v[186:187]
	v_mov_b32_e64 v186, v97
	v_cvt_pk_fp8_f32 v186, v96, v179
	v_med3_f32 v180, v164, s82, v229
	v_med3_f32 v181, v165, s82, v229
	v_mov_b32_e32 v187, v97
	v_lshlrev_b32_e32 v166, 16, v39
	v_and_b32_e32 v167, 0xffff0000, v39
	v_cvt_pk_fp8_f32 v187, v180, v181
	v_pk_mul_f32 v[166:167], v[136:137], v[166:167]
	v_med3_f32 v96, v162, s82, v229
	v_pk_fma_f32 v[166:167], v[166:167], v[182:183], v[188:189]
	v_med3_f32 v179, v163, s82, v229
	v_cvt_pk_fp8_f32 v186, v96, v179 op_sel:[0,0,1]
	v_med3_f32 v96, v166, s82, v229
	v_med3_f32 v179, v167, s82, v229
	v_cvt_pk_fp8_f32 v187, v96, v179 op_sel:[0,0,1]
	global_store_dwordx4 v[138:139], v[184:187], off offset:256
	s_cbranch_vccnz .LBB0_294
	s_nop 0
	v_cvt_pk_bf16_f32 v180, v98, v99
	v_cvt_pk_bf16_f32 v181, v140, v141
	v_cvt_pk_bf16_f32 v182, v156, v157
	v_cvt_pk_bf16_f32 v183, v158, v159
	ds_read_b128 v[156:159], v178 offset:8704
	v_cvt_pk_bf16_f32 v160, v160, v161
	v_cvt_pk_bf16_f32 v161, v162, v163
	v_cvt_pk_bf16_f32 v162, v164, v165
	v_cvt_pk_bf16_f32 v163, v166, v167
	s_waitcnt lgkmcnt(0)
	s_nop 0
	v_mfma_f32_16x16x32_bf16 v[132:135], v[180:183], v[156:159], v[132:135]
	ds_read_b128 v[156:159], v178 offset:8720
	s_waitcnt lgkmcnt(0)
	s_nop 0
	v_mfma_f32_16x16x32_bf16 v[132:135], v[160:163], v[156:159], v[132:135]
.LBB0_294:
	ds_read_b128 v[156:159], v177 offset:1280
	ds_read_b128 v[160:163], v177 offset:1296
	ds_read_b128 v[164:167], v177 offset:1312
	ds_read_b128 v[180:183], v177 offset:1328
	ds_read_b128 v[184:187], v177 offset:5376
	ds_read_b128 v[188:191], v177 offset:5392
	v_lshlrev_b32_e32 v98, 16, v40
	s_nop 0
	v_and_b32_e32 v99, 0xffff0000, v40
	v_pk_mul_f32 v[98:99], v[136:137], v[98:99]
	v_lshlrev_b32_e32 v140, 16, v41
	s_nop 0
	v_and_b32_e32 v141, 0xffff0000, v41
	s_waitcnt lgkmcnt(1)
	s_nop 0
	v_pk_fma_f32 v[98:99], v[98:99], v[156:157], v[184:185]
	v_pk_mul_f32 v[140:141], v[136:137], v[140:141]
	v_lshlrev_b32_e32 v156, 16, v42
	s_nop 0
	v_and_b32_e32 v157, 0xffff0000, v42
	v_pk_fma_f32 v[140:141], v[140:141], v[158:159], v[186:187]
	v_pk_mul_f32 v[156:157], v[136:137], v[156:157]
	v_lshlrev_b32_e32 v158, 16, v43
	s_nop 0
	v_and_b32_e32 v159, 0xffff0000, v43
	s_waitcnt lgkmcnt(0)
	s_nop 0
	v_pk_fma_f32 v[156:157], v[156:157], v[160:161], v[188:189]
	v_pk_mul_f32 v[158:159], v[136:137], v[158:159]
	v_med3_f32 v96, v98, s82, v229
	v_med3_f32 v160, v99, s82, v229
	v_mov_b32_e64 v184, v97
	v_pk_fma_f32 v[158:159], v[158:159], v[162:163], v[190:191]
	v_cvt_pk_fp8_f32 v184, v96, v160
	v_med3_f32 v161, v156, s82, v229
	v_med3_f32 v162, v157, s82, v229
	v_mov_b32_e64 v185, v97
	v_cvt_pk_fp8_f32 v185, v161, v162
	v_med3_f32 v96, v140, s82, v229
	v_med3_f32 v160, v141, s82, v229
	v_cvt_pk_fp8_f32 v184, v96, v160 op_sel:[0,0,1]
	v_med3_f32 v96, v158, s82, v229
	v_med3_f32 v160, v159, s82, v229
	v_cvt_pk_fp8_f32 v185, v96, v160 op_sel:[0,0,1]
	ds_read_b128 v[160:163], v177 offset:5408
	ds_read_b128 v[186:189], v177 offset:5424
	v_lshlrev_b32_e32 v190, 16, v44
	s_nop 0
	v_and_b32_e32 v191, 0xffff0000, v44
	v_pk_mul_f32 v[190:191], v[136:137], v[190:191]
	s_and_b64 vcc, exec, s[2:3]
	s_waitcnt lgkmcnt(1)
	v_pk_fma_f32 v[160:161], v[190:191], v[164:165], v[160:161]
	v_lshlrev_b32_e32 v164, 16, v45
	s_nop 0
	v_and_b32_e32 v165, 0xffff0000, v45
	v_pk_mul_f32 v[164:165], v[136:137], v[164:165]
	v_med3_f32 v96, v160, s82, v229
	v_pk_fma_f32 v[162:163], v[164:165], v[166:167], v[162:163]
	v_lshlrev_b32_e32 v164, 16, v46
	s_nop 0
	v_and_b32_e32 v165, 0xffff0000, v46
	v_pk_mul_f32 v[164:165], v[136:137], v[164:165]
	v_med3_f32 v179, v161, s82, v229
	s_waitcnt lgkmcnt(0)
	s_nop 0
	v_pk_fma_f32 v[164:165], v[164:165], v[180:181], v[186:187]
	v_mov_b32_e64 v186, v97
	v_cvt_pk_fp8_f32 v186, v96, v179
	v_med3_f32 v180, v164, s82, v229
	v_med3_f32 v181, v165, s82, v229
	v_mov_b32_e32 v187, v97
	v_lshlrev_b32_e32 v166, 16, v47
	v_and_b32_e32 v167, 0xffff0000, v47
	v_cvt_pk_fp8_f32 v187, v180, v181
	v_pk_mul_f32 v[166:167], v[136:137], v[166:167]
	v_med3_f32 v96, v162, s82, v229
	v_pk_fma_f32 v[166:167], v[166:167], v[182:183], v[188:189]
	v_med3_f32 v179, v163, s82, v229
	v_cvt_pk_fp8_f32 v186, v96, v179 op_sel:[0,0,1]
	v_med3_f32 v96, v166, s82, v229
	v_med3_f32 v179, v167, s82, v229
	v_cvt_pk_fp8_f32 v187, v96, v179 op_sel:[0,0,1]
	global_store_dwordx4 v[138:139], v[184:187], off offset:320
	s_cbranch_vccnz .LBB0_296
	s_nop 0
	v_cvt_pk_bf16_f32 v180, v98, v99
	v_cvt_pk_bf16_f32 v181, v140, v141
	v_cvt_pk_bf16_f32 v182, v156, v157
	v_cvt_pk_bf16_f32 v183, v158, v159
	ds_read_b128 v[156:159], v178 offset:8832
	v_cvt_pk_bf16_f32 v160, v160, v161
	v_cvt_pk_bf16_f32 v161, v162, v163
	v_cvt_pk_bf16_f32 v162, v164, v165
	v_cvt_pk_bf16_f32 v163, v166, v167
	s_waitcnt lgkmcnt(0)
	s_nop 0
	v_mfma_f32_16x16x32_bf16 v[132:135], v[180:183], v[156:159], v[132:135]
	ds_read_b128 v[156:159], v178 offset:8848
	s_waitcnt lgkmcnt(0)
	s_nop 0
	v_mfma_f32_16x16x32_bf16 v[132:135], v[160:163], v[156:159], v[132:135]
.LBB0_296:
	ds_read_b128 v[156:159], v177 offset:1536
	ds_read_b128 v[160:163], v177 offset:1552
	ds_read_b128 v[164:167], v177 offset:1568
	ds_read_b128 v[180:183], v177 offset:1584
	ds_read_b128 v[184:187], v177 offset:5632
	ds_read_b128 v[188:191], v177 offset:5648
	v_lshlrev_b32_e32 v98, 16, v48
	s_nop 0
	v_and_b32_e32 v99, 0xffff0000, v48
	v_pk_mul_f32 v[98:99], v[136:137], v[98:99]
	v_lshlrev_b32_e32 v140, 16, v49
	s_nop 0
	v_and_b32_e32 v141, 0xffff0000, v49
	s_waitcnt lgkmcnt(1)
	s_nop 0
	v_pk_fma_f32 v[98:99], v[98:99], v[156:157], v[184:185]
	v_pk_mul_f32 v[140:141], v[136:137], v[140:141]
	v_lshlrev_b32_e32 v156, 16, v50
	s_nop 0
	v_and_b32_e32 v157, 0xffff0000, v50
	v_pk_fma_f32 v[140:141], v[140:141], v[158:159], v[186:187]
	v_pk_mul_f32 v[156:157], v[136:137], v[156:157]
	v_lshlrev_b32_e32 v158, 16, v51
	s_nop 0
	v_and_b32_e32 v159, 0xffff0000, v51
	s_waitcnt lgkmcnt(0)
	s_nop 0
	v_pk_fma_f32 v[156:157], v[156:157], v[160:161], v[188:189]
	v_pk_mul_f32 v[158:159], v[136:137], v[158:159]
	v_med3_f32 v96, v98, s82, v229
	v_med3_f32 v160, v99, s82, v229
	v_mov_b32_e64 v184, v97
	v_pk_fma_f32 v[158:159], v[158:159], v[162:163], v[190:191]
	v_cvt_pk_fp8_f32 v184, v96, v160
	v_med3_f32 v161, v156, s82, v229
	v_med3_f32 v162, v157, s82, v229
	v_mov_b32_e64 v185, v97
	v_cvt_pk_fp8_f32 v185, v161, v162
	v_med3_f32 v96, v140, s82, v229
	v_med3_f32 v160, v141, s82, v229
	v_cvt_pk_fp8_f32 v184, v96, v160 op_sel:[0,0,1]
	v_med3_f32 v96, v158, s82, v229
	v_med3_f32 v160, v159, s82, v229
	v_cvt_pk_fp8_f32 v185, v96, v160 op_sel:[0,0,1]
	ds_read_b128 v[160:163], v177 offset:5664
	ds_read_b128 v[186:189], v177 offset:5680
	v_lshlrev_b32_e32 v190, 16, v52
	s_nop 0
	v_and_b32_e32 v191, 0xffff0000, v52
	v_pk_mul_f32 v[190:191], v[136:137], v[190:191]
	s_and_b64 vcc, exec, s[2:3]
	s_waitcnt lgkmcnt(1)
	v_pk_fma_f32 v[160:161], v[190:191], v[164:165], v[160:161]
	v_lshlrev_b32_e32 v164, 16, v53
	s_nop 0
	v_and_b32_e32 v165, 0xffff0000, v53
	v_pk_mul_f32 v[164:165], v[136:137], v[164:165]
	v_med3_f32 v96, v160, s82, v229
	v_pk_fma_f32 v[162:163], v[164:165], v[166:167], v[162:163]
	v_lshlrev_b32_e32 v164, 16, v54
	s_nop 0
	v_and_b32_e32 v165, 0xffff0000, v54
	v_pk_mul_f32 v[164:165], v[136:137], v[164:165]
	v_med3_f32 v179, v161, s82, v229
	s_waitcnt lgkmcnt(0)
	s_nop 0
	v_pk_fma_f32 v[164:165], v[164:165], v[180:181], v[186:187]
	v_mov_b32_e64 v186, v97
	v_cvt_pk_fp8_f32 v186, v96, v179
	v_med3_f32 v180, v164, s82, v229
	v_med3_f32 v181, v165, s82, v229
	v_mov_b32_e32 v187, v97
	v_lshlrev_b32_e32 v166, 16, v55
	v_and_b32_e32 v167, 0xffff0000, v55
	v_cvt_pk_fp8_f32 v187, v180, v181
	v_pk_mul_f32 v[166:167], v[136:137], v[166:167]
	v_med3_f32 v96, v162, s82, v229
	v_pk_fma_f32 v[166:167], v[166:167], v[182:183], v[188:189]
	v_med3_f32 v179, v163, s82, v229
	v_cvt_pk_fp8_f32 v186, v96, v179 op_sel:[0,0,1]
	v_med3_f32 v96, v166, s82, v229
	v_med3_f32 v179, v167, s82, v229
	v_cvt_pk_fp8_f32 v187, v96, v179 op_sel:[0,0,1]
	global_store_dwordx4 v[138:139], v[184:187], off offset:384
	s_cbranch_vccnz .LBB0_298
	s_nop 0
	v_cvt_pk_bf16_f32 v180, v98, v99
	v_cvt_pk_bf16_f32 v181, v140, v141
	v_cvt_pk_bf16_f32 v182, v156, v157
	v_cvt_pk_bf16_f32 v183, v158, v159
	ds_read_b128 v[156:159], v178 offset:8960
	v_cvt_pk_bf16_f32 v160, v160, v161
	v_cvt_pk_bf16_f32 v161, v162, v163
	v_cvt_pk_bf16_f32 v162, v164, v165
	v_cvt_pk_bf16_f32 v163, v166, v167
	s_waitcnt lgkmcnt(0)
	s_nop 0
	v_mfma_f32_16x16x32_bf16 v[132:135], v[180:183], v[156:159], v[132:135]
	ds_read_b128 v[156:159], v178 offset:8976
	s_waitcnt lgkmcnt(0)
	s_nop 0
	v_mfma_f32_16x16x32_bf16 v[132:135], v[160:163], v[156:159], v[132:135]
.LBB0_298:
	ds_read_b128 v[156:159], v177 offset:1792
	ds_read_b128 v[160:163], v177 offset:1808
	ds_read_b128 v[164:167], v177 offset:1824
	ds_read_b128 v[180:183], v177 offset:1840
	ds_read_b128 v[184:187], v177 offset:5888
	ds_read_b128 v[188:191], v177 offset:5904
	v_lshlrev_b32_e32 v98, 16, v56
	s_nop 0
	v_and_b32_e32 v99, 0xffff0000, v56
	v_pk_mul_f32 v[98:99], v[136:137], v[98:99]
	v_lshlrev_b32_e32 v140, 16, v57
	s_nop 0
	v_and_b32_e32 v141, 0xffff0000, v57
	s_waitcnt lgkmcnt(1)
	s_nop 0
	v_pk_fma_f32 v[98:99], v[98:99], v[156:157], v[184:185]
	v_pk_mul_f32 v[140:141], v[136:137], v[140:141]
	v_lshlrev_b32_e32 v156, 16, v58
	s_nop 0
	v_and_b32_e32 v157, 0xffff0000, v58
	v_pk_fma_f32 v[140:141], v[140:141], v[158:159], v[186:187]
	v_pk_mul_f32 v[156:157], v[136:137], v[156:157]
	v_lshlrev_b32_e32 v158, 16, v59
	s_nop 0
	v_and_b32_e32 v159, 0xffff0000, v59
	s_waitcnt lgkmcnt(0)
	s_nop 0
	v_pk_fma_f32 v[156:157], v[156:157], v[160:161], v[188:189]
	v_pk_mul_f32 v[158:159], v[136:137], v[158:159]
	v_med3_f32 v96, v98, s82, v229
	v_med3_f32 v160, v99, s82, v229
	v_mov_b32_e64 v184, v97
	v_pk_fma_f32 v[158:159], v[158:159], v[162:163], v[190:191]
	v_cvt_pk_fp8_f32 v184, v96, v160
	v_med3_f32 v161, v156, s82, v229
	v_med3_f32 v162, v157, s82, v229
	v_mov_b32_e64 v185, v97
	v_cvt_pk_fp8_f32 v185, v161, v162
	v_med3_f32 v96, v140, s82, v229
	v_med3_f32 v160, v141, s82, v229
	v_cvt_pk_fp8_f32 v184, v96, v160 op_sel:[0,0,1]
	v_med3_f32 v96, v158, s82, v229
	v_med3_f32 v160, v159, s82, v229
	v_cvt_pk_fp8_f32 v185, v96, v160 op_sel:[0,0,1]
	ds_read_b128 v[160:163], v177 offset:5920
	ds_read_b128 v[186:189], v177 offset:5936
	v_lshlrev_b32_e32 v190, 16, v60
	s_nop 0
	v_and_b32_e32 v191, 0xffff0000, v60
	v_pk_mul_f32 v[190:191], v[136:137], v[190:191]
	s_and_b64 vcc, exec, s[2:3]
	s_waitcnt lgkmcnt(1)
	v_pk_fma_f32 v[160:161], v[190:191], v[164:165], v[160:161]
	v_lshlrev_b32_e32 v164, 16, v61
	s_nop 0
	v_and_b32_e32 v165, 0xffff0000, v61
	v_pk_mul_f32 v[164:165], v[136:137], v[164:165]
	v_med3_f32 v96, v160, s82, v229
	v_pk_fma_f32 v[162:163], v[164:165], v[166:167], v[162:163]
	v_lshlrev_b32_e32 v164, 16, v62
	s_nop 0
	v_and_b32_e32 v165, 0xffff0000, v62
	v_pk_mul_f32 v[164:165], v[136:137], v[164:165]
	v_med3_f32 v179, v161, s82, v229
	s_waitcnt lgkmcnt(0)
	s_nop 0
	v_pk_fma_f32 v[164:165], v[164:165], v[180:181], v[186:187]
	v_mov_b32_e64 v186, v97
	v_cvt_pk_fp8_f32 v186, v96, v179
	v_med3_f32 v180, v164, s82, v229
	v_med3_f32 v181, v165, s82, v229
	v_mov_b32_e32 v187, v97
	v_lshlrev_b32_e32 v166, 16, v63
	v_and_b32_e32 v167, 0xffff0000, v63
	v_cvt_pk_fp8_f32 v187, v180, v181
	v_pk_mul_f32 v[166:167], v[136:137], v[166:167]
	v_med3_f32 v96, v162, s82, v229
	v_pk_fma_f32 v[166:167], v[166:167], v[182:183], v[188:189]
	v_med3_f32 v179, v163, s82, v229
	v_cvt_pk_fp8_f32 v186, v96, v179 op_sel:[0,0,1]
	v_med3_f32 v96, v166, s82, v229
	v_med3_f32 v179, v167, s82, v229
	v_cvt_pk_fp8_f32 v187, v96, v179 op_sel:[0,0,1]
	global_store_dwordx4 v[138:139], v[184:187], off offset:448
	s_cbranch_vccnz .LBB0_300
	s_nop 0
	v_cvt_pk_bf16_f32 v180, v98, v99
	v_cvt_pk_bf16_f32 v181, v140, v141
	v_cvt_pk_bf16_f32 v182, v156, v157
	v_cvt_pk_bf16_f32 v183, v158, v159
	ds_read_b128 v[156:159], v178 offset:9088
	v_cvt_pk_bf16_f32 v160, v160, v161
	v_cvt_pk_bf16_f32 v161, v162, v163
	v_cvt_pk_bf16_f32 v162, v164, v165
	v_cvt_pk_bf16_f32 v163, v166, v167
	s_waitcnt lgkmcnt(0)
	s_nop 0
	v_mfma_f32_16x16x32_bf16 v[132:135], v[180:183], v[156:159], v[132:135]
	ds_read_b128 v[156:159], v178 offset:9104
	s_waitcnt lgkmcnt(0)
	s_nop 0
	v_mfma_f32_16x16x32_bf16 v[132:135], v[160:163], v[156:159], v[132:135]
.LBB0_300:
	ds_read_b128 v[156:159], v177 offset:2048
	ds_read_b128 v[160:163], v177 offset:2064
	ds_read_b128 v[164:167], v177 offset:2080
	ds_read_b128 v[180:183], v177 offset:2096
	ds_read_b128 v[184:187], v177 offset:6144
	ds_read_b128 v[188:191], v177 offset:6160
	v_lshlrev_b32_e32 v98, 16, v64
	s_nop 0
	v_and_b32_e32 v99, 0xffff0000, v64
	v_pk_mul_f32 v[98:99], v[136:137], v[98:99]
	v_lshlrev_b32_e32 v140, 16, v65
	s_nop 0
	v_and_b32_e32 v141, 0xffff0000, v65
	s_waitcnt lgkmcnt(1)
	s_nop 0
	v_pk_fma_f32 v[98:99], v[98:99], v[156:157], v[184:185]
	v_pk_mul_f32 v[140:141], v[136:137], v[140:141]
	v_lshlrev_b32_e32 v156, 16, v66
	s_nop 0
	v_and_b32_e32 v157, 0xffff0000, v66
	v_pk_fma_f32 v[140:141], v[140:141], v[158:159], v[186:187]
	v_pk_mul_f32 v[156:157], v[136:137], v[156:157]
	v_lshlrev_b32_e32 v158, 16, v67
	s_nop 0
	v_and_b32_e32 v159, 0xffff0000, v67
	s_waitcnt lgkmcnt(0)
	s_nop 0
	v_pk_fma_f32 v[156:157], v[156:157], v[160:161], v[188:189]
	v_pk_mul_f32 v[158:159], v[136:137], v[158:159]
	v_med3_f32 v96, v98, s82, v229
	v_med3_f32 v160, v99, s82, v229
	v_mov_b32_e64 v184, v97
	v_pk_fma_f32 v[158:159], v[158:159], v[162:163], v[190:191]
	v_cvt_pk_fp8_f32 v184, v96, v160
	v_med3_f32 v161, v156, s82, v229
	v_med3_f32 v162, v157, s82, v229
	v_mov_b32_e64 v185, v97
	v_cvt_pk_fp8_f32 v185, v161, v162
	v_med3_f32 v96, v140, s82, v229
	v_med3_f32 v160, v141, s82, v229
	v_cvt_pk_fp8_f32 v184, v96, v160 op_sel:[0,0,1]
	v_med3_f32 v96, v158, s82, v229
	v_med3_f32 v160, v159, s82, v229
	v_cvt_pk_fp8_f32 v185, v96, v160 op_sel:[0,0,1]
	ds_read_b128 v[160:163], v177 offset:6176
	ds_read_b128 v[186:189], v177 offset:6192
	v_lshlrev_b32_e32 v190, 16, v68
	s_nop 0
	v_and_b32_e32 v191, 0xffff0000, v68
	v_pk_mul_f32 v[190:191], v[136:137], v[190:191]
	s_and_b64 vcc, exec, s[2:3]
	s_waitcnt lgkmcnt(1)
	v_pk_fma_f32 v[160:161], v[190:191], v[164:165], v[160:161]
	v_lshlrev_b32_e32 v164, 16, v69
	s_nop 0
	v_and_b32_e32 v165, 0xffff0000, v69
	v_pk_mul_f32 v[164:165], v[136:137], v[164:165]
	v_med3_f32 v96, v160, s82, v229
	v_pk_fma_f32 v[162:163], v[164:165], v[166:167], v[162:163]
	v_lshlrev_b32_e32 v164, 16, v70
	s_nop 0
	v_and_b32_e32 v165, 0xffff0000, v70
	v_pk_mul_f32 v[164:165], v[136:137], v[164:165]
	v_med3_f32 v179, v161, s82, v229
	s_waitcnt lgkmcnt(0)
	s_nop 0
	v_pk_fma_f32 v[164:165], v[164:165], v[180:181], v[186:187]
	v_mov_b32_e64 v186, v97
	v_cvt_pk_fp8_f32 v186, v96, v179
	v_med3_f32 v180, v164, s82, v229
	v_med3_f32 v181, v165, s82, v229
	v_mov_b32_e32 v187, v97
	v_lshlrev_b32_e32 v166, 16, v71
	v_and_b32_e32 v167, 0xffff0000, v71
	v_cvt_pk_fp8_f32 v187, v180, v181
	v_pk_mul_f32 v[166:167], v[136:137], v[166:167]
	v_med3_f32 v96, v162, s82, v229
	v_pk_fma_f32 v[166:167], v[166:167], v[182:183], v[188:189]
	v_med3_f32 v179, v163, s82, v229
	v_cvt_pk_fp8_f32 v186, v96, v179 op_sel:[0,0,1]
	v_med3_f32 v96, v166, s82, v229
	v_med3_f32 v179, v167, s82, v229
	v_cvt_pk_fp8_f32 v187, v96, v179 op_sel:[0,0,1]
	global_store_dwordx4 v[138:139], v[184:187], off offset:512
	s_cbranch_vccnz .LBB0_302
	s_nop 0
	v_cvt_pk_bf16_f32 v180, v98, v99
	v_cvt_pk_bf16_f32 v181, v140, v141
	v_cvt_pk_bf16_f32 v182, v156, v157
	v_cvt_pk_bf16_f32 v183, v158, v159
	ds_read_b128 v[156:159], v178 offset:9216
	v_cvt_pk_bf16_f32 v160, v160, v161
	v_cvt_pk_bf16_f32 v161, v162, v163
	v_cvt_pk_bf16_f32 v162, v164, v165
	v_cvt_pk_bf16_f32 v163, v166, v167
	s_waitcnt lgkmcnt(0)
	s_nop 0
	v_mfma_f32_16x16x32_bf16 v[132:135], v[180:183], v[156:159], v[132:135]
	ds_read_b128 v[156:159], v178 offset:9232
	s_waitcnt lgkmcnt(0)
	s_nop 0
	v_mfma_f32_16x16x32_bf16 v[132:135], v[160:163], v[156:159], v[132:135]
.LBB0_302:
	ds_read_b128 v[156:159], v177 offset:2304
	ds_read_b128 v[160:163], v177 offset:2320
	ds_read_b128 v[164:167], v177 offset:2336
	ds_read_b128 v[180:183], v177 offset:2352
	ds_read_b128 v[184:187], v177 offset:6400
	ds_read_b128 v[188:191], v177 offset:6416
	v_lshlrev_b32_e32 v98, 16, v72
	s_nop 0
	v_and_b32_e32 v99, 0xffff0000, v72
	v_pk_mul_f32 v[98:99], v[136:137], v[98:99]
	v_lshlrev_b32_e32 v140, 16, v73
	s_nop 0
	v_and_b32_e32 v141, 0xffff0000, v73
	s_waitcnt lgkmcnt(1)
	s_nop 0
	v_pk_fma_f32 v[98:99], v[98:99], v[156:157], v[184:185]
	v_pk_mul_f32 v[140:141], v[136:137], v[140:141]
	v_lshlrev_b32_e32 v156, 16, v74
	s_nop 0
	v_and_b32_e32 v157, 0xffff0000, v74
	v_pk_fma_f32 v[140:141], v[140:141], v[158:159], v[186:187]
	v_pk_mul_f32 v[156:157], v[136:137], v[156:157]
	v_lshlrev_b32_e32 v158, 16, v75
	s_nop 0
	v_and_b32_e32 v159, 0xffff0000, v75
	s_waitcnt lgkmcnt(0)
	s_nop 0
	v_pk_fma_f32 v[156:157], v[156:157], v[160:161], v[188:189]
	v_pk_mul_f32 v[158:159], v[136:137], v[158:159]
	v_med3_f32 v96, v98, s82, v229
	v_med3_f32 v160, v99, s82, v229
	v_mov_b32_e64 v184, v97
	v_pk_fma_f32 v[158:159], v[158:159], v[162:163], v[190:191]
	v_cvt_pk_fp8_f32 v184, v96, v160
	v_med3_f32 v161, v156, s82, v229
	v_med3_f32 v162, v157, s82, v229
	v_mov_b32_e64 v185, v97
	v_cvt_pk_fp8_f32 v185, v161, v162
	v_med3_f32 v96, v140, s82, v229
	v_med3_f32 v160, v141, s82, v229
	v_cvt_pk_fp8_f32 v184, v96, v160 op_sel:[0,0,1]
	v_med3_f32 v96, v158, s82, v229
	v_med3_f32 v160, v159, s82, v229
	v_cvt_pk_fp8_f32 v185, v96, v160 op_sel:[0,0,1]
	ds_read_b128 v[160:163], v177 offset:6432
	ds_read_b128 v[186:189], v177 offset:6448
	v_lshlrev_b32_e32 v190, 16, v76
	s_nop 0
	v_and_b32_e32 v191, 0xffff0000, v76
	v_pk_mul_f32 v[190:191], v[136:137], v[190:191]
	s_and_b64 vcc, exec, s[2:3]
	s_waitcnt lgkmcnt(1)
	v_pk_fma_f32 v[160:161], v[190:191], v[164:165], v[160:161]
	v_lshlrev_b32_e32 v164, 16, v77
	s_nop 0
	v_and_b32_e32 v165, 0xffff0000, v77
	v_pk_mul_f32 v[164:165], v[136:137], v[164:165]
	v_med3_f32 v96, v160, s82, v229
	v_pk_fma_f32 v[162:163], v[164:165], v[166:167], v[162:163]
	v_lshlrev_b32_e32 v164, 16, v78
	s_nop 0
	v_and_b32_e32 v165, 0xffff0000, v78
	v_pk_mul_f32 v[164:165], v[136:137], v[164:165]
	v_med3_f32 v179, v161, s82, v229
	s_waitcnt lgkmcnt(0)
	s_nop 0
	v_pk_fma_f32 v[164:165], v[164:165], v[180:181], v[186:187]
	v_mov_b32_e64 v186, v97
	v_cvt_pk_fp8_f32 v186, v96, v179
	v_med3_f32 v180, v164, s82, v229
	v_med3_f32 v181, v165, s82, v229
	v_mov_b32_e32 v187, v97
	v_lshlrev_b32_e32 v166, 16, v79
	v_and_b32_e32 v167, 0xffff0000, v79
	v_cvt_pk_fp8_f32 v187, v180, v181
	v_pk_mul_f32 v[166:167], v[136:137], v[166:167]
	v_med3_f32 v96, v162, s82, v229
	v_pk_fma_f32 v[166:167], v[166:167], v[182:183], v[188:189]
	v_med3_f32 v179, v163, s82, v229
	v_cvt_pk_fp8_f32 v186, v96, v179 op_sel:[0,0,1]
	v_med3_f32 v96, v166, s82, v229
	v_med3_f32 v179, v167, s82, v229
	v_cvt_pk_fp8_f32 v187, v96, v179 op_sel:[0,0,1]
	global_store_dwordx4 v[138:139], v[184:187], off offset:576
	s_cbranch_vccnz .LBB0_304
	s_nop 0
	v_cvt_pk_bf16_f32 v180, v98, v99
	v_cvt_pk_bf16_f32 v181, v140, v141
	v_cvt_pk_bf16_f32 v182, v156, v157
	v_cvt_pk_bf16_f32 v183, v158, v159
	ds_read_b128 v[156:159], v178 offset:9344
	v_cvt_pk_bf16_f32 v160, v160, v161
	v_cvt_pk_bf16_f32 v161, v162, v163
	v_cvt_pk_bf16_f32 v162, v164, v165
	v_cvt_pk_bf16_f32 v163, v166, v167
	s_waitcnt lgkmcnt(0)
	s_nop 0
	v_mfma_f32_16x16x32_bf16 v[132:135], v[180:183], v[156:159], v[132:135]
	ds_read_b128 v[156:159], v178 offset:9360
	s_waitcnt lgkmcnt(0)
	s_nop 0
	v_mfma_f32_16x16x32_bf16 v[132:135], v[160:163], v[156:159], v[132:135]
.LBB0_304:
	ds_read_b128 v[156:159], v177 offset:2560
	ds_read_b128 v[160:163], v177 offset:2576
	ds_read_b128 v[164:167], v177 offset:2592
	ds_read_b128 v[180:183], v177 offset:2608
	ds_read_b128 v[184:187], v177 offset:6656
	ds_read_b128 v[188:191], v177 offset:6672
	v_lshlrev_b32_e32 v98, 16, v80
	s_nop 0
	v_and_b32_e32 v99, 0xffff0000, v80
	v_pk_mul_f32 v[98:99], v[136:137], v[98:99]
	v_lshlrev_b32_e32 v140, 16, v81
	s_nop 0
	v_and_b32_e32 v141, 0xffff0000, v81
	s_waitcnt lgkmcnt(1)
	s_nop 0
	v_pk_fma_f32 v[98:99], v[98:99], v[156:157], v[184:185]
	v_pk_mul_f32 v[140:141], v[136:137], v[140:141]
	v_lshlrev_b32_e32 v156, 16, v82
	s_nop 0
	v_and_b32_e32 v157, 0xffff0000, v82
	v_pk_fma_f32 v[140:141], v[140:141], v[158:159], v[186:187]
	v_pk_mul_f32 v[156:157], v[136:137], v[156:157]
	v_lshlrev_b32_e32 v158, 16, v83
	s_nop 0
	v_and_b32_e32 v159, 0xffff0000, v83
	s_waitcnt lgkmcnt(0)
	s_nop 0
	v_pk_fma_f32 v[156:157], v[156:157], v[160:161], v[188:189]
	v_pk_mul_f32 v[158:159], v[136:137], v[158:159]
	v_med3_f32 v96, v98, s82, v229
	v_med3_f32 v160, v99, s82, v229
	v_mov_b32_e64 v184, v97
	v_pk_fma_f32 v[158:159], v[158:159], v[162:163], v[190:191]
	v_cvt_pk_fp8_f32 v184, v96, v160
	v_med3_f32 v161, v156, s82, v229
	v_med3_f32 v162, v157, s82, v229
	v_mov_b32_e64 v185, v97
	v_cvt_pk_fp8_f32 v185, v161, v162
	v_med3_f32 v96, v140, s82, v229
	v_med3_f32 v160, v141, s82, v229
	v_cvt_pk_fp8_f32 v184, v96, v160 op_sel:[0,0,1]
	v_med3_f32 v96, v158, s82, v229
	v_med3_f32 v160, v159, s82, v229
	v_cvt_pk_fp8_f32 v185, v96, v160 op_sel:[0,0,1]
	ds_read_b128 v[160:163], v177 offset:6688
	ds_read_b128 v[186:189], v177 offset:6704
	v_lshlrev_b32_e32 v190, 16, v84
	s_nop 0
	v_and_b32_e32 v191, 0xffff0000, v84
	v_pk_mul_f32 v[190:191], v[136:137], v[190:191]
	s_and_b64 vcc, exec, s[2:3]
	s_waitcnt lgkmcnt(1)
	v_pk_fma_f32 v[160:161], v[190:191], v[164:165], v[160:161]
	v_lshlrev_b32_e32 v164, 16, v85
	s_nop 0
	v_and_b32_e32 v165, 0xffff0000, v85
	v_pk_mul_f32 v[164:165], v[136:137], v[164:165]
	v_med3_f32 v96, v160, s82, v229
	v_pk_fma_f32 v[162:163], v[164:165], v[166:167], v[162:163]
	v_lshlrev_b32_e32 v164, 16, v86
	s_nop 0
	v_and_b32_e32 v165, 0xffff0000, v86
	v_pk_mul_f32 v[164:165], v[136:137], v[164:165]
	v_med3_f32 v179, v161, s82, v229
	s_waitcnt lgkmcnt(0)
	s_nop 0
	v_pk_fma_f32 v[164:165], v[164:165], v[180:181], v[186:187]
	v_mov_b32_e64 v186, v97
	v_cvt_pk_fp8_f32 v186, v96, v179
	v_med3_f32 v180, v164, s82, v229
	v_med3_f32 v181, v165, s82, v229
	v_mov_b32_e32 v187, v97
	v_lshlrev_b32_e32 v166, 16, v87
	v_and_b32_e32 v167, 0xffff0000, v87
	v_cvt_pk_fp8_f32 v187, v180, v181
	v_pk_mul_f32 v[166:167], v[136:137], v[166:167]
	v_med3_f32 v96, v162, s82, v229
	v_pk_fma_f32 v[166:167], v[166:167], v[182:183], v[188:189]
	v_med3_f32 v179, v163, s82, v229
	v_cvt_pk_fp8_f32 v186, v96, v179 op_sel:[0,0,1]
	v_med3_f32 v96, v166, s82, v229
	v_med3_f32 v179, v167, s82, v229
	v_cvt_pk_fp8_f32 v187, v96, v179 op_sel:[0,0,1]
	global_store_dwordx4 v[138:139], v[184:187], off offset:640
	s_cbranch_vccnz .LBB0_306
	s_nop 0
	v_cvt_pk_bf16_f32 v180, v98, v99
	v_cvt_pk_bf16_f32 v181, v140, v141
	v_cvt_pk_bf16_f32 v182, v156, v157
	v_cvt_pk_bf16_f32 v183, v158, v159
	ds_read_b128 v[156:159], v178 offset:9472
	v_cvt_pk_bf16_f32 v160, v160, v161
	v_cvt_pk_bf16_f32 v161, v162, v163
	v_cvt_pk_bf16_f32 v162, v164, v165
	v_cvt_pk_bf16_f32 v163, v166, v167
	s_waitcnt lgkmcnt(0)
	s_nop 0
	v_mfma_f32_16x16x32_bf16 v[132:135], v[180:183], v[156:159], v[132:135]
	ds_read_b128 v[156:159], v178 offset:9488
	s_waitcnt lgkmcnt(0)
	s_nop 0
	v_mfma_f32_16x16x32_bf16 v[132:135], v[160:163], v[156:159], v[132:135]
.LBB0_306:
	ds_read_b128 v[156:159], v177 offset:2816
	ds_read_b128 v[160:163], v177 offset:2832
	ds_read_b128 v[164:167], v177 offset:2848
	ds_read_b128 v[180:183], v177 offset:2864
	ds_read_b128 v[184:187], v177 offset:6912
	ds_read_b128 v[188:191], v177 offset:6928
	v_lshlrev_b32_e32 v98, 16, v88
	s_nop 0
	v_and_b32_e32 v99, 0xffff0000, v88
	v_pk_mul_f32 v[98:99], v[136:137], v[98:99]
	v_lshlrev_b32_e32 v140, 16, v89
	s_nop 0
	v_and_b32_e32 v141, 0xffff0000, v89
	s_waitcnt lgkmcnt(1)
	s_nop 0
	v_pk_fma_f32 v[98:99], v[98:99], v[156:157], v[184:185]
	v_pk_mul_f32 v[140:141], v[136:137], v[140:141]
	v_lshlrev_b32_e32 v156, 16, v90
	s_nop 0
	v_and_b32_e32 v157, 0xffff0000, v90
	v_pk_fma_f32 v[140:141], v[140:141], v[158:159], v[186:187]
	v_pk_mul_f32 v[156:157], v[136:137], v[156:157]
	v_lshlrev_b32_e32 v158, 16, v91
	s_nop 0
	v_and_b32_e32 v159, 0xffff0000, v91
	s_waitcnt lgkmcnt(0)
	s_nop 0
	v_pk_fma_f32 v[156:157], v[156:157], v[160:161], v[188:189]
	v_pk_mul_f32 v[158:159], v[136:137], v[158:159]
	v_med3_f32 v96, v98, s82, v229
	v_med3_f32 v160, v99, s82, v229
	v_mov_b32_e64 v184, v97
	v_pk_fma_f32 v[158:159], v[158:159], v[162:163], v[190:191]
	v_cvt_pk_fp8_f32 v184, v96, v160
	v_med3_f32 v161, v156, s82, v229
	v_med3_f32 v162, v157, s82, v229
	v_mov_b32_e64 v185, v97
	v_cvt_pk_fp8_f32 v185, v161, v162
	v_med3_f32 v96, v140, s82, v229
	v_med3_f32 v160, v141, s82, v229
	v_cvt_pk_fp8_f32 v184, v96, v160 op_sel:[0,0,1]
	v_med3_f32 v96, v158, s82, v229
	v_med3_f32 v160, v159, s82, v229
	v_cvt_pk_fp8_f32 v185, v96, v160 op_sel:[0,0,1]
	ds_read_b128 v[160:163], v177 offset:6944
	ds_read_b128 v[186:189], v177 offset:6960
	v_lshlrev_b32_e32 v190, 16, v92
	s_nop 0
	v_and_b32_e32 v191, 0xffff0000, v92
	v_pk_mul_f32 v[190:191], v[136:137], v[190:191]
	s_and_b64 vcc, exec, s[2:3]
	s_waitcnt lgkmcnt(1)
	v_pk_fma_f32 v[160:161], v[190:191], v[164:165], v[160:161]
	v_lshlrev_b32_e32 v164, 16, v93
	s_nop 0
	v_and_b32_e32 v165, 0xffff0000, v93
	v_pk_mul_f32 v[164:165], v[136:137], v[164:165]
	v_med3_f32 v96, v160, s82, v229
	v_pk_fma_f32 v[162:163], v[164:165], v[166:167], v[162:163]
	v_lshlrev_b32_e32 v164, 16, v94
	s_nop 0
	v_and_b32_e32 v165, 0xffff0000, v94
	v_pk_mul_f32 v[164:165], v[136:137], v[164:165]
	v_med3_f32 v179, v161, s82, v229
	s_waitcnt lgkmcnt(0)
	s_nop 0
	v_pk_fma_f32 v[164:165], v[164:165], v[180:181], v[186:187]
	v_mov_b32_e64 v186, v97
	v_cvt_pk_fp8_f32 v186, v96, v179
	v_med3_f32 v180, v164, s82, v229
	v_med3_f32 v181, v165, s82, v229
	v_mov_b32_e32 v187, v97
	v_lshlrev_b32_e32 v166, 16, v95
	v_and_b32_e32 v167, 0xffff0000, v95
	v_cvt_pk_fp8_f32 v187, v180, v181
	v_pk_mul_f32 v[166:167], v[136:137], v[166:167]
	v_med3_f32 v96, v162, s82, v229
	v_pk_fma_f32 v[166:167], v[166:167], v[182:183], v[188:189]
	v_med3_f32 v179, v163, s82, v229
	v_cvt_pk_fp8_f32 v186, v96, v179 op_sel:[0,0,1]
	v_med3_f32 v96, v166, s82, v229
	v_med3_f32 v179, v167, s82, v229
	v_cvt_pk_fp8_f32 v187, v96, v179 op_sel:[0,0,1]
	global_store_dwordx4 v[138:139], v[184:187], off offset:704
	s_cbranch_vccnz .LBB0_308
	s_nop 0
	v_cvt_pk_bf16_f32 v180, v98, v99
	v_cvt_pk_bf16_f32 v181, v140, v141
	v_cvt_pk_bf16_f32 v182, v156, v157
	v_cvt_pk_bf16_f32 v183, v158, v159
	ds_read_b128 v[156:159], v178 offset:9600
	v_cvt_pk_bf16_f32 v160, v160, v161
	v_cvt_pk_bf16_f32 v161, v162, v163
	v_cvt_pk_bf16_f32 v162, v164, v165
	v_cvt_pk_bf16_f32 v163, v166, v167
	s_waitcnt lgkmcnt(0)
	s_nop 0
	v_mfma_f32_16x16x32_bf16 v[132:135], v[180:183], v[156:159], v[132:135]
	ds_read_b128 v[156:159], v178 offset:9616
	s_waitcnt lgkmcnt(0)
	s_nop 0
	v_mfma_f32_16x16x32_bf16 v[132:135], v[160:163], v[156:159], v[132:135]
.LBB0_308:
	ds_read_b128 v[156:159], v177 offset:3072
	ds_read_b128 v[160:163], v177 offset:3088
	ds_read_b128 v[164:167], v177 offset:3104
	ds_read_b128 v[180:183], v177 offset:3120
	ds_read_b128 v[184:187], v177 offset:7168
	ds_read_b128 v[188:191], v177 offset:7184
	v_lshlrev_b32_e32 v98, 16, v100
	s_nop 0
	v_and_b32_e32 v99, 0xffff0000, v100
	v_pk_mul_f32 v[98:99], v[136:137], v[98:99]
	v_lshlrev_b32_e32 v140, 16, v101
	s_nop 0
	v_and_b32_e32 v141, 0xffff0000, v101
	s_waitcnt lgkmcnt(1)
	s_nop 0
	v_pk_fma_f32 v[98:99], v[98:99], v[156:157], v[184:185]
	v_pk_mul_f32 v[140:141], v[136:137], v[140:141]
	v_lshlrev_b32_e32 v156, 16, v102
	s_nop 0
	v_and_b32_e32 v157, 0xffff0000, v102
	v_pk_fma_f32 v[140:141], v[140:141], v[158:159], v[186:187]
	v_pk_mul_f32 v[156:157], v[136:137], v[156:157]
	v_lshlrev_b32_e32 v158, 16, v103
	s_nop 0
	v_and_b32_e32 v159, 0xffff0000, v103
	s_waitcnt lgkmcnt(0)
	s_nop 0
	v_pk_fma_f32 v[156:157], v[156:157], v[160:161], v[188:189]
	v_pk_mul_f32 v[158:159], v[136:137], v[158:159]
	v_med3_f32 v96, v98, s82, v229
	v_med3_f32 v160, v99, s82, v229
	v_mov_b32_e64 v184, v97
	v_pk_fma_f32 v[158:159], v[158:159], v[162:163], v[190:191]
	v_cvt_pk_fp8_f32 v184, v96, v160
	v_med3_f32 v161, v156, s82, v229
	v_med3_f32 v162, v157, s82, v229
	v_mov_b32_e64 v185, v97
	v_cvt_pk_fp8_f32 v185, v161, v162
	v_med3_f32 v96, v140, s82, v229
	v_med3_f32 v160, v141, s82, v229
	v_cvt_pk_fp8_f32 v184, v96, v160 op_sel:[0,0,1]
	v_med3_f32 v96, v158, s82, v229
	v_med3_f32 v160, v159, s82, v229
	v_cvt_pk_fp8_f32 v185, v96, v160 op_sel:[0,0,1]
	ds_read_b128 v[160:163], v177 offset:7200
	ds_read_b128 v[186:189], v177 offset:7216
	v_lshlrev_b32_e32 v190, 16, v104
	s_nop 0
	v_and_b32_e32 v191, 0xffff0000, v104
	v_pk_mul_f32 v[190:191], v[136:137], v[190:191]
	s_and_b64 vcc, exec, s[2:3]
	s_waitcnt lgkmcnt(1)
	v_pk_fma_f32 v[160:161], v[190:191], v[164:165], v[160:161]
	v_lshlrev_b32_e32 v164, 16, v105
	s_nop 0
	v_and_b32_e32 v165, 0xffff0000, v105
	v_pk_mul_f32 v[164:165], v[136:137], v[164:165]
	v_med3_f32 v96, v160, s82, v229
	v_pk_fma_f32 v[162:163], v[164:165], v[166:167], v[162:163]
	v_lshlrev_b32_e32 v164, 16, v106
	s_nop 0
	v_and_b32_e32 v165, 0xffff0000, v106
	v_pk_mul_f32 v[164:165], v[136:137], v[164:165]
	v_med3_f32 v179, v161, s82, v229
	s_waitcnt lgkmcnt(0)
	s_nop 0
	v_pk_fma_f32 v[164:165], v[164:165], v[180:181], v[186:187]
	v_mov_b32_e64 v186, v97
	v_cvt_pk_fp8_f32 v186, v96, v179
	v_med3_f32 v180, v164, s82, v229
	v_med3_f32 v181, v165, s82, v229
	v_mov_b32_e32 v187, v97
	v_lshlrev_b32_e32 v166, 16, v107
	v_and_b32_e32 v167, 0xffff0000, v107
	v_cvt_pk_fp8_f32 v187, v180, v181
	v_pk_mul_f32 v[166:167], v[136:137], v[166:167]
	v_med3_f32 v96, v162, s82, v229
	v_pk_fma_f32 v[166:167], v[166:167], v[182:183], v[188:189]
	v_med3_f32 v179, v163, s82, v229
	v_cvt_pk_fp8_f32 v186, v96, v179 op_sel:[0,0,1]
	v_med3_f32 v96, v166, s82, v229
	v_med3_f32 v179, v167, s82, v229
	v_cvt_pk_fp8_f32 v187, v96, v179 op_sel:[0,0,1]
	global_store_dwordx4 v[138:139], v[184:187], off offset:768
	s_cbranch_vccnz .LBB0_310
	s_nop 0
	v_cvt_pk_bf16_f32 v180, v98, v99
	v_cvt_pk_bf16_f32 v181, v140, v141
	v_cvt_pk_bf16_f32 v182, v156, v157
	v_cvt_pk_bf16_f32 v183, v158, v159
	ds_read_b128 v[156:159], v178 offset:9728
	v_cvt_pk_bf16_f32 v160, v160, v161
	v_cvt_pk_bf16_f32 v161, v162, v163
	v_cvt_pk_bf16_f32 v162, v164, v165
	v_cvt_pk_bf16_f32 v163, v166, v167
	s_waitcnt lgkmcnt(0)
	s_nop 0
	v_mfma_f32_16x16x32_bf16 v[132:135], v[180:183], v[156:159], v[132:135]
	ds_read_b128 v[156:159], v178 offset:9744
	s_waitcnt lgkmcnt(0)
	s_nop 0
	v_mfma_f32_16x16x32_bf16 v[132:135], v[160:163], v[156:159], v[132:135]
.LBB0_310:
	ds_read_b128 v[156:159], v177 offset:3328
	ds_read_b128 v[160:163], v177 offset:3344
	ds_read_b128 v[164:167], v177 offset:3360
	ds_read_b128 v[180:183], v177 offset:3376
	ds_read_b128 v[184:187], v177 offset:7424
	ds_read_b128 v[188:191], v177 offset:7440
	v_lshlrev_b32_e32 v98, 16, v108
	s_nop 0
	v_and_b32_e32 v99, 0xffff0000, v108
	v_pk_mul_f32 v[98:99], v[136:137], v[98:99]
	v_lshlrev_b32_e32 v140, 16, v109
	s_nop 0
	v_and_b32_e32 v141, 0xffff0000, v109
	s_waitcnt lgkmcnt(1)
	s_nop 0
	v_pk_fma_f32 v[98:99], v[98:99], v[156:157], v[184:185]
	v_pk_mul_f32 v[140:141], v[136:137], v[140:141]
	v_lshlrev_b32_e32 v156, 16, v110
	s_nop 0
	v_and_b32_e32 v157, 0xffff0000, v110
	v_pk_fma_f32 v[140:141], v[140:141], v[158:159], v[186:187]
	v_pk_mul_f32 v[156:157], v[136:137], v[156:157]
	v_lshlrev_b32_e32 v158, 16, v111
	s_nop 0
	v_and_b32_e32 v159, 0xffff0000, v111
	s_waitcnt lgkmcnt(0)
	s_nop 0
	v_pk_fma_f32 v[156:157], v[156:157], v[160:161], v[188:189]
	v_pk_mul_f32 v[158:159], v[136:137], v[158:159]
	v_med3_f32 v96, v98, s82, v229
	v_med3_f32 v160, v99, s82, v229
	v_mov_b32_e64 v184, v97
	v_pk_fma_f32 v[158:159], v[158:159], v[162:163], v[190:191]
	v_cvt_pk_fp8_f32 v184, v96, v160
	v_med3_f32 v161, v156, s82, v229
	v_med3_f32 v162, v157, s82, v229
	v_mov_b32_e64 v185, v97
	v_cvt_pk_fp8_f32 v185, v161, v162
	v_med3_f32 v96, v140, s82, v229
	v_med3_f32 v160, v141, s82, v229
	v_cvt_pk_fp8_f32 v184, v96, v160 op_sel:[0,0,1]
	v_med3_f32 v96, v158, s82, v229
	v_med3_f32 v160, v159, s82, v229
	v_cvt_pk_fp8_f32 v185, v96, v160 op_sel:[0,0,1]
	ds_read_b128 v[160:163], v177 offset:7456
	ds_read_b128 v[186:189], v177 offset:7472
	v_lshlrev_b32_e32 v190, 16, v112
	s_nop 0
	v_and_b32_e32 v191, 0xffff0000, v112
	v_pk_mul_f32 v[190:191], v[136:137], v[190:191]
	s_and_b64 vcc, exec, s[2:3]
	s_waitcnt lgkmcnt(1)
	v_pk_fma_f32 v[160:161], v[190:191], v[164:165], v[160:161]
	v_lshlrev_b32_e32 v164, 16, v113
	s_nop 0
	v_and_b32_e32 v165, 0xffff0000, v113
	v_pk_mul_f32 v[164:165], v[136:137], v[164:165]
	v_med3_f32 v96, v160, s82, v229
	v_pk_fma_f32 v[162:163], v[164:165], v[166:167], v[162:163]
	v_lshlrev_b32_e32 v164, 16, v114
	s_nop 0
	v_and_b32_e32 v165, 0xffff0000, v114
	v_pk_mul_f32 v[164:165], v[136:137], v[164:165]
	v_med3_f32 v179, v161, s82, v229
	s_waitcnt lgkmcnt(0)
	s_nop 0
	v_pk_fma_f32 v[164:165], v[164:165], v[180:181], v[186:187]
	v_mov_b32_e64 v186, v97
	v_cvt_pk_fp8_f32 v186, v96, v179
	v_med3_f32 v180, v164, s82, v229
	v_med3_f32 v181, v165, s82, v229
	v_mov_b32_e32 v187, v97
	v_lshlrev_b32_e32 v166, 16, v115
	v_and_b32_e32 v167, 0xffff0000, v115
	v_cvt_pk_fp8_f32 v187, v180, v181
	v_pk_mul_f32 v[166:167], v[136:137], v[166:167]
	v_med3_f32 v96, v162, s82, v229
	v_pk_fma_f32 v[166:167], v[166:167], v[182:183], v[188:189]
	v_med3_f32 v179, v163, s82, v229
	v_cvt_pk_fp8_f32 v186, v96, v179 op_sel:[0,0,1]
	v_med3_f32 v96, v166, s82, v229
	v_med3_f32 v179, v167, s82, v229
	v_cvt_pk_fp8_f32 v187, v96, v179 op_sel:[0,0,1]
	global_store_dwordx4 v[138:139], v[184:187], off offset:832
	s_cbranch_vccnz .LBB0_312
	s_nop 0
	v_cvt_pk_bf16_f32 v180, v98, v99
	v_cvt_pk_bf16_f32 v181, v140, v141
	v_cvt_pk_bf16_f32 v182, v156, v157
	v_cvt_pk_bf16_f32 v183, v158, v159
	ds_read_b128 v[156:159], v178 offset:9856
	v_cvt_pk_bf16_f32 v160, v160, v161
	v_cvt_pk_bf16_f32 v161, v162, v163
	v_cvt_pk_bf16_f32 v162, v164, v165
	v_cvt_pk_bf16_f32 v163, v166, v167
	s_waitcnt lgkmcnt(0)
	s_nop 0
	v_mfma_f32_16x16x32_bf16 v[132:135], v[180:183], v[156:159], v[132:135]
	ds_read_b128 v[156:159], v178 offset:9872
	s_waitcnt lgkmcnt(0)
	s_nop 0
	v_mfma_f32_16x16x32_bf16 v[132:135], v[160:163], v[156:159], v[132:135]
.LBB0_312:
	ds_read_b128 v[156:159], v177 offset:3584
	ds_read_b128 v[160:163], v177 offset:3600
	ds_read_b128 v[164:167], v177 offset:3616
	ds_read_b128 v[180:183], v177 offset:3632
	ds_read_b128 v[184:187], v177 offset:7680
	ds_read_b128 v[188:191], v177 offset:7696
	v_lshlrev_b32_e32 v98, 16, v116
	s_nop 0
	v_and_b32_e32 v99, 0xffff0000, v116
	v_pk_mul_f32 v[98:99], v[136:137], v[98:99]
	v_lshlrev_b32_e32 v140, 16, v117
	s_nop 0
	v_and_b32_e32 v141, 0xffff0000, v117
	s_waitcnt lgkmcnt(1)
	s_nop 0
	v_pk_fma_f32 v[98:99], v[98:99], v[156:157], v[184:185]
	v_pk_mul_f32 v[140:141], v[136:137], v[140:141]
	v_lshlrev_b32_e32 v156, 16, v118
	s_nop 0
	v_and_b32_e32 v157, 0xffff0000, v118
	v_pk_fma_f32 v[140:141], v[140:141], v[158:159], v[186:187]
	v_pk_mul_f32 v[156:157], v[136:137], v[156:157]
	v_lshlrev_b32_e32 v158, 16, v119
	s_nop 0
	v_and_b32_e32 v159, 0xffff0000, v119
	s_waitcnt lgkmcnt(0)
	s_nop 0
	v_pk_fma_f32 v[156:157], v[156:157], v[160:161], v[188:189]
	v_pk_mul_f32 v[158:159], v[136:137], v[158:159]
	v_med3_f32 v96, v98, s82, v229
	v_med3_f32 v160, v99, s82, v229
	v_mov_b32_e64 v184, v97
	v_pk_fma_f32 v[158:159], v[158:159], v[162:163], v[190:191]
	v_cvt_pk_fp8_f32 v184, v96, v160
	v_med3_f32 v161, v156, s82, v229
	v_med3_f32 v162, v157, s82, v229
	v_mov_b32_e64 v185, v97
	v_cvt_pk_fp8_f32 v185, v161, v162
	v_med3_f32 v96, v140, s82, v229
	v_med3_f32 v160, v141, s82, v229
	v_cvt_pk_fp8_f32 v184, v96, v160 op_sel:[0,0,1]
	v_med3_f32 v96, v158, s82, v229
	v_med3_f32 v160, v159, s82, v229
	v_cvt_pk_fp8_f32 v185, v96, v160 op_sel:[0,0,1]
	ds_read_b128 v[160:163], v177 offset:7712
	ds_read_b128 v[186:189], v177 offset:7728
	v_lshlrev_b32_e32 v190, 16, v120
	s_nop 0
	v_and_b32_e32 v191, 0xffff0000, v120
	v_pk_mul_f32 v[190:191], v[136:137], v[190:191]
	s_and_b64 vcc, exec, s[2:3]
	s_waitcnt lgkmcnt(1)
	v_pk_fma_f32 v[160:161], v[190:191], v[164:165], v[160:161]
	v_lshlrev_b32_e32 v164, 16, v121
	s_nop 0
	v_and_b32_e32 v165, 0xffff0000, v121
	v_pk_mul_f32 v[164:165], v[136:137], v[164:165]
	v_med3_f32 v96, v160, s82, v229
	v_pk_fma_f32 v[162:163], v[164:165], v[166:167], v[162:163]
	v_lshlrev_b32_e32 v164, 16, v122
	s_nop 0
	v_and_b32_e32 v165, 0xffff0000, v122
	v_pk_mul_f32 v[164:165], v[136:137], v[164:165]
	v_med3_f32 v179, v161, s82, v229
	s_waitcnt lgkmcnt(0)
	s_nop 0
	v_pk_fma_f32 v[164:165], v[164:165], v[180:181], v[186:187]
	v_mov_b32_e64 v186, v97
	v_cvt_pk_fp8_f32 v186, v96, v179
	v_med3_f32 v180, v164, s82, v229
	v_med3_f32 v181, v165, s82, v229
	v_mov_b32_e32 v187, v97
	v_lshlrev_b32_e32 v166, 16, v123
	v_and_b32_e32 v167, 0xffff0000, v123
	v_cvt_pk_fp8_f32 v187, v180, v181
	v_pk_mul_f32 v[166:167], v[136:137], v[166:167]
	v_med3_f32 v96, v162, s82, v229
	v_pk_fma_f32 v[166:167], v[166:167], v[182:183], v[188:189]
	v_med3_f32 v179, v163, s82, v229
	v_cvt_pk_fp8_f32 v186, v96, v179 op_sel:[0,0,1]
	v_med3_f32 v96, v166, s82, v229
	v_med3_f32 v179, v167, s82, v229
	v_cvt_pk_fp8_f32 v187, v96, v179 op_sel:[0,0,1]
	global_store_dwordx4 v[138:139], v[184:187], off offset:896
	s_cbranch_vccnz .LBB0_314
	s_nop 0
	v_cvt_pk_bf16_f32 v180, v98, v99
	v_cvt_pk_bf16_f32 v181, v140, v141
	v_cvt_pk_bf16_f32 v182, v156, v157
	v_cvt_pk_bf16_f32 v183, v158, v159
	ds_read_b128 v[156:159], v178 offset:9984
	v_cvt_pk_bf16_f32 v160, v160, v161
	v_cvt_pk_bf16_f32 v161, v162, v163
	v_cvt_pk_bf16_f32 v162, v164, v165
	v_cvt_pk_bf16_f32 v163, v166, v167
	s_waitcnt lgkmcnt(0)
	s_nop 0
	v_mfma_f32_16x16x32_bf16 v[132:135], v[180:183], v[156:159], v[132:135]
	ds_read_b128 v[156:159], v178 offset:10000
	s_waitcnt lgkmcnt(0)
	s_nop 0
	v_mfma_f32_16x16x32_bf16 v[132:135], v[160:163], v[156:159], v[132:135]
.LBB0_314:
	ds_read_b128 v[156:159], v177 offset:3840
	ds_read_b128 v[160:163], v177 offset:3856
	ds_read_b128 v[164:167], v177 offset:3872
	ds_read_b128 v[180:183], v177 offset:3888
	ds_read_b128 v[184:187], v177 offset:7936
	ds_read_b128 v[188:191], v177 offset:7952
	v_lshlrev_b32_e32 v98, 16, v124
	s_nop 0
	v_and_b32_e32 v99, 0xffff0000, v124
	v_pk_mul_f32 v[98:99], v[136:137], v[98:99]
	v_lshlrev_b32_e32 v140, 16, v125
	s_nop 0
	v_and_b32_e32 v141, 0xffff0000, v125
	s_waitcnt lgkmcnt(1)
	s_nop 0
	v_pk_fma_f32 v[98:99], v[98:99], v[156:157], v[184:185]
	v_pk_mul_f32 v[140:141], v[136:137], v[140:141]
	v_lshlrev_b32_e32 v156, 16, v126
	s_nop 0
	v_and_b32_e32 v157, 0xffff0000, v126
	v_pk_fma_f32 v[140:141], v[140:141], v[158:159], v[186:187]
	v_pk_mul_f32 v[156:157], v[136:137], v[156:157]
	v_lshlrev_b32_e32 v158, 16, v127
	s_nop 0
	v_and_b32_e32 v159, 0xffff0000, v127
	s_waitcnt lgkmcnt(0)
	s_nop 0
	v_pk_fma_f32 v[156:157], v[156:157], v[160:161], v[188:189]
	v_pk_mul_f32 v[158:159], v[136:137], v[158:159]
	v_med3_f32 v96, v98, s82, v229
	v_med3_f32 v160, v99, s82, v229
	v_mov_b32_e64 v184, v97
	v_pk_fma_f32 v[158:159], v[158:159], v[162:163], v[190:191]
	v_cvt_pk_fp8_f32 v184, v96, v160
	v_med3_f32 v161, v156, s82, v229
	v_med3_f32 v162, v157, s82, v229
	v_mov_b32_e64 v185, v97
	v_cvt_pk_fp8_f32 v185, v161, v162
	v_med3_f32 v96, v140, s82, v229
	v_med3_f32 v160, v141, s82, v229
	v_cvt_pk_fp8_f32 v184, v96, v160 op_sel:[0,0,1]
	v_med3_f32 v96, v158, s82, v229
	v_med3_f32 v160, v159, s82, v229
	v_cvt_pk_fp8_f32 v185, v96, v160 op_sel:[0,0,1]
	ds_read_b128 v[160:163], v177 offset:7968
	ds_read_b128 v[186:189], v177 offset:7984
	v_lshlrev_b32_e32 v190, 16, v128
	s_nop 0
	v_and_b32_e32 v191, 0xffff0000, v128
	v_pk_mul_f32 v[190:191], v[136:137], v[190:191]
	s_and_b64 vcc, exec, s[2:3]
	s_waitcnt lgkmcnt(1)
	v_pk_fma_f32 v[160:161], v[190:191], v[164:165], v[160:161]
	v_lshlrev_b32_e32 v164, 16, v129
	s_nop 0
	v_and_b32_e32 v165, 0xffff0000, v129
	v_pk_mul_f32 v[164:165], v[136:137], v[164:165]
	v_med3_f32 v96, v160, s82, v229
	v_pk_fma_f32 v[162:163], v[164:165], v[166:167], v[162:163]
	v_lshlrev_b32_e32 v164, 16, v130
	s_nop 0
	v_and_b32_e32 v165, 0xffff0000, v130
	v_pk_mul_f32 v[164:165], v[136:137], v[164:165]
	v_lshlrev_b32_e32 v166, 16, v131
	s_nop 0
	v_and_b32_e32 v167, 0xffff0000, v131
	s_waitcnt lgkmcnt(0)
	s_nop 0
	v_pk_fma_f32 v[164:165], v[164:165], v[180:181], v[186:187]
	v_pk_mul_f32 v[136:137], v[136:137], v[166:167]
	v_med3_f32 v166, v161, s82, v229
	v_mov_b32_e64 v186, v97
	v_cvt_pk_fp8_f32 v186, v96, v166
	v_med3_f32 v167, v164, s82, v229
	v_med3_f32 v179, v165, s82, v229
	v_mov_b32_e64 v187, v97
	v_cvt_pk_fp8_f32 v187, v167, v179
	v_pk_fma_f32 v[136:137], v[136:137], v[182:183], v[188:189]
	v_med3_f32 v96, v162, s82, v229
	v_med3_f32 v166, v163, s82, v229
	v_cvt_pk_fp8_f32 v186, v96, v166 op_sel:[0,0,1]
	v_med3_f32 v96, v136, s82, v229
	v_med3_f32 v166, v137, s82, v229
	v_cvt_pk_fp8_f32 v187, v96, v166 op_sel:[0,0,1]
	global_store_dwordx4 v[138:139], v[184:187], off offset:960
	s_cbranch_vccnz .LBB0_277
	s_nop 0
	global_load_dword v96, v[150:151], off
	v_cvt_pk_bf16_f32 v138, v98, v99
	v_cvt_pk_bf16_f32 v139, v140, v141
	v_cvt_pk_bf16_f32 v140, v156, v157
	v_cvt_pk_bf16_f32 v141, v158, v159
	ds_read_b128 v[156:159], v178 offset:10112
	v_cvt_pk_bf16_f32 v160, v160, v161
	v_cvt_pk_bf16_f32 v161, v162, v163
	v_cvt_pk_bf16_f32 v162, v164, v165
	v_cvt_pk_bf16_f32 v163, v136, v137
	s_waitcnt lgkmcnt(0)
	s_nop 0
	v_mfma_f32_16x16x32_bf16 v[132:135], v[138:141], v[156:159], v[132:135]
	ds_read_b128 v[136:139], v178 offset:10128
	s_and_b64 vcc, exec, s[0:1]
	s_mov_b64 s[6:7], -1
	s_waitcnt lgkmcnt(0)
	s_nop 0
	v_mfma_f32_16x16x32_bf16 v[132:135], v[160:163], v[136:139], v[132:135]
	s_waitcnt vmcnt(0)
	s_nop 6
	v_add_f32_e32 v98, v96, v132
	s_cbranch_vccnz .LBB0_323
	v_mul_f32_e32 v99, 0x3d888889, v98
	v_cmp_nlt_f32_e64 s[6:7], |v99|, s45
	s_and_saveexec_b64 s[22:23], s[6:7]
	s_xor_b64 s[6:7], exec, s[22:23]
	s_cbranch_execz .LBB0_318
	s_nop 0
	v_add_f32_e64 v132, |v99|, |v99|
	v_mul_f32_e32 v136, 0x3fb8aa3b, v132
	v_rndne_f32_e32 v137, v136
	v_sub_f32_e32 v138, v136, v137
	v_fma_f32 v136, v132, s39, -v136
	v_fmac_f32_e32 v136, 0x32a5705f, v132
	v_add_f32_e32 v136, v138, v136
	v_cvt_i32_f32_e32 v137, v137
	v_exp_f32_e32 v136, v136
	v_cmp_ngt_f32_e32 vcc, s40, v132
	v_ldexp_f32 v136, v136, v137
	s_nop 0
	v_cndmask_b32_e32 v136, 0, v136, vcc
	v_cmp_nlt_f32_e32 vcc, s41, v132
	s_nop 1
	v_cndmask_b32_e32 v132, v230, v136, vcc
	v_add_f32_e32 v132, 1.0, v132
	v_rcp_f32_e32 v132, v132
	s_nop 0
	v_fma_f32 v132, v132, -2.0, 1.0
.LBB0_318:
	s_andn2_saveexec_b64 s[6:7], s[6:7]
	v_mul_f32_e32 v132, v99, v99
	v_fmamk_f32 v136, v132, 0xbbbac73d, v222
	v_fmaak_f32 v136, v132, v136, 0xbd5c1c4e
	v_fmaak_f32 v136, v132, v136, 0x3e088382
	v_fmaak_f32 v136, v132, v136, 0xbeaaaa99
	v_mul_f32_e64 v136, |v99|, v136
	v_fma_f32 v132, v132, v136, |v99|
	s_or_b64 exec, exec, s[6:7]
	s_nop 0
	v_bfi_b32 v99, s43, v132, v99
	v_mul_f32_e32 v132, 0x41700000, v99
	s_and_saveexec_b64 s[6:7], s[4:5]
	s_cbranch_execz .LBB0_322
	v_mul_f32_e64 v99, |v132|, s74
	v_exp_f32_e32 v99, v99
	v_max_f32_e32 v132, v132, v132
	v_min_f32_e32 v132, 0, v132
	v_add_f32_e32 v138, 1.0, v99
	v_add_f32_e32 v136, -1.0, v138
	v_sub_f32_e32 v137, v136, v138
	v_sub_f32_e32 v136, v99, v136
	v_add_f32_e32 v137, 1.0, v137
	v_add_f32_e32 v139, v136, v137
	v_frexp_mant_f32_e32 v140, v138
	v_cvt_f64_f32_e32 v[136:137], v138
	v_frexp_exp_i32_f64_e32 v136, v[136:137]
	v_cmp_gt_f32_e32 vcc, s83, v140
	s_nop 1
	v_subbrev_co_u32_e32 v158, vcc, 0, v136, vcc
	v_sub_u32_e32 v136, 0, v158
	v_ldexp_f32 v137, v138, v136
	v_add_f32_e32 v138, -1.0, v137
	v_add_f32_e32 v140, 1.0, v137
	v_ldexp_f32 v136, v139, v136
	v_add_f32_e32 v139, 1.0, v138
	v_add_f32_e32 v141, -1.0, v140
	v_sub_f32_e32 v139, v137, v139
	v_sub_f32_e32 v137, v137, v141
	v_add_f32_e32 v139, v136, v139
	v_add_f32_e32 v136, v136, v137
	v_add_f32_e32 v159, v140, v136
	v_rcp_f32_e32 v161, v159
	v_sub_f32_e32 v137, v159, v140
	v_sub_f32_e32 v160, v136, v137
	v_add_f32_e32 v137, v138, v139
	v_mul_f32_e32 v163, v137, v161
	v_sub_f32_e32 v136, v137, v138
	v_mul_f32_e32 v138, v159, v163
	v_fma_f32 v140, v163, v159, -v138
	v_fmac_f32_e32 v140, v163, v160
	v_sub_f32_e32 v162, v139, v136
	v_add_f32_e32 v136, v138, v140
	v_sub_f32_e32 v139, v137, v136
	v_pk_add_f32 v[156:157], v[136:137], v[138:139] neg_lo:[0,1] neg_hi:[0,1]
	v_mov_b32_e64 v141, v136
	v_pk_add_f32 v[136:137], v[156:157], v[140:141] neg_lo:[0,1] neg_hi:[0,1]
	v_cmp_neq_f32_e32 vcc, s42, v99
	v_add_f32_e32 v137, v162, v137
	v_add_f32_e32 v136, v136, v137
	v_add_f32_e32 v137, v139, v136
	v_mul_f32_e32 v162, v161, v137
	v_mul_f32_e32 v138, v159, v162
	v_fma_f32 v140, v162, v159, -v138
	v_fmac_f32_e32 v140, v162, v160
	v_sub_f32_e32 v139, v139, v137
	v_add_f32_e32 v159, v136, v139
	v_add_f32_e32 v136, v138, v140
	v_sub_f32_e64 v139, v137, v136
	v_pk_add_f32 v[156:157], v[136:137], v[138:139] neg_lo:[0,1] neg_hi:[0,1]
	v_mov_b32_e64 v141, v136
	v_pk_add_f32 v[136:137], v[156:157], v[140:141] neg_lo:[0,1] neg_hi:[0,1]
	s_nop 0
	v_add_f32_e32 v137, v159, v137
	v_add_f32_e32 v136, v136, v137
	v_add_f32_e32 v137, v163, v162
	v_add_f32_e32 v136, v139, v136
	v_sub_f32_e32 v138, v137, v163
	v_mul_f32_e32 v136, v161, v136
	v_sub_f32_e32 v138, v162, v138
	v_add_f32_e32 v138, v138, v136
	v_add_f32_e32 v140, v137, v138
	v_mul_f32_e64 v141, v140, v140
	v_fmamk_f32 v136, v141, 0x3e9b6dac, v223
	v_fmaak_f32 v199, v141, v136, 0x3f2aaada
	v_cvt_f32_i32_e32 v136, v158
	v_sub_f32_e32 v137, v140, v137
	v_sub_f32_e64 v137, v138, v137
	v_ldexp_f32 v156, v137, 1
	v_mul_f32_e64 v137, v140, v141
	v_ldexp_f32 v139, v140, 1
	v_pk_mul_f32 v[140:141], v[136:137], v[198:199]
	s_nop 0
	s_nop 0
	v_fma_f32 v138, v136, s46, -v140
	v_fmac_f32_e32 v138, 0xb102e308, v136
	v_pk_add_f32 v[136:137], v[140:141], v[138:139]
	s_nop 0
	v_sub_f32_e32 v139, v137, v139
	v_sub_f32_e32 v139, v141, v139
	v_add_f32_e32 v157, v156, v139
	v_mov_b32_e64 v156, v140
	v_pk_add_f32 v[140:141], v[136:137], v[140:141] neg_lo:[0,1] neg_hi:[0,1]
	v_pk_add_f32 v[158:159], v[136:137], v[156:157]
	v_mov_b32_e32 v139, v136
	v_mov_b32_e32 v141, v159
	v_pk_add_f32 v[160:161], v[138:139], v[140:141] neg_lo:[0,1] neg_hi:[0,1]
	v_pk_add_f32 v[138:139], v[138:139], v[140:141]
	v_mov_b32_e64 v156, v157
	v_pk_add_f32 v[140:141], v[138:139], v[136:137] op_sel:[1,0] op_sel_hi:[0,1] neg_lo:[0,1] neg_hi:[0,1]
	v_pk_add_f32 v[162:163], v[158:159], v[140:141] op_sel_hi:[1,0] neg_lo:[0,1] neg_hi:[0,1]
	v_mov_b32_e32 v158, v159
	v_mov_b32_e32 v159, v139
	v_pk_mov_b32 v[140:141], v[136:137], v[140:141] op_sel:[1,0]
	v_mov_b32_e64 v157, v136
	v_pk_add_f32 v[140:141], v[158:159], v[140:141] neg_lo:[0,1] neg_hi:[0,1]
	v_mov_b32_e64 v162, v160
	v_pk_add_f32 v[136:137], v[156:157], v[140:141] neg_lo:[0,1] neg_hi:[0,1]
	v_mov_b32_e64 v161, v139
	v_pk_add_f32 v[140:141], v[162:163], v[136:137]
	s_nop 0
	s_nop 0
	v_pk_add_f32 v[156:157], v[140:141], v[140:141] op_sel:[0,1] op_sel_hi:[1,0]
	s_nop 0
	s_nop 0
	v_pk_add_f32 v[138:139], v[138:139], v[156:157] op_sel:[1,0] op_sel_hi:[0,1]
	v_mov_b32_e64 v141, v138
	v_pk_add_f32 v[158:159], v[140:141], v[160:161] neg_lo:[0,1] neg_hi:[0,1]
	v_mov_b32_e32 v137, v156
	v_sub_f32_e32 v139, v140, v158
	v_pk_add_f32 v[136:137], v[136:137], v[158:159] neg_lo:[0,1] neg_hi:[0,1]
	v_sub_f32_e32 v139, v160, v139
	v_add_f32_e32 v136, v136, v139
	v_add_f32_e64 v136, v136, v137
	v_add_f32_e32 v136, v138, v136
	v_cndmask_b32_e32 v136, v230, v136, vcc
	v_cmp_ngt_f32_e32 vcc, -1.0, v99
	s_nop 1
	v_cndmask_b32_e32 v136, v231, v136, vcc
	v_cmp_neq_f32_e32 vcc, -1.0, v99
	s_nop 1
	v_cndmask_b32_e32 v136, v232, v136, vcc
	v_cmp_lt_f32_e64 vcc, |v99|, s44
	s_nop 1
	v_cndmask_b32_e32 v99, v136, v99, vcc
	v_sub_f32_e64 v132, v132, v99

.LBB0_323:
	s_and_b64 vcc, exec, s[6:7]
	s_cbranch_vccz .LBB0_325
	v_mul_f32_e64 v99, |v98|, s74
	v_exp_f32_e32 v132, v99
	v_max_f32_e32 v98, v98, v98
	v_min_f32_e32 v162, 0, v98
	v_add_f32_e32 v136, 1.0, v132
	v_add_f32_e32 v98, -1.0, v136
	v_sub_f32_e32 v99, v98, v136
	v_sub_f32_e32 v98, v132, v98
	v_add_f32_e32 v99, 1.0, v99
	v_add_f32_e32 v137, v98, v99
	v_frexp_mant_f32_e32 v138, v136
	v_cvt_f64_f32_e32 v[98:99], v136
	v_frexp_exp_i32_f64_e32 v98, v[98:99]
	v_cmp_gt_f32_e32 vcc, s83, v138
	s_nop 1
	v_subbrev_co_u32_e32 v156, vcc, 0, v98, vcc
	v_sub_u32_e32 v98, 0, v156
	v_ldexp_f32 v99, v136, v98
	v_add_f32_e32 v136, -1.0, v99
	v_add_f32_e32 v138, 1.0, v99
	v_ldexp_f32 v98, v137, v98
	v_add_f32_e32 v137, 1.0, v136
	v_add_f32_e32 v139, -1.0, v138
	v_sub_f32_e32 v137, v99, v137
	v_sub_f32_e32 v99, v99, v139
	v_add_f32_e32 v137, v98, v137
	v_add_f32_e32 v98, v98, v99
	v_add_f32_e32 v157, v138, v98
	v_rcp_f32_e32 v159, v157
	v_sub_f32_e32 v99, v157, v138
	v_sub_f32_e32 v158, v98, v99
	v_add_f32_e32 v99, v136, v137
	v_mul_f32_e32 v161, v99, v159
	v_sub_f32_e32 v98, v99, v136
	v_mul_f32_e32 v136, v157, v161
	v_fma_f32 v138, v161, v157, -v136
	v_fmac_f32_e32 v138, v161, v158
	v_sub_f32_e32 v160, v137, v98
	v_add_f32_e32 v98, v136, v138
	v_sub_f32_e32 v137, v99, v98
	v_pk_add_f32 v[140:141], v[98:99], v[136:137] neg_lo:[0,1] neg_hi:[0,1]
	v_mov_b32_e64 v139, v98
	v_pk_add_f32 v[98:99], v[140:141], v[138:139] neg_lo:[0,1] neg_hi:[0,1]
	v_cmp_neq_f32_e32 vcc, s42, v132
	v_add_f32_e32 v99, v160, v99
	v_add_f32_e32 v98, v98, v99
	v_add_f32_e32 v99, v137, v98
	v_mul_f32_e32 v160, v159, v99
	v_mul_f32_e32 v136, v157, v160
	v_fma_f32 v138, v160, v157, -v136
	v_fmac_f32_e32 v138, v160, v158
	v_sub_f32_e32 v137, v137, v99
	v_add_f32_e32 v157, v98, v137
	v_add_f32_e32 v98, v136, v138
	v_sub_f32_e64 v137, v99, v98
	v_pk_add_f32 v[140:141], v[98:99], v[136:137] neg_lo:[0,1] neg_hi:[0,1]
	v_mov_b32_e64 v139, v98
	v_pk_add_f32 v[98:99], v[140:141], v[138:139] neg_lo:[0,1] neg_hi:[0,1]
	s_nop 0
	v_add_f32_e32 v99, v157, v99
	v_add_f32_e32 v98, v98, v99
	v_add_f32_e32 v99, v161, v160
	v_add_f32_e32 v98, v137, v98
	v_sub_f32_e32 v136, v99, v161
	v_mul_f32_e32 v98, v159, v98
	v_sub_f32_e32 v136, v160, v136
	v_add_f32_e32 v136, v136, v98
	v_add_f32_e32 v138, v99, v136
	v_mul_f32_e64 v139, v138, v138
	v_fmamk_f32 v98, v139, 0x3e9b6dac, v223
	v_fmaak_f32 v199, v139, v98, 0x3f2aaada
	v_cvt_f32_i32_e32 v98, v156
	v_sub_f32_e32 v99, v138, v99
	v_sub_f32_e64 v99, v136, v99
	v_ldexp_f32 v140, v99, 1
	v_mul_f32_e64 v99, v138, v139
	v_ldexp_f32 v137, v138, 1
	v_pk_mul_f32 v[138:139], v[98:99], v[198:199]
	s_nop 0
	s_nop 0
	v_fma_f32 v136, v98, s46, -v138
	v_fmac_f32_e32 v136, 0xb102e308, v98
	v_pk_add_f32 v[98:99], v[138:139], v[136:137]
	s_nop 0
	v_sub_f32_e32 v137, v99, v137
	v_sub_f32_e32 v137, v139, v137
	v_add_f32_e32 v141, v140, v137
	v_mov_b32_e64 v140, v138
	v_pk_add_f32 v[138:139], v[98:99], v[138:139] neg_lo:[0,1] neg_hi:[0,1]
	v_pk_add_f32 v[156:157], v[98:99], v[140:141]
	v_mov_b32_e32 v137, v98
	v_mov_b32_e32 v139, v157
	v_pk_add_f32 v[158:159], v[136:137], v[138:139] neg_lo:[0,1] neg_hi:[0,1]
	v_pk_add_f32 v[136:137], v[136:137], v[138:139]
	v_mov_b32_e64 v140, v141
	v_pk_add_f32 v[138:139], v[136:137], v[98:99] op_sel:[1,0] op_sel_hi:[0,1] neg_lo:[0,1] neg_hi:[0,1]
	v_pk_add_f32 v[160:161], v[156:157], v[138:139] op_sel_hi:[1,0] neg_lo:[0,1] neg_hi:[0,1]
	v_mov_b32_e32 v156, v157
	v_mov_b32_e32 v157, v137
	v_pk_mov_b32 v[138:139], v[98:99], v[138:139] op_sel:[1,0]
	v_mov_b32_e64 v141, v98
	v_pk_add_f32 v[138:139], v[156:157], v[138:139] neg_lo:[0,1] neg_hi:[0,1]
	v_mov_b32_e64 v160, v158
	v_pk_add_f32 v[98:99], v[140:141], v[138:139] neg_lo:[0,1] neg_hi:[0,1]
	v_mov_b32_e64 v159, v137
	v_pk_add_f32 v[138:139], v[160:161], v[98:99]
	s_nop 0
	s_nop 0
	v_pk_add_f32 v[140:141], v[138:139], v[138:139] op_sel:[0,1] op_sel_hi:[1,0]
	s_nop 0
	s_nop 0
	v_pk_add_f32 v[136:137], v[136:137], v[140:141] op_sel:[1,0] op_sel_hi:[0,1]
	v_mov_b32_e64 v139, v136
	v_pk_add_f32 v[156:157], v[138:139], v[158:159] neg_lo:[0,1] neg_hi:[0,1]
	v_mov_b32_e32 v99, v140
	v_sub_f32_e32 v137, v138, v156
	v_pk_add_f32 v[98:99], v[98:99], v[156:157] neg_lo:[0,1] neg_hi:[0,1]
	v_sub_f32_e32 v137, v158, v137
	v_add_f32_e32 v98, v98, v137
	v_add_f32_e64 v98, v98, v99
	v_add_f32_e32 v98, v136, v98
	v_cndmask_b32_e32 v98, v230, v98, vcc
	v_cmp_ngt_f32_e32 vcc, -1.0, v132
	s_nop 1
	v_cndmask_b32_e32 v98, v231, v98, vcc
	v_cmp_neq_f32_e32 vcc, -1.0, v132
	s_nop 1
	v_cndmask_b32_e32 v98, v232, v98, vcc
	v_cmp_lt_f32_e64 vcc, |v132|, s44
	s_nop 1
	v_cndmask_b32_e32 v98, v98, v132, vcc
	v_sub_f32_e64 v132, v162, v98
.LBB0_325:
	v_or_b32_e32 v98, s30, v176
	v_ashrrev_i32_e32 v99, 31, v98
	v_lshlrev_b64 v[136:137], 6, v[98:99]
	v_lshl_add_u64 v[136:137], v[152:153], 0, v[136:137]
	v_add_f32_e64 v99, v96, v133
	s_mov_b64 s[6:7], -1
	s_and_b64 vcc, exec, s[8:9]
	global_store_dword v[136:137], v132, off
	s_cbranch_vccz .LBB0_333
	s_nop 0
	v_mul_f32_e32 v132, 0x3d888889, v99
	v_cmp_nlt_f32_e64 s[6:7], |v132|, s45
	s_and_saveexec_b64 s[22:23], s[6:7]
	s_xor_b64 s[6:7], exec, s[22:23]
	s_cbranch_execz .LBB0_328
	s_nop 0
	v_add_f32_e64 v133, |v132|, |v132|
	v_mul_f32_e32 v136, 0x3fb8aa3b, v133
	v_rndne_f32_e32 v137, v136
	v_sub_f32_e32 v138, v136, v137
	v_fma_f32 v136, v133, s39, -v136
	v_fmac_f32_e32 v136, 0x32a5705f, v133
	v_add_f32_e32 v136, v138, v136
	v_cvt_i32_f32_e32 v137, v137
	v_exp_f32_e32 v136, v136
	v_cmp_ngt_f32_e32 vcc, s40, v133
	v_ldexp_f32 v136, v136, v137
	s_nop 0
	v_cndmask_b32_e32 v136, 0, v136, vcc
	v_cmp_nlt_f32_e32 vcc, s41, v133
	s_nop 1
	v_cndmask_b32_e32 v133, v230, v136, vcc
	v_add_f32_e32 v133, 1.0, v133
	v_rcp_f32_e32 v133, v133
	s_nop 0
	v_fma_f32 v133, v133, -2.0, 1.0
.LBB0_328:
	s_andn2_saveexec_b64 s[6:7], s[6:7]
	v_mul_f32_e32 v133, v132, v132
	v_fmamk_f32 v136, v133, 0xbbbac73d, v222
	v_fmaak_f32 v136, v133, v136, 0xbd5c1c4e
	v_fmaak_f32 v136, v133, v136, 0x3e088382
	v_fmaak_f32 v136, v133, v136, 0xbeaaaa99
	v_mul_f32_e64 v136, |v132|, v136
	v_fma_f32 v133, v133, v136, |v132|
	s_or_b64 exec, exec, s[6:7]
	s_nop 0
	v_bfi_b32 v132, s43, v133, v132
	v_mul_f32_e32 v132, 0x41700000, v132
	s_and_saveexec_b64 s[6:7], s[4:5]
	s_cbranch_execz .LBB0_332
	v_mul_f32_e64 v133, |v132|, s74
	v_exp_f32_e32 v162, v133
	v_max_f32_e32 v132, v132, v132
	v_min_f32_e32 v163, 0, v132
	v_add_f32_e32 v136, 1.0, v162
	v_add_f32_e32 v132, -1.0, v136
	v_sub_f32_e32 v133, v132, v136
	v_sub_f32_e32 v132, v162, v132
	v_add_f32_e32 v133, 1.0, v133
	v_add_f32_e32 v137, v132, v133
	v_frexp_mant_f32_e32 v138, v136
	v_cvt_f64_f32_e32 v[132:133], v136
	v_frexp_exp_i32_f64_e32 v132, v[132:133]
	v_cmp_gt_f32_e32 vcc, s83, v138
	s_nop 1
	v_subbrev_co_u32_e32 v156, vcc, 0, v132, vcc
	v_sub_u32_e32 v132, 0, v156
	v_ldexp_f32 v133, v136, v132
	v_add_f32_e32 v136, -1.0, v133
	v_add_f32_e32 v138, 1.0, v133
	v_ldexp_f32 v132, v137, v132
	v_add_f32_e32 v137, 1.0, v136
	v_add_f32_e32 v139, -1.0, v138
	v_sub_f32_e32 v137, v133, v137
	v_sub_f32_e32 v133, v133, v139
	v_add_f32_e32 v137, v132, v137
	v_add_f32_e32 v132, v132, v133
	v_add_f32_e32 v157, v138, v132
	v_rcp_f32_e32 v159, v157
	v_sub_f32_e32 v133, v157, v138
	v_sub_f32_e32 v158, v132, v133
	v_add_f32_e32 v133, v136, v137
	v_mul_f32_e32 v161, v133, v159
	v_sub_f32_e32 v132, v133, v136
	v_mul_f32_e32 v136, v157, v161
	v_fma_f32 v138, v161, v157, -v136
	v_fmac_f32_e32 v138, v161, v158
	v_sub_f32_e32 v160, v137, v132
	v_add_f32_e32 v132, v136, v138
	v_sub_f32_e32 v137, v133, v132
	v_pk_add_f32 v[140:141], v[132:133], v[136:137] neg_lo:[0,1] neg_hi:[0,1]
	v_mov_b32_e64 v139, v132
	v_pk_add_f32 v[132:133], v[140:141], v[138:139] neg_lo:[0,1] neg_hi:[0,1]
	v_cmp_neq_f32_e32 vcc, s42, v162
	v_add_f32_e32 v133, v160, v133
	v_add_f32_e32 v132, v132, v133
	v_add_f32_e32 v133, v137, v132
	v_mul_f32_e32 v160, v159, v133
	v_mul_f32_e32 v136, v157, v160
	v_fma_f32 v138, v160, v157, -v136
	v_fmac_f32_e32 v138, v160, v158
	v_sub_f32_e32 v137, v137, v133
	v_add_f32_e32 v157, v132, v137
	v_add_f32_e32 v132, v136, v138
	v_sub_f32_e64 v137, v133, v132
	v_pk_add_f32 v[140:141], v[132:133], v[136:137] neg_lo:[0,1] neg_hi:[0,1]
	v_mov_b32_e64 v139, v132
	v_pk_add_f32 v[132:133], v[140:141], v[138:139] neg_lo:[0,1] neg_hi:[0,1]
	s_nop 0
	v_add_f32_e32 v133, v157, v133
	v_add_f32_e32 v132, v132, v133
	v_add_f32_e32 v133, v161, v160
	v_add_f32_e32 v132, v137, v132
	v_sub_f32_e32 v136, v133, v161
	v_mul_f32_e32 v132, v159, v132
	v_sub_f32_e32 v136, v160, v136
	v_add_f32_e32 v136, v136, v132
	v_add_f32_e32 v138, v133, v136
	v_mul_f32_e64 v139, v138, v138
	v_fmamk_f32 v132, v139, 0x3e9b6dac, v223
	v_fmaak_f32 v199, v139, v132, 0x3f2aaada
	v_cvt_f32_i32_e32 v132, v156
	v_sub_f32_e32 v133, v138, v133
	v_sub_f32_e64 v133, v136, v133
	v_ldexp_f32 v140, v133, 1
	v_mul_f32_e64 v133, v138, v139
	v_ldexp_f32 v137, v138, 1
	v_pk_mul_f32 v[138:139], v[132:133], v[198:199]
	s_nop 0
	s_nop 0
	v_fma_f32 v136, v132, s46, -v138
	v_fmac_f32_e32 v136, 0xb102e308, v132
	v_pk_add_f32 v[132:133], v[138:139], v[136:137]
	s_nop 0
	v_sub_f32_e32 v137, v133, v137
	v_sub_f32_e32 v137, v139, v137
	v_add_f32_e32 v141, v140, v137
	v_mov_b32_e64 v140, v138
	v_pk_add_f32 v[138:139], v[132:133], v[138:139] neg_lo:[0,1] neg_hi:[0,1]
	v_pk_add_f32 v[156:157], v[132:133], v[140:141]
	v_mov_b32_e32 v137, v132
	v_mov_b32_e32 v139, v157
	v_pk_add_f32 v[158:159], v[136:137], v[138:139] neg_lo:[0,1] neg_hi:[0,1]
	v_pk_add_f32 v[136:137], v[136:137], v[138:139]
	v_mov_b32_e64 v140, v141
	v_pk_add_f32 v[138:139], v[136:137], v[132:133] op_sel:[1,0] op_sel_hi:[0,1] neg_lo:[0,1] neg_hi:[0,1]
	v_pk_add_f32 v[160:161], v[156:157], v[138:139] op_sel_hi:[1,0] neg_lo:[0,1] neg_hi:[0,1]
	v_mov_b32_e32 v156, v157
	v_mov_b32_e32 v157, v137
	v_pk_mov_b32 v[138:139], v[132:133], v[138:139] op_sel:[1,0]
	v_mov_b32_e64 v141, v132
	v_pk_add_f32 v[138:139], v[156:157], v[138:139] neg_lo:[0,1] neg_hi:[0,1]
	v_mov_b32_e64 v160, v158
	v_pk_add_f32 v[132:133], v[140:141], v[138:139] neg_lo:[0,1] neg_hi:[0,1]
	v_mov_b32_e64 v159, v137
	v_pk_add_f32 v[138:139], v[160:161], v[132:133]
	s_nop 0
	s_nop 0
	v_pk_add_f32 v[140:141], v[138:139], v[138:139] op_sel:[0,1] op_sel_hi:[1,0]
	s_nop 0
	s_nop 0
	v_pk_add_f32 v[136:137], v[136:137], v[140:141] op_sel:[1,0] op_sel_hi:[0,1]
	v_mov_b32_e64 v139, v136
	v_pk_add_f32 v[156:157], v[138:139], v[158:159] neg_lo:[0,1] neg_hi:[0,1]
	v_mov_b32_e32 v133, v140
	v_sub_f32_e32 v137, v138, v156
	v_pk_add_f32 v[132:133], v[132:133], v[156:157] neg_lo:[0,1] neg_hi:[0,1]
	v_sub_f32_e32 v137, v158, v137
	v_add_f32_e32 v132, v132, v137
	v_add_f32_e64 v132, v132, v133
	v_add_f32_e32 v132, v136, v132
	v_cndmask_b32_e32 v132, v230, v132, vcc
	v_cmp_ngt_f32_e32 vcc, -1.0, v162
	s_nop 1
	v_cndmask_b32_e32 v132, v231, v132, vcc
	v_cmp_neq_f32_e32 vcc, -1.0, v162
	s_nop 1
	v_cndmask_b32_e32 v132, v232, v132, vcc
	v_cmp_lt_f32_e64 vcc, |v162|, s44
	s_nop 1
	v_cndmask_b32_e32 v132, v132, v162, vcc
	v_sub_f32_e64 v132, v163, v132

.LBB0_333:
	s_and_b64 vcc, exec, s[6:7]
	s_cbranch_vccz .LBB0_335
	v_mul_f32_e64 v132, |v99|, s74
	v_exp_f32_e32 v162, v132
	v_max_f32_e32 v99, v99, v99
	v_min_f32_e32 v99, 0, v99
	v_add_f32_e32 v136, 1.0, v162
	v_add_f32_e32 v132, -1.0, v136
	v_sub_f32_e32 v133, v132, v136
	v_sub_f32_e32 v132, v162, v132
	v_add_f32_e32 v133, 1.0, v133
	v_add_f32_e32 v137, v132, v133
	v_frexp_mant_f32_e32 v138, v136
	v_cvt_f64_f32_e32 v[132:133], v136
	v_frexp_exp_i32_f64_e32 v132, v[132:133]
	v_cmp_gt_f32_e32 vcc, s83, v138
	s_nop 1
	v_subbrev_co_u32_e32 v156, vcc, 0, v132, vcc
	v_sub_u32_e32 v132, 0, v156
	v_ldexp_f32 v133, v136, v132
	v_add_f32_e32 v136, -1.0, v133
	v_add_f32_e32 v138, 1.0, v133
	v_ldexp_f32 v132, v137, v132
	v_add_f32_e32 v137, 1.0, v136
	v_add_f32_e32 v139, -1.0, v138
	v_sub_f32_e32 v137, v133, v137
	v_sub_f32_e32 v133, v133, v139
	v_add_f32_e32 v137, v132, v137
	v_add_f32_e32 v132, v132, v133
	v_add_f32_e32 v157, v138, v132
	v_rcp_f32_e32 v159, v157
	v_sub_f32_e32 v133, v157, v138
	v_sub_f32_e32 v158, v132, v133
	v_add_f32_e32 v133, v136, v137
	v_mul_f32_e32 v161, v133, v159
	v_sub_f32_e32 v132, v133, v136
	v_mul_f32_e32 v136, v157, v161
	v_fma_f32 v138, v161, v157, -v136
	v_fmac_f32_e32 v138, v161, v158
	v_sub_f32_e32 v160, v137, v132
	v_add_f32_e32 v132, v136, v138
	v_sub_f32_e32 v137, v133, v132
	v_pk_add_f32 v[140:141], v[132:133], v[136:137] neg_lo:[0,1] neg_hi:[0,1]
	v_mov_b32_e64 v139, v132
	v_pk_add_f32 v[132:133], v[140:141], v[138:139] neg_lo:[0,1] neg_hi:[0,1]
	v_cmp_neq_f32_e32 vcc, s42, v162
	v_add_f32_e32 v133, v160, v133
	v_add_f32_e32 v132, v132, v133
	v_add_f32_e32 v133, v137, v132
	v_mul_f32_e32 v160, v159, v133
	v_mul_f32_e32 v136, v157, v160
	v_fma_f32 v138, v160, v157, -v136
	v_fmac_f32_e32 v138, v160, v158
	v_sub_f32_e32 v137, v137, v133
	v_add_f32_e32 v157, v132, v137
	v_add_f32_e32 v132, v136, v138
	v_sub_f32_e64 v137, v133, v132
	v_pk_add_f32 v[140:141], v[132:133], v[136:137] neg_lo:[0,1] neg_hi:[0,1]
	v_mov_b32_e64 v139, v132
	v_pk_add_f32 v[132:133], v[140:141], v[138:139] neg_lo:[0,1] neg_hi:[0,1]
	s_nop 0
	v_add_f32_e32 v133, v157, v133
	v_add_f32_e32 v132, v132, v133
	v_add_f32_e32 v133, v161, v160
	v_add_f32_e32 v132, v137, v132
	v_sub_f32_e32 v136, v133, v161
	v_mul_f32_e32 v132, v159, v132
	v_sub_f32_e32 v136, v160, v136
	v_add_f32_e32 v136, v136, v132
	v_add_f32_e32 v138, v133, v136
	v_mul_f32_e64 v139, v138, v138
	v_fmamk_f32 v132, v139, 0x3e9b6dac, v223
	v_fmaak_f32 v199, v139, v132, 0x3f2aaada
	v_cvt_f32_i32_e32 v132, v156
	v_sub_f32_e32 v133, v138, v133
	v_sub_f32_e64 v133, v136, v133
	v_ldexp_f32 v140, v133, 1
	v_mul_f32_e64 v133, v138, v139
	v_ldexp_f32 v137, v138, 1
	v_pk_mul_f32 v[138:139], v[132:133], v[198:199]
	s_nop 0
	s_nop 0
	v_fma_f32 v136, v132, s46, -v138
	v_fmac_f32_e32 v136, 0xb102e308, v132
	v_pk_add_f32 v[132:133], v[138:139], v[136:137]
	s_nop 0
	v_sub_f32_e32 v137, v133, v137
	v_sub_f32_e32 v137, v139, v137
	v_add_f32_e32 v141, v140, v137
	v_mov_b32_e64 v140, v138
	v_pk_add_f32 v[138:139], v[132:133], v[138:139] neg_lo:[0,1] neg_hi:[0,1]
	v_pk_add_f32 v[156:157], v[132:133], v[140:141]
	v_mov_b32_e32 v137, v132
	v_mov_b32_e32 v139, v157
	v_pk_add_f32 v[158:159], v[136:137], v[138:139] neg_lo:[0,1] neg_hi:[0,1]
	v_pk_add_f32 v[136:137], v[136:137], v[138:139]
	v_mov_b32_e64 v140, v141
	v_pk_add_f32 v[138:139], v[136:137], v[132:133] op_sel:[1,0] op_sel_hi:[0,1] neg_lo:[0,1] neg_hi:[0,1]
	v_pk_add_f32 v[160:161], v[156:157], v[138:139] op_sel_hi:[1,0] neg_lo:[0,1] neg_hi:[0,1]
	v_mov_b32_e32 v156, v157
	v_mov_b32_e32 v157, v137
	v_pk_mov_b32 v[138:139], v[132:133], v[138:139] op_sel:[1,0]
	v_mov_b32_e64 v141, v132
	v_pk_add_f32 v[138:139], v[156:157], v[138:139] neg_lo:[0,1] neg_hi:[0,1]
	v_mov_b32_e64 v160, v158
	v_pk_add_f32 v[132:133], v[140:141], v[138:139] neg_lo:[0,1] neg_hi:[0,1]
	v_mov_b32_e64 v159, v137
	v_pk_add_f32 v[138:139], v[160:161], v[132:133]
	s_nop 0
	s_nop 0
	v_pk_add_f32 v[140:141], v[138:139], v[138:139] op_sel:[0,1] op_sel_hi:[1,0]
	s_nop 0
	s_nop 0
	v_pk_add_f32 v[136:137], v[136:137], v[140:141] op_sel:[1,0] op_sel_hi:[0,1]
	v_mov_b32_e64 v139, v136
	v_pk_add_f32 v[156:157], v[138:139], v[158:159] neg_lo:[0,1] neg_hi:[0,1]
	v_mov_b32_e32 v133, v140
	v_sub_f32_e32 v137, v138, v156
	v_pk_add_f32 v[132:133], v[132:133], v[156:157] neg_lo:[0,1] neg_hi:[0,1]
	v_sub_f32_e32 v137, v158, v137
	v_add_f32_e32 v132, v132, v137
	v_add_f32_e64 v132, v132, v133
	v_add_f32_e32 v132, v136, v132
	v_cndmask_b32_e32 v132, v230, v132, vcc
	v_cmp_ngt_f32_e32 vcc, -1.0, v162
	s_nop 1
	v_cndmask_b32_e32 v132, v231, v132, vcc
	v_cmp_neq_f32_e32 vcc, -1.0, v162
	s_nop 1
	v_cndmask_b32_e32 v132, v232, v132, vcc
	v_cmp_lt_f32_e64 vcc, |v162|, s44
	s_nop 1
	v_cndmask_b32_e32 v132, v132, v162, vcc
	v_sub_f32_e64 v132, v99, v132
.LBB0_335:
	v_or_b32_e32 v136, 1, v98
	v_ashrrev_i32_e32 v137, 31, v136
	v_lshlrev_b64 v[136:137], 6, v[136:137]
	v_lshl_add_u64 v[136:137], v[152:153], 0, v[136:137]
	v_add_f32_e64 v99, v96, v134
	s_mov_b64 s[6:7], -1
	s_and_b64 vcc, exec, s[8:9]
	global_store_dword v[136:137], v132, off
	s_cbranch_vccz .LBB0_343
	s_nop 0
	v_mul_f32_e32 v132, 0x3d888889, v99
	v_cmp_nlt_f32_e64 s[6:7], |v132|, s45
	s_and_saveexec_b64 s[22:23], s[6:7]
	s_xor_b64 s[6:7], exec, s[22:23]
	s_cbranch_execz .LBB0_338
	s_nop 0
	v_add_f32_e64 v133, |v132|, |v132|
	v_mul_f32_e32 v134, 0x3fb8aa3b, v133
	v_rndne_f32_e32 v136, v134
	v_sub_f32_e32 v137, v134, v136
	v_fma_f32 v134, v133, s39, -v134
	v_fmac_f32_e32 v134, 0x32a5705f, v133
	v_add_f32_e32 v134, v137, v134
	v_cvt_i32_f32_e32 v136, v136
	v_exp_f32_e32 v134, v134
	v_cmp_ngt_f32_e32 vcc, s40, v133
	v_ldexp_f32 v134, v134, v136
	s_nop 0
	v_cndmask_b32_e32 v134, 0, v134, vcc
	v_cmp_nlt_f32_e32 vcc, s41, v133
	s_nop 1
	v_cndmask_b32_e32 v133, v230, v134, vcc
	v_add_f32_e32 v133, 1.0, v133
	v_rcp_f32_e32 v133, v133
	s_nop 0
	v_fma_f32 v133, v133, -2.0, 1.0
.LBB0_338:
	s_andn2_saveexec_b64 s[6:7], s[6:7]
	v_mul_f32_e32 v133, v132, v132
	v_fmamk_f32 v134, v133, 0xbbbac73d, v222
	v_fmaak_f32 v134, v133, v134, 0xbd5c1c4e
	v_fmaak_f32 v134, v133, v134, 0x3e088382
	v_fmaak_f32 v134, v133, v134, 0xbeaaaa99
	v_mul_f32_e64 v134, |v132|, v134
	v_fma_f32 v133, v133, v134, |v132|
	s_or_b64 exec, exec, s[6:7]
	s_nop 0
	v_bfi_b32 v132, s43, v133, v132
	v_mul_f32_e32 v132, 0x41700000, v132
	s_and_saveexec_b64 s[6:7], s[4:5]
	s_cbranch_execz .LBB0_342
	v_mul_f32_e64 v133, |v132|, s74
	v_exp_f32_e32 v134, v133
	v_max_f32_e32 v132, v132, v132
	v_min_f32_e32 v162, 0, v132
	v_add_f32_e32 v136, 1.0, v134
	v_add_f32_e32 v132, -1.0, v136
	v_sub_f32_e32 v133, v132, v136
	v_sub_f32_e32 v132, v134, v132
	v_add_f32_e32 v133, 1.0, v133
	v_add_f32_e32 v137, v132, v133
	v_frexp_mant_f32_e32 v138, v136
	v_cvt_f64_f32_e32 v[132:133], v136
	v_frexp_exp_i32_f64_e32 v132, v[132:133]
	v_cmp_gt_f32_e32 vcc, s83, v138
	s_nop 1
	v_subbrev_co_u32_e32 v156, vcc, 0, v132, vcc
	v_sub_u32_e32 v132, 0, v156
	v_ldexp_f32 v133, v136, v132
	v_add_f32_e32 v136, -1.0, v133
	v_add_f32_e32 v138, 1.0, v133
	v_ldexp_f32 v132, v137, v132
	v_add_f32_e32 v137, 1.0, v136
	v_add_f32_e32 v139, -1.0, v138
	v_sub_f32_e32 v137, v133, v137
	v_sub_f32_e32 v133, v133, v139
	v_add_f32_e32 v137, v132, v137
	v_add_f32_e32 v132, v132, v133
	v_add_f32_e32 v157, v138, v132
	v_rcp_f32_e32 v159, v157
	v_sub_f32_e32 v133, v157, v138
	v_sub_f32_e32 v158, v132, v133
	v_add_f32_e32 v133, v136, v137
	v_mul_f32_e32 v161, v133, v159
	v_sub_f32_e32 v132, v133, v136
	v_mul_f32_e32 v136, v157, v161
	v_fma_f32 v138, v161, v157, -v136
	v_fmac_f32_e32 v138, v161, v158
	v_sub_f32_e32 v160, v137, v132
	v_add_f32_e32 v132, v136, v138
	v_sub_f32_e32 v137, v133, v132
	v_pk_add_f32 v[140:141], v[132:133], v[136:137] neg_lo:[0,1] neg_hi:[0,1]
	v_mov_b32_e64 v139, v132
	v_pk_add_f32 v[132:133], v[140:141], v[138:139] neg_lo:[0,1] neg_hi:[0,1]
	v_cmp_neq_f32_e32 vcc, s42, v134
	v_add_f32_e32 v133, v160, v133
	v_add_f32_e32 v132, v132, v133
	v_add_f32_e32 v133, v137, v132
	v_mul_f32_e32 v160, v159, v133
	v_mul_f32_e32 v136, v157, v160
	v_fma_f32 v138, v160, v157, -v136
	v_fmac_f32_e32 v138, v160, v158
	v_sub_f32_e32 v137, v137, v133
	v_add_f32_e32 v157, v132, v137
	v_add_f32_e32 v132, v136, v138
	v_sub_f32_e64 v137, v133, v132
	v_pk_add_f32 v[140:141], v[132:133], v[136:137] neg_lo:[0,1] neg_hi:[0,1]
	v_mov_b32_e64 v139, v132
	v_pk_add_f32 v[132:133], v[140:141], v[138:139] neg_lo:[0,1] neg_hi:[0,1]
	s_nop 0
	v_add_f32_e32 v133, v157, v133
	v_add_f32_e32 v132, v132, v133
	v_add_f32_e32 v133, v161, v160
	v_add_f32_e32 v132, v137, v132
	v_sub_f32_e32 v136, v133, v161
	v_mul_f32_e32 v132, v159, v132
	v_sub_f32_e32 v136, v160, v136
	v_add_f32_e32 v136, v136, v132
	v_add_f32_e32 v138, v133, v136
	v_mul_f32_e64 v139, v138, v138
	v_fmamk_f32 v132, v139, 0x3e9b6dac, v223
	v_fmaak_f32 v199, v139, v132, 0x3f2aaada
	v_cvt_f32_i32_e32 v132, v156
	v_sub_f32_e32 v133, v138, v133
	v_sub_f32_e64 v133, v136, v133
	v_ldexp_f32 v140, v133, 1
	v_mul_f32_e64 v133, v138, v139
	v_ldexp_f32 v137, v138, 1
	v_pk_mul_f32 v[138:139], v[132:133], v[198:199]
	s_nop 0
	s_nop 0
	v_fma_f32 v136, v132, s46, -v138
	v_fmac_f32_e32 v136, 0xb102e308, v132
	v_pk_add_f32 v[132:133], v[138:139], v[136:137]
	s_nop 0
	v_sub_f32_e32 v137, v133, v137
	v_sub_f32_e32 v137, v139, v137
	v_add_f32_e32 v141, v140, v137
	v_mov_b32_e64 v140, v138
	v_pk_add_f32 v[138:139], v[132:133], v[138:139] neg_lo:[0,1] neg_hi:[0,1]
	v_pk_add_f32 v[156:157], v[132:133], v[140:141]
	v_mov_b32_e32 v137, v132
	v_mov_b32_e32 v139, v157
	v_pk_add_f32 v[158:159], v[136:137], v[138:139] neg_lo:[0,1] neg_hi:[0,1]
	v_pk_add_f32 v[136:137], v[136:137], v[138:139]
	v_mov_b32_e64 v140, v141
	v_pk_add_f32 v[138:139], v[136:137], v[132:133] op_sel:[1,0] op_sel_hi:[0,1] neg_lo:[0,1] neg_hi:[0,1]
	v_pk_add_f32 v[160:161], v[156:157], v[138:139] op_sel_hi:[1,0] neg_lo:[0,1] neg_hi:[0,1]
	v_mov_b32_e32 v156, v157
	v_mov_b32_e32 v157, v137
	v_pk_mov_b32 v[138:139], v[132:133], v[138:139] op_sel:[1,0]
	v_mov_b32_e64 v141, v132
	v_pk_add_f32 v[138:139], v[156:157], v[138:139] neg_lo:[0,1] neg_hi:[0,1]
	v_mov_b32_e64 v160, v158
	v_pk_add_f32 v[132:133], v[140:141], v[138:139] neg_lo:[0,1] neg_hi:[0,1]
	v_mov_b32_e64 v159, v137
	v_pk_add_f32 v[138:139], v[160:161], v[132:133]
	s_nop 0
	s_nop 0
	v_pk_add_f32 v[140:141], v[138:139], v[138:139] op_sel:[0,1] op_sel_hi:[1,0]
	s_nop 0
	s_nop 0
	v_pk_add_f32 v[136:137], v[136:137], v[140:141] op_sel:[1,0] op_sel_hi:[0,1]
	v_mov_b32_e64 v139, v136
	v_pk_add_f32 v[156:157], v[138:139], v[158:159] neg_lo:[0,1] neg_hi:[0,1]
	v_mov_b32_e32 v133, v140
	v_sub_f32_e32 v137, v138, v156
	v_pk_add_f32 v[132:133], v[132:133], v[156:157] neg_lo:[0,1] neg_hi:[0,1]
	v_sub_f32_e32 v137, v158, v137
	v_add_f32_e32 v132, v132, v137
	v_add_f32_e64 v132, v132, v133
	v_add_f32_e32 v132, v136, v132
	v_cndmask_b32_e32 v132, v230, v132, vcc
	v_cmp_ngt_f32_e32 vcc, -1.0, v134
	s_nop 1
	v_cndmask_b32_e32 v132, v231, v132, vcc
	v_cmp_neq_f32_e32 vcc, -1.0, v134
	s_nop 1
	v_cndmask_b32_e32 v132, v232, v132, vcc
	v_cmp_lt_f32_e64 vcc, |v134|, s44
	s_nop 1
	v_cndmask_b32_e32 v132, v132, v134, vcc
	v_sub_f32_e64 v132, v162, v132

.LBB0_343:
	s_and_b64 vcc, exec, s[6:7]
	s_cbranch_vccz .LBB0_345
	v_mul_f32_e64 v132, |v99|, s74
	v_exp_f32_e32 v134, v132
	v_max_f32_e32 v99, v99, v99
	v_min_f32_e32 v99, 0, v99
	v_add_f32_e32 v136, 1.0, v134
	v_add_f32_e32 v132, -1.0, v136
	v_sub_f32_e32 v133, v132, v136
	v_sub_f32_e32 v132, v134, v132
	v_add_f32_e32 v133, 1.0, v133
	v_add_f32_e32 v137, v132, v133
	v_frexp_mant_f32_e32 v138, v136
	v_cvt_f64_f32_e32 v[132:133], v136
	v_frexp_exp_i32_f64_e32 v132, v[132:133]
	v_cmp_gt_f32_e32 vcc, s83, v138
	s_nop 1
	v_subbrev_co_u32_e32 v156, vcc, 0, v132, vcc
	v_sub_u32_e32 v132, 0, v156
	v_ldexp_f32 v133, v136, v132
	v_add_f32_e32 v136, -1.0, v133
	v_add_f32_e32 v138, 1.0, v133
	v_ldexp_f32 v132, v137, v132
	v_add_f32_e32 v137, 1.0, v136
	v_add_f32_e32 v139, -1.0, v138
	v_sub_f32_e32 v137, v133, v137
	v_sub_f32_e32 v133, v133, v139
	v_add_f32_e32 v137, v132, v137
	v_add_f32_e32 v132, v132, v133
	v_add_f32_e32 v157, v138, v132
	v_rcp_f32_e32 v159, v157
	v_sub_f32_e32 v133, v157, v138
	v_sub_f32_e32 v158, v132, v133
	v_add_f32_e32 v133, v136, v137
	v_mul_f32_e32 v161, v133, v159
	v_sub_f32_e32 v132, v133, v136
	v_mul_f32_e32 v136, v157, v161
	v_fma_f32 v138, v161, v157, -v136
	v_fmac_f32_e32 v138, v161, v158
	v_sub_f32_e32 v160, v137, v132
	v_add_f32_e32 v132, v136, v138
	v_sub_f32_e32 v137, v133, v132
	v_pk_add_f32 v[140:141], v[132:133], v[136:137] neg_lo:[0,1] neg_hi:[0,1]
	v_mov_b32_e64 v139, v132
	v_pk_add_f32 v[132:133], v[140:141], v[138:139] neg_lo:[0,1] neg_hi:[0,1]
	v_cmp_neq_f32_e32 vcc, s42, v134
	v_add_f32_e32 v133, v160, v133
	v_add_f32_e32 v132, v132, v133
	v_add_f32_e32 v133, v137, v132
	v_mul_f32_e32 v160, v159, v133
	v_mul_f32_e32 v136, v157, v160
	v_fma_f32 v138, v160, v157, -v136
	v_fmac_f32_e32 v138, v160, v158
	v_sub_f32_e32 v137, v137, v133
	v_add_f32_e32 v157, v132, v137
	v_add_f32_e32 v132, v136, v138
	v_sub_f32_e64 v137, v133, v132
	v_pk_add_f32 v[140:141], v[132:133], v[136:137] neg_lo:[0,1] neg_hi:[0,1]
	v_mov_b32_e64 v139, v132
	v_pk_add_f32 v[132:133], v[140:141], v[138:139] neg_lo:[0,1] neg_hi:[0,1]
	s_nop 0
	v_add_f32_e32 v133, v157, v133
	v_add_f32_e32 v132, v132, v133
	v_add_f32_e32 v133, v161, v160
	v_add_f32_e32 v132, v137, v132
	v_sub_f32_e32 v136, v133, v161
	v_mul_f32_e32 v132, v159, v132
	v_sub_f32_e32 v136, v160, v136
	v_add_f32_e32 v136, v136, v132
	v_add_f32_e32 v138, v133, v136
	v_mul_f32_e64 v139, v138, v138
	v_fmamk_f32 v132, v139, 0x3e9b6dac, v223
	v_fmaak_f32 v199, v139, v132, 0x3f2aaada
	v_cvt_f32_i32_e32 v132, v156
	v_sub_f32_e32 v133, v138, v133
	v_sub_f32_e64 v133, v136, v133
	v_ldexp_f32 v140, v133, 1
	v_mul_f32_e64 v133, v138, v139
	v_ldexp_f32 v137, v138, 1
	v_pk_mul_f32 v[138:139], v[132:133], v[198:199]
	s_nop 0
	s_nop 0
	v_fma_f32 v136, v132, s46, -v138
	v_fmac_f32_e32 v136, 0xb102e308, v132
	v_pk_add_f32 v[132:133], v[138:139], v[136:137]
	s_nop 0
	v_sub_f32_e32 v137, v133, v137
	v_sub_f32_e32 v137, v139, v137
	v_add_f32_e32 v141, v140, v137
	v_mov_b32_e64 v140, v138
	v_pk_add_f32 v[138:139], v[132:133], v[138:139] neg_lo:[0,1] neg_hi:[0,1]
	v_pk_add_f32 v[156:157], v[132:133], v[140:141]
	v_mov_b32_e32 v137, v132
	v_mov_b32_e32 v139, v157
	v_pk_add_f32 v[158:159], v[136:137], v[138:139] neg_lo:[0,1] neg_hi:[0,1]
	v_pk_add_f32 v[136:137], v[136:137], v[138:139]
	v_mov_b32_e64 v140, v141
	v_pk_add_f32 v[138:139], v[136:137], v[132:133] op_sel:[1,0] op_sel_hi:[0,1] neg_lo:[0,1] neg_hi:[0,1]
	v_pk_add_f32 v[160:161], v[156:157], v[138:139] op_sel_hi:[1,0] neg_lo:[0,1] neg_hi:[0,1]
	v_mov_b32_e32 v156, v157
	v_mov_b32_e32 v157, v137
	v_pk_mov_b32 v[138:139], v[132:133], v[138:139] op_sel:[1,0]
	v_mov_b32_e64 v141, v132
	v_pk_add_f32 v[138:139], v[156:157], v[138:139] neg_lo:[0,1] neg_hi:[0,1]
	v_mov_b32_e64 v160, v158
	v_pk_add_f32 v[132:133], v[140:141], v[138:139] neg_lo:[0,1] neg_hi:[0,1]
	v_mov_b32_e64 v159, v137
	v_pk_add_f32 v[138:139], v[160:161], v[132:133]
	s_nop 0
	s_nop 0
	v_pk_add_f32 v[140:141], v[138:139], v[138:139] op_sel:[0,1] op_sel_hi:[1,0]
	s_nop 0
	s_nop 0
	v_pk_add_f32 v[136:137], v[136:137], v[140:141] op_sel:[1,0] op_sel_hi:[0,1]
	v_mov_b32_e64 v139, v136
	v_pk_add_f32 v[156:157], v[138:139], v[158:159] neg_lo:[0,1] neg_hi:[0,1]
	v_mov_b32_e32 v133, v140
	v_sub_f32_e32 v137, v138, v156
	v_pk_add_f32 v[132:133], v[132:133], v[156:157] neg_lo:[0,1] neg_hi:[0,1]
	v_sub_f32_e32 v137, v158, v137
	v_add_f32_e32 v132, v132, v137
	v_add_f32_e64 v132, v132, v133
	v_add_f32_e32 v132, v136, v132
	v_cndmask_b32_e32 v132, v230, v132, vcc
	v_cmp_ngt_f32_e32 vcc, -1.0, v134
	s_nop 1
	v_cndmask_b32_e32 v132, v231, v132, vcc
	v_cmp_neq_f32_e32 vcc, -1.0, v134
	s_nop 1
	v_cndmask_b32_e32 v132, v232, v132, vcc
	v_cmp_lt_f32_e64 vcc, |v134|, s44
	s_nop 1
	v_cndmask_b32_e32 v132, v132, v134, vcc
	v_sub_f32_e64 v132, v99, v132
.LBB0_345:
	v_or_b32_e32 v136, 2, v98
	v_ashrrev_i32_e32 v137, 31, v136
	v_lshlrev_b64 v[136:137], 6, v[136:137]
	v_lshl_add_u64 v[136:137], v[152:153], 0, v[136:137]
	v_add_f32_e64 v96, v96, v135
	s_mov_b64 s[6:7], -1
	s_and_b64 vcc, exec, s[8:9]
	global_store_dword v[136:137], v132, off
	s_cbranch_vccz .LBB0_353
	s_nop 0
	v_mul_f32_e32 v99, 0x3d888889, v96
	v_cmp_nlt_f32_e64 s[6:7], |v99|, s45
	s_and_saveexec_b64 s[22:23], s[6:7]
	s_xor_b64 s[6:7], exec, s[22:23]
	s_cbranch_execz .LBB0_348
	s_nop 0
	v_add_f32_e64 v132, |v99|, |v99|
	v_mul_f32_e32 v133, 0x3fb8aa3b, v132
	v_rndne_f32_e32 v134, v133
	v_sub_f32_e32 v135, v133, v134
	v_fma_f32 v133, v132, s39, -v133
	v_fmac_f32_e32 v133, 0x32a5705f, v132
	v_add_f32_e32 v133, v135, v133
	v_cvt_i32_f32_e32 v134, v134
	v_exp_f32_e32 v133, v133
	v_cmp_ngt_f32_e32 vcc, s40, v132
	v_ldexp_f32 v133, v133, v134
	s_nop 0
	v_cndmask_b32_e32 v133, 0, v133, vcc
	v_cmp_nlt_f32_e32 vcc, s41, v132
	s_nop 1
	v_cndmask_b32_e32 v132, v230, v133, vcc
	v_add_f32_e32 v132, 1.0, v132
	v_rcp_f32_e32 v132, v132
	s_nop 0
	v_fma_f32 v132, v132, -2.0, 1.0
.LBB0_348:
	s_andn2_saveexec_b64 s[6:7], s[6:7]
	v_mul_f32_e32 v132, v99, v99
	v_fmamk_f32 v133, v132, 0xbbbac73d, v222
	v_fmaak_f32 v133, v132, v133, 0xbd5c1c4e
	v_fmaak_f32 v133, v132, v133, 0x3e088382
	v_fmaak_f32 v133, v132, v133, 0xbeaaaa99
	v_mul_f32_e64 v133, |v99|, v133
	v_fma_f32 v132, v132, v133, |v99|
	s_or_b64 exec, exec, s[6:7]
	s_nop 0
	v_bfi_b32 v99, s43, v132, v99
	v_mul_f32_e32 v99, 0x41700000, v99
	s_and_saveexec_b64 s[6:7], s[4:5]
	s_cbranch_execz .LBB0_352
	v_mul_f32_e64 v132, |v99|, s74
	v_exp_f32_e32 v160, v132
	v_max_f32_e32 v99, v99, v99
	v_min_f32_e32 v99, 0, v99
	v_add_f32_e32 v134, 1.0, v160
	v_add_f32_e32 v132, -1.0, v134
	v_sub_f32_e32 v133, v132, v134
	v_sub_f32_e32 v132, v160, v132
	v_add_f32_e32 v133, 1.0, v133
	v_add_f32_e32 v135, v132, v133
	v_frexp_mant_f32_e32 v136, v134
	v_cvt_f64_f32_e32 v[132:133], v134
	v_frexp_exp_i32_f64_e32 v132, v[132:133]
	v_cmp_gt_f32_e32 vcc, s83, v136
	s_nop 1
	v_subbrev_co_u32_e32 v140, vcc, 0, v132, vcc
	v_sub_u32_e32 v132, 0, v140
	v_ldexp_f32 v133, v134, v132
	v_add_f32_e32 v134, -1.0, v133
	v_add_f32_e32 v136, 1.0, v133
	v_ldexp_f32 v132, v135, v132
	v_add_f32_e32 v135, 1.0, v134
	v_add_f32_e32 v137, -1.0, v136
	v_sub_f32_e32 v135, v133, v135
	v_sub_f32_e32 v133, v133, v137
	v_add_f32_e32 v135, v132, v135
	v_add_f32_e32 v132, v132, v133
	v_add_f32_e32 v141, v136, v132
	v_rcp_f32_e32 v157, v141
	v_sub_f32_e32 v133, v141, v136
	v_sub_f32_e32 v156, v132, v133
	v_add_f32_e32 v133, v134, v135
	v_mul_f32_e32 v159, v133, v157
	v_sub_f32_e32 v132, v133, v134
	v_mul_f32_e32 v134, v141, v159
	v_fma_f32 v136, v159, v141, -v134
	v_fmac_f32_e32 v136, v159, v156
	v_sub_f32_e32 v158, v135, v132
	v_add_f32_e32 v132, v134, v136
	v_sub_f32_e32 v135, v133, v132
	v_pk_add_f32 v[138:139], v[132:133], v[134:135] neg_lo:[0,1] neg_hi:[0,1]
	v_mov_b32_e64 v137, v132
	v_pk_add_f32 v[132:133], v[138:139], v[136:137] neg_lo:[0,1] neg_hi:[0,1]
	v_cmp_neq_f32_e32 vcc, s42, v160
	v_add_f32_e32 v133, v158, v133
	v_add_f32_e32 v132, v132, v133
	v_add_f32_e32 v133, v135, v132
	v_mul_f32_e32 v158, v157, v133
	v_mul_f32_e32 v134, v141, v158
	v_fma_f32 v136, v158, v141, -v134
	v_fmac_f32_e32 v136, v158, v156
	v_sub_f32_e32 v135, v135, v133
	v_add_f32_e32 v141, v132, v135
	v_add_f32_e32 v132, v134, v136
	v_sub_f32_e64 v135, v133, v132
	v_pk_add_f32 v[138:139], v[132:133], v[134:135] neg_lo:[0,1] neg_hi:[0,1]
	v_mov_b32_e64 v137, v132
	v_pk_add_f32 v[132:133], v[138:139], v[136:137] neg_lo:[0,1] neg_hi:[0,1]
	s_nop 0
	v_add_f32_e32 v133, v141, v133
	v_add_f32_e32 v132, v132, v133
	v_add_f32_e32 v133, v159, v158
	v_add_f32_e32 v132, v135, v132
	v_sub_f32_e32 v134, v133, v159
	v_mul_f32_e32 v132, v157, v132
	v_sub_f32_e32 v134, v158, v134
	v_add_f32_e32 v134, v134, v132
	v_add_f32_e32 v136, v133, v134
	v_mul_f32_e64 v137, v136, v136
	v_fmamk_f32 v132, v137, 0x3e9b6dac, v223
	v_fmaak_f32 v199, v137, v132, 0x3f2aaada
	v_cvt_f32_i32_e32 v132, v140
	v_sub_f32_e32 v133, v136, v133
	v_sub_f32_e64 v133, v134, v133
	v_ldexp_f32 v138, v133, 1
	v_mul_f32_e64 v133, v136, v137
	v_ldexp_f32 v135, v136, 1
	v_pk_mul_f32 v[136:137], v[132:133], v[198:199]
	s_nop 0
	s_nop 0
	v_fma_f32 v134, v132, s46, -v136
	v_fmac_f32_e32 v134, 0xb102e308, v132
	v_pk_add_f32 v[132:133], v[136:137], v[134:135]
	s_nop 0
	v_sub_f32_e32 v135, v133, v135
	v_sub_f32_e32 v135, v137, v135
	v_add_f32_e32 v139, v138, v135
	v_mov_b32_e64 v138, v136
	v_pk_add_f32 v[136:137], v[132:133], v[136:137] neg_lo:[0,1] neg_hi:[0,1]
	v_pk_add_f32 v[140:141], v[132:133], v[138:139]
	v_mov_b32_e32 v135, v132
	v_mov_b32_e32 v137, v141
	v_pk_add_f32 v[156:157], v[134:135], v[136:137] neg_lo:[0,1] neg_hi:[0,1]
	v_pk_add_f32 v[134:135], v[134:135], v[136:137]
	v_mov_b32_e64 v138, v139
	v_pk_add_f32 v[136:137], v[134:135], v[132:133] op_sel:[1,0] op_sel_hi:[0,1] neg_lo:[0,1] neg_hi:[0,1]
	v_pk_add_f32 v[158:159], v[140:141], v[136:137] op_sel_hi:[1,0] neg_lo:[0,1] neg_hi:[0,1]
	v_mov_b32_e32 v140, v141
	v_mov_b32_e32 v141, v135
	v_pk_mov_b32 v[136:137], v[132:133], v[136:137] op_sel:[1,0]
	v_mov_b32_e64 v139, v132
	v_pk_add_f32 v[136:137], v[140:141], v[136:137] neg_lo:[0,1] neg_hi:[0,1]
	v_mov_b32_e64 v158, v156
	v_pk_add_f32 v[132:133], v[138:139], v[136:137] neg_lo:[0,1] neg_hi:[0,1]
	v_mov_b32_e64 v157, v135
	v_pk_add_f32 v[136:137], v[158:159], v[132:133]
	s_nop 0
	s_nop 0
	v_pk_add_f32 v[138:139], v[136:137], v[136:137] op_sel:[0,1] op_sel_hi:[1,0]
	s_nop 0
	s_nop 0
	v_pk_add_f32 v[134:135], v[134:135], v[138:139] op_sel:[1,0] op_sel_hi:[0,1]
	v_mov_b32_e64 v137, v134
	v_pk_add_f32 v[140:141], v[136:137], v[156:157] neg_lo:[0,1] neg_hi:[0,1]
	v_mov_b32_e32 v133, v138
	v_sub_f32_e32 v135, v136, v140
	v_pk_add_f32 v[132:133], v[132:133], v[140:141] neg_lo:[0,1] neg_hi:[0,1]
	v_sub_f32_e32 v135, v156, v135
	v_add_f32_e32 v132, v132, v135
	v_add_f32_e64 v132, v132, v133
	v_add_f32_e32 v132, v134, v132
	v_cndmask_b32_e32 v132, v230, v132, vcc
	v_cmp_ngt_f32_e32 vcc, -1.0, v160
	s_nop 1
	v_cndmask_b32_e32 v132, v231, v132, vcc
	v_cmp_neq_f32_e32 vcc, -1.0, v160
	s_nop 1
	v_cndmask_b32_e32 v132, v232, v132, vcc
	v_cmp_lt_f32_e64 vcc, |v160|, s44
	s_nop 1
	v_cndmask_b32_e32 v132, v132, v160, vcc
	v_sub_f32_e64 v99, v99, v132

.LBB0_353:
	s_and_b64 vcc, exec, s[6:7]
	s_cbranch_vccz .LBB0_276
	v_mul_f32_e64 v99, |v96|, s74
	v_exp_f32_e32 v99, v99
	v_max_f32_e32 v96, v96, v96
	v_min_f32_e32 v96, 0, v96
	v_add_f32_e32 v134, 1.0, v99
	v_add_f32_e32 v132, -1.0, v134
	v_sub_f32_e32 v133, v132, v134
	v_sub_f32_e32 v132, v99, v132
	v_add_f32_e32 v133, 1.0, v133
	v_add_f32_e32 v135, v132, v133
	v_frexp_mant_f32_e32 v136, v134
	v_cvt_f64_f32_e32 v[132:133], v134
	v_frexp_exp_i32_f64_e32 v132, v[132:133]
	v_cmp_gt_f32_e32 vcc, s83, v136
	s_nop 1
	v_subbrev_co_u32_e32 v140, vcc, 0, v132, vcc
	v_sub_u32_e32 v132, 0, v140
	v_ldexp_f32 v133, v134, v132
	v_add_f32_e32 v134, -1.0, v133
	v_add_f32_e32 v136, 1.0, v133
	v_ldexp_f32 v132, v135, v132
	v_add_f32_e32 v135, 1.0, v134
	v_add_f32_e32 v137, -1.0, v136
	v_sub_f32_e32 v135, v133, v135
	v_sub_f32_e32 v133, v133, v137
	v_add_f32_e32 v135, v132, v135
	v_add_f32_e32 v132, v132, v133
	v_add_f32_e32 v141, v136, v132
	v_rcp_f32_e32 v157, v141
	v_sub_f32_e32 v133, v141, v136
	v_sub_f32_e32 v156, v132, v133
	v_add_f32_e32 v133, v134, v135
	v_mul_f32_e32 v159, v133, v157
	v_sub_f32_e32 v132, v133, v134
	v_mul_f32_e32 v134, v141, v159
	v_fma_f32 v136, v159, v141, -v134
	v_fmac_f32_e32 v136, v159, v156
	v_sub_f32_e32 v158, v135, v132
	v_add_f32_e32 v132, v134, v136
	v_sub_f32_e32 v135, v133, v132
	v_pk_add_f32 v[138:139], v[132:133], v[134:135] neg_lo:[0,1] neg_hi:[0,1]
	v_mov_b32_e64 v137, v132
	v_pk_add_f32 v[132:133], v[138:139], v[136:137] neg_lo:[0,1] neg_hi:[0,1]
	v_cmp_neq_f32_e32 vcc, s42, v99
	v_add_f32_e32 v133, v158, v133
	v_add_f32_e32 v132, v132, v133
	v_add_f32_e32 v133, v135, v132
	v_mul_f32_e32 v158, v157, v133
	v_mul_f32_e32 v134, v141, v158
	v_fma_f32 v136, v158, v141, -v134
	v_fmac_f32_e32 v136, v158, v156
	v_sub_f32_e32 v135, v135, v133
	v_add_f32_e32 v141, v132, v135
	v_add_f32_e32 v132, v134, v136
	v_sub_f32_e64 v135, v133, v132
	v_pk_add_f32 v[138:139], v[132:133], v[134:135] neg_lo:[0,1] neg_hi:[0,1]
	v_mov_b32_e64 v137, v132
	v_pk_add_f32 v[132:133], v[138:139], v[136:137] neg_lo:[0,1] neg_hi:[0,1]
	s_nop 0
	v_add_f32_e32 v133, v141, v133
	v_add_f32_e32 v132, v132, v133
	v_add_f32_e32 v133, v159, v158
	v_add_f32_e32 v132, v135, v132
	v_sub_f32_e32 v134, v133, v159
	v_mul_f32_e32 v132, v157, v132
	v_sub_f32_e32 v134, v158, v134
	v_add_f32_e32 v134, v134, v132
	v_add_f32_e32 v136, v133, v134
	v_mul_f32_e64 v137, v136, v136
	v_fmamk_f32 v132, v137, 0x3e9b6dac, v223
	v_fmaak_f32 v199, v137, v132, 0x3f2aaada
	v_cvt_f32_i32_e32 v132, v140
	v_sub_f32_e32 v133, v136, v133
	v_sub_f32_e64 v133, v134, v133
	v_ldexp_f32 v138, v133, 1
	v_mul_f32_e64 v133, v136, v137
	v_ldexp_f32 v135, v136, 1
	v_pk_mul_f32 v[136:137], v[132:133], v[198:199]
	s_nop 0
	s_nop 0
	v_fma_f32 v134, v132, s46, -v136
	v_fmac_f32_e32 v134, 0xb102e308, v132
	v_pk_add_f32 v[132:133], v[136:137], v[134:135]
	s_nop 0
	v_sub_f32_e32 v135, v133, v135
	v_sub_f32_e32 v135, v137, v135
	v_add_f32_e32 v139, v138, v135
	v_mov_b32_e64 v138, v136
	v_pk_add_f32 v[136:137], v[132:133], v[136:137] neg_lo:[0,1] neg_hi:[0,1]
	v_pk_add_f32 v[140:141], v[132:133], v[138:139]
	v_mov_b32_e32 v135, v132
	v_mov_b32_e32 v137, v141
	v_pk_add_f32 v[156:157], v[134:135], v[136:137] neg_lo:[0,1] neg_hi:[0,1]
	v_pk_add_f32 v[134:135], v[134:135], v[136:137]
	v_mov_b32_e64 v138, v139
	v_pk_add_f32 v[136:137], v[134:135], v[132:133] op_sel:[1,0] op_sel_hi:[0,1] neg_lo:[0,1] neg_hi:[0,1]
	v_pk_add_f32 v[158:159], v[140:141], v[136:137] op_sel_hi:[1,0] neg_lo:[0,1] neg_hi:[0,1]
	v_mov_b32_e32 v140, v141
	v_mov_b32_e32 v141, v135
	v_pk_mov_b32 v[136:137], v[132:133], v[136:137] op_sel:[1,0]
	v_mov_b32_e64 v139, v132
	v_pk_add_f32 v[136:137], v[140:141], v[136:137] neg_lo:[0,1] neg_hi:[0,1]
	v_mov_b32_e64 v158, v156
	v_pk_add_f32 v[132:133], v[138:139], v[136:137] neg_lo:[0,1] neg_hi:[0,1]
	v_mov_b32_e64 v157, v135
	v_pk_add_f32 v[136:137], v[158:159], v[132:133]
	s_nop 0
	s_nop 0
	v_pk_add_f32 v[138:139], v[136:137], v[136:137] op_sel:[0,1] op_sel_hi:[1,0]
	s_nop 0
	s_nop 0
	v_pk_add_f32 v[134:135], v[134:135], v[138:139] op_sel:[1,0] op_sel_hi:[0,1]
	v_mov_b32_e64 v137, v134
	v_pk_add_f32 v[140:141], v[136:137], v[156:157] neg_lo:[0,1] neg_hi:[0,1]
	v_mov_b32_e32 v133, v138
	v_sub_f32_e32 v135, v136, v140
	v_pk_add_f32 v[132:133], v[132:133], v[140:141] neg_lo:[0,1] neg_hi:[0,1]
	v_sub_f32_e32 v135, v156, v135
	v_add_f32_e32 v132, v132, v135
	v_add_f32_e64 v132, v132, v133
	v_add_f32_e32 v132, v134, v132
	v_cndmask_b32_e32 v132, v230, v132, vcc
	v_cmp_ngt_f32_e32 vcc, -1.0, v99
	s_nop 1
	v_cndmask_b32_e32 v132, v231, v132, vcc
	v_cmp_neq_f32_e32 vcc, -1.0, v99
	s_nop 1
	v_cndmask_b32_e32 v132, v232, v132, vcc
	v_cmp_lt_f32_e64 vcc, |v99|, s44
	s_nop 1
	v_cndmask_b32_e32 v99, v132, v99, vcc
	v_sub_f32_e32 v99, v96, v99
	s_branch .LBB0_276
.LBB0_355:
	v_readlane_b32 s42, v254, 34
	s_mov_b32 s93, s38
	s_nop 0
	v_readlane_b32 s43, v254, 35
	v_readlane_b32 s50, v254, 31

.LBB0_357:
	v_readlane_b32 s2, v254, 5
	s_add_i32 s45, s92, 1
	s_nop 0
	v_readlane_b32 s3, v254, 6
	s_cmp_lt_i32 s45, s3
	s_nop 0
	v_readlane_b32 s2, v254, 24
	s_cselect_b64 s[58:59], -1, 0
	s_nop 0
	v_readlane_b32 s3, v254, 25
	s_and_b64 s[38:39], s[10:11], s[58:59]
	s_and_b64 vcc, exec, s[2:3]
	s_cbranch_vccz .LBB0_363
	s_and_b64 vcc, exec, s[42:43]
	s_cbranch_vccz .LBB0_373
	s_mov_b64 s[40:41], 0
	s_and_b64 vcc, exec, s[38:39]
	s_mov_b64 s[2:3], 0
	s_cbranch_vccz .LBB0_374
	s_mov_b32 s2, s97
	s_waitcnt vmcnt(0)
	s_waitcnt lgkmcnt(0)
	s_barrier
	s_nop 0
	v_mbcnt_lo_u32_b32 v0, -1, s2
	v_mbcnt_hi_u32_b32 v0, -1, v0
	v_cmp_eq_u32_e32 vcc, s65, v0
	s_and_saveexec_b64 s[48:49], vcc
	s_cbranch_execz .LBB0_409
	s_nop 0
	v_readlane_b32 s54, v253, 12
	v_readlane_b32 s2, v253, 14
	v_readlane_b32 s55, v253, 13
	v_readlane_b32 s22, v253, 17
	v_mov_b32_e32 v0, s2
	s_waitcnt vmcnt(0) expcnt(0) lgkmcnt(0)
	ds_read_b32 v2, v0
	ds_read_b32 v0, v0 offset:4
	s_waitcnt lgkmcnt(1)
	v_cmp_ne_u32_e32 vcc, 0, v2
	s_cbranch_vccnz .LBB0_380
	s_nop 0
	v_readlane_b32 s2, v253, 6
	v_readlane_b32 s3, v253, 7
	s_load_dwordx2 s[6:7], s[2:3], 0x4
	s_add_u32 s2, s54, 0x1000
	s_addc_u32 s3, s55, 0
	s_nop 0
	s_add_u32 s4, s54, 0x1100
	s_addc_u32 s5, s55, 0
	s_waitcnt lgkmcnt(0)
	s_mul_i32 s23, s6, s61
	s_nop 0
	s_add_u32 s6, s54, 0x1200
	s_mul_i32 s23, s23, s7
	s_addc_u32 s7, s55, 0
	s_add_u32 s8, s54, 0x1300
	s_addc_u32 s9, s55, 0
	s_mov_b32 s30, 1
	s_mov_b64 s[10:11], 0
	s_branch .LBB0_366

.LBB0_366:
	v_mov_b64_e32 v[12:13], s[54:55]
	s_nop 0
	flat_load_dword v1, v[12:13] offset:1024 sc1
	flat_load_dword v0, v[12:13] offset:1280 sc1
	flat_load_dword v2, v[12:13] offset:1536 sc1
	s_or_b64 s[16:17], s[16:17], exec
	s_or_b64 s[14:15], s[14:15], exec
	s_waitcnt vmcnt(0) lgkmcnt(0)
	v_add_u32_e32 v3, v0, v1
	v_add_u32_e64 v4, v3, v2
	flat_load_dword v3, v[12:13] offset:1792 sc1
	s_waitcnt vmcnt(0) lgkmcnt(0)
	v_add_u32_e32 v5, v4, v3
	flat_load_dword v4, v[12:13] offset:2048 sc1
	s_waitcnt vmcnt(0) lgkmcnt(0)
	v_add_u32_e32 v6, v5, v4
	flat_load_dword v5, v[12:13] offset:2304 sc1
	s_waitcnt vmcnt(0) lgkmcnt(0)
	v_add_u32_e32 v7, v6, v5
	flat_load_dword v6, v[12:13] offset:2560 sc1
	s_waitcnt vmcnt(0) lgkmcnt(0)
	v_add_u32_e32 v8, v7, v6
	flat_load_dword v7, v[12:13] offset:2816 sc1
	s_waitcnt vmcnt(0) lgkmcnt(0)
	v_add_u32_e32 v9, v8, v7
	flat_load_dword v8, v[12:13] offset:3072 sc1
	s_waitcnt vmcnt(0) lgkmcnt(0)
	v_add_u32_e32 v10, v9, v8
	flat_load_dword v9, v[12:13] offset:3328 sc1
	s_waitcnt vmcnt(0) lgkmcnt(0)
	v_add_u32_e32 v11, v10, v9
	flat_load_dword v10, v[12:13] offset:3584 sc1
	s_waitcnt vmcnt(0) lgkmcnt(0)
	v_add_u32_e32 v14, v11, v10
	flat_load_dword v11, v[12:13] offset:3840 sc1
	v_mov_b64_e32 v[12:13], s[2:3]
	s_nop 0
	flat_load_dword v12, v[12:13] sc1
	s_waitcnt vmcnt(0) lgkmcnt(0)
	v_add_u32_e32 v14, v14, v11
	v_add_u32_e32 v16, v14, v12
	v_mov_b64_e32 v[14:15], s[4:5]
	flat_load_dword v13, v[14:15] sc1
	v_mov_b64_e32 v[14:15], s[6:7]
	s_nop 0
	flat_load_dword v14, v[14:15] sc1
	s_waitcnt vmcnt(0) lgkmcnt(0)
	v_add_u32_e32 v16, v16, v13
	v_add_u32_e32 v18, v16, v14
	v_mov_b64_e32 v[16:17], s[8:9]
	flat_load_dword v15, v[16:17] sc1
	s_waitcnt vmcnt(0) lgkmcnt(0)
	v_add_u32_e32 v16, v18, v15
	v_cmp_ne_u32_e32 vcc, s23, v16
	s_and_saveexec_b64 s[18:19], vcc
	s_cbranch_execz .LBB0_365
	s_nop 0
	s_and_b32 s24, s30, 0xff
	s_mov_b64 s[20:21], -1
	s_cmp_eq_u32 s24, 0
	s_mov_b64 s[26:27], -1
	s_mov_b64 s[24:25], -1
	s_sleep 1
	s_cbranch_scc1 .LBB0_369
	s_and_saveexec_b64 s[28:29], s[26:27]
	s_cbranch_execz .LBB0_364
	s_branch .LBB0_372

.LBB0_377:
	s_or_b64 exec, exec, s[10:11]
	s_xor_b64 s[2:3], s[12:13], -1
	s_and_saveexec_b64 s[4:5], s[2:3]
	s_xor_b64 s[2:3], exec, s[4:5]
	s_cbranch_execz .LBB0_379
	v_mov_b64_e32 v[16:17], s[54:55]
	v_mov_b32_e64 v18, 1
	flat_atomic_add v[16:17], v18 offset:512
.LBB0_379:
	s_or_b64 exec, exec, s[2:3]
	s_cmp_eq_u32 s22, 15
	s_cselect_b64 vcc, -1, 0
	s_cmp_eq_u32 s22, 14
	s_cselect_b64 s[2:3], -1, 0
	s_cmp_eq_u32 s22, 13
	s_cselect_b64 s[4:5], -1, 0
	s_cmp_eq_u32 s22, 12
	s_cselect_b64 s[6:7], -1, 0
	s_cmp_eq_u32 s22, 11
	s_cselect_b64 s[8:9], -1, 0
	s_cmp_eq_u32 s22, 10
	s_cselect_b64 s[10:11], -1, 0
	s_cmp_eq_u32 s22, 9
	s_cselect_b64 s[12:13], -1, 0
	s_cmp_eq_u32 s22, 8
	s_cselect_b64 s[14:15], -1, 0
	s_cmp_eq_u32 s22, 7
	s_cselect_b64 s[16:17], -1, 0
	s_cmp_eq_u32 s22, 6
	s_cselect_b64 s[18:19], -1, 0
	s_cmp_eq_u32 s22, 5
	s_cselect_b64 s[20:21], -1, 0
	s_cmp_eq_u32 s22, 4
	s_cselect_b64 s[24:25], -1, 0
	s_cmp_eq_u32 s22, 3
	s_cselect_b64 s[26:27], -1, 0
	s_cmp_eq_u32 s22, 2
	s_cselect_b64 s[28:29], -1, 0
	s_cmp_eq_u32 s22, 1
	s_cselect_b64 s[30:31], -1, 0
	s_cmp_eq_u32 s22, 0
	s_cselect_b64 s[34:35], -1, 0
	s_nop 0
	v_cndmask_b32_e64 v16, 0, v1, s[34:35]
	v_cndmask_b32_e64 v16, v16, v0, s[30:31]
	v_cndmask_b32_e64 v16, v16, v2, s[28:29]
	v_cndmask_b32_e64 v16, v16, v3, s[26:27]
	v_cndmask_b32_e64 v16, v16, v4, s[24:25]
	v_cndmask_b32_e64 v16, v16, v5, s[20:21]
	v_cndmask_b32_e64 v16, v16, v6, s[18:19]
	v_cndmask_b32_e64 v16, v16, v7, s[16:17]
	v_cndmask_b32_e64 v16, v16, v8, s[14:15]
	v_cndmask_b32_e64 v16, v16, v9, s[12:13]
	v_cndmask_b32_e64 v16, v16, v10, s[10:11]
	v_cndmask_b32_e64 v16, v16, v11, s[8:9]
	v_cndmask_b32_e64 v16, v16, v12, s[6:7]
	v_cndmask_b32_e64 v16, v16, v13, s[4:5]
	v_cndmask_b32_e64 v16, v16, v14, s[2:3]
	v_cndmask_b32_e32 v16, v16, v15, vcc
	v_cmp_ne_u32_e32 vcc, 0, v1
	v_readlane_b32 s2, v253, 14
	s_nop 0
	s_nop 0
	v_cndmask_b32_e64 v1, 0, 1, vcc
	v_cmp_ne_u32_e32 vcc, 0, v0
	s_nop 1
	v_addc_co_u32_e32 v0, vcc, 0, v1, vcc
	v_cmp_ne_u32_e32 vcc, 0, v2
	v_max_u32_e32 v2, 1, v16
	s_nop 0
	v_cndmask_b32_e64 v1, 0, 1, vcc
	v_cmp_ne_u32_e32 vcc, 0, v3
	s_nop 1
	v_addc_co_u32_e32 v0, vcc, v0, v1, vcc
	v_cmp_ne_u32_e32 vcc, 0, v4
	s_nop 1
	s_nop 0
	v_cndmask_b32_e64 v1, 0, 1, vcc
	v_cmp_ne_u32_e32 vcc, 0, v5
	s_nop 1
	v_addc_co_u32_e32 v0, vcc, v0, v1, vcc
	v_cmp_ne_u32_e32 vcc, 0, v6
	s_nop 1
	s_nop 0
	v_cndmask_b32_e64 v1, 0, 1, vcc
	v_cmp_ne_u32_e32 vcc, 0, v7
	s_nop 1
	v_addc_co_u32_e32 v0, vcc, v0, v1, vcc
	v_cmp_ne_u32_e32 vcc, 0, v8
	s_nop 1
	s_nop 0
	v_cndmask_b32_e64 v1, 0, 1, vcc
	v_cmp_ne_u32_e32 vcc, 0, v9
	s_nop 1
	v_addc_co_u32_e32 v0, vcc, v0, v1, vcc
	v_cmp_ne_u32_e32 vcc, 0, v10
	s_nop 1
	s_nop 0
	v_cndmask_b32_e64 v1, 0, 1, vcc
	v_cmp_ne_u32_e32 vcc, 0, v11
	s_nop 1
	v_addc_co_u32_e32 v0, vcc, v0, v1, vcc
	v_cmp_ne_u32_e32 vcc, 0, v12
	s_nop 1
	s_nop 0
	v_cndmask_b32_e64 v1, 0, 1, vcc
	v_cmp_ne_u32_e32 vcc, 0, v13
	s_nop 1
	v_addc_co_u32_e32 v0, vcc, v0, v1, vcc
	v_cmp_ne_u32_e32 vcc, 0, v14
	s_nop 1
	s_nop 0
	v_cndmask_b32_e64 v1, 0, 1, vcc
	v_cmp_ne_u32_e32 vcc, 0, v15
	s_nop 1
	v_addc_co_u32_e32 v0, vcc, v0, v1, vcc
	v_max_u32_e32 v0, 1, v0
	v_mov_b32_e64 v1, s2
	ds_write_b32 v1, v2
	ds_write_b32 v1, v0 offset:4
.LBB0_380:
	s_lshl_b32 s22, s22, 6
	s_nop 0
	s_add_i32 s96, s22, 0x500
	s_lshl_b64 s[2:3], s[96:97], 2
	s_add_u32 s2, s54, s2
	s_addc_u32 s3, s55, s3
	v_mov_b64_e32 v[4:5], s[2:3]
	v_mov_b32_e64 v1, 1
	flat_atomic_add v3, v[4:5], v1 sc0
	v_cvt_f32_u32_e32 v1, v2
	v_sub_u32_e32 v4, 0, v2
	v_rcp_iflag_f32_e32 v1, v1
	s_nop 0
	v_mul_f32_e32 v1, 0x4f7ffffe, v1
	v_cvt_u32_f32_e32 v1, v1
	s_nop 0
	v_mul_lo_u32 v4, v4, v1
	v_mul_hi_u32 v4, v1, v4
	v_add_u32_e32 v1, v1, v4
	s_waitcnt vmcnt(0) lgkmcnt(0)
	v_mul_hi_u32 v1, v3, v1
	v_mul_lo_u32 v4, v1, v2
	v_sub_u32_e32 v4, v3, v4
	v_cmp_ge_u32_e32 vcc, v4, v2
	v_add_u32_e32 v5, 1, v1
	s_nop 0
	v_cndmask_b32_e32 v1, v1, v5, vcc
	v_sub_u32_e32 v5, v4, v2
	v_cndmask_b32_e32 v4, v4, v5, vcc
	v_cmp_ge_u32_e32 vcc, v4, v2
	v_add_u32_e32 v4, 1, v1
	s_nop 0
	v_cndmask_b32_e32 v1, v1, v4, vcc
	v_add_u32_e32 v4, 1, v3
	v_mad_u64_u32 v[2:3], s[2:3], v2, v1, v[2:3]
	v_cmp_ne_u32_e32 vcc, v4, v2
	s_and_saveexec_b64 s[2:3], vcc
	s_xor_b64 s[2:3], exec, s[2:3]
	s_cbranch_execz .LBB0_393
	s_add_i32 s96, s22, 0x900
	s_lshl_b64 s[4:5], s[96:97], 2
	s_add_u32 s6, s54, s4
	s_addc_u32 s7, s55, s5
	v_mov_b64_e32 v[2:3], s[6:7]
	flat_load_dword v0, v[2:3] sc1
	s_waitcnt vmcnt(0) lgkmcnt(0)
	v_cmp_eq_u32_e32 vcc, v0, v1
	s_and_saveexec_b64 s[4:5], vcc
	s_cbranch_execz .LBB0_392
	s_mov_b32 s23, 1
	s_mov_b64 s[8:9], 0
	s_branch .LBB0_384

.LBB0_384:
	s_nop 0
	s_and_b32 s16, s23, 0xff
	s_mov_b64 s[14:15], -1
	s_cmp_lg_u32 s16, 0
	s_mov_b64 s[16:17], -1
	s_sleep 1
	s_cbranch_scc1 .LBB0_388
	v_mov_b64_e32 v[2:3], s[54:55]
	flat_load_dword v0, v[2:3] offset:512 sc1
	s_mov_b64 s[16:17], 0
	s_mov_b64 s[18:19], -1
	s_waitcnt vmcnt(0) lgkmcnt(0)
	v_cmp_eq_u32_e32 vcc, 0, v0
	s_and_saveexec_b64 s[20:21], vcc
	s_nop 0
	s_cmp_lt_u32 s23, 0x400001
	s_cselect_b64 s[16:17], -1, 0
	s_xor_b64 s[18:19], exec, -1
	s_and_b64 s[16:17], s[16:17], exec
	s_or_b64 exec, exec, s[20:21]

.LBB0_390:
	s_or_b64 exec, exec, s[8:9]
	s_xor_b64 s[6:7], s[10:11], -1
	s_and_saveexec_b64 s[8:9], s[6:7]
	s_xor_b64 s[8:9], exec, s[8:9]
	s_cbranch_execz .LBB0_392
	v_mov_b64_e32 v[0:1], s[54:55]
	v_mov_b32_e64 v2, 1
	flat_atomic_add v[0:1], v2 offset:512

.LBB0_393:
	s_andn2_saveexec_b64 s[2:3], s[2:3]
	s_cbranch_execz .LBB0_409
	v_mov_b32_e32 v1, s54
	v_add_co_u32_e32 v2, vcc, 0x3000, v1
	v_mov_b32_e64 v1, s55
	buffer_wbl2 sc1
	s_waitcnt vmcnt(0)
	v_addc_co_u32_e32 v3, vcc, 0, v1, vcc
	v_mov_b32_e64 v1, 1
	flat_atomic_add v1, v[2:3], v1 offset:1024 sc0
	v_cvt_f32_u32_e32 v2, v0
	v_sub_u32_e32 v3, 0, v0
	s_mov_b64 s[6:7], -1
	v_rcp_iflag_f32_e32 v2, v2
	s_nop 0
	s_nop 0
	v_mul_f32_e32 v2, 0x4f7ffffe, v2
	v_cvt_u32_f32_e32 v2, v2
	s_nop 0
	v_mul_lo_u32 v3, v3, v2
	v_mul_hi_u32 v3, v2, v3
	v_add_u32_e32 v2, v2, v3
	s_waitcnt vmcnt(0) lgkmcnt(0)
	v_mul_hi_u32 v2, v1, v2
	v_mul_lo_u32 v3, v2, v0
	v_sub_u32_e32 v3, v1, v3
	v_cmp_ge_u32_e32 vcc, v3, v0
	v_add_u32_e32 v4, 1, v2
	s_nop 0
	v_cndmask_b32_e32 v2, v2, v4, vcc
	v_sub_u32_e32 v4, v3, v0
	v_cndmask_b32_e32 v3, v3, v4, vcc
	v_cmp_ge_u32_e32 vcc, v3, v0
	v_add_u32_e32 v3, 1, v2
	s_nop 0
	v_cndmask_b32_e32 v2, v2, v3, vcc
	v_add_u32_e32 v3, 1, v1
	v_mad_u64_u32 v[0:1], s[2:3], v0, v2, v[0:1]
	s_add_u32 s2, s54, 0x3500
	s_addc_u32 s3, s55, 0
	v_cmp_ne_u32_e32 vcc, v3, v0
	v_mov_b64_e32 v[0:1], s[2:3]
	s_and_saveexec_b64 s[4:5], vcc
	s_cbranch_execz .LBB0_406
	v_mov_b64_e32 v[0:1], s[2:3]
	flat_load_dword v0, v[0:1] sc1
	s_mov_b64 s[10:11], 0
	s_waitcnt vmcnt(0) lgkmcnt(0)
	v_cmp_eq_u32_e32 vcc, v0, v2
	s_and_saveexec_b64 s[8:9], vcc
	s_cbranch_execz .LBB0_405
	s_nop 0
	s_add_u32 s6, s54, 0x200
	s_addc_u32 s7, s55, 0
	s_mov_b32 s23, 1
	s_branch .LBB0_398

.LBB0_400:
	v_mov_b64_e32 v[0:1], s[6:7]
	s_nop 0
	flat_load_dword v0, v[0:1] sc1
	s_mov_b64 s[18:19], 0
	s_mov_b64 s[16:17], -1
	s_waitcnt vmcnt(0) lgkmcnt(0)
	v_cmp_eq_u32_e32 vcc, 0, v0
	s_and_saveexec_b64 s[20:21], vcc
	s_nop 0
	s_cmp_lt_u32 s23, 0x400001
	s_cselect_b64 s[18:19], -1, 0
	s_xor_b64 s[16:17], exec, -1
	s_and_b64 s[18:19], s[18:19], exec
	s_or_b64 exec, exec, s[20:21]
	s_and_saveexec_b64 s[20:21], s[18:19]
	s_cbranch_execz .LBB0_397
.LBB0_403:
	v_mov_b64_e32 v[0:1], s[2:3]
	s_nop 0
	flat_load_dword v0, v[0:1] sc1
	s_add_i32 s23, s23, 1
	s_or_b64 s[16:17], s[16:17], exec
	s_waitcnt vmcnt(0) lgkmcnt(0)
	v_cmp_ne_u32_e32 vcc, v0, v2
	s_orn2_b64 s[14:15], vcc, exec
	s_branch .LBB0_397

.LBB0_406:
	s_or_b64 exec, exec, s[4:5]
	s_and_saveexec_b64 s[2:3], s[6:7]
	s_cbranch_execz .LBB0_408
	v_mov_b32_e64 v2, 1
	flat_atomic_add v[0:1], v2
.LBB0_408:
	s_or_b64 exec, exec, s[2:3]
	s_nop 0
	s_add_i32 s96, s22, 0x900
	s_lshl_b64 s[2:3], s[96:97], 2
	s_add_u32 s2, s54, s2
	s_addc_u32 s3, s55, s3
	v_mov_b64_e32 v[0:1], s[2:3]
	v_mov_b32_e32 v2, 1
	s_waitcnt vmcnt(0) lgkmcnt(0)
	buffer_inv sc1
	flat_atomic_add v[0:1], v2
	s_waitcnt vmcnt(0)

.LBB0_411:
	s_and_b64 vcc, exec, s[38:39]
	s_cbranch_vccz .LBB0_457
	s_mov_b32 s2, s97
	s_waitcnt vmcnt(0)
	s_waitcnt lgkmcnt(0)
	s_barrier
	s_nop 0
	s_nop 0
	v_mbcnt_lo_u32_b32 v0, -1, s2
	v_mbcnt_hi_u32_b32 v0, -1, v0
	v_cmp_eq_u32_e32 vcc, s65, v0
	s_and_saveexec_b64 s[38:39], vcc
	s_cbranch_execz .LBB0_456
	s_nop 0
	v_readlane_b32 s40, v253, 12
	v_readlane_b32 s2, v253, 14
	v_readlane_b32 s41, v253, 13
	v_readlane_b32 s22, v253, 17
	v_mov_b32_e32 v0, s2
	s_waitcnt vmcnt(0) expcnt(0) lgkmcnt(0)
	ds_read_b32 v2, v0
	ds_read_b32 v0, v0 offset:4
	s_waitcnt lgkmcnt(1)
	v_cmp_ne_u32_e32 vcc, 0, v2
	s_cbranch_vccnz .LBB0_427
	s_nop 0
	v_readlane_b32 s2, v253, 6
	v_readlane_b32 s3, v253, 7
	s_load_dwordx2 s[6:7], s[2:3], 0x4
	s_add_u32 s2, s40, 0x1000
	s_addc_u32 s3, s41, 0
	s_nop 0
	s_add_u32 s4, s40, 0x1100
	s_addc_u32 s5, s41, 0
	s_waitcnt lgkmcnt(0)
	s_mul_i32 s23, s6, s61
	s_nop 0
	s_add_u32 s6, s40, 0x1200
	s_mul_i32 s23, s23, s7
	s_addc_u32 s7, s41, 0
	s_add_u32 s8, s40, 0x1300
	s_addc_u32 s9, s41, 0
	s_mov_b32 s30, 1
	s_mov_b64 s[10:11], 0
	s_branch .LBB0_417

.LBB0_417:
	v_mov_b64_e32 v[12:13], s[40:41]
	flat_load_dword v1, v[12:13] offset:1024 sc1
	flat_load_dword v0, v[12:13] offset:1280 sc1
	flat_load_dword v2, v[12:13] offset:1536 sc1
	s_or_b64 s[16:17], s[16:17], exec
	s_or_b64 s[14:15], s[14:15], exec
	s_waitcnt vmcnt(0) lgkmcnt(0)
	v_add_u32_e32 v3, v0, v1
	v_add_u32_e64 v4, v3, v2
	flat_load_dword v3, v[12:13] offset:1792 sc1
	s_waitcnt vmcnt(0) lgkmcnt(0)
	v_add_u32_e32 v5, v4, v3
	flat_load_dword v4, v[12:13] offset:2048 sc1
	s_waitcnt vmcnt(0) lgkmcnt(0)
	v_add_u32_e32 v6, v5, v4
	flat_load_dword v5, v[12:13] offset:2304 sc1
	s_waitcnt vmcnt(0) lgkmcnt(0)
	v_add_u32_e32 v7, v6, v5
	flat_load_dword v6, v[12:13] offset:2560 sc1
	s_waitcnt vmcnt(0) lgkmcnt(0)
	v_add_u32_e32 v8, v7, v6
	flat_load_dword v7, v[12:13] offset:2816 sc1
	s_waitcnt vmcnt(0) lgkmcnt(0)
	v_add_u32_e32 v9, v8, v7
	flat_load_dword v8, v[12:13] offset:3072 sc1
	s_waitcnt vmcnt(0) lgkmcnt(0)
	v_add_u32_e32 v10, v9, v8
	flat_load_dword v9, v[12:13] offset:3328 sc1
	s_waitcnt vmcnt(0) lgkmcnt(0)
	v_add_u32_e32 v11, v10, v9
	flat_load_dword v10, v[12:13] offset:3584 sc1
	s_waitcnt vmcnt(0) lgkmcnt(0)
	v_add_u32_e32 v14, v11, v10
	flat_load_dword v11, v[12:13] offset:3840 sc1
	v_mov_b64_e32 v[12:13], s[2:3]
	s_nop 0
	flat_load_dword v12, v[12:13] sc1
	s_waitcnt vmcnt(0) lgkmcnt(0)
	v_add_u32_e32 v14, v14, v11
	v_add_u32_e32 v16, v14, v12
	v_mov_b64_e32 v[14:15], s[4:5]
	flat_load_dword v13, v[14:15] sc1
	v_mov_b64_e32 v[14:15], s[6:7]
	s_nop 0
	flat_load_dword v14, v[14:15] sc1
	s_waitcnt vmcnt(0) lgkmcnt(0)
	v_add_u32_e32 v16, v16, v13
	v_add_u32_e32 v18, v16, v14
	v_mov_b64_e32 v[16:17], s[8:9]
	flat_load_dword v15, v[16:17] sc1
	s_waitcnt vmcnt(0) lgkmcnt(0)
	v_add_u32_e32 v16, v18, v15
	v_cmp_ne_u32_e32 vcc, s23, v16
	s_and_saveexec_b64 s[18:19], vcc
	s_cbranch_execz .LBB0_416
	s_nop 0
	s_and_b32 s24, s30, 0xff
	s_mov_b64 s[20:21], -1
	s_cmp_eq_u32 s24, 0
	s_mov_b64 s[26:27], -1
	s_mov_b64 s[24:25], -1
	s_sleep 1
	s_cbranch_scc1 .LBB0_420
	s_and_saveexec_b64 s[28:29], s[26:27]
	s_cbranch_execz .LBB0_415
	s_branch .LBB0_423

.LBB0_427:
	s_lshl_b32 s22, s22, 6
	s_nop 0
	s_add_i32 s96, s22, 0x500
	s_lshl_b64 s[2:3], s[96:97], 2
	s_add_u32 s2, s40, s2
	s_addc_u32 s3, s41, s3
	v_mov_b64_e32 v[4:5], s[2:3]
	v_mov_b32_e64 v1, 1
	flat_atomic_add v3, v[4:5], v1 sc0
	v_cvt_f32_u32_e32 v1, v2
	v_sub_u32_e32 v4, 0, v2
	v_rcp_iflag_f32_e32 v1, v1
	s_nop 0
	v_mul_f32_e32 v1, 0x4f7ffffe, v1
	v_cvt_u32_f32_e32 v1, v1
	s_nop 0
	v_mul_lo_u32 v4, v4, v1
	v_mul_hi_u32 v4, v1, v4
	v_add_u32_e32 v1, v1, v4
	s_waitcnt vmcnt(0) lgkmcnt(0)
	v_mul_hi_u32 v1, v3, v1
	v_mul_lo_u32 v4, v1, v2
	v_sub_u32_e32 v4, v3, v4
	v_cmp_ge_u32_e32 vcc, v4, v2
	v_add_u32_e32 v5, 1, v1
	s_nop 0
	v_cndmask_b32_e32 v1, v1, v5, vcc
	v_sub_u32_e32 v5, v4, v2
	v_cndmask_b32_e32 v4, v4, v5, vcc
	v_cmp_ge_u32_e32 vcc, v4, v2
	v_add_u32_e32 v4, 1, v1
	s_nop 0
	v_cndmask_b32_e32 v1, v1, v4, vcc
	v_add_u32_e32 v4, 1, v3
	v_mad_u64_u32 v[2:3], s[2:3], v2, v1, v[2:3]
	v_cmp_ne_u32_e32 vcc, v4, v2
	s_and_saveexec_b64 s[2:3], vcc
	s_xor_b64 s[2:3], exec, s[2:3]
	s_cbranch_execz .LBB0_440
	s_add_i32 s96, s22, 0x900
	s_lshl_b64 s[4:5], s[96:97], 2
	s_add_u32 s6, s40, s4
	s_addc_u32 s7, s41, s5
	v_mov_b64_e32 v[2:3], s[6:7]
	flat_load_dword v0, v[2:3] sc1
	s_waitcnt vmcnt(0) lgkmcnt(0)
	v_cmp_eq_u32_e32 vcc, v0, v1
	s_and_saveexec_b64 s[4:5], vcc
	s_cbranch_execz .LBB0_439
	s_mov_b32 s23, 1
	s_mov_b64 s[8:9], 0
	s_branch .LBB0_431

.LBB0_431:
	s_nop 0
	s_and_b32 s16, s23, 0xff
	s_mov_b64 s[14:15], -1
	s_cmp_lg_u32 s16, 0
	s_mov_b64 s[16:17], -1
	s_sleep 1
	s_cbranch_scc1 .LBB0_435
	v_mov_b64_e32 v[2:3], s[40:41]
	flat_load_dword v0, v[2:3] offset:512 sc1
	s_mov_b64 s[16:17], 0
	s_mov_b64 s[18:19], -1
	s_waitcnt vmcnt(0) lgkmcnt(0)
	v_cmp_eq_u32_e32 vcc, 0, v0
	s_and_saveexec_b64 s[20:21], vcc
	s_nop 0
	s_cmp_lt_u32 s23, 0x400001
	s_cselect_b64 s[16:17], -1, 0
	s_xor_b64 s[18:19], exec, -1
	s_and_b64 s[16:17], s[16:17], exec
	s_or_b64 exec, exec, s[20:21]

.LBB0_437:
	s_or_b64 exec, exec, s[8:9]
	s_xor_b64 s[6:7], s[10:11], -1
	s_and_saveexec_b64 s[8:9], s[6:7]
	s_xor_b64 s[8:9], exec, s[8:9]
	s_cbranch_execz .LBB0_439
	v_mov_b64_e32 v[0:1], s[40:41]
	v_mov_b32_e64 v2, 1
	flat_atomic_add v[0:1], v2 offset:512

.LBB0_440:
	s_andn2_saveexec_b64 s[2:3], s[2:3]
	s_cbranch_execz .LBB0_456
	v_mov_b32_e32 v1, s40
	v_add_co_u32_e32 v2, vcc, 0x3000, v1
	v_mov_b32_e64 v1, s41
	buffer_wbl2 sc1
	s_waitcnt vmcnt(0)
	v_addc_co_u32_e32 v3, vcc, 0, v1, vcc
	v_mov_b32_e64 v1, 1
	flat_atomic_add v1, v[2:3], v1 offset:1024 sc0
	v_cvt_f32_u32_e32 v2, v0
	v_sub_u32_e32 v3, 0, v0
	s_mov_b64 s[6:7], -1
	v_rcp_iflag_f32_e32 v2, v2
	s_nop 0
	s_nop 0
	v_mul_f32_e32 v2, 0x4f7ffffe, v2
	v_cvt_u32_f32_e32 v2, v2
	s_nop 0
	v_mul_lo_u32 v3, v3, v2
	v_mul_hi_u32 v3, v2, v3
	v_add_u32_e32 v2, v2, v3
	s_waitcnt vmcnt(0) lgkmcnt(0)
	v_mul_hi_u32 v2, v1, v2
	v_mul_lo_u32 v3, v2, v0
	v_sub_u32_e32 v3, v1, v3
	v_cmp_ge_u32_e32 vcc, v3, v0
	v_add_u32_e32 v4, 1, v2
	s_nop 0
	v_cndmask_b32_e32 v2, v2, v4, vcc
	v_sub_u32_e32 v4, v3, v0
	v_cndmask_b32_e32 v3, v3, v4, vcc
	v_cmp_ge_u32_e32 vcc, v3, v0
	v_add_u32_e32 v3, 1, v2
	s_nop 0
	v_cndmask_b32_e32 v2, v2, v3, vcc
	v_add_u32_e32 v3, 1, v1
	v_mad_u64_u32 v[0:1], s[2:3], v0, v2, v[0:1]
	s_add_u32 s2, s40, 0x3500
	s_addc_u32 s3, s41, 0
	v_cmp_ne_u32_e32 vcc, v3, v0
	v_mov_b64_e32 v[0:1], s[2:3]
	s_and_saveexec_b64 s[4:5], vcc
	s_cbranch_execz .LBB0_453
	v_mov_b64_e32 v[0:1], s[2:3]
	flat_load_dword v0, v[0:1] sc1
	s_mov_b64 s[10:11], 0
	s_waitcnt vmcnt(0) lgkmcnt(0)
	v_cmp_eq_u32_e32 vcc, v0, v2
	s_and_saveexec_b64 s[8:9], vcc
	s_cbranch_execz .LBB0_452
	s_nop 0
	s_add_u32 s6, s40, 0x200
	s_addc_u32 s7, s41, 0
	s_mov_b32 s23, 1
	s_branch .LBB0_445

.LBB0_455:
	s_or_b64 exec, exec, s[2:3]
	s_nop 0
	s_add_i32 s96, s22, 0x900
	s_lshl_b64 s[2:3], s[96:97], 2
	s_add_u32 s2, s40, s2
	s_addc_u32 s3, s41, s3
	v_mov_b64_e32 v[0:1], s[2:3]
	v_mov_b32_e32 v2, 1
	s_waitcnt vmcnt(0) lgkmcnt(0)
	buffer_inv sc1
	flat_atomic_add v[0:1], v2
	s_waitcnt vmcnt(0)

.LBB0_457:
	s_nop 0
	v_writelane_b32 v254, s72, 16
	s_and_b64 vcc, exec, s[2:3]
	s_cbranch_vccz .LBB0_459
	s_waitcnt lgkmcnt(0)
.LBB0_459:
	s_nop 0
	s_add_u32 s54, s70, 0x16e00000
	s_addc_u32 s55, s71, 0
	s_nop 0
	s_add_u32 s90, s70, 0x800000
	s_addc_u32 s91, s71, 0
	s_nop 0
	s_add_u32 s2, s70, 0x26e00000
	s_addc_u32 s3, s71, 0
	s_nop 0
	v_writelane_b32 v254, s2, 26
	s_mov_b32 s51, 0x42700000
	s_nop 0
	s_nop 0
	v_writelane_b32 v254, s3, 27
	s_nop 0
	s_nop 0
	v_readlane_b32 s2, v254, 5
	v_readlane_b32 s3, v254, 6
	s_cmp_gt_i32 s2, s45
	s_cselect_b64 s[2:3], -1, 0
	s_xor_b64 s[4:5], s[58:59], -1
	s_or_b64 s[2:3], s[2:3], s[4:5]
	s_add_i32 s89, s92, 2
	s_and_b64 vcc, exec, s[2:3]
	s_cbranch_vccnz .LBB0_609
	s_andn2_b64 vcc, exec, s[56:57]
	s_cbranch_vccnz .LBB0_469
	s_mov_b32 s2, s97
	s_mov_b32 s16, s93
	s_nop 0
	v_mbcnt_lo_u32_b32 v0, -1, s2
	v_mbcnt_hi_u32_b32 v0, -1, v0
	v_add_u32_e32 v0, s64, v0
	s_cmpk_gt_i32 s16, 0xff
	v_readfirstlane_b32 s2, v0
	s_cbranch_scc1 .LBB0_469
	v_and_b32_e32 v5, 64, v227
	v_add_u32_e32 v6, -1, v227
	v_cmp_lt_i32_e32 vcc, v6, v5
	s_ashr_i32 s22, s2, 6
	s_lshl_b32 s4, s22, 2
	v_cndmask_b32_e32 v6, v6, v227, vcc
	v_lshlrev_b32_e32 v13, 2, v6
	v_add_u32_e32 v6, -2, v227
	v_cmp_lt_i32_e32 vcc, v6, v5
	v_lshlrev_b32_e32 v2, 3, v0
	s_add_i32 s23, s4, 0
	v_cndmask_b32_e32 v6, v6, v227, vcc
	v_lshlrev_b32_e32 v14, 2, v6
	v_add_u32_e32 v6, -4, v227
	v_cmp_lt_i32_e32 vcc, v6, v5
	v_and_b32_e32 v4, 63, v0
	v_ashrrev_i32_e32 v3, 31, v2
	v_cndmask_b32_e32 v6, v6, v227, vcc
	v_lshlrev_b32_e32 v15, 2, v6
	v_add_u32_e32 v6, -8, v227
	v_cmp_lt_i32_e32 vcc, v6, v5
	s_cmp_gt_i32 s22, 0
	v_cmp_eq_u32_e64 s[2:3], 63, v4
	v_cndmask_b32_e32 v6, v6, v227, vcc
	v_lshlrev_b32_e32 v16, 2, v6
	v_add_u32_e64 v6, -16, v227
	v_cmp_lt_i32_e32 vcc, v6, v5
	s_cselect_b64 s[18:19], -1, 0
	v_lshl_add_u64 v[0:1], v[2:3], 2, s[90:91]
	v_cndmask_b32_e32 v6, v6, v227, vcc
	v_lshlrev_b32_e32 v17, 2, v6
	v_subrev_u32_e32 v6, 32, v227
	v_cmp_lt_i32_e32 vcc, v6, v5
	v_cmp_eq_u32_e64 s[4:5], 0, v4
	v_cmp_gt_u32_e64 s[6:7], 2, v4
	v_cndmask_b32_e32 v5, v6, v227, vcc
	s_nop 0
	v_cmp_gt_u32_e64 s[8:9], 4, v4
	v_cmp_gt_u32_e64 s[10:11], 8, v4
	v_cmp_gt_u32_e64 s[12:13], 16, v4
	v_lshlrev_b32_e32 v18, 2, v5
	s_nop 0
	v_cmp_gt_u32_e64 s[14:15], 32, v4
	v_lshlrev_b64 v[2:3], 6, v[2:3]
	s_branch .LBB0_464
.LBB0_463:
	s_ashr_i32 s17, s16, 31
	s_lshl_b64 s[20:21], s[16:17], 14
	s_nop 0
	v_pk_add_f32 v[10:11], v[10:11], v[12:13] op_sel_hi:[1,0]
	v_pk_add_f32 v[8:9], v[8:9], v[12:13] op_sel_hi:[1,0]
	v_pk_add_f32 v[6:7], v[6:7], v[12:13] op_sel_hi:[1,0]
	v_pk_add_f32 v[4:5], v[4:5], v[12:13] op_sel_hi:[1,0]
	s_add_i32 s16, s16, s61
	s_nop 0
	v_lshl_add_u64 v[24:25], v[0:1], 0, s[20:21]
	v_pk_mul_f32 v[20:21], v[10:11], s[74:75] op_sel_hi:[1,0]
	v_pk_mul_f32 v[22:23], v[8:9], s[74:75] op_sel_hi:[1,0]
	v_pk_mul_f32 v[6:7], v[6:7], s[74:75] op_sel_hi:[1,0]
	v_pk_mul_f32 v[8:9], v[4:5], s[74:75] op_sel_hi:[1,0]
	s_cmpk_gt_i32 s16, 0xff
	s_nop 0
	global_store_dwordx4 v[24:25], v[20:23], off
	global_store_dwordx4 v[24:25], v[6:9], off offset:16
	s_barrier
	s_cbranch_scc1 .LBB0_469
.LBB0_464:
	s_ashr_i32 s20, s16, 4
	s_and_b32 s17, s16, 15
	s_ashr_i32 s21, s20, 31
	s_lshl_b32 s17, s17, 2
	v_readlane_b32 s24, v254, 36
	v_readlane_b32 s25, v254, 37
	s_add_u32 s17, s24, s17
	s_addc_u32 s24, s25, 0
	s_lshl_b64 s[20:21], s[20:21], 18
	s_add_u32 s20, s17, s20
	s_addc_u32 s21, s24, s21
	s_nop 0
	v_lshl_add_u64 v[4:5], s[20:21], 0, v[2:3]
	global_load_dword v6, v[4:5], off
	global_load_dword v7, v[4:5], off offset:64
	global_load_dword v8, v[4:5], off offset:128
	global_load_dword v9, v[4:5], off offset:192
	global_load_dword v12, v[4:5], off offset:256
	global_load_dword v19, v[4:5], off offset:320
	global_load_dword v20, v[4:5], off offset:384
	s_nop 0
	s_nop 0
	global_load_dword v5, v[4:5], off offset:448
	s_waitcnt vmcnt(0)
	v_add_f32_e32 v10, 0, v6
	v_add_f32_e32 v11, v10, v7
	v_add_f32_e32 v8, v11, v8
	v_add_f32_e32 v9, v8, v9
	v_add_f32_e32 v6, v9, v12
	v_add_f32_e32 v7, v6, v19
	v_add_f32_e32 v4, v7, v20
	v_add_f32_e64 v5, v4, v5
	ds_bpermute_b32 v12, v13, v5
	s_waitcnt lgkmcnt(0)
	v_add_f32_e32 v12, v5, v12
	v_cndmask_b32_e64 v12, v12, v5, s[4:5]
	ds_bpermute_b32 v19, v14, v12
	s_waitcnt lgkmcnt(0)
	v_add_f32_e32 v19, v12, v19
	v_cndmask_b32_e64 v12, v19, v12, s[6:7]
	ds_bpermute_b32 v19, v15, v12
	s_waitcnt lgkmcnt(0)
	v_add_f32_e32 v19, v12, v19
	v_cndmask_b32_e64 v12, v19, v12, s[8:9]
	ds_bpermute_b32 v19, v16, v12
	s_waitcnt lgkmcnt(0)
	v_add_f32_e32 v19, v12, v19
	v_cndmask_b32_e64 v12, v19, v12, s[10:11]
	ds_bpermute_b32 v19, v17, v12
	s_waitcnt lgkmcnt(0)
	v_add_f32_e32 v19, v12, v19
	v_cndmask_b32_e64 v12, v19, v12, s[12:13]
	ds_bpermute_b32 v19, v18, v12
	s_waitcnt lgkmcnt(0)
	v_add_f32_e32 v19, v12, v19
	s_and_saveexec_b64 s[20:21], s[2:3]
	v_mov_b32_e32 v20, s23
	ds_write_b32 v20, v19
	s_or_b64 exec, exec, s[20:21]
	s_nop 0
	v_cndmask_b32_e64 v12, v19, v12, s[14:15]
	s_andn2_b64 vcc, exec, s[18:19]
	v_sub_f32_e32 v12, v12, v5
	s_waitcnt lgkmcnt(0)
	s_barrier
	s_cbranch_vccnz .LBB0_463
	s_mov_b32 s17, 0
	s_mov_b32 s20, s22
.LBB0_468:
	v_mov_b32_e32 v19, s17
	ds_read_b32 v19, v19
	s_add_i32 s20, s20, -1
	s_add_i32 s17, s17, 4
	s_cmp_eq_u32 s20, 0
	s_waitcnt lgkmcnt(0)
	v_add_f32_e64 v12, v12, v19
	s_cbranch_scc0 .LBB0_468
	s_branch .LBB0_463

.LBB0_471:
	s_andn2_b64 vcc, exec, s[4:5]
	s_mov_b32 s4, 0
	s_cbranch_vccnz .LBB0_476
	s_nop 0
	v_readlane_b32 s6, v254, 24
	v_readlane_b32 s7, v254, 25
	s_and_b64 vcc, exec, s[6:7]
	s_mov_b64 s[8:9], -1
	s_cbranch_vccz .LBB0_474
	s_nop 0
	v_readlane_b32 s6, v254, 22
	v_readlane_b32 s7, v254, 23
	s_mov_b32 s8, s6
	s_ashr_i32 s9, s6, 31
	v_writelane_b32 v254, s6, 22
	s_nop 1
	s_nop 0
	v_writelane_b32 v254, s7, 23
	s_lshl_b64 s[6:7], s[8:9], 20
	s_add_u32 s5, s70, s6
	s_addc_u32 s7, s71, s7
	s_nop 0
	s_add_u32 s6, s5, 0x2300000
	s_addc_u32 s7, s7, 0
	s_mov_b64 s[8:9], 0
.LBB0_474:
	s_andn2_b64 vcc, exec, s[8:9]
	s_cbranch_vccnz .LBB0_477
	s_add_u32 s6, s70, 0x2200000
	s_addc_u32 s7, s71, 0
	s_mov_b64 s[2:3], 0
	s_movk_i32 s40, 0x400
	s_nop 0
	s_mov_b64 s[8:9], 0x4000000
	s_mov_b32 s41, 0
	s_mov_b32 s38, 1.0
	s_mov_b32 s39, 8
	s_movk_i32 s10, 0x800
	s_mov_b64 s[12:13], s[54:55]
	s_branch .LBB0_478
.LBB0_476:
	s_movk_i32 s10, 0xc00
	s_mov_b32 s39, 12
	s_mov_b32 s45, 8
	s_nop 0
	s_mov_b32 s38, 0x3e000000
	s_mov_b32 s41, 2
	s_mov_b64 s[8:9], 0
	s_mov_b64 s[14:15], 0xc00
	s_mov_b64 s[12:13], s[54:55]
	s_mov_b32 s40, 0
	s_branch .LBB0_479
.LBB0_477:
	s_nop 0
	v_readlane_b32 s12, v254, 26
	s_mov_b32 s40, 0
	s_mov_b64 s[8:9], 0
	s_mov_b32 s38, 0x3e38aa3b
	s_mov_b32 s39, 4
	s_movk_i32 s10, 0x400
	s_mov_b32 s41, 4
	s_nop 0
	v_readlane_b32 s13, v254, 27
.LBB0_478:
	s_mov_b32 s45, 2.0
	s_nop 0
	s_mov_b64 s[14:15], 0x400

.Lrot_skip:
	s_mov_b32 s5, s97
	s_cmp_ge_i32 s50, s10
	s_cselect_b64 s[16:17], -1, 0
	v_mbcnt_lo_u32_b32 v0, -1, s5
	s_lshl_b32 s15, s39, 3
	s_nop 0
	v_mbcnt_hi_u32_b32 v0, -1, v0
	v_add_u32_e32 v9, s64, v0
	v_cvt_f32_ubyte0_e32 v0, s15
	v_readlane_b32 s18, v254, 42
	v_rcp_iflag_f32_e32 v8, v0
	s_nop 0
	v_readlane_b32 s19, v254, 43
	s_or_b64 s[16:17], s[18:19], s[16:17]
	s_lshr_b32 s24, s10, 3
	s_and_b64 vcc, exec, s[16:17]
	v_readfirstlane_b32 s9, v9
	s_mov_b32 s53, s93
	s_mov_b64 s[16:17], s[18:19]
	s_cbranch_vccnz .LBB0_481
	s_nop 0
	v_mul_f32_e32 v0, 0x4f7ffffe, v8
	v_cvt_u32_f32_e32 v0, v0
	s_nop 0
	v_readlane_b32 s4, v254, 59
	s_or_b32 s4, s24, s4
	s_nop 0
	v_readlane_b32 s5, v254, 60
	s_sub_i32 s16, 0, s15
	v_readfirstlane_b32 s17, v0
	s_mul_i32 s4, s4, s5
	s_nop 0
	v_readlane_b32 s5, v254, 61
	s_mul_i32 s16, s16, s17
	s_add_i32 s4, s4, s5
	s_mul_hi_u32 s16, s17, s16
	s_abs_i32 s11, s4
	s_add_i32 s17, s17, s16
	s_mul_hi_u32 s16, s11, s17
	s_mul_i32 s17, s16, s15
	s_sub_i32 s11, s11, s17
	s_ashr_i32 s5, s4, 31
	s_add_i32 s17, s16, 1
	s_sub_i32 s18, s11, s15
	s_cmp_ge_u32 s11, s15
	s_cselect_b32 s16, s17, s16
	s_cselect_b32 s11, s18, s11
	s_add_i32 s17, s16, 1
	s_cmp_ge_u32 s11, s15
	s_cselect_b32 s11, s17, s16
	s_xor_b32 s11, s11, s5
	s_sub_i32 s5, s11, s5
	s_lshl_b32 s11, s5, 3
	s_sub_i32 s16, 0x100, s11
	s_min_i32 s16, s16, 8
	s_abs_i32 s17, s16
	v_cvt_f32_u32_e32 v0, s17
	s_sub_i32 s19, 0, s17
	s_mul_i32 s5, s5, s15
	s_sub_i32 s5, s4, s5
	v_rcp_iflag_f32_e32 v0, v0
	s_abs_i32 s18, s5
	s_xor_b32 s4, s5, s16
	s_ashr_i32 s4, s4, 31
	v_mul_f32_e32 v0, 0x4f7ffffe, v0
	v_cvt_u32_f32_e32 v0, v0
	s_nop 0
	v_readfirstlane_b32 s20, v0
	s_mul_i32 s19, s19, s20
	s_mul_hi_u32 s19, s20, s19
	s_add_i32 s20, s20, s19
	s_mul_hi_u32 s19, s18, s20
	s_mul_i32 s20, s19, s17
	s_sub_i32 s18, s18, s20
	s_add_i32 s20, s19, 1
	s_sub_i32 s21, s18, s17
	s_cmp_ge_u32 s18, s17
	s_cselect_b32 s19, s20, s19
	s_cselect_b32 s18, s21, s18
	s_add_i32 s20, s19, 1
	s_cmp_ge_u32 s18, s17
	s_cselect_b32 s17, s20, s19
	s_xor_b32 s17, s17, s4
	s_sub_i32 s4, s17, s4
	s_mul_i32 s16, s4, s16
	s_sub_i32 s5, s5, s16
	s_add_i32 s53, s5, s11
	s_mov_b64 s[16:17], -1
.LBB0_481:
	s_andn2_b64 vcc, exec, s[16:17]
	s_cbranch_vccnz .LBB0_543
	s_nop 0
	v_bfe_i32 v2, v9, 27, 1
	v_lshlrev_b32_e32 v0, 4, v9
	v_lshrrev_b32_e32 v2, 22, v2
	v_add_u32_e64 v2, v0, v2
	v_and_b32_e32 v2, 0xfffffc00, v2
	v_sub_u32_e32 v0, v0, v2
	v_ashrrev_i32_e32 v1, 31, v9
	v_lshrrev_b32_e32 v2, 4, v0
	v_lshrrev_b32_e32 v1, 26, v1
	v_bitop3_b32 v0, v2, v0, 32 bitop3:0x6c
	v_add_u32_e32 v1, v9, v1
	v_ashrrev_i32_e32 v3, 31, v0
	v_ashrrev_i32_e32 v1, 6, v1
	v_lshrrev_b32_e32 v3, 26, v3
	v_lshlrev_b32_e32 v2, 3, v1
	v_add_u32_e32 v3, v0, v3
	v_and_b32_e32 v2, -16, v2
	v_ashrrev_i32_e32 v4, 6, v3
	v_add_u32_e64 v199, v4, v2
	v_and_b32_e32 v2, 0xc0, v3
	v_sub_u32_e32 v0, v0, v2
	v_mov_b32_e32 v2, 1
	v_lshlrev_b32_e32 v1, 5, v1
	s_nop 0
	v_ashrrev_i16_sdwa v0, v2, sext(v0) dst_sel:DWORD dst_unused:UNUSED_PAD src0_sel:DWORD src1_sel:BYTE_0
	v_and_b32_e32 v4, 3, v4
	s_nop 0
	s_mov_b32 s5, 0x3fffe0
	v_and_b32_e32 v1, 32, v1
	s_nop 0
	v_bfe_i32 v0, v0, 0, 16
	v_and_or_b32 v4, v199, s5, v4
	s_lshl_b32 s5, s53, 8
	s_nop 0
	v_add_lshl_u32 v218, v1, v0, 1
	v_add_u32_e32 v0, s5, v199
	v_add_u32_e32 v219, 64, v199
	v_lshl_add_u32 v202, v0, 10, v218
	v_add_u32_e64 v0, s5, v219
	v_add_u32_e32 v235, 0x80, v199
	v_lshl_add_u32 v204, v0, 10, v218
	v_add_u32_e64 v0, s5, v235
	v_add_u32_e32 v236, 0xc0, v199
	s_ashr_i32 s22, s9, 6
	s_nop 0
	v_lshl_add_u32 v96, v0, 10, v218
	v_add_u32_e32 v0, s5, v236
	s_ashr_i32 s5, s4, 31
	s_ashr_i32 s23, s9, 8
	s_lshl_b32 s48, s22, 10
	s_lshl_b64 s[16:17], s[4:5], 18
	v_lshlrev_b32_e32 v2, 1, v199
	v_lshrrev_b32_e32 v3, 2, v199
	s_add_u32 s20, s6, s16
	v_and_b32_e32 v2, 24, v2
	v_and_b32_e32 v3, 4, v3
	s_addc_u32 s21, s7, s17
	s_add_i32 s49, s48, 0
	v_or3_b32 v2, v4, v3, v2
	s_add_i32 s56, s49, 0x10000
	s_add_i32 s57, s49, 0x12000
	v_lshl_add_u32 v194, v2, 10, v218
	s_mov_b32 m0, s56
	s_nop 0
	s_add_u32 s16, s20, 0x20000
	v_add_u32_e32 v196, 0x10000, v194
	global_load_lds_dwordx4 v194, s[20:21]
	s_mov_b32 m0, s57
	s_addc_u32 s17, s21, 0
	s_add_i32 s58, s49, 0x14000
	global_load_lds_dwordx4 v196, s[20:21]
	s_mov_b32 m0, s58
	s_nop 0
	s_add_i32 s59, s49, 0x16000
	v_writelane_b32 v255, s92, 51
	global_load_lds_dwordx4 v194, s[16:17]
	s_mov_b32 m0, s59
	s_nop 0
	v_writelane_b32 v255, s60, 52
	global_load_lds_dwordx4 v196, s[16:17]
	s_mov_b32 m0, s49
	s_nop 0
	s_add_i32 s60, s49, 0x2000
	global_load_lds_dwordx4 v202, s[78:79]
	s_mov_b32 m0, s60
	s_nop 0
	s_add_i32 s61, s49, 0x4000
	global_load_lds_dwordx4 v204, s[78:79]
	s_mov_b32 m0, s61
	s_nop 0
	s_add_i32 s64, s49, 0x6000
	v_lshl_add_u32 v206, v0, 10, v218
	global_load_lds_dwordx4 v96, s[78:79]
	s_mov_b32 m0, s64
	v_mov_b32_e32 v195, v97
	global_load_lds_dwordx4 v206, s[78:79]
	v_mov_b32_e32 v197, v97
	v_mov_b32_e32 v203, v97
	v_mov_b32_e64 v205, v97
	s_cmp_eq_u32 s23, 1
	s_mov_b32 s44, s93
	v_lshl_add_u64 v[6:7], s[20:21], 0, v[194:195]
	v_lshl_add_u64 v[4:5], s[20:21], 0, v[196:197]
	v_lshl_add_u64 v[0:1], s[78:79], 0, v[202:203]
	s_cselect_b64 s[16:17], -1, 0
	s_cmp_lg_u32 s23, 1
	v_lshl_add_u64 v[2:3], s[78:79], 0, v[204:205]
	s_cbranch_scc1 .LBB0_484
	s_barrier
.LBB0_484:
	v_lshrrev_b32_e32 v11, 4, v9
	s_xor_b64 s[18:19], s[2:3], -1
	v_bfe_u32 v11, v11, 1, 1
	s_lshl_b32 s2, s23, 13
	s_nop 0
	v_lshl_or_b32 v15, v11, 10, s2
	s_lshl_b32 s2, s22, 5
	s_nop 0
	s_and_b32 s5, s2, 0x60
	s_lshr_b32 s2, s5, 3
	v_or_b32_e32 v11, s2, v11
	s_mov_b64 s[2:3], 0x80
	s_add_i32 m0, s49, 0x18000
	v_lshl_add_u64 v[6:7], v[6:7], 0, s[2:3]
	s_waitcnt vmcnt(2)
	s_barrier
	global_load_lds_dwordx4 v[6:7], off
	v_lshl_add_u64 v[4:5], v[4:5], 0, s[2:3]
	s_add_i32 m0, s49, 0x1a000
	s_add_i32 s65, s49, 0x8000
	global_load_lds_dwordx4 v[4:5], off
	v_lshl_add_u64 v[0:1], v[0:1], 0, s[2:3]
	s_mov_b32 m0, s65
	s_nop 0
	s_add_i32 s92, s49, 0xa000
	global_load_lds_dwordx4 v[0:1], off
	v_lshl_add_u64 v[0:1], v[2:3], 0, s[2:3]
	s_add_u32 s2, s20, 0x20080
	s_mov_b32 m0, s92
	s_addc_u32 s3, s21, 0
	global_load_lds_dwordx4 v[0:1], off
	s_add_i32 m0, s49, 0x1c000
	v_lshl_add_u64 v[0:1], s[2:3], 0, v[194:195]
	global_load_lds_dwordx4 v[0:1], off
	v_lshl_add_u64 v[0:1], s[2:3], 0, v[196:197]
	s_add_i32 m0, s49, 0x1e000
	s_cmpk_lt_u32 s9, 0x100
	s_nop 0
	global_load_lds_dwordx4 v[0:1], off
	v_mul_f32_e32 v0, 0x4f7ffffe, v8
	v_cvt_u32_f32_e32 v0, v0
	s_cselect_b64 s[20:21], -1, 0
	s_sub_i32 s2, 0, s15
	v_and_b32_e32 v10, 15, v9
	v_readfirstlane_b32 s3, v0
	v_cvt_f32_u32_e32 v0, s40
	s_mul_i32 s2, s2, s3
	s_mul_hi_u32 s2, s3, s2
	s_add_i32 s2, s3, s2
	v_rcp_iflag_f32_e32 v0, v0
	v_lshlrev_b32_e32 v13, 1, v9
	s_nop 0
	v_writelane_b32 v254, s2, 12
	s_sub_i32 s2, 0, s40
	s_nop 0
	v_mul_f32_e32 v0, 0x4f7ffffe, v0
	v_cvt_u32_f32_e32 v0, v0
	s_nop 0
	v_bfe_u32 v12, v9, 4, 2
	v_lshl_or_b32 v203, s23, 6, v10
	v_and_b32_e32 v13, 32, v13
	v_readfirstlane_b32 s3, v0
	v_lshlrev_b32_e32 v10, 6, v10
	v_lshlrev_b32_e32 v9, 2, v9
	s_mul_i32 s2, s2, s3
	v_or_b32_e32 v14, v10, v13
	v_and_b32_e32 v9, 32, v9
	v_lshlrev_b32_e32 v11, 10, v11
	s_mul_hi_u32 s2, s3, s2
	s_nop 0
	v_bitop3_b32 v10, v10, v9, v13 bitop3:0x36
	v_bitop3_b32 v205, v11, v14, v9 bitop3:0xf6
	v_or_b32_e32 v13, 16, v14
	s_nop 0
	v_bitop3_b32 v14, v14, v9, 16 bitop3:0x36
	s_waitcnt vmcnt(6)
	s_add_i32 s47, s3, s2
	v_or_b32_e32 v10, v10, v15
	v_or_b32_e32 v14, v14, v15
	s_add_u32 s46, s70, 0xee00080
	s_mov_b32 s11, s97
	s_nop 0
	v_bitop3_b32 v237, v13, v11, v9 bitop3:0xde
	v_lshl_or_b32 v238, v12, 3, s5
	s_mov_b32 s93, 0
	s_addc_u32 s9, s71, 0
	v_add_u32_e32 v239, 0, v10
	v_add_u32_e32 v240, 0, v14
	v_mbcnt_lo_u32_b32 v0, -1, 0
	v_mbcnt_hi_u32_b32 v0, -1, v0
	v_and_b32_e32 v0, 16, v0
	v_xor_b32_e32 v239, v239, v0
	v_xor_b32_e32 v240, v240, v0
	v_xor_b32_e32 v205, v205, v0
	v_xor_b32_e32 v237, v237, v0
	s_nop 0
	v_add_u32_e32 v205, 0x10000, v205
	v_add_u32_e32 v237, 0x10000, v237
	v_mov_b32_e64 v241, v206
	v_mov_b32_e32 v242, v96
	s_mov_b32 s51, s24
	s_barrier
	s_waitcnt vmcnt(0)
	s_branch .LBB0_487

.LBB0_487:
	s_add_i32 s93, s93, 1
	s_mov_b64 s[2:3], -1
	s_and_b64 vcc, exec, s[42:43]
	s_cbranch_vccz .LBB0_490
	v_readlane_b32 s2, v254, 38
	v_readlane_b32 s22, v254, 3
	s_mul_i32 s2, s93, s2
	s_mul_hi_u32 s3, s93, s22
	s_add_i32 s3, s3, s2
	s_mul_i32 s2, s93, s22
	s_add_u32 s26, s2, s50
	s_nop 0
	v_readlane_b32 s2, v254, 39
	s_addc_u32 s27, s3, s2
	v_mov_b64_e32 v[0:1], s[10:11]
	v_cmp_ge_i64_e32 vcc, s[26:27], v[0:1]
	s_mov_b64 s[2:3], 0
	s_mov_b64 s[24:25], 0
	s_mov_b32 s22, s23
	s_mov_b32 s52, s5
	s_cbranch_vccnz .LBB0_490
	s_ashr_i32 s22, s26, 31
	s_lshr_b32 s22, s22, 29
	s_add_i32 s22, s26, s22
	s_ashr_i32 s24, s22, 3
	s_and_b32 s22, s22, -8
	s_sub_i32 s22, s26, s22
	s_lshr_b32 s25, s22, 31
	s_or_b32 s25, s51, s25
	s_mul_i32 s22, s25, s22
	s_add_i32 s22, s22, s24
	s_abs_i32 s25, s22
	s_nop 0
	v_readlane_b32 s26, v254, 12
	s_mul_hi_u32 s26, s25, s26
	s_mul_i32 s27, s26, s15
	s_sub_i32 s25, s25, s27
	s_ashr_i32 s24, s22, 31
	s_add_i32 s27, s26, 1
	s_sub_i32 s28, s25, s15
	s_cmp_ge_u32 s25, s15
	s_cselect_b32 s26, s27, s26
	s_cselect_b32 s25, s28, s25
	s_add_i32 s27, s26, 1
	s_cmp_ge_u32 s25, s15
	s_cselect_b32 s25, s27, s26
	s_xor_b32 s25, s25, s24
	s_sub_i32 s24, s25, s24
	s_lshl_b32 s25, s24, 3
	s_nop 0
	s_sub_i32 s26, 0x100, s25
	s_min_i32 s26, s26, 8
	s_abs_i32 s27, s26
	v_cvt_f32_u32_e32 v0, s27
	s_sub_i32 s29, 0, s27
	s_mul_i32 s24, s24, s15
	s_sub_i32 s22, s22, s24
	v_rcp_iflag_f32_e32 v0, v0
	s_abs_i32 s28, s22
	s_xor_b32 s24, s22, s26
	s_ashr_i32 s24, s24, 31
	v_mul_f32_e32 v0, 0x4f7ffffe, v0
	v_cvt_u32_f32_e32 v0, v0
	s_nop 0
	v_readfirstlane_b32 s30, v0
	s_mul_i32 s29, s29, s30
	s_mul_hi_u32 s29, s30, s29
	s_add_i32 s30, s30, s29
	s_mul_hi_u32 s29, s28, s30
	s_mul_i32 s30, s29, s27
	s_sub_i32 s28, s28, s30
	s_add_i32 s30, s29, 1
	s_sub_i32 s31, s28, s27
	s_cmp_ge_u32 s28, s27
	s_cselect_b32 s29, s30, s29
	s_cselect_b32 s28, s31, s28
	s_add_i32 s30, s29, 1
	s_cmp_ge_u32 s28, s27
	s_cselect_b32 s27, s30, s29
	s_xor_b32 s27, s27, s24
	s_sub_i32 s52, s27, s24
	s_mul_i32 s24, s52, s26
	s_sub_i32 s22, s22, s24
	s_add_i32 s22, s22, s25
	s_mov_b64 s[24:25], -1

.LBB0_494:
	s_nop 0
	v_cndmask_b32_e64 v0, 0, 1, s[24:25]
	v_cmp_ne_u32_e64 s[2:3], 1, v0
	s_andn2_b64 vcc, exec, s[24:25]
	v_mov_b32_e32 v210, v241
	v_mov_b32_e32 v208, v242
	v_mov_b32_e32 v243, v204
	v_mov_b32_e32 v224, v202
	s_cbranch_vccnz .LBB0_496
	s_lshl_b32 s5, s22, 8
	v_add_u32_e32 v0, s5, v199
	v_lshl_add_u32 v224, v0, 10, v218
	v_add_u32_e64 v0, s5, v219
	v_lshl_add_u32 v243, v0, 10, v218
	v_add_u32_e64 v0, s5, v235
	v_lshl_add_u32 v208, v0, 10, v218
	v_add_u32_e64 v0, s5, v236
	v_lshl_add_u32 v210, v0, 10, v218

.LBB0_497:
	s_cmpk_eq_i32 s26, 0x300
	s_cselect_b64 s[28:29], -1, 0
	s_add_i32 s23, 0, 0x10000
	s_add_i32 s30, 0, 0x14000
	ds_read_b128 v[8:11], v205
	ds_read_b128 v[12:15], v237
	ds_read_b128 v[24:27], v205 offset:2048
	ds_read_b128 v[28:31], v237 offset:2048
	ds_read_b128 v[0:3], v205 offset:16384
	ds_read_b128 v[4:7], v237 offset:16384
	ds_read_b128 v[16:19], v205 offset:18432
	ds_read_b128 v[20:23], v237 offset:18432
	s_add_i32 m0, s49, 0xc000
	s_add_u32 s30, s46, s26
	s_addc_u32 s31, s9, s27
	s_add_i32 s23, s49, 0xe000
	s_cmpk_lg_i32 s26, 0x300
	s_nop 0
	ds_read_b128 v[40:43], v239
	ds_read_b128 v[32:35], v239 offset:2048
	ds_read_b128 v[44:47], v240
	ds_read_b128 v[36:39], v240 offset:2048
	ds_read_b128 v[56:59], v239 offset:4096
	ds_read_b128 v[48:51], v239 offset:6144
	ds_read_b128 v[60:63], v240 offset:4096
	ds_read_b128 v[52:55], v240 offset:6144
	global_load_lds_dwordx4 v96, s[30:31]
	s_mov_b32 m0, s23
	s_nop 0
	global_load_lds_dwordx4 v206, s[30:31]
	s_waitcnt vmcnt(8)
	s_waitcnt lgkmcnt(0)
	s_barrier
	s_setprio 1
	s_waitcnt lgkmcnt(0)
	s_nop 0
	v_mfma_scale_f32_16x16x128_f8f6f4 v[190:193], v[8:15], v[40:47], v[190:193], v226, v225 op_sel_hi:[0,0,0]
	v_mfma_scale_f32_16x16x128_f8f6f4 v[186:189], v[24:31], v[40:47], v[186:189], v226, v225 op_sel_hi:[0,0,0]
	v_mfma_scale_f32_16x16x128_f8f6f4 v[174:177], v[8:15], v[32:39], v[174:177], v226, v225 op_sel_hi:[0,0,0]
	v_mfma_scale_f32_16x16x128_f8f6f4 v[170:173], v[24:31], v[32:39], v[170:173], v226, v225 op_sel_hi:[0,0,0]
	v_mfma_scale_f32_16x16x128_f8f6f4 v[158:161], v[8:15], v[56:63], v[158:161], v226, v225 op_sel_hi:[0,0,0]
	v_mfma_scale_f32_16x16x128_f8f6f4 v[154:157], v[24:31], v[56:63], v[154:157], v226, v225 op_sel_hi:[0,0,0]
	v_mfma_scale_f32_16x16x128_f8f6f4 v[142:145], v[8:15], v[48:55], v[142:145], v226, v225 op_sel_hi:[0,0,0]
	v_mfma_scale_f32_16x16x128_f8f6f4 v[138:141], v[24:31], v[48:55], v[138:141], v226, v225 op_sel_hi:[0,0,0]
	s_setprio 0
	s_setprio 1
	v_mfma_scale_f32_16x16x128_f8f6f4 v[182:185], v[0:7], v[40:47], v[182:185], v226, v225 op_sel_hi:[0,0,0]
	v_mfma_scale_f32_16x16x128_f8f6f4 v[178:181], v[16:23], v[40:47], v[178:181], v226, v225 op_sel_hi:[0,0,0]
	v_mfma_scale_f32_16x16x128_f8f6f4 v[166:169], v[0:7], v[32:39], v[166:169], v226, v225 op_sel_hi:[0,0,0]
	v_mfma_scale_f32_16x16x128_f8f6f4 v[162:165], v[16:23], v[32:39], v[162:165], v226, v225 op_sel_hi:[0,0,0]
	v_mfma_scale_f32_16x16x128_f8f6f4 v[150:153], v[0:7], v[56:63], v[150:153], v226, v225 op_sel_hi:[0,0,0]
	v_mfma_scale_f32_16x16x128_f8f6f4 v[146:149], v[16:23], v[56:63], v[146:149], v226, v225 op_sel_hi:[0,0,0]
	v_mfma_scale_f32_16x16x128_f8f6f4 v[134:137], v[0:7], v[48:55], v[134:137], v226, v225 op_sel_hi:[0,0,0]
	v_mfma_scale_f32_16x16x128_f8f6f4 v[130:133], v[16:23], v[48:55], v[130:133], v226, v225 op_sel_hi:[0,0,0]
	s_setprio 0
	s_barrier
	s_cbranch_scc1 .LBB0_499
	v_mov_b32_e32 v206, v210
	v_mov_b32_e32 v96, v208
	v_mov_b32_e32 v204, v243
	v_mov_b32_e32 v202, v224
	v_mov_b32_e32 v241, v210
	v_mov_b32_e32 v242, v208
	s_branch .LBB0_500
.LBB0_499:
.LBB0_500:
	s_and_b64 s[30:31], s[24:25], s[28:29]
	s_add_i32 s23, s5, 2
	s_and_b64 s[28:29], s[28:29], exec
	s_cselect_b32 s96, 0, s23
	s_and_b64 s[28:29], s[30:31], exec
	s_cselect_b32 s28, s52, s4
	s_ashr_i32 s29, s28, 31
	s_lshl_b64 s[30:31], s[96:97], 7
	s_or_b32 s96, s96, 1
	s_lshl_b64 s[34:35], s[28:29], 18
	s_lshl_b64 s[28:29], s[96:97], 7
	s_add_u32 s72, s6, s34
	s_addc_u32 s73, s7, s35
	s_add_u32 s34, s72, s30
	s_addc_u32 s35, s73, s31
	s_mov_b32 m0, s56
	ds_read_b128 v[56:59], v239 offset:16384
	ds_read_b128 v[60:63], v240 offset:16384
	ds_read_b128 v[48:51], v239 offset:18432
	ds_read_b128 v[52:55], v240 offset:18432
	ds_read_b128 v[40:43], v239 offset:20480
	ds_read_b128 v[44:47], v240 offset:20480
	ds_read_b128 v[32:35], v239 offset:22528
	ds_read_b128 v[36:39], v240 offset:22528
	global_load_lds_dwordx4 v194, s[34:35]
	s_mov_b32 m0, s57
	s_nop 0
	global_load_lds_dwordx4 v196, s[34:35]
	s_add_u32 s34, s34, 0x20000
	s_addc_u32 s35, s35, 0
	s_mov_b32 m0, s58
	s_add_u32 s30, s78, s30
	s_nop 0
	global_load_lds_dwordx4 v194, s[34:35]
	s_mov_b32 m0, s59
	s_addc_u32 s31, s79, s31
	global_load_lds_dwordx4 v196, s[34:35]
	s_mov_b32 m0, s49
	s_nop 0
	global_load_lds_dwordx4 v202, s[30:31]
	s_mov_b32 m0, s60
	s_nop 0
	global_load_lds_dwordx4 v204, s[30:31]
	s_waitcnt vmcnt(8)
	s_waitcnt lgkmcnt(0)
	s_barrier
	s_setprio 1
	s_waitcnt lgkmcnt(0)
	s_nop 0
	v_mfma_scale_f32_16x16x128_f8f6f4 v[126:129], v[8:15], v[56:63], v[126:129], v226, v225 op_sel_hi:[0,0,0]
	v_mfma_scale_f32_16x16x128_f8f6f4 v[122:125], v[24:31], v[56:63], v[122:125], v226, v225 op_sel_hi:[0,0,0]
	v_mfma_scale_f32_16x16x128_f8f6f4 v[110:113], v[8:15], v[48:55], v[110:113], v226, v225 op_sel_hi:[0,0,0]
	v_mfma_scale_f32_16x16x128_f8f6f4 v[106:109], v[24:31], v[48:55], v[106:109], v226, v225 op_sel_hi:[0,0,0]
	v_mfma_scale_f32_16x16x128_f8f6f4 v[92:95], v[8:15], v[40:47], v[92:95], v226, v225 op_sel_hi:[0,0,0]
	v_mfma_scale_f32_16x16x128_f8f6f4 v[88:91], v[24:31], v[40:47], v[88:91], v226, v225 op_sel_hi:[0,0,0]
	v_mfma_scale_f32_16x16x128_f8f6f4 v[76:79], v[8:15], v[32:39], v[76:79], v226, v225 op_sel_hi:[0,0,0]
	v_mfma_scale_f32_16x16x128_f8f6f4 v[72:75], v[24:31], v[32:39], v[72:75], v226, v225 op_sel_hi:[0,0,0]
	s_setprio 0
	s_setprio 1
	v_mfma_scale_f32_16x16x128_f8f6f4 v[118:121], v[0:7], v[56:63], v[118:121], v226, v225 op_sel_hi:[0,0,0]
	v_mfma_scale_f32_16x16x128_f8f6f4 v[114:117], v[16:23], v[56:63], v[114:117], v226, v225 op_sel_hi:[0,0,0]
	v_mfma_scale_f32_16x16x128_f8f6f4 v[102:105], v[0:7], v[48:55], v[102:105], v226, v225 op_sel_hi:[0,0,0]
	v_mfma_scale_f32_16x16x128_f8f6f4 v[98:101], v[16:23], v[48:55], v[98:101], v226, v225 op_sel_hi:[0,0,0]
	v_mfma_scale_f32_16x16x128_f8f6f4 v[84:87], v[0:7], v[40:47], v[84:87], v226, v225 op_sel_hi:[0,0,0]
	v_mfma_scale_f32_16x16x128_f8f6f4 v[80:83], v[16:23], v[40:47], v[80:83], v226, v225 op_sel_hi:[0,0,0]
	v_mfma_scale_f32_16x16x128_f8f6f4 v[68:71], v[0:7], v[32:39], v[68:71], v226, v225 op_sel_hi:[0,0,0]
	v_mfma_scale_f32_16x16x128_f8f6f4 v[64:67], v[16:23], v[32:39], v[64:67], v226, v225 op_sel_hi:[0,0,0]
	s_setprio 0
	s_barrier
	s_add_i32 s34, 0, 0x18000
	s_add_i32 s35, 0, 0x1c000
	ds_read_b128 v[0:3], v205 offset:32768
	ds_read_b128 v[4:7], v237 offset:32768
	ds_read_b128 v[8:11], v205 offset:34816
	ds_read_b128 v[12:15], v237 offset:34816
	ds_read_b128 v[16:19], v205 offset:49152
	ds_read_b128 v[20:23], v237 offset:49152
	ds_read_b128 v[24:27], v205 offset:51200
	ds_read_b128 v[28:31], v237 offset:51200
	s_mov_b32 m0, s61
	s_nop 0
	ds_read_b128 v[32:35], v239 offset:32768
	ds_read_b128 v[40:43], v239 offset:34816
	ds_read_b128 v[36:39], v240 offset:32768
	ds_read_b128 v[44:47], v240 offset:34816
	ds_read_b128 v[48:51], v239 offset:36864
	ds_read_b128 v[56:59], v239 offset:38912
	ds_read_b128 v[52:55], v240 offset:36864
	ds_read_b128 v[60:63], v240 offset:38912
	global_load_lds_dwordx4 v96, s[30:31]
	s_mov_b32 m0, s64
	s_nop 0
	global_load_lds_dwordx4 v206, s[30:31]
	s_waitcnt vmcnt(8)
	s_waitcnt lgkmcnt(0)
	s_barrier
	s_setprio 1
	s_waitcnt lgkmcnt(0)
	s_nop 0
	v_mfma_scale_f32_16x16x128_f8f6f4 v[190:193], v[0:7], v[32:39], v[190:193], v226, v225 op_sel_hi:[0,0,0]
	v_mfma_scale_f32_16x16x128_f8f6f4 v[186:189], v[8:15], v[32:39], v[186:189], v226, v225 op_sel_hi:[0,0,0]
	v_mfma_scale_f32_16x16x128_f8f6f4 v[174:177], v[0:7], v[40:47], v[174:177], v226, v225 op_sel_hi:[0,0,0]
	v_mfma_scale_f32_16x16x128_f8f6f4 v[170:173], v[8:15], v[40:47], v[170:173], v226, v225 op_sel_hi:[0,0,0]
	v_mfma_scale_f32_16x16x128_f8f6f4 v[158:161], v[0:7], v[48:55], v[158:161], v226, v225 op_sel_hi:[0,0,0]
	v_mfma_scale_f32_16x16x128_f8f6f4 v[154:157], v[8:15], v[48:55], v[154:157], v226, v225 op_sel_hi:[0,0,0]
	v_mfma_scale_f32_16x16x128_f8f6f4 v[142:145], v[0:7], v[56:63], v[142:145], v226, v225 op_sel_hi:[0,0,0]
	v_mfma_scale_f32_16x16x128_f8f6f4 v[138:141], v[8:15], v[56:63], v[138:141], v226, v225 op_sel_hi:[0,0,0]
	s_setprio 0
	s_setprio 1
	v_mfma_scale_f32_16x16x128_f8f6f4 v[182:185], v[16:23], v[32:39], v[182:185], v226, v225 op_sel_hi:[0,0,0]
	v_mfma_scale_f32_16x16x128_f8f6f4 v[178:181], v[24:31], v[32:39], v[178:181], v226, v225 op_sel_hi:[0,0,0]
	v_mfma_scale_f32_16x16x128_f8f6f4 v[166:169], v[16:23], v[40:47], v[166:169], v226, v225 op_sel_hi:[0,0,0]
	v_mfma_scale_f32_16x16x128_f8f6f4 v[162:165], v[24:31], v[40:47], v[162:165], v226, v225 op_sel_hi:[0,0,0]
	v_mfma_scale_f32_16x16x128_f8f6f4 v[150:153], v[16:23], v[48:55], v[150:153], v226, v225 op_sel_hi:[0,0,0]
	v_mfma_scale_f32_16x16x128_f8f6f4 v[146:149], v[24:31], v[48:55], v[146:149], v226, v225 op_sel_hi:[0,0,0]
	v_mfma_scale_f32_16x16x128_f8f6f4 v[134:137], v[16:23], v[56:63], v[134:137], v226, v225 op_sel_hi:[0,0,0]
	v_mfma_scale_f32_16x16x128_f8f6f4 v[130:133], v[24:31], v[56:63], v[130:133], v226, v225 op_sel_hi:[0,0,0]
	s_setprio 0
	s_barrier
	s_add_u32 s30, s72, s28
	s_addc_u32 s31, s73, s29
	s_add_i32 s34, s34, s48
	s_mov_b32 m0, s34
	ds_read_b128 v[32:35], v239 offset:49152
	ds_read_b128 v[40:43], v239 offset:51200
	ds_read_b128 v[36:39], v240 offset:49152
	ds_read_b128 v[44:47], v240 offset:51200
	ds_read_b128 v[48:51], v239 offset:53248
	ds_read_b128 v[56:59], v239 offset:55296
	ds_read_b128 v[52:55], v240 offset:53248
	ds_read_b128 v[60:63], v240 offset:55296
	global_load_lds_dwordx4 v194, s[30:31]
	s_add_i32 m0, s34, 0x2000
	s_add_i32 s34, s35, s48
	s_nop 0
	global_load_lds_dwordx4 v196, s[30:31]
	s_add_u32 s30, s30, 0x20000
	s_addc_u32 s31, s31, 0
	s_mov_b32 m0, s34
	s_nop 0
	s_nop 0
	global_load_lds_dwordx4 v194, s[30:31]
	s_add_i32 m0, s34, 0x2000
	s_add_u32 s28, s78, s28
	s_nop 0
	global_load_lds_dwordx4 v196, s[30:31]
	s_addc_u32 s29, s79, s29
	s_mov_b32 m0, s65
	s_nop 0
	s_nop 0
	global_load_lds_dwordx4 v202, s[28:29]
	s_mov_b32 m0, s92
	s_nop 0
	global_load_lds_dwordx4 v204, s[28:29]
	s_waitcnt vmcnt(8)
	s_waitcnt lgkmcnt(0)
	s_barrier
	s_setprio 1
	s_waitcnt lgkmcnt(0)
	s_nop 0
	v_mfma_scale_f32_16x16x128_f8f6f4 v[126:129], v[0:7], v[32:39], v[126:129], v226, v225 op_sel_hi:[0,0,0]
	v_mfma_scale_f32_16x16x128_f8f6f4 v[122:125], v[8:15], v[32:39], v[122:125], v226, v225 op_sel_hi:[0,0,0]
	v_mfma_scale_f32_16x16x128_f8f6f4 v[110:113], v[0:7], v[40:47], v[110:113], v226, v225 op_sel_hi:[0,0,0]
	v_mfma_scale_f32_16x16x128_f8f6f4 v[106:109], v[8:15], v[40:47], v[106:109], v226, v225 op_sel_hi:[0,0,0]
	v_mfma_scale_f32_16x16x128_f8f6f4 v[92:95], v[0:7], v[48:55], v[92:95], v226, v225 op_sel_hi:[0,0,0]
	v_mfma_scale_f32_16x16x128_f8f6f4 v[88:91], v[8:15], v[48:55], v[88:91], v226, v225 op_sel_hi:[0,0,0]
	v_mfma_scale_f32_16x16x128_f8f6f4 v[76:79], v[0:7], v[56:63], v[76:79], v226, v225 op_sel_hi:[0,0,0]
	v_mfma_scale_f32_16x16x128_f8f6f4 v[72:75], v[8:15], v[56:63], v[72:75], v226, v225 op_sel_hi:[0,0,0]
	s_setprio 0
	s_setprio 1
	v_mfma_scale_f32_16x16x128_f8f6f4 v[118:121], v[16:23], v[32:39], v[118:121], v226, v225 op_sel_hi:[0,0,0]
	v_mfma_scale_f32_16x16x128_f8f6f4 v[114:117], v[24:31], v[32:39], v[114:117], v226, v225 op_sel_hi:[0,0,0]
	v_mfma_scale_f32_16x16x128_f8f6f4 v[102:105], v[16:23], v[40:47], v[102:105], v226, v225 op_sel_hi:[0,0,0]
	v_mfma_scale_f32_16x16x128_f8f6f4 v[98:101], v[24:31], v[40:47], v[98:101], v226, v225 op_sel_hi:[0,0,0]
	v_mfma_scale_f32_16x16x128_f8f6f4 v[84:87], v[16:23], v[48:55], v[84:87], v226, v225 op_sel_hi:[0,0,0]
	v_mfma_scale_f32_16x16x128_f8f6f4 v[80:83], v[24:31], v[48:55], v[80:83], v226, v225 op_sel_hi:[0,0,0]
	v_mfma_scale_f32_16x16x128_f8f6f4 v[68:71], v[16:23], v[56:63], v[68:71], v226, v225 op_sel_hi:[0,0,0]
	v_mfma_scale_f32_16x16x128_f8f6f4 v[64:67], v[24:31], v[56:63], v[64:67], v226, v225 op_sel_hi:[0,0,0]
	s_setprio 0
	s_barrier
	s_add_u32 s26, s26, 0x100
	s_addc_u32 s27, s27, 0
	s_cmp_gt_u32 s5, 5
	s_cbranch_scc1 .LBB0_502
	s_mov_b32 s5, s23
	s_branch .LBB0_497

.LBB0_507:
	s_cmp_lt_i32 s4, s41
	v_mov_b32_e32 v0, s38
	s_cselect_b64 vcc, -1, 0
	v_cndmask_b32_e32 v0, 1.0, v0, vcc
	s_cmp_ge_i32 s4, s45
	s_cselect_b64 s[24:25], -1, 0
	s_cmp_lt_i32 s4, s45
	v_pk_mul_f32 v[6:7], v[0:1], v[192:193] op_sel_hi:[0,1]
	v_pk_mul_f32 v[10:11], v[0:1], v[190:191] op_sel_hi:[0,1]
	v_pk_mul_f32 v[8:9], v[0:1], v[188:189] op_sel_hi:[0,1]
	v_pk_mul_f32 v[12:13], v[0:1], v[186:187] op_sel_hi:[0,1]
	s_cbranch_scc1 .LBB0_509
	s_nop 0
	v_mul_f32_e32 v1, 0xbfb8aa3b, v10
	v_exp_f32_e64 v1, v1
	v_mul_f32_e32 v2, 0xbfb8aa3b, v12
	v_exp_f32_e64 v2, v2
	v_mul_f32_e32 v3, 0xbfb8aa3b, v13
	v_add_f32_e32 v1, 1.0, v1
	v_rcp_f32_e32 v10, v1
	v_mul_f32_e32 v1, 0xbfb8aa3b, v11
	v_exp_f32_e32 v1, v1
	v_exp_f32_e32 v3, v3
	v_add_f32_e32 v2, 1.0, v2
	v_rcp_f32_e32 v12, v2
	v_add_f32_e64 v1, 1.0, v1
	v_mul_f32_e32 v2, 0xbfb8aa3b, v6
	v_rcp_f32_e32 v11, v1
	v_add_f32_e32 v1, 1.0, v3
	v_exp_f32_e64 v2, v2
	v_mul_f32_e32 v3, 0xbfb8aa3b, v8
	v_exp_f32_e32 v3, v3
	v_rcp_f32_e32 v13, v1
	v_add_f32_e64 v1, 1.0, v2
	v_mul_f32_e32 v2, 0xbfb8aa3b, v7
	v_rcp_f32_e32 v6, v1
	v_add_f32_e32 v1, 1.0, v3
	v_exp_f32_e64 v2, v2
	v_mul_f32_e32 v3, 0xbfb8aa3b, v9
	v_exp_f32_e32 v3, v3
	v_rcp_f32_e32 v8, v1
	v_add_f32_e32 v1, 1.0, v2
	v_rcp_f32_e32 v7, v1
	v_add_f32_e32 v1, 1.0, v3
	v_rcp_f32_e32 v9, v1
.LBB0_509:
	v_add_u32_e64 v2, s5, v238
	v_lshl_add_u32 v16, s53, 8, v203
	v_ashrrev_i32_e32 v3, 31, v2
	s_nop 0
	v_lshl_add_u64 v[2:3], v[2:3], 1, s[26:27]
	v_mad_i64_i32 v[4:5], s[4:5], s14, v16, 0
	v_mov_b32_e64 v1, v0
	v_lshl_add_u64 v[4:5], v[4:5], 1, v[2:3]
	v_cvt_pk_bf16_f32 v10, v10, v11
	v_cvt_pk_bf16_f32 v11, v6, v7
	v_cvt_pk_bf16_f32 v12, v12, v13
	v_cvt_pk_bf16_f32 v13, v8, v9
	v_mov_b32_e32 v6, v0
	v_mov_b32_e32 v7, v0
	v_cndmask_b32_e64 v14, 0, 1, s[24:25]
	global_store_dwordx4 v[4:5], v[10:13], off
	v_pk_mul_f32 v[8:9], v[6:7], v[184:185]
	v_cmp_ne_u32_e64 s[4:5], 1, v14
	v_pk_mul_f32 v[12:13], v[0:1], v[182:183]
	v_pk_mul_f32 v[10:11], v[6:7], v[180:181]
	s_andn2_b64 vcc, exec, s[24:25]
	s_nop 0
	v_pk_mul_f32 v[14:15], v[0:1], v[178:179]
	s_cbranch_vccnz .LBB0_511
	s_nop 0
	v_mul_f32_e32 v12, 0xbfb8aa3b, v12
	v_mul_f32_e32 v14, 0xbfb8aa3b, v14
	v_mul_f32_e32 v13, 0xbfb8aa3b, v13
	v_mul_f32_e32 v15, 0xbfb8aa3b, v15
	v_mul_f32_e32 v8, 0xbfb8aa3b, v8
	v_mul_f32_e32 v10, 0xbfb8aa3b, v10
	v_mul_f32_e32 v9, 0xbfb8aa3b, v9
	v_mul_f32_e32 v11, 0xbfb8aa3b, v11
	v_exp_f32_e32 v12, v12
	v_exp_f32_e32 v14, v14
	v_exp_f32_e32 v13, v13
	v_exp_f32_e32 v15, v15
	v_exp_f32_e32 v8, v8
	v_exp_f32_e32 v10, v10
	v_exp_f32_e32 v9, v9
	v_exp_f32_e32 v11, v11
	v_add_f32_e32 v12, 1.0, v12
	v_add_f32_e32 v14, 1.0, v14
	v_add_f32_e32 v13, 1.0, v13
	v_add_f32_e32 v15, 1.0, v15
	v_add_f32_e32 v8, 1.0, v8
	v_add_f32_e32 v10, 1.0, v10
	v_add_f32_e32 v9, 1.0, v9
	v_add_f32_e32 v11, 1.0, v11
	v_rcp_f32_e32 v12, v12
	v_rcp_f32_e32 v14, v14
	v_rcp_f32_e32 v13, v13
	v_rcp_f32_e32 v15, v15
	v_rcp_f32_e32 v8, v8
	v_rcp_f32_e32 v10, v10
	v_rcp_f32_e32 v9, v9
	v_rcp_f32_e32 v11, v11
.LBB0_511:
	v_cvt_pk_bf16_f32 v12, v12, v13
	v_cvt_pk_bf16_f32 v13, v8, v9
	v_cvt_pk_bf16_f32 v14, v14, v15
	v_cvt_pk_bf16_f32 v15, v10, v11
	global_store_dwordx4 v[4:5], v[12:15], off offset:256
	v_pk_mul_f32 v[8:9], v[6:7], v[176:177]
	v_pk_mul_f32 v[10:11], v[0:1], v[174:175]
	v_pk_mul_f32 v[6:7], v[6:7], v[172:173]
	s_and_b64 vcc, exec, s[4:5]
	s_nop 0
	v_pk_mul_f32 v[12:13], v[0:1], v[170:171]
	s_cbranch_vccnz .LBB0_513
	s_nop 0
	v_mul_f32_e32 v4, 0xbfb8aa3b, v10
	v_exp_f32_e64 v4, v4
	v_mul_f32_e32 v5, 0xbfb8aa3b, v12
	v_exp_f32_e64 v5, v5
	v_mul_f32_e32 v6, 0xbfb8aa3b, v6
	v_add_f32_e32 v4, 1.0, v4
	v_rcp_f32_e32 v10, v4
	v_mul_f32_e32 v4, 0xbfb8aa3b, v11
	v_add_f32_e32 v5, 1.0, v5
	v_exp_f32_e32 v4, v4
	v_mul_f32_e32 v11, 0xbfb8aa3b, v13
	v_exp_f32_e32 v13, v11
	v_rcp_f32_e32 v12, v5
	v_mul_f32_e32 v5, 0xbfb8aa3b, v8
	v_exp_f32_e32 v5, v5
	v_exp_f32_e32 v6, v6
	v_add_f32_e32 v4, 1.0, v4
	v_rcp_f32_e32 v11, v4
	v_add_f32_e32 v4, 1.0, v13
	v_rcp_f32_e32 v13, v4
	v_add_f32_e64 v4, 1.0, v5
	v_mul_f32_e32 v5, 0xbfb8aa3b, v9
	v_rcp_f32_e32 v8, v4
	v_add_f32_e32 v4, 1.0, v6
	v_exp_f32_e64 v5, v5
	v_mul_f32_e32 v6, 0xbfb8aa3b, v7
	v_exp_f32_e32 v7, v6
	v_rcp_f32_e32 v6, v4
	v_add_f32_e32 v4, 1.0, v5
	v_rcp_f32_e32 v9, v4
	v_add_f32_e64 v4, 1.0, v7
	v_rcp_f32_e32 v7, v4
.LBB0_513:
	v_or_b32_e32 v4, 16, v16
	v_mad_i64_i32 v[4:5], s[24:25], s14, v4, 0
	v_lshl_add_u64 v[4:5], v[4:5], 1, v[2:3]
	v_cvt_pk_bf16_f32 v10, v10, v11
	v_cvt_pk_bf16_f32 v11, v8, v9
	v_cvt_pk_bf16_f32 v12, v12, v13
	v_cvt_pk_bf16_f32 v13, v6, v7
	v_mov_b32_e32 v6, v0
	v_mov_b32_e32 v7, v0
	global_store_dwordx4 v[4:5], v[10:13], off
	v_pk_mul_f32 v[8:9], v[6:7], v[168:169]
	s_and_b64 vcc, exec, s[4:5]
	s_nop 0
	v_pk_mul_f32 v[12:13], v[0:1], v[166:167]
	v_pk_mul_f32 v[10:11], v[6:7], v[164:165]
	v_pk_mul_f32 v[14:15], v[0:1], v[162:163]
	s_cbranch_vccnz .LBB0_515
	s_nop 0
	v_mul_f32_e32 v12, 0xbfb8aa3b, v12
	v_mul_f32_e32 v14, 0xbfb8aa3b, v14
	v_mul_f32_e32 v13, 0xbfb8aa3b, v13
	v_mul_f32_e32 v15, 0xbfb8aa3b, v15
	v_mul_f32_e32 v8, 0xbfb8aa3b, v8
	v_mul_f32_e32 v10, 0xbfb8aa3b, v10
	v_mul_f32_e32 v9, 0xbfb8aa3b, v9
	v_mul_f32_e32 v11, 0xbfb8aa3b, v11
	v_exp_f32_e32 v12, v12
	v_exp_f32_e32 v14, v14
	v_exp_f32_e32 v13, v13
	v_exp_f32_e32 v15, v15
	v_exp_f32_e32 v8, v8
	v_exp_f32_e32 v10, v10
	v_exp_f32_e32 v9, v9
	v_exp_f32_e32 v11, v11
	v_add_f32_e32 v12, 1.0, v12
	v_add_f32_e32 v14, 1.0, v14
	v_add_f32_e32 v13, 1.0, v13
	v_add_f32_e32 v15, 1.0, v15
	v_add_f32_e32 v8, 1.0, v8
	v_add_f32_e32 v10, 1.0, v10
	v_add_f32_e32 v9, 1.0, v9
	v_add_f32_e32 v11, 1.0, v11
	v_rcp_f32_e32 v12, v12
	v_rcp_f32_e32 v14, v14
	v_rcp_f32_e32 v13, v13
	v_rcp_f32_e32 v15, v15
	v_rcp_f32_e32 v8, v8
	v_rcp_f32_e32 v10, v10
	v_rcp_f32_e32 v9, v9
	v_rcp_f32_e32 v11, v11
.LBB0_515:
	v_cvt_pk_bf16_f32 v12, v12, v13
	v_cvt_pk_bf16_f32 v13, v8, v9
	v_cvt_pk_bf16_f32 v14, v14, v15
	v_cvt_pk_bf16_f32 v15, v10, v11
	global_store_dwordx4 v[4:5], v[12:15], off offset:256
	v_pk_mul_f32 v[8:9], v[6:7], v[160:161]
	v_pk_mul_f32 v[10:11], v[0:1], v[158:159]
	v_pk_mul_f32 v[6:7], v[6:7], v[156:157]
	s_and_b64 vcc, exec, s[4:5]
	s_nop 0
	v_pk_mul_f32 v[12:13], v[0:1], v[154:155]
	s_cbranch_vccnz .LBB0_517
	s_nop 0
	v_mul_f32_e32 v4, 0xbfb8aa3b, v10
	v_exp_f32_e64 v4, v4
	v_mul_f32_e32 v5, 0xbfb8aa3b, v12
	v_exp_f32_e64 v5, v5
	v_mul_f32_e32 v6, 0xbfb8aa3b, v6
	v_add_f32_e32 v4, 1.0, v4
	v_rcp_f32_e32 v10, v4
	v_mul_f32_e32 v4, 0xbfb8aa3b, v11
	v_add_f32_e32 v5, 1.0, v5
	v_exp_f32_e32 v4, v4
	v_mul_f32_e32 v11, 0xbfb8aa3b, v13
	v_exp_f32_e32 v13, v11
	v_rcp_f32_e32 v12, v5
	v_mul_f32_e32 v5, 0xbfb8aa3b, v8
	v_exp_f32_e32 v5, v5
	v_exp_f32_e32 v6, v6
	v_add_f32_e32 v4, 1.0, v4
	v_rcp_f32_e32 v11, v4
	v_add_f32_e32 v4, 1.0, v13
	v_rcp_f32_e32 v13, v4
	v_add_f32_e64 v4, 1.0, v5
	v_mul_f32_e32 v5, 0xbfb8aa3b, v9
	v_rcp_f32_e32 v8, v4
	v_add_f32_e32 v4, 1.0, v6
	v_exp_f32_e64 v5, v5
	v_mul_f32_e32 v6, 0xbfb8aa3b, v7
	v_exp_f32_e32 v7, v6
	v_rcp_f32_e32 v6, v4
	v_add_f32_e32 v4, 1.0, v5
	v_rcp_f32_e32 v9, v4
	v_add_f32_e64 v4, 1.0, v7
	v_rcp_f32_e32 v7, v4
.LBB0_517:
	v_or_b32_e32 v4, 32, v16
	v_mad_i64_i32 v[4:5], s[24:25], s14, v4, 0
	v_lshl_add_u64 v[4:5], v[4:5], 1, v[2:3]
	v_cvt_pk_bf16_f32 v10, v10, v11
	v_cvt_pk_bf16_f32 v11, v8, v9
	v_cvt_pk_bf16_f32 v12, v12, v13
	v_cvt_pk_bf16_f32 v13, v6, v7
	v_mov_b32_e32 v6, v0
	v_mov_b32_e32 v7, v0
	global_store_dwordx4 v[4:5], v[10:13], off
	v_pk_mul_f32 v[8:9], v[6:7], v[152:153]
	s_and_b64 vcc, exec, s[4:5]
	s_nop 0
	v_pk_mul_f32 v[12:13], v[0:1], v[150:151]
	v_pk_mul_f32 v[10:11], v[6:7], v[148:149]
	v_pk_mul_f32 v[14:15], v[0:1], v[146:147]
	s_cbranch_vccnz .LBB0_519
	s_nop 0
	v_mul_f32_e32 v12, 0xbfb8aa3b, v12
	v_mul_f32_e32 v14, 0xbfb8aa3b, v14
	v_mul_f32_e32 v13, 0xbfb8aa3b, v13
	v_mul_f32_e32 v15, 0xbfb8aa3b, v15
	v_mul_f32_e32 v8, 0xbfb8aa3b, v8
	v_mul_f32_e32 v10, 0xbfb8aa3b, v10
	v_mul_f32_e32 v9, 0xbfb8aa3b, v9
	v_mul_f32_e32 v11, 0xbfb8aa3b, v11
	v_exp_f32_e32 v12, v12
	v_exp_f32_e32 v14, v14
	v_exp_f32_e32 v13, v13
	v_exp_f32_e32 v15, v15
	v_exp_f32_e32 v8, v8
	v_exp_f32_e32 v10, v10
	v_exp_f32_e32 v9, v9
	v_exp_f32_e32 v11, v11
	v_add_f32_e32 v12, 1.0, v12
	v_add_f32_e32 v14, 1.0, v14
	v_add_f32_e32 v13, 1.0, v13
	v_add_f32_e32 v15, 1.0, v15
	v_add_f32_e32 v8, 1.0, v8
	v_add_f32_e32 v10, 1.0, v10
	v_add_f32_e32 v9, 1.0, v9
	v_add_f32_e32 v11, 1.0, v11
	v_rcp_f32_e32 v12, v12
	v_rcp_f32_e32 v14, v14
	v_rcp_f32_e32 v13, v13
	v_rcp_f32_e32 v15, v15
	v_rcp_f32_e32 v8, v8
	v_rcp_f32_e32 v10, v10
	v_rcp_f32_e32 v9, v9
	v_rcp_f32_e32 v11, v11
.LBB0_519:
	v_cvt_pk_bf16_f32 v12, v12, v13
	v_cvt_pk_bf16_f32 v13, v8, v9
	v_cvt_pk_bf16_f32 v14, v14, v15
	v_cvt_pk_bf16_f32 v15, v10, v11
	global_store_dwordx4 v[4:5], v[12:15], off offset:256
	v_pk_mul_f32 v[8:9], v[6:7], v[144:145]
	v_pk_mul_f32 v[10:11], v[0:1], v[142:143]
	v_pk_mul_f32 v[6:7], v[6:7], v[140:141]
	s_and_b64 vcc, exec, s[4:5]
	s_nop 0
	v_pk_mul_f32 v[12:13], v[0:1], v[138:139]
	s_cbranch_vccnz .LBB0_521
	s_nop 0
	v_mul_f32_e32 v4, 0xbfb8aa3b, v10
	v_exp_f32_e64 v4, v4
	v_mul_f32_e32 v5, 0xbfb8aa3b, v12
	v_exp_f32_e64 v5, v5
	v_mul_f32_e32 v6, 0xbfb8aa3b, v6
	v_add_f32_e32 v4, 1.0, v4
	v_rcp_f32_e32 v10, v4
	v_mul_f32_e32 v4, 0xbfb8aa3b, v11
	v_add_f32_e32 v5, 1.0, v5
	v_exp_f32_e32 v4, v4
	v_mul_f32_e32 v11, 0xbfb8aa3b, v13
	v_exp_f32_e32 v13, v11
	v_rcp_f32_e32 v12, v5
	v_mul_f32_e32 v5, 0xbfb8aa3b, v8
	v_exp_f32_e32 v5, v5
	v_exp_f32_e32 v6, v6
	v_add_f32_e32 v4, 1.0, v4
	v_rcp_f32_e32 v11, v4
	v_add_f32_e32 v4, 1.0, v13
	v_rcp_f32_e32 v13, v4
	v_add_f32_e64 v4, 1.0, v5
	v_mul_f32_e32 v5, 0xbfb8aa3b, v9
	v_rcp_f32_e32 v8, v4
	v_add_f32_e32 v4, 1.0, v6
	v_exp_f32_e64 v5, v5
	v_mul_f32_e32 v6, 0xbfb8aa3b, v7
	v_exp_f32_e32 v7, v6
	v_rcp_f32_e32 v6, v4
	v_add_f32_e32 v4, 1.0, v5
	v_rcp_f32_e32 v9, v4
	v_add_f32_e64 v4, 1.0, v7
	v_rcp_f32_e32 v7, v4
.LBB0_521:
	v_or_b32_e32 v4, 48, v16
	v_mad_i64_i32 v[4:5], s[24:25], s14, v4, 0
	v_lshl_add_u64 v[4:5], v[4:5], 1, v[2:3]
	v_cvt_pk_bf16_f32 v10, v10, v11
	v_cvt_pk_bf16_f32 v11, v8, v9
	v_cvt_pk_bf16_f32 v12, v12, v13
	v_cvt_pk_bf16_f32 v13, v6, v7
	v_mov_b32_e32 v6, v0
	v_mov_b32_e32 v7, v0
	global_store_dwordx4 v[4:5], v[10:13], off
	v_pk_mul_f32 v[8:9], v[6:7], v[136:137]
	s_and_b64 vcc, exec, s[4:5]
	s_nop 0
	v_pk_mul_f32 v[12:13], v[0:1], v[134:135]
	v_pk_mul_f32 v[10:11], v[6:7], v[132:133]
	v_pk_mul_f32 v[14:15], v[0:1], v[130:131]
	s_cbranch_vccnz .LBB0_523
	s_nop 0
	v_mul_f32_e32 v12, 0xbfb8aa3b, v12
	v_mul_f32_e32 v14, 0xbfb8aa3b, v14
	v_mul_f32_e32 v13, 0xbfb8aa3b, v13
	v_mul_f32_e32 v15, 0xbfb8aa3b, v15
	v_mul_f32_e32 v8, 0xbfb8aa3b, v8
	v_mul_f32_e32 v10, 0xbfb8aa3b, v10
	v_mul_f32_e32 v9, 0xbfb8aa3b, v9
	v_mul_f32_e32 v11, 0xbfb8aa3b, v11
	v_exp_f32_e32 v12, v12
	v_exp_f32_e32 v14, v14
	v_exp_f32_e32 v13, v13
	v_exp_f32_e32 v15, v15
	v_exp_f32_e32 v8, v8
	v_exp_f32_e32 v10, v10
	v_exp_f32_e32 v9, v9
	v_exp_f32_e32 v11, v11
	v_add_f32_e32 v12, 1.0, v12
	v_add_f32_e32 v14, 1.0, v14
	v_add_f32_e32 v13, 1.0, v13
	v_add_f32_e32 v15, 1.0, v15
	v_add_f32_e32 v8, 1.0, v8
	v_add_f32_e32 v10, 1.0, v10
	v_add_f32_e32 v9, 1.0, v9
	v_add_f32_e32 v11, 1.0, v11
	v_rcp_f32_e32 v12, v12
	v_rcp_f32_e32 v14, v14
	v_rcp_f32_e32 v13, v13
	v_rcp_f32_e32 v15, v15
	v_rcp_f32_e32 v8, v8
	v_rcp_f32_e32 v10, v10
	v_rcp_f32_e32 v9, v9
	v_rcp_f32_e32 v11, v11
.LBB0_523:
	v_cvt_pk_bf16_f32 v12, v12, v13
	v_cvt_pk_bf16_f32 v13, v8, v9
	v_cvt_pk_bf16_f32 v14, v14, v15
	v_cvt_pk_bf16_f32 v15, v10, v11
	global_store_dwordx4 v[4:5], v[12:15], off offset:256
	v_pk_mul_f32 v[8:9], v[6:7], v[128:129]
	v_pk_mul_f32 v[10:11], v[0:1], v[126:127]
	v_pk_mul_f32 v[6:7], v[6:7], v[124:125]
	s_and_b64 vcc, exec, s[4:5]
	s_nop 0
	v_pk_mul_f32 v[12:13], v[0:1], v[122:123]
	s_cbranch_vccnz .LBB0_525
	s_nop 0
	v_mul_f32_e32 v4, 0xbfb8aa3b, v10
	v_exp_f32_e64 v4, v4
	v_mul_f32_e32 v5, 0xbfb8aa3b, v12
	v_exp_f32_e64 v5, v5
	v_mul_f32_e32 v6, 0xbfb8aa3b, v6
	v_add_f32_e32 v4, 1.0, v4
	v_rcp_f32_e32 v10, v4
	v_mul_f32_e32 v4, 0xbfb8aa3b, v11
	v_add_f32_e32 v5, 1.0, v5
	v_exp_f32_e32 v4, v4
	v_mul_f32_e32 v11, 0xbfb8aa3b, v13
	v_exp_f32_e32 v13, v11
	v_rcp_f32_e32 v12, v5
	v_mul_f32_e32 v5, 0xbfb8aa3b, v8
	v_exp_f32_e32 v5, v5
	v_exp_f32_e32 v6, v6
	v_add_f32_e32 v4, 1.0, v4
	v_rcp_f32_e32 v11, v4
	v_add_f32_e32 v4, 1.0, v13
	v_rcp_f32_e32 v13, v4
	v_add_f32_e64 v4, 1.0, v5
	v_mul_f32_e32 v5, 0xbfb8aa3b, v9
	v_rcp_f32_e32 v8, v4
	v_add_f32_e32 v4, 1.0, v6
	v_exp_f32_e64 v5, v5
	v_mul_f32_e32 v6, 0xbfb8aa3b, v7
	v_exp_f32_e32 v7, v6
	v_rcp_f32_e32 v6, v4
	v_add_f32_e32 v4, 1.0, v5
	v_rcp_f32_e32 v9, v4
	v_add_f32_e32 v4, 1.0, v7
	v_rcp_f32_e32 v7, v4
.LBB0_525:
	v_add_u32_e32 v4, 0x80, v16
	v_mad_i64_i32 v[4:5], s[24:25], s14, v4, 0
	v_lshl_add_u64 v[4:5], v[4:5], 1, v[2:3]
	v_cvt_pk_bf16_f32 v10, v10, v11
	v_cvt_pk_bf16_f32 v11, v8, v9
	v_cvt_pk_bf16_f32 v12, v12, v13
	v_cvt_pk_bf16_f32 v13, v6, v7
	v_mov_b32_e32 v6, v0
	v_mov_b32_e32 v7, v0
	global_store_dwordx4 v[4:5], v[10:13], off
	v_pk_mul_f32 v[8:9], v[6:7], v[120:121]
	s_and_b64 vcc, exec, s[4:5]
	s_nop 0
	v_pk_mul_f32 v[12:13], v[0:1], v[118:119]
	v_pk_mul_f32 v[10:11], v[6:7], v[116:117]
	v_pk_mul_f32 v[14:15], v[0:1], v[114:115]
	s_cbranch_vccnz .LBB0_527
	s_nop 0
	v_mul_f32_e32 v12, 0xbfb8aa3b, v12
	v_mul_f32_e32 v14, 0xbfb8aa3b, v14
	v_mul_f32_e32 v13, 0xbfb8aa3b, v13
	v_mul_f32_e32 v15, 0xbfb8aa3b, v15
	v_mul_f32_e32 v8, 0xbfb8aa3b, v8
	v_mul_f32_e32 v10, 0xbfb8aa3b, v10
	v_mul_f32_e32 v9, 0xbfb8aa3b, v9
	v_mul_f32_e32 v11, 0xbfb8aa3b, v11
	v_exp_f32_e32 v12, v12
	v_exp_f32_e32 v14, v14
	v_exp_f32_e32 v13, v13
	v_exp_f32_e32 v15, v15
	v_exp_f32_e32 v8, v8
	v_exp_f32_e32 v10, v10
	v_exp_f32_e32 v9, v9
	v_exp_f32_e32 v11, v11
	v_add_f32_e32 v12, 1.0, v12
	v_add_f32_e32 v14, 1.0, v14
	v_add_f32_e32 v13, 1.0, v13
	v_add_f32_e32 v15, 1.0, v15
	v_add_f32_e32 v8, 1.0, v8
	v_add_f32_e32 v10, 1.0, v10
	v_add_f32_e32 v9, 1.0, v9
	v_add_f32_e32 v11, 1.0, v11
	v_rcp_f32_e32 v12, v12
	v_rcp_f32_e32 v14, v14
	v_rcp_f32_e32 v13, v13
	v_rcp_f32_e32 v15, v15
	v_rcp_f32_e32 v8, v8
	v_rcp_f32_e32 v10, v10
	v_rcp_f32_e32 v9, v9
	v_rcp_f32_e32 v11, v11
.LBB0_527:
	v_cvt_pk_bf16_f32 v12, v12, v13
	v_cvt_pk_bf16_f32 v13, v8, v9
	v_cvt_pk_bf16_f32 v14, v14, v15
	v_cvt_pk_bf16_f32 v15, v10, v11
	global_store_dwordx4 v[4:5], v[12:15], off offset:256
	v_pk_mul_f32 v[8:9], v[6:7], v[112:113]
	v_pk_mul_f32 v[10:11], v[0:1], v[110:111]
	v_pk_mul_f32 v[6:7], v[6:7], v[108:109]
	s_and_b64 vcc, exec, s[4:5]
	s_nop 0
	v_pk_mul_f32 v[12:13], v[0:1], v[106:107]
	s_cbranch_vccnz .LBB0_529
	s_nop 0
	v_mul_f32_e32 v4, 0xbfb8aa3b, v10
	v_exp_f32_e64 v4, v4
	v_mul_f32_e32 v5, 0xbfb8aa3b, v12
	v_exp_f32_e64 v5, v5
	v_mul_f32_e32 v6, 0xbfb8aa3b, v6
	v_add_f32_e32 v4, 1.0, v4
	v_rcp_f32_e32 v10, v4
	v_mul_f32_e32 v4, 0xbfb8aa3b, v11
	v_add_f32_e32 v5, 1.0, v5
	v_exp_f32_e32 v4, v4
	v_mul_f32_e32 v11, 0xbfb8aa3b, v13
	v_exp_f32_e32 v13, v11
	v_rcp_f32_e32 v12, v5
	v_mul_f32_e32 v5, 0xbfb8aa3b, v8
	v_exp_f32_e32 v5, v5
	v_exp_f32_e32 v6, v6
	v_add_f32_e32 v4, 1.0, v4
	v_rcp_f32_e32 v11, v4
	v_add_f32_e32 v4, 1.0, v13
	v_rcp_f32_e32 v13, v4
	v_add_f32_e64 v4, 1.0, v5
	v_mul_f32_e32 v5, 0xbfb8aa3b, v9
	v_rcp_f32_e32 v8, v4
	v_add_f32_e32 v4, 1.0, v6
	v_exp_f32_e64 v5, v5
	v_mul_f32_e32 v6, 0xbfb8aa3b, v7
	v_exp_f32_e32 v7, v6
	v_rcp_f32_e32 v6, v4
	v_add_f32_e32 v4, 1.0, v5
	v_rcp_f32_e32 v9, v4
	v_add_f32_e32 v4, 1.0, v7
	v_rcp_f32_e32 v7, v4
.LBB0_529:
	v_add_u32_e32 v4, 0x90, v16
	v_mad_i64_i32 v[4:5], s[24:25], s14, v4, 0
	v_lshl_add_u64 v[4:5], v[4:5], 1, v[2:3]
	v_cvt_pk_bf16_f32 v10, v10, v11
	v_cvt_pk_bf16_f32 v11, v8, v9
	v_cvt_pk_bf16_f32 v12, v12, v13
	v_cvt_pk_bf16_f32 v13, v6, v7
	v_mov_b32_e32 v6, v0
	v_mov_b32_e32 v7, v0
	global_store_dwordx4 v[4:5], v[10:13], off
	v_pk_mul_f32 v[8:9], v[6:7], v[104:105]
	s_and_b64 vcc, exec, s[4:5]
	s_nop 0
	v_pk_mul_f32 v[12:13], v[0:1], v[102:103]
	v_pk_mul_f32 v[10:11], v[6:7], v[100:101]
	v_pk_mul_f32 v[14:15], v[0:1], v[98:99]
	s_cbranch_vccnz .LBB0_531
	s_nop 0
	v_mul_f32_e32 v12, 0xbfb8aa3b, v12
	v_mul_f32_e32 v14, 0xbfb8aa3b, v14
	v_mul_f32_e32 v13, 0xbfb8aa3b, v13
	v_mul_f32_e32 v15, 0xbfb8aa3b, v15
	v_mul_f32_e32 v8, 0xbfb8aa3b, v8
	v_mul_f32_e32 v10, 0xbfb8aa3b, v10
	v_mul_f32_e32 v9, 0xbfb8aa3b, v9
	v_mul_f32_e32 v11, 0xbfb8aa3b, v11
	v_exp_f32_e32 v12, v12
	v_exp_f32_e32 v14, v14
	v_exp_f32_e32 v13, v13
	v_exp_f32_e32 v15, v15
	v_exp_f32_e32 v8, v8
	v_exp_f32_e32 v10, v10
	v_exp_f32_e32 v9, v9
	v_exp_f32_e32 v11, v11
	v_add_f32_e32 v12, 1.0, v12
	v_add_f32_e32 v14, 1.0, v14
	v_add_f32_e32 v13, 1.0, v13
	v_add_f32_e32 v15, 1.0, v15
	v_add_f32_e32 v8, 1.0, v8
	v_add_f32_e32 v10, 1.0, v10
	v_add_f32_e32 v9, 1.0, v9
	v_add_f32_e32 v11, 1.0, v11
	v_rcp_f32_e32 v12, v12
	v_rcp_f32_e32 v14, v14
	v_rcp_f32_e32 v13, v13
	v_rcp_f32_e32 v15, v15
	v_rcp_f32_e32 v8, v8
	v_rcp_f32_e32 v10, v10
	v_rcp_f32_e32 v9, v9
	v_rcp_f32_e32 v11, v11
.LBB0_531:
	v_cvt_pk_bf16_f32 v12, v12, v13
	v_cvt_pk_bf16_f32 v13, v8, v9
	v_cvt_pk_bf16_f32 v14, v14, v15
	v_cvt_pk_bf16_f32 v15, v10, v11
	global_store_dwordx4 v[4:5], v[12:15], off offset:256
	v_pk_mul_f32 v[8:9], v[6:7], v[94:95]
	v_pk_mul_f32 v[10:11], v[0:1], v[92:93]
	v_pk_mul_f32 v[6:7], v[6:7], v[90:91]
	s_and_b64 vcc, exec, s[4:5]
	s_nop 0
	v_pk_mul_f32 v[12:13], v[0:1], v[88:89]
	s_cbranch_vccnz .LBB0_533
	s_nop 0
	v_mul_f32_e32 v4, 0xbfb8aa3b, v10
	v_exp_f32_e64 v4, v4
	v_mul_f32_e32 v5, 0xbfb8aa3b, v12
	v_exp_f32_e64 v5, v5
	v_mul_f32_e32 v6, 0xbfb8aa3b, v6
	v_add_f32_e32 v4, 1.0, v4
	v_rcp_f32_e32 v10, v4
	v_mul_f32_e32 v4, 0xbfb8aa3b, v11
	v_add_f32_e32 v5, 1.0, v5
	v_exp_f32_e32 v4, v4
	v_mul_f32_e32 v11, 0xbfb8aa3b, v13
	v_exp_f32_e32 v13, v11
	v_rcp_f32_e32 v12, v5
	v_mul_f32_e32 v5, 0xbfb8aa3b, v8
	v_exp_f32_e32 v5, v5
	v_exp_f32_e32 v6, v6
	v_add_f32_e32 v4, 1.0, v4
	v_rcp_f32_e32 v11, v4
	v_add_f32_e32 v4, 1.0, v13
	v_rcp_f32_e32 v13, v4
	v_add_f32_e64 v4, 1.0, v5
	v_mul_f32_e32 v5, 0xbfb8aa3b, v9
	v_rcp_f32_e32 v8, v4
	v_add_f32_e32 v4, 1.0, v6
	v_exp_f32_e64 v5, v5
	v_mul_f32_e32 v6, 0xbfb8aa3b, v7
	v_exp_f32_e32 v7, v6
	v_rcp_f32_e32 v6, v4
	v_add_f32_e32 v4, 1.0, v5
	v_rcp_f32_e32 v9, v4
	v_add_f32_e32 v4, 1.0, v7
	v_rcp_f32_e32 v7, v4
.LBB0_533:
	v_add_u32_e32 v4, 0xa0, v16
	v_mad_i64_i32 v[4:5], s[24:25], s14, v4, 0
	v_lshl_add_u64 v[4:5], v[4:5], 1, v[2:3]
	v_cvt_pk_bf16_f32 v10, v10, v11
	v_cvt_pk_bf16_f32 v11, v8, v9
	v_cvt_pk_bf16_f32 v12, v12, v13
	v_cvt_pk_bf16_f32 v13, v6, v7
	v_mov_b32_e32 v6, v0
	v_mov_b32_e32 v7, v0
	global_store_dwordx4 v[4:5], v[10:13], off
	v_pk_mul_f32 v[8:9], v[6:7], v[86:87]
	s_and_b64 vcc, exec, s[4:5]
	s_nop 0
	v_pk_mul_f32 v[12:13], v[0:1], v[84:85]
	v_pk_mul_f32 v[10:11], v[6:7], v[82:83]
	v_pk_mul_f32 v[14:15], v[0:1], v[80:81]
	s_cbranch_vccnz .LBB0_535
	s_nop 0
	v_mul_f32_e32 v12, 0xbfb8aa3b, v12
	v_mul_f32_e32 v14, 0xbfb8aa3b, v14
	v_mul_f32_e32 v13, 0xbfb8aa3b, v13
	v_mul_f32_e32 v15, 0xbfb8aa3b, v15
	v_mul_f32_e32 v8, 0xbfb8aa3b, v8
	v_mul_f32_e32 v10, 0xbfb8aa3b, v10
	v_mul_f32_e32 v9, 0xbfb8aa3b, v9
	v_mul_f32_e32 v11, 0xbfb8aa3b, v11
	v_exp_f32_e32 v12, v12
	v_exp_f32_e32 v14, v14
	v_exp_f32_e32 v13, v13
	v_exp_f32_e32 v15, v15
	v_exp_f32_e32 v8, v8
	v_exp_f32_e32 v10, v10
	v_exp_f32_e32 v9, v9
	v_exp_f32_e32 v11, v11
	v_add_f32_e32 v12, 1.0, v12
	v_add_f32_e32 v14, 1.0, v14
	v_add_f32_e32 v13, 1.0, v13
	v_add_f32_e32 v15, 1.0, v15
	v_add_f32_e32 v8, 1.0, v8
	v_add_f32_e32 v10, 1.0, v10
	v_add_f32_e32 v9, 1.0, v9
	v_add_f32_e32 v11, 1.0, v11
	v_rcp_f32_e32 v12, v12
	v_rcp_f32_e32 v14, v14
	v_rcp_f32_e32 v13, v13
	v_rcp_f32_e32 v15, v15
	v_rcp_f32_e32 v8, v8
	v_rcp_f32_e32 v10, v10
	v_rcp_f32_e32 v9, v9
	v_rcp_f32_e32 v11, v11
.LBB0_535:
	v_cvt_pk_bf16_f32 v12, v12, v13
	v_cvt_pk_bf16_f32 v13, v8, v9
	v_cvt_pk_bf16_f32 v14, v14, v15
	v_cvt_pk_bf16_f32 v15, v10, v11
	global_store_dwordx4 v[4:5], v[12:15], off offset:256
	v_pk_mul_f32 v[4:5], v[6:7], v[78:79]
	v_pk_mul_f32 v[8:9], v[0:1], v[76:77]
	v_pk_mul_f32 v[6:7], v[6:7], v[74:75]
	s_and_b64 vcc, exec, s[4:5]
	s_nop 0
	v_pk_mul_f32 v[10:11], v[0:1], v[72:73]
	s_cbranch_vccnz .LBB0_537
	s_nop 0
	v_mul_f32_e32 v8, 0xbfb8aa3b, v8
	v_mul_f32_e32 v10, 0xbfb8aa3b, v10
	v_mul_f32_e32 v9, 0xbfb8aa3b, v9
	v_mul_f32_e32 v11, 0xbfb8aa3b, v11
	v_mul_f32_e32 v4, 0xbfb8aa3b, v4
	v_mul_f32_e32 v6, 0xbfb8aa3b, v6
	v_mul_f32_e32 v5, 0xbfb8aa3b, v5
	v_mul_f32_e32 v7, 0xbfb8aa3b, v7
	v_exp_f32_e32 v8, v8
	v_exp_f32_e32 v10, v10
	v_exp_f32_e32 v9, v9
	v_exp_f32_e32 v11, v11
	v_exp_f32_e32 v4, v4
	v_exp_f32_e32 v6, v6
	v_exp_f32_e32 v5, v5
	v_exp_f32_e32 v7, v7
	v_add_f32_e32 v8, 1.0, v8
	v_add_f32_e32 v10, 1.0, v10
	v_add_f32_e32 v9, 1.0, v9
	v_add_f32_e32 v11, 1.0, v11
	v_add_f32_e32 v4, 1.0, v4
	v_add_f32_e32 v6, 1.0, v6
	v_add_f32_e32 v5, 1.0, v5
	v_add_f32_e32 v7, 1.0, v7
	v_rcp_f32_e32 v8, v8
	v_rcp_f32_e32 v10, v10
	v_rcp_f32_e32 v9, v9
	v_rcp_f32_e32 v11, v11
	v_rcp_f32_e32 v4, v4
	v_rcp_f32_e32 v6, v6
	v_rcp_f32_e32 v5, v5
	v_rcp_f32_e32 v7, v7
.LBB0_537:
	v_add_u32_e32 v12, 0xb0, v16
	v_mad_i64_i32 v[12:13], s[24:25], s14, v12, 0
	v_lshl_add_u64 v[2:3], v[12:13], 1, v[2:3]
	v_cvt_pk_bf16_f32 v8, v8, v9
	v_cvt_pk_bf16_f32 v9, v4, v5
	v_cvt_pk_bf16_f32 v10, v10, v11
	v_cvt_pk_bf16_f32 v11, v6, v7
	v_mov_b32_e32 v6, v0
	v_mov_b32_e32 v7, v0
	global_store_dwordx4 v[2:3], v[8:11], off
	v_pk_mul_f32 v[4:5], v[6:7], v[70:71]
	v_pk_mul_f32 v[6:7], v[6:7], v[66:67]
	v_pk_mul_f32 v[8:9], v[0:1], v[68:69]
	s_and_b64 vcc, exec, s[4:5]
	s_nop 0
	v_pk_mul_f32 v[0:1], v[0:1], v[64:65]
	s_cbranch_vccnz .LBB0_539
	s_nop 0
	v_mul_f32_e32 v8, 0xbfb8aa3b, v8
	v_mul_f32_e32 v0, 0xbfb8aa3b, v0
	v_mul_f32_e32 v9, 0xbfb8aa3b, v9
	v_mul_f32_e32 v1, 0xbfb8aa3b, v1
	v_mul_f32_e32 v4, 0xbfb8aa3b, v4
	v_mul_f32_e32 v6, 0xbfb8aa3b, v6
	v_mul_f32_e32 v5, 0xbfb8aa3b, v5
	v_mul_f32_e32 v7, 0xbfb8aa3b, v7
	v_exp_f32_e32 v8, v8
	v_exp_f32_e32 v0, v0
	v_exp_f32_e32 v9, v9
	v_exp_f32_e32 v1, v1
	v_exp_f32_e32 v4, v4
	v_exp_f32_e32 v6, v6
	v_exp_f32_e32 v5, v5
	v_exp_f32_e32 v7, v7
	v_add_f32_e32 v8, 1.0, v8
	v_add_f32_e32 v0, 1.0, v0
	v_add_f32_e32 v9, 1.0, v9
	v_add_f32_e32 v1, 1.0, v1
	v_add_f32_e32 v4, 1.0, v4
	v_add_f32_e32 v6, 1.0, v6
	v_add_f32_e32 v5, 1.0, v5
	v_add_f32_e32 v7, 1.0, v7
	v_rcp_f32_e32 v8, v8
	v_rcp_f32_e32 v0, v0
	v_rcp_f32_e32 v9, v9
	v_rcp_f32_e32 v1, v1
	v_rcp_f32_e32 v4, v4
	v_rcp_f32_e32 v6, v6
	v_rcp_f32_e32 v5, v5
	v_rcp_f32_e32 v7, v7

.LBB0_543:
	v_readlane_b32 s2, v254, 5
	v_readlane_b32 s3, v254, 6
	s_cmp_ge_i32 s89, s3
	s_cbranch_scc1 .LBB0_609
	v_readlane_b32 s4, v254, 44
	v_readlane_b32 s5, v254, 45
	s_mov_b64 s[2:3], -1
	s_and_b64 vcc, exec, s[4:5]
	s_cbranch_vccz .LBB0_590
	s_mov_b32 s2, s97
	s_waitcnt vmcnt(0)
	s_waitcnt vmcnt(0) lgkmcnt(0)
	s_barrier
	s_nop 0
	v_mbcnt_lo_u32_b32 v0, -1, s2
	v_mbcnt_hi_u32_b32 v0, -1, v0
	v_cmp_eq_u32_e32 vcc, s65, v0
	s_and_saveexec_b64 s[38:39], vcc
	s_cbranch_execz .LBB0_589
	s_nop 0
	v_readlane_b32 s40, v253, 12
	v_readlane_b32 s2, v253, 14
	v_readlane_b32 s22, v253, 17
	v_readlane_b32 s41, v253, 13
	v_mov_b32_e32 v0, s2
	s_waitcnt vmcnt(0) expcnt(0) lgkmcnt(0)
	ds_read_b32 v2, v0
	ds_read_b32 v0, v0 offset:4
	s_waitcnt lgkmcnt(1)
	v_cmp_ne_u32_e32 vcc, 0, v2
	s_cbranch_vccnz .LBB0_560
	s_nop 0
	v_readlane_b32 s2, v253, 6
	v_readlane_b32 s3, v253, 7
	s_load_dwordx2 s[6:7], s[2:3], 0x4
	s_add_u32 s2, s40, 0x1000
	s_addc_u32 s3, s41, 0
	s_nop 0
	s_add_u32 s4, s40, 0x1100
	s_addc_u32 s5, s41, 0
	s_waitcnt lgkmcnt(0)
	s_mul_i32 s23, s6, s61
	s_nop 0
	s_add_u32 s6, s40, 0x1200
	s_mul_i32 s23, s23, s7
	s_addc_u32 s7, s41, 0
	s_add_u32 s8, s40, 0x1300
	s_addc_u32 s9, s41, 0
	s_mov_b32 s30, 1
	s_mov_b64 s[10:11], 0
	s_branch .LBB0_550

.LBB0_590:
	s_and_b64 vcc, exec, s[2:3]
	s_cbranch_vccz .LBB0_608
	s_mov_b32 s2, s97
	s_waitcnt vmcnt(0)
	s_waitcnt vmcnt(0) lgkmcnt(0)
	s_barrier
	s_nop 0
	v_mbcnt_lo_u32_b32 v0, -1, s2
	v_mbcnt_hi_u32_b32 v0, -1, v0
	v_cmp_eq_u32_e32 vcc, s65, v0
	s_and_saveexec_b64 s[2:3], vcc
	s_cbranch_execz .LBB0_607
	s_nop 0
	v_readlane_b32 s12, v253, 12
	v_readlane_b32 s13, v253, 13
	v_readlane_b32 s4, v253, 17
	s_lshl_b32 s6, s4, 6
	s_nop 0
	s_add_i32 s96, s6, 0xdc0
	s_lshl_b64 s[4:5], s[96:97], 2
	s_add_u32 s4, s12, s4
	s_addc_u32 s5, s13, s5
	v_mov_b64_e32 v[0:1], s[4:5]
	v_mov_b32_e64 v2, 1
	flat_atomic_add v2, v[0:1], v2 sc0
	s_add_i32 s96, s6, 0x1200
	s_lshl_b64 s[4:5], s[96:97], 2
	s_add_u32 s6, s12, s4
	s_addc_u32 s7, s13, s5
	s_mov_b64 s[8:9], -1
	s_waitcnt vmcnt(0) lgkmcnt(0)
	v_and_b32_e32 v0, 31, v2
	v_cmp_ne_u32_e32 vcc, 31, v0
	v_mov_b64_e32 v[0:1], s[6:7]
	s_and_saveexec_b64 s[4:5], vcc
	s_cbranch_execz .LBB0_604
	v_mov_b64_e32 v[0:1], s[6:7]
	s_nop 0
	flat_load_dword v1, v[0:1] sc1
	v_lshrrev_b32_e32 v0, 5, v2
	s_mov_b64 s[14:15], 0
	s_waitcnt vmcnt(0) lgkmcnt(0)
	v_cmp_eq_u32_e32 vcc, v1, v0
	s_and_saveexec_b64 s[10:11], vcc
	s_cbranch_execz .LBB0_603
	s_add_u32 s8, s12, 0x200
	s_addc_u32 s9, s13, 0
	s_mov_b32 s22, 1
	s_mov_b64 s[12:13], 0
	s_branch .LBB0_596

.LBB0_596:
	s_nop 0
	s_and_b32 s18, s22, 0xff
	s_mov_b64 s[16:17], -1
	s_cmp_lg_u32 s18, 0
	s_mov_b64 s[20:21], -1
	s_sleep 1
	s_cbranch_scc0 .LBB0_598
	s_and_saveexec_b64 s[24:25], s[20:21]
	s_cbranch_execz .LBB0_595
	s_branch .LBB0_601
.LBB0_598:
	v_mov_b64_e32 v[2:3], s[8:9]
	s_nop 0
	flat_load_dword v1, v[2:3] sc1
	s_mov_b64 s[20:21], 0
	s_mov_b64 s[18:19], -1
	s_waitcnt vmcnt(0) lgkmcnt(0)
	v_cmp_eq_u32_e32 vcc, 0, v1
	s_and_saveexec_b64 s[24:25], vcc
	s_nop 0
	s_cmp_lt_u32 s22, 0x400001
	s_cselect_b64 s[20:21], -1, 0
	s_xor_b64 s[18:19], exec, -1
	s_and_b64 s[20:21], s[20:21], exec
	s_or_b64 exec, exec, s[24:25]
	s_and_saveexec_b64 s[24:25], s[20:21]
	s_cbranch_execz .LBB0_595
.LBB0_601:
	v_mov_b64_e32 v[2:3], s[6:7]
	s_nop 0
	flat_load_dword v1, v[2:3] sc1
	s_add_i32 s22, s22, 1
	s_or_b64 s[18:19], s[18:19], exec
	s_waitcnt vmcnt(0) lgkmcnt(0)
	v_cmp_ne_u32_e32 vcc, v1, v0
	s_orn2_b64 s[16:17], vcc, exec
	s_branch .LBB0_595

.LBB0_604:
	s_or_b64 exec, exec, s[4:5]
	s_and_saveexec_b64 s[4:5], s[8:9]
	s_cbranch_execz .LBB0_606
	v_mov_b32_e64 v2, 1
	flat_atomic_add v[0:1], v2

.LBB0_609:
	v_readlane_b32 s2, v254, 24
	v_readlane_b32 s3, v254, 25
	s_andn2_b64 vcc, exec, s[2:3]
	s_cbranch_vccnz .LBB0_253
	s_add_u32 s56, s70, 0x37000000
	s_addc_u32 s57, s71, 0
	s_nop 0
	s_add_u32 s58, s70, 0x37008000
	s_addc_u32 s59, s71, 0
	s_and_b64 vcc, exec, s[0:1]
	s_cbranch_vccnz .LBB0_656
	s_nop 0
	v_readlane_b32 s4, v254, 5
	v_readlane_b32 s5, v254, 6
	s_cmp_gt_i32 s4, s89
	s_cselect_b64 s[2:3], -1, 0
	s_cmp_ge_i32 s89, s5
	s_cselect_b64 s[4:5], -1, 0
	s_or_b64 s[2:3], s[2:3], s[4:5]
	s_add_i32 s89, s92, 3
	s_and_b64 vcc, exec, s[2:3]
	s_nop 0
	v_readlane_b32 s44, v254, 48
	s_cbranch_vccnz .LBB0_657
	s_nop 0
	v_writelane_b32 v255, s58, 53
	s_mov_b32 s2, s97
	s_mov_b32 s22, s93
	v_writelane_b32 v255, s59, 54
	v_mbcnt_lo_u32_b32 v0, -1, s2
	v_writelane_b32 v255, s90, 55
	v_mbcnt_hi_u32_b32 v0, -1, v0
	v_add_u32_e64 v0, s64, v0
	v_writelane_b32 v255, s91, 56
	v_writelane_b32 v255, s60, 52
	s_cmpk_gt_i32 s22, 0xff
	v_readfirstlane_b32 s2, v0
	s_cbranch_scc1 .LBB0_706
	v_and_b32_e32 v2, 64, v227
	v_add_u32_e32 v5, -1, v227
	v_cmp_lt_i32_e32 vcc, v5, v2
	v_ashrrev_i32_e32 v42, 3, v0
	v_lshlrev_b32_e32 v6, 2, v42
	v_cndmask_b32_e32 v5, v5, v227, vcc
	v_lshlrev_b32_e32 v41, 2, v5
	v_add_u32_e32 v5, -2, v227
	v_cmp_lt_i32_e32 vcc, v5, v2
	v_and_b32_e32 v1, 7, v0
	v_and_b32_e32 v40, 63, v0
	v_cndmask_b32_e32 v5, v5, v227, vcc
	v_lshlrev_b32_e32 v62, 2, v5
	v_add_u32_e32 v5, -4, v227
	v_cmp_lt_i32_e32 vcc, v5, v2
	v_readlane_b32 s18, v255, 53
	v_and_b32_e32 v7, 12, v6
	v_cndmask_b32_e32 v5, v5, v227, vcc
	v_lshlrev_b32_e32 v63, 2, v5
	v_add_u32_e32 v5, -8, v227
	v_cmp_lt_i32_e32 vcc, v5, v2
	s_nop 0
	v_bfe_u32 v8, v42, 2, 2
	v_lshlrev_b32_e32 v96, 2, v40
	v_cndmask_b32_e32 v5, v5, v227, vcc
	v_lshlrev_b32_e32 v64, 2, v5
	v_add_u32_e32 v5, -16, v227
	v_cmp_lt_i32_e32 vcc, v5, v2
	s_nop 0
	v_readlane_b32 s19, v255, 54
	v_bitop3_b32 v9, v7, v1, v8 bitop3:0x36
	v_cndmask_b32_e32 v5, v5, v227, vcc
	v_lshlrev_b32_e32 v65, 2, v5
	v_subrev_u32_e32 v5, 32, v227
	v_cmp_lt_i32_e32 vcc, v5, v2
	s_ashr_i32 s44, s2, 6
	s_ashr_i32 s16, s2, 8
	v_cndmask_b32_e32 v2, v5, v227, vcc
	v_lshlrev_b32_e32 v66, 2, v2
	v_lshlrev_b32_e32 v2, 3, v1
	v_or_b32_e32 v1, 8, v1
	v_lshl_add_u64 v[44:45], s[18:19], 0, v[96:97]
	v_cmp_eq_u32_e64 s[18:19], 0, v0
	v_bitop3_b32 v1, v7, v1, v8 bitop3:0x36
	s_and_b32 s45, s44, 3
	v_and_b32_e32 v4, 15, v0
	s_lshl_b32 s20, s16, 5
	s_nop 0
	v_writelane_b32 v254, s18, 24
	v_lshlrev_b32_e32 v70, 4, v1
	s_nop 0
	v_bfe_u32 v1, v0, 2, 2
	v_lshlrev_b32_e32 v10, 3, v0
	s_lshl_b32 s46, s16, 2
	s_lshl_b32 s16, s44, 2
	v_or_b32_e32 v5, s45, v4
	v_writelane_b32 v254, s19, 25
	v_lshlrev_b32_e32 v69, 4, v9
	s_nop 0
	v_bfe_u32 v7, v0, 1, 1
	v_lshrrev_b32_e32 v9, 3, v0
	v_and_b32_e32 v71, 8, v10
	v_lshlrev_b32_e32 v10, 2, v1
	s_add_i32 s53, s16, 0
	s_add_i32 s16, s44, 8
	s_nop 0
	v_bfe_u32 v3, v0, 4, 2
	s_and_b32 s24, s2, 0xffffffc0
	v_lshl_or_b32 v8, s45, 1, v7
	v_writelane_b32 v254, s16, 12
	s_lshl_b32 s17, s16, 8
	s_add_i32 s16, s44, 24
	v_cmp_eq_u32_e64 s[58:59], 0, v5
	v_and_or_b32 v5, v9, 2, v10
	v_lshlrev_b32_e32 v1, 8, v1
	s_ashr_i32 s21, s20, 31
	s_add_i32 s26, s24, 0x200
	s_add_i32 s28, s24, 0x400
	s_add_i32 s30, s24, 0x600
	s_add_i32 s34, s24, 0x800
	s_add_i32 s38, s24, 0xa00
	s_add_i32 s40, s24, 0xc00
	s_add_i32 s48, s24, 0xe00
	s_lshl_b32 s52, s44, 8
	s_add_i32 s37, s44, 16
	v_writelane_b32 v255, s16, 51
	s_add_i32 s43, s44, 32
	s_add_i32 s23, s44, 40
	s_add_i32 s47, s44, 48
	s_mov_b32 s50, s44
	s_add_i32 s44, s44, 56
	s_nop 0
	v_lshl_or_b32 v73, v3, 11, v1
	v_bitop3_b32 v1, v8, v5, 8 bitop3:0x36
	v_or_b32_e32 v11, s46, v7
	s_ashr_i32 s25, s24, 31
	s_ashr_i32 s27, s26, 31
	s_ashr_i32 s29, s28, 31
	s_ashr_i32 s31, s30, 31
	s_ashr_i32 s35, s34, 31
	s_ashr_i32 s39, s38, 31
	s_ashr_i32 s41, s40, 31
	s_ashr_i32 s49, s48, 31
	s_lshl_b32 s19, s37, 8
	s_lshl_b32 s18, s16, 8
	s_lshl_b32 s16, s43, 8
	v_writelane_b32 v255, s23, 57
	s_lshl_b32 s23, s23, 8
	s_mov_b32 s42, s47
	s_lshl_b32 s72, s47, 8
	s_lshl_b32 s73, s44, 8
	v_bitop3_b32 v7, s46, v5, v7 bitop3:0x36
	v_lshlrev_b32_e32 v74, 4, v1
	v_or_b32_e32 v1, 1, v5
	s_lshl_b64 s[46:47], s[20:21], 2
	s_lshl_b64 s[20:21], s[20:21], 1
	v_writelane_b32 v255, s58, 58
	v_lshlrev_b32_e32 v72, 4, v7
	s_nop 0
	v_bitop3_b32 v7, v8, v1, 8 bitop3:0x36
	s_bitcmp1_b32 s22, 0
	s_nop 0
	v_writelane_b32 v255, s59, 59
	v_lshlrev_b32_e32 v75, 4, v7
	s_nop 0
	v_bitop3_b32 v7, v5, v11, 1 bitop3:0x36
	v_bitop3_b32 v5, v11, v5, 2 bitop3:0x36
	v_bitop3_b32 v1, v11, v1, 2 bitop3:0x36
	v_and_or_b32 v46, v0, 48, s46
	v_lshl_or_b32 v48, v3, 3, s20
	v_lshl_or_b32 v0, s45, 4, v4
	s_cselect_b64 s[58:59], -1, 0
	s_nop 0
	s_add_i32 s20, 0, 0x8000
	v_cmp_eq_u32_e64 s[2:3], 0, v40
	v_cmp_gt_u32_e64 s[4:5], 2, v40
	v_cmp_gt_u32_e64 s[6:7], 4, v40
	v_cmp_gt_u32_e64 s[8:9], 8, v40
	v_cmp_gt_u32_e64 s[10:11], 16, v40
	v_cmp_gt_u32_e64 s[12:13], 32, v40
	v_add_u32_e64 v67, 0, v96
	v_cmp_eq_u32_e64 s[14:15], 63, v40
	v_ashrrev_i32_e32 v43, 31, v42
	v_lshlrev_b32_e32 v68, 8, v42
	s_mov_b32 s36, s44
	v_lshlrev_b32_e32 v76, 4, v7
	v_lshlrev_b32_e32 v77, 4, v5
	v_lshlrev_b32_e32 v78, 4, v1
	v_mov_b32_e32 v47, s47
	v_mov_b32_e32 v49, s21
	v_add_u32_e32 v79, s20, v6
	v_lshlrev_b32_e32 v80, 7, v0
	v_lshlrev_b32_e32 v50, 1, v2
	s_branch .LBB0_615

.LBB0_615:
	s_ashr_i32 s20, s22, 4
	s_ashr_i32 s60, s22, 1
	s_ashr_i32 s21, s20, 31
	s_and_b32 s45, s60, 7
	s_lshl_b64 s[46:47], s[20:21], 12
	s_waitcnt vmcnt(0)
	v_mov_b32_e32 v1, s47
	v_or_b32_e32 v0, s46, v40
	s_lshl_b32 s20, s45, 2
	v_readlane_b32 s64, v254, 36
	v_readlane_b32 s65, v254, 37
	s_add_u32 s20, s64, s20
	s_nop 0
	v_lshl_add_u64 v[2:3], v[0:1], 0, s[24:25]
	s_addc_u32 s21, s65, 0
	s_nop 0
	v_lshlrev_b64 v[2:3], 6, v[2:3]
	v_lshl_add_u64 v[2:3], s[20:21], 0, v[2:3]
	global_load_dword v17, v[2:3], off
	global_load_dword v16, v[2:3], off offset:32
	v_lshl_add_u64 v[2:3], v[0:1], 0, s[26:27]
	v_lshlrev_b64 v[2:3], 6, v[2:3]
	v_lshl_add_u64 v[2:3], s[20:21], 0, v[2:3]
	global_load_dword v12, v[2:3], off
	global_load_dword v13, v[2:3], off offset:32
	v_lshl_add_u64 v[2:3], v[0:1], 0, s[28:29]
	v_lshlrev_b64 v[2:3], 6, v[2:3]
	v_lshl_add_u64 v[2:3], s[20:21], 0, v[2:3]
	global_load_dword v10, v[2:3], off
	global_load_dword v11, v[2:3], off offset:32
	v_lshl_add_u64 v[2:3], v[0:1], 0, s[30:31]
	v_lshlrev_b64 v[2:3], 6, v[2:3]
	v_lshl_add_u64 v[2:3], s[20:21], 0, v[2:3]
	global_load_dword v8, v[2:3], off
	global_load_dword v9, v[2:3], off offset:32
	v_lshl_add_u64 v[2:3], v[0:1], 0, s[34:35]
	v_lshlrev_b64 v[2:3], 6, v[2:3]
	v_lshl_add_u64 v[2:3], s[20:21], 0, v[2:3]
	global_load_dword v6, v[2:3], off
	global_load_dword v7, v[2:3], off offset:32
	v_lshl_add_u64 v[2:3], v[0:1], 0, s[38:39]
	v_lshlrev_b64 v[2:3], 6, v[2:3]
	v_lshl_add_u64 v[2:3], s[20:21], 0, v[2:3]
	global_load_dword v4, v[2:3], off
	global_load_dword v5, v[2:3], off offset:32
	v_lshl_add_u64 v[2:3], v[0:1], 0, s[40:41]
	v_lshlrev_b64 v[2:3], 6, v[2:3]
	v_lshl_add_u64 v[0:1], v[0:1], 0, s[48:49]
	v_lshl_add_u64 v[14:15], s[20:21], 0, v[2:3]
	v_lshlrev_b64 v[0:1], 6, v[0:1]
	global_load_dword v2, v[14:15], off
	global_load_dword v3, v[14:15], off offset:32
	v_lshl_add_u64 v[14:15], s[20:21], 0, v[0:1]
	global_load_dword v0, v[14:15], off
	global_load_dword v1, v[14:15], off offset:32
	s_waitcnt vmcnt(0)
	s_nop 0
	ds_bpermute_b32 v14, v41, v16
	s_waitcnt lgkmcnt(0)
	v_add_f32_e32 v14, v16, v14
	v_cndmask_b32_e64 v14, v14, v16, s[2:3]
	ds_bpermute_b32 v15, v62, v14
	s_waitcnt lgkmcnt(0)
	v_add_f32_e32 v15, v14, v15
	v_cndmask_b32_e64 v14, v15, v14, s[4:5]
	ds_bpermute_b32 v15, v63, v14
	s_waitcnt lgkmcnt(0)
	v_add_f32_e32 v15, v14, v15
	v_cndmask_b32_e64 v14, v15, v14, s[6:7]
	ds_bpermute_b32 v15, v64, v14
	s_waitcnt lgkmcnt(0)
	v_add_f32_e32 v15, v14, v15
	v_cndmask_b32_e64 v14, v15, v14, s[8:9]
	ds_bpermute_b32 v15, v65, v14
	s_waitcnt lgkmcnt(0)
	v_add_f32_e32 v15, v14, v15
	v_cndmask_b32_e64 v14, v15, v14, s[10:11]
	ds_bpermute_b32 v15, v66, v14
	s_waitcnt lgkmcnt(0)
	v_add_f32_e32 v16, v14, v15
	v_cndmask_b32_e64 v14, v16, v14, s[12:13]
	v_sub_f32_e64 v15, v17, v14
	ds_bpermute_b32 v17, v41, v15
	s_waitcnt lgkmcnt(0)
	v_max_f32_e32 v17, v17, v17
	v_max_f32_e64 v17, v15, v17
	v_cndmask_b32_e64 v17, v17, v15, s[2:3]
	ds_bpermute_b32 v18, v62, v17
	s_waitcnt lgkmcnt(0)
	v_max_f32_e32 v18, v18, v18
	v_max_f32_e64 v18, v17, v18
	v_cndmask_b32_e64 v17, v18, v17, s[4:5]
	ds_bpermute_b32 v18, v63, v17
	s_waitcnt lgkmcnt(0)
	v_max_f32_e32 v18, v18, v18
	v_max_f32_e64 v18, v17, v18
	v_cndmask_b32_e64 v17, v18, v17, s[6:7]
	ds_bpermute_b32 v18, v64, v17
	s_waitcnt lgkmcnt(0)
	v_max_f32_e32 v18, v18, v18
	v_max_f32_e64 v18, v17, v18
	v_cndmask_b32_e64 v17, v18, v17, s[8:9]
	ds_bpermute_b32 v18, v65, v17
	s_waitcnt lgkmcnt(0)
	v_max_f32_e32 v18, v18, v18
	v_max_f32_e64 v18, v17, v18
	v_cndmask_b32_e64 v17, v18, v17, s[10:11]
	ds_bpermute_b32 v18, v66, v17
	v_max_f32_e32 v19, v17, v17
	s_waitcnt lgkmcnt(0)
	v_max_f32_e32 v18, v18, v18
	v_max_f32_e32 v18, v19, v18
	v_add_u32_e64 v19, s52, v67
	ds_write_b32 v19, v15 offset:32768
	s_and_saveexec_b64 s[20:21], s[14:15]
	v_mov_b32_e32 v19, s53
	ds_write2st64_b32 v19, v18, v16 offset0:192 offset1:193
	s_mov_b32 s44, s93
	s_mov_b32 s51, s89
	s_or_b64 exec, exec, s[20:21]
	s_and_b32 s61, s22, 1
	s_cmp_eq_u32 s61, 0
	s_cselect_b64 s[64:65], -1, 0
	s_cmp_eq_u32 s61, 1
	s_cselect_b64 s[20:21], -1, 0
	s_lshl_b32 s60, s60, 6
	s_and_b64 vcc, exec, s[20:21]
	s_cbranch_vccnz .LBB0_619
	s_add_i32 s20, s60, s50
	v_cndmask_b32_e64 v18, v18, v17, s[12:13]
	v_mad_i64_i32 v[16:17], s[20:21], s20, v233, v[44:45]
	global_store_dword v[16:17], v15, off
	global_store_dword v[16:17], v18, off offset:256
	global_store_dword v[16:17], v14, off offset:512
.LBB0_619:
	ds_bpermute_b32 v14, v41, v13
	s_waitcnt lgkmcnt(0)
	v_add_f32_e32 v14, v13, v14
	v_cndmask_b32_e64 v13, v14, v13, s[2:3]
	ds_bpermute_b32 v14, v62, v13
	s_waitcnt lgkmcnt(0)
	v_add_f32_e32 v14, v13, v14
	v_cndmask_b32_e64 v13, v14, v13, s[4:5]
	ds_bpermute_b32 v14, v63, v13
	s_waitcnt lgkmcnt(0)
	v_add_f32_e32 v14, v13, v14
	v_cndmask_b32_e64 v13, v14, v13, s[6:7]
	ds_bpermute_b32 v14, v64, v13
	s_waitcnt lgkmcnt(0)
	v_add_f32_e32 v14, v13, v14
	v_cndmask_b32_e64 v13, v14, v13, s[8:9]
	ds_bpermute_b32 v14, v65, v13
	s_waitcnt lgkmcnt(0)
	v_add_f32_e32 v14, v13, v14
	v_cndmask_b32_e64 v13, v14, v13, s[10:11]
	ds_bpermute_b32 v14, v66, v13
	s_waitcnt lgkmcnt(0)
	v_add_f32_e32 v14, v13, v14
	v_cndmask_b32_e64 v13, v14, v13, s[12:13]
	v_sub_f32_e64 v12, v12, v13
	ds_bpermute_b32 v15, v41, v12
	s_waitcnt lgkmcnt(0)
	v_max_f32_e32 v15, v15, v15
	v_max_f32_e64 v15, v12, v15
	v_cndmask_b32_e64 v15, v15, v12, s[2:3]
	ds_bpermute_b32 v16, v62, v15
	s_waitcnt lgkmcnt(0)
	v_max_f32_e32 v16, v16, v16
	v_max_f32_e64 v16, v15, v16
	v_cndmask_b32_e64 v15, v16, v15, s[4:5]
	ds_bpermute_b32 v16, v63, v15
	s_waitcnt lgkmcnt(0)
	v_max_f32_e32 v16, v16, v16
	v_max_f32_e64 v16, v15, v16
	v_cndmask_b32_e64 v15, v16, v15, s[6:7]
	ds_bpermute_b32 v16, v64, v15
	s_waitcnt lgkmcnt(0)
	v_max_f32_e32 v16, v16, v16
	v_max_f32_e64 v16, v15, v16
	v_cndmask_b32_e64 v15, v16, v15, s[8:9]
	ds_bpermute_b32 v16, v65, v15
	s_waitcnt lgkmcnt(0)
	v_max_f32_e32 v16, v16, v16
	v_max_f32_e64 v16, v15, v16
	v_cndmask_b32_e64 v15, v16, v15, s[10:11]
	ds_bpermute_b32 v16, v66, v15
	v_max_f32_e32 v17, v15, v15
	s_waitcnt lgkmcnt(0)
	v_max_f32_e32 v16, v16, v16
	v_max_f32_e32 v16, v17, v16
	v_add_u32_e64 v17, s17, v67
	ds_write_b32 v17, v12 offset:32768
	s_and_saveexec_b64 s[20:21], s[14:15]
	s_nop 0
	v_add_u32_e64 v17, 32, s53
	ds_write2st64_b32 v17, v16, v14 offset0:192 offset1:193
	s_or_b64 exec, exec, s[20:21]
	s_nop 0
	v_cndmask_b32_e64 v14, 0, 1, s[64:65]
	v_cmp_ne_u32_e64 s[20:21], 1, v14
	s_andn2_b64 vcc, exec, s[64:65]
	s_cbranch_vccnz .LBB0_623
	v_readlane_b32 s64, v254, 12
	s_add_i32 s64, s60, s64
	s_nop 0
	v_cndmask_b32_e64 v16, v16, v15, s[12:13]
	v_mad_i64_i32 v[14:15], s[64:65], s64, v233, v[44:45]
	global_store_dword v[14:15], v12, off
	global_store_dword v[14:15], v16, off offset:256
	global_store_dword v[14:15], v13, off offset:512
.LBB0_623:
	ds_bpermute_b32 v12, v41, v11
	s_waitcnt lgkmcnt(0)
	v_add_f32_e32 v12, v11, v12
	v_cndmask_b32_e64 v11, v12, v11, s[2:3]
	ds_bpermute_b32 v12, v62, v11
	s_waitcnt lgkmcnt(0)
	v_add_f32_e32 v12, v11, v12
	v_cndmask_b32_e64 v11, v12, v11, s[4:5]
	ds_bpermute_b32 v12, v63, v11
	s_waitcnt lgkmcnt(0)
	v_add_f32_e32 v12, v11, v12
	v_cndmask_b32_e64 v11, v12, v11, s[6:7]
	ds_bpermute_b32 v12, v64, v11
	s_waitcnt lgkmcnt(0)
	v_add_f32_e32 v12, v11, v12
	v_cndmask_b32_e64 v11, v12, v11, s[8:9]
	ds_bpermute_b32 v12, v65, v11
	s_waitcnt lgkmcnt(0)
	v_add_f32_e32 v12, v11, v12
	v_cndmask_b32_e64 v11, v12, v11, s[10:11]
	ds_bpermute_b32 v12, v66, v11
	s_waitcnt lgkmcnt(0)
	v_add_f32_e32 v12, v11, v12
	v_cndmask_b32_e64 v11, v12, v11, s[12:13]
	v_sub_f32_e64 v10, v10, v11
	ds_bpermute_b32 v13, v41, v10
	s_waitcnt lgkmcnt(0)
	v_max_f32_e32 v13, v13, v13
	v_max_f32_e64 v13, v10, v13
	v_cndmask_b32_e64 v13, v13, v10, s[2:3]
	ds_bpermute_b32 v14, v62, v13
	s_waitcnt lgkmcnt(0)
	v_max_f32_e32 v14, v14, v14
	v_max_f32_e64 v14, v13, v14
	v_cndmask_b32_e64 v13, v14, v13, s[4:5]
	ds_bpermute_b32 v14, v63, v13
	s_waitcnt lgkmcnt(0)
	v_max_f32_e32 v14, v14, v14
	v_max_f32_e64 v14, v13, v14
	v_cndmask_b32_e64 v13, v14, v13, s[6:7]
	ds_bpermute_b32 v14, v64, v13
	s_waitcnt lgkmcnt(0)
	v_max_f32_e32 v14, v14, v14
	v_max_f32_e64 v14, v13, v14
	v_cndmask_b32_e64 v13, v14, v13, s[8:9]
	ds_bpermute_b32 v14, v65, v13
	s_waitcnt lgkmcnt(0)
	v_max_f32_e32 v14, v14, v14
	v_max_f32_e64 v14, v13, v14
	v_cndmask_b32_e64 v13, v14, v13, s[10:11]
	ds_bpermute_b32 v14, v66, v13
	v_max_f32_e32 v15, v13, v13
	s_waitcnt lgkmcnt(0)
	v_max_f32_e32 v14, v14, v14
	v_max_f32_e32 v14, v15, v14
	v_add_u32_e64 v15, s19, v67
	ds_write_b32 v15, v10 offset:32768
	s_and_saveexec_b64 s[64:65], s[14:15]
	s_nop 0
	v_add_u32_e64 v15, 64, s53
	ds_write2st64_b32 v15, v14, v12 offset0:192 offset1:193
	s_or_b64 exec, exec, s[64:65]
	s_and_b64 vcc, exec, s[20:21]
	s_cbranch_vccnz .LBB0_627
	s_add_i32 s64, s60, s37
	v_cndmask_b32_e64 v14, v14, v13, s[12:13]
	v_mad_i64_i32 v[12:13], s[64:65], s64, v233, v[44:45]
	global_store_dword v[12:13], v10, off
	global_store_dword v[12:13], v14, off offset:256
	global_store_dword v[12:13], v11, off offset:512
.LBB0_627:
	ds_bpermute_b32 v10, v41, v9
	s_waitcnt lgkmcnt(0)
	v_add_f32_e32 v10, v9, v10
	v_cndmask_b32_e64 v9, v10, v9, s[2:3]
	ds_bpermute_b32 v10, v62, v9
	s_waitcnt lgkmcnt(0)
	v_add_f32_e32 v10, v9, v10
	v_cndmask_b32_e64 v9, v10, v9, s[4:5]
	ds_bpermute_b32 v10, v63, v9
	s_waitcnt lgkmcnt(0)
	v_add_f32_e32 v10, v9, v10
	v_cndmask_b32_e64 v9, v10, v9, s[6:7]
	ds_bpermute_b32 v10, v64, v9
	s_waitcnt lgkmcnt(0)
	v_add_f32_e32 v10, v9, v10
	v_cndmask_b32_e64 v9, v10, v9, s[8:9]
	ds_bpermute_b32 v10, v65, v9
	s_waitcnt lgkmcnt(0)
	v_add_f32_e32 v10, v9, v10
	v_cndmask_b32_e64 v9, v10, v9, s[10:11]
	ds_bpermute_b32 v10, v66, v9
	s_waitcnt lgkmcnt(0)
	v_add_f32_e32 v10, v9, v10
	v_cndmask_b32_e64 v9, v10, v9, s[12:13]
	v_sub_f32_e64 v8, v8, v9
	ds_bpermute_b32 v11, v41, v8
	s_waitcnt lgkmcnt(0)
	v_max_f32_e32 v11, v11, v11
	v_max_f32_e64 v11, v8, v11
	v_cndmask_b32_e64 v11, v11, v8, s[2:3]
	ds_bpermute_b32 v12, v62, v11
	s_waitcnt lgkmcnt(0)
	v_max_f32_e32 v12, v12, v12
	v_max_f32_e64 v12, v11, v12
	v_cndmask_b32_e64 v11, v12, v11, s[4:5]
	ds_bpermute_b32 v12, v63, v11
	s_waitcnt lgkmcnt(0)
	v_max_f32_e32 v12, v12, v12
	v_max_f32_e64 v12, v11, v12
	v_cndmask_b32_e64 v11, v12, v11, s[6:7]
	ds_bpermute_b32 v12, v64, v11
	s_waitcnt lgkmcnt(0)
	v_max_f32_e32 v12, v12, v12
	v_max_f32_e64 v12, v11, v12
	v_cndmask_b32_e64 v11, v12, v11, s[8:9]
	ds_bpermute_b32 v12, v65, v11
	s_waitcnt lgkmcnt(0)
	v_max_f32_e32 v12, v12, v12
	v_max_f32_e64 v12, v11, v12
	v_cndmask_b32_e64 v11, v12, v11, s[10:11]
	ds_bpermute_b32 v12, v66, v11
	v_max_f32_e32 v13, v11, v11
	s_waitcnt lgkmcnt(0)
	v_max_f32_e32 v12, v12, v12
	v_max_f32_e32 v12, v13, v12
	v_add_u32_e64 v13, s18, v67
	ds_write_b32 v13, v8 offset:32768
	s_and_saveexec_b64 s[64:65], s[14:15]
	v_mov_b32_e32 v13, s53
	v_add_u32_e32 v13, 0x60, v13
	ds_write2st64_b32 v13, v12, v10 offset0:192 offset1:193
	s_or_b64 exec, exec, s[64:65]
	s_and_b64 vcc, exec, s[20:21]
	s_cbranch_vccnz .LBB0_631
	s_nop 0
	v_readlane_b32 s64, v255, 51
	s_add_i32 s64, s60, s64
	s_nop 0
	v_cndmask_b32_e64 v12, v12, v11, s[12:13]
	v_mad_i64_i32 v[10:11], s[64:65], s64, v233, v[44:45]
	global_store_dword v[10:11], v8, off
	global_store_dword v[10:11], v12, off offset:256
	global_store_dword v[10:11], v9, off offset:512
.LBB0_631:
	ds_bpermute_b32 v8, v41, v7
	s_waitcnt lgkmcnt(0)
	v_add_f32_e32 v8, v7, v8
	v_cndmask_b32_e64 v7, v8, v7, s[2:3]
	ds_bpermute_b32 v8, v62, v7
	s_waitcnt lgkmcnt(0)
	v_add_f32_e32 v8, v7, v8
	v_cndmask_b32_e64 v7, v8, v7, s[4:5]
	ds_bpermute_b32 v8, v63, v7
	s_waitcnt lgkmcnt(0)
	v_add_f32_e32 v8, v7, v8
	v_cndmask_b32_e64 v7, v8, v7, s[6:7]
	ds_bpermute_b32 v8, v64, v7
	s_waitcnt lgkmcnt(0)
	v_add_f32_e32 v8, v7, v8
	v_cndmask_b32_e64 v7, v8, v7, s[8:9]
	ds_bpermute_b32 v8, v65, v7
	s_waitcnt lgkmcnt(0)
	v_add_f32_e32 v8, v7, v8
	v_cndmask_b32_e64 v7, v8, v7, s[10:11]
	ds_bpermute_b32 v8, v66, v7
	s_waitcnt lgkmcnt(0)
	v_add_f32_e32 v8, v7, v8
	v_cndmask_b32_e64 v7, v8, v7, s[12:13]
	v_sub_f32_e64 v6, v6, v7
	ds_bpermute_b32 v9, v41, v6
	s_waitcnt lgkmcnt(0)
	v_max_f32_e32 v9, v9, v9
	v_max_f32_e64 v9, v6, v9
	v_cndmask_b32_e64 v9, v9, v6, s[2:3]
	ds_bpermute_b32 v10, v62, v9
	s_waitcnt lgkmcnt(0)
	v_max_f32_e32 v10, v10, v10
	v_max_f32_e64 v10, v9, v10
	v_cndmask_b32_e64 v9, v10, v9, s[4:5]
	ds_bpermute_b32 v10, v63, v9
	s_waitcnt lgkmcnt(0)
	v_max_f32_e32 v10, v10, v10
	v_max_f32_e64 v10, v9, v10
	v_cndmask_b32_e64 v9, v10, v9, s[6:7]
	ds_bpermute_b32 v10, v64, v9
	s_waitcnt lgkmcnt(0)
	v_max_f32_e32 v10, v10, v10
	v_max_f32_e64 v10, v9, v10
	v_cndmask_b32_e64 v9, v10, v9, s[8:9]
	ds_bpermute_b32 v10, v65, v9
	s_waitcnt lgkmcnt(0)
	v_max_f32_e32 v10, v10, v10
	v_max_f32_e64 v10, v9, v10
	v_cndmask_b32_e64 v9, v10, v9, s[10:11]
	ds_bpermute_b32 v10, v66, v9
	v_max_f32_e32 v11, v9, v9
	s_waitcnt lgkmcnt(0)
	v_max_f32_e32 v10, v10, v10
	v_max_f32_e32 v10, v11, v10
	v_add_u32_e64 v11, s16, v67
	ds_write_b32 v11, v6 offset:32768
	s_and_saveexec_b64 s[64:65], s[14:15]
	v_mov_b32_e32 v11, s53
	v_add_u32_e32 v11, 0x80, v11
	ds_write2st64_b32 v11, v10, v8 offset0:192 offset1:193
	s_or_b64 exec, exec, s[64:65]
	s_and_b64 vcc, exec, s[20:21]
	s_cbranch_vccnz .LBB0_635
	s_add_i32 s64, s60, s43
	v_cndmask_b32_e64 v10, v10, v9, s[12:13]
	v_mad_i64_i32 v[8:9], s[64:65], s64, v233, v[44:45]
	global_store_dword v[8:9], v6, off
	global_store_dword v[8:9], v10, off offset:256
	global_store_dword v[8:9], v7, off offset:512
.LBB0_635:
	ds_bpermute_b32 v6, v41, v5
	s_waitcnt lgkmcnt(0)
	v_add_f32_e32 v6, v5, v6
	v_cndmask_b32_e64 v5, v6, v5, s[2:3]
	ds_bpermute_b32 v6, v62, v5
	s_waitcnt lgkmcnt(0)
	v_add_f32_e32 v6, v5, v6
	v_cndmask_b32_e64 v5, v6, v5, s[4:5]
	ds_bpermute_b32 v6, v63, v5
	s_waitcnt lgkmcnt(0)
	v_add_f32_e32 v6, v5, v6
	v_cndmask_b32_e64 v5, v6, v5, s[6:7]
	ds_bpermute_b32 v6, v64, v5
	s_waitcnt lgkmcnt(0)
	v_add_f32_e32 v6, v5, v6
	v_cndmask_b32_e64 v5, v6, v5, s[8:9]
	ds_bpermute_b32 v6, v65, v5
	s_waitcnt lgkmcnt(0)
	v_add_f32_e32 v6, v5, v6
	v_cndmask_b32_e64 v5, v6, v5, s[10:11]
	ds_bpermute_b32 v6, v66, v5
	s_waitcnt lgkmcnt(0)
	v_add_f32_e32 v6, v5, v6
	v_cndmask_b32_e64 v5, v6, v5, s[12:13]
	v_sub_f32_e64 v4, v4, v5
	ds_bpermute_b32 v7, v41, v4
	s_waitcnt lgkmcnt(0)
	v_max_f32_e32 v7, v7, v7
	v_max_f32_e64 v7, v4, v7
	v_cndmask_b32_e64 v7, v7, v4, s[2:3]
	ds_bpermute_b32 v8, v62, v7
	s_waitcnt lgkmcnt(0)
	v_max_f32_e32 v8, v8, v8
	v_max_f32_e64 v8, v7, v8
	v_cndmask_b32_e64 v7, v8, v7, s[4:5]
	ds_bpermute_b32 v8, v63, v7
	s_waitcnt lgkmcnt(0)
	v_max_f32_e32 v8, v8, v8
	v_max_f32_e64 v8, v7, v8
	v_cndmask_b32_e64 v7, v8, v7, s[6:7]
	ds_bpermute_b32 v8, v64, v7
	s_waitcnt lgkmcnt(0)
	v_max_f32_e32 v8, v8, v8
	v_max_f32_e64 v8, v7, v8
	v_cndmask_b32_e64 v7, v8, v7, s[8:9]
	ds_bpermute_b32 v8, v65, v7
	s_waitcnt lgkmcnt(0)
	v_max_f32_e32 v8, v8, v8
	v_max_f32_e64 v8, v7, v8
	v_cndmask_b32_e64 v7, v8, v7, s[10:11]
	ds_bpermute_b32 v8, v66, v7
	v_max_f32_e32 v9, v7, v7
	s_waitcnt lgkmcnt(0)
	v_max_f32_e32 v8, v8, v8
	v_max_f32_e32 v8, v9, v8
	v_add_u32_e64 v9, s23, v67
	ds_write_b32 v9, v4 offset:32768
	s_and_saveexec_b64 s[64:65], s[14:15]
	v_mov_b32_e32 v9, s53
	v_add_u32_e32 v9, 0xa0, v9
	ds_write2st64_b32 v9, v8, v6 offset0:192 offset1:193
	s_or_b64 exec, exec, s[64:65]
	s_and_b64 vcc, exec, s[20:21]
	s_cbranch_vccnz .LBB0_639
	s_nop 0
	v_readlane_b32 s64, v255, 57
	s_add_i32 s64, s60, s64
	s_nop 0
	v_cndmask_b32_e64 v8, v8, v7, s[12:13]
	v_mad_i64_i32 v[6:7], s[64:65], s64, v233, v[44:45]
	global_store_dword v[6:7], v4, off
	global_store_dword v[6:7], v8, off offset:256
	global_store_dword v[6:7], v5, off offset:512
.LBB0_639:
	ds_bpermute_b32 v4, v41, v3
	s_waitcnt lgkmcnt(0)
	v_add_f32_e32 v4, v3, v4
	v_cndmask_b32_e64 v3, v4, v3, s[2:3]
	ds_bpermute_b32 v4, v62, v3
	s_waitcnt lgkmcnt(0)
	v_add_f32_e32 v4, v3, v4
	v_cndmask_b32_e64 v3, v4, v3, s[4:5]
	ds_bpermute_b32 v4, v63, v3
	s_waitcnt lgkmcnt(0)
	v_add_f32_e32 v4, v3, v4
	v_cndmask_b32_e64 v3, v4, v3, s[6:7]
	ds_bpermute_b32 v4, v64, v3
	s_waitcnt lgkmcnt(0)
	v_add_f32_e32 v4, v3, v4
	v_cndmask_b32_e64 v3, v4, v3, s[8:9]
	ds_bpermute_b32 v4, v65, v3
	s_waitcnt lgkmcnt(0)
	v_add_f32_e32 v4, v3, v4
	v_cndmask_b32_e64 v3, v4, v3, s[10:11]
	ds_bpermute_b32 v4, v66, v3
	s_waitcnt lgkmcnt(0)
	v_add_f32_e32 v4, v3, v4
	v_cndmask_b32_e64 v3, v4, v3, s[12:13]
	v_sub_f32_e64 v2, v2, v3
	ds_bpermute_b32 v5, v41, v2
	s_waitcnt lgkmcnt(0)
	v_max_f32_e32 v5, v5, v5
	v_max_f32_e64 v5, v2, v5
	v_cndmask_b32_e64 v5, v5, v2, s[2:3]
	ds_bpermute_b32 v6, v62, v5
	s_waitcnt lgkmcnt(0)
	v_max_f32_e32 v6, v6, v6
	v_max_f32_e64 v6, v5, v6
	v_cndmask_b32_e64 v5, v6, v5, s[4:5]
	ds_bpermute_b32 v6, v63, v5
	s_waitcnt lgkmcnt(0)
	v_max_f32_e32 v6, v6, v6
	v_max_f32_e64 v6, v5, v6
	v_cndmask_b32_e64 v5, v6, v5, s[6:7]
	ds_bpermute_b32 v6, v64, v5
	s_waitcnt lgkmcnt(0)
	v_max_f32_e32 v6, v6, v6
	v_max_f32_e64 v6, v5, v6
	v_cndmask_b32_e64 v5, v6, v5, s[8:9]
	ds_bpermute_b32 v6, v65, v5
	s_waitcnt lgkmcnt(0)
	v_max_f32_e32 v6, v6, v6
	v_max_f32_e64 v6, v5, v6
	v_cndmask_b32_e64 v5, v6, v5, s[10:11]
	ds_bpermute_b32 v6, v66, v5
	v_max_f32_e32 v7, v5, v5
	s_waitcnt lgkmcnt(0)
	v_max_f32_e32 v6, v6, v6
	v_max_f32_e32 v6, v7, v6
	v_add_u32_e64 v7, s72, v67
	ds_write_b32 v7, v2 offset:32768
	s_and_saveexec_b64 s[64:65], s[14:15]
	v_mov_b32_e32 v7, s53
	v_add_u32_e32 v7, 0xc0, v7
	ds_write2st64_b32 v7, v6, v4 offset0:192 offset1:193
	s_or_b64 exec, exec, s[64:65]
	s_and_b64 vcc, exec, s[20:21]
	s_cbranch_vccnz .LBB0_643
	s_add_i32 s64, s60, s42
	v_cndmask_b32_e64 v6, v6, v5, s[12:13]
	v_mad_i64_i32 v[4:5], s[64:65], s64, v233, v[44:45]
	global_store_dword v[4:5], v2, off
	global_store_dword v[4:5], v6, off offset:256
	global_store_dword v[4:5], v3, off offset:512
.LBB0_643:
	ds_bpermute_b32 v2, v41, v1
	s_waitcnt lgkmcnt(0)
	v_add_f32_e32 v2, v1, v2
	v_cndmask_b32_e64 v1, v2, v1, s[2:3]
	ds_bpermute_b32 v2, v62, v1
	s_waitcnt lgkmcnt(0)
	v_add_f32_e32 v2, v1, v2
	v_cndmask_b32_e64 v1, v2, v1, s[4:5]
	ds_bpermute_b32 v2, v63, v1
	s_waitcnt lgkmcnt(0)
	v_add_f32_e32 v2, v1, v2
	v_cndmask_b32_e64 v1, v2, v1, s[6:7]
	ds_bpermute_b32 v2, v64, v1
	s_waitcnt lgkmcnt(0)
	v_add_f32_e32 v2, v1, v2
	v_cndmask_b32_e64 v1, v2, v1, s[8:9]
	ds_bpermute_b32 v2, v65, v1
	s_waitcnt lgkmcnt(0)
	v_add_f32_e32 v2, v1, v2
	v_cndmask_b32_e64 v1, v2, v1, s[10:11]
	ds_bpermute_b32 v2, v66, v1
	s_waitcnt lgkmcnt(0)
	v_add_f32_e32 v2, v1, v2
	v_cndmask_b32_e64 v1, v2, v1, s[12:13]
	v_sub_f32_e64 v0, v0, v1
	ds_bpermute_b32 v3, v41, v0
	s_waitcnt lgkmcnt(0)
	v_max_f32_e32 v3, v3, v3
	v_max_f32_e64 v3, v0, v3
	v_cndmask_b32_e64 v3, v3, v0, s[2:3]
	ds_bpermute_b32 v4, v62, v3
	s_waitcnt lgkmcnt(0)
	v_max_f32_e32 v4, v4, v4
	v_max_f32_e64 v4, v3, v4
	v_cndmask_b32_e64 v3, v4, v3, s[4:5]
	ds_bpermute_b32 v4, v63, v3
	s_waitcnt lgkmcnt(0)
	v_max_f32_e32 v4, v4, v4
	v_max_f32_e64 v4, v3, v4
	v_cndmask_b32_e64 v3, v4, v3, s[6:7]
	ds_bpermute_b32 v4, v64, v3
	s_waitcnt lgkmcnt(0)
	v_max_f32_e32 v4, v4, v4
	v_max_f32_e64 v4, v3, v4
	v_cndmask_b32_e64 v3, v4, v3, s[8:9]
	ds_bpermute_b32 v4, v65, v3
	s_waitcnt lgkmcnt(0)
	v_max_f32_e32 v4, v4, v4
	v_max_f32_e64 v4, v3, v4
	v_cndmask_b32_e64 v3, v4, v3, s[10:11]
	ds_bpermute_b32 v4, v66, v3
	v_max_f32_e32 v5, v3, v3
	s_waitcnt lgkmcnt(0)
	v_max_f32_e32 v4, v4, v4
	v_max_f32_e32 v4, v5, v4
	v_add_u32_e64 v5, s73, v67
	ds_write_b32 v5, v0 offset:32768
	s_and_saveexec_b64 s[64:65], s[14:15]
	v_mov_b32_e32 v5, s53
	v_add_u32_e32 v5, 0xe0, v5
	ds_write2st64_b32 v5, v4, v2 offset0:192 offset1:193
	s_or_b64 exec, exec, s[64:65]
	s_mov_b64 s[64:65], 0
	s_and_b64 vcc, exec, s[20:21]
	s_mov_b64 s[20:21], 0
	s_cbranch_vccnz .LBB0_647
	s_add_i32 s20, s60, s36
	v_cndmask_b32_e64 v4, v4, v3, s[12:13]
	v_mad_i64_i32 v[2:3], s[20:21], s20, v233, v[44:45]
	v_readlane_b32 s20, v254, 24
	v_readlane_b32 s64, v255, 58
	v_readlane_b32 s21, v254, 25
	v_readlane_b32 s65, v255, 59
	s_and_b64 s[20:21], s[20:21], exec
	s_and_b64 s[64:65], s[64:65], exec
	global_store_dword v[2:3], v0, off
	global_store_dword v[2:3], v4, off offset:256
	global_store_dword v[2:3], v1, off offset:512
.LBB0_647:
	v_lshl_add_u64 v[0:1], s[46:47], 0, v[42:43]
	v_mov_b64_e32 v[2:3], s[54:55]
	s_nop 0
	v_mad_u64_u32 v[2:3], s[46:47], v0, s68, v[2:3]
	v_mad_i32_i24 v3, v1, s68, v3
	s_lshl_b32 s96, s45, 7
	s_nop 0
	v_lshl_add_u64 v[0:1], v[2:3], 0, s[96:97]
	v_mov_b32_e32 v51, v97
	s_lshl_b32 s96, s45, 8
	v_lshl_add_u64 v[8:9], v[0:1], 0, v[50:51]
	v_lshl_add_u64 v[0:1], v[2:3], 0, s[96:97]
	s_lshl_b32 s96, s61, 7
	s_nop 0
	v_lshl_add_u64 v[0:1], v[0:1], 0, s[96:97]
	s_mov_b32 s45, 0x60000
	v_lshl_add_u64 v[10:11], v[0:1], 0, v[50:51]
	v_add_co_u32_e32 v0, vcc, s45, v8
	s_nop 0
	global_load_dwordx4 v[36:39], v[8:9], off offset:1024
	global_load_dwordx4 v[32:35], v[10:11], off offset:2048
	v_addc_co_u32_e32 v1, vcc, 0, v9, vcc
	v_add_co_u32_e32 v4, vcc, s45, v10
	s_mov_b64 s[46:47], 0x60400
	s_nop 0
	v_addc_co_u32_e32 v5, vcc, 0, v11, vcc
	global_load_dwordx4 v[0:3], v[0:1], off offset:1024
	s_nop 0
	s_nop 0
	global_load_dwordx4 v[4:7], v[4:5], off offset:2048
	v_lshl_add_u64 v[52:53], v[8:9], 0, s[46:47]
	s_mov_b64 s[46:47], 0x60800
	s_ashr_i32 s61, s60, 31
	s_nop 0
	v_lshl_add_u64 v[54:55], v[10:11], 0, s[46:47]
	s_lshl_b64 s[46:47], s[60:61], 8
	s_nop 0
	v_lshl_add_u64 v[56:57], v[46:47], 0, s[46:47]
	s_lshl_b64 s[46:47], s[60:61], 2
	s_add_u32 s92, s56, s46
	v_cndmask_b32_e64 v12, 0, 1, s[58:59]
	s_addc_u32 s93, s57, s47
	s_lshl_b64 s[46:47], s[60:61], 14
	v_lshl_or_b32 v96, v12, 13, v80
	v_lshl_add_u64 v[8:9], v[48:49], 0, s[46:47]
	s_mov_b32 s96, 0
	s_nop 0
	v_lshl_add_u64 v[58:59], v[8:9], 0, v[96:97]
	s_add_i32 s60, 0, 0xc000
	v_mov_b32_e32 v51, 0
	v_mov_b32_e32 v24, 0
	v_mov_b32_e32 v25, 0
	v_mov_b32_e32 v26, 0
	v_mov_b32_e32 v27, 0
	v_mov_b32_e32 v16, 0
	v_mov_b32_e32 v17, 0
	v_mov_b32_e32 v18, 0
	v_mov_b32_e32 v19, 0
	v_mov_b32_e32 v20, 0
	v_mov_b32_e32 v21, 0
	v_mov_b32_e32 v22, 0
	v_mov_b32_e32 v23, 0
	v_mov_b32_e32 v28, 0
	v_mov_b32_e32 v29, 0
	v_mov_b32_e32 v30, 0
	v_mov_b32_e32 v31, 0
	v_mov_b32_e32 v85, 0
	v_mov_b32_e32 v87, 0
	v_mov_b32_e32 v88, 0
	v_mov_b32_e32 v89, 0
	v_mov_b32_e32 v82, 0
	v_mov_b32_e32 v83, 0
	v_mov_b32_e32 v84, 0
	v_mov_b32_e32 v86, 0
	v_mov_b32_e32 v81, v79
	s_mov_b32 s61, 0
	s_waitcnt lgkmcnt(0)
	s_barrier
	s_branch .LBB0_650

.LBB0_649:
	v_sub_f32_e64 v32, v51, v60
	v_mul_f32_e32 v32, 0x3fb8aa3b, v32
	v_exp_f32_e32 v32, v32
	v_add_u32_e32 v34, s45, v75
	v_add3_u32 v86, s45, v71, v73
	v_add_f32_e64 v51, v61, v60
	v_pk_mul_f32 v[22:23], v[22:23], v[32:33] op_sel_hi:[1,0]
	v_pk_mul_f32 v[20:21], v[20:21], v[32:33] op_sel_hi:[1,0]
	v_pk_mul_f32 v[18:19], v[18:19], v[32:33] op_sel_hi:[1,0]
	v_pk_mul_f32 v[16:17], v[16:17], v[32:33] op_sel_hi:[1,0]
	v_pk_mul_f32 v[30:31], v[30:31], v[32:33] op_sel_hi:[1,0]
	v_pk_mul_f32 v[28:29], v[28:29], v[32:33] op_sel_hi:[1,0]
	v_pk_mul_f32 v[26:27], v[26:27], v[32:33] op_sel_hi:[1,0]
	v_pk_mul_f32 v[24:25], v[24:25], v[32:33] op_sel_hi:[1,0]
	v_add_u32_e64 v32, s45, v74
	v_add3_u32 v60, v32, v73, v71
	v_add3_u32 v61, v34, v73, v71
	v_add_u32_e32 v87, v86, v72
	v_add_u32_e32 v88, v86, v76
	s_waitcnt lgkmcnt(0)
	s_barrier
	ds_read_b64_tr_b16 v[32:33], v60
	ds_read_b64_tr_b16 v[34:35], v61 offset:1024
	ds_read_b64_tr_b16 v[36:37], v87
	ds_read_b64_tr_b16 v[38:39], v88 offset:1024
	s_mov_b32 s89, s88
	s_mov_b32 s90, s88
	s_mov_b32 s91, s88
	v_mov_b64_e32 v[82:83], s[88:89]
	v_mov_b64_e32 v[84:85], s[90:91]
	v_add_u32_e32 v89, v86, v77
	v_add_u32_e32 v86, v86, v78
	s_waitcnt lgkmcnt(0)
	v_mfma_f32_16x16x32_bf16 v[20:23], v[36:39], v[32:35], v[20:23]
	s_add_i32 s61, s61, 1
	s_add_i32 s60, s60, 4
	s_mov_b64 s[46:47], 0x100
	v_mfma_f32_16x16x32_bf16 v[16:19], v[36:39], v[82:85], v[16:19]
	ds_read_b64_tr_b16 v[36:37], v89
	ds_read_b64_tr_b16 v[38:39], v86 offset:1024
	s_add_u32 s92, s92, 4
	s_waitcnt lgkmcnt(0)
	v_mfma_f32_16x16x32_bf16 v[28:31], v[36:39], v[32:35], v[28:31]
	v_lshl_add_u64 v[56:57], v[56:57], 0, s[46:47]
	s_addc_u32 s93, s93, 0
	s_nop 0
	s_mov_b64 s[46:47], 0x4000
	v_mfma_f32_16x16x32_bf16 v[24:27], v[36:39], v[82:85], v[24:27]
	ds_read_b64_tr_b16 v[32:33], v60 offset:8192
	ds_read_b64_tr_b16 v[34:35], v61 offset:9216
	ds_read_b64_tr_b16 v[36:37], v87 offset:8192
	ds_read_b64_tr_b16 v[38:39], v88 offset:9216
	s_addk_i32 s96, 0x4000
	s_nop 0
	v_lshl_add_u64 v[58:59], v[58:59], 0, s[46:47]
	s_waitcnt lgkmcnt(0)
	s_nop 0
	v_mfma_f32_16x16x32_bf16 v[20:23], v[36:39], v[32:35], v[20:23]
	v_add_u32_e32 v81, 0x100, v81
	s_cmp_eq_u32 s61, 64
	s_nop 0
	v_mfma_f32_16x16x32_bf16 v[16:19], v[36:39], v[82:85], v[16:19]
	ds_read_b64_tr_b16 v[36:37], v89 offset:8192
	ds_read_b64_tr_b16 v[38:39], v86 offset:9216
	s_nop 2
	v_mov_b32_e32 v87, v21
	v_mov_b32_e32 v88, v22
	s_waitcnt lgkmcnt(0)
	v_mfma_f32_16x16x32_bf16 v[28:31], v[36:39], v[32:35], v[28:31]
	v_mov_b64_e32 v[34:35], v[14:15]
	v_mov_b64_e32 v[32:33], v[12:13]
	v_mov_b32_e64 v89, v23
	v_mfma_f32_16x16x32_bf16 v[24:27], v[36:39], v[82:85], v[24:27]
	v_mov_b64_e32 v[38:39], v[10:11]
	v_mov_b64_e32 v[36:37], v[8:9]
	v_mov_b32_e32 v85, v20
	s_nop 0
	v_mov_b32_e32 v82, v28
	v_mov_b32_e32 v83, v29
	v_mov_b32_e32 v84, v30
	v_mov_b32_e32 v86, v31
	s_cbranch_scc1 .LBB0_614
.LBB0_650:
	s_waitcnt vmcnt(1)
	v_mov_b64_e32 v[10:11], v[2:3]
	v_mov_b64_e32 v[8:9], v[0:1]
	v_mov_b32_e64 v0, s60
	ds_read2st64_b32 v[60:61], v0 offset1:1
	ds_read_b32 v0, v81
	v_lshl_add_u64 v[2:3], s[70:71], 0, v[58:59]
	s_mov_b32 s45, 0x2ee00000
	s_waitcnt vmcnt(0)
	v_mov_b64_e32 v[14:15], v[6:7]
	v_add_co_u32_e32 v2, vcc, s45, v2
	v_mov_b64_e32 v[12:13], v[4:5]
	v_cvt_pk_bf16_f32 v4, v85, v87
	v_cvt_pk_bf16_f32 v5, v88, v89
	v_addc_co_u32_e32 v3, vcc, 0, v3, vcc
	s_nop 0
	global_store_dwordx2 v[2:3], v[4:5], off
	v_cvt_pk_bf16_f32 v4, v82, v83
	v_cvt_pk_bf16_f32 v5, v84, v86
	global_store_dwordx2 v[2:3], v[4:5], off offset:32
	s_and_saveexec_b64 s[46:47], s[64:65]
	s_cbranch_execz .LBB0_652
	v_lshl_add_u64 v[2:3], s[70:71], 0, v[56:57]
	v_add_co_u32_e32 v2, vcc, 0x36e00000, v2
	s_nop 1
	v_addc_co_u32_e32 v3, vcc, 0, v3, vcc
	global_store_dwordx4 v[2:3], v[16:19], off
	global_store_dwordx4 v[2:3], v[24:27], off offset:64
.LBB0_652:
	s_or_b64 exec, exec, s[46:47]
	s_and_saveexec_b64 s[46:47], s[20:21]
	s_cbranch_execz .LBB0_654
	s_nop 0
	global_store_dword v97, v51, s[92:93]
.LBB0_654:
	s_or_b64 exec, exec, s[46:47]
	s_waitcnt lgkmcnt(1)
	v_max_f32_e32 v1, v60, v60
	v_max_f32_e32 v2, v51, v51
	v_max_f32_e32 v60, v2, v1
	s_waitcnt lgkmcnt(0)
	v_sub_f32_e64 v0, v0, v60
	v_mul_f32_e32 v0, 0x3fb8aa3b, v0
	v_exp_f32_e32 v4, v0
	v_lshlrev_b32_e32 v0, 16, v36
	v_and_b32_e32 v1, 0xffff0000, v36
	v_lshlrev_b32_e32 v2, 16, v37
	s_nop 0
	v_and_b32_e32 v3, 0xffff0000, v37
	v_pk_mul_f32 v[0:1], v[4:5], v[0:1] op_sel_hi:[0,1]
	v_pk_mul_f32 v[2:3], v[4:5], v[2:3] op_sel_hi:[0,1]
	s_and_b32 s45, s96, 0x4000
	v_cvt_pk_bf16_f32 v0, v0, v1
	v_cvt_pk_bf16_f32 v1, v2, v3
	v_lshlrev_b32_e32 v2, 16, v38
	s_nop 0
	v_and_b32_e32 v3, 0xffff0000, v38
	v_lshlrev_b32_e32 v6, 16, v39
	s_nop 0
	v_and_b32_e32 v7, 0xffff0000, v39
	s_add_i32 s45, s45, 0
	s_nop 0
	v_pk_mul_f32 v[2:3], v[4:5], v[2:3] op_sel_hi:[0,1]
	v_pk_mul_f32 v[4:5], v[4:5], v[6:7] op_sel_hi:[0,1]
	v_cvt_pk_bf16_f32 v2, v2, v3
	v_cvt_pk_bf16_f32 v3, v4, v5
	v_add3_u32 v4, s45, v69, v68
	ds_write_b128 v4, v[0:3]
	v_add3_u32 v0, s45, v70, v68
	s_cmp_gt_u32 s61, 61
	s_nop 0
	ds_write_b128 v0, v[32:35]
	s_cbranch_scc0 .LBB0_648
	v_mov_b64_e32 v[0:1], v[8:9]
	v_mov_b64_e32 v[4:5], v[12:13]
	v_mov_b64_e32 v[2:3], v[10:11]
	v_mov_b64_e32 v[6:7], v[14:15]
	s_branch .LBB0_649

.LBB0_657:
	s_add_u32 s34, s70, 0x2ee00000
	s_addc_u32 s35, s71, 0
	s_nop 0
	v_readlane_b32 s4, v254, 5
	v_readlane_b32 s5, v254, 6
	s_cmp_le_i32 s4, s89
	s_cselect_b64 s[2:3], -1, 0
	s_cmp_lt_i32 s89, s5
	s_cselect_b64 s[4:5], -1, 0
	s_and_b64 s[6:7], s[2:3], s[4:5]
	s_andn2_b64 vcc, exec, s[6:7]
	s_cbranch_vccnz .LBB0_806
	s_and_b64 vcc, exec, s[0:1]
	s_cbranch_vccnz .LBB0_712
	s_mov_b32 s2, s97
	s_mov_b32 s4, s93
	s_waitcnt vmcnt(0)
	v_mbcnt_lo_u32_b32 v0, -1, s2
	v_mbcnt_hi_u32_b32 v0, -1, v0
	v_add_u32_e64 v0, s64, v0
	v_readlane_b32 s10, v254, 42
	s_lshl_b32 s5, s4, 2
	s_nop 0
	v_readlane_b32 s11, v254, 43
	s_and_b64 s[2:3], s[10:11], exec
	s_cselect_b32 s8, s5, s4
	s_add_i32 s5, s5, 4
	s_and_b64 s[2:3], s[10:11], exec
	v_writelane_b32 v255, s90, 55
	s_cselect_b32 s45, s5, 0x400
	s_cmp_ge_i32 s8, s45
	s_nop 0
	v_writelane_b32 v255, s91, 56
	s_mov_b32 s90, s60
	v_readfirstlane_b32 s2, v0
	s_cbranch_scc1 .LBB0_711
	s_nop 0
	v_readlane_b32 s4, v254, 22
	s_ashr_i32 s3, s2, 6
	s_nop 0
	v_readlane_b32 s5, v254, 23
	s_lshl_b32 s96, s4, 10
	s_nop 0
	v_readlane_b32 s12, v253, 18
	v_and_b32_e32 v1, 63, v0
	s_and_b32 s46, s3, 3
	s_lshl_b64 s[4:5], s[96:97], 2
	s_nop 0
	v_readlane_b32 s20, v253, 26
	v_bfe_u32 v3, v0, 4, 2
	v_lshlrev_b32_e32 v96, 2, v1
	v_and_b32_e32 v102, 15, v0
	v_readlane_b32 s21, v253, 27
	s_add_u32 s4, s20, s4
	s_mulk_i32 s3, 0x1140
	v_lshl_add_u64 v[110:111], s[58:59], 0, v[96:97]
	v_lshlrev_b32_e32 v96, 5, v3
	s_addc_u32 s5, s21, s5
	s_add_i32 s47, s3, 0
	s_ashr_i32 s9, s2, 7
	v_lshl_add_u64 v[4:5], s[70:71], 0, v[96:97]
	s_mov_b64 s[2:3], 0x36e00000
	v_lshlrev_b32_e32 v96, 7, v102
	v_and_b32_e32 v106, 48, v0
	v_mov_b32_e64 v107, v97
	v_lshl_add_u64 v[112:113], v[4:5], 0, s[2:3]
	v_lshl_add_u64 v[4:5], s[34:35], 0, v[96:97]
	v_lshlrev_b32_e32 v1, 4, v0
	v_lshlrev_b32_e32 v129, 2, v3
	v_lshl_add_u64 v[114:115], v[4:5], 0, v[106:107]
	v_and_b32_e32 v96, 0x70, v1
	v_bfe_u32 v1, v0, 2, 2
	v_lshlrev_b32_e32 v4, 3, v0
	s_nop 0
	v_bfe_u32 v6, v0, 1, 1
	v_and_b32_e32 v133, 8, v4
	v_lshlrev_b32_e32 v7, 2, v1
	v_lshlrev_b32_e32 v4, 2, v96
	v_mov_b32_e32 v5, v97
	v_or_b32_e32 v103, 3, v129
	v_or_b32_e32 v128, 2, v129
	v_bfe_u32 v131, v0, 3, 3
	v_lshl_add_u64 v[116:117], s[4:5], 0, v[4:5]
	v_bitop3_b32 v5, v129, v0, 15 bitop3:0x78
	v_bitop3_b32 v10, v128, v0, 15 bitop3:0x78
	v_bitop3_b32 v11, v103, v0, 15 bitop3:0x78
	v_bitop3_b32 v0, v7, v6, v3 bitop3:0x36
	v_lshlrev_b32_e32 v137, 4, v0
	v_or_b32_e32 v0, v129, v1
	v_lshlrev_b32_e32 v139, 8, v0
	v_or_b32_e32 v0, 2, v6
	v_bitop3_b32 v0, v7, v0, v3 bitop3:0x36
	v_lshlrev_b32_e32 v141, 4, v0
	v_or_b32_e32 v0, 4, v6
	v_bitop3_b32 v0, v7, v0, v3 bitop3:0x36
	s_and_b32 s48, s9, -2
	v_lshlrev_b32_e32 v199, 4, v0
	v_or_b32_e32 v0, 6, v6
	s_lshl_b32 s10, s46, 2
	s_lshl_b32 s4, s48, 14
	s_nop 0
	v_bitop3_b32 v0, v7, v0, v3 bitop3:0x36
	s_add_i32 s52, s4, 0
	s_or_b32 s4, s10, 1
	v_lshlrev_b32_e32 v204, 4, v0
	v_or_b32_e32 v0, 8, v6
	v_lshl_or_b32 v122, s4, 2, v3
	s_lshl_b32 s58, s4, 10
	s_or_b32 s4, s10, 2
	v_bitop3_b32 v0, v7, v0, v3 bitop3:0x36
	v_lshl_or_b32 v124, s4, 2, v3
	s_lshl_b32 s59, s4, 10
	s_or_b32 s4, s10, 3
	v_lshlrev_b32_e32 v205, 4, v0
	v_or_b32_e32 v0, 10, v6
	v_lshl_or_b32 v126, s4, 2, v3
	s_lshl_b32 s60, s4, 10
	s_lshl_b32 s4, s9, 14
	v_bitop3_b32 v0, v7, v0, v3 bitop3:0x36
	s_bitset1_b32 s4, 14
	v_lshlrev_b32_e32 v206, 4, v0
	v_or_b32_e32 v0, 12, v6
	s_nop 0
	s_add_i32 s47, s47, 0x10000
	s_lshl_b32 s11, s46, 4
	s_xor_b32 s49, s46, 3
	s_lshl_b32 s53, s46, 12
	s_add_i32 s61, s4, 0
	v_bitop3_b32 v0, v7, v0, v3 bitop3:0x36
	s_cmp_eq_u32 s46, 0
	v_lshlrev_b32_e32 v207, 4, v0
	v_or_b32_e32 v0, 14, v6
	s_nop 0
	v_readlane_b32 s13, v253, 19
	v_or_b32_e32 v104, s11, v102
	v_or_b32_e32 v120, s11, v3
	s_cselect_b64 s[10:11], -1, 0
	s_cmp_lg_u32 s46, 0
	v_bitop3_b32 v0, v7, v0, v3 bitop3:0x36
	v_readlane_b32 s14, v253, 20
	v_readlane_b32 s15, v253, 21
	v_bitop3_b32 v9, v129, v102, 1 bitop3:0x36
	s_cselect_b64 s[12:13], -1, 0
	s_cmp_gt_u32 s46, 1
	v_lshlrev_b32_e32 v208, 4, v0
	v_lshlrev_b32_e32 v0, 4, v5
	v_mov_b32_e64 v1, v97
	v_readlane_b32 s16, v253, 22
	v_readlane_b32 s17, v253, 23
	s_cselect_b64 s[14:15], -1, 0
	s_cmp_eq_u32 s46, 3
	v_lshl_add_u64 v[142:143], s[54:55], 0, v[0:1]
	v_lshlrev_b32_e32 v0, 4, v9
	s_nop 0
	v_readlane_b32 s18, v253, 24
	v_readlane_b32 s19, v253, 25
	v_or_b32_e32 v135, 1, v129
	s_cselect_b64 s[16:17], -1, 0
	s_cmp_lg_u32 s46, 3
	s_nop 0
	v_lshl_add_u64 v[144:145], s[54:55], 0, v[0:1]
	v_lshlrev_b32_e32 v0, 4, v10
	v_lshlrev_b32_e32 v2, 3, v3
	v_lshl_add_u32 v8, v102, 1, s47
	v_lshl_add_u32 v4, v96, 1, s47
	s_cselect_b64 s[18:19], -1, 0
	s_nop 0
	v_mul_u32_u24_e32 v12, 0x440, v3
	v_mul_u32_u24_e32 v13, 0x110, v135
	v_mul_u32_u24_e32 v14, 0x110, v128
	v_mul_u32_u24_e32 v15, 0x110, v103
	v_mul_u32_u24_e32 v3, 0x110, v131
	v_lshl_add_u32 v6, v131, 2, s47
	s_cmp_gt_u32 s49, 1
	s_nop 0
	v_lshl_add_u64 v[146:147], s[54:55], 0, v[0:1]
	v_lshlrev_b32_e32 v0, 4, v11
	s_nop 0
	v_lshl_add_u64 v[108:109], s[54:55], 0, v[106:107]
	v_cmp_eq_u32_e64 s[2:3], 0, v102
	v_lshl_add_u64 v[118:119], s[78:79], 0, v[96:97]
	v_or_b32_e32 v105, 17, v129
	v_or_b32_e32 v130, 16, v129
	v_or_b32_e32 v107, 19, v129
	v_or_b32_e32 v132, 18, v129
	v_or_b32_e32 v121, 33, v129
	v_or_b32_e32 v134, 32, v129
	v_or_b32_e32 v123, 35, v129
	v_or_b32_e32 v136, 34, v129
	v_or_b32_e32 v125, 49, v129
	v_or_b32_e32 v138, 48, v129
	v_or_b32_e32 v127, 51, v129
	v_or_b32_e32 v140, 50, v129
	s_cselect_b64 s[20:21], -1, 0
	s_nop 0
	v_lshl_add_u64 v[148:149], s[54:55], 0, v[0:1]
	v_lshlrev_b32_e32 v150, 1, v2
	v_lshlrev_b32_e32 v96, 1, v96
	v_add_u32_e32 v209, v4, v3
	v_add_u32_e32 v210, v8, v12
	v_add_u32_e32 v211, v8, v13
	v_add_u32_e32 v212, v8, v14
	v_add_u32_e64 v213, v8, v15
	v_add_u32_e32 v214, 0x1000, v6
	v_readlane_b32 s22, v253, 28
	v_readlane_b32 s23, v253, 29
	v_readlane_b32 s24, v253, 30
	v_readlane_b32 s25, v253, 31
	v_readlane_b32 s26, v253, 32
	v_readlane_b32 s27, v253, 33
	s_branch .LBB0_662

.LBB0_662:
	s_ashr_i32 s9, s8, 31
	s_lshl_b64 s[24:25], s[8:9], 6
	s_ashr_i32 s4, s8, 3
	s_waitcnt vmcnt(7)
	v_or_b32_e32 v24, s24, v104
	s_and_b32 s9, s4, -8
	v_mad_u64_u32 v[152:153], s[4:5], v24, s68, v[108:109]
	v_lshl_or_b32 v24, s49, 4, v102
	v_or_b32_e32 v24, s24, v24
	s_nop 0
	v_mad_u64_u32 v[154:155], s[4:5], v24, s68, v[108:109]
	v_or_b32_e32 v24, s24, v120
	s_nop 0
	v_mad_u64_u32 v[156:157], s[4:5], v24, s68, v[142:143]
	v_or_b32_e32 v24, s24, v122
	s_nop 0
	v_mad_u64_u32 v[158:159], s[4:5], v24, s68, v[144:145]
	v_or_b32_e32 v24, s24, v124
	s_nop 0
	v_mad_u64_u32 v[160:161], s[4:5], v24, s68, v[146:147]
	v_or_b32_e32 v24, s24, v126
	s_nop 0
	v_mad_u64_u32 v[162:163], s[4:5], v24, s68, v[148:149]
	v_or_b32_e32 v26, s24, v102
	v_mov_b64_e32 v[24:25], s[54:55]
	v_mad_u64_u32 v[24:25], s[4:5], v26, s68, v[24:25]
	v_mad_i32_i24 v25, s25, v234, v25
	s_waitcnt vmcnt(3)
	v_mov_b32_e32 v151, v97
	v_lshl_add_u64 v[164:165], v[24:25], 0, v[150:151]
	v_or_b32_e32 v24, 16, v102
	v_or_b32_e32 v24, s24, v24
	v_mad_u64_u32 v[166:167], s[4:5], v24, s68, v[108:109]
	v_or_b32_e32 v24, 32, v102
	v_or_b32_e32 v24, s24, v24
	v_mad_u64_u32 v[168:169], s[4:5], v24, s68, v[108:109]
	v_or_b32_e32 v24, 48, v102
	v_or_b32_e32 v24, s24, v24
	v_mad_u64_u32 v[170:171], s[4:5], v24, s68, v[108:109]
	s_mov_b64 s[4:5], 0x18400
	s_nop 0
	s_nop 0
	v_lshl_add_u64 v[172:173], v[164:165], 0, s[4:5]
	s_mov_b64 s[4:5], 0x30400
	v_lshl_add_u64 v[174:175], v[164:165], 0, s[4:5]
	s_mov_b64 s[4:5], 0x48400
	s_and_b32 s64, s8, 63
	s_nop 0
	v_mad_i32_i24 v153, s25, v234, v153
	v_mad_i32_i24 v155, s25, v234, v155
	v_mad_i32_i24 v157, s25, v234, v157
	v_mad_i32_i24 v159, s25, v234, v159
	v_mad_i32_i24 v161, s25, v234, v161
	v_mad_i32_i24 v163, s25, v234, v163
	v_mad_i32_i24 v167, s25, v234, v167
	v_mad_i32_i24 v169, s25, v234, v169
	v_mad_i32_i24 v171, s25, v234, v171
	v_lshl_add_u64 v[176:177], v[164:165], 0, s[4:5]
	s_mov_b32 s22, 0
	s_mov_b64 s[4:5], -1
	s_branch .LBB0_664

.LBB0_664:
	s_add_i32 s65, s22, s48
	s_lshl_b32 s22, s65, 7
	s_ashr_i32 s23, s22, 31
	s_lshl_b64 s[22:23], s[22:23], 1
	s_waitcnt vmcnt(7)
	v_lshl_add_u64 v[24:25], v[156:157], 0, s[22:23]
	s_mov_b64 s[26:27], 0x800
	v_lshl_add_u64 v[26:27], v[24:25], 0, s[26:27]
	s_add_i32 m0, s52, s53
	s_waitcnt lgkmcnt(0)
	s_barrier
	s_nop 0
	global_load_lds_dwordx4 v[26:27], off
	v_lshl_add_u64 v[26:27], v[158:159], 0, s[22:23]
	s_waitcnt vmcnt(0)
	s_nop 0
	v_lshl_add_u64 v[28:29], v[26:27], 0, s[26:27]
	s_add_i32 m0, s52, s58
	s_andn2_b64 vcc, exec, s[12:13]
	global_load_lds_dwordx4 v[28:29], off
	v_lshl_add_u64 v[28:29], v[160:161], 0, s[22:23]
	v_lshl_add_u64 v[30:31], v[28:29], 0, s[26:27]
	s_add_i32 m0, s52, s59
	s_nop 0
	global_load_lds_dwordx4 v[30:31], off
	v_lshl_add_u64 v[30:31], v[162:163], 0, s[22:23]
	v_lshl_add_u64 v[32:33], v[30:31], 0, s[26:27]
	s_add_i32 m0, s52, s60
	s_nop 0
	s_mov_b64 s[22:23], 0x900
	global_load_lds_dwordx4 v[32:33], off
	v_lshl_add_u64 v[24:25], v[24:25], 0, s[22:23]
	s_add_i32 m0, s61, s53
	s_lshl_b32 s26, s65, 6
	global_load_lds_dwordx4 v[24:25], off
	v_lshl_add_u64 v[24:25], v[26:27], 0, s[22:23]
	s_add_i32 m0, s61, s58
	s_ashr_i32 s27, s26, 31
	global_load_lds_dwordx4 v[24:25], off
	v_lshl_add_u64 v[24:25], v[28:29], 0, s[22:23]
	s_add_i32 m0, s61, s59
	s_nop 0
	global_load_lds_dwordx4 v[24:25], off
	v_lshl_add_u64 v[24:25], v[30:31], 0, s[22:23]
	s_add_i32 m0, s61, s60
	s_lshl_b64 s[22:23], s[26:27], 1
	global_load_lds_dwordx4 v[24:25], off
	v_lshl_add_u64 v[28:29], v[152:153], 0, s[22:23]
	v_lshl_add_u64 v[36:37], v[164:165], 0, s[22:23]
	global_load_dwordx4 v[24:27], v[28:29], off
	s_nop 0
	s_nop 0
	global_load_dwordx4 v[28:31], v[28:29], off offset:64
	s_nop 0
	s_nop 0
	global_load_dwordx4 v[32:35], v[36:37], off offset:1024
	s_nop 0
	s_nop 0
	global_load_dwordx4 v[36:39], v[36:37], off offset:1088
	s_cbranch_vccnz .LBB0_704
	s_nop 0
	v_lshl_add_u64 v[8:9], s[26:27], 1, v[166:167]
	global_load_dwordx4 v[0:3], v[8:9], off offset:1024
	s_nop 0
	s_nop 0
	global_load_dwordx4 v[8:11], v[8:9], off offset:1088
	s_andn2_b64 vcc, exec, s[14:15]
	s_cbranch_vccz .LBB0_705

.LBB0_667:
	v_lshl_add_u64 v[20:21], s[26:27], 1, v[170:171]
	global_load_dwordx4 v[12:15], v[20:21], off offset:1024
	s_nop 0
	s_nop 0
	global_load_dwordx4 v[20:23], v[20:21], off offset:1088
.LBB0_668:
	s_xor_b64 s[26:27], s[4:5], -1
	s_add_i32 s4, s65, s9
	s_lshl_b32 s4, s4, 6
	s_or_b32 s4, s4, s64
	s_ashr_i32 s5, s4, 31
	s_nop 0
	v_mad_i64_i32 v[40:41], s[22:23], s4, v233, v[110:111]
	s_lshl_b64 s[4:5], s[4:5], 2
	s_add_u32 s4, s56, s4
	s_addc_u32 s5, s57, s5
	s_nop 0
	global_load_dword v151, v[40:41], off
	global_load_dword v215, v[40:41], off offset:256
	global_load_dword v216, v[40:41], off offset:512
	global_load_dword v217, v97, s[4:5]
	s_or_b32 s4, s65, 1
	s_add_i32 s22, s4, s9
	s_lshl_b32 s22, s22, 6
	s_lshl_b32 s4, s4, 6
	s_or_b32 s22, s22, s64
	s_ashr_i32 s5, s4, 31
	s_ashr_i32 s23, s22, 31
	s_waitcnt vmcnt(0)
	s_lshl_b64 s[4:5], s[4:5], 1
	s_nop 0
	v_mad_i64_i32 v[180:181], s[28:29], s22, v233, v[110:111]
	s_lshl_b64 s[22:23], s[22:23], 2
	s_add_u32 s28, s56, s22
	v_lshl_add_u64 v[178:179], v[154:155], 0, s[4:5]
	s_addc_u32 s29, s57, s23
	s_nop 0
	v_lshl_add_u64 v[182:183], v[164:165], 0, s[4:5]
	v_lshl_add_u64 v[184:185], v[172:173], 0, s[4:5]
	v_lshl_add_u64 v[186:187], v[174:175], 0, s[4:5]
	v_lshl_add_u64 v[188:189], v[176:177], 0, s[4:5]
	s_mov_b32 s22, 0
	s_mov_b64 s[30:31], -1
	s_waitcnt vmcnt(0) lgkmcnt(0)
	s_barrier
	s_branch .LBB0_672

.LBB0_670:
	s_nop 0
	global_load_dword v151, v[180:181], off
	global_load_dword v215, v[180:181], off offset:256
	global_load_dword v216, v[180:181], off offset:512
	global_load_dword v217, v97, s[28:29]

.LBB0_672:
	s_or_b32 s4, s22, s65
	s_add_i32 s5, s4, s9
	s_lshl_b32 s5, s5, 6
	s_or_b32 s38, s5, s64
	s_ashr_i32 s39, s38, 31
	s_lshl_b64 s[40:41], s[38:39], 8
	s_nop 0
	v_lshl_add_u64 v[44:45], v[112:113], 0, s[40:41]
	s_and_b64 s[40:41], s[30:31], exec
	s_cselect_b32 s5, s46, s49
	s_lshl_b64 s[38:39], s[38:39], 14
	s_nop 0
	v_lshl_add_u64 v[192:193], v[114:115], 0, s[38:39]
	v_add_co_u32_e32 v56, vcc, s75, v192
	s_nop 0
	global_load_dwordx4 v[48:51], v[44:45], off offset:16
	global_load_dwordx4 v[52:55], v[44:45], off
	global_load_dwordx4 v[40:43], v[44:45], off offset:144
	s_nop 0
	s_nop 0
	global_load_dwordx4 v[44:47], v[44:45], off offset:128
	v_addc_co_u32_e32 v57, vcc, 0, v193, vcc
	s_nop 0
	global_load_dwordx4 v[88:91], v[192:193], off
	global_load_dwordx4 v[92:95], v[192:193], off offset:64
	global_load_dwordx4 v[80:83], v[192:193], off offset:2048
	global_load_dwordx4 v[84:87], v[192:193], off offset:2112
	global_load_dwordx4 v[72:75], v[56:57], off
	global_load_dwordx4 v[76:79], v[56:57], off offset:64
	global_load_dwordx4 v[64:67], v[56:57], off offset:2048
	global_load_dwordx4 v[68:71], v[56:57], off offset:2112
	s_waitcnt vmcnt(14)
	v_max_f32_e32 v56, v215, v215
	s_waitcnt vmcnt(12)
	v_max_f32_e32 v57, v217, v217
	v_max_f32_e32 v57, v57, v56
	v_sub_f32_e32 v56, v217, v57
	v_mul_f32_e32 v56, 0x3fb8aa3b, v56
	v_exp_f32_e32 v58, v56
	v_add_f32_e32 v56, v216, v57
	v_mul_f32_e32 v56, 0xbfb8aa3b, v56
	s_lshl_b32 s92, s5, 4
	v_exp_f32_e32 v59, v56
	v_or_b32_e32 v56, s92, v102
	v_and_b32_e32 v101, 64, v227
	v_or_b32_e32 v60, v101, v56
	v_or_b32_e32 v62, v101, v129
	v_lshlrev_b32_e32 v60, 2, v60
	v_lshlrev_b32_e32 v99, 2, v62
	ds_bpermute_b32 v57, v60, v57
	ds_bpermute_b32 v62, v99, v151
	ds_bpermute_b32 v98, v60, v58
	ds_bpermute_b32 v100, v60, v59
	v_mfma_f32_16x16x32_bf16 v[58:61], v[32:35], v[24:27], 0
	v_cmp_le_u32_e32 vcc, v129, v56
	s_waitcnt lgkmcnt(2)
	v_sub_f32_e64 v62, v62, v57
	v_mul_f32_e32 v62, 0x3fb8aa3b, v62
	v_mfma_f32_16x16x32_bf16 v[58:61], v[36:39], v[28:31], v[58:61]
	v_exp_f32_e64 v62, v62
	s_cmp_eq_u32 s5, 0
	s_nop 5
	v_mul_f32_e32 v58, v58, v62
	v_cndmask_b32_e32 v62, 0, v58, vcc
	v_or_b32_e32 v58, v101, v135
	v_lshlrev_b32_e32 v58, 2, v58
	ds_bpermute_b32 v58, v58, v151
	v_cmp_lt_u32_e32 vcc, v129, v56
	s_waitcnt lgkmcnt(0)
	v_sub_f32_e64 v58, v58, v57
	v_mul_f32_e32 v58, 0x3fb8aa3b, v58
	v_exp_f32_e32 v58, v58
	s_nop 0
	v_mul_f32_e32 v58, v59, v58
	v_cndmask_b32_e32 v63, 0, v58, vcc
	v_or_b32_e32 v58, v101, v128
	v_or_b32_e32 v59, v101, v103
	v_lshlrev_b32_e32 v58, 2, v58
	v_lshlrev_b32_e32 v59, 2, v59
	ds_bpermute_b32 v58, v58, v151
	ds_bpermute_b32 v59, v59, v151
	v_cmp_le_u32_e32 vcc, v128, v56
	s_nop 0
	v_cvt_pk_bf16_f32 v191, v62, v63
	s_waitcnt lgkmcnt(1)
	v_sub_f32_e32 v58, v58, v57
	s_waitcnt lgkmcnt(0)
	v_sub_f32_e32 v59, v59, v57
	v_mul_f32_e32 v58, 0x3fb8aa3b, v58
	v_mul_f32_e32 v59, 0x3fb8aa3b, v59
	v_exp_f32_e64 v58, v58
	v_exp_f32_e32 v59, v59
	s_nop 0
	v_pk_mul_f32 v[58:59], v[60:61], v[58:59]
	s_nop 0
	s_nop 0
	v_cvt_pk_bf16_f32 v58, v58, v59
	v_cndmask_b32_e32 v59, 0, v58, vcc
	v_lshrrev_b32_e32 v58, 16, v58
	v_cmp_le_u32_e32 vcc, v103, v56
	s_nop 0
	v_and_b32_e32 v60, 0xffff0000, v191
	s_nop 0
	v_cndmask_b32_e32 v58, 0, v58, vcc
	v_perm_b32 v194, v58, v59, s84
	v_lshlrev_b32_e32 v59, 16, v194
	v_lshlrev_b32_e32 v58, 16, v191
	v_and_b32_e32 v61, 0xffff0000, v194
	v_pk_add_f32 v[58:59], v[58:59], v[60:61]
	s_nop 0
	v_add_f32_e32 v58, v58, v59
	v_add_f32_e32 v190, 0, v58
	s_cbranch_scc1 .LBB0_674
	v_or_b32_e32 v62, v101, v130
	v_or_b32_e32 v63, v101, v105
	v_lshlrev_b32_e32 v62, 2, v62
	v_lshlrev_b32_e32 v63, 2, v63
	ds_bpermute_b32 v62, v62, v151
	ds_bpermute_b32 v63, v63, v151
	v_mfma_f32_16x16x32_bf16 v[58:61], v[0:3], v[24:27], 0
	v_cmp_le_u32_e32 vcc, v130, v56
	s_waitcnt lgkmcnt(1)
	v_sub_f32_e32 v62, v62, v57
	s_waitcnt lgkmcnt(0)
	v_sub_f32_e64 v63, v63, v57
	v_mul_f32_e32 v62, 0x3fb8aa3b, v62
	v_mul_f32_e32 v63, 0x3fb8aa3b, v63
	v_mfma_f32_16x16x32_bf16 v[58:61], v[8:11], v[28:31], v[58:61]
	v_exp_f32_e64 v62, v62
	v_exp_f32_e32 v63, v63
	s_nop 5
	v_pk_mul_f32 v[58:59], v[58:59], v[62:63]
	v_or_b32_e32 v62, v101, v132
	v_or_b32_e32 v63, v101, v107
	v_lshlrev_b32_e32 v62, 2, v62
	v_lshlrev_b32_e32 v63, 2, v63
	ds_bpermute_b32 v62, v62, v151
	ds_bpermute_b32 v63, v63, v151
	v_cvt_pk_bf16_f32 v58, v58, v59
	v_cndmask_b32_e32 v59, 0, v58, vcc
	v_lshrrev_b32_e32 v58, 16, v58
	s_waitcnt lgkmcnt(1)
	v_sub_f32_e32 v62, v62, v57
	s_waitcnt lgkmcnt(0)
	v_sub_f32_e32 v63, v63, v57
	v_mul_f32_e32 v62, 0x3fb8aa3b, v62
	v_mul_f32_e32 v63, 0x3fb8aa3b, v63
	v_exp_f32_e64 v62, v62
	v_exp_f32_e32 v63, v63
	v_cmp_le_u32_e32 vcc, v105, v56
	v_pk_mul_f32 v[60:61], v[60:61], v[62:63]
	s_nop 0
	v_cndmask_b32_e32 v58, 0, v58, vcc
	v_perm_b32 v58, v58, v59, s84
	v_cvt_pk_bf16_f32 v59, v60, v61
	v_cmp_le_u32_e32 vcc, v132, v56
	s_nop 0
	v_and_b32_e32 v62, 0xffff0000, v58
	s_nop 0
	v_cndmask_b32_e32 v60, 0, v59, vcc
	v_lshrrev_b32_e32 v59, 16, v59
	v_cmp_le_u32_e32 vcc, v107, v56
	s_nop 1
	v_cndmask_b32_e32 v59, 0, v59, vcc
	v_perm_b32 v59, v59, v60, s84
	v_lshlrev_b32_e32 v61, 16, v59
	v_lshlrev_b32_e32 v60, 16, v58
	v_and_b32_e32 v63, 0xffff0000, v59
	v_pk_add_f32 v[60:61], v[60:61], v[62:63]
	s_nop 0
	v_add_f32_e32 v60, v60, v61
	v_add_f32_e32 v190, v190, v60
	s_branch .LBB0_675
.LBB0_674:
	v_mov_b32_e64 v59, 0
	v_mov_b32_e32 v58, v59
.LBB0_675:
	s_cmp_gt_u32 s5, 1
	s_cselect_b64 s[40:41], -1, 0
	s_cmp_lt_u32 s5, 2
	v_mov_b32_e32 v63, 0
	s_cbranch_scc1 .LBB0_678
	v_or_b32_e32 v62, v101, v136
	v_lshlrev_b32_e32 v62, 2, v62
	ds_bpermute_b32 v62, v62, v151
	v_or_b32_e32 v60, v101, v134
	v_or_b32_e32 v61, v101, v121
	v_lshlrev_b32_e32 v60, 2, v60
	v_lshlrev_b32_e32 v61, 2, v61
	s_waitcnt lgkmcnt(0)
	v_sub_f32_e32 v62, v62, v57
	ds_bpermute_b32 v60, v60, v151
	ds_bpermute_b32 v61, v61, v151
	v_mul_f32_e32 v62, 0x3fb8aa3b, v62
	v_exp_f32_e64 v196, v62
	v_or_b32_e32 v62, v101, v123
	v_lshlrev_b32_e32 v62, 2, v62
	v_mfma_f32_16x16x32_bf16 v[236:239], v[4:7], v[24:27], 0
	ds_bpermute_b32 v62, v62, v151
	s_waitcnt lgkmcnt(2)
	v_sub_f32_e32 v60, v60, v57
	s_waitcnt lgkmcnt(1)
	v_sub_f32_e32 v61, v61, v57
	v_mul_f32_e32 v60, 0x3fb8aa3b, v60
	v_mul_f32_e32 v61, 0x3fb8aa3b, v61
	v_mfma_f32_16x16x32_bf16 v[236:239], v[16:19], v[28:31], v[236:239]
	v_exp_f32_e32 v60, v60
	v_exp_f32_e32 v61, v61
	s_waitcnt lgkmcnt(0)
	v_sub_f32_e32 v62, v62, v57
	v_mul_f32_e32 v62, 0x3fb8aa3b, v62
	v_exp_f32_e32 v197, v62
	s_nop 1
	v_pk_mul_f32 v[60:61], v[236:237], v[60:61]
	v_cmp_le_u32_e32 vcc, v134, v56
	s_nop 0
	v_cvt_pk_bf16_f32 v60, v60, v61
	v_pk_mul_f32 v[196:197], v[238:239], v[196:197]
	v_cndmask_b32_e32 v61, 0, v60, vcc
	v_lshrrev_b32_e32 v60, 16, v60
	v_cmp_le_u32_e32 vcc, v121, v56
	s_nop 1
	v_cndmask_b32_e32 v60, 0, v60, vcc
	s_nop 0
	v_perm_b32 v60, v60, v61, s84
	v_cvt_pk_bf16_f32 v61, v196, v197
	v_cmp_le_u32_e32 vcc, v136, v56
	v_lshlrev_b32_e32 v196, 16, v60
	v_and_b32_e32 v202, 0xffff0000, v60
	v_cndmask_b32_e32 v62, 0, v61, vcc
	v_lshrrev_b32_e32 v61, 16, v61
	v_cmp_le_u32_e32 vcc, v123, v56
	s_nop 1
	v_cndmask_b32_e32 v61, 0, v61, vcc
	s_nop 0
	v_perm_b32 v61, v61, v62, s84
	v_lshlrev_b32_e32 v197, 16, v61
	s_nop 0
	v_and_b32_e32 v203, 0xffff0000, v61
	v_pk_add_f32 v[196:197], v[196:197], v[202:203]
	s_nop 0
	v_add_f32_e32 v62, v196, v197
	v_add_f32_e32 v190, v190, v62
	s_cmp_lg_u32 s5, 3
	s_cbranch_scc0 .LBB0_679

.LBB0_678:
	v_mov_b32_e32 v61, 0
	v_mov_b32_e64 v60, v63
	s_cmp_lg_u32 s5, 3
	s_cbranch_scc1 .LBB0_677
.LBB0_679:
	v_or_b32_e32 v195, v101, v140
	v_lshlrev_b32_e32 v195, 2, v195
	ds_bpermute_b32 v195, v195, v151
	v_or_b32_e32 v62, v101, v138
	v_or_b32_e32 v63, v101, v125
	v_lshlrev_b32_e32 v62, 2, v62
	v_lshlrev_b32_e32 v63, 2, v63
	s_waitcnt lgkmcnt(0)
	v_sub_f32_e32 v195, v195, v57
	ds_bpermute_b32 v62, v62, v151
	ds_bpermute_b32 v63, v63, v151
	v_mul_f32_e32 v195, 0x3fb8aa3b, v195
	v_exp_f32_e64 v196, v195
	v_or_b32_e32 v195, v101, v127
	v_lshlrev_b32_e32 v195, 2, v195
	v_mfma_f32_16x16x32_bf16 v[236:239], v[12:15], v[24:27], 0
	ds_bpermute_b32 v195, v195, v151
	s_waitcnt lgkmcnt(2)
	v_sub_f32_e32 v62, v62, v57
	s_waitcnt lgkmcnt(1)
	v_sub_f32_e32 v63, v63, v57
	v_mul_f32_e32 v62, 0x3fb8aa3b, v62
	v_mul_f32_e32 v63, 0x3fb8aa3b, v63
	v_mfma_f32_16x16x32_bf16 v[236:239], v[20:23], v[28:31], v[236:239]
	v_exp_f32_e32 v62, v62
	v_exp_f32_e32 v63, v63
	s_waitcnt lgkmcnt(0)
	v_sub_f32_e32 v57, v195, v57
	v_mul_f32_e32 v57, 0x3fb8aa3b, v57
	v_exp_f32_e32 v197, v57
	s_nop 1
	v_pk_mul_f32 v[62:63], v[236:237], v[62:63]
	v_cmp_le_u32_e32 vcc, v138, v56
	s_nop 0
	v_cvt_pk_bf16_f32 v57, v62, v63
	v_pk_mul_f32 v[196:197], v[238:239], v[196:197]
	v_cndmask_b32_e32 v62, 0, v57, vcc
	v_lshrrev_b32_e32 v57, 16, v57
	v_cmp_le_u32_e32 vcc, v125, v56
	s_nop 1
	v_cndmask_b32_e32 v57, 0, v57, vcc
	s_nop 0
	v_perm_b32 v62, v57, v62, s84
	v_cvt_pk_bf16_f32 v57, v196, v197
	v_cmp_le_u32_e32 vcc, v140, v56
	s_nop 0
	v_and_b32_e32 v196, 0xffff0000, v62
	s_nop 0
	v_cndmask_b32_e32 v63, 0, v57, vcc
	v_lshrrev_b32_e32 v57, 16, v57
	v_cmp_le_u32_e32 vcc, v127, v56
	s_nop 1
	v_cndmask_b32_e32 v56, 0, v57, vcc
	v_perm_b32 v63, v56, v63, s84
	v_lshlrev_b32_e32 v57, 16, v63
	v_lshlrev_b32_e32 v56, 16, v62
	v_and_b32_e32 v197, 0xffff0000, v63
	v_pk_add_f32 v[56:57], v[56:57], v[196:197]
	s_nop 0
	v_add_f32_e32 v56, v56, v57
	v_add_f32_e64 v190, v190, v56
.LBB0_680:
	v_lshlrev_b32_e32 v195, 16, v24
	s_waitcnt vmcnt(10)
	v_fma_f32 v52, v52, v195, 0
	v_and_b32_e32 v195, 0xffff0000, v24
	v_fmac_f32_e32 v52, v53, v195
	v_lshlrev_b32_e32 v53, 16, v25
	v_fmac_f32_e32 v52, v54, v53
	s_nop 0
	v_and_b32_e32 v53, 0xffff0000, v25
	v_fmac_f32_e32 v52, v55, v53
	v_lshlrev_b32_e32 v53, 16, v26
	v_fmac_f32_e32 v52, v48, v53
	s_nop 0
	v_and_b32_e32 v48, 0xffff0000, v26
	v_fmac_f32_e32 v52, v49, v48
	v_lshlrev_b32_e32 v48, 16, v27
	v_fmac_f32_e32 v52, v50, v48
	s_nop 0
	v_and_b32_e32 v48, 0xffff0000, v27
	v_fmac_f32_e32 v52, v51, v48
	v_lshlrev_b32_e32 v48, 16, v28
	s_waitcnt vmcnt(8)
	v_fmac_f32_e32 v52, v44, v48
	v_and_b32_e32 v44, 0xffff0000, v28
	v_bfi_b32 v56, s85, v191, v191
	v_xor_b32_e32 v191, 16, v227
	v_add_u32_e32 v218, 64, v101
	v_fmac_f32_e32 v52, v45, v44
	v_lshlrev_b32_e32 v44, 16, v29
	v_cmp_lt_i32_e32 vcc, v191, v218
	v_fmac_f32_e32 v52, v46, v44
	v_and_b32_e32 v44, 0xffff0000, v29
	v_cndmask_b32_e32 v101, v227, v191, vcc
	v_fmac_f32_e32 v52, v47, v44
	v_lshlrev_b32_e32 v44, 16, v30
	v_lshlrev_b32_e32 v101, 2, v101
	v_fmac_f32_e32 v52, v40, v44
	s_nop 0
	v_and_b32_e32 v40, 0xffff0000, v30
	ds_bpermute_b32 v191, v101, v190
	v_fmac_f32_e32 v52, v41, v40
	v_lshlrev_b32_e32 v40, 16, v31
	v_fmac_f32_e32 v52, v42, v40
	s_nop 0
	v_and_b32_e32 v40, 0xffff0000, v31
	v_fmac_f32_e32 v52, v43, v40
	s_nop 0
	ds_bpermute_b32 v41, v101, v52
	s_waitcnt lgkmcnt(1)
	v_add_f32_e32 v190, v190, v191
	v_xor_b32_e32 v191, 32, v227
	v_cmp_lt_i32_e32 vcc, v191, v218
	v_bfi_b32 v57, s85, v194, v194
	s_waitcnt lgkmcnt(0)
	v_add_f32_e32 v41, v52, v41
	v_cndmask_b32_e32 v191, v227, v191, vcc
	v_lshlrev_b32_e32 v191, 2, v191
	ds_bpermute_b32 v194, v191, v190
	ds_bpermute_b32 v42, v191, v41
	s_lshl_b32 s38, s4, 7
	s_or_b32 s5, s22, s48
	s_ashr_i32 s39, s38, 31
	s_waitcnt lgkmcnt(1)
	v_add_f32_e32 v40, v190, v194
	s_waitcnt lgkmcnt(0)
	v_add_f32_e32 v41, v41, v42
	v_fmac_f32_e32 v40, v41, v98
	v_max_f32_e64 v41, v100, v100
	v_max_f32_e64 v100, |v40|, v41
	v_or_b32_e32 v40, s92, v131
	v_or_b32_e32 v190, s24, v40
	v_mov_b64_e32 v[40:41], s[54:55]
	s_nop 0
	v_mad_u64_u32 v[42:43], s[22:23], v190, s68, v[40:41]
	v_mad_i32_i24 v43, s25, v234, v43
	s_lshl_b64 s[22:23], s[38:39], 1
	s_nop 0
	v_lshl_add_u64 v[42:43], v[42:43], 0, s[22:23]
	v_lshl_add_u64 v[42:43], v[42:43], 0, v[96:97]
	v_lshl_add_u64 v[44:45], v[42:43], 0, s[86:87]
	v_add_co_u32_e32 v42, vcc, s75, v42
	s_waitcnt vmcnt(7)
	v_mfma_f32_16x16x32_bf16 v[88:91], v[24:27], v[88:91], 0
	v_addc_co_u32_e32 v43, vcc, 0, v43, vcc
	s_nop 0
	global_load_dwordx4 v[52:55], v[42:43], off
	global_load_dwordx4 v[48:51], v[44:45], off offset:16
	v_or_b32_e32 v42, 8, v190
	s_nop 0
	v_mad_u64_u32 v[40:41], s[72:73], v42, s68, v[40:41]
	v_mad_i32_i24 v41, s25, v234, v41
	v_lshl_add_u64 v[40:41], v[40:41], 0, s[22:23]
	v_div_scale_f32 v101, s[22:23], v100, v100, 1.0
	v_rcp_f32_e32 v194, v101
	s_nop 0
	v_lshl_add_u64 v[40:41], v[40:41], 0, v[96:97]
	v_lshl_add_u64 v[42:43], v[40:41], 0, s[86:87]
	v_add_co_u32_e32 v40, vcc, 0x1000, v40
	v_fma_f32 v195, -v101, v194, 1.0
	s_nop 0
	v_addc_co_u32_e32 v41, vcc, 0, v41, vcc
	v_fmac_f32_e32 v194, v195, v194
	s_nop 0
	v_div_scale_f32 v195, vcc, 1.0, v100, 1.0
	v_mul_f32_e64 v196, v195, v194
	v_fma_f32 v197, -v101, v196, v195
	v_fmac_f32_e32 v196, v197, v194
	s_nop 0
	v_fma_f32 v101, -v101, v196, v195
	v_div_fmas_f32 v101, v101, v194, v196
	v_add_co_u32_e32 v202, vcc, s66, v192
	s_nop 0
	global_load_dwordx4 v[44:47], v[40:41], off
	s_nop 0
	s_nop 0
	global_load_dwordx4 v[40:43], v[42:43], off offset:16
	v_div_fixup_f32 v100, v101, v100, 1.0
	v_addc_co_u32_e32 v203, vcc, 0, v193, vcc
	s_nop 0
	ds_bpermute_b32 v194, v99, v98
	ds_bpermute_b32 v236, v99, v100
	ds_bpermute_b32 v195, v99, v98 offset:4
	ds_bpermute_b32 v235, v99, v100 offset:4
	ds_bpermute_b32 v196, v99, v98 offset:8
	ds_bpermute_b32 v224, v99, v100 offset:8
	ds_bpermute_b32 v197, v99, v98 offset:12
	ds_bpermute_b32 v219, v99, v100 offset:12
	s_waitcnt vmcnt(10)
	s_nop 0
	v_mfma_f32_16x16x32_bf16 v[98:101], v[28:31], v[92:95], v[88:91]
	s_nop 2
	s_nop 0
	global_load_dwordx4 v[88:91], v[202:203], off
	global_load_dwordx4 v[92:95], v[202:203], off offset:64
	s_lshl_b32 s5, s5, 14
	s_add_i32 s22, s5, 0
	v_add_u32_e32 v237, s22, v133
	v_add_u32_e32 v239, v237, v137
	v_add3_u32 v238, s22, v137, v139
	v_add_u32_e32 v238, v238, v133
	v_add_u32_e32 v239, v239, v139
	ds_read_b64_tr_b16 v[240:241], v238
	ds_read_b64_tr_b16 v[242:243], v239 offset:4096
	s_waitcnt lgkmcnt(7)
	s_nop 0
	v_pk_mul_f32 v[98:99], v[98:99], v[194:195]
	s_waitcnt lgkmcnt(3)
	s_nop 0
	v_pk_mul_f32 v[100:101], v[100:101], v[196:197]
	v_mov_b32_e64 v191, s25
	s_andn2_b64 vcc, exec, s[40:41]
	s_waitcnt lgkmcnt(0)
	v_mfma_f32_16x16x32_bf16 v[98:101], v[56:59], v[240:243], v[98:101]
	v_cndmask_b32_e64 v240, 0, 1, s[40:41]
	v_cmp_ne_u32_e64 s[4:5], 1, v240
	s_cbranch_vccnz .LBB0_682
	s_nop 0
	ds_read_b64_tr_b16 v[240:241], v238 offset:8192
	ds_read_b64_tr_b16 v[242:243], v239 offset:12288
	s_waitcnt lgkmcnt(0)
	s_nop 0
	v_mfma_f32_16x16x32_bf16 v[98:101], v[60:63], v[240:243], v[98:101]
.LBB0_682:
	s_nop 7
	v_mul_f32_e32 v238, v98, v236
	v_bfe_u32 v98, v238, 16, 1
	v_add3_u32 v98, v238, v98, s67
	v_mul_f32_e64 v239, v99, v235
	ds_write_b16_d16_hi v210, v98
	v_bfe_u32 v98, v239, 16, 1
	v_add3_u32 v98, v239, v98, s67
	v_mul_f32_e64 v240, v100, v224
	ds_write_b16_d16_hi v211, v98
	v_bfe_u32 v98, v240, 16, 1
	v_add3_u32 v98, v240, v98, s67
	v_mul_f32_e32 v241, v101, v219
	s_waitcnt vmcnt(11)
	v_mfma_f32_16x16x32_bf16 v[80:83], v[24:27], v[80:83], 0
	ds_write_b16_d16_hi v212, v98
	v_bfe_u32 v98, v241, 16, 1
	v_add3_u32 v98, v241, v98, s67
	ds_write_b16_d16_hi v213, v98
	s_waitcnt vmcnt(10)
	s_nop 0
	v_mfma_f32_16x16x32_bf16 v[98:101], v[28:31], v[84:87], v[80:83]
	s_nop 2
	s_nop 0
	global_load_dwordx4 v[80:83], v[202:203], off offset:2048
	global_load_dwordx4 v[84:87], v[202:203], off offset:2112
	v_add_u32_e64 v203, v237, v141
	v_add3_u32 v202, s22, v141, v139
	v_add_u32_e32 v202, v202, v133
	v_add_u32_e32 v203, v203, v139
	ds_read_b64_tr_b16 v[242:243], v202
	ds_read_b64_tr_b16 v[244:245], v203 offset:4096
	v_pk_mul_f32 v[100:101], v[100:101], v[196:197]
	v_pk_mul_f32 v[98:99], v[98:99], v[194:195]
	s_and_b64 vcc, exec, s[4:5]
	s_waitcnt lgkmcnt(0)
	v_mfma_f32_16x16x32_bf16 v[98:101], v[56:59], v[242:245], v[98:101]
	s_cbranch_vccnz .LBB0_684
	s_nop 0
	ds_read_b64_tr_b16 v[242:243], v202 offset:8192
	ds_read_b64_tr_b16 v[244:245], v203 offset:12288
	s_waitcnt lgkmcnt(0)
	s_nop 0
	v_mfma_f32_16x16x32_bf16 v[98:101], v[60:63], v[242:245], v[98:101]
.LBB0_684:
	s_nop 7
	v_mul_f32_e32 v202, v98, v236
	v_bfe_u32 v98, v202, 16, 1
	v_add3_u32 v98, v202, v98, s67
	v_mul_f32_e64 v203, v99, v235
	ds_write_b16_d16_hi v210, v98 offset:32
	v_bfe_u32 v98, v203, 16, 1
	v_add3_u32 v98, v203, v98, s67
	v_mul_f32_e64 v242, v100, v224
	ds_write_b16_d16_hi v211, v98 offset:32
	v_bfe_u32 v98, v242, 16, 1
	v_add3_u32 v98, v242, v98, s67
	v_mul_f32_e32 v243, v101, v219
	s_waitcnt vmcnt(11)
	v_mfma_f32_16x16x32_bf16 v[72:75], v[24:27], v[72:75], 0
	ds_write_b16_d16_hi v212, v98 offset:32
	v_bfe_u32 v98, v243, 16, 1
	s_movk_i32 s23, 0x3000
	s_nop 0
	v_add3_u32 v98, v243, v98, s67
	v_add_co_u32_e32 v192, vcc, s23, v192
	s_nop 0
	ds_write_b16_d16_hi v213, v98 offset:32
	s_nop 0
	v_addc_co_u32_e32 v193, vcc, 0, v193, vcc
	s_waitcnt vmcnt(10)
	s_nop 0
	v_mfma_f32_16x16x32_bf16 v[98:101], v[28:31], v[76:79], v[72:75]
	s_nop 2
	s_nop 0
	global_load_dwordx4 v[72:75], v[192:193], off
	global_load_dwordx4 v[76:79], v[192:193], off offset:64
	v_add_u32_e64 v245, v237, v199
	v_add3_u32 v244, s22, v199, v139
	v_add_u32_e32 v244, v244, v133
	v_add_u32_e32 v245, v245, v139
	ds_read_b64_tr_b16 v[246:247], v244
	ds_read_b64_tr_b16 v[248:249], v245 offset:4096
	v_pk_mul_f32 v[100:101], v[100:101], v[196:197]
	v_pk_mul_f32 v[98:99], v[98:99], v[194:195]
	s_and_b64 vcc, exec, s[4:5]
	s_waitcnt lgkmcnt(0)
	v_mfma_f32_16x16x32_bf16 v[98:101], v[56:59], v[246:249], v[98:101]
	s_cbranch_vccnz .LBB0_686
	s_nop 0
	ds_read_b64_tr_b16 v[246:247], v244 offset:8192
	ds_read_b64_tr_b16 v[248:249], v245 offset:12288
	s_waitcnt lgkmcnt(0)
	s_nop 0
	v_mfma_f32_16x16x32_bf16 v[98:101], v[60:63], v[246:249], v[98:101]
.LBB0_686:
	s_nop 7
	v_mul_f32_e32 v244, v98, v236
	v_bfe_u32 v98, v244, 16, 1
	v_add3_u32 v98, v244, v98, s67
	v_mul_f32_e64 v245, v99, v235
	ds_write_b16_d16_hi v210, v98 offset:64
	v_bfe_u32 v98, v245, 16, 1
	v_add3_u32 v98, v245, v98, s67
	v_mul_f32_e64 v246, v100, v224
	ds_write_b16_d16_hi v211, v98 offset:64
	v_bfe_u32 v98, v246, 16, 1
	v_add3_u32 v98, v246, v98, s67
	v_mul_f32_e32 v247, v101, v219
	s_waitcnt vmcnt(11)
	v_mfma_f32_16x16x32_bf16 v[64:67], v[24:27], v[64:67], 0
	ds_write_b16_d16_hi v212, v98 offset:64
	v_bfe_u32 v98, v247, 16, 1
	v_add3_u32 v98, v247, v98, s67
	ds_write_b16_d16_hi v213, v98 offset:64
	s_waitcnt vmcnt(10)
	s_nop 0
	v_mfma_f32_16x16x32_bf16 v[98:101], v[28:31], v[68:71], v[64:67]
	s_nop 2
	s_nop 0
	global_load_dwordx4 v[64:67], v[192:193], off offset:2048
	global_load_dwordx4 v[68:71], v[192:193], off offset:2112
	v_add_u32_e64 v193, v237, v204
	v_add3_u32 v192, s22, v204, v139
	v_add_u32_e32 v192, v192, v133
	v_add_u32_e32 v193, v193, v139
	ds_read_b64_tr_b16 v[248:249], v192
	ds_read_b64_tr_b16 v[250:251], v193 offset:4096
	v_pk_mul_f32 v[100:101], v[100:101], v[196:197]
	v_pk_mul_f32 v[98:99], v[98:99], v[194:195]
	s_and_b64 vcc, exec, s[4:5]
	s_waitcnt lgkmcnt(0)
	v_mfma_f32_16x16x32_bf16 v[98:101], v[56:59], v[248:251], v[98:101]
	s_cbranch_vccnz .LBB0_688
	s_nop 0
	ds_read_b64_tr_b16 v[248:249], v192 offset:8192
	ds_read_b64_tr_b16 v[250:251], v193 offset:12288
	s_waitcnt lgkmcnt(0)
	s_nop 0
	v_mfma_f32_16x16x32_bf16 v[98:101], v[60:63], v[248:251], v[98:101]
.LBB0_688:
	s_nop 7
	v_mul_f32_e32 v98, v98, v236
	v_bfe_u32 v192, v98, 16, 1
	v_add3_u32 v192, v98, v192, s67
	v_mul_f32_e64 v99, v99, v235
	ds_write_b16_d16_hi v210, v192 offset:96
	v_bfe_u32 v192, v99, 16, 1
	v_add3_u32 v192, v99, v192, s67
	v_mul_f32_e32 v100, v100, v224
	s_waitcnt vmcnt(7)
	v_mfma_f32_16x16x32_bf16 v[88:91], v[24:27], v[88:91], 0
	ds_write_b16_d16_hi v211, v192 offset:96
	v_bfe_u32 v192, v100, 16, 1
	v_add3_u32 v192, v100, v192, s67
	v_mul_f32_e64 v101, v101, v219
	ds_write_b16_d16_hi v212, v192 offset:96
	v_bfe_u32 v192, v101, 16, 1
	v_add3_u32 v192, v101, v192, s67
	s_waitcnt vmcnt(6)
	s_nop 0
	v_mfma_f32_16x16x32_bf16 v[88:91], v[28:31], v[92:95], v[88:91]
	v_add_u32_e64 v93, v237, v205
	v_add3_u32 v92, s22, v205, v139
	ds_write_b16_d16_hi v213, v192 offset:96
	v_add_u32_e32 v92, v92, v133
	v_add_u32_e32 v93, v93, v139
	ds_read_b64_tr_b16 v[248:249], v92
	ds_read_b64_tr_b16 v[250:251], v93 offset:4096
	s_nop 0
	s_nop 0
	v_pk_mul_f32 v[90:91], v[90:91], v[196:197]
	v_pk_mul_f32 v[88:89], v[88:89], v[194:195]
	s_and_b64 vcc, exec, s[4:5]
	s_waitcnt lgkmcnt(0)
	v_mfma_f32_16x16x32_bf16 v[88:91], v[56:59], v[248:251], v[88:91]
	s_cbranch_vccnz .LBB0_690
	s_nop 0
	ds_read_b64_tr_b16 v[248:249], v92 offset:8192
	ds_read_b64_tr_b16 v[250:251], v93 offset:12288
	s_waitcnt lgkmcnt(0)
	s_nop 0
	v_mfma_f32_16x16x32_bf16 v[88:91], v[60:63], v[248:251], v[88:91]
.LBB0_690:
	s_nop 7
	v_mul_f32_e32 v88, v88, v236
	v_bfe_u32 v92, v88, 16, 1
	v_add3_u32 v92, v88, v92, s67
	v_mul_f32_e64 v89, v89, v235
	ds_write_b16_d16_hi v210, v92 offset:128
	v_bfe_u32 v92, v89, 16, 1
	v_add3_u32 v92, v89, v92, s67
	v_mul_f32_e32 v90, v90, v224
	s_waitcnt vmcnt(5)
	v_mfma_f32_16x16x32_bf16 v[80:83], v[24:27], v[80:83], 0
	ds_write_b16_d16_hi v211, v92 offset:128
	v_bfe_u32 v92, v90, 16, 1
	v_add3_u32 v92, v90, v92, s67
	v_mul_f32_e64 v91, v91, v219
	ds_write_b16_d16_hi v212, v92 offset:128
	v_bfe_u32 v92, v91, 16, 1
	v_add3_u32 v92, v91, v92, s67
	s_waitcnt vmcnt(4)
	s_nop 0
	v_mfma_f32_16x16x32_bf16 v[80:83], v[28:31], v[84:87], v[80:83]
	v_add_u32_e64 v85, v237, v206
	v_add3_u32 v84, s22, v206, v139
	ds_write_b16_d16_hi v213, v92 offset:128
	v_add_u32_e32 v84, v84, v133
	v_add_u32_e32 v85, v85, v139
	ds_read_b64_tr_b16 v[92:93], v84
	ds_read_b64_tr_b16 v[94:95], v85 offset:4096
	s_nop 0
	s_nop 0
	v_pk_mul_f32 v[82:83], v[82:83], v[196:197]
	v_pk_mul_f32 v[80:81], v[80:81], v[194:195]
	s_and_b64 vcc, exec, s[4:5]
	s_waitcnt lgkmcnt(0)
	v_mfma_f32_16x16x32_bf16 v[80:83], v[56:59], v[92:95], v[80:83]
	s_cbranch_vccnz .LBB0_692
	s_nop 0
	ds_read_b64_tr_b16 v[92:93], v84 offset:8192
	ds_read_b64_tr_b16 v[94:95], v85 offset:12288
	s_waitcnt lgkmcnt(0)
	s_nop 0
	v_mfma_f32_16x16x32_bf16 v[80:83], v[60:63], v[92:95], v[80:83]
.LBB0_692:
	s_nop 7
	v_mul_f32_e32 v80, v80, v236
	v_bfe_u32 v84, v80, 16, 1
	v_add3_u32 v84, v80, v84, s67
	v_mul_f32_e64 v81, v81, v235
	ds_write_b16_d16_hi v210, v84 offset:160
	v_bfe_u32 v84, v81, 16, 1
	v_add3_u32 v84, v81, v84, s67
	v_mul_f32_e32 v82, v82, v224
	s_waitcnt vmcnt(3)
	v_mfma_f32_16x16x32_bf16 v[72:75], v[24:27], v[72:75], 0
	ds_write_b16_d16_hi v211, v84 offset:160
	v_bfe_u32 v84, v82, 16, 1
	v_add3_u32 v84, v82, v84, s67
	v_mul_f32_e64 v83, v83, v219
	ds_write_b16_d16_hi v212, v84 offset:160
	v_bfe_u32 v84, v83, 16, 1
	v_add3_u32 v84, v83, v84, s67
	s_waitcnt vmcnt(2)
	s_nop 0
	v_mfma_f32_16x16x32_bf16 v[72:75], v[28:31], v[76:79], v[72:75]
	v_add_u32_e64 v77, v237, v207
	v_add3_u32 v76, s22, v207, v139
	ds_write_b16_d16_hi v213, v84 offset:160
	v_add_u32_e32 v76, v76, v133
	v_add_u32_e32 v77, v77, v139
	ds_read_b64_tr_b16 v[84:85], v76
	ds_read_b64_tr_b16 v[86:87], v77 offset:4096
	s_nop 0
	s_nop 0
	v_pk_mul_f32 v[74:75], v[74:75], v[196:197]
	v_pk_mul_f32 v[72:73], v[72:73], v[194:195]
	s_and_b64 vcc, exec, s[4:5]
	s_waitcnt lgkmcnt(0)
	v_mfma_f32_16x16x32_bf16 v[72:75], v[56:59], v[84:87], v[72:75]
	s_cbranch_vccnz .LBB0_694
	s_nop 0
	ds_read_b64_tr_b16 v[84:85], v76 offset:8192
	ds_read_b64_tr_b16 v[86:87], v77 offset:12288
	s_waitcnt lgkmcnt(0)
	s_nop 0
	v_mfma_f32_16x16x32_bf16 v[72:75], v[60:63], v[84:87], v[72:75]
.LBB0_694:
	s_nop 7
	v_mul_f32_e32 v72, v72, v236
	s_waitcnt vmcnt(1)
	s_nop 0
	v_mfma_f32_16x16x32_bf16 v[64:67], v[24:27], v[64:67], 0
	v_bfe_u32 v76, v72, 16, 1
	v_add3_u32 v76, v72, v76, s67
	v_mul_f32_e64 v73, v73, v235
	ds_write_b16_d16_hi v210, v76 offset:192
	v_bfe_u32 v76, v73, 16, 1
	v_add3_u32 v76, v73, v76, s67
	v_mul_f32_e32 v74, v74, v224
	s_waitcnt vmcnt(0)
	v_mfma_f32_16x16x32_bf16 v[64:67], v[28:31], v[68:71], v[64:67]
	ds_write_b16_d16_hi v211, v76 offset:192
	v_bfe_u32 v76, v74, 16, 1
	v_add3_u32 v76, v74, v76, s67
	v_mul_f32_e64 v75, v75, v219
	ds_write_b16_d16_hi v212, v76 offset:192
	v_bfe_u32 v76, v75, 16, 1
	v_add3_u32 v76, v75, v76, s67
	v_add_u32_e64 v70, v237, v208
	v_pk_mul_f32 v[68:69], v[66:67], v[196:197]
	v_pk_mul_f32 v[66:67], v[64:65], v[194:195]
	v_add3_u32 v64, s22, v208, v139
	ds_write_b16_d16_hi v213, v76 offset:192
	v_add_u32_e32 v64, v64, v133
	v_add_u32_e32 v65, v70, v139
	ds_read_b64_tr_b16 v[76:77], v64
	ds_read_b64_tr_b16 v[78:79], v65 offset:4096
	s_waitcnt lgkmcnt(0)
	s_nop 0
	v_mfma_f32_16x16x32_bf16 v[56:59], v[56:59], v[76:79], v[66:69]
	s_and_b64 vcc, exec, s[4:5]
	s_cbranch_vccnz .LBB0_696
	s_nop 0
	s_nop 0
	ds_read_b64_tr_b16 v[66:67], v64 offset:8192
	ds_read_b64_tr_b16 v[68:69], v65 offset:12288
	s_waitcnt lgkmcnt(0)
	s_nop 0
	v_mfma_f32_16x16x32_bf16 v[56:59], v[60:63], v[66:69], v[56:59]
.LBB0_696:
	v_mul_f32_e32 v60, v202, v202
	v_fmac_f32_e32 v60, v238, v238
	v_fmac_f32_e32 v60, v244, v244
	v_mul_f32_e32 v61, v203, v203
	v_fmac_f32_e32 v60, v98, v98
	v_fmac_f32_e32 v61, v239, v239
	v_fmac_f32_e32 v60, v88, v88
	v_fmac_f32_e32 v61, v245, v245
	v_fmac_f32_e32 v60, v80, v80
	v_mul_f32_e32 v56, v56, v236
	v_mul_f32_e64 v62, v242, v242
	v_fmac_f32_e32 v61, v99, v99
	v_fmac_f32_e32 v60, v72, v72
	v_bfe_u32 v64, v56, 16, 1
	v_fmac_f32_e32 v62, v240, v240
	v_fmac_f32_e32 v61, v89, v89
	v_fmac_f32_e32 v60, v56, v56
	s_nop 0
	v_add3_u32 v56, v56, v64, s67
	v_fmac_f32_e32 v62, v246, v246
	v_fmac_f32_e32 v61, v81, v81
	ds_write_b16_d16_hi v210, v56 offset:224
	v_mul_f32_e64 v56, v57, v235
	v_fmac_f32_e32 v62, v100, v100
	v_fmac_f32_e32 v61, v73, v73
	v_bfe_u32 v57, v56, 16, 1
	v_fmac_f32_e32 v62, v90, v90
	v_fmac_f32_e32 v61, v56, v56
	v_add3_u32 v56, v56, v57, s67
	v_fmac_f32_e32 v62, v82, v82
	s_nop 0
	ds_write_b16_d16_hi v211, v56 offset:224
	v_mul_f32_e32 v56, v58, v224
	v_fmac_f32_e32 v62, v74, v74
	v_bfe_u32 v57, v56, 16, 1
	v_fmac_f32_e32 v62, v56, v56
	s_nop 0
	v_add3_u32 v64, v56, v57, s67
	v_xor_b32_e32 v56, 1, v227
	v_cmp_lt_i32_e32 vcc, v56, v218
	v_mul_f32_e32 v65, v59, v219
	v_mul_f32_e32 v63, v243, v243
	v_cndmask_b32_e32 v56, v227, v56, vcc
	v_lshlrev_b32_e32 v58, 2, v56
	ds_bpermute_b32 v57, v58, v60
	v_xor_b32_e32 v56, 2, v227
	v_cmp_lt_i32_e32 vcc, v56, v218
	v_fmac_f32_e32 v63, v241, v241
	v_fmac_f32_e32 v63, v247, v247
	v_cndmask_b32_e32 v56, v227, v56, vcc
	v_lshlrev_b32_e32 v59, 2, v56
	s_waitcnt lgkmcnt(0)
	v_add_f32_e32 v57, v60, v57
	ds_bpermute_b32 v60, v59, v57
	v_xor_b32_e32 v56, 4, v227
	v_cmp_lt_i32_e32 vcc, v56, v218
	v_fmac_f32_e32 v63, v101, v101
	v_fmac_f32_e32 v63, v91, v91
	v_cndmask_b32_e32 v56, v227, v56, vcc
	v_lshlrev_b32_e32 v66, 2, v56
	s_waitcnt lgkmcnt(0)
	v_add_f32_e32 v57, v57, v60
	ds_bpermute_b32 v60, v66, v57
	v_fmac_f32_e32 v63, v83, v83
	v_xor_b32_e32 v56, 8, v227
	v_fmac_f32_e32 v63, v75, v75
	v_cmp_lt_i32_e32 vcc, v56, v218
	v_fmac_f32_e32 v63, v65, v65
	s_nop 0
	ds_bpermute_b32 v68, v58, v61
	v_cndmask_b32_e32 v56, v227, v56, vcc
	v_lshlrev_b32_e32 v67, 2, v56
	s_waitcnt lgkmcnt(1)
	v_add_f32_e32 v56, v57, v60
	ds_bpermute_b32 v60, v58, v62
	ds_bpermute_b32 v58, v58, v63
	s_waitcnt lgkmcnt(2)
	v_add_f32_e32 v61, v61, v68
	ds_bpermute_b32 v68, v59, v61
	ds_bpermute_b32 v57, v67, v56
	s_waitcnt lgkmcnt(3)
	v_add_f32_e32 v60, v62, v60
	s_waitcnt lgkmcnt(2)
	v_add_f32_e32 v58, v63, v58
	ds_bpermute_b32 v62, v59, v60
	ds_bpermute_b32 v59, v59, v58
	s_waitcnt lgkmcnt(3)
	v_add_f32_e32 v61, v61, v68
	ds_bpermute_b32 v63, v66, v61
	ds_write_b16_d16_hi v212, v64 offset:224
	s_waitcnt lgkmcnt(3)
	v_add_f32_e32 v60, v60, v62
	s_waitcnt lgkmcnt(2)
	v_add_f32_e32 v68, v58, v59
	ds_bpermute_b32 v62, v66, v60
	ds_bpermute_b32 v66, v66, v68
	s_waitcnt lgkmcnt(3)
	v_add_f32_e32 v58, v61, v63
	ds_bpermute_b32 v59, v67, v58
	v_bfe_u32 v64, v65, 16, 1
	s_waitcnt lgkmcnt(2)
	v_add_f32_e32 v60, v60, v62
	s_waitcnt lgkmcnt(1)
	v_add_f32_e32 v62, v68, v66
	ds_bpermute_b32 v61, v67, v60
	ds_bpermute_b32 v63, v67, v62
	v_add3_u32 v64, v65, v64, s67
	ds_write_b16_d16_hi v213, v64 offset:224
	s_and_saveexec_b64 s[40:41], s[2:3]
	s_cbranch_execz .LBB0_698
	s_waitcnt lgkmcnt(1)
	v_add_f32_e32 v62, v62, v63
	v_fmamk_f32 v62, v62, 0x3c000000, v220
	v_mul_f32_e32 v63, 0x4f800000, v62
	v_cmp_gt_f32_e32 vcc, s95, v62
	v_add_f32_e32 v60, v60, v61
	v_fmamk_f32 v60, v60, 0x3c000000, v220
	v_cndmask_b32_e32 v62, v62, v63, vcc
	v_sqrt_f32_e32 v63, v62
	v_mul_f32_e32 v61, 0x4f800000, v60
	v_add_f32_e64 v58, v58, v59
	v_fmamk_f32 v58, v58, 0x3c000000, v220
	v_add_u32_e64 v64, -1, v63
	v_fma_f32 v66, -v64, v63, v62
	v_add_u32_e64 v65, 1, v63
	v_cmp_ge_f32_e64 s[4:5], 0, v66
	v_mul_f32_e32 v59, 0x4f800000, v58
	v_add_f32_e64 v56, v56, v57
	v_cndmask_b32_e64 v64, v63, v64, s[4:5]
	v_fma_f32 v63, -v65, v63, v62
	v_cmp_lt_f32_e64 s[4:5], 0, v63
	v_fmamk_f32 v56, v56, 0x3c000000, v220
	v_mul_f32_e32 v57, 0x4f800000, v56
	v_cndmask_b32_e64 v63, v64, v65, s[4:5]
	v_cmp_gt_f32_e64 s[4:5], s95, v60
	v_mul_f32_e32 v64, 0x37800000, v63
	v_cndmask_b32_e32 v63, v63, v64, vcc
	s_nop 0
	v_cndmask_b32_e64 v60, v60, v61, s[4:5]
	v_sqrt_f32_e32 v61, v60
	v_cmp_class_f32_e32 vcc, v62, v221
	s_nop 1
	v_cndmask_b32_e32 v62, v63, v62, vcc
	v_add_u32_e64 v63, -1, v61
	v_fma_f32 v64, -v63, v61, v60
	v_cmp_ge_f32_e32 vcc, 0, v64
	v_add_u32_e32 v64, 1, v61
	s_nop 0
	v_cndmask_b32_e32 v63, v61, v63, vcc
	v_fma_f32 v61, -v64, v61, v60
	v_cmp_lt_f32_e32 vcc, 0, v61
	s_nop 1
	v_cndmask_b32_e32 v61, v63, v64, vcc
	v_cmp_gt_f32_e32 vcc, s95, v58
	v_mul_f32_e32 v63, 0x37800000, v61
	v_cndmask_b32_e64 v61, v61, v63, s[4:5]
	v_cndmask_b32_e32 v58, v58, v59, vcc
	v_sqrt_f32_e32 v59, v58
	v_cmp_class_f32_e64 s[4:5], v60, v221
	s_nop 1
	s_nop 0
	v_cndmask_b32_e64 v60, v61, v60, s[4:5]
	v_add_u32_e64 v61, -1, v59
	v_fma_f32 v63, -v61, v59, v58
	v_cmp_ge_f32_e64 s[4:5], 0, v63
	v_add_u32_e32 v63, 1, v59
	s_nop 0
	v_cndmask_b32_e64 v61, v59, v61, s[4:5]
	v_fma_f32 v59, -v63, v59, v58
	v_cmp_lt_f32_e64 s[4:5], 0, v59
	s_nop 1
	s_nop 0
	v_cndmask_b32_e64 v59, v61, v63, s[4:5]
	v_cmp_gt_f32_e64 s[4:5], s95, v56
	v_mul_f32_e32 v61, 0x37800000, v59
	v_cndmask_b32_e32 v59, v59, v61, vcc
	s_nop 0
	v_cndmask_b32_e64 v56, v56, v57, s[4:5]
	v_sqrt_f32_e32 v57, v56
	v_cmp_class_f32_e32 vcc, v58, v221
	s_nop 1
	v_cndmask_b32_e32 v58, v59, v58, vcc
	v_add_u32_e64 v59, -1, v57
	v_fma_f32 v61, -v59, v57, v56
	v_cmp_ge_f32_e32 vcc, 0, v61
	v_add_u32_e32 v61, 1, v57
	s_nop 0
	v_cndmask_b32_e32 v59, v57, v59, vcc
	v_fma_f32 v57, -v61, v57, v56
	v_cmp_lt_f32_e32 vcc, 0, v57
	s_nop 1
	v_cndmask_b32_e32 v57, v59, v61, vcc
	s_nop 0
	v_div_scale_f32 v61, s[22:23], v58, v58, 1.0
	v_rcp_f32_e32 v63, v61
	s_nop 0
	v_mul_f32_e32 v59, 0x37800000, v57
	v_cndmask_b32_e64 v57, v57, v59, s[4:5]
	v_cmp_class_f32_e32 vcc, v56, v221
	s_nop 1
	v_cndmask_b32_e32 v56, v57, v56, vcc
	s_nop 0
	v_fma_f32 v57, -v61, v63, 1.0
	v_fmac_f32_e32 v63, v57, v63
	s_nop 0
	v_div_scale_f32 v57, vcc, 1.0, v58, 1.0
	v_mul_f32_e64 v59, v57, v63
	v_fma_f32 v64, -v61, v59, v57
	v_fmac_f32_e32 v59, v64, v63
	s_nop 0
	v_fma_f32 v57, -v61, v59, v57
	v_div_scale_f32 v61, s[4:5], v56, v56, 1.0
	v_rcp_f32_e32 v64, v61
	s_nop 0
	v_div_fmas_f32 v57, v57, v63, v59
	v_div_fixup_f32 v57, v57, v58, 1.0
	v_fma_f32 v58, -v61, v64, 1.0
	v_fmac_f32_e32 v64, v58, v64
	s_nop 0
	v_div_scale_f32 v58, vcc, 1.0, v56, 1.0
	v_mul_f32_e64 v59, v58, v64
	v_fma_f32 v63, -v61, v59, v58
	v_fmac_f32_e32 v59, v63, v64
	s_nop 0
	v_fma_f32 v58, -v61, v59, v58
	v_div_scale_f32 v61, s[4:5], v62, v62, 1.0
	v_rcp_f32_e32 v63, v61
	s_nop 0
	v_div_fmas_f32 v58, v58, v64, v59
	v_div_fixup_f32 v56, v58, v56, 1.0
	v_add_u32_e64 v64, s47, v106
	v_fma_f32 v58, -v61, v63, 1.0
	v_fmac_f32_e32 v63, v58, v63
	s_nop 0
	v_div_scale_f32 v58, vcc, 1.0, v62, 1.0
	v_mul_f32_e64 v59, v58, v63
	v_fma_f32 v65, -v61, v59, v58
	v_fmac_f32_e32 v59, v65, v63
	s_nop 0
	v_fma_f32 v58, -v61, v59, v58
	v_div_scale_f32 v61, s[4:5], v60, v60, 1.0
	v_rcp_f32_e32 v65, v61
	s_nop 0
	v_div_fmas_f32 v58, v58, v63, v59
	v_div_fixup_f32 v59, v58, v62, 1.0
	v_fma_f32 v58, -v61, v65, 1.0
	v_fmac_f32_e32 v65, v58, v65
	s_nop 0
	v_div_scale_f32 v58, vcc, 1.0, v60, 1.0
	v_mul_f32_e64 v62, v58, v65
	v_fma_f32 v63, -v61, v62, v58
	v_fmac_f32_e32 v62, v63, v65
	s_nop 0
	v_fma_f32 v58, -v61, v62, v58
	v_div_fmas_f32 v58, v58, v65, v62
	v_div_fixup_f32 v58, v58, v60, 1.0
	ds_write_b128 v64, v[56:59] offset:4352
.LBB0_698:
	s_or_b64 exec, exec, s[40:41]
	s_waitcnt lgkmcnt(0)
	v_lshl_add_u64 v[68:69], s[38:39], 2, v[116:117]
	s_waitcnt lgkmcnt(3)
	s_nop 0
	global_load_dwordx4 v[56:59], v[68:69], off offset:48
	s_waitcnt lgkmcnt(1)
	s_nop 0
	global_load_dwordx4 v[60:63], v[68:69], off offset:16
	global_load_dwordx4 v[64:67], v[68:69], off offset:32
	s_nop 0
	s_nop 0
	global_load_dwordx4 v[68:71], v[68:69], off
	ds_read_b128 v[80:83], v209
	ds_read_b128 v[72:75], v209 offset:16
	ds_read2_b32 v[78:79], v214 offset0:64 offset1:72
	v_lshlrev_b32_e32 v86, 16, v52
	s_nop 0
	v_and_b32_e32 v87, 0xffff0000, v52
	s_waitcnt lgkmcnt(2)
	v_lshlrev_b32_e32 v84, 16, v80
	v_and_b32_e32 v85, 0xffff0000, v80
	v_lshlrev_b32_e32 v80, 16, v81
	s_nop 0
	v_and_b32_e32 v81, 0xffff0000, v81
	s_waitcnt lgkmcnt(0)
	s_nop 0
	v_pk_mul_f32 v[80:81], v[78:79], v[80:81] op_sel_hi:[0,1]
	v_lshlrev_b32_e32 v52, 16, v53
	s_nop 0
	v_and_b32_e32 v53, 0xffff0000, v53
	v_pk_mul_f32 v[84:85], v[78:79], v[84:85] op_sel_hi:[0,1]
	v_lshl_add_u64 v[76:77], v[118:119], 0, s[38:39]
	s_andn2_b64 vcc, exec, s[30:31]
	s_waitcnt vmcnt(0)
	v_pk_mul_f32 v[80:81], v[70:71], v[80:81]
	s_nop 0
	s_nop 0
	v_pk_mul_f32 v[52:53], v[80:81], v[52:53]
	v_pk_mul_f32 v[84:85], v[68:69], v[84:85]
	v_cvt_pk_bf16_f32 v80, v52, v53
	v_lshlrev_b32_e32 v52, 16, v73
	s_nop 0
	v_and_b32_e32 v53, 0xffff0000, v73
	v_pk_mul_f32 v[52:53], v[78:79], v[52:53] op_sel_hi:[0,1]
	v_pk_mul_f32 v[84:85], v[84:85], v[86:87]
	v_lshlrev_b32_e32 v86, 16, v48
	s_nop 0
	v_and_b32_e32 v87, 0xffff0000, v48
	v_pk_mul_f32 v[52:53], v[66:67], v[52:53]
	v_lshlrev_b32_e32 v48, 16, v49
	s_nop 0
	v_and_b32_e32 v49, 0xffff0000, v49
	v_pk_mul_f32 v[48:49], v[52:53], v[48:49]
	v_lshlrev_b32_e32 v52, 16, v54
	s_nop 0
	v_cvt_pk_bf16_f32 v73, v48, v49
	v_lshlrev_b32_e32 v48, 16, v82
	s_nop 0
	v_and_b32_e32 v49, 0xffff0000, v82
	v_pk_mul_f32 v[48:49], v[78:79], v[48:49] op_sel_hi:[0,1]
	v_pk_mul_f32 v[48:49], v[60:61], v[48:49]
	v_and_b32_e32 v53, 0xffff0000, v54
	v_pk_mul_f32 v[48:49], v[48:49], v[52:53]
	v_lshlrev_b32_e32 v52, 16, v50
	s_nop 0
	v_cvt_pk_bf16_f32 v54, v48, v49
	v_lshlrev_b32_e32 v48, 16, v74
	s_nop 0
	v_and_b32_e32 v49, 0xffff0000, v74
	v_pk_mul_f32 v[48:49], v[78:79], v[48:49] op_sel_hi:[0,1]
	v_pk_mul_f32 v[48:49], v[56:57], v[48:49]
	v_and_b32_e32 v53, 0xffff0000, v50
	v_pk_mul_f32 v[48:49], v[48:49], v[52:53]
	v_lshlrev_b32_e32 v52, 16, v55
	s_nop 0
	v_cvt_pk_bf16_f32 v74, v48, v49
	v_lshlrev_b32_e32 v48, 16, v83
	s_nop 0
	v_and_b32_e32 v49, 0xffff0000, v83
	v_pk_mul_f32 v[48:49], v[78:79], v[48:49] op_sel_hi:[0,1]
	v_pk_mul_f32 v[48:49], v[62:63], v[48:49]
	v_and_b32_e32 v53, 0xffff0000, v55
	v_pk_mul_f32 v[48:49], v[48:49], v[52:53]
	v_lshlrev_b32_e32 v50, 16, v51
	s_nop 0
	v_cvt_pk_bf16_f32 v52, v48, v49
	v_lshlrev_b32_e32 v48, 16, v75
	s_nop 0
	v_and_b32_e32 v49, 0xffff0000, v75
	v_pk_mul_f32 v[48:49], v[78:79], v[48:49] op_sel_hi:[0,1]
	v_pk_mul_f32 v[48:49], v[58:59], v[48:49]
	v_and_b32_e32 v51, 0xffff0000, v51
	v_cvt_pk_bf16_f32 v88, v84, v85
	v_pk_mul_f32 v[48:49], v[48:49], v[50:51]
	v_lshlrev_b32_e32 v84, 16, v72
	s_nop 0
	v_cvt_pk_bf16_f32 v53, v48, v49
	v_lshlrev_b32_e32 v48, 16, v88
	s_nop 0
	v_and_b32_e32 v49, 0xffff0000, v88
	v_and_b32_e32 v85, 0xffff0000, v72
	v_med3_f32 v50, v48, s82, v229
	v_med3_f32 v49, v49, s82, v229
	v_mov_b32_e64 v48, v97
	v_pk_mul_f32 v[84:85], v[78:79], v[84:85] op_sel_hi:[0,1]
	v_cvt_pk_fp8_f32 v48, v50, v49
	v_pk_mul_f32 v[84:85], v[64:65], v[84:85]
	v_lshlrev_b32_e32 v49, 16, v80
	s_nop 0
	v_pk_mul_f32 v[84:85], v[84:85], v[86:87]
	v_and_b32_e32 v50, 0xffff0000, v80
	v_cvt_pk_bf16_f32 v72, v84, v85
	v_med3_f32 v49, v49, s82, v229
	v_med3_f32 v50, v50, s82, v229
	v_cvt_pk_fp8_f32 v48, v49, v50 op_sel:[0,0,1]
	v_lshlrev_b32_e32 v49, 16, v72
	s_nop 0
	v_and_b32_e32 v50, 0xffff0000, v72
	v_med3_f32 v49, v49, s82, v229
	v_med3_f32 v51, v50, s82, v229
	v_mov_b32_e64 v50, v97
	v_cvt_pk_fp8_f32 v50, v49, v51
	v_lshlrev_b32_e32 v49, 16, v73
	s_nop 0
	v_and_b32_e32 v51, 0xffff0000, v73
	v_med3_f32 v49, v49, s82, v229
	v_med3_f32 v51, v51, s82, v229
	v_cvt_pk_fp8_f32 v50, v49, v51 op_sel:[0,0,1]
	v_lshlrev_b32_e32 v49, 16, v54
	s_nop 0
	v_and_b32_e32 v51, 0xffff0000, v54
	v_med3_f32 v54, v49, s82, v229
	v_med3_f32 v51, v51, s82, v229
	v_mov_b32_e64 v49, v97
	v_cvt_pk_fp8_f32 v49, v54, v51
	v_lshlrev_b32_e32 v51, 16, v52
	s_nop 0
	v_and_b32_e32 v52, 0xffff0000, v52
	v_med3_f32 v51, v51, s82, v229
	v_med3_f32 v52, v52, s82, v229
	v_cvt_pk_fp8_f32 v49, v51, v52 op_sel:[0,0,1]
	v_lshlrev_b32_e32 v51, 16, v74
	s_nop 0
	v_and_b32_e32 v52, 0xffff0000, v74
	v_med3_f32 v54, v51, s82, v229
	v_med3_f32 v52, v52, s82, v229
	v_mov_b32_e64 v51, v97
	v_cvt_pk_fp8_f32 v51, v54, v52
	v_lshlrev_b32_e32 v52, 16, v53
	s_nop 0
	v_and_b32_e32 v53, 0xffff0000, v53
	v_med3_f32 v52, v52, s82, v229
	v_med3_f32 v53, v53, s82, v229
	v_cvt_pk_fp8_f32 v51, v52, v53 op_sel:[0,0,1]
	v_lshlrev_b64 v[52:53], 10, v[190:191]
	v_lshl_add_u64 v[52:53], v[76:77], 0, v[52:53]
	global_store_dwordx4 v[52:53], v[48:51], off
	ds_read_b128 v[48:51], v209 offset:2176
	ds_read_b128 v[52:55], v209 offset:2192
	s_waitcnt lgkmcnt(1)
	v_lshlrev_b32_e32 v72, 16, v48
	v_and_b32_e32 v73, 0xffff0000, v48
	v_mov_b32_e64 v48, v79
	v_pk_mul_f32 v[72:73], v[48:49], v[72:73] op_sel_hi:[0,1]
	v_pk_mul_f32 v[68:69], v[68:69], v[72:73]
	v_lshlrev_b32_e32 v72, 16, v44
	s_nop 0
	v_and_b32_e32 v73, 0xffff0000, v44
	v_pk_mul_f32 v[68:69], v[68:69], v[72:73]
	v_lshlrev_b32_e32 v44, 16, v45
	s_nop 0
	v_cvt_pk_bf16_f32 v72, v68, v69
	s_waitcnt lgkmcnt(0)
	v_lshlrev_b32_e32 v68, 16, v52
	v_and_b32_e32 v69, 0xffff0000, v52
	v_pk_mul_f32 v[68:69], v[48:49], v[68:69] op_sel_hi:[0,1]
	v_pk_mul_f32 v[64:65], v[64:65], v[68:69]
	v_lshlrev_b32_e32 v68, 16, v40
	s_nop 0
	v_and_b32_e32 v69, 0xffff0000, v40
	v_pk_mul_f32 v[64:65], v[64:65], v[68:69]
	v_and_b32_e32 v45, 0xffff0000, v45
	v_cvt_pk_bf16_f32 v52, v64, v65
	v_lshlrev_b32_e32 v64, 16, v49
	s_nop 0
	v_and_b32_e32 v65, 0xffff0000, v49
	v_pk_mul_f32 v[64:65], v[48:49], v[64:65] op_sel_hi:[0,1]
	v_pk_mul_f32 v[64:65], v[70:71], v[64:65]
	v_lshlrev_b32_e32 v40, 16, v41
	s_nop 0
	v_pk_mul_f32 v[44:45], v[64:65], v[44:45]
	v_and_b32_e32 v41, 0xffff0000, v41
	v_cvt_pk_bf16_f32 v49, v44, v45
	v_lshlrev_b32_e32 v44, 16, v53
	s_nop 0
	v_and_b32_e32 v45, 0xffff0000, v53
	v_pk_mul_f32 v[44:45], v[48:49], v[44:45] op_sel_hi:[0,1]
	v_pk_mul_f32 v[44:45], v[66:67], v[44:45]
	s_nop 0
	s_nop 0
	v_pk_mul_f32 v[40:41], v[44:45], v[40:41]
	v_lshlrev_b32_e32 v44, 16, v46
	s_nop 0
	v_cvt_pk_bf16_f32 v53, v40, v41
	v_lshlrev_b32_e32 v40, 16, v50
	s_nop 0
	v_and_b32_e32 v41, 0xffff0000, v50
	v_pk_mul_f32 v[40:41], v[48:49], v[40:41] op_sel_hi:[0,1]
	v_pk_mul_f32 v[40:41], v[60:61], v[40:41]
	v_and_b32_e32 v45, 0xffff0000, v46
	v_pk_mul_f32 v[40:41], v[40:41], v[44:45]
	v_lshlrev_b32_e32 v44, 16, v42
	s_nop 0
	v_cvt_pk_bf16_f32 v46, v40, v41
	v_lshlrev_b32_e32 v40, 16, v54
	s_nop 0
	v_and_b32_e32 v41, 0xffff0000, v54
	v_pk_mul_f32 v[40:41], v[48:49], v[40:41] op_sel_hi:[0,1]
	v_pk_mul_f32 v[40:41], v[56:57], v[40:41]
	v_and_b32_e32 v45, 0xffff0000, v42
	v_pk_mul_f32 v[40:41], v[40:41], v[44:45]
	v_lshlrev_b32_e32 v44, 16, v47
	s_nop 0
	v_cvt_pk_bf16_f32 v50, v40, v41
	v_lshlrev_b32_e32 v40, 16, v51
	s_nop 0
	v_and_b32_e32 v41, 0xffff0000, v51
	v_pk_mul_f32 v[40:41], v[48:49], v[40:41] op_sel_hi:[0,1]
	v_pk_mul_f32 v[40:41], v[62:63], v[40:41]
	v_and_b32_e32 v45, 0xffff0000, v47
	v_pk_mul_f32 v[40:41], v[40:41], v[44:45]
	v_lshlrev_b32_e32 v42, 16, v43
	s_nop 0
	v_cvt_pk_bf16_f32 v44, v40, v41
	v_lshlrev_b32_e32 v40, 16, v55
	s_nop 0
	v_and_b32_e32 v41, 0xffff0000, v55
	v_pk_mul_f32 v[40:41], v[48:49], v[40:41] op_sel_hi:[0,1]
	v_pk_mul_f32 v[40:41], v[58:59], v[40:41]
	v_and_b32_e32 v43, 0xffff0000, v43
	v_pk_mul_f32 v[40:41], v[40:41], v[42:43]
	s_nop 0
	s_nop 0
	v_cvt_pk_bf16_f32 v45, v40, v41
	v_lshlrev_b32_e32 v40, 16, v72
	s_nop 0
	v_and_b32_e32 v41, 0xffff0000, v72
	v_med3_f32 v42, v40, s82, v229
	v_med3_f32 v41, v41, s82, v229
	v_mov_b32_e64 v40, v97
	v_cvt_pk_fp8_f32 v40, v42, v41
	v_lshlrev_b32_e32 v41, 16, v49
	s_nop 0
	v_and_b32_e32 v42, 0xffff0000, v49
	v_med3_f32 v41, v41, s82, v229
	v_med3_f32 v42, v42, s82, v229
	v_cvt_pk_fp8_f32 v40, v41, v42 op_sel:[0,0,1]
	v_lshlrev_b32_e32 v41, 16, v52
	s_nop 0
	v_and_b32_e32 v42, 0xffff0000, v52
	v_med3_f32 v41, v41, s82, v229
	v_med3_f32 v43, v42, s82, v229
	v_mov_b32_e64 v42, v97
	v_cvt_pk_fp8_f32 v42, v41, v43
	v_lshlrev_b32_e32 v41, 16, v53
	s_nop 0
	v_and_b32_e32 v43, 0xffff0000, v53
	v_med3_f32 v41, v41, s82, v229
	v_med3_f32 v43, v43, s82, v229
	v_cvt_pk_fp8_f32 v42, v41, v43 op_sel:[0,0,1]
	v_lshlrev_b32_e32 v41, 16, v46
	s_nop 0
	v_and_b32_e32 v43, 0xffff0000, v46
	v_med3_f32 v46, v41, s82, v229
	v_med3_f32 v43, v43, s82, v229
	v_mov_b32_e64 v41, v97
	v_cvt_pk_fp8_f32 v41, v46, v43
	v_lshlrev_b32_e32 v43, 16, v44
	s_nop 0
	v_and_b32_e32 v44, 0xffff0000, v44
	v_med3_f32 v43, v43, s82, v229
	v_med3_f32 v44, v44, s82, v229
	v_cvt_pk_fp8_f32 v41, v43, v44 op_sel:[0,0,1]
	v_lshlrev_b32_e32 v43, 16, v50
	s_nop 0
	v_and_b32_e32 v44, 0xffff0000, v50
	v_med3_f32 v46, v43, s82, v229
	v_med3_f32 v44, v44, s82, v229
	v_mov_b32_e64 v43, v97
	v_cvt_pk_fp8_f32 v43, v46, v44
	v_lshlrev_b32_e32 v44, 16, v45
	s_nop 0
	v_and_b32_e32 v45, 0xffff0000, v45
	v_med3_f32 v44, v44, s82, v229
	v_med3_f32 v45, v45, s82, v229
	v_cvt_pk_fp8_f32 v43, v44, v45 op_sel:[0,0,1]
	v_or_b32_e32 v44, 8, v131
	v_or_b32_e32 v44, s92, v44
	v_or_b32_e32 v44, s24, v44
	v_mov_b32_e32 v45, s25
	v_lshlrev_b64 v[44:45], 10, v[44:45]
	v_lshl_add_u64 v[44:45], v[76:77], 0, v[44:45]
	global_store_dwordx4 v[44:45], v[40:43], off
	s_waitcnt lgkmcnt(0)
	s_cbranch_vccnz .LBB0_671
	global_load_dwordx4 v[24:27], v[178:179], off
	global_load_dwordx4 v[28:31], v[178:179], off offset:64
	global_load_dwordx4 v[32:35], v[182:183], off offset:1024
	global_load_dwordx4 v[36:39], v[182:183], off offset:1088
	s_andn2_b64 vcc, exec, s[18:19]
	s_cbranch_vccnz .LBB0_701
	global_load_dwordx4 v[0:3], v[184:185], off
	global_load_dwordx4 v[8:11], v[184:185], off offset:64
	s_andn2_b64 vcc, exec, s[20:21]
	s_cbranch_vccnz .LBB0_669
	s_branch .LBB0_702

.LBB0_702:
	s_nop 0
	global_load_dwordx4 v[4:7], v[186:187], off
	global_load_dwordx4 v[16:19], v[186:187], off offset:64
	s_branch .LBB0_669
.LBB0_703:
	s_nop 0
	global_load_dwordx4 v[12:15], v[188:189], off
	global_load_dwordx4 v[20:23], v[188:189], off offset:64
	s_branch .LBB0_670

.LBB0_705:
	s_nop 0
	v_lshl_add_u64 v[16:17], s[26:27], 1, v[168:169]
	global_load_dwordx4 v[4:7], v[16:17], off offset:1024
	s_nop 0
	s_nop 0
	global_load_dwordx4 v[16:19], v[16:17], off offset:1088
	s_andn2_b64 vcc, exec, s[16:17]
	s_cbranch_vccz .LBB0_667
	s_branch .LBB0_668
.LBB0_706:
	s_nop 0
	v_readlane_b32 s2, v254, 5
	v_readlane_b32 s3, v254, 6
	s_cmp_ge_i32 s89, s3
	s_cbranch_scc1 .LBB0_835
	v_readlane_b32 s4, v254, 44
	v_readlane_b32 s5, v254, 45
	v_readlane_b32 s90, v255, 55
	v_readlane_b32 s58, v255, 53
	v_readlane_b32 s42, v254, 34
	s_mov_b64 s[2:3], -1
	s_and_b64 vcc, exec, s[4:5]
	v_readlane_b32 s64, v254, 4
	v_readlane_b32 s65, v255, 47
	s_mov_b32 s51, 0x42700000
	v_readlane_b32 s60, v255, 52
	v_readlane_b32 s91, v255, 56
	v_readlane_b32 s59, v255, 54
	v_readlane_b32 s44, v254, 48
	v_readlane_b32 s43, v254, 35
	s_cbranch_vccz .LBB0_1617
	s_mov_b32 s2, s97
	s_waitcnt vmcnt(0)
	s_waitcnt vmcnt(0) lgkmcnt(0)
	s_barrier
	s_nop 0
	v_mbcnt_lo_u32_b32 v0, -1, s2
	v_mbcnt_hi_u32_b32 v0, -1, v0
	v_cmp_eq_u32_e32 vcc, s65, v0
	s_and_saveexec_b64 s[38:39], vcc
	s_cbranch_execz .LBB0_1616
	s_nop 0
	v_readlane_b32 s40, v253, 12
	v_readlane_b32 s2, v253, 14
	v_readlane_b32 s41, v253, 13
	v_readlane_b32 s22, v253, 17
	v_mov_b32_e32 v0, s2
	s_waitcnt vmcnt(0) expcnt(0) lgkmcnt(0)
	ds_read_b32 v2, v0
	ds_read_b32 v0, v0 offset:4
	s_waitcnt lgkmcnt(1)
	v_cmp_ne_u32_e32 vcc, 0, v2
	s_cbranch_vccnz .LBB0_866
	s_nop 0
	v_readlane_b32 s2, v253, 6
	v_readlane_b32 s3, v253, 7
	s_load_dwordx2 s[6:7], s[2:3], 0x4
	s_add_u32 s2, s40, 0x1000
	s_addc_u32 s3, s41, 0
	s_nop 0
	s_add_u32 s4, s40, 0x1100
	s_addc_u32 s5, s41, 0
	s_waitcnt lgkmcnt(0)
	s_mul_i32 s23, s6, s61
	s_nop 0
	s_add_u32 s6, s40, 0x1200
	s_mul_i32 s23, s23, s7
	s_addc_u32 s7, s41, 0
	s_add_u32 s8, s40, 0x1300
	s_addc_u32 s9, s41, 0
	s_mov_b32 s30, 1
	s_mov_b64 s[10:11], 0
	s_branch .LBB0_828
.LBB0_711:
	s_mov_b32 s60, s90
	s_nop 0
	v_readlane_b32 s90, v255, 55
	v_readlane_b32 s61, v254, 3
	v_readlane_b32 s64, v254, 4
	v_readlane_b32 s65, v255, 47
	s_mov_b32 s51, 0x42700000
	v_readlane_b32 s91, v255, 56
	s_waitcnt lgkmcnt(0)
	s_barrier
.LBB0_712:
	v_readlane_b32 s2, v254, 22
	s_cmp_lt_u32 s2, 3
	s_nop 0
	v_readlane_b32 s3, v254, 23
	s_cbranch_scc1 .LBB0_806
	s_andn2_b64 vcc, exec, s[42:43]
	s_mov_b32 s24, 16
	s_cbranch_vccnz .LBB0_715
	v_readlane_b32 s24, v255, 8
.LBB0_715:
	s_cmp_lt_i32 s24, 1
	s_cbranch_scc1 .LBB0_806
	s_add_u32 s25, s70, 0x1ee00000
	s_addc_u32 s26, s71, 0
	s_mov_b32 s27, 0
	s_mov_b32 s28, -1
	s_nop 0
	v_readlane_b32 s50, v254, 49
	s_branch .LBB0_718
.LBB0_717:
	s_or_b64 exec, exec, s[2:3]
	s_waitcnt lgkmcnt(0)
	s_nop 0
	ds_read_b128 v[32:35], v219 offset:49280
	ds_read_b128 v[36:39], v219 offset:49312
	s_lshl_b32 s2, s29, 12
	s_add_i32 s2, s2, 0
	v_lshlrev_b32_e32 v48, 1, v214
	s_waitcnt lgkmcnt(1)
	v_rcp_f32_e32 v40, v32
	v_rcp_f32_e32 v41, v33
	v_lshlrev_b32_e32 v49, 9, v215
	s_nop 0
	v_add3_u32 v48, s2, v48, v49
	v_mul_f32_e64 v0, v0, v40
	v_cvt_pk_bf16_f32 v0, v0, s0
	v_rcp_f32_e32 v42, v34
	v_rcp_f32_e32 v43, v35
	s_waitcnt lgkmcnt(0)
	v_rcp_f32_e32 v44, v36
	ds_read_b128 v[32:35], v219 offset:49344
	v_rcp_f32_e32 v45, v37
	v_rcp_f32_e32 v46, v38
	v_rcp_f32_e32 v47, v39
	s_nop 0
	ds_read_b128 v[36:39], v219 offset:49376
	ds_write_b16 v48, v0 offset:51264
	v_mul_f32_e64 v0, v17, v41
	v_cvt_pk_bf16_f32 v0, v0, s0
	ds_write_b16 v48, v0 offset:51328
	v_mul_f32_e64 v0, v1, v41
	v_cvt_pk_bf16_f32 v0, v0, s0
	ds_write_b16 v48, v0 offset:51392
	v_mul_f32_e64 v0, v18, v42
	v_cvt_pk_bf16_f32 v0, v0, s0
	ds_write_b16 v48, v0 offset:51456
	v_mul_f32_e64 v0, v2, v42
	v_cvt_pk_bf16_f32 v0, v0, s0
	ds_write_b16 v48, v0 offset:51520
	v_mul_f32_e64 v0, v19, v43
	v_cvt_pk_bf16_f32 v0, v0, s0
	ds_write_b16 v48, v0 offset:51584
	v_mul_f32_e64 v0, v3, v43
	v_cvt_pk_bf16_f32 v0, v0, s0
	ds_write_b16 v48, v0 offset:51648
	v_mul_f32_e64 v0, v20, v44
	v_cvt_pk_bf16_f32 v0, v0, s0
	ds_write_b16 v48, v0 offset:52224
	v_mul_f32_e64 v0, v4, v44
	v_cvt_pk_bf16_f32 v0, v0, s0
	ds_write_b16 v48, v0 offset:52288
	v_mul_f32_e64 v0, v21, v45
	v_cvt_pk_bf16_f32 v0, v0, s0
	ds_write_b16 v48, v0 offset:52352
	v_mul_f32_e64 v0, v5, v45
	v_cvt_pk_bf16_f32 v0, v0, s0
	ds_write_b16 v48, v0 offset:52416
	v_mul_f32_e64 v0, v22, v46
	v_cvt_pk_bf16_f32 v0, v0, s0
	ds_write_b16 v48, v0 offset:52480
	v_mul_f32_e64 v0, v6, v46
	v_cvt_pk_bf16_f32 v0, v0, s0
	s_waitcnt lgkmcnt(13)
	v_rcp_f32_e32 v32, v32
	ds_write_b16 v48, v0 offset:52544
	v_mul_f32_e64 v0, v23, v47
	v_cvt_pk_bf16_f32 v0, v0, s0
	ds_write_b16 v48, v0 offset:52608
	v_mul_f32_e64 v0, v7, v47
	v_cvt_pk_bf16_f32 v0, v0, s0
	v_rcp_f32_e32 v33, v33
	s_nop 0
	ds_write_b16 v48, v0 offset:52672
	v_mul_f32_e64 v0, v24, v32
	v_cvt_pk_bf16_f32 v0, v0, s0
	ds_write_b16 v48, v0 offset:53248
	v_mul_f32_e64 v0, v8, v32
	v_cvt_pk_bf16_f32 v0, v0, s0
	v_rcp_f32_e32 v34, v34
	s_nop 0
	ds_write_b16 v48, v0 offset:53312
	v_mul_f32_e64 v0, v25, v33
	v_cvt_pk_bf16_f32 v0, v0, s0
	ds_write_b16 v48, v0 offset:53376
	v_mul_f32_e64 v0, v9, v33
	v_cvt_pk_bf16_f32 v0, v0, s0
	v_rcp_f32_e32 v35, v35
	s_nop 0
	ds_write_b16 v48, v0 offset:53440
	v_mul_f32_e64 v0, v26, v34
	v_cvt_pk_bf16_f32 v0, v0, s0
	ds_write_b16 v48, v0 offset:53504
	v_mul_f32_e64 v0, v10, v34
	v_cvt_pk_bf16_f32 v0, v0, s0
	s_waitcnt lgkmcnt(14)
	v_rcp_f32_e32 v36, v36
	ds_write_b16 v48, v0 offset:53568
	v_mul_f32_e64 v0, v27, v35
	v_cvt_pk_bf16_f32 v0, v0, s0
	ds_write_b16 v48, v0 offset:53632
	v_mul_f32_e64 v0, v11, v35
	v_cvt_pk_bf16_f32 v0, v0, s0
	v_rcp_f32_e32 v37, v37
	s_nop 0
	ds_write_b16 v48, v0 offset:53696
	v_mul_f32_e64 v0, v28, v36
	v_cvt_pk_bf16_f32 v0, v0, s0
	ds_write_b16 v48, v0 offset:54272
	v_mul_f32_e64 v0, v12, v36
	v_cvt_pk_bf16_f32 v0, v0, s0
	v_rcp_f32_e32 v38, v38
	s_nop 0
	ds_write_b16 v48, v0 offset:54336
	v_mul_f32_e64 v0, v29, v37
	v_cvt_pk_bf16_f32 v0, v0, s0
	ds_write_b16 v48, v0 offset:54400
	v_mul_f32_e64 v0, v13, v37
	v_cvt_pk_bf16_f32 v0, v0, s0
	v_rcp_f32_e32 v39, v39
	s_nop 0
	ds_write_b16 v48, v0 offset:54464
	v_mul_f32_e64 v0, v30, v38
	v_cvt_pk_bf16_f32 v0, v0, s0
	ds_write_b16 v48, v0 offset:54528
	v_mul_f32_e64 v0, v14, v38
	v_cvt_pk_bf16_f32 v0, v0, s0
	ds_write_b16 v48, v0 offset:54592
	v_mul_f32_e64 v0, v31, v39
	v_cvt_pk_bf16_f32 v0, v0, s0
	v_mul_f32_e64 v16, v16, v40
	ds_write_b16 v48, v0 offset:54656
	v_mul_f32_e64 v0, v15, v39
	v_cvt_pk_bf16_f32 v16, v16, s0
	v_cvt_pk_bf16_f32 v0, v0, s0
	v_and_b32_e32 v96, 56, v203
	s_nop 0
	ds_write_b16 v48, v16 offset:51200
	ds_write_b16 v48, v0 offset:54720
	v_lshrrev_b32_e32 v12, 3, v199
	s_nop 0
	v_lshl_add_u32 v13, v96, 1, s2
	s_waitcnt lgkmcnt(0)
	s_nop 0
	v_lshl_add_u32 v0, v12, 7, v13
	ds_read_b128 v[0:3], v0 offset:51200
	v_or_b32_e32 v14, 8, v12
	s_nop 0
	v_lshl_add_u32 v4, v14, 7, v13
	ds_read_b128 v[4:7], v4 offset:51200
	s_add_u32 s2, s78, s10
	s_waitcnt lgkmcnt(1)
	v_lshlrev_b32_e32 v10, 16, v0
	s_nop 0
	v_and_b32_e32 v0, 0xffff0000, v0
	v_med3_f32 v10, v10, s82, v229
	v_med3_f32 v11, v0, s82, v229
	v_mov_b32_e64 v0, v97
	v_cvt_pk_fp8_f32 v0, v10, v11
	v_lshlrev_b32_e32 v10, 16, v1
	s_nop 0
	v_and_b32_e32 v1, 0xffff0000, v1
	v_med3_f32 v10, v10, s82, v229
	v_med3_f32 v1, v1, s82, v229
	v_cvt_pk_fp8_f32 v0, v10, v1 op_sel:[0,0,1]
	v_lshlrev_b32_e32 v1, 16, v2
	s_nop 0
	v_and_b32_e32 v2, 0xffff0000, v2
	v_med3_f32 v10, v1, s82, v229
	v_med3_f32 v2, v2, s82, v229
	v_mov_b32_e64 v1, v97
	v_cvt_pk_fp8_f32 v1, v10, v2
	v_lshlrev_b32_e32 v2, 16, v3
	s_nop 0
	v_and_b32_e32 v3, 0xffff0000, v3
	v_med3_f32 v2, v2, s82, v229
	v_med3_f32 v3, v3, s82, v229
	v_cvt_pk_fp8_f32 v1, v2, v3 op_sel:[0,0,1]
	s_addc_u32 s3, s79, s11
	v_or_b32_e32 v10, s8, v12
	v_mov_b32_e64 v11, s9
	v_lshl_add_u64 v[8:9], s[2:3], 0, v[96:97]
	v_lshlrev_b64 v[2:3], 10, v[10:11]
	v_lshl_add_u64 v[2:3], v[8:9], 0, v[2:3]
	global_store_dwordx2 v[2:3], v[0:1], off
	s_waitcnt lgkmcnt(0)
	v_lshlrev_b32_e32 v0, 16, v4
	v_and_b32_e32 v1, 0xffff0000, v4
	v_med3_f32 v0, v0, s82, v229
	v_med3_f32 v1, v1, s82, v229
	v_mov_b32_e64 v4, v97
	v_cvt_pk_fp8_f32 v4, v0, v1
	v_lshlrev_b32_e32 v0, 16, v5
	s_nop 0
	v_and_b32_e32 v1, 0xffff0000, v5
	v_med3_f32 v0, v0, s82, v229
	v_med3_f32 v1, v1, s82, v229
	v_cvt_pk_fp8_f32 v4, v0, v1 op_sel:[0,0,1]
	v_lshlrev_b32_e32 v0, 16, v6
	s_nop 0
	v_and_b32_e32 v1, 0xffff0000, v6
	v_med3_f32 v0, v0, s82, v229
	v_med3_f32 v1, v1, s82, v229
	v_mov_b32_e64 v5, v97
	v_cvt_pk_fp8_f32 v5, v0, v1
	v_lshlrev_b32_e32 v0, 16, v7
	s_nop 0
	v_and_b32_e32 v1, 0xffff0000, v7
	v_med3_f32 v0, v0, s82, v229
	v_med3_f32 v1, v1, s82, v229
	v_or_b32_e32 v10, s8, v14
	s_nop 0
	v_cvt_pk_fp8_f32 v5, v0, v1 op_sel:[0,0,1]
	v_lshlrev_b64 v[0:1], 10, v[10:11]
	v_or_b32_e32 v10, 16, v12
	s_nop 0
	v_lshl_add_u64 v[6:7], v[8:9], 0, v[0:1]
	v_lshl_add_u32 v0, v10, 7, v13
	ds_read_b128 v[0:3], v0 offset:51200
	v_or_b32_e32 v12, 24, v12
	s_nop 0
	global_store_dwordx2 v[6:7], v[4:5], off
	v_lshl_add_u32 v4, v12, 7, v13
	ds_read_b128 v[4:7], v4 offset:51200
	s_waitcnt lgkmcnt(1)
	v_lshlrev_b32_e32 v13, 16, v0
	v_and_b32_e32 v0, 0xffff0000, v0
	v_med3_f32 v13, v13, s82, v229
	v_med3_f32 v14, v0, s82, v229
	v_mov_b32_e64 v0, v97
	v_cvt_pk_fp8_f32 v0, v13, v14
	v_lshlrev_b32_e32 v13, 16, v1
	s_nop 0
	v_and_b32_e32 v1, 0xffff0000, v1
	v_med3_f32 v13, v13, s82, v229
	v_med3_f32 v1, v1, s82, v229
	v_cvt_pk_fp8_f32 v0, v13, v1 op_sel:[0,0,1]
	v_lshlrev_b32_e32 v1, 16, v2
	s_nop 0
	v_and_b32_e32 v2, 0xffff0000, v2
	v_med3_f32 v13, v1, s82, v229
	v_med3_f32 v2, v2, s82, v229
	v_mov_b32_e64 v1, v97
	v_cvt_pk_fp8_f32 v1, v13, v2
	v_lshlrev_b32_e32 v2, 16, v3
	s_nop 0
	v_and_b32_e32 v3, 0xffff0000, v3
	v_med3_f32 v2, v2, s82, v229
	v_med3_f32 v3, v3, s82, v229
	v_cvt_pk_fp8_f32 v1, v2, v3 op_sel:[0,0,1]
	v_or_b32_e32 v10, s8, v10
	s_nop 0
	v_lshlrev_b64 v[2:3], 10, v[10:11]
	v_lshl_add_u64 v[2:3], v[8:9], 0, v[2:3]
	global_store_dwordx2 v[2:3], v[0:1], off
	s_waitcnt lgkmcnt(0)
	v_lshlrev_b32_e32 v0, 16, v4
	v_and_b32_e32 v1, 0xffff0000, v4
	v_med3_f32 v2, v0, s82, v229
	v_med3_f32 v1, v1, s82, v229
	v_mov_b32_e64 v0, v97
	v_cvt_pk_fp8_f32 v0, v2, v1
	v_lshlrev_b32_e32 v1, 16, v5
	s_nop 0
	v_and_b32_e32 v2, 0xffff0000, v5
	v_med3_f32 v1, v1, s82, v229
	v_med3_f32 v2, v2, s82, v229
	v_cvt_pk_fp8_f32 v0, v1, v2 op_sel:[0,0,1]
	v_lshlrev_b32_e32 v1, 16, v6
	s_nop 0
	v_and_b32_e32 v2, 0xffff0000, v6
	v_med3_f32 v3, v1, s82, v229
	v_med3_f32 v2, v2, s82, v229
	v_mov_b32_e64 v1, v97
	v_cvt_pk_fp8_f32 v1, v3, v2
	v_lshlrev_b32_e32 v2, 16, v7
	s_nop 0
	v_and_b32_e32 v3, 0xffff0000, v7
	v_med3_f32 v2, v2, s82, v229
	v_med3_f32 v3, v3, s82, v229
	v_cvt_pk_fp8_f32 v1, v2, v3 op_sel:[0,0,1]
	v_or_b32_e32 v10, s8, v12
	s_nop 0
	v_lshlrev_b64 v[2:3], 10, v[10:11]
	v_lshl_add_u64 v[2:3], v[8:9], 0, v[2:3]
	global_store_dwordx2 v[2:3], v[0:1], off
	s_waitcnt lgkmcnt(0)
	s_barrier
	s_add_i32 s27, s27, 1
	s_cmp_lg_u32 s27, s24
	s_cbranch_scc0 .LBB0_806

.LBB0_724:
	v_lshlrev_b32_e32 v32, 1, v118
	v_and_b32_e32 v218, 32, v32
	v_lshrrev_b32_e32 v32, 2, v118
	v_and_or_b32 v32, v32, 3, v236
	v_lshlrev_b32_e32 v217, 6, v32
	v_add_u32_e32 v32, 0, v218
	v_add3_u32 v239, v32, v216, v217
	v_max3_f32 v32, v16, v17, v0
	v_max3_f32 v33, v18, v19, v1
	s_and_b32 s19, s41, 0x3fffffc0
	v_max3_f32 v32, v32, v2, v3
	v_max3_f32 v33, v33, v22, v23
	s_add_i32 s20, s45, 0x100
	v_max3_f32 v32, v32, v20, v21
	v_max3_f32 v33, v33, v6, v7
	s_lshl_b32 s19, s19, 2
	s_nop 0
	v_max3_f32 v32, v32, v4, v5
	v_max3_f32 v33, v33, v26, v27
	s_lshr_b32 s39, s20, 6
	s_nop 0
	v_max3_f32 v32, v32, v24, v25
	v_max3_f32 v33, v33, v10, v11
	s_mov_b64 s[20:21], 0x60000
	v_max3_f32 v32, v32, v8, v9
	v_max3_f32 v33, v33, v30, v31
	s_add_i32 s19, s19, 0
	s_nop 0
	v_max3_f32 v32, v32, v28, v29
	v_max3_f32 v33, v33, v14, v15
	s_cmp_lg_u32 0, -1
	s_nop 0
	v_max3_f32 v32, v32, v12, v13
	s_mov_b32 s96, 1
	v_max_f32_e32 v32, v32, v33
	s_mov_b32 s22, 0
	v_mov_b32_e32 v33, v32
	s_nop 1
	v_permlane32_swap_b32_e32 v32, v33
	v_max_f32_e64 v32, v32, v33
	v_lshl_add_u32 v235, v214, 2, s19
	v_sub_f32_e32 v64, v0, v32
	v_sub_f32_e32 v0, v17, v32
	v_sub_f32_e32 v16, v16, v32
	v_sub_f32_e32 v65, v1, v32
	v_sub_f32_e32 v1, v18, v32
	v_sub_f32_e32 v66, v2, v32
	v_sub_f32_e32 v2, v19, v32
	s_nop 0
	v_exp_f32_e64 v81, v0
	v_lshl_add_u32 v0, v236, 2, 0
	v_sub_f32_e32 v67, v3, v32
	v_sub_f32_e32 v3, v20, v32
	v_sub_f32_e32 v68, v4, v32
	v_sub_f32_e32 v4, v21, v32
	v_sub_f32_e32 v69, v5, v32
	v_sub_f32_e32 v5, v22, v32
	v_sub_f32_e32 v70, v6, v32
	v_sub_f32_e32 v6, v23, v32
	v_sub_f32_e32 v71, v7, v32
	v_sub_f32_e32 v7, v24, v32
	v_sub_f32_e32 v72, v8, v32
	v_sub_f32_e32 v8, v25, v32
	v_sub_f32_e32 v73, v9, v32
	v_sub_f32_e32 v9, v26, v32
	v_sub_f32_e32 v74, v10, v32
	v_sub_f32_e32 v10, v27, v32
	v_sub_f32_e32 v75, v11, v32
	v_sub_f32_e32 v11, v28, v32
	v_sub_f32_e32 v76, v12, v32
	v_sub_f32_e32 v12, v29, v32
	v_sub_f32_e32 v77, v13, v32
	v_sub_f32_e32 v13, v30, v32
	v_sub_f32_e32 v78, v14, v32
	v_sub_f32_e32 v14, v31, v32
	v_add_u32_e32 v28, 0x15100, v0
	v_sub_f32_e32 v79, v15, v32
	v_exp_f32_e32 v80, v16
	v_exp_f32_e32 v82, v1
	v_exp_f32_e32 v83, v2
	v_exp_f32_e32 v84, v3
	v_exp_f32_e32 v85, v4
	v_exp_f32_e32 v86, v5
	v_exp_f32_e32 v87, v6
	v_exp_f32_e32 v88, v7
	v_exp_f32_e32 v89, v8
	v_exp_f32_e32 v90, v9
	v_exp_f32_e32 v91, v10
	v_exp_f32_e32 v92, v11
	v_exp_f32_e32 v93, v12
	v_exp_f32_e32 v94, v13
	v_exp_f32_e32 v95, v14
	ds_read_b128 v[0:3], v28
	ds_read_b128 v[4:7], v28 offset:32
	ds_read_b128 v[8:11], v28 offset:128
	ds_read_b128 v[12:15], v28 offset:160
	ds_read_b128 v[16:19], v28 offset:64
	ds_read_b128 v[20:23], v28 offset:96
	ds_read_b128 v[24:27], v28 offset:192
	ds_read_b128 v[28:31], v28 offset:224
	s_waitcnt vmcnt(0) lgkmcnt(0)
	s_barrier
	v_add_f32_e64 v202, v97, v32
	v_exp_f32_e32 v64, v64
	s_waitcnt lgkmcnt(7)
	v_pk_add_f32 v[48:49], v[202:203], v[0:1] op_sel_hi:[0,1] neg_lo:[1,0] neg_hi:[1,0]
	v_lshl_add_u64 v[0:1], v[114:115], 0, s[20:21]
	s_mov_b32 s20, m0
	s_mov_b32 m0, s30
	s_nop 0
	s_nop 0
	global_load_lds_dwordx4 v[0:1], off
	s_mov_b32 m0, s20
	s_nop 0
	s_mov_b64 s[20:21], 0x20000
	v_lshl_add_u64 v[0:1], v[116:117], 0, s[20:21]
	s_cselect_b32 s20, 0, 0
	s_add_i32 s18, s20, s18
	s_add_i32 s18, s18, 0x8000
	s_mov_b32 s20, m0
	s_mov_b32 m0, s18
	s_nop 0
	s_nop 0
	global_load_lds_dwordx4 v[0:1], off
	s_mov_b32 m0, s20
	s_nop 0
	ds_read_b128 v[158:161], v238 offset:8192
	ds_read_b128 v[146:149], v238 offset:8704
	ds_read_b128 v[154:157], v238 offset:10240
	ds_read_b128 v[142:145], v238 offset:10752
	ds_read_b128 v[150:153], v238 offset:12288
	ds_read_b128 v[138:141], v238 offset:12800
	ds_read_b128 v[134:137], v238 offset:14336
	ds_read_b128 v[130:133], v238 offset:14848
	v_exp_f32_e32 v65, v65
	v_exp_f32_e32 v66, v66
	v_exp_f32_e32 v67, v67
	v_exp_f32_e32 v68, v68
	v_exp_f32_e32 v69, v69
	v_exp_f32_e32 v70, v70
	v_exp_f32_e32 v71, v71
	v_exp_f32_e32 v72, v72
	v_exp_f32_e32 v73, v73
	v_exp_f32_e32 v74, v74
	v_exp_f32_e32 v75, v75
	v_exp_f32_e32 v76, v76
	v_exp_f32_e32 v77, v77
	v_exp_f32_e32 v78, v78
	v_exp_f32_e64 v79, v79
	s_waitcnt vmcnt(2) lgkmcnt(0)
	s_barrier
	v_and_b32_e32 v0, 3, v118
	s_waitcnt lgkmcnt(13)
	v_pk_add_f32 v[32:33], v[202:203], v[8:9] op_sel_hi:[0,1] neg_lo:[1,0] neg_hi:[1,0]
	v_pk_add_f32 v[50:51], v[202:203], v[2:3] op_sel_hi:[0,1] neg_lo:[1,0] neg_hi:[1,0]
	v_pk_add_f32 v[34:35], v[202:203], v[10:11] op_sel_hi:[0,1] neg_lo:[1,0] neg_hi:[1,0]
	v_pk_add_f32 v[52:53], v[202:203], v[4:5] op_sel_hi:[0,1] neg_lo:[1,0] neg_hi:[1,0]
	s_waitcnt lgkmcnt(12)
	s_nop 0
	v_pk_add_f32 v[36:37], v[202:203], v[12:13] op_sel_hi:[0,1] neg_lo:[1,0] neg_hi:[1,0]
	v_pk_add_f32 v[54:55], v[202:203], v[6:7] op_sel_hi:[0,1] neg_lo:[1,0] neg_hi:[1,0]
	v_pk_add_f32 v[38:39], v[202:203], v[14:15] op_sel_hi:[0,1] neg_lo:[1,0] neg_hi:[1,0]
	s_waitcnt lgkmcnt(11)
	s_nop 0
	v_pk_add_f32 v[56:57], v[202:203], v[16:17] op_sel_hi:[0,1] neg_lo:[1,0] neg_hi:[1,0]
	s_waitcnt lgkmcnt(9)
	s_nop 0
	v_pk_add_f32 v[40:41], v[202:203], v[24:25] op_sel_hi:[0,1] neg_lo:[1,0] neg_hi:[1,0]
	v_pk_add_f32 v[58:59], v[202:203], v[18:19] op_sel_hi:[0,1] neg_lo:[1,0] neg_hi:[1,0]
	v_pk_add_f32 v[42:43], v[202:203], v[26:27] op_sel_hi:[0,1] neg_lo:[1,0] neg_hi:[1,0]
	v_pk_add_f32 v[60:61], v[202:203], v[20:21] op_sel_hi:[0,1] neg_lo:[1,0] neg_hi:[1,0]
	s_waitcnt lgkmcnt(8)
	s_nop 0
	v_pk_add_f32 v[44:45], v[202:203], v[28:29] op_sel_hi:[0,1] neg_lo:[1,0] neg_hi:[1,0]
	v_pk_add_f32 v[62:63], v[202:203], v[22:23] op_sel_hi:[0,1] neg_lo:[1,0] neg_hi:[1,0]
	v_pk_add_f32 v[46:47], v[202:203], v[30:31] op_sel_hi:[0,1] neg_lo:[1,0] neg_hi:[1,0]
	s_andn2_b64 vcc, exec, s[2:3]
	s_nop 0
	v_cmp_gt_u32_e64 s[2:3], 32, v199
	v_lshl_add_u32 v219, v236, 2, s19
	v_lshlrev_b32_e32 v204, 4, v0
	s_cbranch_vccnz .LBB0_742
	s_lshl_b64 s[18:19], s[4:5], 1
	s_add_u32 s18, s70, s18
	s_addc_u32 s19, s71, s19
	s_add_u32 s18, s18, s14
	s_addc_u32 s19, s19, s15
	s_nop 0
	v_lshl_add_u64 v[206:207], s[18:19], 0, v[96:97]
	s_lshl_b64 s[18:19], s[16:17], 1
	s_add_u32 s18, s18, s14
	v_mov_b32_e32 v205, v97
	s_addc_u32 s19, s19, s15
	v_lshl_add_u64 v[0:1], s[18:19], 0, v[204:205]
	s_lshl_b32 s18, s41, 9
	s_nop 0
	s_and_b32 s18, s18, 0x18000
	v_lshl_or_b32 v2, v241, 11, s18
	v_mov_b32_e64 v3, v97
	v_lshl_add_u64 v[0:1], v[0:1], 0, v[2:3]
	v_mov_b32_e32 v16, v97
	v_mov_b32_e32 v17, v97
	v_lshl_add_u64 v[208:209], s[70:71], 0, v[0:1]
	v_subrev_u32_e64 v245, s14, v0
	v_add_u32_e32 v245, 0x7fc0000, v245
	v_lshl_add_u32 v244, s4, 1, v96
	s_add_u32 s98, s70, s14
	s_addc_u32 s99, s71, s15
	s_add_u32 s98, s98, s12
	s_addc_u32 s99, s99, s13
	s_add_u32 s98, s98, 0x16e80000
	s_addc_u32 s99, s99, 0
	s_nop 0
	v_readlane_b32 s18, v253, 11
	v_mov_b32_e32 v18, v97
	v_mov_b32_e32 v19, v97
	v_mov_b32_e32 v20, v97
	v_mov_b32_e32 v21, v97
	v_mov_b32_e32 v22, v97
	v_mov_b32_e32 v23, v97
	v_mov_b32_e32 v24, v97
	v_mov_b32_e32 v25, v97
	v_mov_b32_e32 v26, v97
	v_mov_b32_e32 v27, v97
	v_mov_b32_e32 v28, v97
	v_mov_b32_e32 v29, v97
	v_mov_b32_e64 v30, v97
	v_mov_b32_e32 v31, v97
	v_mov_b64_e32 v[0:1], v[16:17]
	v_lshl_add_u32 v205, v215, 4, s18
	s_mov_b32 s18, 0
	s_movk_i32 s22, 0x4000
	s_movk_i32 s38, 0x2000
	v_mov_b32_e32 v240, 0
	s_mov_b32 s23, 6
	v_mov_b64_e32 v[2:3], v[18:19]
	v_mov_b64_e32 v[4:5], v[20:21]
	v_mov_b64_e32 v[6:7], v[22:23]
	v_mov_b64_e32 v[8:9], v[24:25]
	v_mov_b64_e32 v[10:11], v[26:27]
	v_mov_b64_e32 v[12:13], v[28:29]
	v_mov_b64_e32 v[14:15], v[30:31]
	s_nop 0
	s_nop 0

.LBB0_803:
	v_max_f32_e32 v77, v77, v77
	v_max_f32_e32 v78, 0, v77
	v_exp_f32_e64 v77, -v78
	v_cmp_gt_u32_e32 vcc, 32, v199
	s_and_saveexec_b64 s[4:5], vcc
	ds_write_b32 v235, v77 offset:49152
	s_or_b64 exec, exec, s[4:5]
	v_sub_f32_e32 v63, v63, v78
	v_sub_f32_e32 v62, v62, v78
	v_sub_f32_e32 v61, v61, v78
	v_sub_f32_e32 v60, v60, v78
	v_sub_f32_e32 v59, v59, v78
	v_sub_f32_e32 v58, v58, v78
	v_sub_f32_e32 v57, v57, v78
	v_sub_f32_e32 v56, v56, v78
	v_sub_f32_e32 v55, v55, v78
	v_sub_f32_e32 v54, v54, v78
	v_sub_f32_e32 v53, v53, v78
	v_sub_f32_e32 v52, v52, v78
	v_sub_f32_e32 v51, v51, v78
	v_sub_f32_e32 v50, v50, v78
	v_sub_f32_e32 v49, v49, v78
	v_sub_f32_e32 v48, v48, v78
	v_sub_f32_e32 v47, v47, v78
	v_sub_f32_e32 v46, v46, v78
	v_sub_f32_e32 v45, v45, v78
	v_sub_f32_e32 v44, v44, v78
	v_sub_f32_e32 v43, v43, v78
	v_sub_f32_e32 v42, v42, v78
	v_sub_f32_e32 v41, v41, v78
	v_sub_f32_e32 v40, v40, v78
	v_sub_f32_e32 v39, v39, v78
	v_sub_f32_e32 v38, v38, v78
	v_sub_f32_e32 v37, v37, v78
	v_sub_f32_e32 v36, v36, v78
	v_sub_f32_e32 v35, v35, v78
	v_sub_f32_e32 v34, v34, v78
	v_sub_f32_e32 v33, v33, v78
	v_sub_f32_e64 v32, v32, v78
	v_mul_f32_e32 v76, v76, v77
	s_branch .LBB0_745
.LBB0_806:
	v_readlane_b32 s2, v254, 5
	s_add_i32 s45, s89, 1
	s_nop 0
	v_readlane_b32 s3, v254, 6
	s_cmp_lt_i32 s45, s3
	s_cselect_b64 s[46:47], -1, 0
	s_and_b64 vcc, exec, s[0:1]
	s_and_b64 s[38:39], s[6:7], s[46:47]
	s_cbranch_vccnz .LBB0_812
	s_and_b64 vcc, exec, s[42:43]
	s_cbranch_vccz .LBB0_822
	s_mov_b64 s[40:41], 0
	s_and_b64 vcc, exec, s[38:39]
	s_mov_b64 s[0:1], 0
	s_cbranch_vccz .LBB0_823
	s_mov_b32 s0, s97
	s_waitcnt vmcnt(0)
	s_waitcnt vmcnt(0) lgkmcnt(0)
	s_barrier
	s_nop 0
	v_mbcnt_lo_u32_b32 v0, -1, s0
	v_mbcnt_hi_u32_b32 v0, -1, v0
	v_cmp_eq_u32_e32 vcc, s65, v0
	s_and_saveexec_b64 s[48:49], vcc
	s_cbranch_execz .LBB0_881
	s_nop 0
	v_readlane_b32 s52, v253, 12
	v_readlane_b32 s0, v253, 14
	v_readlane_b32 s22, v253, 17
	v_readlane_b32 s53, v253, 13
	v_mov_b32_e32 v0, s0
	s_waitcnt vmcnt(0) expcnt(0) lgkmcnt(0)
	ds_read_b32 v2, v0
	ds_read_b32 v0, v0 offset:4
	s_waitcnt lgkmcnt(1)
	v_cmp_ne_u32_e32 vcc, 0, v2
	s_cbranch_vccnz .LBB0_839
	s_nop 0
	v_readlane_b32 s0, v253, 6
	v_readlane_b32 s1, v253, 7
	s_load_dwordx2 s[4:5], s[0:1], 0x4
	s_add_u32 s0, s52, 0x1000
	s_addc_u32 s1, s53, 0
	s_nop 0
	s_add_u32 s2, s52, 0x1100
	s_addc_u32 s3, s53, 0
	s_waitcnt lgkmcnt(0)
	s_mul_i32 s23, s4, s61
	s_nop 0
	s_add_u32 s4, s52, 0x1200
	s_mul_i32 s23, s23, s5
	s_addc_u32 s5, s53, 0
	s_add_u32 s6, s52, 0x1300
	s_addc_u32 s7, s53, 0
	s_mov_b32 s28, 1
	s_mov_b64 s[8:9], 0
	s_branch .LBB0_815

.LBB0_815:
	v_mov_b64_e32 v[12:13], s[52:53]
	s_nop 0
	flat_load_dword v1, v[12:13] offset:1024 sc1
	flat_load_dword v0, v[12:13] offset:1280 sc1
	flat_load_dword v2, v[12:13] offset:1536 sc1
	s_or_b64 s[14:15], s[14:15], exec
	s_or_b64 s[12:13], s[12:13], exec
	s_waitcnt vmcnt(0) lgkmcnt(0)
	v_add_u32_e32 v3, v0, v1
	v_add_u32_e64 v4, v3, v2
	flat_load_dword v3, v[12:13] offset:1792 sc1
	s_waitcnt vmcnt(0) lgkmcnt(0)
	v_add_u32_e32 v5, v4, v3
	flat_load_dword v4, v[12:13] offset:2048 sc1
	s_waitcnt vmcnt(0) lgkmcnt(0)
	v_add_u32_e32 v6, v5, v4
	flat_load_dword v5, v[12:13] offset:2304 sc1
	s_waitcnt vmcnt(0) lgkmcnt(0)
	v_add_u32_e32 v7, v6, v5
	flat_load_dword v6, v[12:13] offset:2560 sc1
	s_waitcnt vmcnt(0) lgkmcnt(0)
	v_add_u32_e32 v8, v7, v6
	flat_load_dword v7, v[12:13] offset:2816 sc1
	s_waitcnt vmcnt(0) lgkmcnt(0)
	v_add_u32_e32 v9, v8, v7
	flat_load_dword v8, v[12:13] offset:3072 sc1
	s_waitcnt vmcnt(0) lgkmcnt(0)
	v_add_u32_e32 v10, v9, v8
	flat_load_dword v9, v[12:13] offset:3328 sc1
	s_waitcnt vmcnt(0) lgkmcnt(0)
	v_add_u32_e32 v11, v10, v9
	flat_load_dword v10, v[12:13] offset:3584 sc1
	s_waitcnt vmcnt(0) lgkmcnt(0)
	v_add_u32_e32 v14, v11, v10
	flat_load_dword v11, v[12:13] offset:3840 sc1
	v_mov_b64_e32 v[12:13], s[0:1]
	s_nop 0
	flat_load_dword v12, v[12:13] sc1
	s_waitcnt vmcnt(0) lgkmcnt(0)
	v_add_u32_e32 v14, v14, v11
	v_add_u32_e32 v16, v14, v12
	v_mov_b64_e32 v[14:15], s[2:3]
	flat_load_dword v13, v[14:15] sc1
	v_mov_b64_e32 v[14:15], s[4:5]
	s_nop 0
	flat_load_dword v14, v[14:15] sc1
	s_waitcnt vmcnt(0) lgkmcnt(0)
	v_add_u32_e32 v16, v16, v13
	v_add_u32_e32 v18, v16, v14
	v_mov_b64_e32 v[16:17], s[6:7]
	flat_load_dword v15, v[16:17] sc1
	s_waitcnt vmcnt(0) lgkmcnt(0)
	v_add_u32_e32 v16, v18, v15
	v_cmp_ne_u32_e32 vcc, s23, v16
	s_and_saveexec_b64 s[16:17], vcc
	s_cbranch_execz .LBB0_814
	s_nop 0
	s_and_b32 s20, s28, 0xff
	s_mov_b64 s[18:19], -1
	s_cmp_eq_u32 s20, 0
	s_mov_b64 s[24:25], -1
	s_mov_b64 s[20:21], -1
	s_sleep 1
	s_cbranch_scc1 .LBB0_818
	s_and_saveexec_b64 s[26:27], s[24:25]
	s_cbranch_execz .LBB0_813
	s_branch .LBB0_821

.LBB0_835:
	s_nop 0
	v_readlane_b32 s90, v255, 55
	v_readlane_b32 s58, v255, 53
	v_readlane_b32 s42, v254, 34
	v_readlane_b32 s64, v254, 4
	v_readlane_b32 s65, v255, 47
	s_mov_b32 s51, 0x42700000
	v_readlane_b32 s60, v255, 52
	v_readlane_b32 s91, v255, 56
	v_readlane_b32 s59, v255, 54
	v_readlane_b32 s44, v254, 48
	v_readlane_b32 s43, v254, 35
	s_branch .LBB0_657

.LBB0_838:
	s_or_b64 exec, exec, s[0:1]
	s_cmp_eq_u32 s22, 15
	s_cselect_b64 vcc, -1, 0
	s_cmp_eq_u32 s22, 14
	s_cselect_b64 s[0:1], -1, 0
	s_cmp_eq_u32 s22, 13
	s_cselect_b64 s[2:3], -1, 0
	s_cmp_eq_u32 s22, 12
	s_cselect_b64 s[4:5], -1, 0
	s_cmp_eq_u32 s22, 11
	s_cselect_b64 s[6:7], -1, 0
	s_cmp_eq_u32 s22, 10
	s_cselect_b64 s[8:9], -1, 0
	s_cmp_eq_u32 s22, 9
	s_cselect_b64 s[10:11], -1, 0
	s_cmp_eq_u32 s22, 8
	s_cselect_b64 s[12:13], -1, 0
	s_cmp_eq_u32 s22, 7
	s_cselect_b64 s[14:15], -1, 0
	s_cmp_eq_u32 s22, 6
	s_cselect_b64 s[16:17], -1, 0
	s_cmp_eq_u32 s22, 5
	s_cselect_b64 s[18:19], -1, 0
	s_cmp_eq_u32 s22, 4
	s_cselect_b64 s[20:21], -1, 0
	s_cmp_eq_u32 s22, 3
	s_cselect_b64 s[24:25], -1, 0
	s_cmp_eq_u32 s22, 2
	s_cselect_b64 s[26:27], -1, 0
	s_cmp_eq_u32 s22, 1
	s_cselect_b64 s[28:29], -1, 0
	s_cmp_eq_u32 s22, 0
	s_cselect_b64 s[30:31], -1, 0
	s_nop 0
	v_cndmask_b32_e64 v16, 0, v1, s[30:31]
	v_cndmask_b32_e64 v16, v16, v0, s[28:29]
	v_cndmask_b32_e64 v16, v16, v2, s[26:27]
	v_cndmask_b32_e64 v16, v16, v3, s[24:25]
	v_cndmask_b32_e64 v16, v16, v4, s[20:21]
	v_cndmask_b32_e64 v16, v16, v5, s[18:19]
	v_cndmask_b32_e64 v16, v16, v6, s[16:17]
	v_cndmask_b32_e64 v16, v16, v7, s[14:15]
	v_cndmask_b32_e64 v16, v16, v8, s[12:13]
	v_cndmask_b32_e64 v16, v16, v9, s[10:11]
	v_cndmask_b32_e64 v16, v16, v10, s[8:9]
	v_cndmask_b32_e64 v16, v16, v11, s[6:7]
	v_cndmask_b32_e64 v16, v16, v12, s[4:5]
	v_cndmask_b32_e64 v16, v16, v13, s[2:3]
	v_cndmask_b32_e64 v16, v16, v14, s[0:1]
	v_cndmask_b32_e32 v16, v16, v15, vcc
	v_cmp_ne_u32_e32 vcc, 0, v1
	v_readlane_b32 s0, v253, 14
	s_nop 0
	s_nop 0
	v_cndmask_b32_e64 v1, 0, 1, vcc
	v_cmp_ne_u32_e32 vcc, 0, v0
	s_nop 1
	v_addc_co_u32_e32 v0, vcc, 0, v1, vcc
	v_cmp_ne_u32_e32 vcc, 0, v2
	v_max_u32_e32 v2, 1, v16
	s_nop 0
	v_cndmask_b32_e64 v1, 0, 1, vcc
	v_cmp_ne_u32_e32 vcc, 0, v3
	s_nop 1
	v_addc_co_u32_e32 v0, vcc, v0, v1, vcc
	v_cmp_ne_u32_e32 vcc, 0, v4
	s_nop 1
	s_nop 0
	v_cndmask_b32_e64 v1, 0, 1, vcc
	v_cmp_ne_u32_e32 vcc, 0, v5
	s_nop 1
	v_addc_co_u32_e32 v0, vcc, v0, v1, vcc
	v_cmp_ne_u32_e32 vcc, 0, v6
	s_nop 1
	s_nop 0
	v_cndmask_b32_e64 v1, 0, 1, vcc
	v_cmp_ne_u32_e32 vcc, 0, v7
	s_nop 1
	v_addc_co_u32_e32 v0, vcc, v0, v1, vcc
	v_cmp_ne_u32_e32 vcc, 0, v8
	s_nop 1
	s_nop 0
	v_cndmask_b32_e64 v1, 0, 1, vcc
	v_cmp_ne_u32_e32 vcc, 0, v9
	s_nop 1
	v_addc_co_u32_e32 v0, vcc, v0, v1, vcc
	v_cmp_ne_u32_e32 vcc, 0, v10
	s_nop 1
	s_nop 0
	v_cndmask_b32_e64 v1, 0, 1, vcc
	v_cmp_ne_u32_e32 vcc, 0, v11
	s_nop 1
	v_addc_co_u32_e32 v0, vcc, v0, v1, vcc
	v_cmp_ne_u32_e32 vcc, 0, v12
	s_nop 1
	s_nop 0
	v_cndmask_b32_e64 v1, 0, 1, vcc
	v_cmp_ne_u32_e32 vcc, 0, v13
	s_nop 1
	v_addc_co_u32_e32 v0, vcc, v0, v1, vcc
	v_cmp_ne_u32_e32 vcc, 0, v14
	s_nop 1
	s_nop 0
	v_cndmask_b32_e64 v1, 0, 1, vcc
	v_cmp_ne_u32_e32 vcc, 0, v15
	s_nop 1
	v_addc_co_u32_e32 v0, vcc, v0, v1, vcc
	v_max_u32_e32 v0, 1, v0
	v_mov_b32_e64 v1, s0
	ds_write_b32 v1, v2
	ds_write_b32 v1, v0 offset:4
.LBB0_839:
	s_lshl_b32 s20, s22, 6
	s_nop 0
	s_add_i32 s96, s20, 0x500
	s_lshl_b64 s[0:1], s[96:97], 2
	s_add_u32 s0, s52, s0
	s_addc_u32 s1, s53, s1
	v_mov_b64_e32 v[4:5], s[0:1]
	v_mov_b32_e64 v1, 1
	flat_atomic_add v3, v[4:5], v1 sc0
	v_cvt_f32_u32_e32 v1, v2
	v_sub_u32_e32 v4, 0, v2
	v_rcp_iflag_f32_e32 v1, v1
	s_nop 0
	v_mul_f32_e32 v1, 0x4f7ffffe, v1
	v_cvt_u32_f32_e32 v1, v1
	s_nop 0
	v_mul_lo_u32 v4, v4, v1
	v_mul_hi_u32 v4, v1, v4
	v_add_u32_e32 v1, v1, v4
	s_waitcnt vmcnt(0) lgkmcnt(0)
	v_mul_hi_u32 v1, v3, v1
	v_mul_lo_u32 v4, v1, v2
	v_sub_u32_e32 v4, v3, v4
	v_cmp_ge_u32_e32 vcc, v4, v2
	v_add_u32_e32 v5, 1, v1
	s_nop 0
	v_cndmask_b32_e32 v1, v1, v5, vcc
	v_sub_u32_e32 v5, v4, v2
	v_cndmask_b32_e32 v4, v4, v5, vcc
	v_cmp_ge_u32_e32 vcc, v4, v2
	v_add_u32_e32 v4, 1, v1
	s_nop 0
	v_cndmask_b32_e32 v1, v1, v4, vcc
	v_add_u32_e32 v4, 1, v3
	v_mad_u64_u32 v[2:3], s[0:1], v2, v1, v[2:3]
	v_cmp_ne_u32_e32 vcc, v4, v2
	s_and_saveexec_b64 s[0:1], vcc
	s_xor_b64 s[0:1], exec, s[0:1]
	s_cbranch_execz .LBB0_852
	s_add_i32 s96, s20, 0x900
	s_lshl_b64 s[2:3], s[96:97], 2
	s_add_u32 s4, s52, s2
	s_addc_u32 s5, s53, s3
	v_mov_b64_e32 v[2:3], s[4:5]
	flat_load_dword v0, v[2:3] sc1
	s_waitcnt vmcnt(0) lgkmcnt(0)
	v_cmp_eq_u32_e32 vcc, v0, v1
	s_and_saveexec_b64 s[2:3], vcc
	s_cbranch_execz .LBB0_851
	s_mov_b32 s21, 1
	s_mov_b64 s[6:7], 0
	s_branch .LBB0_843

.LBB0_843:
	s_nop 0
	s_and_b32 s14, s21, 0xff
	s_mov_b64 s[12:13], -1
	s_cmp_lg_u32 s14, 0
	s_mov_b64 s[14:15], -1
	s_sleep 1
	s_cbranch_scc1 .LBB0_847
	v_mov_b64_e32 v[2:3], s[52:53]
	flat_load_dword v0, v[2:3] offset:512 sc1
	s_mov_b64 s[14:15], 0
	s_mov_b64 s[16:17], -1
	s_waitcnt vmcnt(0) lgkmcnt(0)
	v_cmp_eq_u32_e32 vcc, 0, v0
	s_and_saveexec_b64 s[18:19], vcc
	s_nop 0
	s_cmp_lt_u32 s21, 0x400001
	s_cselect_b64 s[14:15], -1, 0
	s_xor_b64 s[16:17], exec, -1
	s_and_b64 s[14:15], s[14:15], exec
	s_or_b64 exec, exec, s[18:19]

.LBB0_849:
	s_or_b64 exec, exec, s[6:7]
	s_xor_b64 s[4:5], s[8:9], -1
	s_and_saveexec_b64 s[6:7], s[4:5]
	s_xor_b64 s[6:7], exec, s[6:7]
	s_cbranch_execz .LBB0_851
	v_mov_b64_e32 v[0:1], s[52:53]
	v_mov_b32_e64 v2, 1
	flat_atomic_add v[0:1], v2 offset:512

.LBB0_852:
	s_andn2_saveexec_b64 s[0:1], s[0:1]
	s_cbranch_execz .LBB0_881
	v_mov_b32_e32 v1, s52
	v_add_co_u32_e32 v2, vcc, 0x3000, v1
	v_mov_b32_e64 v1, s53
	buffer_wbl2 sc1
	s_waitcnt vmcnt(0)
	v_addc_co_u32_e32 v3, vcc, 0, v1, vcc
	v_mov_b32_e64 v1, 1
	flat_atomic_add v1, v[2:3], v1 offset:1024 sc0
	v_cvt_f32_u32_e32 v2, v0
	v_sub_u32_e32 v3, 0, v0
	s_mov_b64 s[4:5], -1
	v_rcp_iflag_f32_e32 v2, v2
	s_nop 0
	s_nop 0
	v_mul_f32_e32 v2, 0x4f7ffffe, v2
	v_cvt_u32_f32_e32 v2, v2
	s_nop 0
	v_mul_lo_u32 v3, v3, v2
	v_mul_hi_u32 v3, v2, v3
	v_add_u32_e32 v2, v2, v3
	s_waitcnt vmcnt(0) lgkmcnt(0)
	v_mul_hi_u32 v2, v1, v2
	v_mul_lo_u32 v3, v2, v0
	v_sub_u32_e32 v3, v1, v3
	v_cmp_ge_u32_e32 vcc, v3, v0
	v_add_u32_e32 v4, 1, v2
	s_nop 0
	v_cndmask_b32_e32 v2, v2, v4, vcc
	v_sub_u32_e32 v4, v3, v0
	v_cndmask_b32_e32 v3, v3, v4, vcc
	v_cmp_ge_u32_e32 vcc, v3, v0
	v_add_u32_e32 v3, 1, v2
	s_nop 0
	v_cndmask_b32_e32 v2, v2, v3, vcc
	v_add_u32_e32 v3, 1, v1
	v_mad_u64_u32 v[0:1], s[0:1], v0, v2, v[0:1]
	s_add_u32 s0, s52, 0x3500
	s_addc_u32 s1, s53, 0
	v_cmp_ne_u32_e32 vcc, v3, v0
	v_mov_b64_e32 v[0:1], s[0:1]
	s_and_saveexec_b64 s[2:3], vcc
	s_cbranch_execz .LBB0_878
	v_mov_b64_e32 v[0:1], s[0:1]
	flat_load_dword v0, v[0:1] sc1
	s_mov_b64 s[8:9], 0
	s_waitcnt vmcnt(0) lgkmcnt(0)
	v_cmp_eq_u32_e32 vcc, v0, v2
	s_and_saveexec_b64 s[6:7], vcc
	s_cbranch_execz .LBB0_877
	s_nop 0
	s_add_u32 s4, s52, 0x200
	s_addc_u32 s5, s53, 0
	s_mov_b32 s21, 1
	s_branch .LBB0_857

.LBB0_859:
	v_mov_b64_e32 v[0:1], s[4:5]
	s_nop 0
	flat_load_dword v0, v[0:1] sc1
	s_mov_b64 s[16:17], 0
	s_mov_b64 s[14:15], -1
	s_waitcnt vmcnt(0) lgkmcnt(0)
	v_cmp_eq_u32_e32 vcc, 0, v0
	s_and_saveexec_b64 s[18:19], vcc
	s_nop 0
	s_cmp_lt_u32 s21, 0x400001
	s_cselect_b64 s[16:17], -1, 0
	s_xor_b64 s[14:15], exec, -1
	s_and_b64 s[16:17], s[16:17], exec
	s_or_b64 exec, exec, s[18:19]
	s_and_saveexec_b64 s[18:19], s[16:17]
	s_cbranch_execz .LBB0_856
.LBB0_862:
	v_mov_b64_e32 v[0:1], s[0:1]
	s_nop 0
	flat_load_dword v0, v[0:1] sc1
	s_add_i32 s21, s21, 1
	s_or_b64 s[14:15], s[14:15], exec
	s_waitcnt vmcnt(0) lgkmcnt(0)
	v_cmp_ne_u32_e32 vcc, v0, v2
	s_orn2_b64 s[12:13], vcc, exec
	s_branch .LBB0_856
.LBB0_863:
	s_or_b64 exec, exec, s[10:11]
	s_xor_b64 s[2:3], s[12:13], -1
	s_and_saveexec_b64 s[4:5], s[2:3]
	s_xor_b64 s[2:3], exec, s[4:5]
	s_cbranch_execz .LBB0_865
	v_mov_b64_e32 v[16:17], s[40:41]
	v_mov_b32_e64 v18, 1
	flat_atomic_add v[16:17], v18 offset:512

.LBB0_880:
	s_or_b64 exec, exec, s[0:1]
	s_nop 0
	s_add_i32 s96, s20, 0x900
	s_lshl_b64 s[0:1], s[96:97], 2
	s_add_u32 s0, s52, s0
	s_addc_u32 s1, s53, s1
	v_mov_b64_e32 v[0:1], s[0:1]
	v_mov_b32_e32 v2, 1
	s_waitcnt vmcnt(0) lgkmcnt(0)
	buffer_inv sc1
	flat_atomic_add v[0:1], v2
	s_waitcnt vmcnt(0)

.LBB0_883:
	s_and_b64 vcc, exec, s[38:39]
	s_cbranch_vccz .LBB0_963
	v_readlane_b32 s2, v254, 44
	v_readlane_b32 s3, v254, 45
	s_mov_b64 s[0:1], -1
	s_and_b64 vcc, exec, s[2:3]
	s_cbranch_vccz .LBB0_944
	s_mov_b32 s0, s97
	s_waitcnt vmcnt(0)
	s_waitcnt vmcnt(0) lgkmcnt(0)
	s_barrier
	s_nop 0
	v_mbcnt_lo_u32_b32 v0, -1, s0
	v_mbcnt_hi_u32_b32 v0, -1, v0
	v_cmp_eq_u32_e32 vcc, s65, v0
	s_and_saveexec_b64 s[38:39], vcc
	s_cbranch_execz .LBB0_943
	s_nop 0
	v_readlane_b32 s40, v253, 12
	v_readlane_b32 s0, v253, 14
	v_readlane_b32 s41, v253, 13
	v_readlane_b32 s22, v253, 17
	v_mov_b32_e32 v0, s0
	s_waitcnt vmcnt(0) expcnt(0) lgkmcnt(0)
	ds_read_b32 v2, v0
	ds_read_b32 v0, v0 offset:4
	s_waitcnt lgkmcnt(1)
	v_cmp_ne_u32_e32 vcc, 0, v2
	s_cbranch_vccnz .LBB0_900
	s_nop 0
	v_readlane_b32 s0, v253, 6
	v_readlane_b32 s1, v253, 7
	s_load_dwordx2 s[4:5], s[0:1], 0x4
	s_add_u32 s0, s40, 0x1000
	s_addc_u32 s1, s41, 0
	s_nop 0
	s_add_u32 s2, s40, 0x1100
	s_addc_u32 s3, s41, 0
	s_waitcnt lgkmcnt(0)
	s_mul_i32 s23, s4, s61
	s_nop 0
	s_add_u32 s4, s40, 0x1200
	s_mul_i32 s23, s23, s5
	s_addc_u32 s5, s41, 0
	s_add_u32 s6, s40, 0x1300
	s_addc_u32 s7, s41, 0
	s_mov_b32 s28, 1
	s_mov_b64 s[8:9], 0
	s_branch .LBB0_890

.LBB0_890:
	v_mov_b64_e32 v[12:13], s[40:41]
	flat_load_dword v1, v[12:13] offset:1024 sc1
	flat_load_dword v0, v[12:13] offset:1280 sc1
	flat_load_dword v2, v[12:13] offset:1536 sc1
	s_or_b64 s[14:15], s[14:15], exec
	s_or_b64 s[12:13], s[12:13], exec
	s_waitcnt vmcnt(0) lgkmcnt(0)
	v_add_u32_e32 v3, v0, v1
	v_add_u32_e64 v4, v3, v2
	flat_load_dword v3, v[12:13] offset:1792 sc1
	s_waitcnt vmcnt(0) lgkmcnt(0)
	v_add_u32_e32 v5, v4, v3
	flat_load_dword v4, v[12:13] offset:2048 sc1
	s_waitcnt vmcnt(0) lgkmcnt(0)
	v_add_u32_e32 v6, v5, v4
	flat_load_dword v5, v[12:13] offset:2304 sc1
	s_waitcnt vmcnt(0) lgkmcnt(0)
	v_add_u32_e32 v7, v6, v5
	flat_load_dword v6, v[12:13] offset:2560 sc1
	s_waitcnt vmcnt(0) lgkmcnt(0)
	v_add_u32_e32 v8, v7, v6
	flat_load_dword v7, v[12:13] offset:2816 sc1
	s_waitcnt vmcnt(0) lgkmcnt(0)
	v_add_u32_e32 v9, v8, v7
	flat_load_dword v8, v[12:13] offset:3072 sc1
	s_waitcnt vmcnt(0) lgkmcnt(0)
	v_add_u32_e32 v10, v9, v8
	flat_load_dword v9, v[12:13] offset:3328 sc1
	s_waitcnt vmcnt(0) lgkmcnt(0)
	v_add_u32_e32 v11, v10, v9
	flat_load_dword v10, v[12:13] offset:3584 sc1
	s_waitcnt vmcnt(0) lgkmcnt(0)
	v_add_u32_e32 v14, v11, v10
	flat_load_dword v11, v[12:13] offset:3840 sc1
	v_mov_b64_e32 v[12:13], s[0:1]
	s_nop 0
	flat_load_dword v12, v[12:13] sc1
	s_waitcnt vmcnt(0) lgkmcnt(0)
	v_add_u32_e32 v14, v14, v11
	v_add_u32_e32 v16, v14, v12
	v_mov_b64_e32 v[14:15], s[2:3]
	flat_load_dword v13, v[14:15] sc1
	v_mov_b64_e32 v[14:15], s[4:5]
	s_nop 0
	flat_load_dword v14, v[14:15] sc1
	s_waitcnt vmcnt(0) lgkmcnt(0)
	v_add_u32_e32 v16, v16, v13
	v_add_u32_e32 v18, v16, v14
	v_mov_b64_e32 v[16:17], s[6:7]
	flat_load_dword v15, v[16:17] sc1
	s_waitcnt vmcnt(0) lgkmcnt(0)
	v_add_u32_e32 v16, v18, v15
	v_cmp_ne_u32_e32 vcc, s23, v16
	s_and_saveexec_b64 s[16:17], vcc
	s_cbranch_execz .LBB0_889
	s_nop 0
	s_and_b32 s20, s28, 0xff
	s_mov_b64 s[18:19], -1
	s_cmp_eq_u32 s20, 0
	s_mov_b64 s[24:25], -1
	s_mov_b64 s[20:21], -1
	s_sleep 1
	s_cbranch_scc1 .LBB0_893
	s_and_saveexec_b64 s[26:27], s[24:25]
	s_cbranch_execz .LBB0_888
	s_branch .LBB0_896

.LBB0_900:
	s_lshl_b32 s20, s22, 6
	s_nop 0
	s_add_i32 s96, s20, 0x500
	s_lshl_b64 s[0:1], s[96:97], 2
	s_add_u32 s0, s40, s0
	s_addc_u32 s1, s41, s1
	v_mov_b64_e32 v[4:5], s[0:1]
	v_mov_b32_e64 v1, 1
	flat_atomic_add v3, v[4:5], v1 sc0
	v_cvt_f32_u32_e32 v1, v2
	v_sub_u32_e32 v4, 0, v2
	v_rcp_iflag_f32_e32 v1, v1
	s_nop 0
	v_mul_f32_e32 v1, 0x4f7ffffe, v1
	v_cvt_u32_f32_e32 v1, v1
	s_nop 0
	v_mul_lo_u32 v4, v4, v1
	v_mul_hi_u32 v4, v1, v4
	v_add_u32_e32 v1, v1, v4
	s_waitcnt vmcnt(0) lgkmcnt(0)
	v_mul_hi_u32 v1, v3, v1
	v_mul_lo_u32 v4, v1, v2
	v_sub_u32_e32 v4, v3, v4
	v_cmp_ge_u32_e32 vcc, v4, v2
	v_add_u32_e32 v5, 1, v1
	s_nop 0
	v_cndmask_b32_e32 v1, v1, v5, vcc
	v_sub_u32_e32 v5, v4, v2
	v_cndmask_b32_e32 v4, v4, v5, vcc
	v_cmp_ge_u32_e32 vcc, v4, v2
	v_add_u32_e32 v4, 1, v1
	s_nop 0
	v_cndmask_b32_e32 v1, v1, v4, vcc
	v_add_u32_e32 v4, 1, v3
	v_mad_u64_u32 v[2:3], s[0:1], v2, v1, v[2:3]
	v_cmp_ne_u32_e32 vcc, v4, v2
	s_and_saveexec_b64 s[0:1], vcc
	s_xor_b64 s[0:1], exec, s[0:1]
	s_cbranch_execz .LBB0_913
	s_add_i32 s96, s20, 0x900
	s_lshl_b64 s[2:3], s[96:97], 2
	s_add_u32 s4, s40, s2
	s_addc_u32 s5, s41, s3
	v_mov_b64_e32 v[2:3], s[4:5]
	flat_load_dword v0, v[2:3] sc1
	s_waitcnt vmcnt(0) lgkmcnt(0)
	v_cmp_eq_u32_e32 vcc, v0, v1
	s_and_saveexec_b64 s[2:3], vcc
	s_cbranch_execz .LBB0_912
	s_mov_b32 s21, 1
	s_mov_b64 s[6:7], 0
	s_branch .LBB0_904

.LBB0_904:
	s_nop 0
	s_and_b32 s14, s21, 0xff
	s_mov_b64 s[12:13], -1
	s_cmp_lg_u32 s14, 0
	s_mov_b64 s[14:15], -1
	s_sleep 1
	s_cbranch_scc1 .LBB0_908
	v_mov_b64_e32 v[2:3], s[40:41]
	flat_load_dword v0, v[2:3] offset:512 sc1
	s_mov_b64 s[14:15], 0
	s_mov_b64 s[16:17], -1
	s_waitcnt vmcnt(0) lgkmcnt(0)
	v_cmp_eq_u32_e32 vcc, 0, v0
	s_and_saveexec_b64 s[18:19], vcc
	s_nop 0
	s_cmp_lt_u32 s21, 0x400001
	s_cselect_b64 s[14:15], -1, 0
	s_xor_b64 s[16:17], exec, -1
	s_and_b64 s[14:15], s[14:15], exec
	s_or_b64 exec, exec, s[18:19]

.LBB0_910:
	s_or_b64 exec, exec, s[6:7]
	s_xor_b64 s[4:5], s[8:9], -1
	s_and_saveexec_b64 s[6:7], s[4:5]
	s_xor_b64 s[6:7], exec, s[6:7]
	s_cbranch_execz .LBB0_912
	v_mov_b64_e32 v[0:1], s[40:41]
	v_mov_b32_e64 v2, 1
	flat_atomic_add v[0:1], v2 offset:512

.LBB0_913:
	s_andn2_saveexec_b64 s[0:1], s[0:1]
	s_cbranch_execz .LBB0_943
	v_mov_b32_e32 v1, s40
	v_add_co_u32_e32 v2, vcc, 0x3000, v1
	v_mov_b32_e64 v1, s41
	buffer_wbl2 sc1
	s_waitcnt vmcnt(0)
	v_addc_co_u32_e32 v3, vcc, 0, v1, vcc
	v_mov_b32_e64 v1, 1
	flat_atomic_add v1, v[2:3], v1 offset:1024 sc0
	v_cvt_f32_u32_e32 v2, v0
	v_sub_u32_e32 v3, 0, v0
	s_mov_b64 s[4:5], -1
	v_rcp_iflag_f32_e32 v2, v2
	s_nop 0
	s_nop 0
	v_mul_f32_e32 v2, 0x4f7ffffe, v2
	v_cvt_u32_f32_e32 v2, v2
	s_nop 0
	v_mul_lo_u32 v3, v3, v2
	v_mul_hi_u32 v3, v2, v3
	v_add_u32_e32 v2, v2, v3
	s_waitcnt vmcnt(0) lgkmcnt(0)
	v_mul_hi_u32 v2, v1, v2
	v_mul_lo_u32 v3, v2, v0
	v_sub_u32_e32 v3, v1, v3
	v_cmp_ge_u32_e32 vcc, v3, v0
	v_add_u32_e32 v4, 1, v2
	s_nop 0
	v_cndmask_b32_e32 v2, v2, v4, vcc
	v_sub_u32_e32 v4, v3, v0
	v_cndmask_b32_e32 v3, v3, v4, vcc
	v_cmp_ge_u32_e32 vcc, v3, v0
	v_add_u32_e32 v3, 1, v2
	s_nop 0
	v_cndmask_b32_e32 v2, v2, v3, vcc
	v_add_u32_e32 v3, 1, v1
	v_mad_u64_u32 v[0:1], s[0:1], v0, v2, v[0:1]
	s_add_u32 s0, s40, 0x3500
	s_addc_u32 s1, s41, 0
	v_cmp_ne_u32_e32 vcc, v3, v0
	v_mov_b64_e32 v[0:1], s[0:1]
	s_and_saveexec_b64 s[2:3], vcc
	s_cbranch_execz .LBB0_940
	v_mov_b64_e32 v[0:1], s[0:1]
	flat_load_dword v0, v[0:1] sc1
	s_mov_b64 s[8:9], 0
	s_waitcnt vmcnt(0) lgkmcnt(0)
	v_cmp_eq_u32_e32 vcc, v0, v2
	s_and_saveexec_b64 s[6:7], vcc
	s_cbranch_execz .LBB0_939
	s_nop 0
	s_add_u32 s4, s40, 0x200
	s_addc_u32 s5, s41, 0
	s_mov_b32 s21, 1
	s_branch .LBB0_918

.LBB0_942:
	s_or_b64 exec, exec, s[0:1]
	s_nop 0
	s_add_i32 s96, s20, 0x900
	s_lshl_b64 s[0:1], s[96:97], 2
	s_add_u32 s0, s40, s0
	s_addc_u32 s1, s41, s1
	v_mov_b64_e32 v[0:1], s[0:1]
	v_mov_b32_e32 v2, 1
	s_waitcnt vmcnt(0) lgkmcnt(0)
	buffer_inv sc1
	flat_atomic_add v[0:1], v2
	s_waitcnt vmcnt(0)

.LBB0_944:
	s_and_b64 vcc, exec, s[0:1]
	s_cbranch_vccz .LBB0_962
	s_mov_b32 s0, s97
	s_waitcnt vmcnt(0)
	s_waitcnt vmcnt(0) lgkmcnt(0)
	s_barrier
	s_nop 0
	v_mbcnt_lo_u32_b32 v0, -1, s0
	v_mbcnt_hi_u32_b32 v0, -1, v0
	v_cmp_eq_u32_e32 vcc, s65, v0
	s_and_saveexec_b64 s[0:1], vcc
	s_cbranch_execz .LBB0_961
	s_nop 0
	v_readlane_b32 s10, v253, 12
	v_readlane_b32 s11, v253, 13
	v_readlane_b32 s2, v253, 17
	s_lshl_b32 s4, s2, 6
	s_nop 0
	s_add_i32 s96, s4, 0xdc0
	s_lshl_b64 s[2:3], s[96:97], 2
	s_add_u32 s2, s10, s2
	s_addc_u32 s3, s11, s3
	v_mov_b64_e32 v[0:1], s[2:3]
	v_mov_b32_e64 v2, 1
	flat_atomic_add v2, v[0:1], v2 sc0
	s_add_i32 s96, s4, 0x1200
	s_lshl_b64 s[2:3], s[96:97], 2
	s_add_u32 s4, s10, s2
	s_addc_u32 s5, s11, s3
	s_mov_b64 s[6:7], -1
	s_waitcnt vmcnt(0) lgkmcnt(0)
	v_and_b32_e32 v0, 31, v2
	v_cmp_ne_u32_e32 vcc, 31, v0
	v_mov_b64_e32 v[0:1], s[4:5]
	s_and_saveexec_b64 s[2:3], vcc
	s_cbranch_execz .LBB0_958
	v_mov_b64_e32 v[0:1], s[4:5]
	s_nop 0
	flat_load_dword v1, v[0:1] sc1
	v_lshrrev_b32_e32 v0, 5, v2
	s_mov_b64 s[12:13], 0
	s_waitcnt vmcnt(0) lgkmcnt(0)
	v_cmp_eq_u32_e32 vcc, v1, v0
	s_and_saveexec_b64 s[8:9], vcc
	s_cbranch_execz .LBB0_957
	s_add_u32 s6, s10, 0x200
	s_addc_u32 s7, s11, 0
	s_mov_b32 s22, 1
	s_mov_b64 s[10:11], 0
	s_branch .LBB0_950

.LBB0_950:
	s_nop 0
	s_and_b32 s16, s22, 0xff
	s_mov_b64 s[14:15], -1
	s_cmp_lg_u32 s16, 0
	s_mov_b64 s[18:19], -1
	s_sleep 1
	s_cbranch_scc0 .LBB0_952
	s_and_saveexec_b64 s[20:21], s[18:19]
	s_cbranch_execz .LBB0_949
	s_branch .LBB0_955
.LBB0_952:
	v_mov_b64_e32 v[2:3], s[6:7]
	s_nop 0
	flat_load_dword v1, v[2:3] sc1
	s_mov_b64 s[18:19], 0
	s_mov_b64 s[16:17], -1
	s_waitcnt vmcnt(0) lgkmcnt(0)
	v_cmp_eq_u32_e32 vcc, 0, v1
	s_and_saveexec_b64 s[20:21], vcc
	s_nop 0
	s_cmp_lt_u32 s22, 0x400001
	s_cselect_b64 s[18:19], -1, 0
	s_xor_b64 s[16:17], exec, -1
	s_and_b64 s[18:19], s[18:19], exec
	s_or_b64 exec, exec, s[20:21]
	s_and_saveexec_b64 s[20:21], s[18:19]
	s_cbranch_execz .LBB0_949
.LBB0_955:
	v_mov_b64_e32 v[2:3], s[4:5]
	s_nop 0
	flat_load_dword v1, v[2:3] sc1
	s_add_i32 s22, s22, 1
	s_or_b64 s[16:17], s[16:17], exec
	s_waitcnt vmcnt(0) lgkmcnt(0)
	v_cmp_ne_u32_e32 vcc, v1, v0
	s_orn2_b64 s[14:15], vcc, exec
	s_branch .LBB0_949

.LBB0_958:
	s_or_b64 exec, exec, s[2:3]
	s_and_saveexec_b64 s[2:3], s[6:7]
	s_cbranch_execz .LBB0_960
	v_mov_b32_e64 v2, 1
	flat_atomic_add v[0:1], v2

.LBB0_965:
	s_nop 0
	v_readlane_b32 s0, v254, 5
	v_readlane_b32 s1, v254, 6
	s_cmp_le_i32 s0, s45
	s_cselect_b64 s[0:1], -1, 0
	s_and_b64 s[50:51], s[0:1], s[46:47]
	s_andn2_b64 vcc, exec, s[50:51]
	s_cbranch_vccnz .LBB0_1001
	s_mov_b32 s0, s97
	s_waitcnt vmcnt(0)
	s_nop 0
	v_mbcnt_lo_u32_b32 v0, -1, s0
	v_mbcnt_hi_u32_b32 v0, -1, v0
	v_readlane_b32 s0, v254, 62
	v_add_u32_e64 v8, s64, v0
	v_readlane_b32 s1, v254, 63
	s_andn2_b64 vcc, exec, s[0:1]
	v_readfirstlane_b32 s6, v8
	s_cbranch_vccnz .LBB0_1001
	s_nop 0
	v_bfe_i32 v2, v8, 27, 1
	v_lshlrev_b32_e32 v0, 4, v8
	v_lshrrev_b32_e32 v2, 22, v2
	v_add_u32_e64 v2, v0, v2
	v_and_b32_e32 v2, 0xfffffc00, v2
	v_sub_u32_e32 v0, v0, v2
	v_ashrrev_i32_e32 v1, 31, v8
	v_lshrrev_b32_e32 v2, 4, v0
	s_nop 0
	v_readlane_b32 s0, v255, 48
	v_lshrrev_b32_e32 v1, 26, v1
	s_nop 0
	v_bitop3_b32 v0, v2, v0, 32 bitop3:0x6c
	s_add_i32 s4, s0, -2
	s_nop 0
	v_readlane_b32 s0, v253, 9
	v_add_u32_e64 v1, v8, v1
	v_ashrrev_i32_e32 v3, 31, v0
	s_ashr_i32 s5, s4, 31
	v_readlane_b32 s1, v253, 10
	v_ashrrev_i32_e32 v1, 6, v1
	v_lshrrev_b32_e32 v3, 26, v3
	s_and_b64 s[0:1], s[0:1], exec
	v_lshlrev_b32_e32 v2, 3, v1
	v_add_u32_e64 v3, v0, v3
	v_readlane_b32 s0, v254, 17
	v_and_b32_e32 v2, -16, v2
	v_ashrrev_i32_e32 v4, 6, v3
	s_cselect_b32 s0, s4, s0
	s_nop 0
	s_mov_b32 s4, 0x2a00000
	v_add_u32_e64 v199, v4, v2
	v_and_b32_e32 v2, 0xc0, v3
	v_readlane_b32 s1, v254, 18
	s_cselect_b32 s4, s4, 0x1e00000
	v_sub_u32_e32 v0, v0, v2
	v_mov_b32_e32 v2, 1
	s_cselect_b32 s1, s5, s1
	s_add_u32 s4, s70, s4
	v_lshlrev_b32_e32 v1, 5, v1
	s_nop 0
	v_ashrrev_i16_sdwa v0, v2, sext(v0) dst_sel:DWORD dst_unused:UNUSED_PAD src0_sel:DWORD src1_sel:BYTE_0
	s_addc_u32 s5, s71, 0
	s_lshl_b64 s[0:1], s[0:1], 20
	v_and_b32_e32 v1, 32, v1
	s_nop 0
	v_bfe_i32 v0, v0, 0, 16
	s_add_u32 s18, s4, s0
	s_nop 0
	v_add_lshl_u32 v218, v1, v0, 1
	v_and_b32_e32 v0, 3, v4
	s_nop 0
	s_mov_b32 s0, 0x3fffe0
	v_lshrrev_b32_e32 v1, 2, v199
	v_lshlrev_b32_e32 v2, 1, v199
	v_and_or_b32 v0, v199, s0, v0
	v_and_b32_e32 v1, 4, v1
	v_and_b32_e32 v2, 24, v2
	v_or3_b32 v0, v0, v1, v2
	v_readlane_b32 s0, v255, 1
	v_lshl_add_u32 v194, v0, 10, v218
	v_add_u32_e32 v219, 64, v199
	v_add_u32_e32 v0, s0, v199
	v_lshl_add_u32 v202, v0, 10, v218
	v_add_u32_e64 v0, s0, v219
	v_add_u32_e32 v235, 0x80, v199
	s_addc_u32 s19, s5, s1
	s_ashr_i32 s7, s6, 6
	v_lshl_add_u32 v204, v0, 10, v218
	v_add_u32_e64 v0, s0, v235
	v_add_u32_e32 v236, 0xc0, v199
	s_ashr_i32 s8, s6, 8
	s_lshl_b32 s20, s7, 10
	v_lshl_add_u32 v96, v0, 10, v218
	v_add_u32_e64 v0, s0, v236
	v_readlane_b32 s0, v255, 4
	v_readlane_b32 s1, v255, 5
	s_add_u32 s0, s18, s0
	s_addc_u32 s1, s19, s1
	s_add_i32 s21, s20, 0
	s_nop 0
	s_add_i32 s24, s21, 0x10000
	s_add_i32 s25, s21, 0x12000
	s_mov_b32 m0, s24
	s_nop 0
	s_add_u32 s4, s0, 0x20000
	v_add_u32_e32 v196, 0x10000, v194
	global_load_lds_dwordx4 v194, s[0:1]
	s_mov_b32 m0, s25
	s_addc_u32 s5, s1, 0
	s_add_i32 s26, s21, 0x14000
	global_load_lds_dwordx4 v196, s[0:1]
	s_mov_b32 m0, s26
	s_nop 0
	s_add_i32 s27, s21, 0x16000
	global_load_lds_dwordx4 v194, s[4:5]
	s_mov_b32 m0, s27
	s_nop 0
	s_add_i32 s28, s21, 0x2000
	global_load_lds_dwordx4 v196, s[4:5]
	s_mov_b32 m0, s21
	s_nop 0
	s_add_i32 s29, s21, 0x4000
	global_load_lds_dwordx4 v202, s[78:79]
	s_mov_b32 m0, s28
	s_nop 0
	s_add_i32 s30, s21, 0x6000
	global_load_lds_dwordx4 v204, s[78:79]
	s_mov_b32 m0, s29
	s_nop 0
	v_lshl_add_u32 v206, v0, 10, v218
	global_load_lds_dwordx4 v96, s[78:79]
	s_mov_b32 m0, s30
	v_mov_b32_e32 v195, v97
	global_load_lds_dwordx4 v206, s[78:79]
	v_mov_b32_e32 v197, v97
	v_mov_b32_e32 v203, v97
	v_mov_b32_e32 v205, v97
	s_cmp_eq_u32 s8, 1
	v_lshl_add_u64 v[6:7], s[0:1], 0, v[194:195]
	v_lshl_add_u64 v[4:5], s[0:1], 0, v[196:197]
	v_lshl_add_u64 v[0:1], s[78:79], 0, v[202:203]
	s_cselect_b64 s[56:57], -1, 0
	s_cmp_lg_u32 s8, 1
	v_lshl_add_u64 v[2:3], s[78:79], 0, v[204:205]
	s_cbranch_scc1 .LBB0_969
	s_barrier
.LBB0_969:
	s_add_u32 s31, s60, 0x2000
	v_readlane_b32 s2, v254, 16
	v_and_b32_e32 v9, 15, v8
	v_lshrrev_b32_e32 v10, 4, v8
	s_addc_u32 s38, s2, 0
	s_nop 0
	v_lshl_or_b32 v203, s8, 6, v9
	v_bfe_u32 v10, v10, 1, 1
	s_lshl_b32 s8, s8, 13
	s_lshl_b32 s7, s7, 5
	s_mov_b64 s[2:3], 0x80
	v_lshl_or_b32 v14, v10, 10, s8
	s_and_b32 s8, s7, 0x60
	s_add_i32 m0, s21, 0x18000
	v_lshl_add_u64 v[6:7], v[6:7], 0, s[2:3]
	s_lshr_b32 s7, s8, 3
	s_waitcnt vmcnt(2)
	s_barrier
	s_nop 0
	global_load_lds_dwordx4 v[6:7], off
	v_lshl_add_u64 v[4:5], v[4:5], 0, s[2:3]
	s_add_i32 m0, s21, 0x1a000
	s_add_i32 s39, s21, 0x8000
	s_add_i32 s40, s21, 0xa000
	global_load_lds_dwordx4 v[4:5], off
	v_lshl_add_u64 v[0:1], v[0:1], 0, s[2:3]
	s_mov_b32 m0, s39
	s_nop 0
	s_add_u32 s0, s0, 0x20080
	global_load_lds_dwordx4 v[0:1], off
	v_lshl_add_u64 v[0:1], v[2:3], 0, s[2:3]
	s_mov_b32 m0, s40
	s_addc_u32 s1, s1, 0
	global_load_lds_dwordx4 v[0:1], off
	s_add_i32 m0, s21, 0x1c000
	v_lshl_add_u64 v[0:1], s[0:1], 0, v[194:195]
	global_load_lds_dwordx4 v[0:1], off
	v_lshl_add_u64 v[0:1], s[0:1], 0, v[196:197]
	s_add_i32 m0, s21, 0x1e000
	v_lshlrev_b32_e32 v12, 1, v8
	s_nop 0
	global_load_lds_dwordx4 v[0:1], off
	v_bfe_u32 v11, v8, 4, 2
	v_and_b32_e32 v12, 32, v12
	v_lshlrev_b32_e32 v9, 6, v9
	v_lshlrev_b32_e32 v8, 2, v8
	v_or_b32_e32 v10, s7, v10
	v_or_b32_e32 v13, v9, v12
	v_and_b32_e32 v8, 32, v8
	v_lshlrev_b32_e32 v10, 10, v10
	s_nop 0
	v_bitop3_b32 v9, v9, v8, v12 bitop3:0x36
	v_bitop3_b32 v205, v10, v13, v8 bitop3:0xf6
	v_or_b32_e32 v12, 16, v13
	s_nop 0
	v_bitop3_b32 v13, v13, v8, 16 bitop3:0x36
	s_waitcnt vmcnt(6)
	s_cmpk_lt_u32 s6, 0x100
	v_or_b32_e32 v9, v9, v14
	v_or_b32_e32 v13, v13, v14
	s_cselect_b64 s[58:59], -1, 0
	s_nop 0
	s_add_u32 s41, s70, 0xee00080
	v_readlane_b32 s0, v255, 2
	v_bitop3_b32 v237, v12, v10, v8 bitop3:0xde
	v_lshl_or_b32 v238, v11, 3, s8
	s_addc_u32 s45, s71, 0
	s_mov_b32 s14, 0
	v_add_u32_e32 v239, 0, v9
	v_add_u32_e32 v240, 0, v13
	v_mbcnt_lo_u32_b32 v0, -1, 0
	v_mbcnt_hi_u32_b32 v0, -1, v0
	v_and_b32_e32 v0, 16, v0
	v_xor_b32_e32 v239, v239, v0
	v_xor_b32_e32 v240, v240, v0
	v_xor_b32_e32 v205, v205, v0
	v_xor_b32_e32 v237, v237, v0
	s_mov_b32 s23, s0
	v_readlane_b32 s22, v255, 0
	v_mov_b32_e64 v241, v206
	v_mov_b32_e32 v242, v96
	s_barrier
	v_readlane_b32 s1, v255, 3
	s_branch .LBB0_972

.LBB0_972:
	s_add_i32 s46, s14, 1
	s_mov_b64 s[0:1], -1
	s_and_b64 vcc, exec, s[42:43]
	s_cbranch_vccz .LBB0_979
	s_nop 0
	v_readlane_b32 s0, v254, 38
	s_mul_i32 s0, s46, s0
	s_mul_hi_u32 s1, s46, s61
	s_add_i32 s1, s1, s0
	s_mul_i32 s0, s46, s61
	v_readlane_b32 s2, v254, 31
	s_add_u32 s10, s0, s2
	s_nop 0
	v_readlane_b32 s0, v254, 39
	s_addc_u32 s11, s1, s0
	s_waitcnt vmcnt(0)
	v_mov_b64_e32 v[0:1], 0x3ff
	v_cmp_gt_i64_e32 vcc, s[10:11], v[0:1]
	s_mov_b64 s[0:1], 0
	s_mov_b64 s[8:9], 0
	s_mov_b32 s48, s13
	s_mov_b32 s47, s12
	s_cbranch_vccnz .LBB0_979
	s_ashr_i32 s8, s10, 31
	s_lshr_b32 s8, s8, 29
	s_add_i32 s11, s10, s8
	s_and_b32 s8, s11, -8
	s_sub_i32 s10, s10, s8
	s_cmp_gt_i32 s10, -1
	s_mov_b64 s[8:9], -1
	s_cbranch_scc0 .LBB0_976
	s_lshl_b32 s15, s10, 7
	s_mov_b64 s[8:9], 0

.LBB0_978:
	s_ashr_i32 s8, s11, 3
	s_add_i32 s8, s15, s8
	s_ashr_i32 s9, s8, 31
	s_lshr_b32 s9, s9, 27
	s_add_i32 s9, s8, s9
	s_ashr_i32 s10, s9, 5
	s_lshl_b32 s10, s10, 3
	s_nop 0
	s_sub_i32 s11, 0x100, s10
	s_min_i32 s11, s11, 8
	s_abs_i32 s15, s11
	v_cvt_f32_u32_e32 v0, s15
	s_sub_i32 s17, 0, s15
	s_andn2_b32 s9, s9, 31
	s_sub_i32 s8, s8, s9
	v_rcp_iflag_f32_e32 v0, v0
	s_abs_i32 s9, s8
	s_xor_b32 s16, s8, s11
	s_ashr_i32 s16, s16, 31
	v_mul_f32_e32 v0, 0x4f7ffffe, v0
	v_cvt_u32_f32_e32 v0, v0
	s_nop 0
	v_readfirstlane_b32 s47, v0
	s_mul_i32 s17, s17, s47
	s_mul_hi_u32 s17, s47, s17
	s_add_i32 s47, s47, s17
	s_mul_hi_u32 s17, s9, s47
	s_mul_i32 s47, s17, s15
	s_sub_i32 s9, s9, s47
	s_add_i32 s48, s17, 1
	s_sub_i32 s47, s9, s15
	s_cmp_ge_u32 s9, s15
	s_cselect_b32 s17, s48, s17
	s_cselect_b32 s9, s47, s9
	s_add_i32 s47, s17, 1
	s_cmp_ge_u32 s9, s15
	s_cselect_b32 s9, s47, s17
	s_xor_b32 s9, s9, s16
	s_sub_i32 s47, s9, s16
	s_mul_i32 s9, s47, s11
	s_sub_i32 s8, s8, s9
	s_add_i32 s48, s10, s8
	s_mov_b64 s[8:9], -1

.LBB0_983:
	s_waitcnt vmcnt(0)
	v_cndmask_b32_e64 v0, 0, 1, s[8:9]
	v_cmp_ne_u32_e64 s[42:43], 1, v0
	s_andn2_b64 vcc, exec, s[8:9]
	v_mov_b32_e32 v210, v241
	v_mov_b32_e32 v208, v242
	v_mov_b32_e32 v243, v204
	v_mov_b32_e32 v224, v202
	s_cbranch_vccnz .LBB0_985
	s_lshl_b32 s10, s48, 8
	v_add_u32_e32 v0, s10, v199
	v_lshl_add_u32 v224, v0, 10, v218
	v_add_u32_e64 v0, s10, v219
	v_lshl_add_u32 v243, v0, 10, v218
	v_add_u32_e64 v0, s10, v235
	v_lshl_add_u32 v208, v0, 10, v218
	v_add_u32_e64 v0, s10, v236
	v_lshl_add_u32 v210, v0, 10, v218

.LBB0_993:
	s_ashr_i32 s8, s22, 4
	s_nop 0
	s_mul_hi_i32 s9, s8, 0x6000
	s_mulk_i32 s8, 0x6000
	s_nop 0
	v_lshl_or_b32 v24, s23, 8, v238
	s_add_u32 s8, s31, s8
	s_addc_u32 s9, s38, s9
	v_ashrrev_i32_e32 v25, 31, v24
	s_nop 0
	v_lshl_add_u64 v[4:5], v[24:25], 2, s[8:9]
	global_load_dwordx4 v[8:11], v[4:5], off offset:16
	global_load_dwordx4 v[12:15], v[4:5], off
	global_load_dwordx4 v[0:3], v[4:5], off offset:528
	s_nop 0
	s_nop 0
	global_load_dwordx4 v[4:7], v[4:5], off offset:512
	v_lshl_add_u32 v26, s22, 8, v203
	s_mov_b64 s[8:9], -1
	s_and_b64 vcc, exec, s[80:81]
	s_cbranch_vccz .LBB0_996
	s_nop 0
	v_readlane_b32 s0, v253, 18
	v_readlane_b32 s1, v253, 19
	v_ashrrev_i32_e32 v27, 31, v26
	s_nop 0
	v_lshlrev_b64 v[18:19], 12, v[26:27]
	v_lshl_add_u64 v[16:17], v[24:25], 2, s[0:1]
	v_lshl_add_u64 v[22:23], v[16:17], 0, v[18:19]
	global_load_dwordx4 v[18:21], v[22:23], off offset:16
	global_load_dwordx4 v[28:31], v[22:23], off
	global_load_dwordx4 v[32:35], v[22:23], off offset:528
	global_load_dwordx4 v[36:39], v[22:23], off offset:512
	v_or_b32_e32 v22, 16, v26
	v_ashrrev_i32_e32 v23, 31, v22
	v_lshlrev_b64 v[40:41], 12, v[22:23]
	v_lshl_add_u64 v[52:53], v[16:17], 0, v[40:41]
	global_load_dwordx4 v[40:43], v[52:53], off offset:16
	global_load_dwordx4 v[44:47], v[52:53], off
	global_load_dwordx4 v[48:51], v[52:53], off offset:528
	s_nop 0
	s_nop 0
	global_load_dwordx4 v[52:55], v[52:53], off offset:512
	v_readlane_b32 s0, v254, 32
	v_lshlrev_b64 v[56:57], 11, v[26:27]
	v_readlane_b32 s1, v254, 33
	v_lshlrev_b64 v[22:23], 11, v[22:23]
	v_readlane_b32 s8, v253, 26
	v_lshl_add_u64 v[22:23], s[0:1], 0, v[22:23]
	v_readlane_b32 s9, v253, 27
	v_readlane_b32 s2, v253, 20
	v_readlane_b32 s3, v253, 21
	v_readlane_b32 s4, v253, 22
	v_readlane_b32 s5, v253, 23
	v_readlane_b32 s6, v253, 24
	v_readlane_b32 s7, v253, 25
	v_readlane_b32 s10, v253, 28
	v_readlane_b32 s11, v253, 29
	v_readlane_b32 s12, v253, 30
	v_readlane_b32 s13, v253, 31
	v_readlane_b32 s14, v253, 32
	v_readlane_b32 s15, v253, 33
	s_waitcnt vmcnt(0)
	s_nop 0
	v_pk_fma_f32 v[58:59], v[192:193], v[10:11], v[20:21]
	v_pk_fma_f32 v[30:31], v[188:189], v[14:15], v[30:31]
	v_pk_fma_f32 v[28:29], v[186:187], v[12:13], v[28:29]
	v_pk_fma_f32 v[20:21], v[190:191], v[8:9], v[18:19]
	v_cvt_pk_bf16_f32 v18, v28, v29
	v_cvt_pk_bf16_f32 v19, v30, v31
	v_lshl_add_u64 v[30:31], s[0:1], 0, v[56:57]
	v_lshlrev_b64 v[28:29], 1, v[24:25]
	v_cvt_pk_bf16_f32 v20, v20, v21
	v_cvt_pk_bf16_f32 v21, v58, v59
	v_lshl_add_u64 v[30:31], v[30:31], 0, v[28:29]
	global_store_dwordx4 v[30:31], v[18:21], off
	v_pk_fma_f32 v[34:35], v[180:181], v[2:3], v[34:35]
	v_pk_fma_f32 v[32:33], v[178:179], v[0:1], v[32:33]
	v_pk_fma_f32 v[20:21], v[184:185], v[6:7], v[38:39]
	v_pk_fma_f32 v[18:19], v[182:183], v[4:5], v[36:37]
	v_lshl_add_u64 v[22:23], v[22:23], 0, v[28:29]
	v_cvt_pk_bf16_f32 v18, v18, v19
	v_cvt_pk_bf16_f32 v19, v20, v21
	v_cvt_pk_bf16_f32 v20, v32, v33
	v_cvt_pk_bf16_f32 v21, v34, v35
	global_store_dwordx4 v[30:31], v[18:21], off offset:256
	v_pk_fma_f32 v[30:31], v[172:173], v[10:11], v[42:43]
	v_pk_fma_f32 v[32:33], v[170:171], v[8:9], v[40:41]
	v_pk_fma_f32 v[20:21], v[176:177], v[14:15], v[46:47]
	v_pk_fma_f32 v[18:19], v[174:175], v[12:13], v[44:45]
	v_or_b32_e32 v58, 48, v26
	s_nop 0
	v_cvt_pk_bf16_f32 v18, v18, v19
	v_cvt_pk_bf16_f32 v19, v20, v21
	v_cvt_pk_bf16_f32 v20, v32, v33
	v_cvt_pk_bf16_f32 v21, v30, v31
	global_store_dwordx4 v[22:23], v[18:21], off
	v_pk_fma_f32 v[30:31], v[164:165], v[2:3], v[50:51]
	v_pk_fma_f32 v[32:33], v[162:163], v[0:1], v[48:49]
	v_pk_fma_f32 v[20:21], v[168:169], v[6:7], v[54:55]
	v_pk_fma_f32 v[18:19], v[166:167], v[4:5], v[52:53]
	v_ashrrev_i32_e32 v59, 31, v58
	s_nop 0
	v_cvt_pk_bf16_f32 v18, v18, v19
	v_cvt_pk_bf16_f32 v19, v20, v21
	v_cvt_pk_bf16_f32 v20, v32, v33
	v_cvt_pk_bf16_f32 v21, v30, v31
	global_store_dwordx4 v[22:23], v[18:21], off offset:256
	v_or_b32_e32 v22, 32, v26
	v_ashrrev_i32_e32 v23, 31, v22
	v_lshlrev_b64 v[18:19], 12, v[22:23]
	v_lshl_add_u64 v[38:39], v[16:17], 0, v[18:19]
	global_load_dwordx4 v[18:21], v[38:39], off offset:16
	global_load_dwordx4 v[30:33], v[38:39], off
	global_load_dwordx4 v[34:37], v[38:39], off offset:528
	s_nop 0
	s_nop 0
	global_load_dwordx4 v[38:41], v[38:39], off offset:512
	v_lshlrev_b64 v[42:43], 12, v[58:59]
	v_lshl_add_u64 v[54:55], v[16:17], 0, v[42:43]
	global_load_dwordx4 v[42:45], v[54:55], off offset:16
	global_load_dwordx4 v[46:49], v[54:55], off
	global_load_dwordx4 v[50:53], v[54:55], off offset:528
	s_nop 0
	s_nop 0
	global_load_dwordx4 v[54:57], v[54:55], off offset:512
	v_lshlrev_b64 v[22:23], 11, v[22:23]
	v_lshl_add_u64 v[22:23], s[0:1], 0, v[22:23]
	v_lshl_add_u64 v[22:23], v[22:23], 0, v[28:29]
	s_waitcnt vmcnt(7)
	s_nop 0
	v_pk_fma_f32 v[60:61], v[156:157], v[10:11], v[20:21]
	v_pk_fma_f32 v[20:21], v[154:155], v[8:9], v[18:19]
	s_waitcnt vmcnt(6)
	s_nop 0
	v_pk_fma_f32 v[32:33], v[160:161], v[14:15], v[32:33]
	v_pk_fma_f32 v[30:31], v[158:159], v[12:13], v[30:31]
	s_nop 0
	s_nop 0
	v_cvt_pk_bf16_f32 v18, v30, v31
	v_cvt_pk_bf16_f32 v19, v32, v33
	v_cvt_pk_bf16_f32 v20, v20, v21
	v_cvt_pk_bf16_f32 v21, v60, v61
	global_store_dwordx4 v[22:23], v[18:21], off
	s_waitcnt vmcnt(6)
	s_nop 0
	v_pk_fma_f32 v[30:31], v[148:149], v[2:3], v[36:37]
	v_pk_fma_f32 v[32:33], v[146:147], v[0:1], v[34:35]
	s_waitcnt vmcnt(5)
	s_nop 0
	v_pk_fma_f32 v[20:21], v[152:153], v[6:7], v[40:41]
	v_pk_fma_f32 v[18:19], v[150:151], v[4:5], v[38:39]
	s_nop 0
	s_nop 0
	v_cvt_pk_bf16_f32 v18, v18, v19
	v_cvt_pk_bf16_f32 v19, v20, v21
	v_cvt_pk_bf16_f32 v20, v32, v33
	v_cvt_pk_bf16_f32 v21, v30, v31
	global_store_dwordx4 v[22:23], v[18:21], off offset:256
	v_lshlrev_b64 v[22:23], 11, v[58:59]
	v_lshl_add_u64 v[22:23], s[0:1], 0, v[22:23]
	s_waitcnt vmcnt(4)
	s_nop 0
	v_pk_fma_f32 v[20:21], v[144:145], v[14:15], v[48:49]
	v_pk_fma_f32 v[18:19], v[142:143], v[12:13], v[46:47]
	v_pk_fma_f32 v[30:31], v[140:141], v[10:11], v[44:45]
	v_pk_fma_f32 v[32:33], v[138:139], v[8:9], v[42:43]
	v_cvt_pk_bf16_f32 v18, v18, v19
	v_cvt_pk_bf16_f32 v19, v20, v21
	v_lshl_add_u64 v[22:23], v[22:23], 0, v[28:29]
	v_cvt_pk_bf16_f32 v20, v32, v33
	v_cvt_pk_bf16_f32 v21, v30, v31
	global_store_dwordx4 v[22:23], v[18:21], off
	s_waitcnt vmcnt(4)
	s_nop 0
	v_pk_fma_f32 v[30:31], v[132:133], v[2:3], v[52:53]
	v_pk_fma_f32 v[32:33], v[130:131], v[0:1], v[50:51]
	s_waitcnt vmcnt(3)
	s_nop 0
	v_pk_fma_f32 v[20:21], v[136:137], v[6:7], v[56:57]
	v_pk_fma_f32 v[18:19], v[134:135], v[4:5], v[54:55]
	v_add_u32_e32 v58, 0x90, v26
	v_cvt_pk_bf16_f32 v18, v18, v19
	v_cvt_pk_bf16_f32 v19, v20, v21
	v_cvt_pk_bf16_f32 v20, v32, v33
	v_cvt_pk_bf16_f32 v21, v30, v31
	global_store_dwordx4 v[22:23], v[18:21], off offset:256
	v_add_u32_e32 v22, 0x80, v26
	v_ashrrev_i32_e32 v23, 31, v22
	s_nop 0
	v_lshlrev_b64 v[18:19], 12, v[22:23]
	v_lshl_add_u64 v[38:39], v[16:17], 0, v[18:19]
	global_load_dwordx4 v[18:21], v[38:39], off offset:16
	global_load_dwordx4 v[30:33], v[38:39], off
	global_load_dwordx4 v[34:37], v[38:39], off offset:528
	s_nop 0
	s_nop 0
	global_load_dwordx4 v[38:41], v[38:39], off offset:512
	v_ashrrev_i32_e32 v59, 31, v58
	s_nop 0
	v_lshlrev_b64 v[42:43], 12, v[58:59]
	v_lshl_add_u64 v[54:55], v[16:17], 0, v[42:43]
	global_load_dwordx4 v[42:45], v[54:55], off offset:16
	global_load_dwordx4 v[46:49], v[54:55], off
	global_load_dwordx4 v[50:53], v[54:55], off offset:528
	s_nop 0
	s_nop 0
	global_load_dwordx4 v[54:57], v[54:55], off offset:512
	v_lshlrev_b64 v[22:23], 11, v[22:23]
	v_lshl_add_u64 v[22:23], s[0:1], 0, v[22:23]
	v_lshl_add_u64 v[22:23], v[22:23], 0, v[28:29]
	s_waitcnt vmcnt(7)
	s_nop 0
	v_pk_fma_f32 v[60:61], v[124:125], v[10:11], v[20:21]
	v_pk_fma_f32 v[20:21], v[122:123], v[8:9], v[18:19]
	s_waitcnt vmcnt(6)
	s_nop 0
	v_pk_fma_f32 v[32:33], v[128:129], v[14:15], v[32:33]
	v_pk_fma_f32 v[30:31], v[126:127], v[12:13], v[30:31]
	s_nop 0
	s_nop 0
	v_cvt_pk_bf16_f32 v18, v30, v31
	v_cvt_pk_bf16_f32 v19, v32, v33
	v_cvt_pk_bf16_f32 v20, v20, v21
	v_cvt_pk_bf16_f32 v21, v60, v61
	global_store_dwordx4 v[22:23], v[18:21], off
	s_waitcnt vmcnt(6)
	s_nop 0
	v_pk_fma_f32 v[30:31], v[116:117], v[2:3], v[36:37]
	v_pk_fma_f32 v[32:33], v[114:115], v[0:1], v[34:35]
	s_waitcnt vmcnt(5)
	s_nop 0
	v_pk_fma_f32 v[20:21], v[120:121], v[6:7], v[40:41]
	v_pk_fma_f32 v[18:19], v[118:119], v[4:5], v[38:39]
	s_nop 0
	s_nop 0
	v_cvt_pk_bf16_f32 v18, v18, v19
	v_cvt_pk_bf16_f32 v19, v20, v21
	v_cvt_pk_bf16_f32 v20, v32, v33
	v_cvt_pk_bf16_f32 v21, v30, v31
	global_store_dwordx4 v[22:23], v[18:21], off offset:256
	v_lshlrev_b64 v[22:23], 11, v[58:59]
	v_lshl_add_u64 v[22:23], s[0:1], 0, v[22:23]
	s_waitcnt vmcnt(4)
	s_nop 0
	v_pk_fma_f32 v[18:19], v[110:111], v[12:13], v[46:47]
	v_pk_fma_f32 v[20:21], v[112:113], v[14:15], v[48:49]
	v_cvt_pk_bf16_f32 v18, v18, v19
	v_lshl_add_u64 v[22:23], v[22:23], 0, v[28:29]
	v_cvt_pk_bf16_f32 v19, v20, v21
	v_pk_fma_f32 v[30:31], v[108:109], v[10:11], v[44:45]
	v_pk_fma_f32 v[32:33], v[106:107], v[8:9], v[42:43]
	s_nop 0
	s_nop 0
	v_cvt_pk_bf16_f32 v20, v32, v33
	v_cvt_pk_bf16_f32 v21, v30, v31
	global_store_dwordx4 v[22:23], v[18:21], off
	s_waitcnt vmcnt(4)
	s_nop 0
	v_pk_fma_f32 v[30:31], v[100:101], v[2:3], v[52:53]
	v_pk_fma_f32 v[32:33], v[98:99], v[0:1], v[50:51]
	s_waitcnt vmcnt(3)
	s_nop 0
	v_pk_fma_f32 v[18:19], v[102:103], v[4:5], v[54:55]
	v_add_u32_e32 v54, 0xa0, v26
	v_pk_fma_f32 v[20:21], v[104:105], v[6:7], v[56:57]
	v_cvt_pk_bf16_f32 v18, v18, v19
	v_ashrrev_i32_e32 v55, 31, v54
	s_nop 0
	v_cvt_pk_bf16_f32 v19, v20, v21
	v_cvt_pk_bf16_f32 v20, v32, v33
	v_cvt_pk_bf16_f32 v21, v30, v31
	global_store_dwordx4 v[22:23], v[18:21], off offset:256
	v_add_u32_e32 v56, 0xb0, v26
	v_ashrrev_i32_e32 v57, 31, v56
	s_nop 0
	v_lshlrev_b64 v[18:19], 12, v[54:55]
	v_lshl_add_u64 v[18:19], v[16:17], 0, v[18:19]
	global_load_dwordx4 v[30:33], v[18:19], off offset:16
	global_load_dwordx4 v[34:37], v[18:19], off
	global_load_dwordx4 v[38:41], v[18:19], off offset:528
	global_load_dwordx4 v[42:45], v[18:19], off offset:512
	v_lshlrev_b64 v[18:19], 12, v[56:57]
	v_lshl_add_u64 v[20:21], v[16:17], 0, v[18:19]
	global_load_dwordx4 v[46:49], v[20:21], off offset:16
	global_load_dwordx4 v[50:53], v[20:21], off
	global_load_dwordx4 v[16:19], v[20:21], off offset:528
	s_nop 0
	s_nop 0
	global_load_dwordx4 v[20:23], v[20:21], off offset:512
	v_lshlrev_b64 v[54:55], 11, v[54:55]
	s_waitcnt vmcnt(7)
	s_nop 0
	v_pk_fma_f32 v[58:59], v[90:91], v[10:11], v[32:33]
	s_waitcnt vmcnt(6)
	s_nop 0
	v_pk_fma_f32 v[34:35], v[92:93], v[12:13], v[34:35]
	v_pk_fma_f32 v[32:33], v[88:89], v[8:9], v[30:31]
	v_cvt_pk_bf16_f32 v30, v34, v35
	v_lshl_add_u64 v[34:35], s[0:1], 0, v[54:55]
	v_pk_fma_f32 v[36:37], v[94:95], v[14:15], v[36:37]
	v_lshl_add_u64 v[34:35], v[34:35], 0, v[28:29]
	v_cvt_pk_bf16_f32 v31, v36, v37
	v_cvt_pk_bf16_f32 v32, v32, v33
	v_cvt_pk_bf16_f32 v33, v58, v59
	global_store_dwordx4 v[34:35], v[30:33], off
	s_waitcnt vmcnt(6)
	s_nop 0
	v_pk_fma_f32 v[36:37], v[82:83], v[2:3], v[40:41]
	v_pk_fma_f32 v[38:39], v[80:81], v[0:1], v[38:39]
	s_waitcnt vmcnt(5)
	s_nop 0
	v_pk_fma_f32 v[32:33], v[86:87], v[6:7], v[44:45]
	v_pk_fma_f32 v[30:31], v[84:85], v[4:5], v[42:43]
	s_waitcnt vmcnt(1)
	s_nop 0
	v_pk_fma_f32 v[22:23], v[70:71], v[6:7], v[22:23]
	v_cvt_pk_bf16_f32 v30, v30, v31
	v_cvt_pk_bf16_f32 v31, v32, v33
	v_cvt_pk_bf16_f32 v32, v38, v39
	v_cvt_pk_bf16_f32 v33, v36, v37
	global_store_dwordx4 v[34:35], v[30:33], off offset:256
	v_lshlrev_b64 v[34:35], 11, v[56:57]
	v_lshl_add_u64 v[34:35], s[0:1], 0, v[34:35]
	v_pk_fma_f32 v[30:31], v[76:77], v[12:13], v[50:51]
	v_pk_fma_f32 v[32:33], v[78:79], v[14:15], v[52:53]
	v_cvt_pk_bf16_f32 v30, v30, v31
	v_lshl_add_u64 v[28:29], v[34:35], 0, v[28:29]
	v_cvt_pk_bf16_f32 v31, v32, v33
	v_pk_fma_f32 v[36:37], v[74:75], v[10:11], v[48:49]
	v_pk_fma_f32 v[38:39], v[72:73], v[8:9], v[46:47]
	v_pk_fma_f32 v[20:21], v[68:69], v[4:5], v[20:21]
	v_cvt_pk_bf16_f32 v32, v38, v39
	v_cvt_pk_bf16_f32 v33, v36, v37
	global_store_dwordx4 v[28:29], v[30:33], off
	s_nop 1
	s_nop 0
	v_pk_fma_f32 v[30:31], v[66:67], v[2:3], v[18:19]
	v_pk_fma_f32 v[18:19], v[64:65], v[0:1], v[16:17]
	v_cvt_pk_bf16_f32 v16, v20, v21
	v_cvt_pk_bf16_f32 v17, v22, v23
	s_nop 0
	s_nop 0
	v_cvt_pk_bf16_f32 v18, v18, v19
	v_cvt_pk_bf16_f32 v19, v30, v31
	s_cbranch_execz .LBB0_997
.LBB0_995:
	s_and_b64 vcc, exec, s[42:43]
	s_mov_b64 s[0:1], -1
	s_nop 0
	global_store_dwordx4 v[28:29], v[16:19], off offset:256
	s_cbranch_vccnz .LBB0_971
	s_branch .LBB0_998

.LBB0_997:
	v_lshlrev_b32_e32 v16, 1, v24
	s_nop 0
	v_readlane_b32 s2, v254, 20
	v_lshl_add_u32 v36, v26, 11, v16
	v_readlane_b32 s3, v254, 21
	s_nop 4
	s_nop 0
	global_load_dwordx4 v[40:43], v36, s[2:3]
	global_load_dwordx4 v[44:47], v36, s[2:3] offset:256
	v_add_u32_e32 v39, 0x8000, v36
	global_load_dwordx4 v[48:51], v39, s[2:3]
	global_load_dwordx4 v[32:35], v39, s[2:3] offset:256
	v_add_u32_e32 v38, 0x10000, v36
	global_load_dwordx4 v[28:31], v38, s[2:3]
	global_load_dwordx4 v[24:27], v38, s[2:3] offset:256
	v_add_u32_e32 v37, 0x18000, v36
	global_load_dwordx4 v[20:23], v37, s[2:3]
	global_load_dwordx4 v[16:19], v37, s[2:3] offset:256
	v_readlane_b32 s0, v254, 32
	v_readlane_b32 s1, v254, 33
	v_add_u32_e32 v58, 0x50000, v36
	s_waitcnt vmcnt(0)
	v_lshlrev_b32_e32 v52, 16, v40
	v_and_b32_e32 v53, 0xffff0000, v40
	v_lshlrev_b32_e32 v40, 16, v41
	s_nop 0
	v_and_b32_e32 v41, 0xffff0000, v41
	v_lshlrev_b32_e32 v54, 16, v42
	s_nop 0
	v_and_b32_e32 v55, 0xffff0000, v42
	v_lshlrev_b32_e32 v42, 16, v43
	s_nop 0
	v_and_b32_e32 v43, 0xffff0000, v43
	v_pk_fma_f32 v[56:57], v[188:189], v[14:15], v[40:41]
	v_pk_fma_f32 v[40:41], v[186:187], v[12:13], v[52:53]
	v_pk_fma_f32 v[52:53], v[192:193], v[10:11], v[42:43]
	v_pk_fma_f32 v[42:43], v[190:191], v[8:9], v[54:55]
	v_cvt_pk_bf16_f32 v40, v40, v41
	v_cvt_pk_bf16_f32 v41, v56, v57
	v_add_u32_e32 v56, 0x40000, v36
	v_cvt_pk_bf16_f32 v42, v42, v43
	v_cvt_pk_bf16_f32 v43, v52, v53
	global_store_dwordx4 v36, v[40:43], s[0:1]
	v_add_u32_e32 v57, 0x48000, v36
	s_nop 0
	v_lshlrev_b32_e32 v40, 16, v44
	v_and_b32_e32 v41, 0xffff0000, v44
	v_lshlrev_b32_e32 v42, 16, v45
	s_nop 0
	v_and_b32_e32 v43, 0xffff0000, v45
	v_lshlrev_b32_e32 v44, 16, v46
	s_nop 0
	v_and_b32_e32 v45, 0xffff0000, v46
	v_lshlrev_b32_e32 v46, 16, v47
	s_nop 0
	v_and_b32_e32 v47, 0xffff0000, v47
	v_pk_fma_f32 v[42:43], v[184:185], v[6:7], v[42:43]
	v_pk_fma_f32 v[40:41], v[182:183], v[4:5], v[40:41]
	v_pk_fma_f32 v[46:47], v[180:181], v[2:3], v[46:47]
	v_pk_fma_f32 v[44:45], v[178:179], v[0:1], v[44:45]
	v_cvt_pk_bf16_f32 v40, v40, v41
	v_cvt_pk_bf16_f32 v41, v42, v43
	s_nop 0
	s_nop 0
	v_cvt_pk_bf16_f32 v42, v44, v45
	v_cvt_pk_bf16_f32 v43, v46, v47
	global_store_dwordx4 v36, v[40:43], s[0:1] offset:256
	v_lshlrev_b32_e32 v44, 16, v50
	s_nop 0
	v_and_b32_e32 v45, 0xffff0000, v50
	v_lshlrev_b32_e32 v40, 16, v48
	s_nop 0
	v_and_b32_e32 v41, 0xffff0000, v48
	v_lshlrev_b32_e32 v42, 16, v49
	s_nop 0
	v_and_b32_e32 v43, 0xffff0000, v49
	v_lshlrev_b32_e32 v46, 16, v51
	s_nop 0
	v_and_b32_e32 v47, 0xffff0000, v51
	v_pk_fma_f32 v[42:43], v[176:177], v[14:15], v[42:43]
	v_pk_fma_f32 v[40:41], v[174:175], v[12:13], v[40:41]
	v_pk_fma_f32 v[46:47], v[172:173], v[10:11], v[46:47]
	v_pk_fma_f32 v[44:45], v[170:171], v[8:9], v[44:45]
	v_cvt_pk_bf16_f32 v40, v40, v41
	v_cvt_pk_bf16_f32 v41, v42, v43
	s_nop 0
	s_nop 0
	v_cvt_pk_bf16_f32 v42, v44, v45
	v_cvt_pk_bf16_f32 v43, v46, v47
	global_store_dwordx4 v39, v[40:43], s[0:1]
	s_nop 1
	v_lshlrev_b32_e32 v40, 16, v32
	v_and_b32_e32 v41, 0xffff0000, v32
	v_lshlrev_b32_e32 v32, 16, v33
	s_nop 0
	v_and_b32_e32 v33, 0xffff0000, v33
	v_lshlrev_b32_e32 v42, 16, v34
	s_nop 0
	v_and_b32_e32 v43, 0xffff0000, v34
	v_lshlrev_b32_e32 v34, 16, v35
	s_nop 0
	v_and_b32_e32 v35, 0xffff0000, v35
	v_pk_fma_f32 v[44:45], v[168:169], v[6:7], v[32:33]
	v_pk_fma_f32 v[32:33], v[166:167], v[4:5], v[40:41]
	v_pk_fma_f32 v[40:41], v[164:165], v[2:3], v[34:35]
	v_pk_fma_f32 v[34:35], v[162:163], v[0:1], v[42:43]
	v_cvt_pk_bf16_f32 v32, v32, v33
	v_cvt_pk_bf16_f32 v33, v44, v45
	s_nop 0
	s_nop 0
	v_cvt_pk_bf16_f32 v34, v34, v35
	v_cvt_pk_bf16_f32 v35, v40, v41
	global_store_dwordx4 v39, v[32:35], s[0:1] offset:256
	s_nop 1
	v_lshlrev_b32_e32 v32, 16, v28
	v_and_b32_e32 v33, 0xffff0000, v28
	v_lshlrev_b32_e32 v28, 16, v29
	s_nop 0
	v_and_b32_e32 v29, 0xffff0000, v29
	v_lshlrev_b32_e32 v34, 16, v30
	s_nop 0
	v_and_b32_e32 v35, 0xffff0000, v30
	v_lshlrev_b32_e32 v30, 16, v31
	s_nop 0
	v_and_b32_e32 v31, 0xffff0000, v31
	v_pk_fma_f32 v[40:41], v[160:161], v[14:15], v[28:29]
	v_pk_fma_f32 v[28:29], v[158:159], v[12:13], v[32:33]
	v_pk_fma_f32 v[32:33], v[156:157], v[10:11], v[30:31]
	v_pk_fma_f32 v[30:31], v[154:155], v[8:9], v[34:35]
	v_cvt_pk_bf16_f32 v28, v28, v29
	v_cvt_pk_bf16_f32 v29, v40, v41
	s_nop 0
	s_nop 0
	v_cvt_pk_bf16_f32 v30, v30, v31
	v_cvt_pk_bf16_f32 v31, v32, v33
	global_store_dwordx4 v38, v[28:31], s[0:1]
	s_nop 1
	v_lshlrev_b32_e32 v28, 16, v24
	v_and_b32_e32 v29, 0xffff0000, v24
	v_lshlrev_b32_e32 v24, 16, v25
	s_nop 0
	v_and_b32_e32 v25, 0xffff0000, v25
	v_lshlrev_b32_e32 v30, 16, v26
	s_nop 0
	v_and_b32_e32 v31, 0xffff0000, v26
	v_lshlrev_b32_e32 v26, 16, v27
	s_nop 0
	v_and_b32_e32 v27, 0xffff0000, v27
	v_pk_fma_f32 v[32:33], v[152:153], v[6:7], v[24:25]
	v_pk_fma_f32 v[24:25], v[150:151], v[4:5], v[28:29]
	v_pk_fma_f32 v[28:29], v[148:149], v[2:3], v[26:27]
	v_pk_fma_f32 v[26:27], v[146:147], v[0:1], v[30:31]
	v_cvt_pk_bf16_f32 v24, v24, v25
	v_cvt_pk_bf16_f32 v25, v32, v33
	s_nop 0
	s_nop 0
	v_cvt_pk_bf16_f32 v26, v26, v27
	v_cvt_pk_bf16_f32 v27, v28, v29
	global_store_dwordx4 v38, v[24:27], s[0:1] offset:256
	s_nop 1
	v_lshlrev_b32_e32 v24, 16, v20
	v_and_b32_e32 v25, 0xffff0000, v20
	v_lshlrev_b32_e32 v20, 16, v21
	s_nop 0
	v_and_b32_e32 v21, 0xffff0000, v21
	v_lshlrev_b32_e32 v26, 16, v22
	s_nop 0
	v_and_b32_e32 v27, 0xffff0000, v22
	v_lshlrev_b32_e32 v22, 16, v23
	s_nop 0
	v_and_b32_e32 v23, 0xffff0000, v23
	v_pk_fma_f32 v[28:29], v[144:145], v[14:15], v[20:21]
	v_pk_fma_f32 v[20:21], v[142:143], v[12:13], v[24:25]
	v_pk_fma_f32 v[24:25], v[140:141], v[10:11], v[22:23]
	v_pk_fma_f32 v[22:23], v[138:139], v[8:9], v[26:27]
	v_cvt_pk_bf16_f32 v20, v20, v21
	v_cvt_pk_bf16_f32 v21, v28, v29
	s_nop 0
	s_nop 0
	v_cvt_pk_bf16_f32 v22, v22, v23
	v_cvt_pk_bf16_f32 v23, v24, v25
	global_store_dwordx4 v37, v[20:23], s[0:1]
	s_nop 1
	v_lshlrev_b32_e32 v20, 16, v16
	v_and_b32_e32 v21, 0xffff0000, v16
	v_lshlrev_b32_e32 v16, 16, v17
	s_nop 0
	v_and_b32_e32 v17, 0xffff0000, v17
	v_lshlrev_b32_e32 v22, 16, v18
	s_nop 0
	v_and_b32_e32 v23, 0xffff0000, v18
	v_lshlrev_b32_e32 v18, 16, v19
	s_nop 0
	v_and_b32_e32 v19, 0xffff0000, v19
	v_pk_fma_f32 v[24:25], v[136:137], v[6:7], v[16:17]
	v_pk_fma_f32 v[16:17], v[134:135], v[4:5], v[20:21]
	v_pk_fma_f32 v[20:21], v[132:133], v[2:3], v[18:19]
	v_pk_fma_f32 v[18:19], v[130:131], v[0:1], v[22:23]
	v_cvt_pk_bf16_f32 v16, v16, v17
	v_cvt_pk_bf16_f32 v17, v24, v25
	v_add_u32_e32 v24, 0x58000, v36
	v_cvt_pk_bf16_f32 v18, v18, v19
	v_cvt_pk_bf16_f32 v19, v20, v21
	global_store_dwordx4 v37, v[16:19], s[0:1] offset:256
	global_load_dwordx4 v[26:29], v56, s[2:3]
	global_load_dwordx4 v[30:33], v56, s[2:3] offset:256
	global_load_dwordx4 v[38:41], v57, s[2:3]
	global_load_dwordx4 v[42:45], v57, s[2:3] offset:256
	global_load_dwordx4 v[46:49], v58, s[2:3]
	global_load_dwordx4 v[50:53], v58, s[2:3] offset:256
	global_load_dwordx4 v[20:23], v24, s[2:3]
	global_load_dwordx4 v[16:19], v24, s[2:3] offset:256
	v_mov_b32_e64 v25, v97
	s_waitcnt vmcnt(7)
	v_lshlrev_b32_e32 v34, 16, v26
	v_and_b32_e32 v35, 0xffff0000, v26
	v_lshlrev_b32_e32 v26, 16, v27
	s_nop 0
	v_and_b32_e32 v27, 0xffff0000, v27
	v_lshlrev_b32_e32 v36, 16, v28
	s_nop 0
	v_and_b32_e32 v37, 0xffff0000, v28
	v_lshlrev_b32_e32 v28, 16, v29
	s_nop 0
	v_and_b32_e32 v29, 0xffff0000, v29
	v_pk_fma_f32 v[54:55], v[128:129], v[14:15], v[26:27]
	v_pk_fma_f32 v[26:27], v[126:127], v[12:13], v[34:35]
	v_pk_fma_f32 v[34:35], v[124:125], v[10:11], v[28:29]
	v_pk_fma_f32 v[28:29], v[122:123], v[8:9], v[36:37]
	v_cvt_pk_bf16_f32 v26, v26, v27
	v_cvt_pk_bf16_f32 v27, v54, v55
	s_nop 0
	s_nop 0
	v_cvt_pk_bf16_f32 v28, v28, v29
	v_cvt_pk_bf16_f32 v29, v34, v35
	global_store_dwordx4 v56, v[26:29], s[0:1]
	s_waitcnt vmcnt(7)
	s_nop 0
	v_lshlrev_b32_e32 v26, 16, v30
	s_nop 0
	v_and_b32_e32 v27, 0xffff0000, v30
	v_lshlrev_b32_e32 v28, 16, v31
	s_nop 0
	v_and_b32_e32 v29, 0xffff0000, v31
	v_lshlrev_b32_e32 v30, 16, v32
	s_nop 0
	v_and_b32_e32 v31, 0xffff0000, v32
	v_lshlrev_b32_e32 v32, 16, v33
	s_nop 0
	v_and_b32_e32 v33, 0xffff0000, v33
	v_pk_fma_f32 v[28:29], v[120:121], v[6:7], v[28:29]
	v_pk_fma_f32 v[26:27], v[118:119], v[4:5], v[26:27]
	v_pk_fma_f32 v[32:33], v[116:117], v[2:3], v[32:33]
	v_pk_fma_f32 v[30:31], v[114:115], v[0:1], v[30:31]
	v_cvt_pk_bf16_f32 v26, v26, v27
	v_cvt_pk_bf16_f32 v27, v28, v29
	s_nop 0
	s_nop 0
	v_cvt_pk_bf16_f32 v28, v30, v31
	v_cvt_pk_bf16_f32 v29, v32, v33
	global_store_dwordx4 v56, v[26:29], s[0:1] offset:256
	s_waitcnt vmcnt(7)
	v_lshlrev_b32_e32 v30, 16, v40
	v_and_b32_e32 v31, 0xffff0000, v40
	v_lshlrev_b32_e32 v26, 16, v38
	s_nop 0
	v_and_b32_e32 v27, 0xffff0000, v38
	v_lshlrev_b32_e32 v28, 16, v39
	s_nop 0
	v_and_b32_e32 v29, 0xffff0000, v39
	v_lshlrev_b32_e32 v32, 16, v41
	s_nop 0
	v_and_b32_e32 v33, 0xffff0000, v41
	v_pk_fma_f32 v[28:29], v[112:113], v[14:15], v[28:29]
	v_pk_fma_f32 v[26:27], v[110:111], v[12:13], v[26:27]
	v_pk_fma_f32 v[32:33], v[108:109], v[10:11], v[32:33]
	v_pk_fma_f32 v[30:31], v[106:107], v[8:9], v[30:31]
	v_cvt_pk_bf16_f32 v26, v26, v27
	v_cvt_pk_bf16_f32 v27, v28, v29
	s_nop 0
	s_nop 0
	v_cvt_pk_bf16_f32 v28, v30, v31
	v_cvt_pk_bf16_f32 v29, v32, v33
	global_store_dwordx4 v57, v[26:29], s[0:1]
	s_waitcnt vmcnt(7)
	v_lshlrev_b32_e32 v30, 16, v44
	v_and_b32_e32 v31, 0xffff0000, v44
	v_lshlrev_b32_e32 v26, 16, v42
	s_nop 0
	v_and_b32_e32 v27, 0xffff0000, v42
	v_lshlrev_b32_e32 v28, 16, v43
	s_nop 0
	v_and_b32_e32 v29, 0xffff0000, v43
	v_lshlrev_b32_e32 v32, 16, v45
	s_nop 0
	v_and_b32_e32 v33, 0xffff0000, v45
	v_pk_fma_f32 v[28:29], v[104:105], v[6:7], v[28:29]
	v_pk_fma_f32 v[26:27], v[102:103], v[4:5], v[26:27]
	v_pk_fma_f32 v[32:33], v[100:101], v[2:3], v[32:33]
	v_pk_fma_f32 v[30:31], v[98:99], v[0:1], v[30:31]
	v_cvt_pk_bf16_f32 v26, v26, v27
	v_cvt_pk_bf16_f32 v27, v28, v29
	s_nop 0
	s_nop 0
	v_cvt_pk_bf16_f32 v28, v30, v31
	v_cvt_pk_bf16_f32 v29, v32, v33
	global_store_dwordx4 v57, v[26:29], s[0:1] offset:256
	s_waitcnt vmcnt(7)
	v_lshlrev_b32_e32 v30, 16, v48
	v_and_b32_e32 v31, 0xffff0000, v48
	v_lshlrev_b32_e32 v26, 16, v46
	s_nop 0
	v_and_b32_e32 v27, 0xffff0000, v46
	v_lshlrev_b32_e32 v28, 16, v47
	s_nop 0
	v_and_b32_e32 v29, 0xffff0000, v47
	v_lshlrev_b32_e32 v32, 16, v49
	s_nop 0
	v_and_b32_e32 v33, 0xffff0000, v49
	v_pk_fma_f32 v[28:29], v[94:95], v[14:15], v[28:29]
	v_pk_fma_f32 v[26:27], v[92:93], v[12:13], v[26:27]
	v_pk_fma_f32 v[32:33], v[90:91], v[10:11], v[32:33]
	v_pk_fma_f32 v[30:31], v[88:89], v[8:9], v[30:31]
	v_cvt_pk_bf16_f32 v26, v26, v27
	v_cvt_pk_bf16_f32 v27, v28, v29
	s_nop 0
	s_nop 0
	v_cvt_pk_bf16_f32 v28, v30, v31
	v_cvt_pk_bf16_f32 v29, v32, v33
	global_store_dwordx4 v58, v[26:29], s[0:1]
	s_waitcnt vmcnt(7)
	v_lshlrev_b32_e32 v30, 16, v52
	v_and_b32_e32 v31, 0xffff0000, v52
	v_lshlrev_b32_e32 v26, 16, v50
	s_nop 0
	v_and_b32_e32 v27, 0xffff0000, v50
	v_lshlrev_b32_e32 v28, 16, v51
	s_nop 0
	v_and_b32_e32 v29, 0xffff0000, v51
	v_lshlrev_b32_e32 v32, 16, v53
	s_nop 0
	v_and_b32_e32 v33, 0xffff0000, v53
	v_pk_fma_f32 v[28:29], v[86:87], v[6:7], v[28:29]
	v_pk_fma_f32 v[26:27], v[84:85], v[4:5], v[26:27]
	v_pk_fma_f32 v[32:33], v[82:83], v[2:3], v[32:33]
	v_pk_fma_f32 v[30:31], v[80:81], v[0:1], v[30:31]
	v_cvt_pk_bf16_f32 v26, v26, v27
	v_cvt_pk_bf16_f32 v27, v28, v29
	s_nop 0
	s_nop 0
	v_cvt_pk_bf16_f32 v28, v30, v31
	v_cvt_pk_bf16_f32 v29, v32, v33
	global_store_dwordx4 v58, v[26:29], s[0:1] offset:256
	s_waitcnt vmcnt(7)
	s_nop 0
	v_lshlrev_b32_e32 v26, 16, v20
	s_nop 0
	v_and_b32_e32 v27, 0xffff0000, v20
	v_lshlrev_b32_e32 v20, 16, v21
	s_nop 0
	v_and_b32_e32 v21, 0xffff0000, v21
	v_lshlrev_b32_e32 v28, 16, v22
	s_nop 0
	v_and_b32_e32 v29, 0xffff0000, v22
	v_lshlrev_b32_e32 v22, 16, v23
	s_nop 0
	v_and_b32_e32 v23, 0xffff0000, v23
	v_pk_fma_f32 v[14:15], v[78:79], v[14:15], v[20:21]
	v_pk_fma_f32 v[20:21], v[74:75], v[10:11], v[22:23]
	v_pk_fma_f32 v[10:11], v[72:73], v[8:9], v[28:29]
	v_pk_fma_f32 v[12:13], v[76:77], v[12:13], v[26:27]
	v_lshl_add_u64 v[28:29], s[0:1], 0, v[24:25]
	v_cvt_pk_bf16_f32 v8, v12, v13
	v_cvt_pk_bf16_f32 v9, v14, v15
	v_cvt_pk_bf16_f32 v10, v10, v11
	v_cvt_pk_bf16_f32 v11, v20, v21
	global_store_dwordx4 v24, v[8:11], s[0:1]
	s_waitcnt vmcnt(7)
	v_lshlrev_b32_e32 v12, 16, v18
	v_and_b32_e32 v13, 0xffff0000, v18
	v_lshlrev_b32_e32 v8, 16, v16
	s_nop 0
	v_and_b32_e32 v9, 0xffff0000, v16
	v_lshlrev_b32_e32 v10, 16, v17
	s_nop 0
	v_and_b32_e32 v11, 0xffff0000, v17
	v_lshlrev_b32_e32 v14, 16, v19
	s_nop 0
	v_and_b32_e32 v15, 0xffff0000, v19
	v_pk_fma_f32 v[6:7], v[70:71], v[6:7], v[10:11]
	v_pk_fma_f32 v[4:5], v[68:69], v[4:5], v[8:9]
	v_pk_fma_f32 v[2:3], v[66:67], v[2:3], v[14:15]
	v_pk_fma_f32 v[0:1], v[64:65], v[0:1], v[12:13]
	v_cvt_pk_bf16_f32 v16, v4, v5
	v_cvt_pk_bf16_f32 v17, v6, v7
	s_nop 0
	s_nop 0
	v_cvt_pk_bf16_f32 v18, v0, v1
	v_cvt_pk_bf16_f32 v19, v2, v3
	s_and_b64 vcc, exec, s[42:43]
	s_mov_b64 s[0:1], -1
	global_store_dwordx4 v[28:29], v[16:19], off offset:256
	s_cbranch_vccnz .LBB0_971

.LBB0_1001:
	s_nop 0
	v_readlane_b32 s36, v254, 5
	s_add_i32 s22, s89, 2
	s_nop 0
	v_readlane_b32 s37, v254, 6
	s_cmp_lt_i32 s22, s37
	s_cselect_b64 s[38:39], -1, 0
	s_and_b64 s[40:41], s[50:51], s[38:39]
	s_and_b64 vcc, exec, s[42:43]
	s_cbranch_vccz .LBB0_1015
	s_nop 0
	v_readlane_b32 s72, v254, 17
	s_mov_b64 s[46:47], 0
	s_and_b64 vcc, exec, s[40:41]
	s_mov_b64 s[0:1], 0
	s_nop 0
	v_readlane_b32 s50, v254, 31
	v_readlane_b32 s51, v254, 8
	v_readlane_b32 s73, v254, 18
	s_cbranch_vccz .LBB0_1016
	s_mov_b32 s0, s97
	s_waitcnt vmcnt(0)
	s_waitcnt vmcnt(0) lgkmcnt(0)
	s_barrier
	s_nop 0
	v_mbcnt_lo_u32_b32 v0, -1, s0
	v_mbcnt_hi_u32_b32 v0, -1, v0
	v_cmp_eq_u32_e32 vcc, s65, v0
	s_and_saveexec_b64 s[48:49], vcc
	s_cbranch_execz .LBB0_1051
	s_nop 0
	v_readlane_b32 s52, v253, 12
	v_readlane_b32 s0, v253, 14
	v_readlane_b32 s53, v253, 13
	v_readlane_b32 s23, v253, 17
	v_mov_b32_e32 v0, s0
	s_waitcnt vmcnt(0) expcnt(0) lgkmcnt(0)
	ds_read_b32 v2, v0
	ds_read_b32 v0, v0 offset:4
	s_waitcnt lgkmcnt(1)
	v_cmp_ne_u32_e32 vcc, 0, v2
	s_cbranch_vccnz .LBB0_1022
	s_nop 0
	v_readlane_b32 s0, v253, 6
	v_readlane_b32 s1, v253, 7
	s_load_dwordx2 s[4:5], s[0:1], 0x4
	s_add_u32 s0, s52, 0x1000
	s_addc_u32 s1, s53, 0
	s_nop 0
	s_add_u32 s2, s52, 0x1100
	s_addc_u32 s3, s53, 0
	s_waitcnt lgkmcnt(0)
	s_mul_i32 s28, s4, s61
	s_nop 0
	s_add_u32 s4, s52, 0x1200
	s_mul_i32 s28, s28, s5
	s_addc_u32 s5, s53, 0
	s_add_u32 s6, s52, 0x1300
	s_addc_u32 s7, s53, 0
	s_mov_b32 s29, 1
	s_mov_b64 s[8:9], 0
	s_branch .LBB0_1008

.LBB0_1008:
	v_mov_b64_e32 v[12:13], s[52:53]
	flat_load_dword v1, v[12:13] offset:1024 sc1
	flat_load_dword v0, v[12:13] offset:1280 sc1
	flat_load_dword v2, v[12:13] offset:1536 sc1
	s_or_b64 s[14:15], s[14:15], exec
	s_or_b64 s[12:13], s[12:13], exec
	s_waitcnt vmcnt(0) lgkmcnt(0)
	v_add_u32_e32 v3, v0, v1
	v_add_u32_e64 v4, v3, v2
	flat_load_dword v3, v[12:13] offset:1792 sc1
	s_waitcnt vmcnt(0) lgkmcnt(0)
	v_add_u32_e32 v5, v4, v3
	flat_load_dword v4, v[12:13] offset:2048 sc1
	s_waitcnt vmcnt(0) lgkmcnt(0)
	v_add_u32_e32 v6, v5, v4
	flat_load_dword v5, v[12:13] offset:2304 sc1
	s_waitcnt vmcnt(0) lgkmcnt(0)
	v_add_u32_e32 v7, v6, v5
	flat_load_dword v6, v[12:13] offset:2560 sc1
	s_waitcnt vmcnt(0) lgkmcnt(0)
	v_add_u32_e32 v8, v7, v6
	flat_load_dword v7, v[12:13] offset:2816 sc1
	s_waitcnt vmcnt(0) lgkmcnt(0)
	v_add_u32_e32 v9, v8, v7
	flat_load_dword v8, v[12:13] offset:3072 sc1
	s_waitcnt vmcnt(0) lgkmcnt(0)
	v_add_u32_e32 v10, v9, v8
	flat_load_dword v9, v[12:13] offset:3328 sc1
	s_waitcnt vmcnt(0) lgkmcnt(0)
	v_add_u32_e32 v11, v10, v9
	flat_load_dword v10, v[12:13] offset:3584 sc1
	s_waitcnt vmcnt(0) lgkmcnt(0)
	v_add_u32_e32 v14, v11, v10
	flat_load_dword v11, v[12:13] offset:3840 sc1
	v_mov_b64_e32 v[12:13], s[0:1]
	s_nop 0
	flat_load_dword v12, v[12:13] sc1
	s_waitcnt vmcnt(0) lgkmcnt(0)
	v_add_u32_e32 v14, v14, v11
	v_add_u32_e32 v16, v14, v12
	v_mov_b64_e32 v[14:15], s[2:3]
	flat_load_dword v13, v[14:15] sc1
	v_mov_b64_e32 v[14:15], s[4:5]
	s_nop 0
	flat_load_dword v14, v[14:15] sc1
	s_waitcnt vmcnt(0) lgkmcnt(0)
	v_add_u32_e32 v16, v16, v13
	v_add_u32_e32 v18, v16, v14
	v_mov_b64_e32 v[16:17], s[6:7]
	flat_load_dword v15, v[16:17] sc1
	s_waitcnt vmcnt(0) lgkmcnt(0)
	v_add_u32_e32 v16, v18, v15
	v_cmp_ne_u32_e32 vcc, s28, v16
	s_and_saveexec_b64 s[16:17], vcc
	s_cbranch_execz .LBB0_1007
	s_nop 0
	s_and_b32 s20, s29, 0xff
	s_mov_b64 s[18:19], -1
	s_cmp_eq_u32 s20, 0
	s_mov_b64 s[24:25], -1
	s_mov_b64 s[20:21], -1
	s_sleep 1
	s_cbranch_scc1 .LBB0_1011
	s_and_saveexec_b64 s[26:27], s[24:25]
	s_cbranch_execz .LBB0_1006
	s_branch .LBB0_1014

.LBB0_1015:
	s_nop 0
	v_readlane_b32 s72, v254, 17
	s_mov_b64 s[46:47], -1
	s_mov_b64 s[0:1], 0
	v_readlane_b32 s50, v254, 31
	v_readlane_b32 s51, v254, 8
	v_readlane_b32 s73, v254, 18

.LBB0_1021:
	s_or_b64 exec, exec, s[0:1]
	s_cmp_eq_u32 s23, 15
	s_cselect_b64 vcc, -1, 0
	s_cmp_eq_u32 s23, 14
	s_cselect_b64 s[0:1], -1, 0
	s_cmp_eq_u32 s23, 13
	s_cselect_b64 s[2:3], -1, 0
	s_cmp_eq_u32 s23, 12
	s_cselect_b64 s[4:5], -1, 0
	s_cmp_eq_u32 s23, 11
	s_cselect_b64 s[6:7], -1, 0
	s_cmp_eq_u32 s23, 10
	s_cselect_b64 s[8:9], -1, 0
	s_cmp_eq_u32 s23, 9
	s_cselect_b64 s[10:11], -1, 0
	s_cmp_eq_u32 s23, 8
	s_cselect_b64 s[12:13], -1, 0
	s_cmp_eq_u32 s23, 7
	s_cselect_b64 s[14:15], -1, 0
	s_cmp_eq_u32 s23, 6
	s_cselect_b64 s[16:17], -1, 0
	s_cmp_eq_u32 s23, 5
	s_cselect_b64 s[18:19], -1, 0
	s_cmp_eq_u32 s23, 4
	s_cselect_b64 s[20:21], -1, 0
	s_cmp_eq_u32 s23, 3
	s_cselect_b64 s[24:25], -1, 0
	s_cmp_eq_u32 s23, 2
	s_cselect_b64 s[26:27], -1, 0
	s_cmp_eq_u32 s23, 1
	s_cselect_b64 s[28:29], -1, 0
	s_cmp_eq_u32 s23, 0
	s_cselect_b64 s[30:31], -1, 0
	s_nop 0
	v_cndmask_b32_e64 v16, 0, v1, s[30:31]
	v_cndmask_b32_e64 v16, v16, v0, s[28:29]
	v_cndmask_b32_e64 v16, v16, v2, s[26:27]
	v_cndmask_b32_e64 v16, v16, v3, s[24:25]
	v_cndmask_b32_e64 v16, v16, v4, s[20:21]
	v_cndmask_b32_e64 v16, v16, v5, s[18:19]
	v_cndmask_b32_e64 v16, v16, v6, s[16:17]
	v_cndmask_b32_e64 v16, v16, v7, s[14:15]
	v_cndmask_b32_e64 v16, v16, v8, s[12:13]
	v_cndmask_b32_e64 v16, v16, v9, s[10:11]
	v_cndmask_b32_e64 v16, v16, v10, s[8:9]
	v_cndmask_b32_e64 v16, v16, v11, s[6:7]
	v_cndmask_b32_e64 v16, v16, v12, s[4:5]
	v_cndmask_b32_e64 v16, v16, v13, s[2:3]
	v_cndmask_b32_e64 v16, v16, v14, s[0:1]
	v_cndmask_b32_e32 v16, v16, v15, vcc
	v_cmp_ne_u32_e32 vcc, 0, v1
	v_readlane_b32 s0, v253, 14
	s_nop 0
	s_nop 0
	v_cndmask_b32_e64 v1, 0, 1, vcc
	v_cmp_ne_u32_e32 vcc, 0, v0
	s_nop 1
	v_addc_co_u32_e32 v0, vcc, 0, v1, vcc
	v_cmp_ne_u32_e32 vcc, 0, v2
	v_max_u32_e32 v2, 1, v16
	s_nop 0
	v_cndmask_b32_e64 v1, 0, 1, vcc
	v_cmp_ne_u32_e32 vcc, 0, v3
	s_nop 1
	v_addc_co_u32_e32 v0, vcc, v0, v1, vcc
	v_cmp_ne_u32_e32 vcc, 0, v4
	s_nop 1
	s_nop 0
	v_cndmask_b32_e64 v1, 0, 1, vcc
	v_cmp_ne_u32_e32 vcc, 0, v5
	s_nop 1
	v_addc_co_u32_e32 v0, vcc, v0, v1, vcc
	v_cmp_ne_u32_e32 vcc, 0, v6
	s_nop 1
	s_nop 0
	v_cndmask_b32_e64 v1, 0, 1, vcc
	v_cmp_ne_u32_e32 vcc, 0, v7
	s_nop 1
	v_addc_co_u32_e32 v0, vcc, v0, v1, vcc
	v_cmp_ne_u32_e32 vcc, 0, v8
	s_nop 1
	s_nop 0
	v_cndmask_b32_e64 v1, 0, 1, vcc
	v_cmp_ne_u32_e32 vcc, 0, v9
	s_nop 1
	v_addc_co_u32_e32 v0, vcc, v0, v1, vcc
	v_cmp_ne_u32_e32 vcc, 0, v10
	s_nop 1
	s_nop 0
	v_cndmask_b32_e64 v1, 0, 1, vcc
	v_cmp_ne_u32_e32 vcc, 0, v11
	s_nop 1
	v_addc_co_u32_e32 v0, vcc, v0, v1, vcc
	v_cmp_ne_u32_e32 vcc, 0, v12
	s_nop 1
	s_nop 0
	v_cndmask_b32_e64 v1, 0, 1, vcc
	v_cmp_ne_u32_e32 vcc, 0, v13
	s_nop 1
	v_addc_co_u32_e32 v0, vcc, v0, v1, vcc
	v_cmp_ne_u32_e32 vcc, 0, v14
	s_nop 1
	s_nop 0
	v_cndmask_b32_e64 v1, 0, 1, vcc
	v_cmp_ne_u32_e32 vcc, 0, v15
	s_nop 1
	v_addc_co_u32_e32 v0, vcc, v0, v1, vcc
	v_max_u32_e32 v0, 1, v0
	v_mov_b32_e64 v1, s0
	ds_write_b32 v1, v2
	ds_write_b32 v1, v0 offset:4
.LBB0_1022:
	s_lshl_b32 s20, s23, 6
	s_nop 0
	s_add_i32 s96, s20, 0x500
	s_lshl_b64 s[0:1], s[96:97], 2
	s_add_u32 s0, s52, s0
	s_addc_u32 s1, s53, s1
	v_mov_b64_e32 v[4:5], s[0:1]
	v_mov_b32_e64 v1, 1
	flat_atomic_add v3, v[4:5], v1 sc0
	v_cvt_f32_u32_e32 v1, v2
	v_sub_u32_e32 v4, 0, v2
	v_rcp_iflag_f32_e32 v1, v1
	s_nop 0
	v_mul_f32_e32 v1, 0x4f7ffffe, v1
	v_cvt_u32_f32_e32 v1, v1
	s_nop 0
	v_mul_lo_u32 v4, v4, v1
	v_mul_hi_u32 v4, v1, v4
	v_add_u32_e32 v1, v1, v4
	s_waitcnt vmcnt(0) lgkmcnt(0)
	v_mul_hi_u32 v1, v3, v1
	v_mul_lo_u32 v4, v1, v2
	v_sub_u32_e32 v4, v3, v4
	v_cmp_ge_u32_e32 vcc, v4, v2
	v_add_u32_e32 v5, 1, v1
	s_nop 0
	v_cndmask_b32_e32 v1, v1, v5, vcc
	v_sub_u32_e32 v5, v4, v2
	v_cndmask_b32_e32 v4, v4, v5, vcc
	v_cmp_ge_u32_e32 vcc, v4, v2
	v_add_u32_e32 v4, 1, v1
	s_nop 0
	v_cndmask_b32_e32 v1, v1, v4, vcc
	v_add_u32_e32 v4, 1, v3
	v_mad_u64_u32 v[2:3], s[0:1], v2, v1, v[2:3]
	v_cmp_ne_u32_e32 vcc, v4, v2
	s_and_saveexec_b64 s[0:1], vcc
	s_xor_b64 s[0:1], exec, s[0:1]
	s_cbranch_execz .LBB0_1035
	s_add_i32 s96, s20, 0x900
	s_lshl_b64 s[2:3], s[96:97], 2
	s_add_u32 s4, s52, s2
	s_addc_u32 s5, s53, s3
	v_mov_b64_e32 v[2:3], s[4:5]
	flat_load_dword v0, v[2:3] sc1
	s_waitcnt vmcnt(0) lgkmcnt(0)
	v_cmp_eq_u32_e32 vcc, v0, v1
	s_and_saveexec_b64 s[2:3], vcc
	s_cbranch_execz .LBB0_1034
	s_mov_b32 s21, 1
	s_mov_b64 s[6:7], 0
	s_branch .LBB0_1026

.LBB0_1054:
	s_add_u32 s54, s70, 0x6e00000
	s_addc_u32 s55, s71, 0
	s_nop 0
	s_add_u32 s90, s70, 0xc00000
	s_addc_u32 s91, s71, 0
	s_lshl_b32 s0, s72, 5
	s_ashr_i32 s1, s0, 31
	s_lshl_b64 s[0:1], s[0:1], 2
	s_add_u32 s0, s70, s0
	s_addc_u32 s1, s71, s1
	s_add_u32 s80, s0, 0x10000
	s_addc_u32 s81, s1, 0
	s_cmp_gt_i32 s36, s22
	s_cselect_b64 s[0:1], -1, 0
	s_xor_b64 s[2:3], s[38:39], -1
	s_or_b64 s[0:1], s[0:1], s[2:3]
	s_add_i32 s22, s89, 3
	s_and_b64 vcc, exec, s[0:1]
	s_cbranch_vccnz .LBB0_1192
	s_lshl_b32 s0, s72, 10
	s_nop 0
	v_readlane_b32 s4, v253, 34
	s_ashr_i32 s1, s0, 31
	s_nop 0
	v_readlane_b32 s12, v253, 42
	v_readlane_b32 s13, v253, 43
	v_readlane_b32 s16, v253, 46
	v_readlane_b32 s17, v253, 47
	s_lshl_b64 s[0:1], s[0:1], 2
	s_mov_b64 s[12:13], s[16:17]
	s_add_u32 s20, s12, s0
	s_addc_u32 s21, s13, s1
	s_add_u32 s30, s60, 0x3000
	v_readlane_b32 s0, v254, 16
	s_addc_u32 s31, s0, 0
	s_nop 0
	s_add_u32 s52, s60, 0x4000
	s_addc_u32 s53, s0, 0
	s_mov_b32 s0, s97
	s_mov_b32 s23, s93
	s_waitcnt vmcnt(0)
	v_mbcnt_lo_u32_b32 v0, -1, s0
	v_mbcnt_hi_u32_b32 v0, -1, v0
	v_add_u32_e32 v158, s64, v0
	s_cmpk_lt_i32 s23, 0x100
	v_readfirstlane_b32 s2, v158
	v_mov_b32_e32 v205, 0
	s_cselect_b64 s[0:1], -1, 0
	s_cmpk_gt_i32 s23, 0xff
	v_ashrrev_i32_e32 v159, 31, v158
	v_mov_b32_e32 v206, 0
	v_mov_b32_e32 v203, 0
	v_mov_b32_e32 v204, 0
	v_mov_b32_e32 v199, 0
	v_mov_b32_e32 v202, 0
	v_readlane_b32 s5, v253, 35
	v_readlane_b32 s6, v253, 36
	v_readlane_b32 s7, v253, 37
	v_readlane_b32 s8, v253, 38
	v_readlane_b32 s9, v253, 39
	v_readlane_b32 s10, v253, 40
	v_readlane_b32 s11, v253, 41
	v_readlane_b32 s14, v253, 44
	v_readlane_b32 s15, v253, 45
	v_readlane_b32 s18, v253, 48
	v_readlane_b32 s19, v253, 49
	s_cbranch_scc1 .LBB0_1057
	s_ashr_i32 s3, s23, 4
	v_lshl_add_u64 v[0:1], v[158:159], 2, s[20:21]
	global_load_dword v202, v[0:1], off
	global_load_dword v199, v[0:1], off offset:2048
	v_mad_i64_i32 v[0:1], s[6:7], s3, v234, v[158:159]
	v_lshlrev_b64 v[0:1], 2, v[0:1]
	v_lshl_add_u64 v[2:3], s[52:53], 0, v[0:1]
	v_lshl_add_u64 v[0:1], s[30:31], 0, v[0:1]
	global_load_dword v204, v[2:3], off
	global_load_dword v203, v[2:3], off offset:2048
	global_load_dword v206, v[0:1], off
	global_load_dword v205, v[0:1], off offset:2048
.LBB0_1057:
	v_and_b32_e32 v207, 15, v158
	s_nop 0
	v_readlane_b32 s4, v253, 50
	v_ashrrev_i32_e32 v196, 4, v158
	s_nop 0
	v_add_u32_e32 v4, 0x200, v158
	v_add_u32_e32 v6, 0x400, v158
	v_add_u32_e32 v8, 0x600, v158
	v_add_u32_e32 v10, 0x800, v158
	v_add_u32_e32 v12, 0xa00, v158
	v_add_u32_e32 v14, 0xc00, v158
	v_add_u32_e32 v16, 0xe00, v158
	v_lshlrev_b32_e32 v96, 2, v207
	s_nop 0
	v_readlane_b32 s6, v253, 52
	v_readlane_b32 s7, v253, 53
	v_ashrrev_i32_e32 v197, 31, v196
	v_ashrrev_i32_e32 v194, 4, v4
	v_ashrrev_i32_e32 v192, 4, v6
	v_ashrrev_i32_e32 v190, 4, v8
	v_ashrrev_i32_e32 v188, 4, v10
	v_ashrrev_i32_e32 v184, 4, v12
	v_ashrrev_i32_e32 v180, 4, v14
	v_ashrrev_i32_e32 v176, 4, v16
	v_lshl_add_u64 v[0:1], s[6:7], 0, v[96:97]
	v_lshlrev_b64 v[2:3], 6, v[196:197]
	v_ashrrev_i32_e32 v195, 31, v194
	v_ashrrev_i32_e32 v193, 31, v192
	v_ashrrev_i32_e32 v191, 31, v190
	v_ashrrev_i32_e32 v189, 31, v188
	v_ashrrev_i32_e32 v185, 31, v184
	v_ashrrev_i32_e32 v181, 31, v180
	v_ashrrev_i32_e32 v177, 31, v176
	s_nop 0
	v_lshl_add_u64 v[2:3], v[0:1], 0, v[2:3]
	v_lshlrev_b64 v[4:5], 6, v[194:195]
	v_lshlrev_b64 v[6:7], 6, v[192:193]
	v_lshlrev_b64 v[8:9], 6, v[190:191]
	v_lshlrev_b64 v[10:11], 6, v[188:189]
	v_lshlrev_b64 v[12:13], 6, v[184:185]
	v_lshlrev_b64 v[14:15], 6, v[180:181]
	v_lshlrev_b64 v[16:17], 6, v[176:177]
	v_lshl_add_u64 v[4:5], v[0:1], 0, v[4:5]
	v_lshl_add_u64 v[6:7], v[0:1], 0, v[6:7]
	v_lshl_add_u64 v[8:9], v[0:1], 0, v[8:9]
	v_lshl_add_u64 v[10:11], v[0:1], 0, v[10:11]
	v_lshl_add_u64 v[12:13], v[0:1], 0, v[12:13]
	v_lshl_add_u64 v[14:15], v[0:1], 0, v[14:15]
	v_lshl_add_u64 v[16:17], v[0:1], 0, v[16:17]
	global_load_dword v197, v[2:3], off
	global_load_dword v195, v[4:5], off
	global_load_dword v193, v[6:7], off
	global_load_dword v191, v[8:9], off
	global_load_dword v189, v[10:11], off
	global_load_dword v185, v[12:13], off
	global_load_dword v181, v[14:15], off
	global_load_dword v177, v[16:17], off
	v_add_u32_e32 v2, 0x1000, v158
	v_ashrrev_i32_e32 v186, 4, v2
	s_nop 0
	v_add_u32_e32 v4, 0x1200, v158
	v_add_u32_e32 v6, 0x1400, v158
	v_add_u32_e32 v8, 0x1600, v158
	v_add_u32_e32 v10, 0x1800, v158
	v_add_u32_e32 v12, 0x1a00, v158
	v_add_u32_e32 v14, 0x1c00, v158
	v_add_u32_e32 v16, 0x1e00, v158
	v_ashrrev_i32_e32 v187, 31, v186
	v_ashrrev_i32_e32 v182, 4, v4
	v_ashrrev_i32_e32 v178, 4, v6
	v_ashrrev_i32_e32 v174, 4, v8
	v_ashrrev_i32_e32 v172, 4, v10
	v_ashrrev_i32_e32 v168, 4, v12
	v_ashrrev_i32_e32 v164, 4, v14
	v_ashrrev_i32_e32 v160, 4, v16
	v_lshlrev_b64 v[2:3], 6, v[186:187]
	v_ashrrev_i32_e32 v183, 31, v182
	v_ashrrev_i32_e32 v179, 31, v178
	v_ashrrev_i32_e32 v175, 31, v174
	v_ashrrev_i32_e32 v173, 31, v172
	v_ashrrev_i32_e32 v169, 31, v168
	v_ashrrev_i32_e32 v165, 31, v164
	v_ashrrev_i32_e32 v161, 31, v160
	s_nop 0
	v_lshl_add_u64 v[2:3], v[0:1], 0, v[2:3]
	v_lshlrev_b64 v[4:5], 6, v[182:183]
	v_lshlrev_b64 v[6:7], 6, v[178:179]
	v_lshlrev_b64 v[8:9], 6, v[174:175]
	v_lshlrev_b64 v[10:11], 6, v[172:173]
	v_lshlrev_b64 v[12:13], 6, v[168:169]
	v_lshlrev_b64 v[14:15], 6, v[164:165]
	v_lshlrev_b64 v[16:17], 6, v[160:161]
	v_lshl_add_u64 v[4:5], v[0:1], 0, v[4:5]
	v_lshl_add_u64 v[6:7], v[0:1], 0, v[6:7]
	v_lshl_add_u64 v[8:9], v[0:1], 0, v[8:9]
	v_lshl_add_u64 v[10:11], v[0:1], 0, v[10:11]
	v_lshl_add_u64 v[12:13], v[0:1], 0, v[12:13]
	v_lshl_add_u64 v[14:15], v[0:1], 0, v[14:15]
	v_lshl_add_u64 v[16:17], v[0:1], 0, v[16:17]
	global_load_dword v187, v[2:3], off
	global_load_dword v183, v[4:5], off
	global_load_dword v179, v[6:7], off
	global_load_dword v175, v[8:9], off
	global_load_dword v173, v[10:11], off
	global_load_dword v169, v[12:13], off
	global_load_dword v165, v[14:15], off
	global_load_dword v161, v[16:17], off
	v_add_u32_e32 v2, 0x2000, v158
	v_ashrrev_i32_e32 v170, 4, v2
	s_nop 0
	v_add_u32_e32 v4, 0x2200, v158
	v_add_u32_e32 v6, 0x2400, v158
	v_add_u32_e32 v8, 0x2600, v158
	v_add_u32_e32 v10, 0x2800, v158
	v_add_u32_e32 v12, 0x2a00, v158
	v_add_u32_e32 v14, 0x2c00, v158
	v_add_u32_e32 v16, 0x2e00, v158
	v_ashrrev_i32_e32 v171, 31, v170
	v_ashrrev_i32_e32 v166, 4, v4
	v_ashrrev_i32_e32 v162, 4, v6
	v_ashrrev_i32_e32 v156, 4, v8
	v_ashrrev_i32_e32 v154, 4, v10
	v_ashrrev_i32_e32 v150, 4, v12
	v_ashrrev_i32_e32 v146, 4, v14
	v_ashrrev_i32_e32 v142, 4, v16
	v_lshlrev_b64 v[2:3], 6, v[170:171]
	v_ashrrev_i32_e32 v167, 31, v166
	v_ashrrev_i32_e32 v163, 31, v162
	v_ashrrev_i32_e32 v157, 31, v156
	v_ashrrev_i32_e32 v155, 31, v154
	v_ashrrev_i32_e32 v151, 31, v150
	v_ashrrev_i32_e32 v147, 31, v146
	v_ashrrev_i32_e32 v143, 31, v142
	s_nop 0
	v_lshl_add_u64 v[2:3], v[0:1], 0, v[2:3]
	v_lshlrev_b64 v[4:5], 6, v[166:167]
	v_lshlrev_b64 v[6:7], 6, v[162:163]
	v_lshlrev_b64 v[8:9], 6, v[156:157]
	v_lshlrev_b64 v[10:11], 6, v[154:155]
	v_lshlrev_b64 v[12:13], 6, v[150:151]
	v_lshlrev_b64 v[14:15], 6, v[146:147]
	v_lshlrev_b64 v[16:17], 6, v[142:143]
	v_lshl_add_u64 v[4:5], v[0:1], 0, v[4:5]
	v_lshl_add_u64 v[6:7], v[0:1], 0, v[6:7]
	v_lshl_add_u64 v[8:9], v[0:1], 0, v[8:9]
	v_lshl_add_u64 v[10:11], v[0:1], 0, v[10:11]
	v_lshl_add_u64 v[12:13], v[0:1], 0, v[12:13]
	v_lshl_add_u64 v[14:15], v[0:1], 0, v[14:15]
	v_lshl_add_u64 v[16:17], v[0:1], 0, v[16:17]
	global_load_dword v171, v[2:3], off
	global_load_dword v167, v[4:5], off
	global_load_dword v163, v[6:7], off
	global_load_dword v157, v[8:9], off
	global_load_dword v155, v[10:11], off
	global_load_dword v151, v[12:13], off
	global_load_dword v147, v[14:15], off
	global_load_dword v143, v[16:17], off
	v_add_u32_e32 v2, 0x3000, v158
	v_ashrrev_i32_e32 v152, 4, v2
	s_nop 0
	v_add_u32_e32 v4, 0x3200, v158
	v_add_u32_e32 v6, 0x3400, v158
	v_add_u32_e32 v8, 0x3600, v158
	v_add_u32_e32 v10, 0x3800, v158
	v_add_u32_e32 v12, 0x3a00, v158
	v_add_u32_e32 v14, 0x3c00, v158
	v_add_u32_e32 v16, 0x3e00, v158
	v_ashrrev_i32_e32 v153, 31, v152
	v_ashrrev_i32_e32 v148, 4, v4
	v_ashrrev_i32_e32 v144, 4, v6
	v_ashrrev_i32_e32 v140, 4, v8
	v_ashrrev_i32_e32 v138, 4, v10
	v_ashrrev_i32_e32 v136, 4, v12
	v_ashrrev_i32_e32 v134, 4, v14
	v_ashrrev_i32_e32 v132, 4, v16
	v_lshlrev_b64 v[2:3], 6, v[152:153]
	v_ashrrev_i32_e32 v149, 31, v148
	v_ashrrev_i32_e32 v145, 31, v144
	v_ashrrev_i32_e32 v141, 31, v140
	v_ashrrev_i32_e32 v139, 31, v138
	v_ashrrev_i32_e32 v137, 31, v136
	v_ashrrev_i32_e32 v135, 31, v134
	v_ashrrev_i32_e32 v133, 31, v132
	s_nop 0
	v_lshl_add_u64 v[2:3], v[0:1], 0, v[2:3]
	v_lshlrev_b64 v[4:5], 6, v[148:149]
	v_lshlrev_b64 v[6:7], 6, v[144:145]
	v_lshlrev_b64 v[8:9], 6, v[140:141]
	v_lshlrev_b64 v[10:11], 6, v[138:139]
	v_lshlrev_b64 v[12:13], 6, v[136:137]
	v_lshlrev_b64 v[14:15], 6, v[134:135]
	v_lshlrev_b64 v[16:17], 6, v[132:133]
	v_lshl_add_u64 v[4:5], v[0:1], 0, v[4:5]
	v_lshl_add_u64 v[6:7], v[0:1], 0, v[6:7]
	v_lshl_add_u64 v[8:9], v[0:1], 0, v[8:9]
	v_lshl_add_u64 v[10:11], v[0:1], 0, v[10:11]
	v_lshl_add_u64 v[12:13], v[0:1], 0, v[12:13]
	v_lshl_add_u64 v[14:15], v[0:1], 0, v[14:15]
	v_lshl_add_u64 v[0:1], v[0:1], 0, v[16:17]
	global_load_dword v149, v[2:3], off
	global_load_dword v145, v[4:5], off
	global_load_dword v141, v[6:7], off
	global_load_dword v139, v[8:9], off
	global_load_dword v137, v[10:11], off
	global_load_dword v135, v[12:13], off
	global_load_dword v133, v[14:15], off
	global_load_dword v131, v[0:1], off
	v_readlane_b32 s8, v253, 54
	v_cndmask_b32_e64 v0, 0, 1, s[0:1]
	v_and_b32_e32 v130, 48, v158
	s_ashr_i32 s8, s2, 6
	v_cmp_ne_u32_e64 s[2:3], 1, v0
	s_andn2_b64 vcc, exec, s[0:1]
	v_lshlrev_b32_e32 v96, 1, v130
	v_readlane_b32 s5, v253, 51
	v_readlane_b32 s9, v253, 55
	v_readlane_b32 s10, v253, 56
	v_readlane_b32 s11, v253, 57
	v_readlane_b32 s12, v253, 58
	v_readlane_b32 s13, v253, 59
	v_readlane_b32 s14, v253, 60
	v_readlane_b32 s15, v253, 61
	v_readlane_b32 s16, v253, 62
	v_readlane_b32 s17, v253, 63
	v_readlane_b32 s18, v254, 0
	v_readlane_b32 s19, v254, 1
	s_cbranch_vccnz .LBB0_1059
	s_lshl_b32 s0, s23, 8
	s_lshl_b32 s1, s8, 5
	s_add_i32 s1, s1, s0
	v_or_b32_e32 v0, s1, v207
	v_ashrrev_i32_e32 v1, 31, v0
	v_readlane_b32 s0, v254, 32
	v_lshlrev_b64 v[0:1], 11, v[0:1]
	v_readlane_b32 s1, v254, 33
	s_nop 1
	s_nop 0
	v_lshl_add_u64 v[0:1], s[0:1], 0, v[0:1]
	v_lshl_add_u64 v[126:127], v[0:1], 0, v[96:97]
	global_load_dwordx4 v[0:3], v[126:127], off offset:16
	global_load_dwordx4 v[4:7], v[126:127], off
	global_load_dwordx4 v[8:11], v[126:127], off offset:144
	global_load_dwordx4 v[12:15], v[126:127], off offset:128
	global_load_dwordx4 v[16:19], v[126:127], off offset:272
	global_load_dwordx4 v[20:23], v[126:127], off offset:256
	global_load_dwordx4 v[24:27], v[126:127], off offset:400
	global_load_dwordx4 v[28:31], v[126:127], off offset:384
	global_load_dwordx4 v[32:35], v[126:127], off offset:528
	global_load_dwordx4 v[36:39], v[126:127], off offset:512
	global_load_dwordx4 v[40:43], v[126:127], off offset:656
	global_load_dwordx4 v[44:47], v[126:127], off offset:640
	global_load_dwordx4 v[48:51], v[126:127], off offset:784
	global_load_dwordx4 v[52:55], v[126:127], off offset:768
	global_load_dwordx4 v[56:59], v[126:127], off offset:912
	global_load_dwordx4 v[60:63], v[126:127], off offset:896
	global_load_dwordx4 v[64:67], v[126:127], off offset:1040
	global_load_dwordx4 v[68:71], v[126:127], off offset:1024
	global_load_dwordx4 v[72:75], v[126:127], off offset:1168
	global_load_dwordx4 v[76:79], v[126:127], off offset:1152
	global_load_dwordx4 v[80:83], v[126:127], off offset:1296
	global_load_dwordx4 v[84:87], v[126:127], off offset:1280
	global_load_dwordx4 v[88:91], v[126:127], off offset:1424
	global_load_dwordx4 v[92:95], v[126:127], off offset:1408
	global_load_dwordx4 v[98:101], v[126:127], off offset:1552
	global_load_dwordx4 v[102:105], v[126:127], off offset:1536
	global_load_dwordx4 v[106:109], v[126:127], off offset:1680
	global_load_dwordx4 v[110:113], v[126:127], off offset:1664
	global_load_dwordx4 v[114:117], v[126:127], off offset:1808
	global_load_dwordx4 v[118:121], v[126:127], off offset:1792
	global_load_dwordx4 v[122:125], v[126:127], off offset:1936
	s_nop 0
	s_nop 0
	global_load_dwordx4 v[126:129], v[126:127], off offset:1920
.LBB0_1059:
	s_movk_i32 s0, 0x408
	s_waitcnt vmcnt(31)
	v_bfe_u32 v153, v197, 16, 1
	v_mad_u32_u24 v196, v207, s0, v196
	v_add3_u32 v153, v197, v153, s67
	v_lshl_add_u32 v196, v196, 1, 0
	ds_write_b16_d16_hi v196, v153 offset:8192
	v_and_b32_e32 v153, 0xffff0000, v153
	v_sub_f32_e64 v153, v197, v153
	v_bfe_u32 v197, v153, 16, 1
	v_add3_u32 v153, v153, v197, s67
	ds_write_b16_d16_hi v196, v153 offset:41216
	s_waitcnt vmcnt(30)
	s_nop 0
	v_bfe_u32 v153, v195, 16, 1
	v_mad_u32_u24 v194, v207, s0, v194
	v_add3_u32 v153, v195, v153, s67
	v_lshl_add_u32 v194, v194, 1, 0
	ds_write_b16_d16_hi v194, v153 offset:8192
	v_and_b32_e32 v153, 0xffff0000, v153
	v_sub_f32_e64 v153, v195, v153
	v_bfe_u32 v195, v153, 16, 1
	v_add3_u32 v153, v153, v195, s67
	ds_write_b16_d16_hi v194, v153 offset:41216
	s_waitcnt vmcnt(29)
	s_nop 0
	v_bfe_u32 v153, v193, 16, 1
	v_mad_u32_u24 v192, v207, s0, v192
	v_add3_u32 v153, v193, v153, s67
	v_lshl_add_u32 v192, v192, 1, 0
	ds_write_b16_d16_hi v192, v153 offset:8192
	v_and_b32_e32 v153, 0xffff0000, v153
	v_sub_f32_e64 v153, v193, v153
	v_bfe_u32 v193, v153, 16, 1
	v_add3_u32 v153, v153, v193, s67
	ds_write_b16_d16_hi v192, v153 offset:41216
	s_waitcnt vmcnt(28)
	s_nop 0
	v_bfe_u32 v153, v191, 16, 1
	v_mad_u32_u24 v190, v207, s0, v190
	v_add3_u32 v153, v191, v153, s67
	v_lshl_add_u32 v190, v190, 1, 0
	ds_write_b16_d16_hi v190, v153 offset:8192
	v_and_b32_e32 v153, 0xffff0000, v153
	v_sub_f32_e64 v153, v191, v153
	v_bfe_u32 v191, v153, 16, 1
	v_add3_u32 v153, v153, v191, s67
	ds_write_b16_d16_hi v190, v153 offset:41216
	s_waitcnt vmcnt(27)
	s_nop 0
	v_bfe_u32 v153, v189, 16, 1
	v_mad_u32_u24 v188, v207, s0, v188
	v_add3_u32 v153, v189, v153, s67
	v_lshl_add_u32 v188, v188, 1, 0
	ds_write_b16_d16_hi v188, v153 offset:8192
	v_and_b32_e32 v153, 0xffff0000, v153
	v_sub_f32_e64 v153, v189, v153
	v_bfe_u32 v189, v153, 16, 1
	v_add3_u32 v153, v153, v189, s67
	ds_write_b16_d16_hi v188, v153 offset:41216
	s_waitcnt vmcnt(26)
	s_nop 0
	v_bfe_u32 v153, v185, 16, 1
	v_mad_u32_u24 v184, v207, s0, v184
	v_add3_u32 v153, v185, v153, s67
	v_lshl_add_u32 v184, v184, 1, 0
	ds_write_b16_d16_hi v184, v153 offset:8192
	v_and_b32_e32 v153, 0xffff0000, v153
	v_sub_f32_e64 v153, v185, v153
	v_bfe_u32 v185, v153, 16, 1
	v_add3_u32 v153, v153, v185, s67
	ds_write_b16_d16_hi v184, v153 offset:41216
	s_waitcnt vmcnt(25)
	s_nop 0
	v_bfe_u32 v153, v181, 16, 1
	v_mad_u32_u24 v180, v207, s0, v180
	v_add3_u32 v153, v181, v153, s67
	v_lshl_add_u32 v180, v180, 1, 0
	ds_write_b16_d16_hi v180, v153 offset:8192
	v_and_b32_e32 v153, 0xffff0000, v153
	v_sub_f32_e64 v153, v181, v153
	v_bfe_u32 v181, v153, 16, 1
	v_add3_u32 v153, v153, v181, s67
	ds_write_b16_d16_hi v180, v153 offset:41216
	s_waitcnt vmcnt(24)
	s_nop 0
	v_bfe_u32 v153, v177, 16, 1
	v_mad_u32_u24 v176, v207, s0, v176
	v_add3_u32 v153, v177, v153, s67
	v_lshl_add_u32 v176, v176, 1, 0
	ds_write_b16_d16_hi v176, v153 offset:8192
	v_and_b32_e32 v153, 0xffff0000, v153
	v_sub_f32_e64 v153, v177, v153
	v_bfe_u32 v177, v153, 16, 1
	v_add3_u32 v153, v153, v177, s67
	ds_write_b16_d16_hi v176, v153 offset:41216
	s_waitcnt vmcnt(23)
	s_nop 0
	v_bfe_u32 v153, v187, 16, 1
	v_mad_u32_u24 v176, v207, s0, v186
	v_add3_u32 v153, v187, v153, s67
	v_lshl_add_u32 v176, v176, 1, 0
	ds_write_b16_d16_hi v176, v153 offset:8192
	v_and_b32_e32 v153, 0xffff0000, v153
	v_sub_f32_e64 v153, v187, v153
	v_bfe_u32 v177, v153, 16, 1
	v_add3_u32 v153, v153, v177, s67
	ds_write_b16_d16_hi v176, v153 offset:41216
	s_waitcnt vmcnt(22)
	s_nop 0
	v_bfe_u32 v153, v183, 16, 1
	v_mad_u32_u24 v176, v207, s0, v182
	v_add3_u32 v153, v183, v153, s67
	v_lshl_add_u32 v176, v176, 1, 0
	ds_write_b16_d16_hi v176, v153 offset:8192
	v_and_b32_e32 v153, 0xffff0000, v153
	v_sub_f32_e64 v153, v183, v153
	v_bfe_u32 v177, v153, 16, 1
	v_add3_u32 v153, v153, v177, s67
	ds_write_b16_d16_hi v176, v153 offset:41216
	s_waitcnt vmcnt(21)
	s_nop 0
	v_bfe_u32 v153, v179, 16, 1
	v_mad_u32_u24 v176, v207, s0, v178
	v_add3_u32 v153, v179, v153, s67
	v_lshl_add_u32 v176, v176, 1, 0
	ds_write_b16_d16_hi v176, v153 offset:8192
	v_and_b32_e32 v153, 0xffff0000, v153
	v_sub_f32_e64 v153, v179, v153
	v_bfe_u32 v177, v153, 16, 1
	v_add3_u32 v153, v153, v177, s67
	ds_write_b16_d16_hi v176, v153 offset:41216
	s_waitcnt vmcnt(20)
	s_nop 0
	v_bfe_u32 v153, v175, 16, 1
	v_mad_u32_u24 v174, v207, s0, v174
	v_add3_u32 v153, v175, v153, s67
	v_lshl_add_u32 v174, v174, 1, 0
	ds_write_b16_d16_hi v174, v153 offset:8192
	v_and_b32_e32 v153, 0xffff0000, v153
	v_sub_f32_e64 v153, v175, v153
	v_bfe_u32 v175, v153, 16, 1
	v_add3_u32 v153, v153, v175, s67
	ds_write_b16_d16_hi v174, v153 offset:41216
	s_waitcnt vmcnt(19)
	s_nop 0
	v_bfe_u32 v153, v173, 16, 1
	v_mad_u32_u24 v172, v207, s0, v172
	v_add3_u32 v153, v173, v153, s67
	v_lshl_add_u32 v172, v172, 1, 0
	ds_write_b16_d16_hi v172, v153 offset:8192
	v_and_b32_e32 v153, 0xffff0000, v153
	v_sub_f32_e64 v153, v173, v153
	v_bfe_u32 v173, v153, 16, 1
	v_add3_u32 v153, v153, v173, s67
	ds_write_b16_d16_hi v172, v153 offset:41216
	s_waitcnt vmcnt(18)
	s_nop 0
	v_bfe_u32 v153, v169, 16, 1
	v_mad_u32_u24 v168, v207, s0, v168
	v_add3_u32 v153, v169, v153, s67
	v_lshl_add_u32 v168, v168, 1, 0
	ds_write_b16_d16_hi v168, v153 offset:8192
	v_and_b32_e32 v153, 0xffff0000, v153
	v_sub_f32_e64 v153, v169, v153
	v_bfe_u32 v169, v153, 16, 1
	v_add3_u32 v153, v153, v169, s67
	ds_write_b16_d16_hi v168, v153 offset:41216
	s_waitcnt vmcnt(17)
	s_nop 0
	v_bfe_u32 v153, v165, 16, 1
	v_mad_u32_u24 v164, v207, s0, v164
	v_add3_u32 v153, v165, v153, s67
	v_lshl_add_u32 v164, v164, 1, 0
	ds_write_b16_d16_hi v164, v153 offset:8192
	v_and_b32_e32 v153, 0xffff0000, v153
	v_sub_f32_e64 v153, v165, v153
	v_bfe_u32 v165, v153, 16, 1
	v_add3_u32 v153, v153, v165, s67
	ds_write_b16_d16_hi v164, v153 offset:41216
	s_waitcnt vmcnt(16)
	s_nop 0
	v_bfe_u32 v153, v161, 16, 1
	v_mad_u32_u24 v160, v207, s0, v160
	v_add3_u32 v153, v161, v153, s67
	v_lshl_add_u32 v160, v160, 1, 0
	ds_write_b16_d16_hi v160, v153 offset:8192
	v_and_b32_e32 v153, 0xffff0000, v153
	v_sub_f32_e64 v153, v161, v153
	v_bfe_u32 v161, v153, 16, 1
	v_add3_u32 v153, v153, v161, s67
	ds_write_b16_d16_hi v160, v153 offset:41216
	s_waitcnt vmcnt(15)
	s_nop 0
	v_bfe_u32 v153, v171, 16, 1
	v_mad_u32_u24 v160, v207, s0, v170
	v_add3_u32 v153, v171, v153, s67
	v_lshl_add_u32 v160, v160, 1, 0
	ds_write_b16_d16_hi v160, v153 offset:8192
	v_and_b32_e32 v153, 0xffff0000, v153
	v_sub_f32_e64 v153, v171, v153
	v_bfe_u32 v161, v153, 16, 1
	v_add3_u32 v153, v153, v161, s67
	ds_write_b16_d16_hi v160, v153 offset:41216
	s_waitcnt vmcnt(14)
	s_nop 0
	v_bfe_u32 v153, v167, 16, 1
	v_mad_u32_u24 v160, v207, s0, v166
	v_add3_u32 v153, v167, v153, s67
	v_lshl_add_u32 v160, v160, 1, 0
	ds_write_b16_d16_hi v160, v153 offset:8192
	v_and_b32_e32 v153, 0xffff0000, v153
	v_sub_f32_e64 v153, v167, v153
	v_bfe_u32 v161, v153, 16, 1
	v_add3_u32 v153, v153, v161, s67
	ds_write_b16_d16_hi v160, v153 offset:41216
	s_waitcnt vmcnt(13)
	s_nop 0
	v_bfe_u32 v153, v163, 16, 1
	v_mad_u32_u24 v160, v207, s0, v162
	v_add3_u32 v153, v163, v153, s67
	v_lshl_add_u32 v160, v160, 1, 0
	ds_write_b16_d16_hi v160, v153 offset:8192
	v_and_b32_e32 v153, 0xffff0000, v153
	v_sub_f32_e64 v153, v163, v153
	v_bfe_u32 v161, v153, 16, 1
	v_add3_u32 v153, v153, v161, s67
	ds_write_b16_d16_hi v160, v153 offset:41216
	s_waitcnt vmcnt(12)
	s_nop 0
	v_bfe_u32 v153, v157, 16, 1
	v_mad_u32_u24 v156, v207, s0, v156
	v_add3_u32 v153, v157, v153, s67
	v_lshl_add_u32 v156, v156, 1, 0
	ds_write_b16_d16_hi v156, v153 offset:8192
	v_and_b32_e32 v153, 0xffff0000, v153
	v_sub_f32_e64 v153, v157, v153
	v_bfe_u32 v157, v153, 16, 1
	v_add3_u32 v153, v153, v157, s67
	ds_write_b16_d16_hi v156, v153 offset:41216
	s_waitcnt vmcnt(11)
	s_nop 0
	v_bfe_u32 v153, v155, 16, 1
	v_mad_u32_u24 v154, v207, s0, v154
	v_add3_u32 v153, v155, v153, s67
	v_lshl_add_u32 v154, v154, 1, 0
	ds_write_b16_d16_hi v154, v153 offset:8192
	v_and_b32_e32 v153, 0xffff0000, v153
	v_sub_f32_e64 v153, v155, v153
	v_bfe_u32 v155, v153, 16, 1
	v_add3_u32 v153, v153, v155, s67
	ds_write_b16_d16_hi v154, v153 offset:41216
	s_waitcnt vmcnt(10)
	s_nop 0
	v_bfe_u32 v153, v151, 16, 1
	v_mad_u32_u24 v150, v207, s0, v150
	v_add3_u32 v153, v151, v153, s67
	v_lshl_add_u32 v150, v150, 1, 0
	ds_write_b16_d16_hi v150, v153 offset:8192
	v_and_b32_e32 v153, 0xffff0000, v153
	v_sub_f32_e64 v151, v151, v153
	v_bfe_u32 v153, v151, 16, 1
	v_add3_u32 v151, v151, v153, s67
	ds_write_b16_d16_hi v150, v151 offset:41216
	s_waitcnt vmcnt(9)
	s_nop 0
	v_bfe_u32 v150, v147, 16, 1
	v_mad_u32_u24 v146, v207, s0, v146
	v_add3_u32 v150, v147, v150, s67
	v_lshl_add_u32 v146, v146, 1, 0
	ds_write_b16_d16_hi v146, v150 offset:8192
	v_and_b32_e32 v150, 0xffff0000, v150
	v_sub_f32_e64 v147, v147, v150
	v_bfe_u32 v150, v147, 16, 1
	v_add3_u32 v147, v147, v150, s67
	ds_write_b16_d16_hi v146, v147 offset:41216
	s_waitcnt vmcnt(8)
	s_nop 0
	v_bfe_u32 v146, v143, 16, 1
	v_mad_u32_u24 v142, v207, s0, v142
	v_add3_u32 v146, v143, v146, s67
	v_lshl_add_u32 v142, v142, 1, 0
	ds_write_b16_d16_hi v142, v146 offset:8192
	v_and_b32_e32 v146, 0xffff0000, v146
	v_sub_f32_e64 v143, v143, v146
	v_bfe_u32 v146, v143, 16, 1
	v_add3_u32 v143, v143, v146, s67
	ds_write_b16_d16_hi v142, v143 offset:41216
	s_waitcnt vmcnt(7)
	s_nop 0
	v_bfe_u32 v142, v149, 16, 1
	v_mad_u32_u24 v143, v207, s0, v152
	v_add3_u32 v142, v149, v142, s67
	v_lshl_add_u32 v143, v143, 1, 0
	ds_write_b16_d16_hi v143, v142 offset:8192
	v_and_b32_e32 v142, 0xffff0000, v142
	v_sub_f32_e64 v142, v149, v142
	v_bfe_u32 v146, v142, 16, 1
	v_add3_u32 v142, v142, v146, s67
	ds_write_b16_d16_hi v143, v142 offset:41216
	s_waitcnt vmcnt(6)
	s_nop 0
	v_bfe_u32 v142, v145, 16, 1
	v_mad_u32_u24 v143, v207, s0, v148
	v_add3_u32 v142, v145, v142, s67
	v_lshl_add_u32 v143, v143, 1, 0
	ds_write_b16_d16_hi v143, v142 offset:8192
	v_and_b32_e32 v142, 0xffff0000, v142
	v_sub_f32_e64 v142, v145, v142
	v_bfe_u32 v145, v142, 16, 1
	v_add3_u32 v142, v142, v145, s67
	ds_write_b16_d16_hi v143, v142 offset:41216
	s_waitcnt vmcnt(5)
	s_nop 0
	v_bfe_u32 v142, v141, 16, 1
	v_mad_u32_u24 v143, v207, s0, v144
	v_add3_u32 v142, v141, v142, s67
	v_lshl_add_u32 v143, v143, 1, 0
	ds_write_b16_d16_hi v143, v142 offset:8192
	v_and_b32_e32 v142, 0xffff0000, v142
	v_sub_f32_e64 v141, v141, v142
	v_bfe_u32 v142, v141, 16, 1
	v_add3_u32 v141, v141, v142, s67
	ds_write_b16_d16_hi v143, v141 offset:41216
	s_waitcnt vmcnt(4)
	s_nop 0
	v_bfe_u32 v141, v139, 16, 1
	v_mad_u32_u24 v140, v207, s0, v140
	v_add3_u32 v141, v139, v141, s67
	v_lshl_add_u32 v140, v140, 1, 0
	ds_write_b16_d16_hi v140, v141 offset:8192
	v_and_b32_e32 v141, 0xffff0000, v141
	v_sub_f32_e64 v139, v139, v141
	v_bfe_u32 v141, v139, 16, 1
	v_add3_u32 v139, v139, v141, s67
	ds_write_b16_d16_hi v140, v139 offset:41216
	s_waitcnt vmcnt(3)
	s_nop 0
	v_bfe_u32 v139, v137, 16, 1
	v_mad_u32_u24 v138, v207, s0, v138
	v_add3_u32 v139, v137, v139, s67
	v_lshl_add_u32 v138, v138, 1, 0
	ds_write_b16_d16_hi v138, v139 offset:8192
	v_and_b32_e32 v139, 0xffff0000, v139
	v_sub_f32_e64 v137, v137, v139
	v_bfe_u32 v139, v137, 16, 1
	v_add3_u32 v137, v137, v139, s67
	ds_write_b16_d16_hi v138, v137 offset:41216
	s_waitcnt vmcnt(2)
	s_nop 0
	v_bfe_u32 v137, v135, 16, 1
	v_mad_u32_u24 v136, v207, s0, v136
	v_add3_u32 v137, v135, v137, s67
	v_lshl_add_u32 v136, v136, 1, 0
	ds_write_b16_d16_hi v136, v137 offset:8192
	v_and_b32_e32 v137, 0xffff0000, v137
	v_sub_f32_e64 v135, v135, v137
	v_bfe_u32 v137, v135, 16, 1
	v_add3_u32 v135, v135, v137, s67
	ds_write_b16_d16_hi v136, v135 offset:41216
	s_waitcnt vmcnt(1)
	s_nop 0
	v_bfe_u32 v135, v133, 16, 1
	v_mad_u32_u24 v134, v207, s0, v134
	v_add3_u32 v135, v133, v135, s67
	v_lshl_add_u32 v134, v134, 1, 0
	ds_write_b16_d16_hi v134, v135 offset:8192
	v_and_b32_e32 v135, 0xffff0000, v135
	v_sub_f32_e64 v133, v133, v135
	v_bfe_u32 v135, v133, 16, 1
	v_add3_u32 v133, v133, v135, s67
	ds_write_b16_d16_hi v134, v133 offset:41216
	s_waitcnt vmcnt(0)
	s_nop 0
	v_bfe_u32 v133, v131, 16, 1
	v_mad_u32_u24 v132, v207, s0, v132
	v_add3_u32 v133, v131, v133, s67
	v_lshl_add_u32 v132, v132, 1, 0
	ds_write_b16_d16_hi v132, v133 offset:8192
	v_and_b32_e32 v133, 0xffff0000, v133
	v_sub_f32_e64 v131, v131, v133
	v_bfe_u32 v133, v131, 16, 1
	v_add3_u32 v131, v131, v133, s67
	v_cmp_gt_i32_e64 s[0:1], 32, v158
	ds_write_b16_d16_hi v132, v131 offset:41216
	s_and_saveexec_b64 s[6:7], s[0:1]
	s_nop 0
	v_lshl_add_u32 v131, v158, 2, 0
	v_add_u32_e32 v131, 0x16200, v131
	ds_write_b32 v131, v97
	s_or_b64 exec, exec, s[6:7]
	s_and_b64 vcc, exec, s[2:3]
	s_cbranch_vccnz .LBB0_1146
	v_and_b32_e32 v136, 64, v227
	v_xor_b32_e32 v131, 16, v227
	v_add_u32_e32 v136, 64, v136
	v_cmp_lt_i32_e32 vcc, v131, v136
	s_nop 0
	v_readlane_b32 s2, v254, 32
	v_and_b32_e32 v134, 63, v158
	v_cndmask_b32_e32 v131, v227, v131, vcc
	v_lshlrev_b32_e32 v170, 2, v131
	v_xor_b32_e32 v131, 32, v227
	v_lshlrev_b32_e32 v135, 2, v158
	s_lshl_b32 s4, s8, 5
	v_cmp_lt_i32_e32 vcc, v131, v136
	s_nop 0
	v_readlane_b32 s3, v254, 33
	v_lshrrev_b32_e32 v137, 2, v158
	s_nop 0
	s_add_i32 s6, 0, 0x16200
	v_cndmask_b32_e32 v131, v227, v131, vcc
	s_nop 0
	v_lshl_add_u64 v[162:163], s[2:3], 0, v[96:97]
	v_mul_u32_u24_e32 v136, 0x810, v207
	v_and_or_b32 v172, v137, 12, s4
	v_readlane_b32 s2, v255, 15
	v_add_lshl_u32 v137, s4, v134, 6
	v_add_u32_e64 v176, s6, v135
	v_readlane_b32 s6, v255, 18
	v_lshlrev_b64 v[132:133], 2, v[158:159]
	v_lshlrev_b32_e32 v171, 2, v131
	v_mov_b32_e32 v131, v97
	v_lshl_add_u32 v173, v207, 2, s2
	v_cmp_gt_u32_e64 s[2:3], 32, v134
	v_or_b32_e32 v134, s4, v134
	s_nop 0
	v_readlane_b32 s8, v255, 16
	v_readlane_b32 s9, v255, 17
	v_add_u32_e32 v177, s6, v135
	s_movk_i32 s6, 0x100
	v_add3_u32 v181, 0, v136, v96
	v_add_u32_e64 v96, 0, v137
	v_lshl_add_u64 v[160:161], s[20:21], 0, v[132:133]
	v_add_u32_e64 v168, 0, v135
	v_or_b32_e32 v169, s4, v207
	s_mov_b32 s24, -1
	v_lshl_add_u32 v174, v134, 2, s8
	v_lshl_add_u32 v175, v134, 3, s9
	v_cmp_gt_i32_e64 s[4:5], 24, v158
	v_lshl_add_u64 v[164:165], s[80:81], 0, v[132:133]
	v_cmp_gt_i32_e64 s[6:7], s6, v158
	v_add_u32_e64 v178, s8, v135
	v_lshl_add_u32 v179, v158, 3, s9
	v_lshl_add_u32 v180, v130, 2, 0
	v_lshl_add_u64 v[166:167], s[78:79], 0, v[130:131]
	v_add_u32_e32 v182, 0x12200, v96
	s_mov_b32 s25, s23
	s_branch .LBB0_1064

.LBB0_1064:
	s_ashr_i32 s8, s25, 4
	s_cmp_eq_u32 s8, s24
	s_cbranch_scc1 .LBB0_1068
	s_cmp_eq_u32 s25, s23
	v_mov_b32_e32 v133, v205
	v_mov_b32_e32 v134, v206
	v_mov_b32_e32 v131, v203
	v_mov_b32_e32 v132, v204
	v_mov_b32_e64 v96, v199
	v_mov_b32_e32 v130, v202
	s_waitcnt lgkmcnt(0)
	s_barrier
	s_cbranch_scc1 .LBB0_1067
	v_mad_i64_i32 v[132:133], s[10:11], s8, v234, v[158:159]
	v_lshlrev_b64 v[134:135], 2, v[132:133]
	v_lshl_add_u64 v[136:137], s[52:53], 0, v[134:135]
	global_load_dword v130, v[160:161], off
	global_load_dword v96, v[160:161], off offset:2048
	global_load_dword v132, v[136:137], off
	global_load_dword v131, v[136:137], off offset:2048
	v_lshl_add_u64 v[136:137], s[30:31], 0, v[134:135]
	global_load_dword v134, v[136:137], off
	global_load_dword v133, v[136:137], off offset:2048
.LBB0_1067:
	s_waitcnt vmcnt(3)
	v_add_f32_e32 v132, 1.0, v132
	s_waitcnt vmcnt(2)
	v_add_f32_e32 v131, 1.0, v131
	v_mul_f32_e64 v130, v132, v130
	v_mul_f32_e32 v96, v131, v96
	s_mov_b32 s24, s8
	ds_write2st64_b32 v168, v130, v96 offset1:8
	s_waitcnt vmcnt(0)
	s_nop 0
	ds_write2st64_b32 v168, v134, v133 offset0:16 offset1:24

.LBB0_1069:
	s_waitcnt vmcnt(30)
	v_and_b32_e32 v133, 0xffff0000, v4
	v_lshlrev_b32_e32 v96, 16, v4
	v_mul_f32_e32 v133, v133, v133
	v_and_b32_e32 v134, 0xffff0000, v5
	v_fmac_f32_e32 v133, v96, v96
	v_lshlrev_b32_e32 v96, 16, v5
	v_mul_f32_e32 v134, v134, v134
	v_fmac_f32_e32 v134, v96, v96
	v_add_f32_e64 v96, v133, v134
	v_and_b32_e32 v134, 0xffff0000, v6
	v_lshlrev_b32_e32 v133, 16, v6
	v_mul_f32_e32 v134, v134, v134
	v_fmac_f32_e32 v134, v133, v133
	v_add_f32_e32 v96, v134, v96
	v_and_b32_e32 v134, 0xffff0000, v7
	v_lshlrev_b32_e32 v133, 16, v7
	v_mul_f32_e32 v134, v134, v134
	v_fmac_f32_e32 v134, v133, v133
	v_add_f32_e32 v96, v134, v96
	v_and_b32_e32 v134, 0xffff0000, v0
	v_lshlrev_b32_e32 v133, 16, v0
	v_mul_f32_e32 v134, v134, v134
	v_fmac_f32_e32 v134, v133, v133
	v_add_f32_e32 v96, v134, v96
	v_and_b32_e32 v134, 0xffff0000, v1
	v_lshlrev_b32_e32 v133, 16, v1
	v_mul_f32_e32 v134, v134, v134
	v_fmac_f32_e32 v134, v133, v133
	v_add_f32_e32 v96, v134, v96
	v_and_b32_e32 v134, 0xffff0000, v2
	v_lshlrev_b32_e32 v133, 16, v2
	v_mul_f32_e32 v134, v134, v134
	v_fmac_f32_e32 v134, v133, v133
	v_add_f32_e32 v96, v134, v96
	v_and_b32_e32 v134, 0xffff0000, v3
	v_lshlrev_b32_e32 v133, 16, v3
	v_mul_f32_e32 v134, v134, v134
	v_fmac_f32_e32 v134, v133, v133
	v_add_f32_e32 v96, v134, v96
	s_waitcnt vmcnt(28)
	s_nop 0
	v_and_b32_e32 v134, 0xffff0000, v12
	v_lshlrev_b32_e32 v133, 16, v12
	v_mul_f32_e32 v134, v134, v134
	v_fmac_f32_e32 v134, v133, v133
	v_add_f32_e32 v96, v134, v96
	v_and_b32_e32 v134, 0xffff0000, v13
	v_lshlrev_b32_e32 v133, 16, v13
	v_mul_f32_e32 v134, v134, v134
	v_fmac_f32_e32 v134, v133, v133
	v_add_f32_e32 v96, v134, v96
	v_and_b32_e32 v134, 0xffff0000, v14
	v_lshlrev_b32_e32 v133, 16, v14
	v_mul_f32_e32 v134, v134, v134
	v_fmac_f32_e32 v134, v133, v133
	v_add_f32_e32 v96, v134, v96
	v_and_b32_e32 v134, 0xffff0000, v15
	v_lshlrev_b32_e32 v133, 16, v15
	v_mul_f32_e32 v134, v134, v134
	v_fmac_f32_e32 v134, v133, v133
	v_add_f32_e32 v96, v134, v96
	v_and_b32_e32 v134, 0xffff0000, v8
	v_lshlrev_b32_e32 v133, 16, v8
	v_mul_f32_e32 v134, v134, v134
	v_fmac_f32_e32 v134, v133, v133
	v_add_f32_e32 v96, v134, v96
	v_and_b32_e32 v134, 0xffff0000, v9
	v_lshlrev_b32_e32 v133, 16, v9
	v_mul_f32_e32 v134, v134, v134
	v_fmac_f32_e32 v134, v133, v133
	v_add_f32_e32 v96, v134, v96
	v_and_b32_e32 v134, 0xffff0000, v10
	v_lshlrev_b32_e32 v133, 16, v10
	v_mul_f32_e32 v134, v134, v134
	v_fmac_f32_e32 v134, v133, v133
	v_add_f32_e32 v96, v134, v96
	v_and_b32_e32 v134, 0xffff0000, v11
	v_lshlrev_b32_e32 v133, 16, v11
	v_mul_f32_e32 v134, v134, v134
	v_fmac_f32_e32 v134, v133, v133
	v_add_f32_e32 v96, v134, v96
	s_waitcnt vmcnt(26)
	s_nop 0
	v_and_b32_e32 v134, 0xffff0000, v20
	v_lshlrev_b32_e32 v133, 16, v20
	v_mul_f32_e32 v134, v134, v134
	v_fmac_f32_e32 v134, v133, v133
	v_add_f32_e32 v96, v134, v96
	v_and_b32_e32 v134, 0xffff0000, v21
	v_lshlrev_b32_e32 v133, 16, v21
	v_mul_f32_e32 v134, v134, v134
	v_fmac_f32_e32 v134, v133, v133
	v_add_f32_e32 v96, v134, v96
	v_and_b32_e32 v134, 0xffff0000, v22
	v_lshlrev_b32_e32 v133, 16, v22
	v_mul_f32_e32 v134, v134, v134
	v_fmac_f32_e32 v134, v133, v133
	v_add_f32_e32 v96, v134, v96
	v_and_b32_e32 v134, 0xffff0000, v23
	v_lshlrev_b32_e32 v133, 16, v23
	v_mul_f32_e32 v134, v134, v134
	v_fmac_f32_e32 v134, v133, v133
	v_add_f32_e32 v96, v134, v96
	v_and_b32_e32 v134, 0xffff0000, v16
	v_lshlrev_b32_e32 v133, 16, v16
	v_mul_f32_e32 v134, v134, v134
	v_fmac_f32_e32 v134, v133, v133
	v_add_f32_e32 v96, v134, v96
	v_and_b32_e32 v134, 0xffff0000, v17
	v_lshlrev_b32_e32 v133, 16, v17
	v_mul_f32_e32 v134, v134, v134
	v_fmac_f32_e32 v134, v133, v133
	v_add_f32_e32 v96, v134, v96
	v_and_b32_e32 v134, 0xffff0000, v18
	v_lshlrev_b32_e32 v133, 16, v18
	v_mul_f32_e32 v134, v134, v134
	v_fmac_f32_e32 v134, v133, v133
	v_add_f32_e32 v96, v134, v96
	v_and_b32_e32 v134, 0xffff0000, v19
	v_lshlrev_b32_e32 v133, 16, v19
	v_mul_f32_e32 v134, v134, v134
	v_fmac_f32_e32 v134, v133, v133
	v_add_f32_e32 v96, v134, v96
	s_waitcnt vmcnt(24)
	s_nop 0
	v_and_b32_e32 v134, 0xffff0000, v28
	v_lshlrev_b32_e32 v133, 16, v28
	v_mul_f32_e32 v134, v134, v134
	v_fmac_f32_e32 v134, v133, v133
	v_add_f32_e32 v96, v134, v96
	v_and_b32_e32 v134, 0xffff0000, v29
	v_lshlrev_b32_e32 v133, 16, v29
	v_mul_f32_e32 v134, v134, v134
	v_fmac_f32_e32 v134, v133, v133
	v_add_f32_e32 v96, v134, v96
	v_and_b32_e32 v134, 0xffff0000, v30
	v_lshlrev_b32_e32 v133, 16, v30
	v_mul_f32_e32 v134, v134, v134
	v_fmac_f32_e32 v134, v133, v133
	v_add_f32_e32 v96, v134, v96
	v_and_b32_e32 v134, 0xffff0000, v31
	v_lshlrev_b32_e32 v133, 16, v31
	v_mul_f32_e32 v134, v134, v134
	v_fmac_f32_e32 v134, v133, v133
	v_add_f32_e32 v96, v134, v96
	v_and_b32_e32 v134, 0xffff0000, v24
	v_lshlrev_b32_e32 v133, 16, v24
	v_mul_f32_e32 v134, v134, v134
	v_fmac_f32_e32 v134, v133, v133
	v_add_f32_e32 v96, v134, v96
	v_and_b32_e32 v134, 0xffff0000, v25
	v_lshlrev_b32_e32 v133, 16, v25
	v_mul_f32_e32 v134, v134, v134
	v_fmac_f32_e32 v134, v133, v133
	v_add_f32_e32 v96, v134, v96
	v_and_b32_e32 v134, 0xffff0000, v26
	v_lshlrev_b32_e32 v133, 16, v26
	v_mul_f32_e32 v134, v134, v134
	v_fmac_f32_e32 v134, v133, v133
	v_add_f32_e32 v96, v134, v96
	v_and_b32_e32 v134, 0xffff0000, v27
	v_lshlrev_b32_e32 v133, 16, v27
	v_mul_f32_e32 v134, v134, v134
	v_fmac_f32_e32 v134, v133, v133
	v_add_f32_e32 v96, v134, v96
	s_waitcnt vmcnt(22)
	s_nop 0
	v_and_b32_e32 v134, 0xffff0000, v36
	v_lshlrev_b32_e32 v133, 16, v36
	v_mul_f32_e32 v134, v134, v134
	v_fmac_f32_e32 v134, v133, v133
	v_add_f32_e32 v96, v134, v96
	v_and_b32_e32 v134, 0xffff0000, v37
	v_lshlrev_b32_e32 v133, 16, v37
	v_mul_f32_e32 v134, v134, v134
	v_fmac_f32_e32 v134, v133, v133
	v_add_f32_e32 v96, v134, v96
	v_and_b32_e32 v134, 0xffff0000, v38
	v_lshlrev_b32_e32 v133, 16, v38
	v_mul_f32_e32 v134, v134, v134
	v_fmac_f32_e32 v134, v133, v133
	v_add_f32_e32 v96, v134, v96
	v_and_b32_e32 v134, 0xffff0000, v39
	v_lshlrev_b32_e32 v133, 16, v39
	v_mul_f32_e32 v134, v134, v134
	v_fmac_f32_e32 v134, v133, v133
	v_add_f32_e32 v96, v134, v96
	v_and_b32_e32 v134, 0xffff0000, v32
	v_lshlrev_b32_e32 v133, 16, v32
	v_mul_f32_e32 v134, v134, v134
	v_fmac_f32_e32 v134, v133, v133
	v_add_f32_e32 v96, v134, v96
	v_and_b32_e32 v134, 0xffff0000, v33
	v_lshlrev_b32_e32 v133, 16, v33
	v_mul_f32_e32 v134, v134, v134
	v_fmac_f32_e32 v134, v133, v133
	v_add_f32_e32 v96, v134, v96
	v_and_b32_e32 v134, 0xffff0000, v34
	v_lshlrev_b32_e32 v133, 16, v34
	v_mul_f32_e32 v134, v134, v134
	v_fmac_f32_e32 v134, v133, v133
	v_add_f32_e32 v96, v134, v96
	v_and_b32_e32 v134, 0xffff0000, v35
	v_lshlrev_b32_e32 v133, 16, v35
	v_mul_f32_e32 v134, v134, v134
	v_fmac_f32_e32 v134, v133, v133
	v_add_f32_e32 v96, v134, v96
	s_waitcnt vmcnt(20)
	s_nop 0
	v_and_b32_e32 v134, 0xffff0000, v44
	v_lshlrev_b32_e32 v133, 16, v44
	v_mul_f32_e32 v134, v134, v134
	v_fmac_f32_e32 v134, v133, v133
	v_add_f32_e32 v96, v134, v96
	v_and_b32_e32 v134, 0xffff0000, v45
	v_lshlrev_b32_e32 v133, 16, v45
	v_mul_f32_e32 v134, v134, v134
	v_fmac_f32_e32 v134, v133, v133
	v_add_f32_e32 v96, v134, v96
	v_and_b32_e32 v134, 0xffff0000, v46
	v_lshlrev_b32_e32 v133, 16, v46
	v_mul_f32_e32 v134, v134, v134
	v_fmac_f32_e32 v134, v133, v133
	v_add_f32_e32 v96, v134, v96
	v_and_b32_e32 v134, 0xffff0000, v47
	v_lshlrev_b32_e32 v133, 16, v47
	v_mul_f32_e32 v134, v134, v134
	v_fmac_f32_e32 v134, v133, v133
	v_add_f32_e32 v96, v134, v96
	v_and_b32_e32 v134, 0xffff0000, v40
	v_lshlrev_b32_e32 v133, 16, v40
	v_mul_f32_e32 v134, v134, v134
	v_fmac_f32_e32 v134, v133, v133
	v_add_f32_e32 v96, v134, v96
	v_and_b32_e32 v134, 0xffff0000, v41
	v_lshlrev_b32_e32 v133, 16, v41
	v_mul_f32_e32 v134, v134, v134
	v_fmac_f32_e32 v134, v133, v133
	v_add_f32_e32 v96, v134, v96
	v_and_b32_e32 v134, 0xffff0000, v42
	v_lshlrev_b32_e32 v133, 16, v42
	v_mul_f32_e32 v134, v134, v134
	v_fmac_f32_e32 v134, v133, v133
	v_add_f32_e32 v96, v134, v96
	v_and_b32_e32 v134, 0xffff0000, v43
	v_lshlrev_b32_e32 v133, 16, v43
	v_mul_f32_e32 v134, v134, v134
	v_fmac_f32_e32 v134, v133, v133
	v_add_f32_e32 v96, v134, v96
	s_waitcnt vmcnt(18)
	s_nop 0
	v_and_b32_e32 v134, 0xffff0000, v52
	v_lshlrev_b32_e32 v133, 16, v52
	v_mul_f32_e32 v134, v134, v134
	v_fmac_f32_e32 v134, v133, v133
	v_add_f32_e32 v96, v134, v96
	v_and_b32_e32 v134, 0xffff0000, v53
	v_lshlrev_b32_e32 v133, 16, v53
	v_mul_f32_e32 v134, v134, v134
	v_fmac_f32_e32 v134, v133, v133
	v_add_f32_e32 v96, v134, v96
	v_and_b32_e32 v134, 0xffff0000, v54
	v_lshlrev_b32_e32 v133, 16, v54
	v_mul_f32_e32 v134, v134, v134
	v_fmac_f32_e32 v134, v133, v133
	v_add_f32_e32 v96, v134, v96
	v_and_b32_e32 v134, 0xffff0000, v55
	v_lshlrev_b32_e32 v133, 16, v55
	v_mul_f32_e32 v134, v134, v134
	v_fmac_f32_e32 v134, v133, v133
	v_add_f32_e32 v96, v134, v96
	v_and_b32_e32 v134, 0xffff0000, v48
	v_lshlrev_b32_e32 v133, 16, v48
	v_mul_f32_e32 v134, v134, v134
	v_fmac_f32_e32 v134, v133, v133
	v_add_f32_e32 v96, v134, v96
	v_and_b32_e32 v134, 0xffff0000, v49
	v_lshlrev_b32_e32 v133, 16, v49
	v_mul_f32_e32 v134, v134, v134
	v_fmac_f32_e32 v134, v133, v133
	v_add_f32_e32 v96, v134, v96
	v_and_b32_e32 v134, 0xffff0000, v50
	v_lshlrev_b32_e32 v133, 16, v50
	v_mul_f32_e32 v134, v134, v134
	v_fmac_f32_e32 v134, v133, v133
	v_add_f32_e32 v96, v134, v96
	v_and_b32_e32 v134, 0xffff0000, v51
	v_lshlrev_b32_e32 v133, 16, v51
	v_mul_f32_e32 v134, v134, v134
	v_fmac_f32_e32 v134, v133, v133
	v_add_f32_e32 v96, v134, v96
	s_waitcnt vmcnt(16)
	s_nop 0
	v_and_b32_e32 v134, 0xffff0000, v60
	v_lshlrev_b32_e32 v133, 16, v60
	v_mul_f32_e32 v134, v134, v134
	v_fmac_f32_e32 v134, v133, v133
	v_add_f32_e32 v96, v134, v96
	v_and_b32_e32 v134, 0xffff0000, v61
	v_lshlrev_b32_e32 v133, 16, v61
	v_mul_f32_e32 v134, v134, v134
	v_fmac_f32_e32 v134, v133, v133
	v_add_f32_e32 v96, v134, v96
	v_and_b32_e32 v134, 0xffff0000, v62
	v_lshlrev_b32_e32 v133, 16, v62
	v_mul_f32_e32 v134, v134, v134
	v_fmac_f32_e32 v134, v133, v133
	v_add_f32_e32 v96, v134, v96
	v_and_b32_e32 v134, 0xffff0000, v63
	v_lshlrev_b32_e32 v133, 16, v63
	v_mul_f32_e32 v134, v134, v134
	v_fmac_f32_e32 v134, v133, v133
	v_add_f32_e32 v96, v134, v96
	v_and_b32_e32 v134, 0xffff0000, v56
	v_lshlrev_b32_e32 v133, 16, v56
	v_mul_f32_e32 v134, v134, v134
	v_fmac_f32_e32 v134, v133, v133
	v_add_f32_e32 v96, v134, v96
	v_and_b32_e32 v134, 0xffff0000, v57
	v_lshlrev_b32_e32 v133, 16, v57
	v_mul_f32_e32 v134, v134, v134
	v_fmac_f32_e32 v134, v133, v133
	v_add_f32_e32 v96, v134, v96
	v_and_b32_e32 v134, 0xffff0000, v58
	v_lshlrev_b32_e32 v133, 16, v58
	v_mul_f32_e32 v134, v134, v134
	v_fmac_f32_e32 v134, v133, v133
	v_add_f32_e32 v96, v134, v96
	v_and_b32_e32 v134, 0xffff0000, v59
	v_lshlrev_b32_e32 v133, 16, v59
	v_mul_f32_e32 v134, v134, v134
	v_fmac_f32_e32 v134, v133, v133
	v_add_f32_e32 v96, v134, v96
	s_waitcnt vmcnt(14)
	s_nop 0
	v_and_b32_e32 v134, 0xffff0000, v68
	v_lshlrev_b32_e32 v133, 16, v68
	v_mul_f32_e32 v134, v134, v134
	v_fmac_f32_e32 v134, v133, v133
	v_add_f32_e32 v96, v134, v96
	v_and_b32_e32 v134, 0xffff0000, v69
	v_lshlrev_b32_e32 v133, 16, v69
	v_mul_f32_e32 v134, v134, v134
	v_fmac_f32_e32 v134, v133, v133
	v_add_f32_e32 v96, v134, v96
	v_and_b32_e32 v134, 0xffff0000, v70
	v_lshlrev_b32_e32 v133, 16, v70
	v_mul_f32_e32 v134, v134, v134
	v_fmac_f32_e32 v134, v133, v133
	v_add_f32_e32 v96, v134, v96
	v_and_b32_e32 v134, 0xffff0000, v71
	v_lshlrev_b32_e32 v133, 16, v71
	v_mul_f32_e32 v134, v134, v134
	v_fmac_f32_e32 v134, v133, v133
	v_add_f32_e32 v96, v134, v96
	v_and_b32_e32 v134, 0xffff0000, v64
	v_lshlrev_b32_e32 v133, 16, v64
	v_mul_f32_e32 v134, v134, v134
	v_fmac_f32_e32 v134, v133, v133
	v_add_f32_e32 v96, v134, v96
	v_and_b32_e32 v134, 0xffff0000, v65
	v_lshlrev_b32_e32 v133, 16, v65
	v_mul_f32_e32 v134, v134, v134
	v_fmac_f32_e32 v134, v133, v133
	v_add_f32_e32 v96, v134, v96
	v_and_b32_e32 v134, 0xffff0000, v66
	v_lshlrev_b32_e32 v133, 16, v66
	v_mul_f32_e32 v134, v134, v134
	v_fmac_f32_e32 v134, v133, v133
	v_add_f32_e32 v96, v134, v96
	v_and_b32_e32 v134, 0xffff0000, v67
	v_lshlrev_b32_e32 v133, 16, v67
	v_mul_f32_e32 v134, v134, v134
	v_fmac_f32_e32 v134, v133, v133
	v_add_f32_e32 v96, v134, v96
	s_waitcnt vmcnt(12)
	s_nop 0
	v_and_b32_e32 v134, 0xffff0000, v76
	v_lshlrev_b32_e32 v133, 16, v76
	v_mul_f32_e32 v134, v134, v134
	v_fmac_f32_e32 v134, v133, v133
	v_add_f32_e32 v96, v134, v96
	v_and_b32_e32 v134, 0xffff0000, v77
	v_lshlrev_b32_e32 v133, 16, v77
	v_mul_f32_e32 v134, v134, v134
	v_fmac_f32_e32 v134, v133, v133
	v_add_f32_e32 v96, v134, v96
	v_and_b32_e32 v134, 0xffff0000, v78
	v_lshlrev_b32_e32 v133, 16, v78
	v_mul_f32_e32 v134, v134, v134
	v_fmac_f32_e32 v134, v133, v133
	v_add_f32_e32 v96, v134, v96
	v_and_b32_e32 v134, 0xffff0000, v79
	v_lshlrev_b32_e32 v133, 16, v79
	v_mul_f32_e32 v134, v134, v134
	v_fmac_f32_e32 v134, v133, v133
	v_add_f32_e32 v96, v134, v96
	v_and_b32_e32 v134, 0xffff0000, v72
	v_lshlrev_b32_e32 v133, 16, v72
	v_mul_f32_e32 v134, v134, v134
	v_fmac_f32_e32 v134, v133, v133
	v_add_f32_e32 v96, v134, v96
	v_and_b32_e32 v134, 0xffff0000, v73
	v_lshlrev_b32_e32 v133, 16, v73
	v_mul_f32_e32 v134, v134, v134
	v_fmac_f32_e32 v134, v133, v133
	v_add_f32_e32 v96, v134, v96
	v_and_b32_e32 v134, 0xffff0000, v74
	v_lshlrev_b32_e32 v133, 16, v74
	v_mul_f32_e32 v134, v134, v134
	v_fmac_f32_e32 v134, v133, v133
	v_add_f32_e32 v96, v134, v96
	v_and_b32_e32 v134, 0xffff0000, v75
	v_lshlrev_b32_e32 v133, 16, v75
	v_mul_f32_e32 v134, v134, v134
	v_fmac_f32_e32 v134, v133, v133
	v_add_f32_e32 v96, v134, v96
	s_waitcnt vmcnt(10)
	s_nop 0
	v_and_b32_e32 v134, 0xffff0000, v84
	v_lshlrev_b32_e32 v133, 16, v84
	v_mul_f32_e32 v134, v134, v134
	v_fmac_f32_e32 v134, v133, v133
	v_add_f32_e32 v96, v134, v96
	v_and_b32_e32 v134, 0xffff0000, v85
	v_lshlrev_b32_e32 v133, 16, v85
	v_mul_f32_e32 v134, v134, v134
	v_fmac_f32_e32 v134, v133, v133
	v_add_f32_e32 v96, v134, v96
	v_and_b32_e32 v134, 0xffff0000, v86
	v_lshlrev_b32_e32 v133, 16, v86
	v_mul_f32_e32 v134, v134, v134
	v_fmac_f32_e32 v134, v133, v133
	v_add_f32_e32 v96, v134, v96
	v_and_b32_e32 v134, 0xffff0000, v87
	v_lshlrev_b32_e32 v133, 16, v87
	v_mul_f32_e32 v134, v134, v134
	v_fmac_f32_e32 v134, v133, v133
	v_add_f32_e32 v96, v134, v96
	v_and_b32_e32 v134, 0xffff0000, v80
	v_lshlrev_b32_e32 v133, 16, v80
	v_mul_f32_e32 v134, v134, v134
	v_fmac_f32_e32 v134, v133, v133
	v_add_f32_e32 v96, v134, v96
	v_and_b32_e32 v134, 0xffff0000, v81
	v_lshlrev_b32_e32 v133, 16, v81
	v_mul_f32_e32 v134, v134, v134
	v_fmac_f32_e32 v134, v133, v133
	v_add_f32_e32 v96, v134, v96
	v_and_b32_e32 v134, 0xffff0000, v82
	v_lshlrev_b32_e32 v133, 16, v82
	v_mul_f32_e32 v134, v134, v134
	v_fmac_f32_e32 v134, v133, v133
	v_add_f32_e32 v96, v134, v96
	v_and_b32_e32 v134, 0xffff0000, v83
	v_lshlrev_b32_e32 v133, 16, v83
	v_mul_f32_e32 v134, v134, v134
	v_fmac_f32_e32 v134, v133, v133
	v_add_f32_e32 v96, v134, v96
	s_waitcnt vmcnt(8)
	s_nop 0
	v_and_b32_e32 v134, 0xffff0000, v92
	v_lshlrev_b32_e32 v133, 16, v92
	v_mul_f32_e32 v134, v134, v134
	v_fmac_f32_e32 v134, v133, v133
	v_add_f32_e32 v96, v134, v96
	v_and_b32_e32 v134, 0xffff0000, v93
	v_lshlrev_b32_e32 v133, 16, v93
	v_mul_f32_e32 v134, v134, v134
	v_fmac_f32_e32 v134, v133, v133
	v_add_f32_e32 v96, v134, v96
	v_and_b32_e32 v134, 0xffff0000, v94
	v_lshlrev_b32_e32 v133, 16, v94
	v_mul_f32_e32 v134, v134, v134
	v_fmac_f32_e32 v134, v133, v133
	v_add_f32_e32 v96, v134, v96
	v_and_b32_e32 v134, 0xffff0000, v95
	v_lshlrev_b32_e32 v133, 16, v95
	v_mul_f32_e32 v134, v134, v134
	v_fmac_f32_e32 v134, v133, v133
	v_add_f32_e32 v96, v134, v96
	v_and_b32_e32 v134, 0xffff0000, v88
	v_lshlrev_b32_e32 v133, 16, v88
	v_mul_f32_e32 v134, v134, v134
	v_fmac_f32_e32 v134, v133, v133
	v_add_f32_e32 v96, v134, v96
	v_and_b32_e32 v134, 0xffff0000, v89
	v_lshlrev_b32_e32 v133, 16, v89
	v_mul_f32_e32 v134, v134, v134
	v_fmac_f32_e32 v134, v133, v133
	v_add_f32_e32 v96, v134, v96
	v_and_b32_e32 v134, 0xffff0000, v90
	v_lshlrev_b32_e32 v133, 16, v90
	v_mul_f32_e32 v134, v134, v134
	v_fmac_f32_e32 v134, v133, v133
	v_add_f32_e32 v96, v134, v96
	v_and_b32_e32 v134, 0xffff0000, v91
	v_lshlrev_b32_e32 v133, 16, v91
	v_mul_f32_e32 v134, v134, v134
	v_fmac_f32_e32 v134, v133, v133
	v_add_f32_e32 v96, v134, v96
	s_waitcnt vmcnt(6)
	s_nop 0
	v_and_b32_e32 v134, 0xffff0000, v102
	v_lshlrev_b32_e32 v133, 16, v102
	v_mul_f32_e32 v134, v134, v134
	v_fmac_f32_e32 v134, v133, v133
	v_add_f32_e32 v96, v134, v96
	v_and_b32_e32 v134, 0xffff0000, v103
	v_lshlrev_b32_e32 v133, 16, v103
	v_mul_f32_e32 v134, v134, v134
	v_fmac_f32_e32 v134, v133, v133
	v_add_f32_e32 v96, v134, v96
	v_and_b32_e32 v134, 0xffff0000, v104
	v_lshlrev_b32_e32 v133, 16, v104
	v_mul_f32_e32 v134, v134, v134
	v_fmac_f32_e32 v134, v133, v133
	v_add_f32_e32 v96, v134, v96
	v_and_b32_e32 v134, 0xffff0000, v105
	v_lshlrev_b32_e32 v133, 16, v105
	v_mul_f32_e32 v134, v134, v134
	v_fmac_f32_e32 v134, v133, v133
	v_add_f32_e32 v96, v134, v96
	v_and_b32_e32 v134, 0xffff0000, v98
	v_lshlrev_b32_e32 v133, 16, v98
	v_mul_f32_e32 v134, v134, v134
	v_fmac_f32_e32 v134, v133, v133
	v_add_f32_e32 v96, v134, v96
	v_and_b32_e32 v134, 0xffff0000, v99
	v_lshlrev_b32_e32 v133, 16, v99
	v_mul_f32_e32 v134, v134, v134
	v_fmac_f32_e32 v134, v133, v133
	v_add_f32_e32 v96, v134, v96
	v_and_b32_e32 v134, 0xffff0000, v100
	v_lshlrev_b32_e32 v133, 16, v100
	v_mul_f32_e32 v134, v134, v134
	v_fmac_f32_e32 v134, v133, v133
	v_add_f32_e32 v96, v134, v96
	v_and_b32_e32 v134, 0xffff0000, v101
	v_lshlrev_b32_e32 v133, 16, v101
	v_mul_f32_e32 v134, v134, v134
	v_fmac_f32_e32 v134, v133, v133
	v_add_f32_e32 v96, v134, v96
	s_waitcnt vmcnt(4)
	s_nop 0
	v_and_b32_e32 v134, 0xffff0000, v110
	v_lshlrev_b32_e32 v133, 16, v110
	v_mul_f32_e32 v134, v134, v134
	v_fmac_f32_e32 v134, v133, v133
	v_add_f32_e32 v96, v134, v96
	v_and_b32_e32 v134, 0xffff0000, v111
	v_lshlrev_b32_e32 v133, 16, v111
	v_mul_f32_e32 v134, v134, v134
	v_fmac_f32_e32 v134, v133, v133
	v_add_f32_e32 v96, v134, v96
	v_and_b32_e32 v134, 0xffff0000, v112
	v_lshlrev_b32_e32 v133, 16, v112
	v_mul_f32_e32 v134, v134, v134
	v_fmac_f32_e32 v134, v133, v133
	v_add_f32_e32 v96, v134, v96
	v_and_b32_e32 v134, 0xffff0000, v113
	v_lshlrev_b32_e32 v133, 16, v113
	v_mul_f32_e32 v134, v134, v134
	v_fmac_f32_e32 v134, v133, v133
	v_add_f32_e32 v96, v134, v96
	v_and_b32_e32 v134, 0xffff0000, v106
	v_lshlrev_b32_e32 v133, 16, v106
	v_mul_f32_e32 v134, v134, v134
	v_fmac_f32_e32 v134, v133, v133
	v_add_f32_e32 v96, v134, v96
	v_and_b32_e32 v134, 0xffff0000, v107
	v_lshlrev_b32_e32 v133, 16, v107
	v_mul_f32_e32 v134, v134, v134
	v_fmac_f32_e32 v134, v133, v133
	v_add_f32_e32 v96, v134, v96
	v_and_b32_e32 v134, 0xffff0000, v108
	v_lshlrev_b32_e32 v133, 16, v108
	v_mul_f32_e32 v134, v134, v134
	v_fmac_f32_e32 v134, v133, v133
	v_add_f32_e32 v96, v134, v96
	v_and_b32_e32 v134, 0xffff0000, v109
	v_lshlrev_b32_e32 v133, 16, v109
	v_mul_f32_e32 v134, v134, v134
	v_fmac_f32_e32 v134, v133, v133
	v_add_f32_e32 v96, v134, v96
	s_waitcnt vmcnt(2)
	s_nop 0
	v_and_b32_e32 v134, 0xffff0000, v118
	v_lshlrev_b32_e32 v133, 16, v118
	v_mul_f32_e32 v134, v134, v134
	v_fmac_f32_e32 v134, v133, v133
	v_add_f32_e32 v96, v134, v96
	v_and_b32_e32 v134, 0xffff0000, v119
	v_lshlrev_b32_e32 v133, 16, v119
	v_mul_f32_e32 v134, v134, v134
	v_fmac_f32_e32 v134, v133, v133
	v_add_f32_e32 v96, v134, v96
	v_and_b32_e32 v134, 0xffff0000, v120
	v_lshlrev_b32_e32 v133, 16, v120
	v_mul_f32_e32 v134, v134, v134
	v_fmac_f32_e32 v134, v133, v133
	v_add_f32_e32 v96, v134, v96
	v_and_b32_e32 v134, 0xffff0000, v121
	v_lshlrev_b32_e32 v133, 16, v121
	v_mul_f32_e32 v134, v134, v134
	v_fmac_f32_e32 v134, v133, v133
	v_add_f32_e32 v96, v134, v96
	v_and_b32_e32 v134, 0xffff0000, v114
	v_lshlrev_b32_e32 v133, 16, v114
	v_mul_f32_e32 v134, v134, v134
	v_fmac_f32_e32 v134, v133, v133
	v_add_f32_e32 v96, v134, v96
	v_and_b32_e32 v134, 0xffff0000, v115
	v_lshlrev_b32_e32 v133, 16, v115
	v_mul_f32_e32 v134, v134, v134
	v_fmac_f32_e32 v134, v133, v133
	v_add_f32_e32 v96, v134, v96
	v_and_b32_e32 v134, 0xffff0000, v116
	v_lshlrev_b32_e32 v133, 16, v116
	v_mul_f32_e32 v134, v134, v134
	v_fmac_f32_e32 v134, v133, v133
	v_add_f32_e32 v96, v134, v96
	v_and_b32_e32 v134, 0xffff0000, v117
	v_lshlrev_b32_e32 v133, 16, v117
	v_mul_f32_e32 v134, v134, v134
	v_fmac_f32_e32 v134, v133, v133
	v_add_f32_e32 v96, v134, v96
	s_waitcnt vmcnt(0)
	s_nop 0
	v_and_b32_e32 v134, 0xffff0000, v126
	v_lshlrev_b32_e32 v133, 16, v126
	v_mul_f32_e32 v134, v134, v134
	v_fmac_f32_e32 v134, v133, v133
	v_add_f32_e32 v96, v134, v96
	v_and_b32_e32 v134, 0xffff0000, v127
	v_lshlrev_b32_e32 v133, 16, v127
	v_mul_f32_e32 v134, v134, v134
	v_fmac_f32_e32 v134, v133, v133
	s_nop 0
	v_and_b32_e32 v137, 0xffff0000, v129
	v_and_b32_e32 v136, 0xffff0000, v128
	v_add_f32_e64 v96, v134, v96
	v_lshlrev_b32_e32 v135, 16, v129
	v_lshlrev_b32_e32 v134, 16, v128
	v_pk_mul_f32 v[136:137], v[136:137], v[136:137]
	s_nop 0
	s_nop 0
	v_pk_fma_f32 v[134:135], v[134:135], v[134:135], v[136:137]
	v_and_b32_e32 v137, 0xffff0000, v123
	v_add_f32_e64 v96, v134, v96
	v_and_b32_e32 v136, 0xffff0000, v122
	v_add_f32_e64 v96, v135, v96
	v_lshlrev_b32_e32 v135, 16, v123
	v_lshlrev_b32_e32 v134, 16, v122
	v_pk_mul_f32 v[136:137], v[136:137], v[136:137]
	s_nop 0
	s_nop 0
	v_pk_fma_f32 v[134:135], v[134:135], v[134:135], v[136:137]
	v_and_b32_e32 v137, 0xffff0000, v125
	v_add_f32_e64 v96, v134, v96
	v_and_b32_e32 v136, 0xffff0000, v124
	v_add_f32_e64 v96, v135, v96
	v_lshlrev_b32_e32 v135, 16, v125
	v_lshlrev_b32_e32 v134, 16, v124
	v_pk_mul_f32 v[136:137], v[136:137], v[136:137]
	s_nop 0
	s_nop 0
	v_pk_fma_f32 v[134:135], v[134:135], v[134:135], v[136:137]
	v_lshlrev_b32_e32 v184, 16, v4
	v_add_f32_e32 v96, v134, v96
	v_add_f32_e64 v96, v135, v96
	ds_bpermute_b32 v133, v170, v96
	v_and_b32_e32 v185, 0xffff0000, v4
	v_lshlrev_b64 v[130:131], 10, v[130:131]
	v_lshl_add_u64 v[130:131], v[166:167], 0, v[130:131]
	v_lshlrev_b32_e32 v188, 16, v12
	s_waitcnt lgkmcnt(0)
	v_add_f32_e64 v96, v96, v133
	ds_bpermute_b32 v133, v171, v96
	v_and_b32_e32 v189, 0xffff0000, v12
	s_waitcnt lgkmcnt(0)
	v_add_f32_e32 v96, v96, v133
	v_fmamk_f32 v96, v96, 0x3a800000, v220
	v_mul_f32_e32 v133, 0x4f800000, v96
	v_cmp_gt_f32_e32 vcc, s95, v96
	s_nop 1
	v_cndmask_b32_e32 v96, v96, v133, vcc
	v_sqrt_f32_e32 v133, v96
	s_nop 0
	v_add_u32_e32 v134, -1, v133
	v_fma_f32 v135, -v134, v133, v96
	v_cmp_ge_f32_e64 s[8:9], 0, v135
	v_add_u32_e32 v135, 1, v133
	s_nop 0
	v_cndmask_b32_e64 v134, v133, v134, s[8:9]
	v_fma_f32 v133, -v135, v133, v96
	v_cmp_lt_f32_e64 s[8:9], 0, v133
	s_nop 1
	s_nop 0
	v_cndmask_b32_e64 v133, v134, v135, s[8:9]
	v_mul_f32_e32 v134, 0x37800000, v133
	v_cndmask_b32_e32 v133, v133, v134, vcc
	v_cmp_class_f32_e32 vcc, v96, v221
	s_nop 1
	v_cndmask_b32_e32 v96, v133, v96, vcc
	v_div_scale_f32 v133, s[8:9], v96, v96, 1.0
	v_rcp_f32_e32 v134, v133
	s_xor_b64 s[8:9], s[12:13], -1
	s_mov_b64 s[12:13], 0
	s_nop 0
	v_fma_f32 v135, -v133, v134, 1.0
	v_fmac_f32_e32 v134, v135, v134
	s_nop 0
	v_div_scale_f32 v135, vcc, 1.0, v96, 1.0
	v_mul_f32_e64 v136, v135, v134
	v_fma_f32 v137, -v133, v136, v135
	v_fmac_f32_e32 v136, v137, v134
	s_nop 0
	v_fma_f32 v133, -v133, v136, v135
	v_div_fmas_f32 v133, v133, v134, v136
	ds_read_b128 v[134:137], v180
	ds_read_b128 v[138:141], v180 offset:16
	ds_read_b128 v[142:145], v180 offset:32
	ds_read_b128 v[146:149], v180 offset:48
	ds_read_b128 v[150:153], v180 offset:4096
	ds_read_b128 v[154:157], v180 offset:4112
	v_div_fixup_f32 v96, v133, v96, 1.0
	v_pk_mul_f32 v[184:185], v[96:97], v[184:185] op_sel_hi:[0,1]
	v_pk_mul_f32 v[188:189], v[96:97], v[188:189] op_sel_hi:[0,1]
	s_waitcnt lgkmcnt(1)
	s_nop 0
	v_pk_fma_f32 v[150:151], v[134:135], v[184:185], v[150:151]
	v_lshlrev_b32_e32 v134, 16, v5
	s_nop 0
	v_and_b32_e32 v135, 0xffff0000, v5
	v_pk_mul_f32 v[134:135], v[96:97], v[134:135] op_sel_hi:[0,1]
	v_pk_fma_f32 v[152:153], v[136:137], v[134:135], v[152:153]
	v_lshlrev_b32_e32 v134, 16, v6
	s_nop 0
	v_and_b32_e32 v135, 0xffff0000, v6
	v_pk_mul_f32 v[134:135], v[96:97], v[134:135] op_sel_hi:[0,1]
	s_waitcnt lgkmcnt(0)
	s_nop 0
	v_pk_fma_f32 v[154:155], v[138:139], v[134:135], v[154:155]
	v_lshlrev_b32_e32 v134, 16, v7
	s_nop 0
	v_and_b32_e32 v135, 0xffff0000, v7
	v_med3_f32 v133, v150, s82, v229
	v_med3_f32 v139, v151, s82, v229
	v_mov_b32_e64 v138, v97
	v_pk_mul_f32 v[134:135], v[96:97], v[134:135] op_sel_hi:[0,1]
	v_cvt_pk_fp8_f32 v138, v133, v139
	v_pk_fma_f32 v[140:141], v[140:141], v[134:135], v[156:157]
	v_cvt_pk_bf16_f32 v134, v150, v151
	v_cvt_pk_bf16_f32 v135, v152, v153
	v_med3_f32 v133, v152, s82, v229
	v_med3_f32 v151, v154, s82, v229
	v_med3_f32 v152, v155, s82, v229
	v_mov_b32_e64 v139, v97
	v_cvt_pk_fp8_f32 v139, v151, v152
	v_med3_f32 v150, v153, s82, v229
	v_cvt_pk_bf16_f32 v136, v154, v155
	v_cvt_pk_fp8_f32 v138, v133, v150 op_sel:[0,0,1]
	ds_read_b128 v[150:153], v180 offset:4128
	ds_read_b128 v[154:157], v180 offset:4144
	v_cvt_pk_bf16_f32 v137, v140, v141
	v_med3_f32 v133, v140, s82, v229
	v_med3_f32 v140, v141, s82, v229
	v_cvt_pk_fp8_f32 v139, v133, v140 op_sel:[0,0,1]
	v_lshlrev_b32_e32 v140, 16, v0
	s_nop 0
	v_and_b32_e32 v141, 0xffff0000, v0
	v_pk_mul_f32 v[140:141], v[96:97], v[140:141] op_sel_hi:[0,1]
	s_waitcnt lgkmcnt(1)
	s_nop 0
	v_pk_fma_f32 v[140:141], v[142:143], v[140:141], v[150:151]
	v_lshlrev_b32_e32 v142, 16, v1
	s_nop 0
	v_and_b32_e32 v143, 0xffff0000, v1
	v_pk_mul_f32 v[142:143], v[96:97], v[142:143] op_sel_hi:[0,1]
	v_pk_fma_f32 v[150:151], v[144:145], v[142:143], v[152:153]
	v_lshlrev_b32_e32 v142, 16, v2
	s_nop 0
	v_and_b32_e32 v143, 0xffff0000, v2
	v_pk_mul_f32 v[142:143], v[96:97], v[142:143] op_sel_hi:[0,1]
	s_waitcnt lgkmcnt(0)
	s_nop 0
	v_pk_fma_f32 v[146:147], v[146:147], v[142:143], v[154:155]
	v_lshlrev_b32_e32 v142, 16, v3
	s_nop 0
	v_and_b32_e32 v143, 0xffff0000, v3
	v_pk_mul_f32 v[142:143], v[96:97], v[142:143] op_sel_hi:[0,1]
	v_pk_fma_f32 v[152:153], v[148:149], v[142:143], v[156:157]
	v_cvt_pk_bf16_f32 v142, v140, v141
	v_med3_f32 v133, v140, s82, v229
	v_med3_f32 v141, v141, s82, v229
	v_mov_b32_e64 v140, v97
	v_cvt_pk_fp8_f32 v140, v133, v141
	v_med3_f32 v133, v150, s82, v229
	v_med3_f32 v141, v151, s82, v229
	v_cvt_pk_bf16_f32 v144, v146, v147
	v_cvt_pk_fp8_f32 v140, v133, v141 op_sel:[0,0,1]
	v_med3_f32 v133, v146, s82, v229
	v_med3_f32 v146, v147, s82, v229
	v_mov_b32_e64 v141, v97
	v_cvt_pk_fp8_f32 v141, v133, v146
	ds_read_b128 v[146:149], v181 offset:8192
	v_cvt_pk_bf16_f32 v143, v150, v151
	v_med3_f32 v133, v152, s82, v229
	v_med3_f32 v150, v153, s82, v229
	v_cvt_pk_fp8_f32 v141, v133, v150 op_sel:[0,0,1]
	v_cvt_pk_bf16_f32 v145, v152, v153
	ds_read_b128 v[150:153], v181 offset:8208
	s_waitcnt lgkmcnt(1)
	s_nop 0
	v_mfma_f32_16x16x32_bf16 v[134:137], v[134:137], v[146:149], 0
	global_store_dwordx4 v[130:131], v[138:141], off
	s_and_b64 vcc, exec, s[8:9]
	s_waitcnt lgkmcnt(0)
	v_mfma_f32_16x16x32_bf16 v[134:137], v[142:145], v[150:153], v[134:137]
	ds_read_b128 v[138:141], v180 offset:256
	ds_read_b128 v[142:145], v180 offset:272
	ds_read_b128 v[146:149], v180 offset:288
	ds_read_b128 v[150:153], v180 offset:304
	ds_read_b128 v[154:157], v180 offset:4352
	ds_read_b128 v[184:187], v180 offset:4368
	s_waitcnt lgkmcnt(1)
	s_nop 0
	v_pk_fma_f32 v[154:155], v[138:139], v[188:189], v[154:155]
	v_lshlrev_b32_e32 v138, 16, v13
	s_nop 0
	v_and_b32_e32 v139, 0xffff0000, v13
	v_pk_mul_f32 v[138:139], v[96:97], v[138:139] op_sel_hi:[0,1]
	v_pk_fma_f32 v[156:157], v[140:141], v[138:139], v[156:157]
	v_lshlrev_b32_e32 v138, 16, v14
	s_nop 0
	v_and_b32_e32 v139, 0xffff0000, v14
	v_pk_mul_f32 v[138:139], v[96:97], v[138:139] op_sel_hi:[0,1]
	s_waitcnt lgkmcnt(0)
	s_nop 0
	v_pk_fma_f32 v[184:185], v[142:143], v[138:139], v[184:185]
	v_lshlrev_b32_e32 v138, 16, v15
	s_nop 0
	v_and_b32_e32 v139, 0xffff0000, v15
	v_med3_f32 v133, v154, s82, v229
	v_med3_f32 v143, v155, s82, v229
	v_mov_b32_e64 v142, v97
	v_pk_mul_f32 v[138:139], v[96:97], v[138:139] op_sel_hi:[0,1]
	v_cvt_pk_fp8_f32 v142, v133, v143
	v_pk_fma_f32 v[144:145], v[144:145], v[138:139], v[186:187]
	v_cvt_pk_bf16_f32 v138, v154, v155
	v_cvt_pk_bf16_f32 v139, v156, v157
	v_med3_f32 v133, v156, s82, v229
	v_med3_f32 v155, v184, s82, v229
	v_med3_f32 v156, v185, s82, v229
	v_mov_b32_e64 v143, v97
	v_cvt_pk_fp8_f32 v143, v155, v156
	v_med3_f32 v154, v157, s82, v229
	v_cvt_pk_bf16_f32 v140, v184, v185
	v_cvt_pk_fp8_f32 v142, v133, v154 op_sel:[0,0,1]
	ds_read_b128 v[154:157], v180 offset:4384
	ds_read_b128 v[184:187], v180 offset:4400
	v_cvt_pk_bf16_f32 v141, v144, v145
	v_med3_f32 v133, v144, s82, v229
	v_med3_f32 v144, v145, s82, v229
	v_cvt_pk_fp8_f32 v143, v133, v144 op_sel:[0,0,1]
	v_lshlrev_b32_e32 v144, 16, v8
	s_nop 0
	v_and_b32_e32 v145, 0xffff0000, v8
	v_pk_mul_f32 v[144:145], v[96:97], v[144:145] op_sel_hi:[0,1]
	s_waitcnt lgkmcnt(1)
	s_nop 0
	v_pk_fma_f32 v[144:145], v[146:147], v[144:145], v[154:155]
	v_lshlrev_b32_e32 v146, 16, v9
	s_nop 0
	v_and_b32_e32 v147, 0xffff0000, v9
	v_pk_mul_f32 v[146:147], v[96:97], v[146:147] op_sel_hi:[0,1]
	v_pk_fma_f32 v[154:155], v[148:149], v[146:147], v[156:157]
	v_lshlrev_b32_e32 v146, 16, v10
	s_nop 0
	v_and_b32_e32 v147, 0xffff0000, v10
	v_pk_mul_f32 v[146:147], v[96:97], v[146:147] op_sel_hi:[0,1]
	s_waitcnt lgkmcnt(0)
	s_nop 0
	v_pk_fma_f32 v[150:151], v[150:151], v[146:147], v[184:185]
	v_lshlrev_b32_e32 v146, 16, v11
	s_nop 0
	v_and_b32_e32 v147, 0xffff0000, v11
	v_pk_mul_f32 v[146:147], v[96:97], v[146:147] op_sel_hi:[0,1]
	v_pk_fma_f32 v[156:157], v[152:153], v[146:147], v[186:187]
	v_cvt_pk_bf16_f32 v146, v144, v145
	v_med3_f32 v133, v144, s82, v229
	v_med3_f32 v145, v145, s82, v229
	v_mov_b32_e64 v144, v97
	v_cvt_pk_fp8_f32 v144, v133, v145
	v_med3_f32 v133, v154, s82, v229
	v_med3_f32 v145, v155, s82, v229
	v_cvt_pk_bf16_f32 v147, v154, v155
	v_cvt_pk_fp8_f32 v144, v133, v145 op_sel:[0,0,1]
	v_med3_f32 v133, v150, s82, v229
	v_med3_f32 v154, v151, s82, v229
	v_mov_b32_e64 v145, v97
	v_cvt_pk_fp8_f32 v145, v133, v154
	v_cvt_pk_bf16_f32 v148, v150, v151
	ds_read_b128 v[150:153], v181 offset:8320
	v_med3_f32 v133, v156, s82, v229
	v_med3_f32 v183, v157, s82, v229
	v_cvt_pk_fp8_f32 v145, v133, v183 op_sel:[0,0,1]
	v_cvt_pk_bf16_f32 v149, v156, v157
	ds_read_b128 v[154:157], v181 offset:8336
	s_waitcnt lgkmcnt(1)
	s_nop 0
	v_mfma_f32_16x16x32_bf16 v[134:137], v[138:141], v[150:153], v[134:137]
	global_store_dwordx4 v[130:131], v[142:145], off offset:64
	v_lshlrev_b32_e32 v188, 16, v20
	s_waitcnt lgkmcnt(0)
	v_mfma_f32_16x16x32_bf16 v[134:137], v[146:149], v[154:157], v[134:137]
	ds_read_b128 v[138:141], v180 offset:512
	ds_read_b128 v[142:145], v180 offset:528
	ds_read_b128 v[146:149], v180 offset:544
	ds_read_b128 v[150:153], v180 offset:560
	ds_read_b128 v[154:157], v180 offset:4608
	ds_read_b128 v[184:187], v180 offset:4624
	v_and_b32_e32 v189, 0xffff0000, v20
	v_pk_mul_f32 v[188:189], v[96:97], v[188:189] op_sel_hi:[0,1]
	s_waitcnt lgkmcnt(1)
	s_nop 0
	v_pk_fma_f32 v[154:155], v[138:139], v[188:189], v[154:155]
	v_lshlrev_b32_e32 v138, 16, v21
	s_nop 0
	v_and_b32_e32 v139, 0xffff0000, v21
	v_pk_mul_f32 v[138:139], v[96:97], v[138:139] op_sel_hi:[0,1]
	v_pk_fma_f32 v[156:157], v[140:141], v[138:139], v[156:157]
	v_lshlrev_b32_e32 v138, 16, v22
	s_nop 0
	v_and_b32_e32 v139, 0xffff0000, v22
	v_pk_mul_f32 v[138:139], v[96:97], v[138:139] op_sel_hi:[0,1]
	s_waitcnt lgkmcnt(0)
	s_nop 0
	v_pk_fma_f32 v[184:185], v[142:143], v[138:139], v[184:185]
	v_lshlrev_b32_e32 v138, 16, v23
	s_nop 0
	v_and_b32_e32 v139, 0xffff0000, v23
	v_med3_f32 v133, v154, s82, v229
	v_med3_f32 v143, v155, s82, v229
	v_mov_b32_e64 v142, v97
	v_pk_mul_f32 v[138:139], v[96:97], v[138:139] op_sel_hi:[0,1]
	v_cvt_pk_fp8_f32 v142, v133, v143
	v_pk_fma_f32 v[144:145], v[144:145], v[138:139], v[186:187]
	v_cvt_pk_bf16_f32 v138, v154, v155
	v_cvt_pk_bf16_f32 v139, v156, v157
	v_med3_f32 v133, v156, s82, v229
	v_med3_f32 v155, v184, s82, v229
	v_med3_f32 v156, v185, s82, v229
	v_mov_b32_e64 v143, v97
	v_cvt_pk_fp8_f32 v143, v155, v156
	v_med3_f32 v154, v157, s82, v229
	v_cvt_pk_bf16_f32 v140, v184, v185
	v_cvt_pk_fp8_f32 v142, v133, v154 op_sel:[0,0,1]
	ds_read_b128 v[154:157], v180 offset:4640
	ds_read_b128 v[184:187], v180 offset:4656
	v_cvt_pk_bf16_f32 v141, v144, v145
	v_med3_f32 v133, v144, s82, v229
	v_med3_f32 v144, v145, s82, v229
	v_cvt_pk_fp8_f32 v143, v133, v144 op_sel:[0,0,1]
	v_lshlrev_b32_e32 v144, 16, v16
	s_nop 0
	v_and_b32_e32 v145, 0xffff0000, v16
	v_pk_mul_f32 v[144:145], v[96:97], v[144:145] op_sel_hi:[0,1]
	s_waitcnt lgkmcnt(1)
	s_nop 0
	v_pk_fma_f32 v[144:145], v[146:147], v[144:145], v[154:155]
	v_lshlrev_b32_e32 v146, 16, v17
	s_nop 0
	v_and_b32_e32 v147, 0xffff0000, v17
	v_pk_mul_f32 v[146:147], v[96:97], v[146:147] op_sel_hi:[0,1]
	v_pk_fma_f32 v[154:155], v[148:149], v[146:147], v[156:157]
	v_lshlrev_b32_e32 v146, 16, v18
	s_nop 0
	v_and_b32_e32 v147, 0xffff0000, v18
	v_pk_mul_f32 v[146:147], v[96:97], v[146:147] op_sel_hi:[0,1]
	s_waitcnt lgkmcnt(0)
	s_nop 0
	v_pk_fma_f32 v[150:151], v[150:151], v[146:147], v[184:185]
	v_lshlrev_b32_e32 v146, 16, v19
	s_nop 0
	v_and_b32_e32 v147, 0xffff0000, v19
	v_pk_mul_f32 v[146:147], v[96:97], v[146:147] op_sel_hi:[0,1]
	v_pk_fma_f32 v[156:157], v[152:153], v[146:147], v[186:187]
	v_cvt_pk_bf16_f32 v146, v144, v145
	v_med3_f32 v133, v144, s82, v229
	v_med3_f32 v145, v145, s82, v229
	v_mov_b32_e64 v144, v97
	v_cvt_pk_fp8_f32 v144, v133, v145
	v_med3_f32 v133, v154, s82, v229
	v_med3_f32 v145, v155, s82, v229
	v_cvt_pk_bf16_f32 v147, v154, v155
	v_cvt_pk_fp8_f32 v144, v133, v145 op_sel:[0,0,1]
	v_med3_f32 v133, v150, s82, v229
	v_med3_f32 v154, v151, s82, v229
	v_mov_b32_e64 v145, v97
	v_cvt_pk_fp8_f32 v145, v133, v154
	v_cvt_pk_bf16_f32 v148, v150, v151
	ds_read_b128 v[150:153], v181 offset:8448
	v_med3_f32 v133, v156, s82, v229
	v_med3_f32 v183, v157, s82, v229
	v_cvt_pk_fp8_f32 v145, v133, v183 op_sel:[0,0,1]
	v_cvt_pk_bf16_f32 v149, v156, v157
	ds_read_b128 v[154:157], v181 offset:8464
	s_waitcnt lgkmcnt(1)
	s_nop 0
	v_mfma_f32_16x16x32_bf16 v[134:137], v[138:141], v[150:153], v[134:137]
	global_store_dwordx4 v[130:131], v[142:145], off offset:128
	v_lshlrev_b32_e32 v188, 16, v28
	s_waitcnt lgkmcnt(0)
	v_mfma_f32_16x16x32_bf16 v[134:137], v[146:149], v[154:157], v[134:137]
	ds_read_b128 v[138:141], v180 offset:768
	ds_read_b128 v[142:145], v180 offset:784
	ds_read_b128 v[146:149], v180 offset:800
	ds_read_b128 v[150:153], v180 offset:816
	ds_read_b128 v[154:157], v180 offset:4864
	ds_read_b128 v[184:187], v180 offset:4880
	v_and_b32_e32 v189, 0xffff0000, v28
	v_pk_mul_f32 v[188:189], v[96:97], v[188:189] op_sel_hi:[0,1]
	s_waitcnt lgkmcnt(1)
	s_nop 0
	v_pk_fma_f32 v[154:155], v[138:139], v[188:189], v[154:155]
	v_lshlrev_b32_e32 v138, 16, v29
	s_nop 0
	v_and_b32_e32 v139, 0xffff0000, v29
	v_pk_mul_f32 v[138:139], v[96:97], v[138:139] op_sel_hi:[0,1]
	v_pk_fma_f32 v[156:157], v[140:141], v[138:139], v[156:157]
	v_lshlrev_b32_e32 v138, 16, v30
	s_nop 0
	v_and_b32_e32 v139, 0xffff0000, v30
	v_pk_mul_f32 v[138:139], v[96:97], v[138:139] op_sel_hi:[0,1]
	s_waitcnt lgkmcnt(0)
	s_nop 0
	v_pk_fma_f32 v[184:185], v[142:143], v[138:139], v[184:185]
	v_lshlrev_b32_e32 v138, 16, v31
	s_nop 0
	v_and_b32_e32 v139, 0xffff0000, v31
	v_med3_f32 v133, v154, s82, v229
	v_med3_f32 v143, v155, s82, v229
	v_mov_b32_e64 v142, v97
	v_pk_mul_f32 v[138:139], v[96:97], v[138:139] op_sel_hi:[0,1]
	v_cvt_pk_fp8_f32 v142, v133, v143
	v_pk_fma_f32 v[144:145], v[144:145], v[138:139], v[186:187]
	v_cvt_pk_bf16_f32 v138, v154, v155
	v_cvt_pk_bf16_f32 v139, v156, v157
	v_med3_f32 v133, v156, s82, v229
	v_med3_f32 v155, v184, s82, v229
	v_med3_f32 v156, v185, s82, v229
	v_mov_b32_e64 v143, v97
	v_cvt_pk_fp8_f32 v143, v155, v156
	v_med3_f32 v154, v157, s82, v229
	v_cvt_pk_bf16_f32 v140, v184, v185
	v_cvt_pk_fp8_f32 v142, v133, v154 op_sel:[0,0,1]
	ds_read_b128 v[154:157], v180 offset:4896
	ds_read_b128 v[184:187], v180 offset:4912
	v_cvt_pk_bf16_f32 v141, v144, v145
	v_med3_f32 v133, v144, s82, v229
	v_med3_f32 v144, v145, s82, v229
	v_cvt_pk_fp8_f32 v143, v133, v144 op_sel:[0,0,1]
	v_lshlrev_b32_e32 v144, 16, v24
	s_nop 0
	v_and_b32_e32 v145, 0xffff0000, v24
	v_pk_mul_f32 v[144:145], v[96:97], v[144:145] op_sel_hi:[0,1]
	s_waitcnt lgkmcnt(1)
	s_nop 0
	v_pk_fma_f32 v[144:145], v[146:147], v[144:145], v[154:155]
	v_lshlrev_b32_e32 v146, 16, v25
	s_nop 0
	v_and_b32_e32 v147, 0xffff0000, v25
	v_pk_mul_f32 v[146:147], v[96:97], v[146:147] op_sel_hi:[0,1]
	v_pk_fma_f32 v[154:155], v[148:149], v[146:147], v[156:157]
	v_lshlrev_b32_e32 v146, 16, v26
	s_nop 0
	v_and_b32_e32 v147, 0xffff0000, v26
	v_pk_mul_f32 v[146:147], v[96:97], v[146:147] op_sel_hi:[0,1]
	s_waitcnt lgkmcnt(0)
	s_nop 0
	v_pk_fma_f32 v[150:151], v[150:151], v[146:147], v[184:185]
	v_lshlrev_b32_e32 v146, 16, v27
	s_nop 0
	v_and_b32_e32 v147, 0xffff0000, v27
	v_pk_mul_f32 v[146:147], v[96:97], v[146:147] op_sel_hi:[0,1]
	v_pk_fma_f32 v[156:157], v[152:153], v[146:147], v[186:187]
	v_cvt_pk_bf16_f32 v146, v144, v145
	v_med3_f32 v133, v144, s82, v229
	v_med3_f32 v145, v145, s82, v229
	v_mov_b32_e64 v144, v97
	v_cvt_pk_fp8_f32 v144, v133, v145
	v_med3_f32 v133, v154, s82, v229
	v_med3_f32 v145, v155, s82, v229
	v_cvt_pk_bf16_f32 v147, v154, v155
	v_cvt_pk_fp8_f32 v144, v133, v145 op_sel:[0,0,1]
	v_med3_f32 v133, v150, s82, v229
	v_med3_f32 v154, v151, s82, v229
	v_mov_b32_e64 v145, v97
	v_cvt_pk_fp8_f32 v145, v133, v154
	v_cvt_pk_bf16_f32 v148, v150, v151
	ds_read_b128 v[150:153], v181 offset:8576
	v_med3_f32 v133, v156, s82, v229
	v_med3_f32 v183, v157, s82, v229
	v_cvt_pk_fp8_f32 v145, v133, v183 op_sel:[0,0,1]
	v_cvt_pk_bf16_f32 v149, v156, v157
	ds_read_b128 v[154:157], v181 offset:8592
	s_waitcnt lgkmcnt(1)
	s_nop 0
	v_mfma_f32_16x16x32_bf16 v[134:137], v[138:141], v[150:153], v[134:137]
	global_store_dwordx4 v[130:131], v[142:145], off offset:192
	v_lshlrev_b32_e32 v188, 16, v36
	s_waitcnt lgkmcnt(0)
	v_mfma_f32_16x16x32_bf16 v[134:137], v[146:149], v[154:157], v[134:137]
	ds_read_b128 v[138:141], v180 offset:1024
	ds_read_b128 v[142:145], v180 offset:1040
	ds_read_b128 v[146:149], v180 offset:1056
	ds_read_b128 v[150:153], v180 offset:1072
	ds_read_b128 v[154:157], v180 offset:5120
	ds_read_b128 v[184:187], v180 offset:5136
	v_and_b32_e32 v189, 0xffff0000, v36
	v_pk_mul_f32 v[188:189], v[96:97], v[188:189] op_sel_hi:[0,1]
	s_waitcnt lgkmcnt(1)
	s_nop 0
	v_pk_fma_f32 v[154:155], v[188:189], v[138:139], v[154:155]
	v_lshlrev_b32_e32 v138, 16, v37
	s_nop 0
	v_and_b32_e32 v139, 0xffff0000, v37
	v_pk_mul_f32 v[138:139], v[96:97], v[138:139] op_sel_hi:[0,1]
	v_pk_fma_f32 v[156:157], v[138:139], v[140:141], v[156:157]
	v_lshlrev_b32_e32 v138, 16, v38
	s_nop 0
	v_and_b32_e32 v139, 0xffff0000, v38
	v_pk_mul_f32 v[138:139], v[96:97], v[138:139] op_sel_hi:[0,1]
	s_waitcnt lgkmcnt(0)
	s_nop 0
	v_pk_fma_f32 v[184:185], v[138:139], v[142:143], v[184:185]
	v_lshlrev_b32_e32 v138, 16, v39
	s_nop 0
	v_and_b32_e32 v139, 0xffff0000, v39
	v_med3_f32 v133, v154, s82, v229
	v_med3_f32 v143, v155, s82, v229
	v_mov_b32_e64 v142, v97
	v_pk_mul_f32 v[138:139], v[96:97], v[138:139] op_sel_hi:[0,1]
	v_cvt_pk_fp8_f32 v142, v133, v143
	v_pk_fma_f32 v[144:145], v[138:139], v[144:145], v[186:187]
	v_cvt_pk_bf16_f32 v138, v154, v155
	v_cvt_pk_bf16_f32 v139, v156, v157
	v_med3_f32 v133, v156, s82, v229
	v_med3_f32 v155, v184, s82, v229
	v_med3_f32 v156, v185, s82, v229
	v_mov_b32_e64 v143, v97
	v_cvt_pk_fp8_f32 v143, v155, v156
	v_med3_f32 v154, v157, s82, v229
	v_cvt_pk_bf16_f32 v140, v184, v185
	v_cvt_pk_fp8_f32 v142, v133, v154 op_sel:[0,0,1]
	ds_read_b128 v[154:157], v180 offset:5152
	ds_read_b128 v[184:187], v180 offset:5168
	v_cvt_pk_bf16_f32 v141, v144, v145
	v_med3_f32 v133, v144, s82, v229
	v_med3_f32 v144, v145, s82, v229
	v_cvt_pk_fp8_f32 v143, v133, v144 op_sel:[0,0,1]
	v_lshlrev_b32_e32 v144, 16, v32
	s_nop 0
	v_and_b32_e32 v145, 0xffff0000, v32
	v_pk_mul_f32 v[144:145], v[96:97], v[144:145] op_sel_hi:[0,1]
	s_waitcnt lgkmcnt(1)
	s_nop 0
	v_pk_fma_f32 v[144:145], v[144:145], v[146:147], v[154:155]
	v_lshlrev_b32_e32 v146, 16, v33
	s_nop 0
	v_and_b32_e32 v147, 0xffff0000, v33
	v_pk_mul_f32 v[146:147], v[96:97], v[146:147] op_sel_hi:[0,1]
	v_pk_fma_f32 v[154:155], v[146:147], v[148:149], v[156:157]
	v_lshlrev_b32_e32 v146, 16, v34
	s_nop 0
	v_and_b32_e32 v147, 0xffff0000, v34
	v_pk_mul_f32 v[146:147], v[96:97], v[146:147] op_sel_hi:[0,1]
	s_waitcnt lgkmcnt(0)
	s_nop 0
	v_pk_fma_f32 v[150:151], v[146:147], v[150:151], v[184:185]
	v_lshlrev_b32_e32 v146, 16, v35
	s_nop 0
	v_and_b32_e32 v147, 0xffff0000, v35
	v_pk_mul_f32 v[146:147], v[96:97], v[146:147] op_sel_hi:[0,1]
	v_pk_fma_f32 v[156:157], v[146:147], v[152:153], v[186:187]
	v_cvt_pk_bf16_f32 v146, v144, v145
	v_med3_f32 v133, v144, s82, v229
	v_med3_f32 v145, v145, s82, v229
	v_mov_b32_e64 v144, v97
	v_cvt_pk_fp8_f32 v144, v133, v145
	v_med3_f32 v133, v154, s82, v229
	v_med3_f32 v145, v155, s82, v229
	v_cvt_pk_bf16_f32 v147, v154, v155
	v_cvt_pk_fp8_f32 v144, v133, v145 op_sel:[0,0,1]
	v_med3_f32 v133, v150, s82, v229
	v_med3_f32 v154, v151, s82, v229
	v_mov_b32_e64 v145, v97
	v_cvt_pk_fp8_f32 v145, v133, v154
	v_cvt_pk_bf16_f32 v148, v150, v151
	ds_read_b128 v[150:153], v181 offset:8704
	v_med3_f32 v133, v156, s82, v229
	v_med3_f32 v183, v157, s82, v229
	v_cvt_pk_fp8_f32 v145, v133, v183 op_sel:[0,0,1]
	v_cvt_pk_bf16_f32 v149, v156, v157
	ds_read_b128 v[154:157], v181 offset:8720
	s_waitcnt lgkmcnt(1)
	s_nop 0
	v_mfma_f32_16x16x32_bf16 v[134:137], v[138:141], v[150:153], v[134:137]
	global_store_dwordx4 v[130:131], v[142:145], off offset:256
	v_lshlrev_b32_e32 v188, 16, v44
	s_waitcnt lgkmcnt(0)
	v_mfma_f32_16x16x32_bf16 v[134:137], v[146:149], v[154:157], v[134:137]
	ds_read_b128 v[138:141], v180 offset:1280
	ds_read_b128 v[142:145], v180 offset:1296
	ds_read_b128 v[146:149], v180 offset:1312
	ds_read_b128 v[150:153], v180 offset:1328
	ds_read_b128 v[154:157], v180 offset:5376
	ds_read_b128 v[184:187], v180 offset:5392
	v_and_b32_e32 v189, 0xffff0000, v44
	v_pk_mul_f32 v[188:189], v[96:97], v[188:189] op_sel_hi:[0,1]
	s_waitcnt lgkmcnt(1)
	s_nop 0
	v_pk_fma_f32 v[154:155], v[188:189], v[138:139], v[154:155]
	v_lshlrev_b32_e32 v138, 16, v45
	s_nop 0
	v_and_b32_e32 v139, 0xffff0000, v45
	v_pk_mul_f32 v[138:139], v[96:97], v[138:139] op_sel_hi:[0,1]
	v_pk_fma_f32 v[156:157], v[138:139], v[140:141], v[156:157]
	v_lshlrev_b32_e32 v138, 16, v46
	s_nop 0
	v_and_b32_e32 v139, 0xffff0000, v46
	v_pk_mul_f32 v[138:139], v[96:97], v[138:139] op_sel_hi:[0,1]
	s_waitcnt lgkmcnt(0)
	s_nop 0
	v_pk_fma_f32 v[184:185], v[138:139], v[142:143], v[184:185]
	v_lshlrev_b32_e32 v138, 16, v47
	s_nop 0
	v_and_b32_e32 v139, 0xffff0000, v47
	v_med3_f32 v133, v154, s82, v229
	v_med3_f32 v143, v155, s82, v229
	v_mov_b32_e64 v142, v97
	v_pk_mul_f32 v[138:139], v[96:97], v[138:139] op_sel_hi:[0,1]
	v_cvt_pk_fp8_f32 v142, v133, v143
	v_pk_fma_f32 v[144:145], v[138:139], v[144:145], v[186:187]
	v_cvt_pk_bf16_f32 v138, v154, v155
	v_cvt_pk_bf16_f32 v139, v156, v157
	v_med3_f32 v133, v156, s82, v229
	v_med3_f32 v155, v184, s82, v229
	v_med3_f32 v156, v185, s82, v229
	v_mov_b32_e64 v143, v97
	v_cvt_pk_fp8_f32 v143, v155, v156
	v_med3_f32 v154, v157, s82, v229
	v_cvt_pk_bf16_f32 v140, v184, v185
	v_cvt_pk_fp8_f32 v142, v133, v154 op_sel:[0,0,1]
	ds_read_b128 v[154:157], v180 offset:5408
	ds_read_b128 v[184:187], v180 offset:5424
	v_cvt_pk_bf16_f32 v141, v144, v145
	v_med3_f32 v133, v144, s82, v229
	v_med3_f32 v144, v145, s82, v229
	v_cvt_pk_fp8_f32 v143, v133, v144 op_sel:[0,0,1]
	v_lshlrev_b32_e32 v144, 16, v40
	s_nop 0
	v_and_b32_e32 v145, 0xffff0000, v40
	v_pk_mul_f32 v[144:145], v[96:97], v[144:145] op_sel_hi:[0,1]
	s_waitcnt lgkmcnt(1)
	s_nop 0
	v_pk_fma_f32 v[144:145], v[144:145], v[146:147], v[154:155]
	v_lshlrev_b32_e32 v146, 16, v41
	s_nop 0
	v_and_b32_e32 v147, 0xffff0000, v41
	v_pk_mul_f32 v[146:147], v[96:97], v[146:147] op_sel_hi:[0,1]
	v_pk_fma_f32 v[154:155], v[146:147], v[148:149], v[156:157]
	v_lshlrev_b32_e32 v146, 16, v42
	s_nop 0
	v_and_b32_e32 v147, 0xffff0000, v42
	v_pk_mul_f32 v[146:147], v[96:97], v[146:147] op_sel_hi:[0,1]
	s_waitcnt lgkmcnt(0)
	s_nop 0
	v_pk_fma_f32 v[150:151], v[146:147], v[150:151], v[184:185]
	v_lshlrev_b32_e32 v146, 16, v43
	s_nop 0
	v_and_b32_e32 v147, 0xffff0000, v43
	v_pk_mul_f32 v[146:147], v[96:97], v[146:147] op_sel_hi:[0,1]
	v_pk_fma_f32 v[156:157], v[146:147], v[152:153], v[186:187]
	v_cvt_pk_bf16_f32 v146, v144, v145
	v_med3_f32 v133, v144, s82, v229
	v_med3_f32 v145, v145, s82, v229
	v_mov_b32_e64 v144, v97
	v_cvt_pk_fp8_f32 v144, v133, v145
	v_med3_f32 v133, v154, s82, v229
	v_med3_f32 v145, v155, s82, v229
	v_cvt_pk_bf16_f32 v147, v154, v155
	v_cvt_pk_fp8_f32 v144, v133, v145 op_sel:[0,0,1]
	v_med3_f32 v133, v150, s82, v229
	v_med3_f32 v154, v151, s82, v229
	v_mov_b32_e64 v145, v97
	v_cvt_pk_fp8_f32 v145, v133, v154
	v_cvt_pk_bf16_f32 v148, v150, v151
	ds_read_b128 v[150:153], v181 offset:8832
	v_med3_f32 v133, v156, s82, v229
	v_med3_f32 v183, v157, s82, v229
	v_cvt_pk_fp8_f32 v145, v133, v183 op_sel:[0,0,1]
	v_cvt_pk_bf16_f32 v149, v156, v157
	ds_read_b128 v[154:157], v181 offset:8848
	s_waitcnt lgkmcnt(1)
	s_nop 0
	v_mfma_f32_16x16x32_bf16 v[134:137], v[138:141], v[150:153], v[134:137]
	global_store_dwordx4 v[130:131], v[142:145], off offset:320
	v_lshlrev_b32_e32 v188, 16, v52
	s_waitcnt lgkmcnt(0)
	v_mfma_f32_16x16x32_bf16 v[134:137], v[146:149], v[154:157], v[134:137]
	ds_read_b128 v[138:141], v180 offset:1536
	ds_read_b128 v[142:145], v180 offset:1552
	ds_read_b128 v[146:149], v180 offset:1568
	ds_read_b128 v[150:153], v180 offset:1584
	ds_read_b128 v[154:157], v180 offset:5632
	ds_read_b128 v[184:187], v180 offset:5648
	v_and_b32_e32 v189, 0xffff0000, v52
	v_pk_mul_f32 v[188:189], v[96:97], v[188:189] op_sel_hi:[0,1]
	s_waitcnt lgkmcnt(1)
	s_nop 0
	v_pk_fma_f32 v[154:155], v[188:189], v[138:139], v[154:155]
	v_lshlrev_b32_e32 v138, 16, v53
	s_nop 0
	v_and_b32_e32 v139, 0xffff0000, v53
	v_pk_mul_f32 v[138:139], v[96:97], v[138:139] op_sel_hi:[0,1]
	v_pk_fma_f32 v[156:157], v[138:139], v[140:141], v[156:157]
	v_lshlrev_b32_e32 v138, 16, v54
	s_nop 0
	v_and_b32_e32 v139, 0xffff0000, v54
	v_pk_mul_f32 v[138:139], v[96:97], v[138:139] op_sel_hi:[0,1]
	s_waitcnt lgkmcnt(0)
	s_nop 0
	v_pk_fma_f32 v[184:185], v[138:139], v[142:143], v[184:185]
	v_lshlrev_b32_e32 v138, 16, v55
	s_nop 0
	v_and_b32_e32 v139, 0xffff0000, v55
	v_med3_f32 v133, v154, s82, v229
	v_med3_f32 v143, v155, s82, v229
	v_mov_b32_e64 v142, v97
	v_pk_mul_f32 v[138:139], v[96:97], v[138:139] op_sel_hi:[0,1]
	v_cvt_pk_fp8_f32 v142, v133, v143
	v_pk_fma_f32 v[144:145], v[138:139], v[144:145], v[186:187]
	v_cvt_pk_bf16_f32 v138, v154, v155
	v_cvt_pk_bf16_f32 v139, v156, v157
	v_med3_f32 v133, v156, s82, v229
	v_med3_f32 v155, v184, s82, v229
	v_med3_f32 v156, v185, s82, v229
	v_mov_b32_e64 v143, v97
	v_cvt_pk_fp8_f32 v143, v155, v156
	v_med3_f32 v154, v157, s82, v229
	v_cvt_pk_bf16_f32 v140, v184, v185
	v_cvt_pk_fp8_f32 v142, v133, v154 op_sel:[0,0,1]
	ds_read_b128 v[154:157], v180 offset:5664
	ds_read_b128 v[184:187], v180 offset:5680
	v_cvt_pk_bf16_f32 v141, v144, v145
	v_med3_f32 v133, v144, s82, v229
	v_med3_f32 v144, v145, s82, v229
	v_cvt_pk_fp8_f32 v143, v133, v144 op_sel:[0,0,1]
	v_lshlrev_b32_e32 v144, 16, v48
	s_nop 0
	v_and_b32_e32 v145, 0xffff0000, v48
	v_pk_mul_f32 v[144:145], v[96:97], v[144:145] op_sel_hi:[0,1]
	s_waitcnt lgkmcnt(1)
	s_nop 0
	v_pk_fma_f32 v[144:145], v[144:145], v[146:147], v[154:155]
	v_lshlrev_b32_e32 v146, 16, v49
	s_nop 0
	v_and_b32_e32 v147, 0xffff0000, v49
	v_pk_mul_f32 v[146:147], v[96:97], v[146:147] op_sel_hi:[0,1]
	v_pk_fma_f32 v[154:155], v[146:147], v[148:149], v[156:157]
	v_lshlrev_b32_e32 v146, 16, v50
	s_nop 0
	v_and_b32_e32 v147, 0xffff0000, v50
	v_pk_mul_f32 v[146:147], v[96:97], v[146:147] op_sel_hi:[0,1]
	s_waitcnt lgkmcnt(0)
	s_nop 0
	v_pk_fma_f32 v[150:151], v[146:147], v[150:151], v[184:185]
	v_lshlrev_b32_e32 v146, 16, v51
	s_nop 0
	v_and_b32_e32 v147, 0xffff0000, v51
	v_pk_mul_f32 v[146:147], v[96:97], v[146:147] op_sel_hi:[0,1]
	v_pk_fma_f32 v[156:157], v[146:147], v[152:153], v[186:187]
	v_cvt_pk_bf16_f32 v146, v144, v145
	v_med3_f32 v133, v144, s82, v229
	v_med3_f32 v145, v145, s82, v229
	v_mov_b32_e64 v144, v97
	v_cvt_pk_fp8_f32 v144, v133, v145
	v_med3_f32 v133, v154, s82, v229
	v_med3_f32 v145, v155, s82, v229
	v_cvt_pk_bf16_f32 v147, v154, v155
	v_cvt_pk_fp8_f32 v144, v133, v145 op_sel:[0,0,1]
	v_med3_f32 v133, v150, s82, v229
	v_med3_f32 v154, v151, s82, v229
	v_mov_b32_e64 v145, v97
	v_cvt_pk_fp8_f32 v145, v133, v154
	v_cvt_pk_bf16_f32 v148, v150, v151
	ds_read_b128 v[150:153], v181 offset:8960
	v_med3_f32 v133, v156, s82, v229
	v_med3_f32 v183, v157, s82, v229
	v_cvt_pk_fp8_f32 v145, v133, v183 op_sel:[0,0,1]
	v_cvt_pk_bf16_f32 v149, v156, v157
	ds_read_b128 v[154:157], v181 offset:8976
	s_waitcnt lgkmcnt(1)
	s_nop 0
	v_mfma_f32_16x16x32_bf16 v[134:137], v[138:141], v[150:153], v[134:137]
	global_store_dwordx4 v[130:131], v[142:145], off offset:384
	v_lshlrev_b32_e32 v188, 16, v60
	s_waitcnt lgkmcnt(0)
	v_mfma_f32_16x16x32_bf16 v[134:137], v[146:149], v[154:157], v[134:137]
	ds_read_b128 v[138:141], v180 offset:1792
	ds_read_b128 v[142:145], v180 offset:1808
	ds_read_b128 v[146:149], v180 offset:1824
	ds_read_b128 v[150:153], v180 offset:1840
	ds_read_b128 v[154:157], v180 offset:5888
	ds_read_b128 v[184:187], v180 offset:5904
	v_and_b32_e32 v189, 0xffff0000, v60
	v_pk_mul_f32 v[188:189], v[96:97], v[188:189] op_sel_hi:[0,1]
	s_waitcnt lgkmcnt(1)
	s_nop 0
	v_pk_fma_f32 v[154:155], v[188:189], v[138:139], v[154:155]
	v_lshlrev_b32_e32 v138, 16, v61
	s_nop 0
	v_and_b32_e32 v139, 0xffff0000, v61
	v_pk_mul_f32 v[138:139], v[96:97], v[138:139] op_sel_hi:[0,1]
	v_pk_fma_f32 v[156:157], v[138:139], v[140:141], v[156:157]
	v_lshlrev_b32_e32 v138, 16, v62
	s_nop 0
	v_and_b32_e32 v139, 0xffff0000, v62
	v_pk_mul_f32 v[138:139], v[96:97], v[138:139] op_sel_hi:[0,1]
	s_waitcnt lgkmcnt(0)
	s_nop 0
	v_pk_fma_f32 v[184:185], v[138:139], v[142:143], v[184:185]
	v_lshlrev_b32_e32 v138, 16, v63
	s_nop 0
	v_and_b32_e32 v139, 0xffff0000, v63
	v_med3_f32 v133, v154, s82, v229
	v_med3_f32 v143, v155, s82, v229
	v_mov_b32_e64 v142, v97
	v_pk_mul_f32 v[138:139], v[96:97], v[138:139] op_sel_hi:[0,1]
	v_cvt_pk_fp8_f32 v142, v133, v143
	v_pk_fma_f32 v[144:145], v[138:139], v[144:145], v[186:187]
	v_cvt_pk_bf16_f32 v138, v154, v155
	v_cvt_pk_bf16_f32 v139, v156, v157
	v_med3_f32 v133, v156, s82, v229
	v_med3_f32 v155, v184, s82, v229
	v_med3_f32 v156, v185, s82, v229
	v_mov_b32_e64 v143, v97
	v_cvt_pk_fp8_f32 v143, v155, v156
	v_med3_f32 v154, v157, s82, v229
	v_cvt_pk_bf16_f32 v140, v184, v185
	v_cvt_pk_fp8_f32 v142, v133, v154 op_sel:[0,0,1]
	ds_read_b128 v[154:157], v180 offset:5920
	ds_read_b128 v[184:187], v180 offset:5936
	v_cvt_pk_bf16_f32 v141, v144, v145
	v_med3_f32 v133, v144, s82, v229
	v_med3_f32 v144, v145, s82, v229
	v_cvt_pk_fp8_f32 v143, v133, v144 op_sel:[0,0,1]
	v_lshlrev_b32_e32 v144, 16, v56
	s_nop 0
	v_and_b32_e32 v145, 0xffff0000, v56
	v_pk_mul_f32 v[144:145], v[96:97], v[144:145] op_sel_hi:[0,1]
	s_waitcnt lgkmcnt(1)
	s_nop 0
	v_pk_fma_f32 v[144:145], v[144:145], v[146:147], v[154:155]
	v_lshlrev_b32_e32 v146, 16, v57
	s_nop 0
	v_and_b32_e32 v147, 0xffff0000, v57
	v_pk_mul_f32 v[146:147], v[96:97], v[146:147] op_sel_hi:[0,1]
	v_pk_fma_f32 v[154:155], v[146:147], v[148:149], v[156:157]
	v_lshlrev_b32_e32 v146, 16, v58
	s_nop 0
	v_and_b32_e32 v147, 0xffff0000, v58
	v_pk_mul_f32 v[146:147], v[96:97], v[146:147] op_sel_hi:[0,1]
	s_waitcnt lgkmcnt(0)
	s_nop 0
	v_pk_fma_f32 v[150:151], v[146:147], v[150:151], v[184:185]
	v_lshlrev_b32_e32 v146, 16, v59
	s_nop 0
	v_and_b32_e32 v147, 0xffff0000, v59
	v_pk_mul_f32 v[146:147], v[96:97], v[146:147] op_sel_hi:[0,1]
	v_pk_fma_f32 v[156:157], v[146:147], v[152:153], v[186:187]
	v_cvt_pk_bf16_f32 v146, v144, v145
	v_med3_f32 v133, v144, s82, v229
	v_med3_f32 v145, v145, s82, v229
	v_mov_b32_e64 v144, v97
	v_cvt_pk_fp8_f32 v144, v133, v145
	v_med3_f32 v133, v154, s82, v229
	v_med3_f32 v145, v155, s82, v229
	v_cvt_pk_bf16_f32 v147, v154, v155
	v_cvt_pk_fp8_f32 v144, v133, v145 op_sel:[0,0,1]
	v_med3_f32 v133, v150, s82, v229
	v_med3_f32 v154, v151, s82, v229
	v_mov_b32_e64 v145, v97
	v_cvt_pk_fp8_f32 v145, v133, v154
	v_cvt_pk_bf16_f32 v148, v150, v151
	ds_read_b128 v[150:153], v181 offset:9088
	v_med3_f32 v133, v156, s82, v229
	v_med3_f32 v183, v157, s82, v229
	v_cvt_pk_fp8_f32 v145, v133, v183 op_sel:[0,0,1]
	v_cvt_pk_bf16_f32 v149, v156, v157
	ds_read_b128 v[154:157], v181 offset:9104
	s_waitcnt lgkmcnt(1)
	s_nop 0
	v_mfma_f32_16x16x32_bf16 v[134:137], v[138:141], v[150:153], v[134:137]
	global_store_dwordx4 v[130:131], v[142:145], off offset:448
	v_lshlrev_b32_e32 v188, 16, v68
	s_waitcnt lgkmcnt(0)
	v_mfma_f32_16x16x32_bf16 v[134:137], v[146:149], v[154:157], v[134:137]
	ds_read_b128 v[138:141], v180 offset:2048
	ds_read_b128 v[142:145], v180 offset:2064
	ds_read_b128 v[146:149], v180 offset:2080
	ds_read_b128 v[150:153], v180 offset:2096
	ds_read_b128 v[154:157], v180 offset:6144
	ds_read_b128 v[184:187], v180 offset:6160
	v_and_b32_e32 v189, 0xffff0000, v68
	v_pk_mul_f32 v[188:189], v[96:97], v[188:189] op_sel_hi:[0,1]
	s_waitcnt lgkmcnt(1)
	s_nop 0
	v_pk_fma_f32 v[154:155], v[188:189], v[138:139], v[154:155]
	v_lshlrev_b32_e32 v138, 16, v69
	s_nop 0
	v_and_b32_e32 v139, 0xffff0000, v69
	v_pk_mul_f32 v[138:139], v[96:97], v[138:139] op_sel_hi:[0,1]
	v_pk_fma_f32 v[156:157], v[138:139], v[140:141], v[156:157]
	v_lshlrev_b32_e32 v138, 16, v70
	s_nop 0
	v_and_b32_e32 v139, 0xffff0000, v70
	v_pk_mul_f32 v[138:139], v[96:97], v[138:139] op_sel_hi:[0,1]
	s_waitcnt lgkmcnt(0)
	s_nop 0
	v_pk_fma_f32 v[184:185], v[138:139], v[142:143], v[184:185]
	v_lshlrev_b32_e32 v138, 16, v71
	s_nop 0
	v_and_b32_e32 v139, 0xffff0000, v71
	v_med3_f32 v133, v154, s82, v229
	v_med3_f32 v143, v155, s82, v229
	v_mov_b32_e64 v142, v97
	v_pk_mul_f32 v[138:139], v[96:97], v[138:139] op_sel_hi:[0,1]
	v_cvt_pk_fp8_f32 v142, v133, v143
	v_pk_fma_f32 v[144:145], v[138:139], v[144:145], v[186:187]
	v_cvt_pk_bf16_f32 v138, v154, v155
	v_cvt_pk_bf16_f32 v139, v156, v157
	v_med3_f32 v133, v156, s82, v229
	v_med3_f32 v155, v184, s82, v229
	v_med3_f32 v156, v185, s82, v229
	v_mov_b32_e64 v143, v97
	v_cvt_pk_fp8_f32 v143, v155, v156
	v_med3_f32 v154, v157, s82, v229
	v_cvt_pk_bf16_f32 v140, v184, v185
	v_cvt_pk_fp8_f32 v142, v133, v154 op_sel:[0,0,1]
	ds_read_b128 v[154:157], v180 offset:6176
	ds_read_b128 v[184:187], v180 offset:6192
	v_cvt_pk_bf16_f32 v141, v144, v145
	v_med3_f32 v133, v144, s82, v229
	v_med3_f32 v144, v145, s82, v229
	v_cvt_pk_fp8_f32 v143, v133, v144 op_sel:[0,0,1]
	v_lshlrev_b32_e32 v144, 16, v64
	s_nop 0
	v_and_b32_e32 v145, 0xffff0000, v64
	v_pk_mul_f32 v[144:145], v[96:97], v[144:145] op_sel_hi:[0,1]
	s_waitcnt lgkmcnt(1)
	s_nop 0
	v_pk_fma_f32 v[144:145], v[144:145], v[146:147], v[154:155]
	v_lshlrev_b32_e32 v146, 16, v65
	s_nop 0
	v_and_b32_e32 v147, 0xffff0000, v65
	v_pk_mul_f32 v[146:147], v[96:97], v[146:147] op_sel_hi:[0,1]
	v_pk_fma_f32 v[154:155], v[146:147], v[148:149], v[156:157]
	v_lshlrev_b32_e32 v146, 16, v66
	s_nop 0
	v_and_b32_e32 v147, 0xffff0000, v66
	v_pk_mul_f32 v[146:147], v[96:97], v[146:147] op_sel_hi:[0,1]
	s_waitcnt lgkmcnt(0)
	s_nop 0
	v_pk_fma_f32 v[150:151], v[146:147], v[150:151], v[184:185]
	v_lshlrev_b32_e32 v146, 16, v67
	s_nop 0
	v_and_b32_e32 v147, 0xffff0000, v67
	v_pk_mul_f32 v[146:147], v[96:97], v[146:147] op_sel_hi:[0,1]
	v_pk_fma_f32 v[156:157], v[146:147], v[152:153], v[186:187]
	v_cvt_pk_bf16_f32 v146, v144, v145
	v_med3_f32 v133, v144, s82, v229
	v_med3_f32 v145, v145, s82, v229
	v_mov_b32_e64 v144, v97
	v_cvt_pk_fp8_f32 v144, v133, v145
	v_med3_f32 v133, v154, s82, v229
	v_med3_f32 v145, v155, s82, v229
	v_cvt_pk_bf16_f32 v147, v154, v155
	v_cvt_pk_fp8_f32 v144, v133, v145 op_sel:[0,0,1]
	v_med3_f32 v133, v150, s82, v229
	v_med3_f32 v154, v151, s82, v229
	v_mov_b32_e64 v145, v97
	v_cvt_pk_fp8_f32 v145, v133, v154
	v_cvt_pk_bf16_f32 v148, v150, v151
	ds_read_b128 v[150:153], v181 offset:9216
	v_med3_f32 v133, v156, s82, v229
	v_med3_f32 v183, v157, s82, v229
	v_cvt_pk_fp8_f32 v145, v133, v183 op_sel:[0,0,1]
	v_cvt_pk_bf16_f32 v149, v156, v157
	ds_read_b128 v[154:157], v181 offset:9232
	s_waitcnt lgkmcnt(1)
	s_nop 0
	v_mfma_f32_16x16x32_bf16 v[134:137], v[138:141], v[150:153], v[134:137]
	global_store_dwordx4 v[130:131], v[142:145], off offset:512
	v_lshlrev_b32_e32 v188, 16, v76
	s_waitcnt lgkmcnt(0)
	v_mfma_f32_16x16x32_bf16 v[134:137], v[146:149], v[154:157], v[134:137]
	ds_read_b128 v[138:141], v180 offset:2304
	ds_read_b128 v[142:145], v180 offset:2320
	ds_read_b128 v[146:149], v180 offset:2336
	ds_read_b128 v[150:153], v180 offset:2352
	ds_read_b128 v[154:157], v180 offset:6400
	ds_read_b128 v[184:187], v180 offset:6416
	v_and_b32_e32 v189, 0xffff0000, v76
	v_pk_mul_f32 v[188:189], v[96:97], v[188:189] op_sel_hi:[0,1]
	s_waitcnt lgkmcnt(1)
	s_nop 0
	v_pk_fma_f32 v[154:155], v[188:189], v[138:139], v[154:155]
	v_lshlrev_b32_e32 v138, 16, v77
	s_nop 0
	v_and_b32_e32 v139, 0xffff0000, v77
	v_pk_mul_f32 v[138:139], v[96:97], v[138:139] op_sel_hi:[0,1]
	v_pk_fma_f32 v[156:157], v[138:139], v[140:141], v[156:157]
	v_lshlrev_b32_e32 v138, 16, v78
	s_nop 0
	v_and_b32_e32 v139, 0xffff0000, v78
	v_pk_mul_f32 v[138:139], v[96:97], v[138:139] op_sel_hi:[0,1]
	s_waitcnt lgkmcnt(0)
	s_nop 0
	v_pk_fma_f32 v[184:185], v[138:139], v[142:143], v[184:185]
	v_lshlrev_b32_e32 v138, 16, v79
	s_nop 0
	v_and_b32_e32 v139, 0xffff0000, v79
	v_med3_f32 v133, v154, s82, v229
	v_med3_f32 v143, v155, s82, v229
	v_mov_b32_e64 v142, v97
	v_pk_mul_f32 v[138:139], v[96:97], v[138:139] op_sel_hi:[0,1]
	v_cvt_pk_fp8_f32 v142, v133, v143
	v_pk_fma_f32 v[144:145], v[138:139], v[144:145], v[186:187]
	v_cvt_pk_bf16_f32 v138, v154, v155
	v_cvt_pk_bf16_f32 v139, v156, v157
	v_med3_f32 v133, v156, s82, v229
	v_med3_f32 v155, v184, s82, v229
	v_med3_f32 v156, v185, s82, v229
	v_mov_b32_e64 v143, v97
	v_cvt_pk_fp8_f32 v143, v155, v156
	v_med3_f32 v154, v157, s82, v229
	v_cvt_pk_bf16_f32 v140, v184, v185
	v_cvt_pk_fp8_f32 v142, v133, v154 op_sel:[0,0,1]
	ds_read_b128 v[154:157], v180 offset:6432
	ds_read_b128 v[184:187], v180 offset:6448
	v_cvt_pk_bf16_f32 v141, v144, v145
	v_med3_f32 v133, v144, s82, v229
	v_med3_f32 v144, v145, s82, v229
	v_cvt_pk_fp8_f32 v143, v133, v144 op_sel:[0,0,1]
	v_lshlrev_b32_e32 v144, 16, v72
	s_nop 0
	v_and_b32_e32 v145, 0xffff0000, v72
	v_pk_mul_f32 v[144:145], v[96:97], v[144:145] op_sel_hi:[0,1]
	s_waitcnt lgkmcnt(1)
	s_nop 0
	v_pk_fma_f32 v[144:145], v[144:145], v[146:147], v[154:155]
	v_lshlrev_b32_e32 v146, 16, v73
	s_nop 0
	v_and_b32_e32 v147, 0xffff0000, v73
	v_pk_mul_f32 v[146:147], v[96:97], v[146:147] op_sel_hi:[0,1]
	v_pk_fma_f32 v[154:155], v[146:147], v[148:149], v[156:157]
	v_lshlrev_b32_e32 v146, 16, v74
	s_nop 0
	v_and_b32_e32 v147, 0xffff0000, v74
	v_pk_mul_f32 v[146:147], v[96:97], v[146:147] op_sel_hi:[0,1]
	s_waitcnt lgkmcnt(0)
	s_nop 0
	v_pk_fma_f32 v[150:151], v[146:147], v[150:151], v[184:185]
	v_lshlrev_b32_e32 v146, 16, v75
	s_nop 0
	v_and_b32_e32 v147, 0xffff0000, v75
	v_pk_mul_f32 v[146:147], v[96:97], v[146:147] op_sel_hi:[0,1]
	v_pk_fma_f32 v[156:157], v[146:147], v[152:153], v[186:187]
	v_cvt_pk_bf16_f32 v146, v144, v145
	v_med3_f32 v133, v144, s82, v229
	v_med3_f32 v145, v145, s82, v229
	v_mov_b32_e64 v144, v97
	v_cvt_pk_fp8_f32 v144, v133, v145
	v_med3_f32 v133, v154, s82, v229
	v_med3_f32 v145, v155, s82, v229
	v_cvt_pk_bf16_f32 v147, v154, v155
	v_cvt_pk_fp8_f32 v144, v133, v145 op_sel:[0,0,1]
	v_med3_f32 v133, v150, s82, v229
	v_med3_f32 v154, v151, s82, v229
	v_mov_b32_e64 v145, v97
	v_cvt_pk_fp8_f32 v145, v133, v154
	v_cvt_pk_bf16_f32 v148, v150, v151
	ds_read_b128 v[150:153], v181 offset:9344
	v_med3_f32 v133, v156, s82, v229
	v_med3_f32 v183, v157, s82, v229
	v_cvt_pk_fp8_f32 v145, v133, v183 op_sel:[0,0,1]
	v_cvt_pk_bf16_f32 v149, v156, v157
	ds_read_b128 v[154:157], v181 offset:9360
	s_waitcnt lgkmcnt(1)
	s_nop 0
	v_mfma_f32_16x16x32_bf16 v[134:137], v[138:141], v[150:153], v[134:137]
	global_store_dwordx4 v[130:131], v[142:145], off offset:576
	v_lshlrev_b32_e32 v188, 16, v84
	s_waitcnt lgkmcnt(0)
	v_mfma_f32_16x16x32_bf16 v[134:137], v[146:149], v[154:157], v[134:137]
	ds_read_b128 v[138:141], v180 offset:2560
	ds_read_b128 v[142:145], v180 offset:2576
	ds_read_b128 v[146:149], v180 offset:2592
	ds_read_b128 v[150:153], v180 offset:2608
	ds_read_b128 v[154:157], v180 offset:6656
	ds_read_b128 v[184:187], v180 offset:6672
	v_and_b32_e32 v189, 0xffff0000, v84
	v_pk_mul_f32 v[188:189], v[96:97], v[188:189] op_sel_hi:[0,1]
	s_waitcnt lgkmcnt(1)
	s_nop 0
	v_pk_fma_f32 v[154:155], v[188:189], v[138:139], v[154:155]
	v_lshlrev_b32_e32 v138, 16, v85
	s_nop 0
	v_and_b32_e32 v139, 0xffff0000, v85
	v_pk_mul_f32 v[138:139], v[96:97], v[138:139] op_sel_hi:[0,1]
	v_pk_fma_f32 v[156:157], v[138:139], v[140:141], v[156:157]
	v_lshlrev_b32_e32 v138, 16, v86
	s_nop 0
	v_and_b32_e32 v139, 0xffff0000, v86
	v_pk_mul_f32 v[138:139], v[96:97], v[138:139] op_sel_hi:[0,1]
	s_waitcnt lgkmcnt(0)
	s_nop 0
	v_pk_fma_f32 v[184:185], v[138:139], v[142:143], v[184:185]
	v_lshlrev_b32_e32 v138, 16, v87
	s_nop 0
	v_and_b32_e32 v139, 0xffff0000, v87
	v_med3_f32 v133, v154, s82, v229
	v_med3_f32 v143, v155, s82, v229
	v_mov_b32_e64 v142, v97
	v_pk_mul_f32 v[138:139], v[96:97], v[138:139] op_sel_hi:[0,1]
	v_cvt_pk_fp8_f32 v142, v133, v143
	v_pk_fma_f32 v[144:145], v[138:139], v[144:145], v[186:187]
	v_cvt_pk_bf16_f32 v138, v154, v155
	v_cvt_pk_bf16_f32 v139, v156, v157
	v_med3_f32 v133, v156, s82, v229
	v_med3_f32 v155, v184, s82, v229
	v_med3_f32 v156, v185, s82, v229
	v_mov_b32_e64 v143, v97
	v_cvt_pk_fp8_f32 v143, v155, v156
	v_med3_f32 v154, v157, s82, v229
	v_cvt_pk_bf16_f32 v140, v184, v185
	v_cvt_pk_fp8_f32 v142, v133, v154 op_sel:[0,0,1]
	ds_read_b128 v[154:157], v180 offset:6688
	ds_read_b128 v[184:187], v180 offset:6704
	v_cvt_pk_bf16_f32 v141, v144, v145
	v_med3_f32 v133, v144, s82, v229
	v_med3_f32 v144, v145, s82, v229
	v_cvt_pk_fp8_f32 v143, v133, v144 op_sel:[0,0,1]
	v_lshlrev_b32_e32 v144, 16, v80
	s_nop 0
	v_and_b32_e32 v145, 0xffff0000, v80
	v_pk_mul_f32 v[144:145], v[96:97], v[144:145] op_sel_hi:[0,1]
	s_waitcnt lgkmcnt(1)
	s_nop 0
	v_pk_fma_f32 v[144:145], v[144:145], v[146:147], v[154:155]
	v_lshlrev_b32_e32 v146, 16, v81
	s_nop 0
	v_and_b32_e32 v147, 0xffff0000, v81
	v_pk_mul_f32 v[146:147], v[96:97], v[146:147] op_sel_hi:[0,1]
	v_pk_fma_f32 v[154:155], v[146:147], v[148:149], v[156:157]
	v_lshlrev_b32_e32 v146, 16, v82
	s_nop 0
	v_and_b32_e32 v147, 0xffff0000, v82
	v_pk_mul_f32 v[146:147], v[96:97], v[146:147] op_sel_hi:[0,1]
	s_waitcnt lgkmcnt(0)
	s_nop 0
	v_pk_fma_f32 v[150:151], v[146:147], v[150:151], v[184:185]
	v_lshlrev_b32_e32 v146, 16, v83
	s_nop 0
	v_and_b32_e32 v147, 0xffff0000, v83
	v_pk_mul_f32 v[146:147], v[96:97], v[146:147] op_sel_hi:[0,1]
	v_pk_fma_f32 v[156:157], v[146:147], v[152:153], v[186:187]
	v_cvt_pk_bf16_f32 v146, v144, v145
	v_med3_f32 v133, v144, s82, v229
	v_med3_f32 v145, v145, s82, v229
	v_mov_b32_e64 v144, v97
	v_cvt_pk_fp8_f32 v144, v133, v145
	v_med3_f32 v133, v154, s82, v229
	v_med3_f32 v145, v155, s82, v229
	v_cvt_pk_bf16_f32 v147, v154, v155
	v_cvt_pk_fp8_f32 v144, v133, v145 op_sel:[0,0,1]
	v_med3_f32 v133, v150, s82, v229
	v_med3_f32 v154, v151, s82, v229
	v_mov_b32_e64 v145, v97
	v_cvt_pk_fp8_f32 v145, v133, v154
	v_cvt_pk_bf16_f32 v148, v150, v151
	ds_read_b128 v[150:153], v181 offset:9472
	v_med3_f32 v133, v156, s82, v229
	v_med3_f32 v183, v157, s82, v229
	v_cvt_pk_fp8_f32 v145, v133, v183 op_sel:[0,0,1]
	v_cvt_pk_bf16_f32 v149, v156, v157
	ds_read_b128 v[154:157], v181 offset:9488
	s_waitcnt lgkmcnt(1)
	s_nop 0
	v_mfma_f32_16x16x32_bf16 v[134:137], v[138:141], v[150:153], v[134:137]
	global_store_dwordx4 v[130:131], v[142:145], off offset:640
	v_lshlrev_b32_e32 v188, 16, v92
	s_waitcnt lgkmcnt(0)
	v_mfma_f32_16x16x32_bf16 v[134:137], v[146:149], v[154:157], v[134:137]
	ds_read_b128 v[138:141], v180 offset:2816
	ds_read_b128 v[142:145], v180 offset:2832
	ds_read_b128 v[146:149], v180 offset:2848
	ds_read_b128 v[150:153], v180 offset:2864
	ds_read_b128 v[154:157], v180 offset:6912
	ds_read_b128 v[184:187], v180 offset:6928
	v_and_b32_e32 v189, 0xffff0000, v92
	v_pk_mul_f32 v[188:189], v[96:97], v[188:189] op_sel_hi:[0,1]
	s_waitcnt lgkmcnt(1)
	s_nop 0
	v_pk_fma_f32 v[154:155], v[188:189], v[138:139], v[154:155]
	v_lshlrev_b32_e32 v138, 16, v93
	s_nop 0
	v_and_b32_e32 v139, 0xffff0000, v93
	v_pk_mul_f32 v[138:139], v[96:97], v[138:139] op_sel_hi:[0,1]
	v_pk_fma_f32 v[156:157], v[138:139], v[140:141], v[156:157]
	v_lshlrev_b32_e32 v138, 16, v94
	s_nop 0
	v_and_b32_e32 v139, 0xffff0000, v94
	v_pk_mul_f32 v[138:139], v[96:97], v[138:139] op_sel_hi:[0,1]
	s_waitcnt lgkmcnt(0)
	s_nop 0
	v_pk_fma_f32 v[184:185], v[138:139], v[142:143], v[184:185]
	v_lshlrev_b32_e32 v138, 16, v95
	s_nop 0
	v_and_b32_e32 v139, 0xffff0000, v95
	v_med3_f32 v133, v154, s82, v229
	v_med3_f32 v143, v155, s82, v229
	v_mov_b32_e64 v142, v97
	v_pk_mul_f32 v[138:139], v[96:97], v[138:139] op_sel_hi:[0,1]
	v_cvt_pk_fp8_f32 v142, v133, v143
	v_pk_fma_f32 v[144:145], v[138:139], v[144:145], v[186:187]
	v_cvt_pk_bf16_f32 v138, v154, v155
	v_cvt_pk_bf16_f32 v139, v156, v157
	v_med3_f32 v133, v156, s82, v229
	v_med3_f32 v155, v184, s82, v229
	v_med3_f32 v156, v185, s82, v229
	v_mov_b32_e64 v143, v97
	v_cvt_pk_fp8_f32 v143, v155, v156
	v_med3_f32 v154, v157, s82, v229
	v_cvt_pk_bf16_f32 v140, v184, v185
	v_cvt_pk_fp8_f32 v142, v133, v154 op_sel:[0,0,1]
	ds_read_b128 v[154:157], v180 offset:6944
	ds_read_b128 v[184:187], v180 offset:6960
	v_cvt_pk_bf16_f32 v141, v144, v145
	v_med3_f32 v133, v144, s82, v229
	v_med3_f32 v144, v145, s82, v229
	v_cvt_pk_fp8_f32 v143, v133, v144 op_sel:[0,0,1]
	v_lshlrev_b32_e32 v144, 16, v88
	s_nop 0
	v_and_b32_e32 v145, 0xffff0000, v88
	v_pk_mul_f32 v[144:145], v[96:97], v[144:145] op_sel_hi:[0,1]
	s_waitcnt lgkmcnt(1)
	s_nop 0
	v_pk_fma_f32 v[144:145], v[144:145], v[146:147], v[154:155]
	v_lshlrev_b32_e32 v146, 16, v89
	s_nop 0
	v_and_b32_e32 v147, 0xffff0000, v89
	v_pk_mul_f32 v[146:147], v[96:97], v[146:147] op_sel_hi:[0,1]
	v_pk_fma_f32 v[154:155], v[146:147], v[148:149], v[156:157]
	v_lshlrev_b32_e32 v146, 16, v90
	s_nop 0
	v_and_b32_e32 v147, 0xffff0000, v90
	v_pk_mul_f32 v[146:147], v[96:97], v[146:147] op_sel_hi:[0,1]
	s_waitcnt lgkmcnt(0)
	s_nop 0
	v_pk_fma_f32 v[150:151], v[146:147], v[150:151], v[184:185]
	v_lshlrev_b32_e32 v146, 16, v91
	s_nop 0
	v_and_b32_e32 v147, 0xffff0000, v91
	v_pk_mul_f32 v[146:147], v[96:97], v[146:147] op_sel_hi:[0,1]
	v_pk_fma_f32 v[156:157], v[146:147], v[152:153], v[186:187]
	v_cvt_pk_bf16_f32 v146, v144, v145
	v_med3_f32 v133, v144, s82, v229
	v_med3_f32 v145, v145, s82, v229
	v_mov_b32_e64 v144, v97
	v_cvt_pk_fp8_f32 v144, v133, v145
	v_med3_f32 v133, v154, s82, v229
	v_med3_f32 v145, v155, s82, v229
	v_cvt_pk_bf16_f32 v147, v154, v155
	v_cvt_pk_fp8_f32 v144, v133, v145 op_sel:[0,0,1]
	v_med3_f32 v133, v150, s82, v229
	v_med3_f32 v154, v151, s82, v229
	v_mov_b32_e64 v145, v97
	v_cvt_pk_fp8_f32 v145, v133, v154
	v_cvt_pk_bf16_f32 v148, v150, v151
	ds_read_b128 v[150:153], v181 offset:9600
	v_med3_f32 v133, v156, s82, v229
	v_med3_f32 v183, v157, s82, v229
	v_cvt_pk_fp8_f32 v145, v133, v183 op_sel:[0,0,1]
	v_cvt_pk_bf16_f32 v149, v156, v157
	ds_read_b128 v[154:157], v181 offset:9616
	s_waitcnt lgkmcnt(1)
	s_nop 0
	v_mfma_f32_16x16x32_bf16 v[134:137], v[138:141], v[150:153], v[134:137]
	global_store_dwordx4 v[130:131], v[142:145], off offset:704
	v_lshlrev_b32_e32 v188, 16, v102
	s_waitcnt lgkmcnt(0)
	v_mfma_f32_16x16x32_bf16 v[134:137], v[146:149], v[154:157], v[134:137]
	ds_read_b128 v[138:141], v180 offset:3072
	ds_read_b128 v[142:145], v180 offset:3088
	ds_read_b128 v[146:149], v180 offset:3104
	ds_read_b128 v[150:153], v180 offset:3120
	ds_read_b128 v[154:157], v180 offset:7168
	ds_read_b128 v[184:187], v180 offset:7184
	v_and_b32_e32 v189, 0xffff0000, v102
	v_pk_mul_f32 v[188:189], v[96:97], v[188:189] op_sel_hi:[0,1]
	s_waitcnt lgkmcnt(1)
	s_nop 0
	v_pk_fma_f32 v[154:155], v[188:189], v[138:139], v[154:155]
	v_lshlrev_b32_e32 v138, 16, v103
	s_nop 0
	v_and_b32_e32 v139, 0xffff0000, v103
	v_pk_mul_f32 v[138:139], v[96:97], v[138:139] op_sel_hi:[0,1]
	v_pk_fma_f32 v[156:157], v[138:139], v[140:141], v[156:157]
	v_lshlrev_b32_e32 v138, 16, v104
	s_nop 0
	v_and_b32_e32 v139, 0xffff0000, v104
	v_pk_mul_f32 v[138:139], v[96:97], v[138:139] op_sel_hi:[0,1]
	s_waitcnt lgkmcnt(0)
	s_nop 0
	v_pk_fma_f32 v[184:185], v[138:139], v[142:143], v[184:185]
	v_lshlrev_b32_e32 v138, 16, v105
	s_nop 0
	v_and_b32_e32 v139, 0xffff0000, v105
	v_med3_f32 v133, v154, s82, v229
	v_med3_f32 v143, v155, s82, v229
	v_mov_b32_e64 v142, v97
	v_pk_mul_f32 v[138:139], v[96:97], v[138:139] op_sel_hi:[0,1]
	v_cvt_pk_fp8_f32 v142, v133, v143
	v_pk_fma_f32 v[144:145], v[138:139], v[144:145], v[186:187]
	v_cvt_pk_bf16_f32 v138, v154, v155
	v_cvt_pk_bf16_f32 v139, v156, v157
	v_med3_f32 v133, v156, s82, v229
	v_med3_f32 v155, v184, s82, v229
	v_med3_f32 v156, v185, s82, v229
	v_mov_b32_e64 v143, v97
	v_cvt_pk_fp8_f32 v143, v155, v156
	v_med3_f32 v154, v157, s82, v229
	v_cvt_pk_bf16_f32 v140, v184, v185
	v_cvt_pk_fp8_f32 v142, v133, v154 op_sel:[0,0,1]
	ds_read_b128 v[154:157], v180 offset:7200
	ds_read_b128 v[184:187], v180 offset:7216
	v_cvt_pk_bf16_f32 v141, v144, v145
	v_med3_f32 v133, v144, s82, v229
	v_med3_f32 v144, v145, s82, v229
	v_cvt_pk_fp8_f32 v143, v133, v144 op_sel:[0,0,1]
	v_lshlrev_b32_e32 v144, 16, v98
	s_nop 0
	v_and_b32_e32 v145, 0xffff0000, v98
	v_pk_mul_f32 v[144:145], v[96:97], v[144:145] op_sel_hi:[0,1]
	s_waitcnt lgkmcnt(1)
	s_nop 0
	v_pk_fma_f32 v[144:145], v[144:145], v[146:147], v[154:155]
	v_lshlrev_b32_e32 v146, 16, v99
	s_nop 0
	v_and_b32_e32 v147, 0xffff0000, v99
	v_pk_mul_f32 v[146:147], v[96:97], v[146:147] op_sel_hi:[0,1]
	v_pk_fma_f32 v[154:155], v[146:147], v[148:149], v[156:157]
	v_lshlrev_b32_e32 v146, 16, v100
	s_nop 0
	v_and_b32_e32 v147, 0xffff0000, v100
	v_pk_mul_f32 v[146:147], v[96:97], v[146:147] op_sel_hi:[0,1]
	s_waitcnt lgkmcnt(0)
	s_nop 0
	v_pk_fma_f32 v[150:151], v[146:147], v[150:151], v[184:185]
	v_lshlrev_b32_e32 v146, 16, v101
	s_nop 0
	v_and_b32_e32 v147, 0xffff0000, v101
	v_pk_mul_f32 v[146:147], v[96:97], v[146:147] op_sel_hi:[0,1]
	v_pk_fma_f32 v[156:157], v[146:147], v[152:153], v[186:187]
	v_cvt_pk_bf16_f32 v146, v144, v145
	v_med3_f32 v133, v144, s82, v229
	v_med3_f32 v145, v145, s82, v229
	v_mov_b32_e64 v144, v97
	v_cvt_pk_fp8_f32 v144, v133, v145
	v_med3_f32 v133, v154, s82, v229
	v_med3_f32 v145, v155, s82, v229
	v_cvt_pk_bf16_f32 v147, v154, v155
	v_cvt_pk_fp8_f32 v144, v133, v145 op_sel:[0,0,1]
	v_med3_f32 v133, v150, s82, v229
	v_med3_f32 v154, v151, s82, v229
	v_mov_b32_e64 v145, v97
	v_cvt_pk_fp8_f32 v145, v133, v154
	v_cvt_pk_bf16_f32 v148, v150, v151
	ds_read_b128 v[150:153], v181 offset:9728
	v_med3_f32 v133, v156, s82, v229
	v_med3_f32 v183, v157, s82, v229
	v_cvt_pk_fp8_f32 v145, v133, v183 op_sel:[0,0,1]
	v_cvt_pk_bf16_f32 v149, v156, v157
	ds_read_b128 v[154:157], v181 offset:9744
	s_waitcnt lgkmcnt(1)
	s_nop 0
	v_mfma_f32_16x16x32_bf16 v[134:137], v[138:141], v[150:153], v[134:137]
	global_store_dwordx4 v[130:131], v[142:145], off offset:768
	v_lshlrev_b32_e32 v188, 16, v110
	s_waitcnt lgkmcnt(0)
	v_mfma_f32_16x16x32_bf16 v[134:137], v[146:149], v[154:157], v[134:137]
	ds_read_b128 v[138:141], v180 offset:3328
	ds_read_b128 v[142:145], v180 offset:3344
	ds_read_b128 v[146:149], v180 offset:3360
	ds_read_b128 v[150:153], v180 offset:3376
	ds_read_b128 v[154:157], v180 offset:7424
	ds_read_b128 v[184:187], v180 offset:7440
	v_and_b32_e32 v189, 0xffff0000, v110
	v_pk_mul_f32 v[188:189], v[96:97], v[188:189] op_sel_hi:[0,1]
	s_waitcnt lgkmcnt(1)
	s_nop 0
	v_pk_fma_f32 v[154:155], v[188:189], v[138:139], v[154:155]
	v_lshlrev_b32_e32 v138, 16, v111
	s_nop 0
	v_and_b32_e32 v139, 0xffff0000, v111
	v_pk_mul_f32 v[138:139], v[96:97], v[138:139] op_sel_hi:[0,1]
	v_pk_fma_f32 v[156:157], v[138:139], v[140:141], v[156:157]
	v_lshlrev_b32_e32 v138, 16, v112
	s_nop 0
	v_and_b32_e32 v139, 0xffff0000, v112
	v_pk_mul_f32 v[138:139], v[96:97], v[138:139] op_sel_hi:[0,1]
	s_waitcnt lgkmcnt(0)
	s_nop 0
	v_pk_fma_f32 v[184:185], v[138:139], v[142:143], v[184:185]
	v_lshlrev_b32_e32 v138, 16, v113
	s_nop 0
	v_and_b32_e32 v139, 0xffff0000, v113
	v_med3_f32 v133, v154, s82, v229
	v_med3_f32 v143, v155, s82, v229
	v_mov_b32_e64 v142, v97
	v_pk_mul_f32 v[138:139], v[96:97], v[138:139] op_sel_hi:[0,1]
	v_cvt_pk_fp8_f32 v142, v133, v143
	v_pk_fma_f32 v[144:145], v[138:139], v[144:145], v[186:187]
	v_cvt_pk_bf16_f32 v138, v154, v155
	v_cvt_pk_bf16_f32 v139, v156, v157
	v_med3_f32 v133, v156, s82, v229
	v_med3_f32 v155, v184, s82, v229
	v_med3_f32 v156, v185, s82, v229
	v_mov_b32_e64 v143, v97
	v_cvt_pk_fp8_f32 v143, v155, v156
	v_med3_f32 v154, v157, s82, v229
	v_cvt_pk_bf16_f32 v140, v184, v185
	v_cvt_pk_fp8_f32 v142, v133, v154 op_sel:[0,0,1]
	ds_read_b128 v[154:157], v180 offset:7456
	ds_read_b128 v[184:187], v180 offset:7472
	v_cvt_pk_bf16_f32 v141, v144, v145
	v_med3_f32 v133, v144, s82, v229
	v_med3_f32 v144, v145, s82, v229
	v_cvt_pk_fp8_f32 v143, v133, v144 op_sel:[0,0,1]
	v_lshlrev_b32_e32 v144, 16, v106
	s_nop 0
	v_and_b32_e32 v145, 0xffff0000, v106
	v_pk_mul_f32 v[144:145], v[96:97], v[144:145] op_sel_hi:[0,1]
	s_waitcnt lgkmcnt(1)
	s_nop 0
	v_pk_fma_f32 v[144:145], v[144:145], v[146:147], v[154:155]
	v_lshlrev_b32_e32 v146, 16, v107
	s_nop 0
	v_and_b32_e32 v147, 0xffff0000, v107
	v_pk_mul_f32 v[146:147], v[96:97], v[146:147] op_sel_hi:[0,1]
	v_pk_fma_f32 v[154:155], v[146:147], v[148:149], v[156:157]
	v_lshlrev_b32_e32 v146, 16, v108
	s_nop 0
	v_and_b32_e32 v147, 0xffff0000, v108
	v_pk_mul_f32 v[146:147], v[96:97], v[146:147] op_sel_hi:[0,1]
	s_waitcnt lgkmcnt(0)
	s_nop 0
	v_pk_fma_f32 v[150:151], v[146:147], v[150:151], v[184:185]
	v_lshlrev_b32_e32 v146, 16, v109
	s_nop 0
	v_and_b32_e32 v147, 0xffff0000, v109
	v_pk_mul_f32 v[146:147], v[96:97], v[146:147] op_sel_hi:[0,1]
	v_pk_fma_f32 v[156:157], v[146:147], v[152:153], v[186:187]
	v_cvt_pk_bf16_f32 v146, v144, v145
	v_med3_f32 v133, v144, s82, v229
	v_med3_f32 v145, v145, s82, v229
	v_mov_b32_e64 v144, v97
	v_cvt_pk_fp8_f32 v144, v133, v145
	v_med3_f32 v133, v154, s82, v229
	v_med3_f32 v145, v155, s82, v229
	v_cvt_pk_bf16_f32 v147, v154, v155
	v_cvt_pk_fp8_f32 v144, v133, v145 op_sel:[0,0,1]
	v_med3_f32 v133, v150, s82, v229
	v_med3_f32 v154, v151, s82, v229
	v_mov_b32_e64 v145, v97
	v_cvt_pk_fp8_f32 v145, v133, v154
	v_cvt_pk_bf16_f32 v148, v150, v151
	ds_read_b128 v[150:153], v181 offset:9856
	v_med3_f32 v133, v156, s82, v229
	v_med3_f32 v183, v157, s82, v229
	v_cvt_pk_fp8_f32 v145, v133, v183 op_sel:[0,0,1]
	v_cvt_pk_bf16_f32 v149, v156, v157
	ds_read_b128 v[154:157], v181 offset:9872
	s_waitcnt lgkmcnt(1)
	s_nop 0
	v_mfma_f32_16x16x32_bf16 v[134:137], v[138:141], v[150:153], v[134:137]
	global_store_dwordx4 v[130:131], v[142:145], off offset:832
	v_lshlrev_b32_e32 v188, 16, v118
	s_waitcnt lgkmcnt(0)
	v_mfma_f32_16x16x32_bf16 v[134:137], v[146:149], v[154:157], v[134:137]
	ds_read_b128 v[138:141], v180 offset:3584
	ds_read_b128 v[142:145], v180 offset:3600
	ds_read_b128 v[146:149], v180 offset:3616
	ds_read_b128 v[150:153], v180 offset:3632
	ds_read_b128 v[154:157], v180 offset:7680
	ds_read_b128 v[184:187], v180 offset:7696
	v_and_b32_e32 v189, 0xffff0000, v118
	v_pk_mul_f32 v[188:189], v[96:97], v[188:189] op_sel_hi:[0,1]
	s_waitcnt lgkmcnt(1)
	s_nop 0
	v_pk_fma_f32 v[154:155], v[188:189], v[138:139], v[154:155]
	v_lshlrev_b32_e32 v138, 16, v119
	s_nop 0
	v_and_b32_e32 v139, 0xffff0000, v119
	v_pk_mul_f32 v[138:139], v[96:97], v[138:139] op_sel_hi:[0,1]
	v_pk_fma_f32 v[156:157], v[138:139], v[140:141], v[156:157]
	v_lshlrev_b32_e32 v138, 16, v120
	s_nop 0
	v_and_b32_e32 v139, 0xffff0000, v120
	v_pk_mul_f32 v[138:139], v[96:97], v[138:139] op_sel_hi:[0,1]
	s_waitcnt lgkmcnt(0)
	s_nop 0
	v_pk_fma_f32 v[184:185], v[138:139], v[142:143], v[184:185]
	v_lshlrev_b32_e32 v138, 16, v121
	s_nop 0
	v_and_b32_e32 v139, 0xffff0000, v121
	v_med3_f32 v133, v154, s82, v229
	v_med3_f32 v143, v155, s82, v229
	v_mov_b32_e64 v142, v97
	v_pk_mul_f32 v[138:139], v[96:97], v[138:139] op_sel_hi:[0,1]
	v_cvt_pk_fp8_f32 v142, v133, v143
	v_pk_fma_f32 v[144:145], v[138:139], v[144:145], v[186:187]
	v_cvt_pk_bf16_f32 v138, v154, v155
	v_cvt_pk_bf16_f32 v139, v156, v157
	v_med3_f32 v133, v156, s82, v229
	v_med3_f32 v155, v184, s82, v229
	v_med3_f32 v156, v185, s82, v229
	v_mov_b32_e64 v143, v97
	v_cvt_pk_fp8_f32 v143, v155, v156
	v_med3_f32 v154, v157, s82, v229
	v_cvt_pk_bf16_f32 v140, v184, v185
	v_cvt_pk_fp8_f32 v142, v133, v154 op_sel:[0,0,1]
	ds_read_b128 v[154:157], v180 offset:7712
	ds_read_b128 v[184:187], v180 offset:7728
	v_cvt_pk_bf16_f32 v141, v144, v145
	v_med3_f32 v133, v144, s82, v229
	v_med3_f32 v144, v145, s82, v229
	v_cvt_pk_fp8_f32 v143, v133, v144 op_sel:[0,0,1]
	v_lshlrev_b32_e32 v144, 16, v114
	s_nop 0
	v_and_b32_e32 v145, 0xffff0000, v114
	v_pk_mul_f32 v[144:145], v[96:97], v[144:145] op_sel_hi:[0,1]
	s_waitcnt lgkmcnt(1)
	s_nop 0
	v_pk_fma_f32 v[144:145], v[144:145], v[146:147], v[154:155]
	v_lshlrev_b32_e32 v146, 16, v115
	s_nop 0
	v_and_b32_e32 v147, 0xffff0000, v115
	v_pk_mul_f32 v[146:147], v[96:97], v[146:147] op_sel_hi:[0,1]
	v_pk_fma_f32 v[154:155], v[146:147], v[148:149], v[156:157]
	v_lshlrev_b32_e32 v146, 16, v116
	s_nop 0
	v_and_b32_e32 v147, 0xffff0000, v116
	v_pk_mul_f32 v[146:147], v[96:97], v[146:147] op_sel_hi:[0,1]
	s_waitcnt lgkmcnt(0)
	s_nop 0
	v_pk_fma_f32 v[150:151], v[146:147], v[150:151], v[184:185]
	v_lshlrev_b32_e32 v146, 16, v117
	s_nop 0
	v_and_b32_e32 v147, 0xffff0000, v117
	v_pk_mul_f32 v[146:147], v[96:97], v[146:147] op_sel_hi:[0,1]
	v_pk_fma_f32 v[156:157], v[146:147], v[152:153], v[186:187]
	v_cvt_pk_bf16_f32 v146, v144, v145
	v_med3_f32 v133, v144, s82, v229
	v_med3_f32 v145, v145, s82, v229
	v_mov_b32_e64 v144, v97
	v_cvt_pk_fp8_f32 v144, v133, v145
	v_med3_f32 v133, v154, s82, v229
	v_med3_f32 v145, v155, s82, v229
	v_cvt_pk_bf16_f32 v147, v154, v155
	v_cvt_pk_fp8_f32 v144, v133, v145 op_sel:[0,0,1]
	v_med3_f32 v133, v150, s82, v229
	v_med3_f32 v154, v151, s82, v229
	v_mov_b32_e64 v145, v97
	v_cvt_pk_fp8_f32 v145, v133, v154
	v_cvt_pk_bf16_f32 v148, v150, v151
	ds_read_b128 v[150:153], v181 offset:9984
	v_med3_f32 v133, v156, s82, v229
	v_med3_f32 v183, v157, s82, v229
	v_cvt_pk_fp8_f32 v145, v133, v183 op_sel:[0,0,1]
	v_cvt_pk_bf16_f32 v149, v156, v157
	ds_read_b128 v[154:157], v181 offset:10000
	s_waitcnt lgkmcnt(1)
	s_nop 0
	v_mfma_f32_16x16x32_bf16 v[134:137], v[138:141], v[150:153], v[134:137]
	global_store_dwordx4 v[130:131], v[142:145], off offset:896
	v_lshlrev_b32_e32 v188, 16, v126
	s_waitcnt lgkmcnt(0)
	v_mfma_f32_16x16x32_bf16 v[134:137], v[146:149], v[154:157], v[134:137]
	ds_read_b128 v[138:141], v180 offset:3840
	ds_read_b128 v[142:145], v180 offset:3856
	ds_read_b128 v[146:149], v180 offset:3872
	ds_read_b128 v[150:153], v180 offset:3888
	ds_read_b128 v[154:157], v180 offset:7936
	ds_read_b128 v[184:187], v180 offset:7952
	v_and_b32_e32 v189, 0xffff0000, v126
	v_pk_mul_f32 v[188:189], v[96:97], v[188:189] op_sel_hi:[0,1]
	s_waitcnt lgkmcnt(1)
	s_nop 0
	v_pk_fma_f32 v[154:155], v[188:189], v[138:139], v[154:155]
	v_lshlrev_b32_e32 v138, 16, v127
	s_nop 0
	v_and_b32_e32 v139, 0xffff0000, v127
	v_pk_mul_f32 v[138:139], v[96:97], v[138:139] op_sel_hi:[0,1]
	v_pk_fma_f32 v[156:157], v[138:139], v[140:141], v[156:157]
	v_lshlrev_b32_e32 v138, 16, v128
	s_nop 0
	v_and_b32_e32 v139, 0xffff0000, v128
	v_pk_mul_f32 v[138:139], v[96:97], v[138:139] op_sel_hi:[0,1]
	s_waitcnt lgkmcnt(0)
	s_nop 0
	v_pk_fma_f32 v[184:185], v[138:139], v[142:143], v[184:185]
	v_lshlrev_b32_e32 v138, 16, v129
	s_nop 0
	v_and_b32_e32 v139, 0xffff0000, v129
	v_med3_f32 v133, v154, s82, v229
	v_med3_f32 v143, v155, s82, v229
	v_mov_b32_e64 v142, v97
	v_pk_mul_f32 v[138:139], v[96:97], v[138:139] op_sel_hi:[0,1]
	v_cvt_pk_fp8_f32 v142, v133, v143
	v_pk_fma_f32 v[144:145], v[138:139], v[144:145], v[186:187]
	v_cvt_pk_bf16_f32 v138, v154, v155
	v_cvt_pk_bf16_f32 v139, v156, v157
	v_med3_f32 v133, v156, s82, v229
	v_med3_f32 v155, v184, s82, v229
	v_med3_f32 v156, v185, s82, v229
	v_mov_b32_e64 v143, v97
	v_cvt_pk_fp8_f32 v143, v155, v156
	v_med3_f32 v154, v157, s82, v229
	v_cvt_pk_bf16_f32 v140, v184, v185
	v_cvt_pk_fp8_f32 v142, v133, v154 op_sel:[0,0,1]
	ds_read_b128 v[154:157], v180 offset:7968
	ds_read_b128 v[184:187], v180 offset:7984
	v_cvt_pk_bf16_f32 v141, v144, v145
	v_med3_f32 v133, v144, s82, v229
	v_med3_f32 v144, v145, s82, v229
	v_cvt_pk_fp8_f32 v143, v133, v144 op_sel:[0,0,1]
	v_lshlrev_b32_e32 v144, 16, v122
	s_nop 0
	v_and_b32_e32 v145, 0xffff0000, v122
	v_pk_mul_f32 v[144:145], v[96:97], v[144:145] op_sel_hi:[0,1]
	s_waitcnt lgkmcnt(1)
	s_nop 0
	v_pk_fma_f32 v[144:145], v[144:145], v[146:147], v[154:155]
	v_lshlrev_b32_e32 v146, 16, v123
	s_nop 0
	v_and_b32_e32 v147, 0xffff0000, v123
	v_pk_mul_f32 v[146:147], v[96:97], v[146:147] op_sel_hi:[0,1]
	v_pk_fma_f32 v[154:155], v[146:147], v[148:149], v[156:157]
	v_lshlrev_b32_e32 v146, 16, v124
	s_nop 0
	v_and_b32_e32 v147, 0xffff0000, v124
	v_pk_mul_f32 v[146:147], v[96:97], v[146:147] op_sel_hi:[0,1]
	s_waitcnt lgkmcnt(0)
	s_nop 0
	v_pk_fma_f32 v[150:151], v[146:147], v[150:151], v[184:185]
	v_lshlrev_b32_e32 v146, 16, v125
	s_nop 0
	v_and_b32_e32 v147, 0xffff0000, v125
	v_pk_mul_f32 v[146:147], v[96:97], v[146:147] op_sel_hi:[0,1]
	v_pk_fma_f32 v[156:157], v[146:147], v[152:153], v[186:187]
	v_cvt_pk_bf16_f32 v146, v144, v145
	v_med3_f32 v96, v144, s82, v229
	v_med3_f32 v133, v145, s82, v229
	v_mov_b32_e64 v144, v97
	v_cvt_pk_fp8_f32 v144, v96, v133
	v_med3_f32 v96, v154, s82, v229
	v_med3_f32 v133, v155, s82, v229
	v_cvt_pk_bf16_f32 v148, v150, v151
	v_cvt_pk_fp8_f32 v144, v96, v133 op_sel:[0,0,1]
	v_med3_f32 v96, v150, s82, v229
	v_med3_f32 v133, v151, s82, v229
	ds_read_b128 v[150:153], v181 offset:10112
	v_mov_b32_e64 v145, v97
	v_cvt_pk_bf16_f32 v147, v154, v155
	v_cvt_pk_bf16_f32 v149, v156, v157
	v_cvt_pk_fp8_f32 v145, v96, v133
	v_med3_f32 v96, v156, s82, v229
	v_med3_f32 v133, v157, s82, v229
	ds_read_b128 v[154:157], v181 offset:10128
	s_waitcnt lgkmcnt(1)
	s_nop 0
	v_mfma_f32_16x16x32_bf16 v[134:137], v[138:141], v[150:153], v[134:137]
	v_cvt_pk_fp8_f32 v145, v96, v133 op_sel:[0,0,1]
	v_or_b32_e32 v96, s14, v172
	s_nop 0
	v_lshl_add_u32 v96, v96, 6, v173
	s_waitcnt lgkmcnt(0)
	s_nop 0
	v_mfma_f32_16x16x32_bf16 v[134:137], v[146:149], v[154:157], v[134:137]
	s_mov_b32 s14, 16
	s_nop 0
	global_store_dwordx4 v[130:131], v[142:145], off offset:960
	s_nop 5
	s_nop 0
	ds_write2_b32 v96, v134, v135 offset1:16
	ds_write2_b32 v96, v136, v137 offset0:32 offset1:48
	s_cbranch_vccnz .LBB0_1072
.LBB0_1070:
	v_or_b32_e32 v130, s14, v132
	s_and_b64 s[8:9], s[10:11], s[12:13]
	v_ashrrev_i32_e32 v131, 31, v130
	s_and_b64 vcc, exec, s[8:9]
	s_cbranch_vccnz .LBB0_1069
	v_lshlrev_b64 v[0:1], 11, v[130:131]
	v_lshl_add_u64 v[126:127], v[162:163], 0, v[0:1]
	global_load_dwordx4 v[0:3], v[126:127], off offset:16
	global_load_dwordx4 v[4:7], v[126:127], off
	global_load_dwordx4 v[8:11], v[126:127], off offset:144
	global_load_dwordx4 v[12:15], v[126:127], off offset:128
	global_load_dwordx4 v[16:19], v[126:127], off offset:272
	global_load_dwordx4 v[20:23], v[126:127], off offset:256
	global_load_dwordx4 v[24:27], v[126:127], off offset:400
	global_load_dwordx4 v[28:31], v[126:127], off offset:384
	global_load_dwordx4 v[32:35], v[126:127], off offset:528
	global_load_dwordx4 v[36:39], v[126:127], off offset:512
	global_load_dwordx4 v[40:43], v[126:127], off offset:656
	global_load_dwordx4 v[44:47], v[126:127], off offset:640
	global_load_dwordx4 v[48:51], v[126:127], off offset:784
	global_load_dwordx4 v[52:55], v[126:127], off offset:768
	global_load_dwordx4 v[56:59], v[126:127], off offset:912
	global_load_dwordx4 v[60:63], v[126:127], off offset:896
	global_load_dwordx4 v[64:67], v[126:127], off offset:1040
	global_load_dwordx4 v[68:71], v[126:127], off offset:1024
	global_load_dwordx4 v[72:75], v[126:127], off offset:1168
	global_load_dwordx4 v[76:79], v[126:127], off offset:1152
	global_load_dwordx4 v[80:83], v[126:127], off offset:1296
	global_load_dwordx4 v[84:87], v[126:127], off offset:1280
	global_load_dwordx4 v[88:91], v[126:127], off offset:1424
	global_load_dwordx4 v[92:95], v[126:127], off offset:1408
	global_load_dwordx4 v[98:101], v[126:127], off offset:1552
	global_load_dwordx4 v[102:105], v[126:127], off offset:1536
	global_load_dwordx4 v[106:109], v[126:127], off offset:1680
	global_load_dwordx4 v[110:113], v[126:127], off offset:1664
	global_load_dwordx4 v[114:117], v[126:127], off offset:1808
	global_load_dwordx4 v[118:121], v[126:127], off offset:1792
	global_load_dwordx4 v[122:125], v[126:127], off offset:1936
	s_nop 0
	s_nop 0
	global_load_dwordx4 v[126:129], v[126:127], off offset:1920
	s_branch .LBB0_1069
.LBB0_1072:
	s_and_saveexec_b64 s[20:21], s[2:3]
	s_cbranch_execz .LBB0_1138
	s_nop 0
	ds_read_b128 v[154:157], v182
	ds_read_b128 v[150:153], v182 offset:16
	ds_read_b128 v[142:145], v182 offset:32
	ds_read_b128 v[134:137], v182 offset:48
	v_readlane_b32 s36, v253, 50
	s_waitcnt lgkmcnt(3)
	s_nop 0
	v_mul_f32_e32 v96, 0xbfb8aa3b, v154
	v_exp_f32_e64 v96, v96
	v_readlane_b32 s40, v253, 54
	v_readlane_b32 s41, v253, 55
	v_mul_f32_e32 v155, 0xbfb8aa3b, v155
	v_add_f32_e64 v96, 1.0, v96
	v_div_scale_f32 v130, s[8:9], v96, v96, 1.0
	v_rcp_f32_e32 v131, v130
	v_exp_f32_e32 v155, v155
	v_mul_f32_e32 v156, 0xbfb8aa3b, v156
	v_exp_f32_e64 v156, v156
	v_fma_f32 v132, -v130, v131, 1.0
	v_fmac_f32_e32 v131, v132, v131
	s_nop 0
	v_div_scale_f32 v132, vcc, 1.0, v96, 1.0
	v_mul_f32_e64 v133, v132, v131
	v_fma_f32 v138, -v130, v133, v132
	v_fmac_f32_e32 v133, v138, v131
	s_nop 0
	v_fma_f32 v130, -v130, v133, v132
	v_div_fmas_f32 v130, v130, v131, v133
	v_div_fixup_f32 v96, v130, v96, 1.0
	global_load_dwordx4 v[130:133], v97, s[40:41] offset:48
	global_load_dwordx4 v[138:141], v97, s[40:41] offset:32
	global_load_dwordx4 v[146:149], v97, s[40:41] offset:16
	global_load_dwordx4 v[184:187], v97, s[40:41]
	v_add_f32_e64 v155, 1.0, v155
	v_div_scale_f32 v183, s[8:9], v155, v155, 1.0
	v_add_f32_e64 v156, 1.0, v156
	v_mul_f32_e32 v157, 0xbfb8aa3b, v157
	v_exp_f32_e32 v157, v157
	s_waitcnt lgkmcnt(2)
	v_mul_f32_e32 v150, 0xbfb8aa3b, v150
	v_exp_f32_e32 v150, v150
	s_waitcnt lgkmcnt(1)
	v_mul_f32_e32 v142, 0xbfb8aa3b, v142
	v_add_f32_e32 v157, 1.0, v157
	v_exp_f32_e32 v142, v142
	v_add_f32_e32 v150, 1.0, v150
	s_waitcnt lgkmcnt(0)
	v_mul_f32_e32 v134, 0xbfb8aa3b, v134
	v_exp_f32_e64 v134, v134
	v_add_f32_e32 v142, 1.0, v142
	s_mov_b32 s16, s93
	v_readlane_b32 s37, v253, 51
	v_add_f32_e64 v134, 1.0, v134
	v_readlane_b32 s38, v253, 52
	v_readlane_b32 s39, v253, 53
	v_readlane_b32 s42, v253, 56
	v_readlane_b32 s43, v253, 57
	v_readlane_b32 s44, v253, 58
	v_readlane_b32 s45, v253, 59
	v_readlane_b32 s46, v253, 60
	v_readlane_b32 s47, v253, 61
	v_readlane_b32 s48, v253, 62
	v_readlane_b32 s49, v253, 63
	v_readlane_b32 s50, v254, 0
	v_readlane_b32 s51, v254, 1
	s_waitcnt vmcnt(0)
	v_add_f32_e32 v154, v184, v96
	v_rcp_f32_e32 v184, v183
	s_nop 0
	v_fma_f32 v188, -v183, v184, 1.0
	v_fmac_f32_e32 v184, v188, v184
	s_nop 0
	v_div_scale_f32 v188, vcc, 1.0, v155, 1.0
	v_mul_f32_e64 v189, v188, v184
	v_fma_f32 v190, -v183, v189, v188
	v_fmac_f32_e32 v189, v190, v184
	s_nop 0
	v_fma_f32 v183, -v183, v189, v188
	v_div_fmas_f32 v183, v183, v184, v189
	v_div_fixup_f32 v155, v183, v155, 1.0
	v_div_scale_f32 v184, s[8:9], v156, v156, 1.0
	v_add_f32_e64 v183, v185, v155
	v_rcp_f32_e32 v185, v184
	s_nop 0
	v_fma_f32 v188, -v184, v185, 1.0
	v_fmac_f32_e32 v185, v188, v185
	s_nop 0
	v_div_scale_f32 v188, vcc, 1.0, v156, 1.0
	v_mul_f32_e64 v189, v188, v185
	v_fma_f32 v190, -v184, v189, v188
	v_fmac_f32_e32 v189, v190, v185
	s_nop 0
	v_fma_f32 v184, -v184, v189, v188
	v_div_fmas_f32 v184, v184, v185, v189
	v_div_fixup_f32 v156, v184, v156, 1.0
	v_div_scale_f32 v185, s[8:9], v157, v157, 1.0
	v_add_f32_e64 v184, v186, v156
	v_rcp_f32_e32 v186, v185
	s_nop 0
	v_fma_f32 v188, -v185, v186, 1.0
	v_fmac_f32_e32 v186, v188, v186
	s_nop 0
	v_div_scale_f32 v188, vcc, 1.0, v157, 1.0
	v_mul_f32_e64 v189, v188, v186
	v_fma_f32 v190, -v185, v189, v188
	v_fmac_f32_e32 v189, v190, v186
	s_nop 0
	v_fma_f32 v185, -v185, v189, v188
	v_div_fmas_f32 v185, v185, v186, v189
	v_div_fixup_f32 v157, v185, v157, 1.0
	v_div_scale_f32 v186, s[8:9], v150, v150, 1.0
	v_add_f32_e64 v185, v187, v157
	v_rcp_f32_e32 v187, v186
	s_nop 0
	v_fma_f32 v188, -v186, v187, 1.0
	v_fmac_f32_e32 v187, v188, v187
	s_nop 0
	v_div_scale_f32 v188, vcc, 1.0, v150, 1.0
	v_mul_f32_e64 v189, v188, v187
	v_fma_f32 v190, -v186, v189, v188
	v_fmac_f32_e32 v189, v190, v187
	s_nop 0
	v_fma_f32 v186, -v186, v189, v188
	v_div_fmas_f32 v186, v186, v187, v189
	v_div_fixup_f32 v186, v186, v150, 1.0
	v_add_f32_e64 v188, v146, v186
	v_mul_f32_e32 v146, 0xbfb8aa3b, v151
	v_exp_f32_e32 v146, v146
	s_nop 0
	v_add_f32_e64 v146, 1.0, v146
	v_div_scale_f32 v150, s[8:9], v146, v146, 1.0
	v_rcp_f32_e32 v151, v150
	s_nop 0
	v_fma_f32 v187, -v150, v151, 1.0
	v_fmac_f32_e32 v151, v187, v151
	s_nop 0
	v_div_scale_f32 v187, vcc, 1.0, v146, 1.0
	v_mul_f32_e64 v189, v187, v151
	v_fma_f32 v190, -v150, v189, v187
	v_fmac_f32_e32 v189, v190, v151
	s_nop 0
	v_fma_f32 v150, -v150, v189, v187
	v_div_fmas_f32 v150, v150, v151, v189
	v_div_fixup_f32 v150, v150, v146, 1.0
	v_mul_f32_e32 v146, 0xbfb8aa3b, v152
	v_exp_f32_e32 v146, v146
	v_add_f32_e32 v187, v147, v150
	v_add_f32_e64 v146, 1.0, v146
	v_div_scale_f32 v147, s[8:9], v146, v146, 1.0
	v_rcp_f32_e32 v151, v147
	s_nop 0
	v_fma_f32 v152, -v147, v151, 1.0
	v_fmac_f32_e32 v151, v152, v151
	s_nop 0
	v_div_scale_f32 v152, vcc, 1.0, v146, 1.0
	v_mul_f32_e64 v189, v152, v151
	v_fma_f32 v190, -v147, v189, v152
	v_fmac_f32_e32 v189, v190, v151
	s_nop 0
	v_fma_f32 v147, -v147, v189, v152
	v_div_fmas_f32 v147, v147, v151, v189
	v_div_fixup_f32 v147, v147, v146, 1.0
	v_mul_f32_e32 v146, 0xbfb8aa3b, v153
	v_exp_f32_e32 v146, v146
	v_add_f32_e32 v151, v148, v147
	v_add_f32_e64 v146, 1.0, v146
	v_div_scale_f32 v148, s[8:9], v146, v146, 1.0
	v_rcp_f32_e32 v152, v148
	s_nop 0
	v_fma_f32 v153, -v148, v152, 1.0
	v_fmac_f32_e32 v152, v153, v152
	s_nop 0
	v_div_scale_f32 v153, vcc, 1.0, v146, 1.0
	v_mul_f32_e64 v189, v153, v152
	v_fma_f32 v190, -v148, v189, v153
	v_fmac_f32_e32 v189, v190, v152
	s_nop 0
	v_fma_f32 v148, -v148, v189, v153
	v_div_fmas_f32 v148, v148, v152, v189
	v_div_fixup_f32 v146, v148, v146, 1.0
	v_add_f32_e64 v148, v149, v146
	v_div_scale_f32 v149, s[8:9], v142, v142, 1.0
	v_rcp_f32_e32 v152, v149
	s_nop 0
	v_fma_f32 v153, -v149, v152, 1.0
	v_fmac_f32_e32 v152, v153, v152
	s_nop 0
	v_div_scale_f32 v153, vcc, 1.0, v142, 1.0
	v_mul_f32_e64 v189, v153, v152
	v_fma_f32 v190, -v149, v189, v153
	v_fmac_f32_e32 v189, v190, v152
	s_nop 0
	v_fma_f32 v149, -v149, v189, v153
	v_div_fmas_f32 v149, v149, v152, v189
	v_div_fixup_f32 v149, v149, v142, 1.0
	v_add_f32_e64 v153, v138, v149
	v_mul_f32_e32 v138, 0xbfb8aa3b, v143
	v_exp_f32_e32 v138, v138
	s_nop 0
	v_add_f32_e64 v138, 1.0, v138
	v_div_scale_f32 v142, s[8:9], v138, v138, 1.0
	v_rcp_f32_e32 v143, v142
	s_nop 0
	v_fma_f32 v152, -v142, v143, 1.0
	v_fmac_f32_e32 v143, v152, v143
	s_nop 0
	v_div_scale_f32 v152, vcc, 1.0, v138, 1.0
	v_mul_f32_e64 v189, v152, v143
	v_fma_f32 v190, -v142, v189, v152
	v_fmac_f32_e32 v189, v190, v143
	s_nop 0
	v_fma_f32 v142, -v142, v189, v152
	v_div_fmas_f32 v142, v142, v143, v189
	v_div_fixup_f32 v142, v142, v138, 1.0
	v_mul_f32_e32 v138, 0xbfb8aa3b, v144
	v_exp_f32_e32 v138, v138
	v_add_f32_e32 v152, v139, v142
	v_add_f32_e64 v138, 1.0, v138
	v_div_scale_f32 v139, s[8:9], v138, v138, 1.0
	v_rcp_f32_e32 v143, v139
	s_nop 0
	v_fma_f32 v144, -v139, v143, 1.0
	v_fmac_f32_e32 v143, v144, v143
	s_nop 0
	v_div_scale_f32 v144, vcc, 1.0, v138, 1.0
	v_mul_f32_e64 v189, v144, v143
	v_fma_f32 v190, -v139, v189, v144
	v_fmac_f32_e32 v189, v190, v143
	s_nop 0
	v_fma_f32 v139, -v139, v189, v144
	v_div_fmas_f32 v139, v139, v143, v189
	v_div_fixup_f32 v139, v139, v138, 1.0
	v_mul_f32_e32 v138, 0xbfb8aa3b, v145
	v_exp_f32_e32 v138, v138
	v_add_f32_e32 v143, v140, v139
	v_add_f32_e64 v138, 1.0, v138
	v_div_scale_f32 v140, s[8:9], v138, v138, 1.0
	v_rcp_f32_e32 v144, v140
	s_nop 0
	v_fma_f32 v145, -v140, v144, 1.0
	v_fmac_f32_e32 v144, v145, v144
	s_nop 0
	v_div_scale_f32 v145, vcc, 1.0, v138, 1.0
	v_mul_f32_e64 v189, v145, v144
	v_fma_f32 v190, -v140, v189, v145
	v_fmac_f32_e32 v189, v190, v144
	s_nop 0
	v_fma_f32 v140, -v140, v189, v145
	v_div_fmas_f32 v140, v140, v144, v189
	v_div_fixup_f32 v138, v140, v138, 1.0
	v_add_f32_e64 v140, v141, v138
	v_div_scale_f32 v141, s[8:9], v134, v134, 1.0
	v_rcp_f32_e32 v144, v141
	s_nop 0
	v_fma_f32 v145, -v141, v144, 1.0
	v_fmac_f32_e32 v144, v145, v144
	s_nop 0
	v_div_scale_f32 v145, vcc, 1.0, v134, 1.0
	v_mul_f32_e64 v189, v145, v144
	v_fma_f32 v190, -v141, v189, v145
	v_fmac_f32_e32 v189, v190, v144
	s_nop 0
	v_fma_f32 v141, -v141, v189, v145
	v_div_fmas_f32 v141, v141, v144, v189
	v_div_fixup_f32 v141, v141, v134, 1.0
	v_add_f32_e64 v145, v130, v141
	v_mul_f32_e32 v130, 0xbfb8aa3b, v135
	v_exp_f32_e32 v130, v130
	s_nop 0
	v_add_f32_e64 v130, 1.0, v130
	v_div_scale_f32 v134, s[8:9], v130, v130, 1.0
	v_rcp_f32_e32 v135, v134
	s_nop 0
	v_fma_f32 v144, -v134, v135, 1.0
	v_fmac_f32_e32 v135, v144, v135
	s_nop 0
	v_div_scale_f32 v144, vcc, 1.0, v130, 1.0
	v_mul_f32_e64 v189, v144, v135
	v_fma_f32 v190, -v134, v189, v144
	v_fmac_f32_e32 v189, v190, v135
	s_nop 0
	v_fma_f32 v134, -v134, v189, v144
	v_div_fmas_f32 v134, v134, v135, v189
	v_div_fixup_f32 v135, v134, v130, 1.0
	v_mul_f32_e32 v130, 0xbfb8aa3b, v136
	v_exp_f32_e32 v130, v130
	v_add_f32_e32 v144, v131, v135
	v_add_f32_e64 v130, 1.0, v130
	v_div_scale_f32 v131, s[8:9], v130, v130, 1.0
	v_rcp_f32_e32 v134, v131
	s_nop 0
	v_fma_f32 v136, -v131, v134, 1.0
	v_fmac_f32_e32 v134, v136, v134
	s_nop 0
	v_div_scale_f32 v136, vcc, 1.0, v130, 1.0
	v_mul_f32_e64 v189, v136, v134
	v_fma_f32 v190, -v131, v189, v136
	v_fmac_f32_e32 v189, v190, v134
	s_nop 0
	v_fma_f32 v131, -v131, v189, v136
	v_div_fmas_f32 v131, v131, v134, v189
	v_div_fixup_f32 v134, v131, v130, 1.0
	v_mul_f32_e32 v130, 0xbfb8aa3b, v137
	v_exp_f32_e32 v130, v130
	v_add_f32_e32 v136, v132, v134
	v_add_f32_e64 v130, 1.0, v130
	v_div_scale_f32 v131, s[8:9], v130, v130, 1.0
	v_rcp_f32_e32 v132, v131
	s_nop 0
	v_fma_f32 v137, -v131, v132, 1.0
	v_fmac_f32_e32 v132, v137, v132
	s_nop 0
	v_div_scale_f32 v137, vcc, 1.0, v130, 1.0
	v_mul_f32_e64 v189, v137, v132
	v_fma_f32 v190, -v131, v189, v137
	v_fmac_f32_e32 v189, v190, v132
	s_nop 0
	v_fma_f32 v131, -v131, v189, v137
	v_div_fmas_f32 v131, v131, v132, v189
	v_div_fixup_f32 v131, v131, v130, 1.0
	v_max_f32_e32 v130, v154, v183
	v_max_f32_e32 v137, v184, v185
	v_add_f32_e64 v132, v133, v131
	v_min_f32_e32 v133, v154, v183
	v_min_f32_e32 v189, v184, v185
	v_max_f32_e32 v191, v130, v137
	v_min_f32_e32 v130, v130, v137
	v_max3_f32 v193, v130, v133, v189
	v_max_f32_e32 v130, v188, v187
	v_max_f32_e32 v137, v151, v148
	v_min_f32_e32 v133, v188, v187
	v_min_f32_e32 v189, v151, v148
	v_max_f32_e32 v190, v130, v137
	v_min_f32_e32 v130, v130, v137
	v_max3_f32 v192, v130, v133, v189
	v_max_f32_e32 v130, v153, v152
	v_max_f32_e32 v137, v143, v140
	v_pk_add_f32 v[190:191], v[190:191], v[192:193]
	v_min_f32_e32 v133, v153, v152
	v_min_f32_e32 v189, v143, v140
	v_max_f32_e32 v192, v130, v137
	v_min_f32_e32 v130, v130, v137
	v_max3_f32 v130, v130, v133, v189
	v_max_f32_e32 v133, v145, v144
	v_max_f32_e32 v189, v136, v132
	v_cmp_gt_f32_e32 vcc, v190, v191
	v_add_f32_e32 v130, v192, v130
	v_min_f32_e32 v137, v145, v144
	v_min_f32_e32 v192, v136, v132
	v_max_f32_e64 v193, v133, v189
	v_min_f32_e32 v133, v133, v189
	v_cndmask_b32_e32 v189, v191, v190, vcc
	v_max3_f32 v133, v133, v137, v192
	v_cndmask_b32_e64 v137, 0, 1, vcc
	v_cmp_gt_f32_e32 vcc, v130, v189
	v_add_f32_e32 v133, v193, v133
	s_nop 0
	v_cndmask_b32_e32 v130, v189, v130, vcc
	v_cndmask_b32_e64 v137, v137, 2, vcc
	v_cmp_ngt_f32_e32 vcc, v133, v130
	s_nop 1
	v_cndmask_b32_e32 v130, 3, v137, vcc
	v_cmp_ne_u32_e32 vcc, 0, v130
	s_and_saveexec_b64 s[10:11], vcc
	s_cbranch_execz .LBB0_1081
	v_cmp_lt_i32_e64 s[8:9], 1, v130
	s_and_saveexec_b64 s[12:13], s[8:9]
	s_cbranch_execz .LBB0_1080
	v_cmp_ne_u32_e64 s[8:9], 2, v130
	s_and_saveexec_b64 s[14:15], s[8:9]
	s_xor_b64 s[8:9], exec, s[14:15]
	s_andn2_saveexec_b64 s[8:9], s[8:9]
	v_mov_b32_e32 v145, v153
	s_or_b64 exec, exec, s[8:9]
	v_mov_b32_e32 v188, v145

.LBB0_1081:
	s_or_b64 exec, exec, s[10:11]
	s_and_saveexec_b64 s[10:11], vcc
	v_readlane_b32 s36, v254, 5
	v_readlane_b32 s42, v254, 34
	s_mov_b32 s93, s16
	s_nop 0
	v_readlane_b32 s37, v254, 6
	v_readlane_b32 s43, v254, 35
	v_readlane_b32 s50, v254, 31
	v_readlane_b32 s51, v254, 8
	s_cbranch_execz .LBB0_1106
	s_nop 0
	v_cmp_lt_i32_e64 s[8:9], 1, v130
	s_and_saveexec_b64 s[12:13], s[8:9]
	s_cbranch_execz .LBB0_1088
	v_cmp_ne_u32_e64 s[8:9], 2, v130
	s_and_saveexec_b64 s[14:15], s[8:9]
	s_xor_b64 s[8:9], exec, s[14:15]
	s_andn2_saveexec_b64 s[8:9], s[8:9]
	v_mov_b32_e32 v141, v149
	s_or_b64 exec, exec, s[8:9]
	v_mov_b32_e32 v186, v141

.LBB0_1090:
	v_cmp_lt_i32_e64 s[8:9], 1, v130
	s_and_saveexec_b64 s[12:13], s[8:9]
	s_xor_b64 s[12:13], exec, s[12:13]
	s_cbranch_execz .LBB0_1094
	s_nop 0
	v_cmp_ne_u32_e64 s[8:9], 2, v130
	s_and_saveexec_b64 s[14:15], s[8:9]
	v_mov_b32_e32 v142, v135
	s_or_b64 exec, exec, s[14:15]
.LBB0_1094:
	s_andn2_saveexec_b64 s[8:9], s[12:13]
	v_mov_b32_e32 v142, v150
	s_or_b64 exec, exec, s[8:9]
	v_mov_b32_e64 v155, v142
	s_or_b64 exec, exec, s[10:11]
	s_and_saveexec_b64 s[10:11], vcc
	s_cbranch_execnz .LBB0_1115

.LBB0_1098:
	v_cmp_lt_i32_e64 s[8:9], 1, v130
	s_and_saveexec_b64 s[12:13], s[8:9]
	s_xor_b64 s[12:13], exec, s[12:13]
	s_cbranch_execz .LBB0_1102
	s_nop 0
	v_cmp_ne_u32_e64 s[8:9], 2, v130
	s_and_saveexec_b64 s[14:15], s[8:9]
	v_mov_b32_e32 v139, v134
	s_or_b64 exec, exec, s[14:15]
.LBB0_1102:
	s_andn2_saveexec_b64 s[8:9], s[12:13]
	v_mov_b32_e32 v139, v147
	s_or_b64 exec, exec, s[8:9]
	v_mov_b32_e64 v156, v139
	s_or_b64 exec, exec, s[10:11]
	s_and_saveexec_b64 s[10:11], vcc
	s_cbranch_execnz .LBB0_1123

.LBB0_1107:
	v_cmp_lt_i32_e64 s[8:9], 1, v130
	s_and_saveexec_b64 s[12:13], s[8:9]
	s_xor_b64 s[12:13], exec, s[12:13]
	s_cbranch_execz .LBB0_1111
	s_nop 0
	v_cmp_ne_u32_e64 s[8:9], 2, v130
	s_and_saveexec_b64 s[14:15], s[8:9]
	v_mov_b32_e32 v152, v144
	s_or_b64 exec, exec, s[14:15]
.LBB0_1111:
	s_andn2_saveexec_b64 s[8:9], s[12:13]
	v_mov_b32_e32 v152, v187
	s_or_b64 exec, exec, s[8:9]
	v_mov_b32_e64 v183, v152
	s_or_b64 exec, exec, s[10:11]
	s_and_saveexec_b64 s[10:11], vcc
	s_cbranch_execnz .LBB0_1090

.LBB0_1115:
	v_cmp_lt_i32_e64 s[8:9], 1, v130
	s_and_saveexec_b64 s[12:13], s[8:9]
	s_xor_b64 s[12:13], exec, s[12:13]
	s_cbranch_execz .LBB0_1119
	s_nop 0
	v_cmp_ne_u32_e64 s[8:9], 2, v130
	s_and_saveexec_b64 s[14:15], s[8:9]
	v_mov_b32_e32 v143, v136
	s_or_b64 exec, exec, s[14:15]
.LBB0_1119:
	s_andn2_saveexec_b64 s[8:9], s[12:13]
	v_mov_b32_e32 v143, v151
	s_or_b64 exec, exec, s[8:9]
	v_mov_b32_e64 v184, v143
	s_or_b64 exec, exec, s[10:11]
	s_and_saveexec_b64 s[10:11], vcc
	s_cbranch_execnz .LBB0_1098

.LBB0_1123:
	v_cmp_lt_i32_e64 s[8:9], 1, v130
	s_and_saveexec_b64 s[12:13], s[8:9]
	s_xor_b64 s[12:13], exec, s[12:13]
	s_cbranch_execz .LBB0_1127
	s_nop 0
	v_cmp_ne_u32_e64 s[8:9], 2, v130
	s_and_saveexec_b64 s[14:15], s[8:9]
	v_mov_b32_e32 v140, v132
	s_or_b64 exec, exec, s[14:15]

.LBB0_1137:
	s_or_b64 exec, exec, s[8:9]
	v_cmp_gt_f32_e32 vcc, v183, v154
	s_nop 1
	v_cndmask_b32_e32 v132, v154, v183, vcc
	v_cmp_gt_f32_e64 s[8:9], v184, v132
	v_cndmask_b32_e64 v131, 0, 1, vcc
	s_nop 0
	s_nop 0
	v_cndmask_b32_e64 v132, v132, v184, s[8:9]
	v_cndmask_b32_e64 v131, v131, 2, s[8:9]
	v_cmp_ngt_f32_e64 s[10:11], v185, v132
	s_nop 1
	s_nop 0
	v_cndmask_b32_e64 v131, 3, v131, s[10:11]
	v_cmp_eq_u32_e64 s[12:13], 0, v131
	v_cmp_ne_u32_e64 s[14:15], 1, v131
	s_or_b64 s[12:13], s[12:13], vcc
	s_and_b64 vcc, s[14:15], s[12:13]
	v_cndmask_b32_e32 v133, v154, v183, vcc
	s_nop 0
	v_cndmask_b32_e64 v132, 0, 1, vcc
	v_cmp_gt_f32_e32 vcc, v184, v133
	s_nop 1
	v_cndmask_b32_e64 v134, v132, 2, vcc
	v_cndmask_b32_e32 v135, v133, v184, vcc
	s_and_b64 vcc, s[8:9], s[10:11]
	v_cndmask_b32_e32 v133, v135, v133, vcc
	v_cndmask_b32_e32 v132, v134, v132, vcc
	v_cmp_gt_f32_e32 vcc, v185, v133
	s_and_b64 s[8:9], s[10:11], vcc
	v_cndmask_b32_e64 v132, v132, 3, s[8:9]
	v_min_u32_e32 v133, v131, v132
	v_max_u32_e32 v131, v131, v132
	v_cmp_eq_u32_e32 vcc, 1, v133
	s_nop 0
	v_cmp_eq_u32_e64 s[8:9], 0, v133
	v_cmp_eq_u32_e64 s[10:11], 2, v131
	v_cndmask_b32_e32 v132, v156, v155, vcc
	s_nop 0
	v_cndmask_b32_e64 v96, v132, v96, s[8:9]
	v_cndmask_b32_e64 v132, v157, v156, s[10:11]
	v_cmp_eq_u32_e64 s[10:11], 1, v131
	s_nop 1
	s_nop 0
	v_cndmask_b32_e64 v132, v132, v155, s[10:11]
	v_add_f32_e64 v133, v96, v132
	v_div_scale_f32 v134, s[10:11], v133, v133, 1.0
	v_rcp_f32_e32 v135, v134
	s_nop 0
	v_fma_f32 v136, -v134, v135, 1.0
	v_fmac_f32_e32 v135, v136, v135
	s_nop 0
	v_div_scale_f32 v136, s[10:11], 1.0, v133, 1.0
	v_mul_f32_e64 v137, v136, v135
	v_fma_f32 v138, -v134, v137, v136
	v_fmac_f32_e32 v137, v138, v135
	v_add_u32_e32 v138, -1, v131
	v_add_u32_e32 v131, 1, v131
	v_cndmask_b32_e32 v131, 5, v131, vcc
	v_cndmask_b32_e64 v131, v131, v138, s[8:9]
	v_mad_u32_u24 v130, v130, 6, v131
	v_lshl_add_u32 v131, v130, 2, 0
	v_add_u32_e32 v131, 0x16200, v131
	v_mov_b32_e64 v138, 1
	ds_add_rtn_u32 v131, v131, v138
	v_fma_f32 v134, -v134, v137, v136
	s_mov_b64 vcc, s[10:11]
	s_nop 0
	v_div_fmas_f32 v134, v134, v135, v137
	v_div_fixup_f32 v133, v134, v133, 1.0
	s_waitcnt lgkmcnt(0)
	s_nop 0
	v_lshl_or_b32 v130, v131, 8, v130
	ds_write_b32 v174, v130
	v_mul_f32_e32 v130, v96, v133
	v_mul_f32_e32 v131, v132, v133
	ds_write_b64 v175, v[130:131]
.LBB0_1138:
	s_or_b64 exec, exec, s[20:21]
	s_waitcnt lgkmcnt(0)
	s_barrier
	s_and_saveexec_b64 s[8:9], s[4:5]
	s_cbranch_execz .LBB0_1142
	s_nop 0
	ds_read_b32 v130, v176
	v_mov_b32_e64 v96, 0
	s_waitcnt lgkmcnt(0)
	v_cmp_ne_u32_e32 vcc, 0, v130
	s_and_saveexec_b64 s[10:11], vcc
	s_cbranch_execz .LBB0_1141
	global_atomic_add v96, v[164:165], v130, off sc0

.LBB0_1142:
	s_or_b64 exec, exec, s[8:9]
	s_waitcnt lgkmcnt(0)
	s_barrier
	s_and_saveexec_b64 s[8:9], s[6:7]
	s_cbranch_execz .LBB0_1144
	s_nop 0
	ds_read_b32 v96, v178
	ds_read_b64 v[132:133], v179
	s_waitcnt lgkmcnt(1)
	s_nop 0
	v_and_b32_e32 v131, 0xff, v96
	v_ashrrev_i32_e32 v130, 8, v96
	v_lshlrev_b32_e32 v96, 16, v131
	v_lshl_add_u32 v131, v131, 2, 0
	v_add_u32_e32 v131, 0x16280, v131
	ds_read_b32 v134, v131
	v_ashrrev_i32_e32 v131, 31, v130
	s_waitcnt lgkmcnt(0)
	v_ashrrev_i32_e32 v135, 31, v134
	s_nop 0
	v_lshl_add_u64 v[130:131], v[134:135], 0, v[130:131]
	v_lshl_add_u64 v[134:135], v[130:131], 0, v[96:97]
	v_add_u32_e64 v130, s26, v158
	v_lshl_add_u64 v[136:137], v[134:135], 2, s[90:91]
	v_mov_b32_e32 v131, v132
	v_mov_b32_e32 v132, v133
	v_mov_b32_e64 v133, v97
	v_lshl_add_u64 v[134:135], v[134:135], 4, s[54:55]
	global_store_dword v[136:137], v130, off
	global_store_dwordx4 v[134:135], v[130:133], off

.LBB0_1146:
	s_cmp_ge_i32 s22, s37
	s_waitcnt lgkmcnt(0)
	s_barrier
	s_cbranch_scc1 .LBB0_1192
	s_mov_b32 s0, s97
	s_waitcnt vmcnt(0)
	s_barrier
	s_nop 0
	s_nop 0
	v_mbcnt_lo_u32_b32 v0, -1, s0
	v_mbcnt_hi_u32_b32 v0, -1, v0
	v_cmp_eq_u32_e32 vcc, s65, v0
	s_and_saveexec_b64 s[38:39], vcc
	s_cbranch_execz .LBB0_1191
	s_nop 0
	v_readlane_b32 s40, v253, 12
	v_readlane_b32 s0, v253, 14
	v_readlane_b32 s23, v253, 17
	v_readlane_b32 s41, v253, 13
	v_mov_b32_e32 v0, s0
	s_waitcnt vmcnt(0) expcnt(0) lgkmcnt(0)
	ds_read_b32 v2, v0
	ds_read_b32 v0, v0 offset:4
	s_waitcnt lgkmcnt(1)
	v_cmp_ne_u32_e32 vcc, 0, v2
	s_cbranch_vccnz .LBB0_1162
	s_nop 0
	v_readlane_b32 s0, v253, 6
	v_readlane_b32 s1, v253, 7
	s_load_dwordx2 s[4:5], s[0:1], 0x4
	s_add_u32 s0, s40, 0x1000
	s_addc_u32 s1, s41, 0
	s_nop 0
	s_add_u32 s2, s40, 0x1100
	s_addc_u32 s3, s41, 0
	s_waitcnt lgkmcnt(0)
	s_mul_i32 s28, s4, s61
	s_nop 0
	s_add_u32 s4, s40, 0x1200
	s_mul_i32 s28, s28, s5
	s_addc_u32 s5, s41, 0
	s_add_u32 s6, s40, 0x1300
	s_addc_u32 s7, s41, 0
	s_mov_b32 s29, 1
	s_mov_b64 s[8:9], 0
	s_branch .LBB0_1152

.LBB0_1152:
	v_mov_b64_e32 v[12:13], s[40:41]
	flat_load_dword v1, v[12:13] offset:1024 sc1
	flat_load_dword v0, v[12:13] offset:1280 sc1
	flat_load_dword v2, v[12:13] offset:1536 sc1
	s_or_b64 s[14:15], s[14:15], exec
	s_or_b64 s[12:13], s[12:13], exec
	s_waitcnt vmcnt(0) lgkmcnt(0)
	v_add_u32_e32 v3, v0, v1
	v_add_u32_e64 v4, v3, v2
	flat_load_dword v3, v[12:13] offset:1792 sc1
	s_waitcnt vmcnt(0) lgkmcnt(0)
	v_add_u32_e32 v5, v4, v3
	flat_load_dword v4, v[12:13] offset:2048 sc1
	s_waitcnt vmcnt(0) lgkmcnt(0)
	v_add_u32_e32 v6, v5, v4
	flat_load_dword v5, v[12:13] offset:2304 sc1
	s_waitcnt vmcnt(0) lgkmcnt(0)
	v_add_u32_e32 v7, v6, v5
	flat_load_dword v6, v[12:13] offset:2560 sc1
	s_waitcnt vmcnt(0) lgkmcnt(0)
	v_add_u32_e32 v8, v7, v6
	flat_load_dword v7, v[12:13] offset:2816 sc1
	s_waitcnt vmcnt(0) lgkmcnt(0)
	v_add_u32_e32 v9, v8, v7
	flat_load_dword v8, v[12:13] offset:3072 sc1
	s_waitcnt vmcnt(0) lgkmcnt(0)
	v_add_u32_e32 v10, v9, v8
	flat_load_dword v9, v[12:13] offset:3328 sc1
	s_waitcnt vmcnt(0) lgkmcnt(0)
	v_add_u32_e32 v11, v10, v9
	flat_load_dword v10, v[12:13] offset:3584 sc1
	s_waitcnt vmcnt(0) lgkmcnt(0)
	v_add_u32_e32 v14, v11, v10
	flat_load_dword v11, v[12:13] offset:3840 sc1
	v_mov_b64_e32 v[12:13], s[0:1]
	s_nop 0
	flat_load_dword v12, v[12:13] sc1
	s_waitcnt vmcnt(0) lgkmcnt(0)
	v_add_u32_e32 v14, v14, v11
	v_add_u32_e32 v16, v14, v12
	v_mov_b64_e32 v[14:15], s[2:3]
	flat_load_dword v13, v[14:15] sc1
	v_mov_b64_e32 v[14:15], s[4:5]
	s_nop 0
	flat_load_dword v14, v[14:15] sc1
	s_waitcnt vmcnt(0) lgkmcnt(0)
	v_add_u32_e32 v16, v16, v13
	v_add_u32_e32 v18, v16, v14
	v_mov_b64_e32 v[16:17], s[6:7]
	flat_load_dword v15, v[16:17] sc1
	s_waitcnt vmcnt(0) lgkmcnt(0)
	v_add_u32_e32 v16, v18, v15
	v_cmp_ne_u32_e32 vcc, s28, v16
	s_and_saveexec_b64 s[16:17], vcc
	s_cbranch_execz .LBB0_1151
	s_nop 0
	s_and_b32 s20, s29, 0xff
	s_mov_b64 s[18:19], -1
	s_cmp_eq_u32 s20, 0
	s_mov_b64 s[24:25], -1
	s_mov_b64 s[20:21], -1
	s_sleep 1
	s_cbranch_scc1 .LBB0_1155
	s_and_saveexec_b64 s[26:27], s[24:25]
	s_cbranch_execz .LBB0_1150
	s_branch .LBB0_1158

.LBB0_1162:
	s_lshl_b32 s20, s23, 6
	s_nop 0
	s_add_i32 s96, s20, 0x500
	s_lshl_b64 s[0:1], s[96:97], 2
	s_add_u32 s0, s40, s0
	s_addc_u32 s1, s41, s1
	v_mov_b64_e32 v[4:5], s[0:1]
	v_mov_b32_e64 v1, 1
	flat_atomic_add v3, v[4:5], v1 sc0
	v_cvt_f32_u32_e32 v1, v2
	v_sub_u32_e32 v4, 0, v2
	v_rcp_iflag_f32_e32 v1, v1
	s_nop 0
	v_mul_f32_e32 v1, 0x4f7ffffe, v1
	v_cvt_u32_f32_e32 v1, v1
	s_nop 0
	v_mul_lo_u32 v4, v4, v1
	v_mul_hi_u32 v4, v1, v4
	v_add_u32_e32 v1, v1, v4
	s_waitcnt vmcnt(0) lgkmcnt(0)
	v_mul_hi_u32 v1, v3, v1
	v_mul_lo_u32 v4, v1, v2
	v_sub_u32_e32 v4, v3, v4
	v_cmp_ge_u32_e32 vcc, v4, v2
	v_add_u32_e32 v5, 1, v1
	s_nop 0
	v_cndmask_b32_e32 v1, v1, v5, vcc
	v_sub_u32_e32 v5, v4, v2
	v_cndmask_b32_e32 v4, v4, v5, vcc
	v_cmp_ge_u32_e32 vcc, v4, v2
	v_add_u32_e32 v4, 1, v1
	s_nop 0
	v_cndmask_b32_e32 v1, v1, v4, vcc
	v_add_u32_e32 v4, 1, v3
	v_mad_u64_u32 v[2:3], s[0:1], v2, v1, v[2:3]
	v_cmp_ne_u32_e32 vcc, v4, v2
	s_and_saveexec_b64 s[0:1], vcc
	s_xor_b64 s[0:1], exec, s[0:1]
	s_cbranch_execz .LBB0_1175
	s_add_i32 s96, s20, 0x900
	s_lshl_b64 s[2:3], s[96:97], 2
	s_add_u32 s4, s40, s2
	s_addc_u32 s5, s41, s3
	v_mov_b64_e32 v[2:3], s[4:5]
	flat_load_dword v0, v[2:3] sc1
	s_waitcnt vmcnt(0) lgkmcnt(0)
	v_cmp_eq_u32_e32 vcc, v0, v1
	s_and_saveexec_b64 s[2:3], vcc
	s_cbranch_execz .LBB0_1174
	s_mov_b32 s21, 1
	s_mov_b64 s[6:7], 0
	s_branch .LBB0_1166

.LBB0_1192:
	s_cmp_gt_i32 s36, s22
	s_cselect_b64 s[0:1], -1, 0
	s_cmp_ge_i32 s22, s37
	s_cselect_b64 s[2:3], -1, 0
	s_or_b64 s[4:5], s[0:1], s[2:3]
	s_and_b64 vcc, exec, s[4:5]
	s_mul_i32 s56, s72, 0x4800
	s_cbranch_vccnz .LBB0_1291
	s_mov_b32 s0, s97
	s_waitcnt vmcnt(0)
	s_nop 0
	v_mbcnt_lo_u32_b32 v0, -1, s0
	v_mbcnt_hi_u32_b32 v0, -1, v0
	v_add_u32_e64 v0, s64, v0
	v_cmp_gt_i32_e32 vcc, 24, v0
	s_and_saveexec_b64 s[0:1], vcc
	s_cbranch_execz .LBB0_1195
	v_ashrrev_i32_e32 v1, 31, v0
	v_lshl_add_u64 v[2:3], v[0:1], 2, s[80:81]
	global_load_dword v2, v[2:3], off sc1
	v_lshl_add_u32 v1, v0, 2, 0
	v_add_u32_e32 v1, 0x20240, v1
	s_waitcnt vmcnt(0)
	s_nop 0
	ds_write_b32 v1, v2
.LBB0_1195:
	s_or_b64 exec, exec, s[0:1]
	v_cmp_eq_u32_e32 vcc, 0, v0
	s_waitcnt lgkmcnt(0)
	s_barrier
	s_and_saveexec_b64 s[0:1], vcc
	s_cbranch_execz .LBB0_1197
	s_add_i32 s2, 0, 0x20240
	v_mov_b32_e64 v1, s2
	ds_read_b128 v[2:5], v1
	v_readlane_b32 s2, v254, 30
	v_mov_b32_e32 v6, v97
	s_waitcnt lgkmcnt(0)
	v_add_u32_e32 v1, 0xff, v2
	v_ashrrev_i32_e32 v7, 8, v1
	s_nop 0
	v_add_u32_e32 v1, 0xff, v3
	v_ashrrev_i32_e32 v1, 8, v1
	v_add_u32_e32 v8, v1, v7
	v_add_u32_e32 v1, 0xff, v4
	v_ashrrev_i32_e32 v1, 8, v1
	v_add_u32_e32 v9, v1, v8
	v_mov_b32_e64 v1, s2
	ds_write_b128 v1, v[6:9]
	v_add_u32_e32 v1, 0xff, v5
	v_ashrrev_i32_e32 v1, 8, v1
	s_nop 0
	v_readlane_b32 s2, v255, 19
	v_add_u32_e32 v2, v1, v9
	s_nop 0
	v_mov_b32_e64 v1, s2
	ds_read_b128 v[4:7], v1
	v_readlane_b32 s2, v255, 20
	s_waitcnt lgkmcnt(0)
	s_nop 0
	v_add_u32_e32 v1, 0xff, v4
	v_ashrrev_i32_e32 v1, 8, v1
	v_add_u32_e32 v3, v1, v2
	v_add_u32_e32 v1, 0xff, v5
	v_ashrrev_i32_e32 v1, 8, v1
	v_add_u32_e32 v4, v1, v3
	v_add_u32_e32 v1, 0xff, v6
	v_ashrrev_i32_e32 v1, 8, v1
	v_add_u32_e32 v5, v1, v4
	v_mov_b32_e64 v1, s2
	ds_write_b128 v1, v[2:5]
	v_add_u32_e32 v1, 0xff, v7
	v_ashrrev_i32_e32 v1, 8, v1
	s_nop 0
	v_readlane_b32 s2, v255, 21
	v_add_u32_e32 v2, v1, v5
	s_nop 0
	v_mov_b32_e64 v1, s2
	ds_read_b128 v[4:7], v1
	v_readlane_b32 s2, v255, 22
	s_waitcnt lgkmcnt(0)
	s_nop 0
	v_add_u32_e32 v1, 0xff, v4
	v_ashrrev_i32_e32 v1, 8, v1
	v_add_u32_e32 v3, v1, v2
	v_add_u32_e32 v1, 0xff, v5
	v_ashrrev_i32_e32 v1, 8, v1
	v_add_u32_e32 v4, v1, v3
	v_add_u32_e32 v1, 0xff, v6
	v_ashrrev_i32_e32 v1, 8, v1
	v_add_u32_e32 v5, v1, v4
	v_mov_b32_e64 v1, s2
	ds_write_b128 v1, v[2:5]
	v_add_u32_e32 v1, 0xff, v7
	v_ashrrev_i32_e32 v1, 8, v1
	s_nop 0
	v_readlane_b32 s2, v255, 23
	v_add_u32_e32 v2, v1, v5
	s_nop 0
	v_mov_b32_e64 v1, s2
	ds_read_b128 v[4:7], v1
	v_readlane_b32 s2, v255, 24
	s_waitcnt lgkmcnt(0)
	s_nop 0
	v_add_u32_e32 v1, 0xff, v4
	v_ashrrev_i32_e32 v1, 8, v1
	v_add_u32_e32 v3, v1, v2
	v_add_u32_e32 v1, 0xff, v5
	v_ashrrev_i32_e32 v1, 8, v1
	v_add_u32_e32 v4, v1, v3
	v_add_u32_e32 v1, 0xff, v6
	v_ashrrev_i32_e32 v1, 8, v1
	v_add_u32_e32 v5, v1, v4
	v_mov_b32_e64 v1, s2
	ds_write_b128 v1, v[2:5]
	v_add_u32_e32 v1, 0xff, v7
	v_ashrrev_i32_e32 v1, 8, v1
	s_nop 0
	v_readlane_b32 s2, v255, 25
	v_add_u32_e32 v2, v1, v5
	s_nop 0
	v_mov_b32_e64 v1, s2
	ds_read_b128 v[4:7], v1
	v_readlane_b32 s2, v255, 26
	s_waitcnt lgkmcnt(0)
	s_nop 0
	v_add_u32_e32 v1, 0xff, v4
	v_ashrrev_i32_e32 v1, 8, v1
	v_add_u32_e32 v3, v1, v2
	v_add_u32_e32 v1, 0xff, v5
	v_ashrrev_i32_e32 v1, 8, v1
	v_add_u32_e32 v4, v1, v3
	v_add_u32_e32 v1, 0xff, v6
	v_ashrrev_i32_e32 v1, 8, v1
	v_add_u32_e32 v5, v1, v4
	v_mov_b32_e64 v1, s2
	ds_write_b128 v1, v[2:5]
	v_add_u32_e32 v1, 0xff, v7
	v_ashrrev_i32_e32 v1, 8, v1
	s_nop 0
	v_readlane_b32 s2, v255, 27
	v_add_u32_e32 v2, v1, v5
	s_nop 0
	v_mov_b32_e64 v1, s2
	ds_read_b128 v[4:7], v1
	v_readlane_b32 s2, v255, 28
	s_waitcnt lgkmcnt(0)
	s_nop 0
	v_add_u32_e32 v1, 0xff, v4
	v_ashrrev_i32_e32 v1, 8, v1
	v_add_u32_e32 v3, v1, v2
	v_add_u32_e32 v1, 0xff, v5
	v_ashrrev_i32_e32 v1, 8, v1
	v_add_u32_e32 v4, v1, v3
	v_add_u32_e32 v1, 0xff, v6
	v_ashrrev_i32_e32 v1, 8, v1
	v_add_u32_e32 v5, v1, v4
	v_mov_b32_e64 v1, s2
	ds_write_b128 v1, v[2:5]
	v_add_u32_e32 v1, 0xff, v7
	v_ashrrev_i32_e32 v1, 8, v1
	s_nop 0
	v_readlane_b32 s2, v254, 15
	v_add_u32_e32 v1, v1, v5
	s_nop 0
	v_mov_b32_e64 v2, s2
	ds_write_b32 v2, v1
.LBB0_1197:
	s_or_b64 exec, exec, s[0:1]
	s_nop 0
	v_readlane_b32 s0, v254, 15
	s_waitcnt lgkmcnt(0)
	s_barrier
	v_mov_b32_e64 v1, s0
	ds_read_b32 v1, v1
	s_waitcnt lgkmcnt(0)
	v_cmp_lt_i32_e32 vcc, v0, v1
	s_and_saveexec_b64 s[0:1], vcc
	s_cbranch_execz .LBB0_1243
	v_readlane_b32 s2, v255, 29
	s_nop 1
	v_mov_b32_e32 v1, s2
	ds_read_b32 v1, v1
	s_waitcnt lgkmcnt(0)
	v_cmp_ge_i32_e32 vcc, v0, v1
	v_mov_b32_e64 v1, 0
	s_and_saveexec_b64 s[2:3], vcc
	s_cbranch_execz .LBB0_1242
	v_readlane_b32 s6, v255, 30
	s_nop 1
	v_mov_b32_e32 v1, s6
	ds_read_b32 v1, v1
	s_waitcnt lgkmcnt(0)
	v_cmp_ge_i32_e32 vcc, v0, v1
	v_mov_b32_e64 v1, 1
	s_and_saveexec_b64 s[6:7], vcc
	s_cbranch_execz .LBB0_1241
	v_readlane_b32 s8, v255, 31
	s_nop 1
	v_mov_b32_e32 v1, s8
	ds_read_b32 v1, v1
	s_waitcnt lgkmcnt(0)
	v_cmp_ge_i32_e32 vcc, v0, v1
	v_mov_b32_e64 v1, 2
	s_and_saveexec_b64 s[8:9], vcc
	s_cbranch_execz .LBB0_1240
	v_readlane_b32 s10, v255, 20
	s_nop 1
	v_mov_b32_e32 v1, s10
	ds_read_b32 v1, v1
	s_waitcnt lgkmcnt(0)
	v_cmp_ge_i32_e32 vcc, v0, v1
	v_mov_b32_e64 v1, 3
	s_and_saveexec_b64 s[10:11], vcc
	s_cbranch_execz .LBB0_1239
	v_readlane_b32 s12, v255, 32
	s_nop 1
	v_mov_b32_e32 v1, s12
	ds_read_b32 v1, v1
	s_waitcnt lgkmcnt(0)
	v_cmp_ge_i32_e32 vcc, v0, v1
	v_mov_b32_e64 v1, 4
	s_and_saveexec_b64 s[12:13], vcc
	s_cbranch_execz .LBB0_1238
	v_readlane_b32 s14, v255, 33
	s_nop 1
	v_mov_b32_e32 v1, s14
	ds_read_b32 v1, v1
	s_waitcnt lgkmcnt(0)
	v_cmp_ge_i32_e32 vcc, v0, v1
	v_mov_b32_e64 v1, 5
	s_and_saveexec_b64 s[14:15], vcc
	s_cbranch_execz .LBB0_1237
	v_readlane_b32 s16, v255, 34
	s_nop 1
	v_mov_b32_e32 v1, s16
	ds_read_b32 v1, v1
	s_waitcnt lgkmcnt(0)
	v_cmp_ge_i32_e32 vcc, v0, v1
	v_mov_b32_e64 v1, 6
	s_and_saveexec_b64 s[16:17], vcc
	s_cbranch_execz .LBB0_1236
	v_readlane_b32 s18, v255, 22
	s_nop 1
	v_mov_b32_e32 v1, s18
	ds_read_b32 v1, v1
	s_waitcnt lgkmcnt(0)
	v_cmp_ge_i32_e32 vcc, v0, v1
	v_mov_b32_e64 v1, 7
	s_and_saveexec_b64 s[18:19], vcc
	s_cbranch_execz .LBB0_1235
	v_readlane_b32 s20, v255, 35
	s_nop 1
	v_mov_b32_e32 v1, s20
	ds_read_b32 v1, v1
	s_waitcnt lgkmcnt(0)
	v_cmp_ge_i32_e32 vcc, v0, v1
	v_mov_b32_e64 v1, 8
	s_and_saveexec_b64 s[20:21], vcc
	s_cbranch_execz .LBB0_1234
	v_readlane_b32 s22, v255, 36
	s_nop 1
	v_mov_b32_e32 v1, s22
	ds_read_b32 v1, v1
	s_waitcnt lgkmcnt(0)
	v_cmp_ge_i32_e32 vcc, v0, v1
	v_mov_b32_e64 v1, 9
	s_and_saveexec_b64 s[24:25], vcc
	s_cbranch_execz .LBB0_1233
	v_readlane_b32 s22, v255, 37
	s_nop 1
	v_mov_b32_e32 v1, s22
	ds_read_b32 v1, v1
	s_waitcnt lgkmcnt(0)
	v_cmp_ge_i32_e32 vcc, v0, v1
	v_mov_b32_e64 v1, 10
	s_and_saveexec_b64 s[26:27], vcc
	s_cbranch_execz .LBB0_1232
	v_readlane_b32 s22, v255, 24
	s_nop 1
	v_mov_b32_e32 v1, s22
	ds_read_b32 v1, v1
	s_waitcnt lgkmcnt(0)
	v_cmp_ge_i32_e32 vcc, v0, v1
	v_mov_b32_e64 v1, 11
	s_and_saveexec_b64 s[28:29], vcc
	s_cbranch_execz .LBB0_1231
	v_readlane_b32 s22, v255, 38
	s_nop 1
	v_mov_b32_e32 v1, s22
	ds_read_b32 v1, v1
	s_waitcnt lgkmcnt(0)
	v_cmp_ge_i32_e32 vcc, v0, v1
	v_mov_b32_e64 v1, 12
	s_and_saveexec_b64 s[30:31], vcc
	s_cbranch_execz .LBB0_1230
	v_readlane_b32 s22, v255, 39
	s_nop 1
	v_mov_b32_e32 v1, s22
	ds_read_b32 v1, v1
	s_waitcnt lgkmcnt(0)
	v_cmp_ge_i32_e32 vcc, v0, v1
	v_mov_b32_e64 v1, 13
	s_and_saveexec_b64 s[38:39], vcc
	s_cbranch_execz .LBB0_1229
	v_readlane_b32 s22, v255, 40
	s_nop 1
	v_mov_b32_e32 v1, s22
	ds_read_b32 v1, v1
	s_waitcnt lgkmcnt(0)
	v_cmp_ge_i32_e32 vcc, v0, v1
	v_mov_b32_e64 v1, 14
	s_and_saveexec_b64 s[40:41], vcc
	s_cbranch_execz .LBB0_1228
	v_readlane_b32 s22, v255, 26
	s_nop 1
	v_mov_b32_e32 v1, s22
	ds_read_b32 v1, v1
	s_waitcnt lgkmcnt(0)
	v_cmp_ge_i32_e32 vcc, v0, v1
	v_mov_b32_e64 v1, 15
	s_and_saveexec_b64 s[48:49], vcc
	s_cbranch_execz .LBB0_1227
	v_readlane_b32 s22, v255, 41
	s_nop 1
	v_mov_b32_e32 v1, s22
	ds_read_b32 v1, v1
	s_waitcnt lgkmcnt(0)
	v_cmp_ge_i32_e32 vcc, v0, v1
	v_mov_b32_e64 v1, 16
	s_and_saveexec_b64 s[58:59], vcc
	s_cbranch_execz .LBB0_1226
	v_readlane_b32 s22, v255, 42
	s_mov_b64 s[46:47], s[80:81]
	s_mov_b32 s50, s93
	v_mov_b32_e64 v1, s22
	ds_read_b32 v1, v1
	s_waitcnt lgkmcnt(0)
	v_cmp_ge_i32_e32 vcc, v0, v1
	v_mov_b32_e64 v1, 17
	s_and_saveexec_b64 s[60:61], vcc
	s_cbranch_execz .LBB0_1225
	v_readlane_b32 s22, v255, 43
	s_nop 1
	v_mov_b32_e32 v1, s22
	ds_read_b32 v1, v1
	s_waitcnt lgkmcnt(0)
	v_cmp_ge_i32_e32 vcc, v0, v1
	v_mov_b32_e64 v1, 18
	s_and_saveexec_b64 s[64:65], vcc
	s_cbranch_execz .LBB0_1224
	v_readlane_b32 s22, v255, 28
	s_nop 1
	v_mov_b32_e32 v1, s22
	ds_read_b32 v1, v1
	s_waitcnt lgkmcnt(0)
	v_cmp_ge_i32_e32 vcc, v0, v1
	v_mov_b32_e64 v1, 19
	s_and_saveexec_b64 s[22:23], vcc
	s_cbranch_execz .LBB0_1223
	v_readlane_b32 s36, v255, 44
	s_nop 1
	v_mov_b32_e32 v1, s36
	ds_read_b32 v1, v1
	s_waitcnt lgkmcnt(0)
	v_cmp_ge_i32_e32 vcc, v0, v1
	v_mov_b32_e64 v1, 20
	s_and_saveexec_b64 s[80:81], vcc
	s_cbranch_execz .LBB0_1222
	v_readlane_b32 s36, v255, 45
	s_nop 1
	v_mov_b32_e32 v1, s36
	ds_read_b32 v1, v1
	s_waitcnt lgkmcnt(0)
	v_cmp_ge_i32_e32 vcc, v0, v1
	v_mov_b32_e64 v1, 21
	s_and_saveexec_b64 s[92:93], vcc
	s_cbranch_execz .LBB0_1221
	v_readlane_b32 s36, v255, 46
	s_nop 1
	v_mov_b32_e32 v1, s36
	ds_read_b32 v1, v1
	s_waitcnt lgkmcnt(0)
	v_cmp_lt_i32_e32 vcc, v0, v1
	s_nop 1
	s_nop 0
	v_cndmask_b32_e64 v1, 23, 22, vcc

.LBB0_1225:
	s_or_b64 exec, exec, s[60:61]
	s_nop 0
	v_readlane_b32 s36, v254, 5
	v_readlane_b32 s42, v254, 34
	v_readlane_b32 s72, v254, 17
	v_readlane_b32 s61, v254, 3
	v_readlane_b32 s64, v254, 4
	s_mov_b32 s93, s50
	s_nop 0
	v_readlane_b32 s37, v254, 6
	v_readlane_b32 s43, v254, 35
	v_readlane_b32 s50, v254, 31
	v_readlane_b32 s65, v255, 47
	v_readlane_b32 s51, v254, 8
	v_readlane_b32 s73, v254, 18
	s_mov_b64 s[80:81], s[46:47]

.LBB0_1242:
	s_or_b64 exec, exec, s[2:3]
	v_readlane_b32 s2, v254, 30
	s_nop 1
	s_nop 0
	v_lshl_add_u32 v0, v0, 2, s2
	ds_write_b32 v0, v1 offset:256
.LBB0_1243:
	s_or_b64 exec, exec, s[0:1]
	s_nop 0
	v_readlane_b32 s0, v254, 15
	s_waitcnt lgkmcnt(0)
	s_barrier
	v_mov_b32_e64 v0, s0
	ds_read_b32 v0, v0
	s_ashr_i32 s57, s56, 31
	s_lshl_b64 s[0:1], s[56:57], 2
	s_add_u32 s0, s70, s0
	s_addc_u32 s1, s71, s1
	s_add_u32 s22, s0, 0x20000
	s_mov_b32 s0, s97
	s_waitcnt lgkmcnt(0)
	v_readfirstlane_b32 s26, v0
	v_lshlrev_b32_e32 v194, 3, v0
	s_addc_u32 s23, s1, 0
	s_nop 0
	v_mbcnt_lo_u32_b32 v0, -1, s0
	v_mbcnt_hi_u32_b32 v0, -1, v0
	v_readlane_b32 s0, v254, 40
	v_add_u32_e64 v8, s64, v0
	v_readlane_b32 s1, v254, 41
	s_mov_b32 s44, s93
	v_ashrrev_i32_e32 v195, 31, v194
	s_and_b64 vcc, exec, s[0:1]
	v_readfirstlane_b32 s8, v8
	s_cbranch_vccz .LBB0_1246
	v_cmp_lt_i32_e32 vcc, s50, v194
	s_mov_b64 s[0:1], 0
	s_mov_b32 s52, -1
	s_mov_b64 s[2:3], 0
	s_cbranch_vccz .LBB0_1247
	v_readlane_b32 s2, v254, 59
	s_add_i32 s2, s26, s2
	s_nop 0
	v_readlane_b32 s3, v254, 60
	s_mul_i32 s2, s2, s3
	s_nop 0
	v_readlane_b32 s3, v254, 61
	s_add_i32 s2, s2, s3
	s_ashr_i32 s3, s2, 31
	s_lshr_b32 s3, s3, 26
	s_add_i32 s3, s2, s3
	s_ashr_i32 s6, s3, 6
	s_lshl_b32 s6, s6, 3
	s_sub_i32 s7, s26, s6
	s_min_i32 s7, s7, 8
	s_abs_i32 s9, s7
	v_cvt_f32_u32_e32 v0, s9
	s_sub_i32 s11, 0, s9
	s_andn2_b32 s3, s3, 63
	s_sub_i32 s2, s2, s3
	v_rcp_iflag_f32_e32 v0, v0
	s_abs_i32 s3, s2
	s_xor_b32 s10, s2, s7
	s_ashr_i32 s10, s10, 31
	s_nop 0
	v_mul_f32_e32 v0, 0x4f7ffffe, v0
	v_cvt_u32_f32_e32 v0, v0
	s_nop 0
	v_readfirstlane_b32 s12, v0
	s_mul_i32 s11, s11, s12
	s_mul_hi_u32 s11, s12, s11
	s_add_i32 s12, s12, s11
	s_mul_hi_u32 s11, s3, s12
	s_mul_i32 s12, s11, s9
	s_sub_i32 s3, s3, s12
	s_add_i32 s13, s11, 1
	s_sub_i32 s12, s3, s9
	s_cmp_ge_u32 s3, s9
	s_cselect_b32 s11, s13, s11
	s_cselect_b32 s3, s12, s3
	s_add_i32 s12, s11, 1
	s_cmp_ge_u32 s3, s9
	s_cselect_b32 s3, s12, s11
	s_xor_b32 s3, s3, s10
	s_sub_i32 s93, s3, s10
	s_mul_i32 s3, s93, s7
	s_sub_i32 s2, s2, s3
	s_add_i32 s52, s6, s2
	s_mov_b64 s[2:3], -1
	s_branch .LBB0_1247

.LBB0_1247:
	v_readlane_b32 s6, v254, 50
	s_mul_i32 s6, s26, s6
	s_ashr_i32 s28, s6, 3
	s_add_i32 s6, s6, s26
	s_ashr_i32 s6, s6, 3
	s_sub_i32 s29, s6, s28
	s_lshl_b32 s30, s29, 3
	s_and_b64 vcc, exec, s[0:1]
	s_cbranch_vccz .LBB0_1250
	v_readlane_b32 s0, v254, 19
	s_cmp_lt_i32 s0, s30
	s_mov_b32 s52, -1
	s_cbranch_scc0 .LBB0_1250
	s_nop 0
	v_readlane_b32 s2, v254, 51
	s_sub_i32 s0, s29, s2
	s_min_i32 s0, s0, 8
	s_abs_i32 s1, s0
	v_cvt_f32_u32_e32 v0, s1
	s_ashr_i32 s3, s0, 31
	s_nop 0
	v_readlane_b32 s6, v255, 9
	s_xor_b32 s3, s6, s3
	v_rcp_iflag_f32_e32 v0, v0
	s_sub_i32 s6, 0, s1
	s_nop 0
	v_readlane_b32 s10, v255, 11
	s_add_i32 s2, s28, s2
	s_nop 0
	v_mul_f32_e32 v0, 0x4f7ffffe, v0
	v_cvt_u32_f32_e32 v0, v0
	s_nop 0
	v_readfirstlane_b32 s7, v0
	s_mul_i32 s6, s6, s7
	s_mul_hi_u32 s6, s7, s6
	s_add_i32 s7, s7, s6
	s_mul_hi_u32 s6, s10, s7
	s_mul_i32 s7, s6, s1
	s_sub_i32 s7, s10, s7
	s_add_i32 s9, s6, 1
	s_sub_i32 s10, s7, s1
	s_cmp_ge_u32 s7, s1
	s_cselect_b32 s6, s9, s6
	s_cselect_b32 s7, s10, s7
	s_add_i32 s9, s6, 1
	s_cmp_ge_u32 s7, s1
	s_cselect_b32 s1, s9, s6
	s_xor_b32 s1, s1, s3
	s_sub_i32 s93, s1, s3
	s_mul_i32 s0, s93, s0
	v_readlane_b32 s1, v255, 10
	s_sub_i32 s0, s1, s0
	s_add_i32 s52, s2, s0
	s_mov_b64 s[2:3], -1
.LBB0_1250:
	s_and_b64 vcc, exec, s[2:3]
	s_cbranch_vccz .LBB0_1286
	v_ashrrev_i32_e32 v1, 31, v8
	v_lshrrev_b32_e32 v1, 26, v1
	v_add_u32_e32 v1, v8, v1
	s_lshl_b64 s[0:1], s[72:73], 24
	v_ashrrev_i32_e32 v9, 6, v1
	v_bfe_i32 v1, v8, 27, 1
	s_add_u32 s0, s70, s0
	v_lshlrev_b32_e32 v0, 4, v8
	v_lshrrev_b32_e32 v1, 22, v1
	s_addc_u32 s1, s71, s1
	v_add_u32_e64 v1, v0, v1
	s_add_u32 s31, s0, 0x2e00000
	v_and_b32_e32 v1, 0xfffffc00, v1
	s_addc_u32 s38, s1, 0
	v_sub_u32_e32 v0, v0, v1
	s_lshl_b32 s0, s52, 2
	s_nop 0
	v_readlane_b32 s1, v254, 30
	v_lshrrev_b32_e32 v1, 4, v0
	s_add_i32 s0, s1, s0
	v_bitop3_b32 v10, v1, v0, 32 bitop3:0x6c
	v_mov_b32_e64 v1, s0
	ds_read_b32 v1, v1 offset:256
	v_ashrrev_i32_e32 v2, 31, v10
	v_lshrrev_b32_e32 v2, 26, v2
	v_add_u32_e64 v11, v10, v2
	v_lshlrev_b32_e32 v0, 3, v9
	s_waitcnt lgkmcnt(0)
	v_readfirstlane_b32 s12, v1
	s_lshl_b32 s0, s12, 2
	s_add_i32 s1, s1, s0
	s_add_i32 s0, s0, 0
	s_add_i32 s0, s0, 0x20240
	v_mov_b32_e32 v1, s1
	v_mov_b32_e32 v2, s0
	ds_read_b32 v1, v1
	ds_read_b32 v2, v2
	v_and_b32_e32 v0, -16, v0
	v_ashrrev_i32_e32 v12, 6, v11
	v_add_u32_e32 v199, v12, v0
	s_waitcnt lgkmcnt(1)
	v_sub_u32_e32 v249, s52, v1
	s_ashr_i32 s2, s8, 6
	v_lshlrev_b32_e32 v7, 8, v249
	s_ashr_i32 s13, s12, 31
	v_add_u32_e32 v235, 64, v199
	s_ashr_i32 s3, s8, 8
	s_lshl_b32 s39, s2, 10
	s_waitcnt lgkmcnt(0)
	v_add_u32_e32 v6, -1, v2
	v_add_u32_e32 v0, v7, v199
	s_lshl_b64 s[0:1], s[12:13], 18
	v_add_u32_e32 v2, v7, v235
	v_add_u32_e32 v236, 0x80, v199
	v_add_u32_e32 v237, 0xc0, v199
	v_min_i32_e32 v0, v0, v6
	s_add_u32 s0, s90, s0
	v_min_i32_e32 v2, v2, v6
	v_add_u32_e32 v4, v7, v236
	v_add_u32_e32 v7, v7, v237
	v_ashrrev_i32_e32 v1, 31, v0
	s_addc_u32 s1, s91, s1
	v_ashrrev_i32_e32 v3, 31, v2
	v_min_i32_e32 v4, v4, v6
	v_min_i32_e32 v6, v7, v6
	v_lshl_add_u64 v[0:1], v[0:1], 2, s[0:1]
	v_lshl_add_u64 v[2:3], v[2:3], 2, s[0:1]
	v_ashrrev_i32_e32 v5, 31, v4
	v_ashrrev_i32_e32 v7, 31, v6
	v_lshl_add_u64 v[4:5], v[4:5], 2, s[0:1]
	v_lshl_add_u64 v[6:7], v[6:7], 2, s[0:1]
	global_load_dword v0, v[0:1], off
	s_nop 0
	s_nop 0
	global_load_dword v1, v[2:3], off
	s_nop 0
	s_nop 0
	global_load_dword v2, v[4:5], off
	global_load_dword v3, v[6:7], off
	v_and_b32_e32 v6, 3, v12
	s_nop 0
	s_mov_b32 s0, 0x3fffe0
	v_and_or_b32 v6, v199, s0, v6
	s_mul_hi_i32 s0, s12, 0x2aaaaaab
	s_lshr_b32 s1, s0, 31
	s_add_i32 s0, s0, s1
	s_mul_i32 s1, s0, 6
	s_sub_i32 s1, s12, s1
	s_cmp_lt_u32 s1, 5
	s_cselect_b32 s6, 1, 2
	s_min_u32 s9, s1, 4
	s_add_i32 s7, s1, 1
	s_add_i32 s9, s9, -1
	s_cmp_lt_i32 s1, 3
	s_cselect_b32 s1, 0, s6
	s_cselect_b32 s6, s7, s9
	s_lshl_b32 s0, s0, 2
	s_or_b32 s1, s1, s0
	s_add_i32 s6, s6, s0
	s_cmp_lt_i32 s93, 4
	s_cselect_b32 s0, s1, s6
	s_ashr_i32 s1, s0, 31
	s_lshl_b32 s6, s93, 18
	s_nop 0
	s_and_b32 s6, s6, 0xc0000
	s_lshl_b64 s[0:1], s[0:1], 20
	s_nop 0
	v_and_b32_e32 v5, 0xc0, v11
	s_add_u32 s0, s31, s0
	v_sub_u32_e32 v5, v10, v5
	v_mov_b32_e64 v7, 1
	s_addc_u32 s1, s38, s1
	v_lshlrev_b32_e32 v4, 5, v9
	v_ashrrev_i16_sdwa v5, v7, sext(v5) dst_sel:DWORD dst_unused:UNUSED_PAD src0_sel:DWORD src1_sel:BYTE_0
	v_lshlrev_b32_e32 v7, 1, v199
	v_lshrrev_b32_e32 v9, 2, v199
	s_add_u32 s0, s0, s6
	v_and_b32_e32 v4, 32, v4
	v_bfe_i32 v5, v5, 0, 16
	v_and_b32_e32 v7, 24, v7
	v_and_b32_e32 v9, 4, v9
	s_addc_u32 s1, s1, 0
	s_add_i32 s40, s39, 0
	v_or3_b32 v6, v6, v9, v7
	v_add_lshl_u32 v238, v4, v5, 1
	s_add_i32 s41, s40, 0x10000
	s_add_i32 s45, s40, 0x12000
	v_lshl_add_u32 v196, v6, 10, v238
	s_mov_b32 m0, s41
	s_nop 0
	s_add_u32 s6, s0, 0x20000
	v_add_u32_e32 v202, 0x10000, v196
	global_load_lds_dwordx4 v196, s[0:1]
	s_mov_b32 m0, s45
	s_addc_u32 s7, s1, 0
	s_add_i32 s48, s40, 0x14000
	global_load_lds_dwordx4 v202, s[0:1]
	s_mov_b32 m0, s48
	s_nop 0
	s_add_i32 s49, s40, 0x16000
	global_load_lds_dwordx4 v196, s[6:7]
	s_mov_b32 m0, s49
	s_nop 0
	s_add_i32 s57, s40, 0x2000
	global_load_lds_dwordx4 v202, s[6:7]
	s_mov_b32 m0, s40
	s_nop 0
	s_add_i32 s58, s40, 0x4000
	s_add_i32 s59, s40, 0x6000
	v_mov_b32_e32 v197, v97
	v_mov_b32_e32 v203, v97
	v_mov_b32_e32 v209, v97
	v_mov_b32_e32 v207, v97
	s_cmp_eq_u32 s3, 1
	s_mov_b64 s[46:47], s[80:81]
	v_lshl_add_u64 v[6:7], s[0:1], 0, v[196:197]
	v_lshl_add_u64 v[4:5], s[0:1], 0, v[202:203]
	s_cselect_b64 s[6:7], -1, 0
	s_waitcnt vmcnt(0)
	v_lshl_add_u32 v208, v0, 10, v238
	v_lshl_add_u32 v206, v1, 10, v238
	global_load_lds_dwordx4 v208, s[78:79]
	s_mov_b32 m0, s57
	s_nop 0
	v_lshl_add_u32 v96, v2, 10, v238
	global_load_lds_dwordx4 v206, s[78:79]
	s_mov_b32 m0, s58
	s_nop 0
	v_lshl_add_u32 v204, v3, 10, v238
	global_load_lds_dwordx4 v96, s[78:79]
	s_mov_b32 m0, s59
	s_nop 0
	v_lshl_add_u64 v[0:1], s[78:79], 0, v[208:209]
	global_load_lds_dwordx4 v204, s[78:79]
	s_cmp_lg_u32 s3, 1
	s_nop 0
	v_lshl_add_u64 v[2:3], s[78:79], 0, v[206:207]
	s_cbranch_scc1 .LBB0_1253
	s_barrier
.LBB0_1253:
	v_and_b32_e32 v9, 15, v8
	v_lshrrev_b32_e32 v10, 4, v8
	s_lshl_b32 s2, s2, 5
	s_nop 0
	s_mov_b64 s[10:11], 0x80
	v_lshl_or_b32 v207, s3, 6, v9
	v_bfe_u32 v10, v10, 1, 1
	s_lshl_b32 s3, s3, 13
	s_nop 0
	s_and_b32 s2, s2, 0x60
	s_add_i32 m0, s40, 0x18000
	v_lshl_add_u64 v[6:7], v[6:7], 0, s[10:11]
	v_lshl_or_b32 v15, v10, 10, s3
	s_lshr_b32 s3, s2, 3
	s_waitcnt vmcnt(2)
	s_barrier
	s_nop 0
	global_load_lds_dwordx4 v[6:7], off
	v_lshl_add_u64 v[4:5], v[4:5], 0, s[10:11]
	s_add_i32 m0, s40, 0x1a000
	s_add_i32 s60, s40, 0x8000
	s_add_i32 s61, s40, 0xa000
	global_load_lds_dwordx4 v[4:5], off
	v_lshl_add_u64 v[0:1], v[0:1], 0, s[10:11]
	s_mov_b32 m0, s60
	s_nop 0
	s_add_u32 s0, s0, 0x20080
	global_load_lds_dwordx4 v[0:1], off
	v_lshl_add_u64 v[0:1], v[2:3], 0, s[10:11]
	s_mov_b32 m0, s61
	s_addc_u32 s1, s1, 0
	global_load_lds_dwordx4 v[0:1], off
	s_add_i32 m0, s40, 0x1c000
	v_lshl_add_u64 v[0:1], s[0:1], 0, v[196:197]
	global_load_lds_dwordx4 v[0:1], off
	v_lshl_add_u64 v[0:1], s[0:1], 0, v[202:203]
	s_add_i32 m0, s40, 0x1e000
	v_lshlrev_b32_e32 v12, 1, v8
	s_nop 0
	global_load_lds_dwordx4 v[0:1], off
	v_bfe_u32 v11, v8, 4, 2
	v_and_b32_e32 v12, 32, v12
	v_lshlrev_b32_e32 v13, 6, v9
	v_lshlrev_b32_e32 v8, 2, v8
	v_or_b32_e32 v10, s3, v10
	v_or_b32_e32 v14, v13, v12
	v_and_b32_e32 v8, 32, v8
	v_lshlrev_b32_e32 v10, 10, v10
	s_nop 0
	v_bitop3_b32 v12, v13, v8, v12 bitop3:0x36
	v_bitop3_b32 v209, v10, v14, v8 bitop3:0xf6
	v_or_b32_e32 v13, 16, v14
	s_nop 0
	v_bitop3_b32 v14, v14, v8, 16 bitop3:0x36
	s_waitcnt vmcnt(6)
	s_cmpk_lt_u32 s8, 0x100
	v_or_b32_e32 v12, v12, v15
	v_or_b32_e32 v14, v14, v15
	s_cselect_b64 s[8:9], -1, 0
	v_or_b32_e32 v0, v11, v9
	s_add_u32 s65, s70, 0xee00080
	v_bitop3_b32 v239, v13, v10, v8 bitop3:0xde
	s_mov_b32 s64, 0
	s_nop 0
	v_cmp_eq_u32_e64 s[0:1], 0, v0
	v_or_b32_e32 v240, 16, v207
	v_or_b32_e32 v241, 32, v207
	v_or_b32_e32 v242, 48, v207
	s_nop 0
	v_lshl_or_b32 v243, v11, 3, s2
	s_addc_u32 s80, s71, 0
	s_mov_b32 s27, -1
	v_add_u32_e32 v244, 0, v12
	v_add_u32_e32 v245, 0, v14
	v_mbcnt_lo_u32_b32 v0, -1, 0
	v_mbcnt_hi_u32_b32 v0, -1, v0
	v_and_b32_e32 v0, 16, v0
	v_xor_b32_e32 v244, v244, v0
	v_xor_b32_e32 v245, v245, v0
	v_xor_b32_e32 v209, v209, v0
	v_xor_b32_e32 v239, v239, v0
	v_mov_b32_e32 v246, v204
	v_mov_b32_e32 v247, v96
	s_barrier
.LBB0_1254:
	v_readlane_b32 s2, v254, 40
	v_readlane_b32 s3, v254, 41
	s_add_i32 s64, s64, 1
	s_and_b64 vcc, exec, s[2:3]
	s_cbranch_vccz .LBB0_1260
	s_nop 0
	v_readlane_b32 s2, v254, 38
	v_readlane_b32 s11, v254, 3
	s_mul_i32 s2, s64, s2
	s_mul_hi_u32 s3, s64, s11
	s_add_i32 s3, s3, s2
	s_mul_i32 s2, s64, s11
	s_add_u32 s14, s2, s50
	s_nop 0
	v_readlane_b32 s2, v254, 39
	s_addc_u32 s15, s3, s2
	v_cmp_lt_i64_e32 vcc, s[14:15], v[194:195]
	s_mov_b64 s[2:3], 0
	s_mov_b32 s13, s92
	s_mov_b32 s11, s81
	s_mov_b64 s[16:17], 0
	s_cbranch_vccz .LBB0_1257
	s_ashr_i32 s11, s14, 31
	s_lshr_b32 s11, s11, 29
	s_add_i32 s11, s14, s11
	s_ashr_i32 s13, s11, 3
	s_and_b32 s11, s11, -8
	s_sub_i32 s11, s14, s11
	s_lshr_b32 s14, s11, 31
	s_add_i32 s14, s26, s14
	s_mul_i32 s11, s14, s11
	s_add_i32 s11, s11, s13
	s_ashr_i32 s13, s11, 31
	s_lshr_b32 s13, s13, 26
	s_add_i32 s13, s11, s13
	s_ashr_i32 s14, s13, 6
	s_lshl_b32 s14, s14, 3
	s_sub_i32 s15, s26, s14
	s_min_i32 s15, s15, 8
	s_abs_i32 s16, s15
	v_cvt_f32_u32_e32 v0, s16
	s_sub_i32 s18, 0, s16
	s_andn2_b32 s13, s13, 63
	s_sub_i32 s13, s11, s13
	v_rcp_iflag_f32_e32 v0, v0
	s_abs_i32 s11, s13
	s_xor_b32 s17, s13, s15
	s_ashr_i32 s17, s17, 31
	s_nop 0
	v_mul_f32_e32 v0, 0x4f7ffffe, v0
	v_cvt_u32_f32_e32 v0, v0
	s_nop 0
	v_readfirstlane_b32 s19, v0
	s_mul_i32 s18, s18, s19
	s_mul_hi_u32 s18, s19, s18
	s_add_i32 s19, s19, s18
	s_mul_hi_u32 s18, s11, s19
	s_mul_i32 s19, s18, s16
	s_sub_i32 s11, s11, s19
	s_add_i32 s20, s18, 1
	s_sub_i32 s19, s11, s16
	s_cmp_ge_u32 s11, s16
	s_cselect_b32 s18, s20, s18
	s_cselect_b32 s11, s19, s11
	s_add_i32 s19, s18, 1
	s_cmp_ge_u32 s11, s16
	s_cselect_b32 s11, s19, s18
	s_xor_b32 s11, s11, s17
	s_sub_i32 s11, s11, s17
	s_mul_i32 s15, s11, s15
	s_sub_i32 s13, s13, s15
	s_add_i32 s13, s13, s14
	s_mov_b64 s[16:17], -1

.LBB0_1258:
	s_lshl_b32 s2, s64, 5
	v_readlane_b32 s3, v254, 19
	s_add_i32 s2, s2, s3
	s_cmp_lt_i32 s2, s30
	s_cbranch_scc0 .LBB0_1262
	s_ashr_i32 s3, s2, 31
	s_lshr_b32 s3, s3, 26
	s_add_i32 s3, s2, s3
	s_ashr_i32 s11, s3, 6
	s_lshl_b32 s11, s11, 3
	s_sub_i32 s13, s29, s11
	s_min_i32 s13, s13, 8
	s_abs_i32 s14, s13
	v_cvt_f32_u32_e32 v0, s14
	s_sub_i32 s16, 0, s14
	s_andn2_b32 s3, s3, 63
	s_sub_i32 s2, s2, s3
	v_rcp_iflag_f32_e32 v0, v0
	s_add_i32 s3, s11, s28
	s_abs_i32 s11, s2
	s_xor_b32 s15, s2, s13
	s_nop 0
	v_mul_f32_e32 v0, 0x4f7ffffe, v0
	v_cvt_u32_f32_e32 v0, v0
	s_ashr_i32 s15, s15, 31
	v_readfirstlane_b32 s17, v0
	s_mul_i32 s16, s16, s17
	s_mul_hi_u32 s16, s17, s16
	s_add_i32 s17, s17, s16
	s_mul_hi_u32 s16, s11, s17
	s_mul_i32 s17, s16, s14
	s_sub_i32 s11, s11, s17
	s_add_i32 s18, s16, 1
	s_sub_i32 s17, s11, s14
	s_cmp_ge_u32 s11, s14
	s_cselect_b32 s16, s18, s16
	s_cselect_b32 s11, s17, s11
	s_add_i32 s17, s16, 1
	s_cmp_ge_u32 s11, s14
	s_cselect_b32 s11, s17, s16
	s_xor_b32 s11, s11, s15
	s_sub_i32 s81, s11, s15
	s_mul_i32 s11, s81, s13
	s_sub_i32 s2, s2, s11
	s_add_i32 s92, s3, s2
	s_mov_b64 s[16:17], -1
	s_branch .LBB0_1262

.LBB0_1262:
	s_mov_b64 s[14:15], 0
	s_and_b64 vcc, exec, s[16:17]
	s_cbranch_vccz .LBB0_1264
	s_lshl_b32 s2, s92, 2
	v_readlane_b32 s3, v254, 30
	s_add_i32 s2, s3, s2
	v_mov_b32_e32 v0, s2
	ds_read_b32 v0, v0 offset:256
	s_mov_b64 s[14:15], -1
	s_waitcnt lgkmcnt(0)
	v_readfirstlane_b32 s10, v0
	v_lshlrev_b32_e32 v0, 2, v0
	v_add_u32_e64 v0, s3, v0
	ds_read_b32 v0, v0
	s_waitcnt lgkmcnt(0)
	v_sub_u32_e32 v248, s92, v0
.LBB0_1264:
	v_cndmask_b32_e64 v0, 0, 1, s[14:15]
	v_cmp_ne_u32_e64 s[2:3], 1, v0
	s_andn2_b64 vcc, exec, s[14:15]
	v_mov_b32_e32 v212, v246
	v_mov_b32_e32 v210, v247
	v_mov_b32_e32 v224, v206
	v_mov_b32_e32 v250, v208
	s_cbranch_vccnz .LBB0_1266
	s_lshl_b32 s11, s10, 2
	s_add_i32 s11, s11, 0
	s_add_i32 s11, s11, 0x20240
	v_mov_b32_e64 v0, s11
	ds_read_b32 v0, v0
	v_lshlrev_b32_e32 v2, 8, v248
	s_ashr_i32 s11, s10, 31
	v_add_u32_e32 v1, v2, v199
	s_lshl_b64 s[16:17], s[10:11], 18
	s_waitcnt lgkmcnt(0)
	v_add_u32_e32 v3, -1, v0
	v_min_i32_e32 v0, v1, v3
	s_add_u32 s16, s90, s16
	v_ashrrev_i32_e32 v1, 31, v0
	s_addc_u32 s17, s91, s17
	v_lshl_add_u64 v[0:1], v[0:1], 2, s[16:17]
	global_load_dword v4, v[0:1], off
	v_add_u32_e64 v0, v2, v235
	v_min_i32_e32 v0, v0, v3
	v_ashrrev_i32_e32 v1, 31, v0
	v_lshl_add_u64 v[0:1], v[0:1], 2, s[16:17]
	global_load_dword v5, v[0:1], off
	v_add_u32_e64 v0, v2, v236
	v_min_i32_e32 v0, v0, v3
	v_ashrrev_i32_e32 v1, 31, v0
	v_lshl_add_u64 v[0:1], v[0:1], 2, s[16:17]
	global_load_dword v6, v[0:1], off
	v_add_u32_e64 v0, v2, v237
	v_min_i32_e32 v0, v0, v3
	v_ashrrev_i32_e32 v1, 31, v0
	v_lshl_add_u64 v[0:1], v[0:1], 2, s[16:17]
	global_load_dword v0, v[0:1], off
	s_waitcnt vmcnt(0)
	s_nop 0
	v_lshl_add_u32 v250, v4, 10, v238
	v_lshl_add_u32 v224, v5, 10, v238
	v_lshl_add_u32 v210, v6, 10, v238
	v_lshl_add_u32 v212, v0, 10, v238

.LBB0_1274:
	s_lshl_b32 s11, s12, 2
	s_add_i32 s11, s11, 0
	s_add_i32 s11, s11, 0x20240
	v_mov_b32_e64 v0, s11
	ds_read_b32 v0, v0
	v_lshl_add_u32 v14, v249, 8, v207
	s_ashr_i32 s13, s12, 31
	s_lshl_b64 s[12:13], s[12:13], 20
	v_or_b32_e32 v4, 32, v14
	s_waitcnt lgkmcnt(0)
	v_add_u32_e32 v15, -1, v0
	s_add_u32 s12, s54, s12
	v_min_i32_e32 v4, v4, v15
	s_addc_u32 s13, s55, s13
	v_or_b32_e32 v2, 16, v14
	v_ashrrev_i32_e32 v5, 31, v4
	v_min_i32_e32 v0, v14, v15
	v_min_i32_e32 v2, v2, v15
	v_lshl_add_u64 v[6:7], v[4:5], 4, s[12:13]
	v_or_b32_e32 v4, 48, v14
	v_ashrrev_i32_e32 v1, 31, v0
	v_ashrrev_i32_e32 v3, 31, v2
	v_min_i32_e32 v4, v4, v15
	v_lshl_add_u64 v[0:1], v[0:1], 4, s[12:13]
	v_lshl_add_u64 v[2:3], v[2:3], 4, s[12:13]
	v_ashrrev_i32_e32 v5, 31, v4
	s_nop 0
	v_lshl_add_u64 v[10:11], v[4:5], 4, s[12:13]
	global_load_dwordx2 v[4:5], v[0:1], off offset:4
	global_load_dwordx2 v[8:9], v[2:3], off offset:4
	global_load_dwordx2 v[12:13], v[6:7], off offset:4
	global_load_dwordx2 v[16:17], v[10:11], off offset:4
	v_add_u32_e32 v0, 0x80, v14
	v_add_u32_e32 v2, 0x90, v14
	v_add_u32_e32 v6, 0xa0, v14
	v_min_i32_e32 v0, v0, v15
	v_min_i32_e32 v2, v2, v15
	v_min_i32_e32 v6, v6, v15
	s_nop 0
	v_add_u32_e32 v10, 0xb0, v14
	v_ashrrev_i32_e32 v1, 31, v0
	v_ashrrev_i32_e32 v3, 31, v2
	v_ashrrev_i32_e32 v7, 31, v6
	v_min_i32_e32 v10, v10, v15
	v_lshl_add_u64 v[0:1], v[0:1], 4, s[12:13]
	v_lshl_add_u64 v[2:3], v[2:3], 4, s[12:13]
	v_lshl_add_u64 v[6:7], v[6:7], 4, s[12:13]
	v_ashrrev_i32_e32 v11, 31, v10
	s_nop 0
	v_lshl_add_u64 v[18:19], v[10:11], 4, s[12:13]
	global_load_dwordx2 v[14:15], v[0:1], off offset:4
	global_load_dwordx2 v[10:11], v[2:3], off offset:4
	s_nop 0
	s_nop 0
	global_load_dwordx2 v[6:7], v[6:7], off offset:4
	s_nop 0
	s_nop 0
	global_load_dwordx2 v[2:3], v[18:19], off offset:4
	s_cmp_gt_i32 s27, -1
	s_nop 0
	v_readlane_b32 s14, v254, 28
	s_cselect_b64 s[12:13], -1, 0
	s_nop 0
	v_readlane_b32 s15, v254, 29
	s_and_b64 s[12:13], s[14:15], s[12:13]
	s_andn2_b64 vcc, exec, s[12:13]
	s_cbranch_vccnz .LBB0_1279
	s_waitcnt vmcnt(0)
	s_and_saveexec_b64 s[12:13], s[0:1]
	s_cbranch_execz .LBB0_1278
	s_mov_b64 s[14:15], exec
	s_nop 0
	v_mbcnt_lo_u32_b32 v0, s14, 0
	v_mbcnt_hi_u32_b32 v0, s15, v0
	v_cmp_eq_u32_e32 vcc, 0, v0
	s_and_b64 s[16:17], exec, vcc
	s_mov_b64 exec, s[16:17]
	s_cbranch_execz .LBB0_1278
	s_lshl_b32 s96, s27, 6
	s_lshl_b64 s[16:17], s[96:97], 2
	s_add_u32 s16, s22, s16
	s_addc_u32 s17, s23, s17
	s_bcnt1_i32_b64 s11, s[14:15]
	v_mov_b32_e32 v0, s11
	global_atomic_add v97, v0, s[16:17]

.LBB0_1279:
	s_nop 0
	v_pk_mul_f32 v[20:21], v[188:189], s[74:75] op_sel_hi:[1,0]
	s_cmp_lt_u32 s93, 4
	v_exp_f32_e32 v20, v20
	v_exp_f32_e32 v21, v21
	s_cselect_b64 vcc, -1, 0
	s_waitcnt vmcnt(0)
	v_cndmask_b32_e32 v1, v3, v2, vcc
	v_mul_f32_e64 v18, 4.0, v1
	v_pk_add_f32 v[20:21], v[20:21], 1.0 op_sel_hi:[1,0]
	v_pk_mul_f32 v[2:3], v[192:193], v[18:19] op_sel_hi:[1,0]
	v_rcp_f32_e32 v20, v20
	v_rcp_f32_e32 v21, v21
	v_pk_mul_f32 v[22:23], v[180:181], s[74:75] op_sel_hi:[1,0]
	s_lshl_b32 s11, s52, 8
	v_exp_f32_e32 v22, v22
	v_pk_mul_f32 v[20:21], v[188:189], v[20:21]
	v_exp_f32_e64 v23, v23
	v_pk_mul_f32 v[2:3], v[20:21], v[2:3]
	v_pk_mul_f32 v[20:21], v[186:187], s[74:75] op_sel_hi:[1,0]
	v_med3_f32 v19, v3, s82, v229
	v_exp_f32_e32 v20, v20
	v_exp_f32_e32 v21, v21
	v_med3_f32 v1, v2, s82, v229
	v_pk_mul_f32 v[2:3], v[190:191], v[18:19] op_sel_hi:[1,0]
	v_pk_add_f32 v[22:23], v[22:23], 1.0 op_sel_hi:[1,0]
	v_pk_add_f32 v[20:21], v[20:21], 1.0 op_sel_hi:[1,0]
	v_rcp_f32_e32 v22, v22
	v_rcp_f32_e32 v20, v20
	v_rcp_f32_e32 v21, v21
	v_rcp_f32_e32 v23, v23
	v_lshl_or_b32 v0, s93, 7, v243
	s_mov_b64 s[12:13], -1
	s_nop 0
	v_pk_mul_f32 v[20:21], v[186:187], v[20:21]
	v_pk_mul_f32 v[22:23], v[180:181], v[22:23]
	v_pk_mul_f32 v[2:3], v[20:21], v[2:3]
	s_nop 0
	s_nop 0
	v_med3_f32 v20, v2, s82, v229
	v_med3_f32 v3, v3, s82, v229
	v_mov_b32_e64 v2, v97
	v_cvt_pk_fp8_f32 v2, v20, v3
	v_pk_mul_f32 v[20:21], v[184:185], v[18:19] op_sel_hi:[1,0]
	v_mov_b32_e64 v3, v97
	v_pk_mul_f32 v[20:21], v[22:23], v[20:21]
	v_cvt_pk_fp8_f32 v2, v1, v19 op_sel:[0,0,1]
	v_med3_f32 v1, v20, s82, v229
	v_med3_f32 v22, v21, s82, v229
	v_pk_mul_f32 v[20:21], v[178:179], s[74:75] op_sel_hi:[1,0]
	v_pk_mul_f32 v[18:19], v[182:183], v[18:19] op_sel_hi:[1,0]
	v_exp_f32_e64 v20, v20
	v_exp_f32_e32 v21, v21
	s_nop 0
	v_pk_add_f32 v[20:21], v[20:21], 1.0 op_sel_hi:[1,0]
	s_nop 0
	v_rcp_f32_e32 v20, v20
	v_rcp_f32_e32 v21, v21
	s_nop 0
	v_pk_mul_f32 v[20:21], v[178:179], v[20:21]
	s_nop 0
	s_nop 0
	v_pk_mul_f32 v[18:19], v[20:21], v[18:19]
	v_pk_mul_f32 v[20:21], v[172:173], s[74:75] op_sel_hi:[1,0]
	v_med3_f32 v18, v18, s82, v229
	v_exp_f32_e32 v20, v20
	v_exp_f32_e32 v21, v21
	v_med3_f32 v19, v19, s82, v229
	v_cvt_pk_fp8_f32 v3, v18, v19
	v_pk_add_f32 v[20:21], v[20:21], 1.0 op_sel_hi:[1,0]
	s_nop 0
	v_rcp_f32_e32 v20, v20
	v_rcp_f32_e32 v21, v21
	s_nop 0
	v_cvt_pk_fp8_f32 v3, v1, v22 op_sel:[0,0,1]
	v_cndmask_b32_e32 v1, v7, v6, vcc
	v_mul_f32_e32 v18, 4.0, v1
	v_pk_mul_f32 v[6:7], v[176:177], v[18:19] op_sel_hi:[1,0]
	v_pk_mul_f32 v[20:21], v[172:173], v[20:21]
	v_pk_mul_f32 v[22:23], v[156:157], s[74:75] op_sel_hi:[1,0]
	v_pk_mul_f32 v[6:7], v[20:21], v[6:7]
	v_pk_mul_f32 v[20:21], v[170:171], s[74:75] op_sel_hi:[1,0]
	v_exp_f32_e32 v22, v22
	v_exp_f32_e32 v20, v20
	v_exp_f32_e32 v21, v21
	v_exp_f32_e32 v23, v23
	v_med3_f32 v19, v7, s82, v229
	v_med3_f32 v1, v6, s82, v229
	v_pk_add_f32 v[20:21], v[20:21], 1.0 op_sel_hi:[1,0]
	v_pk_mul_f32 v[6:7], v[174:175], v[18:19] op_sel_hi:[1,0]
	v_rcp_f32_e32 v20, v20
	v_rcp_f32_e32 v21, v21
	v_pk_add_f32 v[22:23], v[22:23], 1.0 op_sel_hi:[1,0]
	v_pk_mul_f32 v[20:21], v[170:171], v[20:21]
	s_nop 0
	s_nop 0
	v_pk_mul_f32 v[6:7], v[20:21], v[6:7]
	v_rcp_f32_e32 v22, v22
	v_rcp_f32_e32 v23, v23
	v_med3_f32 v20, v6, s82, v229
	v_med3_f32 v7, v7, s82, v229
	v_mov_b32_e64 v6, v97
	v_cvt_pk_fp8_f32 v6, v20, v7
	v_pk_mul_f32 v[20:21], v[164:165], v[18:19] op_sel_hi:[1,0]
	v_pk_mul_f32 v[22:23], v[156:157], v[22:23]
	v_mov_b32_e64 v7, v97
	v_pk_mul_f32 v[20:21], v[22:23], v[20:21]
	v_cvt_pk_fp8_f32 v6, v1, v19 op_sel:[0,0,1]
	v_med3_f32 v1, v20, s82, v229
	v_med3_f32 v22, v21, s82, v229
	v_pk_mul_f32 v[20:21], v[154:155], s[74:75] op_sel_hi:[1,0]
	v_pk_mul_f32 v[18:19], v[162:163], v[18:19] op_sel_hi:[1,0]
	v_exp_f32_e64 v20, v20
	v_exp_f32_e32 v21, v21
	s_nop 0
	v_pk_add_f32 v[20:21], v[20:21], 1.0 op_sel_hi:[1,0]
	s_nop 0
	v_rcp_f32_e32 v20, v20
	v_rcp_f32_e32 v21, v21
	s_nop 0
	v_pk_mul_f32 v[20:21], v[154:155], v[20:21]
	s_nop 0
	s_nop 0
	v_pk_mul_f32 v[18:19], v[20:21], v[18:19]
	v_pk_mul_f32 v[20:21], v[140:141], s[74:75] op_sel_hi:[1,0]
	v_med3_f32 v18, v18, s82, v229
	v_exp_f32_e32 v20, v20
	v_exp_f32_e32 v21, v21
	v_med3_f32 v19, v19, s82, v229
	v_cvt_pk_fp8_f32 v7, v18, v19
	v_pk_add_f32 v[20:21], v[20:21], 1.0 op_sel_hi:[1,0]
	s_nop 0
	v_rcp_f32_e32 v20, v20
	v_rcp_f32_e32 v21, v21
	s_nop 0
	v_cvt_pk_fp8_f32 v7, v1, v22 op_sel:[0,0,1]
	v_cndmask_b32_e32 v1, v11, v10, vcc
	v_mul_f32_e32 v18, 4.0, v1
	v_pk_mul_f32 v[10:11], v[148:149], v[18:19] op_sel_hi:[1,0]
	v_pk_mul_f32 v[20:21], v[140:141], v[20:21]
	v_pk_mul_f32 v[22:23], v[124:125], s[74:75] op_sel_hi:[1,0]
	v_pk_mul_f32 v[10:11], v[20:21], v[10:11]
	v_pk_mul_f32 v[20:21], v[138:139], s[74:75] op_sel_hi:[1,0]
	v_exp_f32_e32 v22, v22
	v_exp_f32_e32 v20, v20
	v_exp_f32_e32 v21, v21
	v_exp_f32_e32 v23, v23
	v_med3_f32 v19, v11, s82, v229
	v_med3_f32 v1, v10, s82, v229
	v_pk_add_f32 v[20:21], v[20:21], 1.0 op_sel_hi:[1,0]
	v_pk_mul_f32 v[10:11], v[146:147], v[18:19] op_sel_hi:[1,0]
	v_rcp_f32_e32 v20, v20
	v_rcp_f32_e32 v21, v21
	v_pk_add_f32 v[22:23], v[22:23], 1.0 op_sel_hi:[1,0]
	v_pk_mul_f32 v[20:21], v[138:139], v[20:21]
	s_nop 0
	s_nop 0
	v_pk_mul_f32 v[10:11], v[20:21], v[10:11]
	v_rcp_f32_e32 v22, v22
	v_rcp_f32_e32 v23, v23
	v_med3_f32 v20, v10, s82, v229
	v_med3_f32 v11, v11, s82, v229
	v_mov_b32_e64 v10, v97
	v_cvt_pk_fp8_f32 v10, v20, v11
	v_pk_mul_f32 v[20:21], v[132:133], v[18:19] op_sel_hi:[1,0]
	v_pk_mul_f32 v[22:23], v[124:125], v[22:23]
	v_mov_b32_e64 v11, v97
	v_pk_mul_f32 v[20:21], v[22:23], v[20:21]
	v_cvt_pk_fp8_f32 v10, v1, v19 op_sel:[0,0,1]
	v_med3_f32 v1, v20, s82, v229
	v_med3_f32 v22, v21, s82, v229
	v_pk_mul_f32 v[20:21], v[122:123], s[74:75] op_sel_hi:[1,0]
	v_pk_mul_f32 v[18:19], v[130:131], v[18:19] op_sel_hi:[1,0]
	v_exp_f32_e64 v20, v20
	v_exp_f32_e32 v21, v21
	s_nop 0
	v_pk_add_f32 v[20:21], v[20:21], 1.0 op_sel_hi:[1,0]
	s_nop 0
	v_rcp_f32_e32 v20, v20
	v_rcp_f32_e32 v21, v21
	s_nop 0
	v_pk_mul_f32 v[20:21], v[122:123], v[20:21]
	s_nop 0
	s_nop 0
	v_pk_mul_f32 v[18:19], v[20:21], v[18:19]
	v_pk_mul_f32 v[20:21], v[112:113], s[74:75] op_sel_hi:[1,0]
	v_med3_f32 v18, v18, s82, v229
	v_exp_f32_e32 v20, v20
	v_exp_f32_e32 v21, v21
	v_med3_f32 v19, v19, s82, v229
	v_cvt_pk_fp8_f32 v11, v18, v19
	v_pk_add_f32 v[20:21], v[20:21], 1.0 op_sel_hi:[1,0]
	s_nop 0
	v_rcp_f32_e32 v20, v20
	v_rcp_f32_e32 v21, v21
	s_nop 0
	v_cvt_pk_fp8_f32 v11, v1, v22 op_sel:[0,0,1]
	v_cndmask_b32_e32 v1, v15, v14, vcc
	v_mul_f32_e32 v18, 4.0, v1
	v_pk_mul_f32 v[14:15], v[116:117], v[18:19] op_sel_hi:[1,0]
	v_pk_mul_f32 v[20:21], v[112:113], v[20:21]
	v_pk_mul_f32 v[22:23], v[94:95], s[74:75] op_sel_hi:[1,0]
	v_pk_mul_f32 v[14:15], v[20:21], v[14:15]
	v_pk_mul_f32 v[20:21], v[110:111], s[74:75] op_sel_hi:[1,0]
	v_exp_f32_e32 v22, v22
	v_exp_f32_e32 v20, v20
	v_exp_f32_e32 v21, v21
	v_exp_f32_e32 v23, v23
	v_med3_f32 v19, v15, s82, v229
	v_med3_f32 v1, v14, s82, v229
	v_pk_add_f32 v[20:21], v[20:21], 1.0 op_sel_hi:[1,0]
	v_pk_mul_f32 v[14:15], v[114:115], v[18:19] op_sel_hi:[1,0]
	v_rcp_f32_e32 v20, v20
	v_rcp_f32_e32 v21, v21
	v_pk_add_f32 v[22:23], v[22:23], 1.0 op_sel_hi:[1,0]
	v_pk_mul_f32 v[20:21], v[110:111], v[20:21]
	s_nop 0
	s_nop 0
	v_pk_mul_f32 v[14:15], v[20:21], v[14:15]
	v_rcp_f32_e32 v22, v22
	v_rcp_f32_e32 v23, v23
	v_med3_f32 v20, v14, s82, v229
	v_med3_f32 v15, v15, s82, v229
	v_mov_b32_e64 v14, v97
	v_cvt_pk_fp8_f32 v14, v20, v15
	v_pk_mul_f32 v[20:21], v[100:101], v[18:19] op_sel_hi:[1,0]
	v_pk_mul_f32 v[22:23], v[94:95], v[22:23]
	v_mov_b32_e64 v15, v97
	v_pk_mul_f32 v[20:21], v[22:23], v[20:21]
	v_cvt_pk_fp8_f32 v14, v1, v19 op_sel:[0,0,1]
	v_med3_f32 v1, v20, s82, v229
	v_med3_f32 v22, v21, s82, v229
	v_pk_mul_f32 v[20:21], v[92:93], s[74:75] op_sel_hi:[1,0]
	v_pk_mul_f32 v[18:19], v[98:99], v[18:19] op_sel_hi:[1,0]
	v_exp_f32_e64 v20, v20
	v_exp_f32_e32 v21, v21
	s_nop 0
	v_pk_add_f32 v[20:21], v[20:21], 1.0 op_sel_hi:[1,0]
	s_nop 0
	v_rcp_f32_e32 v20, v20
	v_rcp_f32_e32 v21, v21
	s_nop 0
	v_pk_mul_f32 v[20:21], v[92:93], v[20:21]
	s_nop 0
	s_nop 0
	v_pk_mul_f32 v[18:19], v[20:21], v[18:19]
	v_pk_mul_f32 v[20:21], v[160:161], s[74:75] op_sel_hi:[1,0]
	v_med3_f32 v18, v18, s82, v229
	v_exp_f32_e32 v20, v20
	v_exp_f32_e32 v21, v21
	v_med3_f32 v19, v19, s82, v229
	v_cvt_pk_fp8_f32 v15, v18, v19
	v_pk_add_f32 v[20:21], v[20:21], 1.0 op_sel_hi:[1,0]
	s_nop 0
	v_rcp_f32_e32 v20, v20
	v_rcp_f32_e32 v21, v21
	s_nop 0
	v_cvt_pk_fp8_f32 v15, v1, v22 op_sel:[0,0,1]
	v_cndmask_b32_e32 v1, v17, v16, vcc
	v_mul_f32_e32 v18, 4.0, v1
	v_pk_mul_f32 v[16:17], v[168:169], v[18:19] op_sel_hi:[1,0]
	v_pk_mul_f32 v[20:21], v[160:161], v[20:21]
	v_pk_mul_f32 v[22:23], v[144:145], s[74:75] op_sel_hi:[1,0]
	v_pk_mul_f32 v[16:17], v[20:21], v[16:17]
	v_pk_mul_f32 v[20:21], v[158:159], s[74:75] op_sel_hi:[1,0]
	v_exp_f32_e32 v22, v22
	v_exp_f32_e32 v20, v20
	v_exp_f32_e32 v21, v21
	v_exp_f32_e32 v23, v23
	v_med3_f32 v19, v17, s82, v229
	v_med3_f32 v1, v16, s82, v229
	v_pk_add_f32 v[20:21], v[20:21], 1.0 op_sel_hi:[1,0]
	v_pk_mul_f32 v[16:17], v[166:167], v[18:19] op_sel_hi:[1,0]
	v_rcp_f32_e32 v20, v20
	v_rcp_f32_e32 v21, v21
	v_pk_add_f32 v[22:23], v[22:23], 1.0 op_sel_hi:[1,0]
	v_pk_mul_f32 v[20:21], v[158:159], v[20:21]
	s_nop 0
	s_nop 0
	v_pk_mul_f32 v[16:17], v[20:21], v[16:17]
	v_rcp_f32_e32 v22, v22
	v_rcp_f32_e32 v23, v23
	v_med3_f32 v20, v16, s82, v229
	v_med3_f32 v17, v17, s82, v229
	v_mov_b32_e64 v16, v97
	v_cvt_pk_fp8_f32 v16, v20, v17
	v_pk_mul_f32 v[20:21], v[152:153], v[18:19] op_sel_hi:[1,0]
	v_pk_mul_f32 v[22:23], v[144:145], v[22:23]
	v_mov_b32_e64 v17, v97
	v_pk_mul_f32 v[20:21], v[22:23], v[20:21]
	v_cvt_pk_fp8_f32 v16, v1, v19 op_sel:[0,0,1]
	v_med3_f32 v1, v20, s82, v229
	v_med3_f32 v22, v21, s82, v229
	v_pk_mul_f32 v[20:21], v[142:143], s[74:75] op_sel_hi:[1,0]
	v_pk_mul_f32 v[18:19], v[150:151], v[18:19] op_sel_hi:[1,0]
	v_exp_f32_e64 v20, v20
	v_exp_f32_e32 v21, v21
	s_nop 0
	v_pk_add_f32 v[20:21], v[20:21], 1.0 op_sel_hi:[1,0]
	s_nop 0
	v_rcp_f32_e32 v20, v20
	v_rcp_f32_e32 v21, v21
	s_nop 0
	v_pk_mul_f32 v[20:21], v[142:143], v[20:21]
	s_nop 0
	s_nop 0
	v_pk_mul_f32 v[18:19], v[20:21], v[18:19]
	v_pk_mul_f32 v[20:21], v[128:129], s[74:75] op_sel_hi:[1,0]
	v_med3_f32 v18, v18, s82, v229
	v_exp_f32_e32 v20, v20
	v_exp_f32_e32 v21, v21
	v_med3_f32 v19, v19, s82, v229
	v_cvt_pk_fp8_f32 v17, v18, v19
	v_pk_add_f32 v[20:21], v[20:21], 1.0 op_sel_hi:[1,0]
	s_nop 0
	v_rcp_f32_e32 v20, v20
	v_rcp_f32_e32 v21, v21
	s_nop 0
	v_cvt_pk_fp8_f32 v17, v1, v22 op_sel:[0,0,1]
	v_cndmask_b32_e32 v1, v13, v12, vcc
	v_mul_f32_e32 v18, 4.0, v1
	v_pk_mul_f32 v[12:13], v[136:137], v[18:19] op_sel_hi:[1,0]
	v_pk_mul_f32 v[20:21], v[128:129], v[20:21]
	v_pk_mul_f32 v[22:23], v[108:109], s[74:75] op_sel_hi:[1,0]
	v_pk_mul_f32 v[12:13], v[20:21], v[12:13]
	v_pk_mul_f32 v[20:21], v[126:127], s[74:75] op_sel_hi:[1,0]
	v_exp_f32_e32 v22, v22
	v_exp_f32_e32 v20, v20
	v_exp_f32_e32 v21, v21
	v_exp_f32_e32 v23, v23
	v_med3_f32 v19, v13, s82, v229
	v_med3_f32 v1, v12, s82, v229
	v_pk_add_f32 v[20:21], v[20:21], 1.0 op_sel_hi:[1,0]
	v_pk_mul_f32 v[12:13], v[134:135], v[18:19] op_sel_hi:[1,0]
	v_rcp_f32_e32 v20, v20
	v_rcp_f32_e32 v21, v21
	v_pk_add_f32 v[22:23], v[22:23], 1.0 op_sel_hi:[1,0]
	v_pk_mul_f32 v[20:21], v[126:127], v[20:21]
	s_nop 0
	s_nop 0
	v_pk_mul_f32 v[12:13], v[20:21], v[12:13]
	v_rcp_f32_e32 v22, v22
	v_rcp_f32_e32 v23, v23
	v_med3_f32 v20, v12, s82, v229
	v_med3_f32 v13, v13, s82, v229
	v_mov_b32_e64 v12, v97
	v_cvt_pk_fp8_f32 v12, v20, v13
	v_pk_mul_f32 v[20:21], v[120:121], v[18:19] op_sel_hi:[1,0]
	v_pk_mul_f32 v[22:23], v[108:109], v[22:23]
	v_mov_b32_e64 v13, v97
	v_pk_mul_f32 v[20:21], v[22:23], v[20:21]
	v_cvt_pk_fp8_f32 v12, v1, v19 op_sel:[0,0,1]
	v_med3_f32 v1, v20, s82, v229
	v_med3_f32 v22, v21, s82, v229
	v_pk_mul_f32 v[20:21], v[106:107], s[74:75] op_sel_hi:[1,0]
	v_pk_mul_f32 v[18:19], v[118:119], v[18:19] op_sel_hi:[1,0]
	v_exp_f32_e64 v20, v20
	v_exp_f32_e32 v21, v21
	s_nop 0
	v_pk_add_f32 v[20:21], v[20:21], 1.0 op_sel_hi:[1,0]
	s_nop 0
	v_rcp_f32_e32 v20, v20
	v_rcp_f32_e32 v21, v21
	s_nop 0
	v_pk_mul_f32 v[20:21], v[106:107], v[20:21]
	s_nop 0
	s_nop 0
	v_pk_mul_f32 v[18:19], v[20:21], v[18:19]
	v_pk_mul_f32 v[20:21], v[90:91], s[74:75] op_sel_hi:[1,0]
	v_med3_f32 v18, v18, s82, v229
	v_exp_f32_e32 v20, v20
	v_exp_f32_e32 v21, v21
	v_med3_f32 v19, v19, s82, v229
	v_cvt_pk_fp8_f32 v13, v18, v19
	v_pk_add_f32 v[20:21], v[20:21], 1.0 op_sel_hi:[1,0]
	s_nop 0
	v_rcp_f32_e32 v20, v20
	v_rcp_f32_e32 v21, v21
	s_nop 0
	v_cvt_pk_fp8_f32 v13, v1, v22 op_sel:[0,0,1]
	v_cndmask_b32_e32 v1, v9, v8, vcc
	v_mul_f32_e32 v18, 4.0, v1
	v_pk_mul_f32 v[8:9], v[104:105], v[18:19] op_sel_hi:[1,0]
	v_pk_mul_f32 v[20:21], v[90:91], v[20:21]
	v_pk_mul_f32 v[22:23], v[82:83], s[74:75] op_sel_hi:[1,0]
	v_pk_mul_f32 v[8:9], v[20:21], v[8:9]
	v_pk_mul_f32 v[20:21], v[88:89], s[74:75] op_sel_hi:[1,0]
	v_exp_f32_e32 v22, v22
	v_exp_f32_e32 v20, v20
	v_exp_f32_e32 v21, v21
	v_exp_f32_e32 v23, v23
	v_med3_f32 v19, v9, s82, v229
	v_med3_f32 v1, v8, s82, v229
	v_pk_add_f32 v[20:21], v[20:21], 1.0 op_sel_hi:[1,0]
	v_pk_mul_f32 v[8:9], v[102:103], v[18:19] op_sel_hi:[1,0]
	v_rcp_f32_e32 v20, v20
	v_rcp_f32_e32 v21, v21
	v_pk_add_f32 v[22:23], v[22:23], 1.0 op_sel_hi:[1,0]
	v_pk_mul_f32 v[20:21], v[88:89], v[20:21]
	s_nop 0
	s_nop 0
	v_pk_mul_f32 v[8:9], v[20:21], v[8:9]
	v_rcp_f32_e32 v22, v22
	v_rcp_f32_e32 v23, v23
	v_med3_f32 v20, v8, s82, v229
	v_med3_f32 v9, v9, s82, v229
	v_mov_b32_e64 v8, v97
	v_cvt_pk_fp8_f32 v8, v20, v9
	v_pk_mul_f32 v[20:21], v[86:87], v[18:19] op_sel_hi:[1,0]
	v_pk_mul_f32 v[22:23], v[82:83], v[22:23]
	v_mov_b32_e64 v9, v97
	v_pk_mul_f32 v[20:21], v[22:23], v[20:21]
	v_cvt_pk_fp8_f32 v8, v1, v19 op_sel:[0,0,1]
	v_med3_f32 v1, v20, s82, v229
	v_med3_f32 v22, v21, s82, v229
	v_pk_mul_f32 v[20:21], v[80:81], s[74:75] op_sel_hi:[1,0]
	v_pk_mul_f32 v[18:19], v[84:85], v[18:19] op_sel_hi:[1,0]
	v_exp_f32_e64 v20, v20
	v_exp_f32_e32 v21, v21
	s_nop 0
	v_pk_add_f32 v[20:21], v[20:21], 1.0 op_sel_hi:[1,0]
	s_nop 0
	v_rcp_f32_e32 v20, v20
	v_rcp_f32_e32 v21, v21
	s_nop 0
	v_pk_mul_f32 v[20:21], v[80:81], v[20:21]
	s_nop 0
	s_nop 0
	v_pk_mul_f32 v[18:19], v[20:21], v[18:19]
	v_pk_mul_f32 v[20:21], v[74:75], s[74:75] op_sel_hi:[1,0]
	v_med3_f32 v18, v18, s82, v229
	v_exp_f32_e32 v20, v20
	v_exp_f32_e32 v21, v21
	v_med3_f32 v19, v19, s82, v229
	v_cvt_pk_fp8_f32 v9, v18, v19
	v_pk_add_f32 v[20:21], v[20:21], 1.0 op_sel_hi:[1,0]
	s_nop 0
	v_rcp_f32_e32 v20, v20
	v_rcp_f32_e32 v21, v21
	s_nop 0
	v_cvt_pk_fp8_f32 v9, v1, v22 op_sel:[0,0,1]
	v_cndmask_b32_e32 v1, v5, v4, vcc
	v_mul_f32_e32 v4, 4.0, v1
	v_pk_mul_f32 v[18:19], v[78:79], v[4:5] op_sel_hi:[1,0]
	v_pk_mul_f32 v[20:21], v[74:75], v[20:21]
	v_pk_mul_f32 v[22:23], v[66:67], s[74:75] op_sel_hi:[1,0]
	v_pk_mul_f32 v[18:19], v[20:21], v[18:19]
	v_pk_mul_f32 v[20:21], v[72:73], s[74:75] op_sel_hi:[1,0]
	v_exp_f32_e32 v22, v22
	v_exp_f32_e32 v20, v20
	v_exp_f32_e32 v21, v21
	v_exp_f32_e32 v23, v23
	v_med3_f32 v5, v19, s82, v229
	v_med3_f32 v1, v18, s82, v229
	v_pk_add_f32 v[20:21], v[20:21], 1.0 op_sel_hi:[1,0]
	v_pk_mul_f32 v[18:19], v[76:77], v[4:5] op_sel_hi:[1,0]
	v_rcp_f32_e32 v20, v20
	v_rcp_f32_e32 v21, v21
	v_pk_add_f32 v[22:23], v[22:23], 1.0 op_sel_hi:[1,0]
	s_and_b64 vcc, exec, s[2:3]
	v_rcp_f32_e32 v22, v22
	v_pk_mul_f32 v[20:21], v[72:73], v[20:21]
	v_rcp_f32_e32 v23, v23
	s_nop 0
	v_pk_mul_f32 v[18:19], v[20:21], v[18:19]
	v_pk_mul_f32 v[22:23], v[66:67], v[22:23]
	v_med3_f32 v20, v18, s82, v229
	v_med3_f32 v19, v19, s82, v229
	v_mov_b32_e64 v18, v97
	v_cvt_pk_fp8_f32 v18, v20, v19
	v_pk_mul_f32 v[20:21], v[70:71], v[4:5] op_sel_hi:[1,0]
	v_mov_b32_e64 v19, v97
	v_pk_mul_f32 v[20:21], v[22:23], v[20:21]
	v_cvt_pk_fp8_f32 v18, v1, v5 op_sel:[0,0,1]
	v_med3_f32 v1, v20, s82, v229
	v_med3_f32 v22, v21, s82, v229
	v_pk_mul_f32 v[20:21], v[64:65], s[74:75] op_sel_hi:[1,0]
	v_pk_mul_f32 v[4:5], v[68:69], v[4:5] op_sel_hi:[1,0]
	v_exp_f32_e64 v20, v20
	v_exp_f32_e32 v21, v21
	s_nop 0
	v_pk_add_f32 v[20:21], v[20:21], 1.0 op_sel_hi:[1,0]
	s_nop 0
	v_rcp_f32_e32 v20, v20
	v_rcp_f32_e32 v21, v21
	s_nop 0
	v_pk_mul_f32 v[20:21], v[64:65], v[20:21]
	s_nop 0
	s_nop 0
	v_pk_mul_f32 v[4:5], v[20:21], v[4:5]
	s_nop 0
	s_nop 0
	v_med3_f32 v4, v4, s82, v229
	v_med3_f32 v5, v5, s82, v229
	v_cvt_pk_fp8_f32 v19, v4, v5
	v_add_u32_e32 v4, s11, v207
	v_ashrrev_i32_e32 v5, 31, v4
	v_lshlrev_b64 v[20:21], 10, v[4:5]
	v_cvt_pk_fp8_f32 v19, v1, v22 op_sel:[0,0,1]
	v_ashrrev_i32_e32 v1, 31, v0
	s_nop 0
	v_lshl_add_u64 v[20:21], s[34:35], 0, v[20:21]
	v_lshl_add_u64 v[20:21], v[20:21], 0, v[0:1]
	global_store_dwordx2 v[20:21], v[18:19], off
	v_add_u32_e32 v18, s11, v240
	v_ashrrev_i32_e32 v19, 31, v18
	v_lshlrev_b64 v[18:19], 10, v[18:19]
	v_lshl_add_u64 v[18:19], s[34:35], 0, v[18:19]
	v_lshl_add_u64 v[18:19], v[18:19], 0, v[0:1]
	global_store_dwordx2 v[18:19], v[8:9], off
	v_add_u32_e32 v8, s11, v241
	v_ashrrev_i32_e32 v9, 31, v8
	v_lshlrev_b64 v[8:9], 10, v[8:9]
	v_lshl_add_u64 v[8:9], s[34:35], 0, v[8:9]
	v_lshl_add_u64 v[8:9], v[8:9], 0, v[0:1]
	global_store_dwordx2 v[8:9], v[12:13], off
	v_add_u32_e32 v8, s11, v242
	v_ashrrev_i32_e32 v9, 31, v8
	v_lshlrev_b64 v[8:9], 10, v[8:9]
	v_lshl_add_u64 v[8:9], s[34:35], 0, v[8:9]
	v_lshl_add_u64 v[8:9], v[8:9], 0, v[0:1]
	global_store_dwordx2 v[8:9], v[16:17], off
	v_add_u32_e32 v8, 0x80, v4
	v_ashrrev_i32_e32 v9, 31, v8
	s_nop 0
	v_lshlrev_b64 v[8:9], 10, v[8:9]
	v_lshl_add_u64 v[8:9], s[34:35], 0, v[8:9]
	v_lshl_add_u64 v[8:9], v[8:9], 0, v[0:1]
	global_store_dwordx2 v[8:9], v[14:15], off
	v_add_u32_e32 v8, 0x90, v4
	v_ashrrev_i32_e32 v9, 31, v8
	s_nop 0
	v_lshlrev_b64 v[8:9], 10, v[8:9]
	v_lshl_add_u64 v[8:9], s[34:35], 0, v[8:9]
	v_lshl_add_u64 v[8:9], v[8:9], 0, v[0:1]
	global_store_dwordx2 v[8:9], v[10:11], off
	v_add_u32_e32 v8, 0xa0, v4
	v_add_u32_e32 v4, 0xb0, v4
	v_ashrrev_i32_e32 v9, 31, v8
	v_ashrrev_i32_e32 v5, 31, v4
	v_lshlrev_b64 v[8:9], 10, v[8:9]
	v_lshlrev_b64 v[4:5], 10, v[4:5]
	v_lshl_add_u64 v[8:9], s[34:35], 0, v[8:9]
	v_lshl_add_u64 v[4:5], s[34:35], 0, v[4:5]
	v_lshl_add_u64 v[8:9], v[8:9], 0, v[0:1]
	v_lshl_add_u64 v[0:1], v[4:5], 0, v[0:1]
	global_store_dwordx2 v[8:9], v[6:7], off
	global_store_dwordx2 v[0:1], v[2:3], off
	s_cbranch_vccnz .LBB0_1283
	s_andn2_b64 vcc, exec, s[6:7]
	s_cbranch_vccnz .LBB0_1282
	s_barrier

.LBB0_1286:
	s_cmp_gt_i32 s52, -1
	s_nop 0
	v_readlane_b32 s6, v254, 28
	s_cselect_b64 s[2:3], -1, 0
	s_nop 0
	v_readlane_b32 s7, v254, 29
	s_and_b64 s[2:3], s[6:7], s[2:3]
	s_mov_b32 s93, s44
	s_mov_b32 s0, s97
	s_and_b64 vcc, exec, s[2:3]
	s_cbranch_vccz .LBB0_1291
	s_nop 0
	v_mbcnt_lo_u32_b32 v0, -1, s0
	v_mbcnt_hi_u32_b32 v0, -1, v0
	s_waitcnt vmcnt(0)
	v_and_b32_e32 v0, 63, v0
	v_cmp_eq_u32_e32 vcc, 0, v0
	s_and_saveexec_b64 s[0:1], vcc
	s_cbranch_execz .LBB0_1290
	s_mov_b64 s[2:3], exec
	v_mbcnt_lo_u32_b32 v0, s2, 0
	v_mbcnt_hi_u32_b32 v0, s3, v0
	v_cmp_eq_u32_e32 vcc, 0, v0
	s_and_b64 s[6:7], exec, vcc
	s_mov_b64 exec, s[6:7]
	s_cbranch_execz .LBB0_1290
	s_lshl_b32 s96, s52, 6
	s_lshl_b64 s[6:7], s[96:97], 2
	s_add_u32 s6, s22, s6
	s_addc_u32 s7, s23, s7
	s_bcnt1_i32_b64 s2, s[2:3]
	v_mov_b32_e32 v0, s2
	global_atomic_add v97, v0, s[6:7]

.LBB0_1291:
	s_nop 0
	v_readlane_b32 s0, v254, 28
	v_readlane_b32 s1, v254, 29
	s_add_i32 s22, s89, 4
	s_nor_b64 s[0:1], s[0:1], s[4:5]
	s_cmp_lt_i32 s22, s37
	s_cselect_b64 s[38:39], -1, 0
	s_and_b64 s[0:1], s[0:1], s[38:39]
	s_andn2_b64 vcc, exec, s[0:1]
	s_cbranch_vccnz .LBB0_1337
	s_mov_b32 s0, s97
	s_waitcnt vmcnt(0)
	s_waitcnt vmcnt(0) lgkmcnt(0)
	s_barrier
	s_nop 0
	v_mbcnt_lo_u32_b32 v0, -1, s0
	v_mbcnt_hi_u32_b32 v0, -1, v0
	v_cmp_eq_u32_e32 vcc, s65, v0
	s_and_saveexec_b64 s[40:41], vcc
	s_cbranch_execz .LBB0_1336
	s_nop 0
	v_readlane_b32 s48, v253, 12
	v_readlane_b32 s0, v253, 14
	v_readlane_b32 s49, v253, 13
	v_readlane_b32 s23, v253, 17
	v_mov_b32_e32 v0, s0
	s_waitcnt vmcnt(0) expcnt(0) lgkmcnt(0)
	ds_read_b32 v2, v0
	ds_read_b32 v0, v0 offset:4
	s_waitcnt lgkmcnt(1)
	v_cmp_ne_u32_e32 vcc, 0, v2
	s_cbranch_vccnz .LBB0_1307
	s_nop 0
	v_readlane_b32 s0, v253, 6
	v_readlane_b32 s1, v253, 7
	s_load_dwordx2 s[4:5], s[0:1], 0x4
	s_add_u32 s0, s48, 0x1000
	s_addc_u32 s1, s49, 0
	s_nop 0
	s_add_u32 s2, s48, 0x1100
	s_addc_u32 s3, s49, 0
	s_waitcnt lgkmcnt(0)
	s_mul_i32 s28, s4, s61
	s_nop 0
	s_add_u32 s4, s48, 0x1200
	s_mul_i32 s28, s28, s5
	s_addc_u32 s5, s49, 0
	s_add_u32 s6, s48, 0x1300
	s_addc_u32 s7, s49, 0
	s_mov_b32 s29, 1
	s_mov_b64 s[8:9], 0
	s_branch .LBB0_1297

.LBB0_1297:
	v_mov_b64_e32 v[12:13], s[48:49]
	flat_load_dword v1, v[12:13] offset:1024 sc1
	flat_load_dword v0, v[12:13] offset:1280 sc1
	flat_load_dword v2, v[12:13] offset:1536 sc1
	s_or_b64 s[14:15], s[14:15], exec
	s_or_b64 s[12:13], s[12:13], exec
	s_waitcnt vmcnt(0) lgkmcnt(0)
	v_add_u32_e32 v3, v0, v1
	v_add_u32_e64 v4, v3, v2
	flat_load_dword v3, v[12:13] offset:1792 sc1
	s_waitcnt vmcnt(0) lgkmcnt(0)
	v_add_u32_e32 v5, v4, v3
	flat_load_dword v4, v[12:13] offset:2048 sc1
	s_waitcnt vmcnt(0) lgkmcnt(0)
	v_add_u32_e32 v6, v5, v4
	flat_load_dword v5, v[12:13] offset:2304 sc1
	s_waitcnt vmcnt(0) lgkmcnt(0)
	v_add_u32_e32 v7, v6, v5
	flat_load_dword v6, v[12:13] offset:2560 sc1
	s_waitcnt vmcnt(0) lgkmcnt(0)
	v_add_u32_e32 v8, v7, v6
	flat_load_dword v7, v[12:13] offset:2816 sc1
	s_waitcnt vmcnt(0) lgkmcnt(0)
	v_add_u32_e32 v9, v8, v7
	flat_load_dword v8, v[12:13] offset:3072 sc1
	s_waitcnt vmcnt(0) lgkmcnt(0)
	v_add_u32_e32 v10, v9, v8
	flat_load_dword v9, v[12:13] offset:3328 sc1
	s_waitcnt vmcnt(0) lgkmcnt(0)
	v_add_u32_e32 v11, v10, v9
	flat_load_dword v10, v[12:13] offset:3584 sc1
	s_waitcnt vmcnt(0) lgkmcnt(0)
	v_add_u32_e32 v14, v11, v10
	flat_load_dword v11, v[12:13] offset:3840 sc1
	v_mov_b64_e32 v[12:13], s[0:1]
	s_nop 0
	flat_load_dword v12, v[12:13] sc1
	s_waitcnt vmcnt(0) lgkmcnt(0)
	v_add_u32_e32 v14, v14, v11
	v_add_u32_e32 v16, v14, v12
	v_mov_b64_e32 v[14:15], s[2:3]
	flat_load_dword v13, v[14:15] sc1
	v_mov_b64_e32 v[14:15], s[4:5]
	s_nop 0
	flat_load_dword v14, v[14:15] sc1
	s_waitcnt vmcnt(0) lgkmcnt(0)
	v_add_u32_e32 v16, v16, v13
	v_add_u32_e32 v18, v16, v14
	v_mov_b64_e32 v[16:17], s[6:7]
	flat_load_dword v15, v[16:17] sc1
	s_waitcnt vmcnt(0) lgkmcnt(0)
	v_add_u32_e32 v16, v18, v15
	v_cmp_ne_u32_e32 vcc, s28, v16
	s_and_saveexec_b64 s[16:17], vcc
	s_cbranch_execz .LBB0_1296
	s_nop 0
	s_and_b32 s20, s29, 0xff
	s_mov_b64 s[18:19], -1
	s_cmp_eq_u32 s20, 0
	s_mov_b64 s[24:25], -1
	s_mov_b64 s[20:21], -1
	s_sleep 1
	s_cbranch_scc1 .LBB0_1300
	s_and_saveexec_b64 s[26:27], s[24:25]
	s_cbranch_execz .LBB0_1295
	s_branch .LBB0_1303

.LBB0_1307:
	s_lshl_b32 s20, s23, 6
	s_nop 0
	s_add_i32 s96, s20, 0x500
	s_lshl_b64 s[0:1], s[96:97], 2
	s_add_u32 s0, s48, s0
	s_addc_u32 s1, s49, s1
	v_mov_b64_e32 v[4:5], s[0:1]
	v_mov_b32_e64 v1, 1
	flat_atomic_add v3, v[4:5], v1 sc0
	v_cvt_f32_u32_e32 v1, v2
	v_sub_u32_e32 v4, 0, v2
	v_rcp_iflag_f32_e32 v1, v1
	s_nop 0
	v_mul_f32_e32 v1, 0x4f7ffffe, v1
	v_cvt_u32_f32_e32 v1, v1
	s_nop 0
	v_mul_lo_u32 v4, v4, v1
	v_mul_hi_u32 v4, v1, v4
	v_add_u32_e32 v1, v1, v4
	s_waitcnt vmcnt(0) lgkmcnt(0)
	v_mul_hi_u32 v1, v3, v1
	v_mul_lo_u32 v4, v1, v2
	v_sub_u32_e32 v4, v3, v4
	v_cmp_ge_u32_e32 vcc, v4, v2
	v_add_u32_e32 v5, 1, v1
	s_nop 0
	v_cndmask_b32_e32 v1, v1, v5, vcc
	v_sub_u32_e32 v5, v4, v2
	v_cndmask_b32_e32 v4, v4, v5, vcc
	v_cmp_ge_u32_e32 vcc, v4, v2
	v_add_u32_e32 v4, 1, v1
	s_nop 0
	v_cndmask_b32_e32 v1, v1, v4, vcc
	v_add_u32_e32 v4, 1, v3
	v_mad_u64_u32 v[2:3], s[0:1], v2, v1, v[2:3]
	v_cmp_ne_u32_e32 vcc, v4, v2
	s_and_saveexec_b64 s[0:1], vcc
	s_xor_b64 s[0:1], exec, s[0:1]
	s_cbranch_execz .LBB0_1320
	s_add_i32 s96, s20, 0x900
	s_lshl_b64 s[2:3], s[96:97], 2
	s_add_u32 s4, s48, s2
	s_addc_u32 s5, s49, s3
	v_mov_b64_e32 v[2:3], s[4:5]
	flat_load_dword v0, v[2:3] sc1
	s_waitcnt vmcnt(0) lgkmcnt(0)
	v_cmp_eq_u32_e32 vcc, v0, v1
	s_and_saveexec_b64 s[2:3], vcc
	s_cbranch_execz .LBB0_1319
	s_mov_b32 s21, 1
	s_mov_b64 s[6:7], 0
	s_branch .LBB0_1311

.LBB0_1311:
	s_nop 0
	s_and_b32 s14, s21, 0xff
	s_mov_b64 s[12:13], -1
	s_cmp_lg_u32 s14, 0
	s_mov_b64 s[14:15], -1
	s_sleep 1
	s_cbranch_scc1 .LBB0_1315
	v_mov_b64_e32 v[2:3], s[48:49]
	flat_load_dword v0, v[2:3] offset:512 sc1
	s_mov_b64 s[14:15], 0
	s_mov_b64 s[16:17], -1
	s_waitcnt vmcnt(0) lgkmcnt(0)
	v_cmp_eq_u32_e32 vcc, 0, v0
	s_and_saveexec_b64 s[18:19], vcc
	s_nop 0
	s_cmp_lt_u32 s21, 0x400001
	s_cselect_b64 s[14:15], -1, 0
	s_xor_b64 s[16:17], exec, -1
	s_and_b64 s[14:15], s[14:15], exec
	s_or_b64 exec, exec, s[18:19]

.LBB0_1317:
	s_or_b64 exec, exec, s[6:7]
	s_xor_b64 s[4:5], s[8:9], -1
	s_and_saveexec_b64 s[6:7], s[4:5]
	s_xor_b64 s[6:7], exec, s[6:7]
	s_cbranch_execz .LBB0_1319
	v_mov_b64_e32 v[0:1], s[48:49]
	v_mov_b32_e64 v2, 1
	flat_atomic_add v[0:1], v2 offset:512

.LBB0_1320:
	s_andn2_saveexec_b64 s[0:1], s[0:1]
	s_cbranch_execz .LBB0_1336
	v_mov_b32_e32 v1, s48
	v_add_co_u32_e32 v2, vcc, 0x3000, v1
	v_mov_b32_e64 v1, s49
	buffer_wbl2 sc1
	s_waitcnt vmcnt(0)
	v_addc_co_u32_e32 v3, vcc, 0, v1, vcc
	v_mov_b32_e64 v1, 1
	flat_atomic_add v1, v[2:3], v1 offset:1024 sc0
	v_cvt_f32_u32_e32 v2, v0
	v_sub_u32_e32 v3, 0, v0
	s_mov_b64 s[4:5], -1
	v_rcp_iflag_f32_e32 v2, v2
	s_nop 0
	s_nop 0
	v_mul_f32_e32 v2, 0x4f7ffffe, v2
	v_cvt_u32_f32_e32 v2, v2
	s_nop 0
	v_mul_lo_u32 v3, v3, v2
	v_mul_hi_u32 v3, v2, v3
	v_add_u32_e32 v2, v2, v3
	s_waitcnt vmcnt(0) lgkmcnt(0)
	v_mul_hi_u32 v2, v1, v2
	v_mul_lo_u32 v3, v2, v0
	v_sub_u32_e32 v3, v1, v3
	v_cmp_ge_u32_e32 vcc, v3, v0
	v_add_u32_e32 v4, 1, v2
	s_nop 0
	v_cndmask_b32_e32 v2, v2, v4, vcc
	v_sub_u32_e32 v4, v3, v0
	v_cndmask_b32_e32 v3, v3, v4, vcc
	v_cmp_ge_u32_e32 vcc, v3, v0
	v_add_u32_e32 v3, 1, v2
	s_nop 0
	v_cndmask_b32_e32 v2, v2, v3, vcc
	v_add_u32_e32 v3, 1, v1
	v_mad_u64_u32 v[0:1], s[0:1], v0, v2, v[0:1]
	s_add_u32 s0, s48, 0x3500
	s_addc_u32 s1, s49, 0
	v_cmp_ne_u32_e32 vcc, v3, v0
	v_mov_b64_e32 v[0:1], s[0:1]
	s_and_saveexec_b64 s[2:3], vcc
	s_cbranch_execz .LBB0_1333
	v_mov_b64_e32 v[0:1], s[0:1]
	flat_load_dword v0, v[0:1] sc1
	s_mov_b64 s[8:9], 0
	s_waitcnt vmcnt(0) lgkmcnt(0)
	v_cmp_eq_u32_e32 vcc, v0, v2
	s_and_saveexec_b64 s[6:7], vcc
	s_cbranch_execz .LBB0_1332
	s_nop 0
	s_add_u32 s4, s48, 0x200
	s_addc_u32 s5, s49, 0
	s_mov_b32 s21, 1
	s_branch .LBB0_1325

.LBB0_1335:
	s_or_b64 exec, exec, s[0:1]
	s_nop 0
	s_add_i32 s96, s20, 0x900
	s_lshl_b64 s[0:1], s[96:97], 2
	s_add_u32 s0, s48, s0
	s_addc_u32 s1, s49, s1
	v_mov_b64_e32 v[0:1], s[0:1]
	v_mov_b32_e32 v2, 1
	s_waitcnt vmcnt(0) lgkmcnt(0)
	buffer_inv sc1
	flat_atomic_add v[0:1], v2
	s_waitcnt vmcnt(0)

.LBB0_1337:
	s_cmp_gt_i32 s36, s22
	s_cselect_b64 s[0:1], -1, 0
	s_xor_b64 s[2:3], s[38:39], -1
	s_or_b64 s[0:1], s[0:1], s[2:3]
	s_add_i32 s92, s89, 5
	s_and_b64 vcc, exec, s[0:1]
	s_cbranch_vccnz .LBB0_1590
	s_mov_b32 s0, s97
	s_waitcnt vmcnt(0)
	s_nop 0
	v_mbcnt_lo_u32_b32 v0, -1, s0
	v_mbcnt_hi_u32_b32 v0, -1, v0
	v_add_u32_e64 v0, s64, v0
	v_cmp_gt_i32_e32 vcc, 24, v0
	s_and_saveexec_b64 s[0:1], vcc
	s_cbranch_execz .LBB0_1340
	v_ashrrev_i32_e32 v1, 31, v0
	v_lshl_add_u64 v[2:3], v[0:1], 2, s[80:81]
	global_load_dword v2, v[2:3], off sc1
	v_lshl_add_u32 v1, v0, 2, 0
	v_add_u32_e32 v1, 0x20240, v1
	s_waitcnt vmcnt(0)
	s_nop 0
	ds_write_b32 v1, v2

.LBB0_1342:
	s_or_b64 exec, exec, s[0:1]
	s_nop 0
	v_readlane_b32 s0, v254, 15
	s_waitcnt lgkmcnt(0)
	s_barrier
	v_mov_b32_e64 v1, s0
	ds_read_b32 v1, v1
	s_waitcnt lgkmcnt(0)
	v_cmp_lt_i32_e32 vcc, v0, v1
	s_and_saveexec_b64 s[0:1], vcc
	s_cbranch_execz .LBB0_1388
	v_readlane_b32 s2, v255, 29
	s_nop 1
	v_mov_b32_e32 v1, s2
	ds_read_b32 v1, v1
	s_waitcnt lgkmcnt(0)
	v_cmp_ge_i32_e32 vcc, v0, v1
	v_mov_b32_e64 v1, 0
	s_and_saveexec_b64 s[2:3], vcc
	s_cbranch_execz .LBB0_1387
	v_readlane_b32 s4, v255, 30
	s_nop 1
	v_mov_b32_e32 v1, s4
	ds_read_b32 v1, v1
	s_waitcnt lgkmcnt(0)
	v_cmp_ge_i32_e32 vcc, v0, v1
	v_mov_b32_e64 v1, 1
	s_and_saveexec_b64 s[4:5], vcc
	s_cbranch_execz .LBB0_1386
	v_readlane_b32 s6, v255, 31
	s_nop 1
	v_mov_b32_e32 v1, s6
	ds_read_b32 v1, v1
	s_waitcnt lgkmcnt(0)
	v_cmp_ge_i32_e32 vcc, v0, v1
	v_mov_b32_e64 v1, 2
	s_and_saveexec_b64 s[6:7], vcc
	s_cbranch_execz .LBB0_1385
	v_readlane_b32 s8, v255, 20
	s_nop 1
	v_mov_b32_e32 v1, s8
	ds_read_b32 v1, v1
	s_waitcnt lgkmcnt(0)
	v_cmp_ge_i32_e32 vcc, v0, v1
	v_mov_b32_e64 v1, 3
	s_and_saveexec_b64 s[8:9], vcc
	s_cbranch_execz .LBB0_1384
	v_readlane_b32 s10, v255, 32
	s_nop 1
	v_mov_b32_e32 v1, s10
	ds_read_b32 v1, v1
	s_waitcnt lgkmcnt(0)
	v_cmp_ge_i32_e32 vcc, v0, v1
	v_mov_b32_e64 v1, 4
	s_and_saveexec_b64 s[10:11], vcc
	s_cbranch_execz .LBB0_1383
	v_readlane_b32 s12, v255, 33
	s_nop 1
	v_mov_b32_e32 v1, s12
	ds_read_b32 v1, v1
	s_waitcnt lgkmcnt(0)
	v_cmp_ge_i32_e32 vcc, v0, v1
	v_mov_b32_e64 v1, 5
	s_and_saveexec_b64 s[12:13], vcc
	s_cbranch_execz .LBB0_1382
	v_readlane_b32 s14, v255, 34
	s_nop 1
	v_mov_b32_e32 v1, s14
	ds_read_b32 v1, v1
	s_waitcnt lgkmcnt(0)
	v_cmp_ge_i32_e32 vcc, v0, v1
	v_mov_b32_e64 v1, 6
	s_and_saveexec_b64 s[14:15], vcc
	s_cbranch_execz .LBB0_1381
	v_readlane_b32 s16, v255, 22
	s_nop 1
	v_mov_b32_e32 v1, s16
	ds_read_b32 v1, v1
	s_waitcnt lgkmcnt(0)
	v_cmp_ge_i32_e32 vcc, v0, v1
	v_mov_b32_e64 v1, 7
	s_and_saveexec_b64 s[16:17], vcc
	s_cbranch_execz .LBB0_1380
	v_readlane_b32 s18, v255, 35
	s_nop 1
	v_mov_b32_e32 v1, s18
	ds_read_b32 v1, v1
	s_waitcnt lgkmcnt(0)
	v_cmp_ge_i32_e32 vcc, v0, v1
	v_mov_b32_e64 v1, 8
	s_and_saveexec_b64 s[18:19], vcc
	s_cbranch_execz .LBB0_1379
	v_readlane_b32 s20, v255, 36
	s_nop 1
	v_mov_b32_e32 v1, s20
	ds_read_b32 v1, v1
	s_waitcnt lgkmcnt(0)
	v_cmp_ge_i32_e32 vcc, v0, v1
	v_mov_b32_e64 v1, 9
	s_and_saveexec_b64 s[20:21], vcc
	s_cbranch_execz .LBB0_1378
	v_readlane_b32 s22, v255, 37
	s_nop 1
	v_mov_b32_e32 v1, s22
	ds_read_b32 v1, v1
	s_waitcnt lgkmcnt(0)
	v_cmp_ge_i32_e32 vcc, v0, v1
	v_mov_b32_e64 v1, 10
	s_and_saveexec_b64 s[24:25], vcc
	s_cbranch_execz .LBB0_1377
	v_readlane_b32 s22, v255, 24
	s_nop 1
	v_mov_b32_e32 v1, s22
	ds_read_b32 v1, v1
	s_waitcnt lgkmcnt(0)
	v_cmp_ge_i32_e32 vcc, v0, v1
	v_mov_b32_e64 v1, 11
	s_and_saveexec_b64 s[26:27], vcc
	s_cbranch_execz .LBB0_1376
	v_readlane_b32 s22, v255, 38
	s_nop 1
	v_mov_b32_e32 v1, s22
	ds_read_b32 v1, v1
	s_waitcnt lgkmcnt(0)
	v_cmp_ge_i32_e32 vcc, v0, v1
	v_mov_b32_e64 v1, 12
	s_and_saveexec_b64 s[28:29], vcc
	s_cbranch_execz .LBB0_1375
	v_readlane_b32 s22, v255, 39
	s_nop 1
	v_mov_b32_e32 v1, s22
	ds_read_b32 v1, v1
	s_waitcnt lgkmcnt(0)
	v_cmp_ge_i32_e32 vcc, v0, v1
	v_mov_b32_e64 v1, 13
	s_and_saveexec_b64 s[30:31], vcc
	s_cbranch_execz .LBB0_1374
	v_readlane_b32 s22, v255, 40
	s_nop 1
	v_mov_b32_e32 v1, s22
	ds_read_b32 v1, v1
	s_waitcnt lgkmcnt(0)
	v_cmp_ge_i32_e32 vcc, v0, v1
	v_mov_b32_e64 v1, 14
	s_and_saveexec_b64 s[38:39], vcc
	s_cbranch_execz .LBB0_1373
	v_readlane_b32 s22, v255, 26
	s_nop 1
	v_mov_b32_e32 v1, s22
	ds_read_b32 v1, v1
	s_waitcnt lgkmcnt(0)
	v_cmp_ge_i32_e32 vcc, v0, v1
	v_mov_b32_e64 v1, 15
	s_and_saveexec_b64 s[40:41], vcc
	s_cbranch_execz .LBB0_1372
	v_readlane_b32 s22, v255, 41
	s_nop 1
	v_mov_b32_e32 v1, s22
	ds_read_b32 v1, v1
	s_waitcnt lgkmcnt(0)
	v_cmp_ge_i32_e32 vcc, v0, v1
	v_mov_b32_e64 v1, 16
	s_and_saveexec_b64 s[48:49], vcc
	s_cbranch_execz .LBB0_1371
	v_readlane_b32 s22, v255, 42
	s_mov_b32 s50, s93
	s_nop 0
	v_mov_b32_e64 v1, s22
	ds_read_b32 v1, v1
	s_waitcnt lgkmcnt(0)
	v_cmp_ge_i32_e32 vcc, v0, v1
	v_mov_b32_e64 v1, 17
	s_and_saveexec_b64 s[52:53], vcc
	s_cbranch_execz .LBB0_1370
	v_readlane_b32 s22, v255, 43
	s_nop 1
	v_mov_b32_e32 v1, s22
	ds_read_b32 v1, v1
	s_waitcnt lgkmcnt(0)
	v_cmp_ge_i32_e32 vcc, v0, v1
	v_mov_b32_e64 v1, 18
	s_and_saveexec_b64 s[54:55], vcc
	s_cbranch_execz .LBB0_1369
	v_readlane_b32 s22, v255, 28
	s_nop 1
	v_mov_b32_e32 v1, s22
	ds_read_b32 v1, v1
	s_waitcnt lgkmcnt(0)
	v_cmp_ge_i32_e32 vcc, v0, v1
	v_mov_b32_e64 v1, 19
	s_and_saveexec_b64 s[58:59], vcc
	s_cbranch_execz .LBB0_1368
	v_readlane_b32 s22, v255, 44
	s_nop 1
	v_mov_b32_e32 v1, s22
	ds_read_b32 v1, v1
	s_waitcnt lgkmcnt(0)
	v_cmp_ge_i32_e32 vcc, v0, v1
	v_mov_b32_e64 v1, 20
	s_and_saveexec_b64 s[60:61], vcc
	s_cbranch_execz .LBB0_1367
	v_readlane_b32 s22, v255, 45
	s_nop 1
	v_mov_b32_e32 v1, s22
	ds_read_b32 v1, v1
	s_waitcnt lgkmcnt(0)
	v_cmp_ge_i32_e32 vcc, v0, v1
	v_mov_b32_e64 v1, 21
	s_and_saveexec_b64 s[64:65], vcc
	s_cbranch_execz .LBB0_1366
	v_readlane_b32 s22, v255, 46
	s_nop 1
	v_mov_b32_e32 v1, s22
	ds_read_b32 v1, v1
	s_waitcnt lgkmcnt(0)
	v_cmp_lt_i32_e32 vcc, v0, v1
	s_nop 1
	s_nop 0
	v_cndmask_b32_e64 v1, 23, 22, vcc

.LBB0_1370:
	s_or_b64 exec, exec, s[52:53]
	s_nop 0
	v_readlane_b32 s36, v254, 5
	v_readlane_b32 s42, v254, 34
	v_readlane_b32 s72, v254, 17
	v_readlane_b32 s61, v254, 3
	v_readlane_b32 s64, v254, 4
	s_mov_b32 s93, s50
	s_nop 0
	v_readlane_b32 s37, v254, 6
	v_readlane_b32 s43, v254, 35
	v_readlane_b32 s50, v254, 31
	v_readlane_b32 s65, v255, 47
	v_readlane_b32 s51, v254, 8
	v_readlane_b32 s73, v254, 18

.LBB0_1387:
	s_or_b64 exec, exec, s[2:3]
	s_nop 0
	v_readlane_b32 s2, v254, 30
	s_nop 1
	s_nop 0
	v_lshl_add_u32 v0, v0, 2, s2
	ds_write_b32 v0, v1 offset:256
.LBB0_1388:
	s_or_b64 exec, exec, s[0:1]
	s_nop 0
	v_readlane_b32 s0, v254, 15
	s_waitcnt lgkmcnt(0)
	s_barrier
	v_mov_b32_e64 v0, s0
	ds_read_b32 v0, v0
	s_mov_b32 s0, s97
	s_waitcnt lgkmcnt(0)
	v_readfirstlane_b32 s58, v0
	s_nop 0
	v_mbcnt_lo_u32_b32 v0, -1, s0
	v_mbcnt_hi_u32_b32 v0, -1, v0
	v_readlane_b32 s0, v254, 52
	s_nop 1
	v_cmp_eq_u32_e32 vcc, s0, v0
	s_and_saveexec_b64 s[0:1], vcc
	s_cbranch_execz .LBB0_1390
	v_readlane_b32 s2, v254, 40
	v_readlane_b32 s3, v254, 41
	v_mov_b32_e32 v0, s51
	s_nop 0
	v_cndmask_b32_e64 v1, 0, 1, s[2:3]
	ds_write_b32 v0, v1
.LBB0_1390:
	s_or_b64 exec, exec, s[0:1]
	s_nop 0
	v_readlane_b32 s0, v254, 15
	s_lshl_b32 s6, s58, 2
	s_nop 0
	v_mov_b32_e64 v0, s0
	s_lshr_b32 s0, s58, 31
	s_add_i32 s0, s58, s0
	ds_read_b32 v0, v0
	s_ashr_i32 s31, s0, 1
	s_nop 0
	s_bfe_i32 s0, s58, 0x1001d
	s_lshr_b32 s0, s0, 29
	s_add_i32 s0, s6, s0
	s_and_b32 s0, s0, -8
	s_sub_i32 s46, s6, s0
	s_mov_b32 s0, s97
	s_waitcnt lgkmcnt(0)
	v_readfirstlane_b32 s7, v0
	s_add_i32 s30, s31, 1
	v_mbcnt_lo_u32_b32 v0, -1, s0
	v_mbcnt_hi_u32_b32 v0, -1, v0
	v_readlane_b32 s0, v254, 40
	s_mul_i32 s8, s30, s46
	v_add_u32_e32 v8, s64, v0
	v_readlane_b32 s1, v254, 41
	s_and_b64 vcc, exec, s[0:1]
	v_readfirstlane_b32 s12, v8
	v_writelane_b32 v254, s8, 16
	s_cbranch_vccz .LBB0_1394
	s_cmp_lt_i32 s50, s6
	v_readlane_b32 s11, v254, 60
	s_cselect_b64 s[4:5], -1, 0
	s_cmp_lt_i32 s11, s46
	s_cselect_b64 s[2:3], -1, 0
	s_sub_i32 s0, s11, s46
	s_mul_i32 s13, s0, s31
	s_ashr_i32 s0, s6, 31
	v_readlane_b32 s1, v254, 38
	s_add_i32 s13, s13, s8
	s_xor_b32 s0, s0, s1
	s_abs_i32 s1, s6
	s_nop 0
	v_readlane_b32 s8, v255, 6
	s_mul_hi_u32 s8, s1, s8
	s_nop 0
	v_readlane_b32 s14, v255, 7
	s_mul_i32 s9, s8, s14
	s_sub_i32 s1, s1, s9
	s_add_i32 s9, s8, 1
	s_sub_i32 s10, s1, s14
	s_cmp_ge_u32 s1, s14
	s_cselect_b32 s8, s9, s8
	s_cselect_b32 s1, s10, s1
	s_add_i32 s9, s8, 1
	s_cmp_ge_u32 s1, s14
	s_cselect_b32 s1, s9, s8
	s_xor_b32 s1, s1, s0
	s_sub_i32 s0, s1, s0
	s_mul_i32 s1, s0, s61
	s_sub_i32 s1, s6, s1
	s_lshl_b32 s1, s1, 1
	s_cmp_le_i32 s1, s61
	s_mul_i32 s14, s30, s11
	s_cbranch_scc0 .LBB0_1395
	s_cmp_gt_i32 s0, 0
	s_cselect_b64 s[0:1], -1, 0
	s_and_b64 s[0:1], s[0:1], s[4:5]
	s_mov_b64 s[8:9], 0
	s_and_b64 vcc, exec, s[0:1]
	s_mov_b64 s[0:1], 0
	s_cbranch_vccz .LBB0_1396
	s_and_b64 s[0:1], s[2:3], exec
	s_cselect_b32 s0, s14, s13
	s_nop 0
	v_readlane_b32 s1, v254, 61
	s_add_i32 s0, s0, s1
	s_ashr_i32 s1, s0, 31
	s_lshr_b32 s1, s1, 27
	s_add_i32 s1, s0, s1
	s_ashr_i32 s10, s1, 5
	s_lshl_b32 s11, s10, 3
	s_sub_i32 s10, s58, s11
	s_min_i32 s15, s10, 8
	s_abs_i32 s10, s15
	v_cvt_f32_u32_e32 v0, s10
	s_sub_i32 s17, 0, s10
	s_andn2_b32 s1, s1, 31
	s_sub_i32 s0, s0, s1
	v_rcp_iflag_f32_e32 v0, v0
	s_abs_i32 s1, s0
	s_xor_b32 s16, s0, s15
	s_ashr_i32 s16, s16, 31
	s_nop 0
	v_mul_f32_e32 v0, 0x4f7ffffe, v0
	v_cvt_u32_f32_e32 v0, v0
	s_nop 0
	v_readfirstlane_b32 s18, v0
	s_mul_i32 s17, s17, s18
	s_mul_hi_u32 s17, s18, s17
	s_add_i32 s18, s18, s17
	s_mul_hi_u32 s17, s1, s18
	s_mul_i32 s18, s17, s10
	s_sub_i32 s1, s1, s18
	s_add_i32 s19, s17, 1
	s_sub_i32 s18, s1, s10
	s_cmp_ge_u32 s1, s10
	s_cselect_b32 s17, s19, s17
	s_cselect_b32 s1, s18, s1
	s_add_i32 s18, s17, 1
	s_cmp_ge_u32 s1, s10
	s_cselect_b32 s1, s18, s17
	s_xor_b32 s1, s1, s16
	s_sub_i32 s10, s1, s16
	s_mul_i32 s1, s10, s15
	s_sub_i32 s0, s0, s1
	s_add_i32 s11, s11, s0
	s_mov_b64 s[0:1], -1
	s_branch .LBB0_1396

.LBB0_1396:
	s_and_b64 vcc, exec, s[8:9]
	s_cbranch_vccz .LBB0_1399
	s_and_b64 vcc, exec, s[4:5]
	s_cbranch_vccz .LBB0_1399
	s_and_b64 s[0:1], s[2:3], exec
	s_cselect_b32 s0, s14, s13
	s_nop 0
	v_readlane_b32 s1, v254, 61
	s_add_i32 s0, s0, s1
	s_ashr_i32 s1, s0, 31
	s_lshr_b32 s1, s1, 27
	s_add_i32 s1, s0, s1
	s_ashr_i32 s2, s1, 5
	s_lshl_b32 s2, s2, 3
	s_sub_i32 s3, s58, s2
	s_min_i32 s3, s3, 8
	s_abs_i32 s4, s3
	v_cvt_f32_u32_e32 v0, s4
	s_sub_i32 s8, 0, s4
	s_andn2_b32 s1, s1, 31
	s_sub_i32 s0, s0, s1
	v_rcp_iflag_f32_e32 v0, v0
	s_abs_i32 s1, s0
	s_xor_b32 s5, s0, s3
	s_ashr_i32 s5, s5, 31
	s_nop 0
	v_mul_f32_e32 v0, 0x4f7ffffe, v0
	v_cvt_u32_f32_e32 v0, v0
	s_nop 0
	v_readfirstlane_b32 s9, v0
	s_mul_i32 s8, s8, s9
	s_mul_hi_u32 s8, s9, s8
	s_add_i32 s9, s9, s8
	s_mul_hi_u32 s8, s1, s9
	s_mul_i32 s9, s8, s4
	s_sub_i32 s1, s1, s9
	s_add_i32 s10, s8, 1
	s_sub_i32 s9, s1, s4
	s_cmp_ge_u32 s1, s4
	s_cselect_b32 s8, s10, s8
	s_cselect_b32 s1, s9, s1
	s_add_i32 s9, s8, 1
	s_cmp_ge_u32 s1, s4
	s_cselect_b32 s1, s9, s8
	s_xor_b32 s1, s1, s5
	s_sub_i32 s10, s1, s5
	s_mul_i32 s1, s10, s3
	s_sub_i32 s0, s0, s1
	s_add_i32 s11, s2, s0
	s_mov_b64 s[0:1], -1

.LBB0_1400:
	v_readlane_b32 s4, v254, 50
	s_mul_i32 s4, s7, s4
	s_ashr_i32 s47, s4, 3
	s_add_i32 s4, s4, s7
	s_ashr_i32 s4, s4, 3
	s_sub_i32 s89, s4, s47
	s_lshl_b32 s44, s89, 2
	s_lshl_b32 s38, s89, 3
	s_and_b64 vcc, exec, s[2:3]
	s_cbranch_vccz .LBB0_1408
	s_nop 0
	v_readlane_b32 s2, v254, 19
	s_cmp_lt_i32 s2, s44
	s_nop 0
	v_readlane_b32 s5, v254, 53
	s_cselect_b64 s[2:3], -1, 0
	s_sub_i32 s4, s89, s5
	s_min_i32 s8, s4, 8
	s_lshr_b32 s4, s89, 29
	s_add_i32 s4, s89, s4
	s_lshl_b32 s4, s4, 3
	s_andn2_b32 s4, s4, 63
	s_add_i32 s7, s47, s5
	s_sub_i32 s4, s38, s4
	s_cmp_lt_i32 s4, 33
	s_mov_b64 s[4:5], -1
	s_cbranch_scc0 .LBB0_1405
	s_cmp_gt_i32 s89, 7
	s_cselect_b64 s[4:5], -1, 0
	s_and_b64 s[4:5], s[4:5], s[2:3]
	s_and_b64 vcc, exec, s[4:5]
	s_cbranch_vccz .LBB0_1404
	s_abs_i32 s0, s8
	v_cvt_f32_u32_e32 v0, s0
	s_ashr_i32 s1, s8, 31
	v_readlane_b32 s4, v255, 12
	s_xor_b32 s1, s4, s1
	v_rcp_iflag_f32_e32 v0, v0
	s_sub_i32 s4, 0, s0
	s_nop 0
	v_readlane_b32 s10, v255, 14
	v_mul_f32_e32 v0, 0x4f7ffffe, v0
	v_cvt_u32_f32_e32 v0, v0
	s_nop 0
	v_readfirstlane_b32 s5, v0
	s_mul_i32 s4, s4, s5
	s_mul_hi_u32 s4, s5, s4
	s_add_i32 s5, s5, s4
	s_mul_hi_u32 s4, s10, s5
	s_mul_i32 s5, s4, s0
	s_sub_i32 s5, s10, s5
	s_add_i32 s9, s4, 1
	s_sub_i32 s10, s5, s0
	s_cmp_ge_u32 s5, s0
	s_cselect_b32 s4, s9, s4
	s_cselect_b32 s5, s10, s5
	s_add_i32 s9, s4, 1
	s_cmp_ge_u32 s5, s0
	s_cselect_b32 s0, s9, s4
	s_xor_b32 s0, s0, s1
	s_sub_i32 s10, s0, s1
	s_mul_i32 s0, s10, s8
	v_readlane_b32 s1, v255, 13
	s_sub_i32 s0, s1, s0
	s_add_i32 s11, s7, s0
	s_mov_b64 s[0:1], -1

.LBB0_1405:
	s_and_b64 vcc, exec, s[4:5]
	s_cbranch_vccz .LBB0_1408
	s_and_b64 vcc, exec, s[2:3]
	s_cbranch_vccz .LBB0_1408
	s_abs_i32 s0, s8
	v_cvt_f32_u32_e32 v0, s0
	s_sub_i32 s2, 0, s0
	s_nop 0
	v_readlane_b32 s5, v255, 14
	s_ashr_i32 s1, s8, 31
	v_rcp_iflag_f32_e32 v0, v0
	s_nop 0
	s_nop 0
	v_mul_f32_e32 v0, 0x4f7ffffe, v0
	v_cvt_u32_f32_e32 v0, v0
	s_nop 0
	v_readfirstlane_b32 s3, v0
	s_mul_i32 s2, s2, s3
	s_mul_hi_u32 s2, s3, s2
	s_add_i32 s3, s3, s2
	s_mul_hi_u32 s2, s5, s3
	s_mul_i32 s3, s2, s0
	s_sub_i32 s3, s5, s3
	s_add_i32 s4, s2, 1
	s_sub_i32 s5, s3, s0
	s_cmp_ge_u32 s3, s0
	s_cselect_b32 s3, s5, s3
	s_cselect_b32 s2, s4, s2
	s_sub_i32 s4, s3, s0
	s_add_i32 s5, s2, 1
	s_cmp_ge_u32 s3, s0
	s_cselect_b32 s0, s4, s3
	v_readlane_b32 s3, v255, 12
	s_cselect_b32 s2, s5, s2
	s_xor_b32 s1, s3, s1
	s_xor_b32 s0, s0, s3
	s_xor_b32 s2, s2, s1
	s_sub_i32 s0, s0, s3
	s_sub_i32 s10, s2, s1
	s_add_i32 s11, s7, s0
	s_mov_b64 s[0:1], -1
.LBB0_1408:
	s_and_b64 vcc, exec, s[0:1]
	s_cbranch_vccz .LBB0_1410
	s_lshl_b32 s0, s11, 2
	s_nop 0
	v_readlane_b32 s1, v254, 30
	s_add_i32 s0, s1, s0
	v_mov_b32_e32 v0, s0
	ds_read_b32 v0, v0 offset:256
	s_waitcnt lgkmcnt(0)
	v_readfirstlane_b32 s14, v0
	v_lshlrev_b32_e32 v0, 2, v0
	v_add_u32_e32 v0, s1, v0
	ds_read_b32 v0, v0
	s_mov_b64 s[0:1], -1
	s_waitcnt lgkmcnt(0)
	v_sub_u32_e32 v199, s11, v0
	s_branch .LBB0_1411

.LBB0_1411:
	s_nop 0
	v_readlane_b32 s2, v255, 49
	v_readlane_b32 s3, v255, 50
	s_lshl_b64 s[2:3], s[2:3], 1
	s_add_u32 s2, s70, s2
	s_addc_u32 s3, s71, s3
	s_nop 0
	s_add_u32 s2, s2, 0x302800
	s_addc_u32 s3, s3, 0
	s_lshr_b32 s4, s89, 29
	s_add_i32 s4, s89, s4
	s_ashr_i32 s4, s4, 3
	v_writelane_b32 v254, s4, 24
	s_lshl_b32 s4, s4, 6
	s_ashr_i32 s7, s6, 31
	s_sub_i32 s39, s38, s4
	s_cmp_lt_i32 s39, 33
	s_cselect_b64 s[4:5], -1, 0
	s_nop 0
	v_writelane_b32 v254, s4, 36
	s_nop 1
	s_nop 0
	v_writelane_b32 v254, s5, 37
	s_lshl_b64 s[4:5], s[72:73], 23
	s_add_u32 s4, s70, s4
	s_addc_u32 s5, s71, s5
	s_nop 0
	s_add_u32 s59, s4, 0xae00000
	s_addc_u32 s60, s5, 0
	s_ashr_i32 s57, s56, 31
	s_lshl_b64 s[4:5], s[56:57], 2
	s_add_u32 s4, s70, s4
	s_addc_u32 s5, s71, s5
	s_nop 0
	s_add_u32 s4, s4, 0x20000
	s_addc_u32 s5, s5, 0
	s_nop 0
	s_add_u32 s8, s70, 0x13880
	s_addc_u32 s9, s71, 0
	s_andn2_b64 vcc, exec, s[0:1]
	v_readlane_b32 s0, v254, 54
	v_readlane_b32 s1, v254, 55
	s_nop 1
	s_nop 0
	v_cndmask_b32_e64 v0, 0, 1, s[0:1]
	v_cmp_ne_u32_e64 s[0:1], 1, v0
	s_cbranch_vccnz .LBB0_1513
	s_and_b64 vcc, exec, s[0:1]
	s_cbranch_vccnz .LBB0_1437
	v_mov_b32_e32 v0, s51
	ds_read_b32 v0, v0
	s_waitcnt lgkmcnt(0)
	v_cmp_ne_u32_e32 vcc, 0, v0
	s_cbranch_vccnz .LBB0_1437
	s_nop 0
	s_memrealtime s[16:17]
	s_lshl_b32 s18, s11, 6
	s_ashr_i32 s19, s18, 31
	s_lshl_b64 s[18:19], s[18:19], 2
	s_add_u32 s18, s4, s18
	s_addc_u32 s19, s5, s19
	s_mov_b32 s13, 1
	s_branch .LBB0_1417

.LBB0_1421:
	s_nop 0
	s_memrealtime s[20:21]
	s_waitcnt lgkmcnt(0)
	s_sub_u32 s20, s20, s16
	s_subb_u32 s21, s21, s17
	v_cmp_lt_u64_e32 vcc, s[20:21], v[200:201]
	s_cbranch_vccz .LBB0_1415
	s_add_i32 s13, s13, 1
	s_mov_b64 s[22:23], 0
	s_sleep 2
	s_branch .LBB0_1415

.LBB0_1425:
	v_cmp_gt_i32_e32 vcc, s58, v227
	s_waitcnt lgkmcnt(0)
	s_mov_b64 s[16:17], -1
	s_mov_b64 s[18:19], -1
	s_and_saveexec_b64 s[20:21], vcc
	s_cbranch_execz .LBB0_1427
	v_lshlrev_b32_e32 v0, 8, v227
	s_nop 0
	global_load_dword v0, v0, s[4:5] sc1
	s_waitcnt vmcnt(0)
	v_cmp_le_u32_e32 vcc, s69, v0
	s_orn2_b64 s[18:19], vcc, exec
.LBB0_1427:
	s_or_b64 exec, exec, s[20:21]
	v_add_u32_e64 v0, 64, v227
	v_cmp_gt_i32_e32 vcc, s58, v0
	s_and_saveexec_b64 s[20:21], vcc
	s_cbranch_execz .LBB0_1429
	v_lshlrev_b32_e32 v0, 8, v0
	global_load_dword v0, v0, s[4:5] sc1
	s_waitcnt vmcnt(0)
	v_cmp_le_u32_e32 vcc, s69, v0
	s_orn2_b64 s[16:17], vcc, exec

.LBB0_1433:
	s_or_b64 exec, exec, s[24:25]
	v_or_b32_e32 v0, 0x100, v227
	v_cmp_gt_i32_e32 vcc, s58, v0
	s_mov_b64 s[24:25], -1
	s_and_saveexec_b64 s[26:27], vcc
	s_cbranch_execz .LBB0_1435
	v_lshlrev_b32_e32 v0, 8, v0
	s_nop 0
	global_load_dword v0, v0, s[4:5] sc1
	s_waitcnt vmcnt(0)
	v_cmp_le_u32_e32 vcc, s69, v0
	s_orn2_b64 s[24:25], vcc, exec
.LBB0_1435:
	s_or_b64 exec, exec, s[26:27]
	s_and_b64 s[16:17], s[18:19], s[16:17]
	s_and_b64 s[16:17], s[16:17], s[22:23]
	s_and_b64 s[16:17], s[16:17], s[20:21]
	s_and_b64 s[16:17], s[16:17], s[24:25]
	s_xor_b64 s[16:17], s[16:17], -1
	s_waitcnt vmcnt(0)
	buffer_inv sc1
	s_waitcnt vmcnt(0)
	s_nop 0
	v_cndmask_b32_e64 v0, 0, 1, s[16:17]
	v_cmp_ne_u32_e32 vcc, 0, v0
	s_cbranch_vccnz .LBB0_1437
	v_mov_b32_e32 v0, s51
	v_mov_b32_e32 v1, 1
	ds_write_b32 v0, v1
.LBB0_1437:
	v_bfe_i32 v2, v8, 27, 1
	v_lshlrev_b32_e32 v0, 4, v8
	v_lshrrev_b32_e32 v2, 22, v2
	v_add_u32_e64 v2, v0, v2
	v_and_b32_e32 v2, 0xfffffc00, v2
	v_sub_u32_e32 v0, v0, v2
	v_lshrrev_b32_e32 v2, 4, v0
	v_bitop3_b32 v0, v2, v0, 32 bitop3:0x6c
	v_ashrrev_i32_e32 v1, 31, v8
	v_ashrrev_i32_e32 v3, 31, v0
	v_lshrrev_b32_e32 v1, 26, v1
	v_lshrrev_b32_e32 v3, 26, v3
	v_add_u32_e32 v1, v8, v1
	v_add_u32_e32 v3, v0, v3
	v_ashrrev_i32_e32 v1, 6, v1
	v_ashrrev_i32_e32 v4, 6, v3
	v_and_b32_e32 v3, 0xc0, v3
	v_lshlrev_b32_e32 v2, 3, v1
	v_sub_u32_e32 v0, v0, v3
	v_mov_b32_e64 v3, 1
	v_and_b32_e32 v2, -16, v2
	v_lshlrev_b32_e32 v1, 5, v1
	v_ashrrev_i16_sdwa v0, v3, sext(v0) dst_sel:DWORD dst_unused:UNUSED_PAD src0_sel:DWORD src1_sel:BYTE_0
	v_add_u32_e32 v2, v4, v2
	v_and_b32_e32 v1, 32, v1
	v_bfe_i32 v0, v0, 0, 16
	v_add_lshl_u32 v218, v1, v0, 1
	s_lshl_b32 s11, s11, 18
	v_lshlrev_b32_e32 v219, 10, v2
	v_add_u32_e64 v0, s11, v219
	v_add_u32_e32 v235, 0x10000, v218
	v_add_u32_e32 v194, v0, v218
	v_add_u32_e32 v196, v235, v0
	v_add_u32_e32 v0, 0x20000, v219
	v_add_u32_e32 v0, s11, v0
	v_and_b32_e32 v3, 3, v4
	s_mov_b32 s11, 0x7fffe0
	v_add_u32_e32 v96, v0, v218
	v_add_u32_e32 v202, v235, v0
	v_lshlrev_b32_e32 v0, 1, v2
	v_lshrrev_b32_e32 v1, 2, v2
	v_and_or_b32 v2, v2, s11, v3
	s_mul_hi_i32 s11, s14, 0x2aaaaaab
	s_lshr_b32 s16, s11, 31
	s_add_i32 s11, s11, s16
	s_ashr_i32 s13, s12, 6
	s_mul_i32 s16, s11, 6
	s_ashr_i32 s15, s12, 8
	s_lshl_b32 s78, s13, 10
	s_sub_i32 s16, s14, s16
	s_cmp_lt_u32 s16, 5
	s_cselect_b32 s17, 1, 2
	s_cmp_gt_i32 s16, 2
	s_cselect_b32 s16, s17, 0
	s_lshl_b32 s11, s11, 2
	s_or_b32 s16, s16, s11
	s_ashr_i32 s17, s16, 31
	s_ashr_i32 s11, s10, 31
	s_lshl_b64 s[16:17], s[16:17], 19
	s_lshl_b64 s[18:19], s[10:11], 17
	s_add_u32 s11, s59, s16
	s_addc_u32 s16, s60, s17
	s_add_u32 s18, s11, s18
	v_writelane_b32 v255, s39, 49
	v_and_b32_e32 v0, 24, v0
	v_and_b32_e32 v1, 4, v1
	s_addc_u32 s19, s16, s19
	s_add_i32 s11, s78, 0
	v_writelane_b32 v255, s92, 51
	v_or3_b32 v0, v2, v1, v0
	s_add_i32 s92, s11, 0x10000
	s_add_i32 s61, s11, 0x12000
	v_lshl_add_u32 v204, v0, 9, v218
	s_barrier
	s_mov_b32 m0, s92
	s_add_u32 s16, s18, 0x10000
	v_add_u32_e32 v206, 0x8000, v204
	global_load_lds_dwordx4 v204, s[18:19]
	s_mov_b32 m0, s61
	s_addc_u32 s17, s19, 0
	s_add_i32 s64, s11, 0x14000
	global_load_lds_dwordx4 v206, s[18:19]
	s_mov_b32 m0, s64
	s_nop 0
	s_add_i32 s45, s11, 0x16000
	global_load_lds_dwordx4 v204, s[16:17]
	s_mov_b32 m0, s45
	s_nop 0
	s_add_i32 s79, s11, 0x2000
	global_load_lds_dwordx4 v206, s[16:17]
	s_mov_b32 m0, s11
	s_nop 0
	s_add_i32 s93, s11, 0x4000
	global_load_lds_dwordx4 v194, s[34:35]
	s_mov_b32 m0, s79
	s_nop 0
	s_add_i32 s65, s11, 0x6000
	global_load_lds_dwordx4 v196, s[34:35]
	s_mov_b32 m0, s93
	s_nop 0
	v_writelane_b32 v254, s31, 12
	global_load_lds_dwordx4 v96, s[34:35]
	s_mov_b32 m0, s65
	s_cmp_eq_u32 s15, 1
	global_load_lds_dwordx4 v202, s[34:35]
	v_writelane_b32 v254, s30, 17
	s_cselect_b64 s[16:17], -1, 0
	v_mov_b32_e32 v205, v97
	v_mov_b32_e32 v207, v97
	v_mov_b32_e32 v195, v97
	v_mov_b32_e64 v197, v97
	v_writelane_b32 v254, s16, 26
	v_writelane_b32 v253, s38, 9
	v_lshl_add_u64 v[6:7], s[18:19], 0, v[204:205]
	v_lshl_add_u64 v[2:3], s[18:19], 0, v[206:207]
	v_lshl_add_u64 v[0:1], s[34:35], 0, v[194:195]
	v_writelane_b32 v254, s17, 27
	s_cmp_lg_u32 s15, 1
	s_nop 0
	v_lshl_add_u64 v[4:5], s[34:35], 0, v[196:197]
	s_cbranch_scc1 .LBB0_1439
	s_barrier
.LBB0_1439:
	s_mov_b64 s[16:17], 0x80
	s_add_i32 m0, s11, 0x18000
	v_lshl_add_u64 v[6:7], v[6:7], 0, s[16:17]
	v_and_b32_e32 v9, 15, v8
	v_lshrrev_b32_e32 v10, 4, v8
	s_lshl_b32 s13, s13, 5
	s_waitcnt vmcnt(2)
	s_barrier
	s_nop 0
	global_load_lds_dwordx4 v[6:7], off
	v_lshl_add_u64 v[2:3], v[2:3], 0, s[16:17]
	s_add_i32 m0, s11, 0x1a000
	s_add_i32 s81, s11, 0x8000
	v_lshl_or_b32 v195, s15, 6, v9
	v_bfe_u32 v10, v10, 1, 1
	s_lshl_b32 s15, s15, 13
	s_nop 0
	s_and_b32 s13, s13, 0x60
	global_load_lds_dwordx4 v[2:3], off
	v_lshl_add_u64 v[0:1], v[0:1], 0, s[16:17]
	s_mov_b32 m0, s81
	s_nop 0
	v_lshl_or_b32 v14, v10, 10, s15
	s_lshr_b32 s15, s13, 3
	s_nop 0
	global_load_lds_dwordx4 v[0:1], off
	v_lshl_add_u64 v[0:1], v[4:5], 0, s[16:17]
	s_add_i32 s16, s11, 0xa000
	s_add_u32 s18, s18, 0x10080
	s_mov_b32 m0, s16
	s_addc_u32 s19, s19, 0
	global_load_lds_dwordx4 v[0:1], off
	s_add_i32 m0, s11, 0x1c000
	v_lshl_add_u64 v[0:1], s[18:19], 0, v[204:205]
	global_load_lds_dwordx4 v[0:1], off
	v_lshl_add_u64 v[0:1], s[18:19], 0, v[206:207]
	s_add_i32 m0, s11, 0x1e000
	v_bfe_u32 v11, v8, 4, 2
	global_load_lds_dwordx4 v[0:1], off
	s_cmpk_lt_u32 s12, 0x100
	v_or_b32_e32 v10, s15, v10
	s_cselect_b64 s[18:19], -1, 0
	s_nop 0
	v_lshl_or_b32 v247, v11, 3, s13
	s_abs_i32 s13, s6
	s_nop 0
	v_readlane_b32 s15, v255, 6
	s_mul_hi_u32 s15, s13, s15
	s_nop 0
	v_readlane_b32 s21, v255, 7
	s_mul_i32 s17, s15, s21
	s_nop 0
	v_readlane_b32 s12, v254, 38
	s_sub_i32 s13, s13, s17
	s_xor_b32 s12, s7, s12
	s_add_i32 s17, s15, 1
	s_sub_i32 s20, s13, s21
	s_cmp_ge_u32 s13, s21
	s_cselect_b32 s15, s17, s15
	s_cselect_b32 s13, s20, s13
	s_add_i32 s17, s15, 1
	s_cmp_ge_u32 s13, s21
	s_cselect_b32 s13, s17, s15
	s_xor_b32 s13, s13, s12
	s_sub_i32 s12, s13, s12
	v_readlane_b32 s15, v254, 3
	s_mov_b32 s36, s12
	s_mul_i32 s12, s12, s15
	s_sub_i32 s12, s6, s12
	v_lshlrev_b32_e32 v12, 1, v8
	s_lshl_b32 s13, s12, 1
	v_and_b32_e32 v12, 32, v12
	v_lshlrev_b32_e32 v9, 6, v9
	v_lshlrev_b32_e32 v8, 2, v8
	s_cmp_le_i32 s13, s15
	v_or_b32_e32 v13, v9, v12
	v_and_b32_e32 v8, 32, v8
	v_lshlrev_b32_e32 v10, 10, v10
	s_cselect_b64 s[20:21], -1, 0
	s_nop 0
	v_bitop3_b32 v9, v9, v8, v12 bitop3:0x36
	v_bitop3_b32 v197, v10, v13, v8 bitop3:0xf6
	v_or_b32_e32 v12, 16, v13
	s_nop 0
	v_bitop3_b32 v13, v13, v8, 16 bitop3:0x36
	s_waitcnt vmcnt(6)
	s_nop 0
	v_writelane_b32 v254, s20, 20
	v_or_b32_e32 v9, v9, v14
	v_or_b32_e32 v13, v13, v14
	v_add_u32_e32 v243, 0xa0, v195
	v_add_u32_e32 v245, 0xb0, v195
	v_mov_b32_e64 v64, 0
	v_writelane_b32 v254, s21, 21
	v_bitop3_b32 v237, v12, v10, v8 bitop3:0xde
	v_or_b32_e32 v238, 16, v195
	v_or_b32_e32 v239, 32, v195
	v_or_b32_e32 v240, 48, v195
	s_nop 0
	v_add_u32_e32 v241, 0x80, v195
	v_add_u32_e32 v242, 0x90, v195
	v_lshlrev_b32_e32 v244, 11, v243
	v_lshlrev_b32_e32 v246, 11, v245
	s_mov_b32 s12, 0
	v_add_u32_e32 v248, 0, v9
	v_add_u32_e64 v249, 0, v13
	v_mbcnt_lo_u32_b32 v0, -1, 0
	v_mbcnt_hi_u32_b32 v0, -1, v0
	v_and_b32_e32 v0, 16, v0
	v_xor_b32_e32 v248, v248, v0
	v_xor_b32_e32 v249, v249, v0
	v_xor_b32_e32 v197, v197, v0
	v_xor_b32_e32 v237, v237, v0
	v_mov_b32_e32 v250, v202
	v_mov_b32_e32 v251, v96
	v_mov_b32_e32 v65, v64
	v_mov_b32_e32 v66, v64
	v_mov_b32_e32 v67, v64
	v_mov_b32_e32 v68, v64
	v_mov_b32_e32 v69, v64
	v_mov_b32_e32 v70, v64
	v_mov_b32_e32 v71, v64
	v_mov_b32_e32 v72, v64
	v_mov_b32_e32 v73, v64
	v_mov_b32_e32 v74, v64
	v_mov_b32_e32 v75, v64
	v_mov_b32_e32 v76, v64
	v_mov_b32_e32 v77, v64
	v_mov_b32_e32 v78, v64
	v_mov_b32_e32 v79, v64
	v_mov_b32_e32 v80, v64
	v_mov_b32_e32 v81, v64
	v_mov_b32_e32 v82, v64
	v_mov_b32_e32 v83, v64
	v_mov_b32_e32 v84, v64
	v_mov_b32_e32 v85, v64
	v_mov_b32_e32 v86, v64
	v_mov_b32_e32 v87, v64
	v_mov_b32_e32 v88, v64
	v_mov_b32_e32 v89, v64
	v_mov_b32_e32 v90, v64
	v_mov_b32_e32 v91, v64
	v_mov_b32_e32 v92, v64
	v_mov_b32_e32 v93, v64
	v_mov_b32_e32 v94, v64
	v_mov_b32_e32 v95, v64
	v_mov_b32_e32 v98, v64
	v_mov_b32_e32 v99, v64
	v_mov_b32_e32 v100, v64
	v_mov_b32_e32 v101, v64
	v_mov_b32_e32 v102, v64
	v_mov_b32_e32 v103, v64
	v_mov_b32_e32 v104, v64
	v_mov_b32_e32 v105, v64
	v_mov_b32_e32 v106, v64
	v_mov_b32_e32 v107, v64
	v_mov_b32_e32 v108, v64
	v_mov_b32_e32 v109, v64
	v_mov_b32_e32 v110, v64
	v_mov_b32_e32 v111, v64
	v_mov_b32_e32 v112, v64
	v_mov_b32_e32 v113, v64
	v_mov_b32_e32 v114, v64
	v_mov_b32_e32 v115, v64
	v_mov_b32_e32 v116, v64
	v_mov_b32_e32 v117, v64
	v_mov_b32_e32 v118, v64
	v_mov_b32_e32 v119, v64
	v_mov_b32_e32 v120, v64
	v_mov_b32_e32 v121, v64
	v_mov_b32_e32 v122, v64
	v_mov_b32_e32 v123, v64
	v_mov_b32_e32 v124, v64
	v_mov_b32_e32 v125, v64
	v_mov_b32_e32 v126, v64
	v_mov_b32_e32 v127, v64
	v_mov_b32_e32 v128, v64
	v_mov_b32_e32 v129, v64
	v_mov_b32_e32 v130, v64
	v_mov_b32_e32 v131, v64
	v_mov_b32_e32 v132, v64
	v_mov_b32_e32 v133, v64
	v_mov_b32_e32 v134, v64
	v_mov_b32_e32 v135, v64
	v_mov_b32_e32 v136, v64
	v_mov_b32_e32 v137, v64
	v_mov_b32_e32 v138, v64
	v_mov_b32_e32 v139, v64
	v_mov_b32_e32 v140, v64
	v_mov_b32_e32 v141, v64
	v_mov_b32_e32 v142, v64
	v_mov_b32_e32 v143, v64
	v_mov_b32_e32 v144, v64
	v_mov_b32_e32 v145, v64
	v_mov_b32_e32 v146, v64
	v_mov_b32_e32 v147, v64
	v_mov_b32_e32 v148, v64
	v_mov_b32_e32 v149, v64
	v_mov_b32_e32 v150, v64
	v_mov_b32_e32 v151, v64
	v_mov_b32_e32 v152, v64
	v_mov_b32_e32 v153, v64
	v_mov_b32_e32 v158, v64
	v_mov_b32_e32 v159, v64
	v_mov_b32_e32 v160, v64
	v_mov_b32_e32 v161, v64
	v_mov_b32_e32 v162, v64
	v_mov_b32_e32 v163, v64
	v_mov_b32_e32 v164, v64
	v_mov_b32_e32 v165, v64
	v_mov_b32_e32 v154, v64
	v_mov_b32_e32 v155, v64
	v_mov_b32_e32 v156, v64
	v_mov_b32_e32 v157, v64
	v_mov_b32_e32 v166, v64
	v_mov_b32_e32 v167, v64
	v_mov_b32_e32 v168, v64
	v_mov_b32_e32 v169, v64
	v_mov_b32_e32 v170, v64
	v_mov_b32_e32 v171, v64
	v_mov_b32_e32 v172, v64
	v_mov_b32_e32 v173, v64
	v_mov_b32_e32 v174, v64
	v_mov_b32_e32 v175, v64
	v_mov_b32_e32 v176, v64
	v_mov_b32_e32 v177, v64
	v_mov_b32_e32 v178, v64
	v_mov_b32_e32 v179, v64
	v_mov_b32_e32 v180, v64
	v_mov_b32_e32 v181, v64
	v_mov_b32_e32 v182, v64
	v_mov_b32_e32 v183, v64
	v_mov_b32_e32 v184, v64
	v_mov_b32_e32 v185, v64
	v_mov_b32_e32 v186, v64
	v_mov_b32_e32 v187, v64
	v_mov_b32_e32 v188, v64
	v_mov_b32_e32 v189, v64
	v_mov_b32_e32 v190, v64
	v_mov_b32_e32 v191, v64
	v_mov_b32_e32 v192, v64
	v_mov_b32_e32 v193, v64
	v_readlane_b32 s37, v254, 16
	s_barrier
	s_branch .LBB0_1442

.LBB0_1442:
	v_readlane_b32 s22, v254, 40
	v_readlane_b32 s23, v254, 41
	s_add_i32 s17, s12, 1
	s_and_b64 vcc, exec, s[22:23]
	s_cbranch_vccz .LBB0_1451
	s_nop 0
	v_readlane_b32 s22, v254, 20
	v_readlane_b32 s23, v254, 21
	s_and_b64 vcc, exec, s[22:23]
	s_cbranch_vccz .LBB0_1452
	s_mov_b64 s[24:25], 0
	s_cmp_lt_i32 s17, s36
	s_mov_b64 s[22:23], 0
	s_cbranch_scc0 .LBB0_1453
	v_readlane_b32 s15, v254, 3
	s_mul_hi_i32 s13, s17, s15
	s_mul_i32 s15, s17, s15
	s_add_u32 s26, s15, s50
	s_nop 0
	v_readlane_b32 s15, v254, 39
	s_addc_u32 s27, s13, s15
	v_mov_b64_e32 v[0:1], s[6:7]
	v_cmp_lt_i64_e32 vcc, s[26:27], v[0:1]
	s_cbranch_vccz .LBB0_1453
	s_ashr_i32 s13, s26, 31
	s_lshr_b32 s13, s13, 29
	s_add_i32 s13, s26, s13
	s_and_b32 s15, s13, -8
	s_sub_i32 s15, s26, s15
	s_cmp_ge_i32 s15, s46
	s_mov_b64 s[22:23], -1
	s_cbranch_scc0 .LBB0_1448
	s_sub_i32 s22, s15, s46
	s_nop 0
	v_readlane_b32 s23, v254, 12
	s_mul_i32 s22, s22, s23
	s_add_i32 s26, s22, s37
	s_mov_b64 s[22:23], 0
.LBB0_1448:
	s_andn2_b64 vcc, exec, s[22:23]
	s_cbranch_vccnz .LBB0_1450
	s_nop 0
	v_readlane_b32 s22, v254, 17
	s_mul_i32 s26, s15, s22

.LBB0_1453:
	s_and_b64 vcc, exec, s[24:25]
	s_cbranch_vccz .LBB0_1460
	s_nop 0
	v_readlane_b32 s15, v254, 3
	s_mul_hi_i32 s13, s17, s15
	s_mul_i32 s15, s17, s15
	s_add_u32 s24, s15, s50
	s_nop 0
	v_readlane_b32 s15, v254, 39
	s_addc_u32 s25, s13, s15
	v_mov_b64_e32 v[0:1], s[6:7]
	v_cmp_lt_i64_e32 vcc, s[24:25], v[0:1]
	s_cbranch_vccz .LBB0_1460
	s_ashr_i32 s13, s24, 31
	s_lshr_b32 s13, s13, 29
	s_add_i32 s13, s24, s13
	s_and_b32 s15, s13, -8
	s_sub_i32 s15, s24, s15
	s_cmp_ge_i32 s15, s46
	s_mov_b64 s[22:23], -1
	s_cbranch_scc0 .LBB0_1457
	s_sub_i32 s22, s15, s46
	s_nop 0
	v_readlane_b32 s23, v254, 12
	s_mul_i32 s22, s22, s23
	s_add_i32 s24, s22, s37
	s_mov_b64 s[22:23], 0
.LBB0_1457:
	s_andn2_b64 vcc, exec, s[22:23]
	s_cbranch_vccnz .LBB0_1459
	s_nop 0
	v_readlane_b32 s22, v254, 17
	s_mul_i32 s24, s15, s22

.LBB0_1461:
	v_readlane_b32 s26, v254, 36
	v_readlane_b32 s27, v254, 37
	s_mov_b64 s[24:25], -1
	s_and_b64 vcc, exec, s[26:27]
	s_cbranch_vccz .LBB0_1465
	s_nop 0
	v_readlane_b32 s13, v254, 24
	s_cmp_lt_i32 s17, s13
	s_cbranch_scc0 .LBB0_1466
	s_lshl_b32 s13, s17, 5
	s_nop 0
	v_readlane_b32 s15, v254, 19
	s_add_i32 s27, s13, s15
	s_cmp_lt_i32 s27, s44
	s_cbranch_scc0 .LBB0_1467
	s_ashr_i32 s13, s27, 31
	s_lshr_b32 s13, s13, 27
	s_add_i32 s13, s27, s13
	s_ashr_i32 s13, s13, 5
	s_lshl_b32 s13, s13, 3
	s_sub_i32 s15, s89, s13
	s_min_i32 s15, s15, 8
	s_add_i32 s13, s13, s47
	s_mov_b64 s[22:23], -1
	s_branch .LBB0_1470

.LBB0_1470:
	s_mov_b64 s[24:25], 0
	s_and_b64 vcc, exec, s[22:23]
	s_cbranch_vccz .LBB0_1472
	s_abs_i32 s23, s15
	v_cvt_f32_u32_e32 v0, s23
	s_ashr_i32 s20, s27, 31
	s_lshr_b32 s20, s20, 27
	s_add_i32 s20, s27, s20
	v_rcp_iflag_f32_e32 v0, v0
	s_sub_i32 s24, 0, s23
	s_andn2_b32 s20, s20, 31
	s_sub_i32 s21, s27, s20
	v_mul_f32_e32 v0, 0x4f7ffffe, v0
	v_cvt_u32_f32_e32 v0, v0
	s_abs_i32 s22, s21
	s_xor_b32 s20, s21, s15
	s_ashr_i32 s20, s20, 31
	v_readfirstlane_b32 s25, v0
	s_mul_i32 s24, s24, s25
	s_mul_hi_u32 s24, s25, s24
	s_add_i32 s25, s25, s24
	s_mul_hi_u32 s24, s22, s25
	s_mul_i32 s25, s24, s23
	s_sub_i32 s22, s22, s25
	s_add_i32 s25, s24, 1
	s_sub_i32 s26, s22, s23
	s_cmp_ge_u32 s22, s23
	s_cselect_b32 s24, s25, s24
	s_cselect_b32 s22, s26, s22
	s_add_i32 s25, s24, 1
	s_cmp_ge_u32 s22, s23
	s_cselect_b32 s22, s25, s24
	s_xor_b32 s22, s22, s20
	s_sub_i32 s20, s22, s20
	s_mul_i32 s15, s20, s15
	s_sub_i32 s15, s21, s15
	s_add_i32 s21, s13, s15
	s_lshl_b32 s13, s21, 2
	s_nop 0
	v_readlane_b32 s15, v254, 30
	s_add_i32 s13, s15, s13
	v_mov_b32_e32 v0, s13
	ds_read_b32 v0, v0 offset:256
	s_mov_b64 s[24:25], -1
	s_waitcnt lgkmcnt(0)
	v_readfirstlane_b32 s80, v0
	v_lshlrev_b32_e32 v0, 2, v0
	v_add_u32_e64 v0, s15, v0
	ds_read_b32 v0, v0
	s_waitcnt lgkmcnt(0)
	v_sub_u32_e32 v252, s21, v0
.LBB0_1472:
	s_xor_b64 s[22:23], s[24:25], -1
	s_and_b64 vcc, exec, s[22:23]
	v_mov_b32_e32 v208, v250
	v_mov_b32_e32 v210, v251
	v_mov_b32_e32 v224, v196
	v_mov_b32_e32 v236, v194
	s_cbranch_vccnz .LBB0_1474
	s_lshl_b32 s13, s21, 18
	v_add_u32_e32 v0, s13, v219
	v_add_u32_e32 v236, v0, v218
	v_add_u32_e64 v224, v235, v0
	v_add_u32_e32 v0, 0x20000, v219
	v_add_u32_e32 v0, s13, v0
	v_add_u32_e32 v210, v0, v218
	v_add_u32_e32 v208, v235, v0

.LBB0_1475:
	s_cmp_eq_u32 s13, 6
	s_cselect_b64 s[30:31], -1, 0
	s_and_b64 s[28:29], s[24:25], s[30:31]
	s_andn2_b64 vcc, exec, s[28:29]
	s_cbranch_vccnz .LBB0_1502
	s_and_b64 vcc, exec, s[0:1]
	s_cbranch_vccnz .LBB0_1501
	v_mov_b32_e64 v0, s51
	ds_read_b32 v0, v0
	s_waitcnt lgkmcnt(0)
	v_cmp_ne_u32_e32 vcc, 0, v0
	s_cbranch_vccnz .LBB0_1501
	s_nop 0
	s_memrealtime s[38:39]
	s_mov_b32 s15, 1
	s_branch .LBB0_1481

.LBB0_1509:
	s_lshl_b32 s13, s14, 2
	s_add_i32 s13, s13, 0
	s_nop 0
	s_add_i32 s13, s13, 0x20240
	v_mov_b32_e64 v0, s13
	ds_read_b32 v16, v0
	v_lshlrev_b32_e32 v17, 8, v199
	s_ashr_i32 s15, s14, 31
	v_add_u32_e32 v27, v17, v195
	s_lshl_b64 s[26:27], s[14:15], 18
	s_waitcnt lgkmcnt(0)
	v_add_u32_e32 v2, -1, v16
	s_add_u32 s26, s90, s26
	v_min_i32_e32 v0, v27, v2
	s_addc_u32 s27, s91, s27
	v_ashrrev_i32_e32 v1, 31, v0
	v_lshl_add_u64 v[0:1], v[0:1], 2, s[26:27]
	global_load_dword v3, v[0:1], off
	v_or_b32_e32 v0, 16, v27
	v_min_i32_e32 v0, v0, v2
	v_ashrrev_i32_e32 v1, 31, v0
	s_nop 0
	v_lshl_add_u64 v[0:1], v[0:1], 2, s[26:27]
	global_load_dword v4, v[0:1], off
	v_or_b32_e32 v0, 32, v27
	v_min_i32_e32 v0, v0, v2
	v_ashrrev_i32_e32 v1, 31, v0
	s_nop 0
	v_lshl_add_u64 v[0:1], v[0:1], 2, s[26:27]
	global_load_dword v26, v[0:1], off
	v_or_b32_e32 v0, 48, v27
	v_min_i32_e32 v0, v0, v2
	v_ashrrev_i32_e32 v1, 31, v0
	s_nop 0
	v_lshl_add_u64 v[0:1], v[0:1], 2, s[26:27]
	global_load_dword v25, v[0:1], off
	v_add_u32_e32 v0, 0x80, v27
	v_min_i32_e32 v0, v0, v2
	v_ashrrev_i32_e32 v1, 31, v0
	v_lshl_add_u64 v[0:1], v[0:1], 2, s[26:27]
	global_load_dword v24, v[0:1], off
	v_add_u32_e32 v0, 0x90, v27
	v_min_i32_e32 v0, v0, v2
	v_ashrrev_i32_e32 v1, 31, v0
	v_lshl_add_u64 v[0:1], v[0:1], 2, s[26:27]
	global_load_dword v23, v[0:1], off
	v_add_u32_e32 v0, 0xa0, v27
	v_min_i32_e32 v0, v0, v2
	v_ashrrev_i32_e32 v1, 31, v0
	v_lshl_add_u64 v[0:1], v[0:1], 2, s[26:27]
	global_load_dword v20, v[0:1], off
	v_add_u32_e32 v0, 0xb0, v27
	v_min_i32_e32 v0, v0, v2
	v_ashrrev_i32_e32 v1, 31, v0
	v_lshl_add_u64 v[0:1], v[0:1], 2, s[26:27]
	v_lshl_or_b32 v21, s10, 8, v247
	global_load_dword v19, v[0:1], off
	v_lshlrev_b32_e32 v0, 1, v21
	s_nop 0
	v_add_u32_e32 v18, 0x2000000, v0
	v_add_u32_e32 v22, 0x37a00000, v0
	v_cmp_lt_i32_e32 vcc, v27, v16
	v_lshlrev_b32_e32 v27, 11, v195
	v_add_u32_e32 v27, v18, v27
	v_mov_b32_e32 v45, v97
	s_waitcnt vmcnt(0)
	v_ashrrev_i32_e32 v0, 12, v3
	v_lshl_add_u32 v44, v3, 11, v22
	v_mul_i32_i24_e32 v0, 0x1800, v0
	v_add_lshl_u32 v0, v0, v21, 1
	global_load_dwordx4 v[28:31], v44, s[70:71]
	global_load_dwordx4 v[32:35], v0, s[2:3]
	global_load_dwordx4 v[36:39], v44, s[70:71] offset:256
	global_load_dwordx4 v[40:43], v0, s[2:3] offset:256
	v_ashrrev_i32_e32 v0, 12, v4
	s_nop 0
	v_mul_i32_i24_e32 v0, 0x1800, v0
	v_lshl_add_u32 v54, v4, 11, v22
	v_add_lshl_u32 v4, v0, v21, 1
	global_load_dwordx4 v[12:15], v54, s[70:71]
	global_load_dwordx4 v[8:11], v4, s[2:3]
	global_load_dwordx4 v[0:3], v54, s[70:71] offset:256
	s_nop 0
	s_nop 0
	global_load_dwordx4 v[4:7], v4, s[2:3] offset:256
	v_cndmask_b32_e32 v44, v27, v44, vcc
	s_nop 0
	v_lshl_add_u64 v[44:45], s[70:71], 0, v[44:45]
	v_add_u32_e64 v27, v17, v238
	v_cmp_lt_i32_e32 vcc, v27, v16
	v_lshlrev_b32_e32 v27, 11, v238
	v_add_u32_e32 v27, v18, v27
	v_cndmask_b32_e32 v27, v27, v54, vcc
	s_waitcnt vmcnt(7)
	v_lshlrev_b32_e32 v46, 16, v28
	v_and_b32_e32 v47, 0xffff0000, v28
	v_lshlrev_b32_e32 v28, 16, v29
	s_nop 0
	v_and_b32_e32 v29, 0xffff0000, v29
	v_lshlrev_b32_e32 v48, 16, v30
	s_nop 0
	v_and_b32_e32 v49, 0xffff0000, v30
	v_lshlrev_b32_e32 v30, 16, v31
	s_nop 0
	v_and_b32_e32 v31, 0xffff0000, v31
	s_waitcnt vmcnt(6)
	v_lshlrev_b32_e32 v50, 16, v32
	v_and_b32_e32 v51, 0xffff0000, v32
	v_lshlrev_b32_e32 v32, 16, v33
	s_nop 0
	v_and_b32_e32 v33, 0xffff0000, v33
	v_lshlrev_b32_e32 v52, 16, v34
	s_nop 0
	v_and_b32_e32 v53, 0xffff0000, v34
	v_lshlrev_b32_e32 v34, 16, v35
	s_nop 0
	v_and_b32_e32 v35, 0xffff0000, v35
	v_pk_fma_f32 v[32:33], v[192:193], v[32:33], v[28:29]
	v_pk_fma_f32 v[28:29], v[190:191], v[50:51], v[46:47]
	v_pk_fma_f32 v[34:35], v[188:189], v[34:35], v[30:31]
	v_pk_fma_f32 v[30:31], v[186:187], v[52:53], v[48:49]
	v_cvt_pk_bf16_f32 v28, v28, v29
	v_cvt_pk_bf16_f32 v29, v32, v33
	s_waitcnt vmcnt(5)
	v_lshlrev_b32_e32 v32, 16, v38
	v_cvt_pk_bf16_f32 v30, v30, v31
	v_cvt_pk_bf16_f32 v31, v34, v35
	global_store_dwordx4 v[44:45], v[28:31], off
	v_and_b32_e32 v33, 0xffff0000, v38
	v_lshlrev_b32_e32 v34, 16, v39
	v_lshlrev_b32_e32 v28, 16, v36
	v_and_b32_e32 v29, 0xffff0000, v36
	v_lshlrev_b32_e32 v30, 16, v37
	s_nop 0
	v_and_b32_e32 v31, 0xffff0000, v37
	s_waitcnt vmcnt(5)
	v_lshlrev_b32_e32 v36, 16, v40
	v_and_b32_e32 v37, 0xffff0000, v40
	v_and_b32_e32 v35, 0xffff0000, v39
	v_lshlrev_b32_e32 v38, 16, v41
	s_nop 0
	v_and_b32_e32 v39, 0xffff0000, v41
	v_lshlrev_b32_e32 v40, 16, v42
	s_nop 0
	v_and_b32_e32 v41, 0xffff0000, v42
	v_pk_fma_f32 v[28:29], v[162:163], v[36:37], v[28:29]
	v_lshlrev_b32_e32 v42, 16, v43
	s_nop 0
	v_and_b32_e32 v43, 0xffff0000, v43
	v_pk_fma_f32 v[30:31], v[164:165], v[38:39], v[30:31]
	v_pk_fma_f32 v[32:33], v[158:159], v[40:41], v[32:33]
	v_cvt_pk_bf16_f32 v28, v28, v29
	v_cvt_pk_bf16_f32 v29, v30, v31
	v_pk_fma_f32 v[34:35], v[160:161], v[42:43], v[34:35]
	v_cvt_pk_bf16_f32 v30, v32, v33
	s_waitcnt vmcnt(3)
	v_lshlrev_b32_e32 v32, 16, v8
	v_cvt_pk_bf16_f32 v31, v34, v35
	global_store_dwordx4 v[44:45], v[28:31], off offset:256
	v_and_b32_e32 v33, 0xffff0000, v8
	v_lshlrev_b32_e32 v8, 16, v9
	v_lshlrev_b32_e32 v28, 16, v12
	v_and_b32_e32 v29, 0xffff0000, v12
	v_lshlrev_b32_e32 v12, 16, v13
	s_nop 0
	v_and_b32_e32 v13, 0xffff0000, v13
	v_and_b32_e32 v9, 0xffff0000, v9
	v_lshlrev_b32_e32 v30, 16, v14
	s_nop 0
	v_and_b32_e32 v31, 0xffff0000, v14
	v_lshlrev_b32_e32 v14, 16, v15
	s_nop 0
	v_and_b32_e32 v15, 0xffff0000, v15
	v_lshlrev_b32_e32 v34, 16, v10
	s_nop 0
	v_and_b32_e32 v35, 0xffff0000, v10
	v_lshlrev_b32_e32 v10, 16, v11
	s_nop 0
	v_and_b32_e32 v11, 0xffff0000, v11
	v_pk_fma_f32 v[12:13], v[184:185], v[8:9], v[12:13]
	v_pk_fma_f32 v[8:9], v[182:183], v[32:33], v[28:29]
	v_pk_fma_f32 v[14:15], v[180:181], v[10:11], v[14:15]
	v_pk_fma_f32 v[10:11], v[178:179], v[34:35], v[30:31]
	v_cvt_pk_bf16_f32 v8, v8, v9
	v_cvt_pk_bf16_f32 v9, v12, v13
	s_waitcnt vmcnt(2)
	v_lshlrev_b32_e32 v12, 16, v4
	v_cvt_pk_bf16_f32 v10, v10, v11
	v_cvt_pk_bf16_f32 v11, v14, v15
	global_store_dwordx4 v27, v[8:11], s[70:71]
	v_and_b32_e32 v13, 0xffff0000, v4
	v_lshlrev_b32_e32 v4, 16, v5
	v_lshlrev_b32_e32 v8, 16, v0
	v_and_b32_e32 v9, 0xffff0000, v0
	v_lshlrev_b32_e32 v0, 16, v1
	s_nop 0
	v_and_b32_e32 v1, 0xffff0000, v1
	v_and_b32_e32 v5, 0xffff0000, v5
	v_lshlrev_b32_e32 v10, 16, v2
	s_nop 0
	v_and_b32_e32 v11, 0xffff0000, v2
	v_lshlrev_b32_e32 v2, 16, v3
	s_nop 0
	v_and_b32_e32 v3, 0xffff0000, v3
	v_lshlrev_b32_e32 v14, 16, v6
	s_nop 0
	v_and_b32_e32 v15, 0xffff0000, v6
	v_lshlrev_b32_e32 v6, 16, v7
	s_nop 0
	v_and_b32_e32 v7, 0xffff0000, v7
	v_pk_fma_f32 v[4:5], v[152:153], v[4:5], v[0:1]
	v_pk_fma_f32 v[0:1], v[150:151], v[12:13], v[8:9]
	v_pk_fma_f32 v[6:7], v[148:149], v[6:7], v[2:3]
	v_pk_fma_f32 v[2:3], v[146:147], v[14:15], v[10:11]
	v_cvt_pk_bf16_f32 v0, v0, v1
	v_cvt_pk_bf16_f32 v1, v4, v5
	v_lshl_add_u32 v42, v26, 11, v22
	v_cvt_pk_bf16_f32 v2, v2, v3
	v_cvt_pk_bf16_f32 v3, v6, v7
	global_store_dwordx4 v27, v[0:3], s[70:71] offset:256
	v_lshl_add_u32 v52, v25, 11, v22
	v_mov_b32_e32 v43, v97
	v_ashrrev_i32_e32 v0, 12, v26
	v_mul_i32_i24_e32 v0, 0x1800, v0
	v_add_lshl_u32 v0, v0, v21, 1
	global_load_dwordx4 v[26:29], v42, s[70:71]
	global_load_dwordx4 v[30:33], v0, s[2:3]
	global_load_dwordx4 v[34:37], v42, s[70:71] offset:256
	global_load_dwordx4 v[38:41], v0, s[2:3] offset:256
	v_ashrrev_i32_e32 v0, 12, v25
	s_nop 0
	v_mul_i32_i24_e32 v0, 0x1800, v0
	v_add_lshl_u32 v0, v0, v21, 1
	global_load_dwordx4 v[12:15], v52, s[70:71]
	global_load_dwordx4 v[8:11], v0, s[2:3]
	global_load_dwordx4 v[4:7], v52, s[70:71] offset:256
	s_nop 0
	s_nop 0
	global_load_dwordx4 v[0:3], v0, s[2:3] offset:256
	v_add_u32_e64 v25, v17, v239
	v_cmp_lt_i32_e32 vcc, v25, v16
	v_lshlrev_b32_e32 v25, 11, v239
	v_add_u32_e32 v25, v18, v25
	v_cndmask_b32_e32 v42, v25, v42, vcc
	v_lshl_add_u64 v[42:43], s[70:71], 0, v[42:43]
	v_add_u32_e64 v25, v17, v240
	v_cmp_lt_i32_e32 vcc, v25, v16
	v_lshlrev_b32_e32 v25, 11, v240
	v_add_u32_e32 v25, v18, v25
	v_cndmask_b32_e32 v25, v25, v52, vcc
	s_waitcnt vmcnt(7)
	v_lshlrev_b32_e32 v44, 16, v26
	v_and_b32_e32 v45, 0xffff0000, v26
	v_lshlrev_b32_e32 v26, 16, v27
	s_nop 0
	v_and_b32_e32 v27, 0xffff0000, v27
	v_lshlrev_b32_e32 v46, 16, v28
	s_nop 0
	v_and_b32_e32 v47, 0xffff0000, v28
	v_lshlrev_b32_e32 v28, 16, v29
	s_nop 0
	v_and_b32_e32 v29, 0xffff0000, v29
	s_waitcnt vmcnt(6)
	v_lshlrev_b32_e32 v48, 16, v30
	v_and_b32_e32 v49, 0xffff0000, v30
	v_lshlrev_b32_e32 v30, 16, v31
	s_nop 0
	v_and_b32_e32 v31, 0xffff0000, v31
	v_lshlrev_b32_e32 v50, 16, v32
	s_nop 0
	v_and_b32_e32 v51, 0xffff0000, v32
	v_lshlrev_b32_e32 v32, 16, v33
	s_nop 0
	v_and_b32_e32 v33, 0xffff0000, v33
	v_pk_fma_f32 v[30:31], v[176:177], v[30:31], v[26:27]
	v_pk_fma_f32 v[26:27], v[174:175], v[48:49], v[44:45]
	v_pk_fma_f32 v[32:33], v[172:173], v[32:33], v[28:29]
	v_pk_fma_f32 v[28:29], v[170:171], v[50:51], v[46:47]
	v_cvt_pk_bf16_f32 v26, v26, v27
	v_cvt_pk_bf16_f32 v27, v30, v31
	s_waitcnt vmcnt(5)
	v_lshlrev_b32_e32 v30, 16, v36
	v_cvt_pk_bf16_f32 v28, v28, v29
	v_cvt_pk_bf16_f32 v29, v32, v33
	global_store_dwordx4 v[42:43], v[26:29], off
	v_and_b32_e32 v31, 0xffff0000, v36
	v_lshlrev_b32_e32 v32, 16, v37
	v_lshlrev_b32_e32 v26, 16, v34
	v_and_b32_e32 v27, 0xffff0000, v34
	v_lshlrev_b32_e32 v28, 16, v35
	s_nop 0
	v_and_b32_e32 v29, 0xffff0000, v35
	s_waitcnt vmcnt(5)
	v_lshlrev_b32_e32 v34, 16, v38
	v_and_b32_e32 v35, 0xffff0000, v38
	v_and_b32_e32 v33, 0xffff0000, v37
	v_lshlrev_b32_e32 v36, 16, v39
	s_nop 0
	v_and_b32_e32 v37, 0xffff0000, v39
	v_lshlrev_b32_e32 v38, 16, v40
	s_nop 0
	v_and_b32_e32 v39, 0xffff0000, v40
	v_pk_fma_f32 v[26:27], v[142:143], v[34:35], v[26:27]
	v_lshlrev_b32_e32 v40, 16, v41
	s_nop 0
	v_and_b32_e32 v41, 0xffff0000, v41
	v_pk_fma_f32 v[28:29], v[144:145], v[36:37], v[28:29]
	v_pk_fma_f32 v[30:31], v[138:139], v[38:39], v[30:31]
	v_cvt_pk_bf16_f32 v26, v26, v27
	v_cvt_pk_bf16_f32 v27, v28, v29
	v_pk_fma_f32 v[32:33], v[140:141], v[40:41], v[32:33]
	v_cvt_pk_bf16_f32 v28, v30, v31
	s_waitcnt vmcnt(3)
	v_lshlrev_b32_e32 v30, 16, v8
	v_cvt_pk_bf16_f32 v29, v32, v33
	global_store_dwordx4 v[42:43], v[26:29], off offset:256
	v_and_b32_e32 v31, 0xffff0000, v8
	v_lshlrev_b32_e32 v8, 16, v9
	v_lshlrev_b32_e32 v26, 16, v12
	v_and_b32_e32 v27, 0xffff0000, v12
	v_lshlrev_b32_e32 v12, 16, v13
	s_nop 0
	v_and_b32_e32 v13, 0xffff0000, v13
	v_and_b32_e32 v9, 0xffff0000, v9
	v_lshlrev_b32_e32 v28, 16, v14
	s_nop 0
	v_and_b32_e32 v29, 0xffff0000, v14
	v_lshlrev_b32_e32 v14, 16, v15
	s_nop 0
	v_and_b32_e32 v15, 0xffff0000, v15
	v_lshlrev_b32_e32 v32, 16, v10
	s_nop 0
	v_and_b32_e32 v33, 0xffff0000, v10
	v_lshlrev_b32_e32 v10, 16, v11
	s_nop 0
	v_and_b32_e32 v11, 0xffff0000, v11
	v_pk_fma_f32 v[12:13], v[168:169], v[8:9], v[12:13]
	v_pk_fma_f32 v[8:9], v[166:167], v[30:31], v[26:27]
	v_pk_fma_f32 v[14:15], v[156:157], v[10:11], v[14:15]
	v_pk_fma_f32 v[10:11], v[154:155], v[32:33], v[28:29]
	v_cvt_pk_bf16_f32 v8, v8, v9
	v_cvt_pk_bf16_f32 v9, v12, v13
	s_waitcnt vmcnt(2)
	v_lshlrev_b32_e32 v12, 16, v0
	v_cvt_pk_bf16_f32 v10, v10, v11
	v_cvt_pk_bf16_f32 v11, v14, v15
	global_store_dwordx4 v25, v[8:11], s[70:71]
	v_and_b32_e32 v13, 0xffff0000, v0
	v_lshlrev_b32_e32 v0, 16, v1
	v_lshlrev_b32_e32 v8, 16, v4
	v_and_b32_e32 v9, 0xffff0000, v4
	v_lshlrev_b32_e32 v4, 16, v5
	s_nop 0
	v_and_b32_e32 v5, 0xffff0000, v5
	v_and_b32_e32 v1, 0xffff0000, v1
	v_lshlrev_b32_e32 v10, 16, v6
	s_nop 0
	v_and_b32_e32 v11, 0xffff0000, v6
	v_lshlrev_b32_e32 v6, 16, v7
	s_nop 0
	v_and_b32_e32 v7, 0xffff0000, v7
	v_lshlrev_b32_e32 v14, 16, v2
	s_nop 0
	v_and_b32_e32 v15, 0xffff0000, v2
	v_lshlrev_b32_e32 v2, 16, v3
	s_nop 0
	v_and_b32_e32 v3, 0xffff0000, v3
	v_pk_fma_f32 v[4:5], v[136:137], v[0:1], v[4:5]
	v_pk_fma_f32 v[0:1], v[134:135], v[12:13], v[8:9]
	v_pk_fma_f32 v[6:7], v[132:133], v[2:3], v[6:7]
	v_pk_fma_f32 v[2:3], v[130:131], v[14:15], v[10:11]
	v_cvt_pk_bf16_f32 v0, v0, v1
	v_cvt_pk_bf16_f32 v1, v4, v5
	v_lshl_add_u32 v40, v24, 11, v22
	v_cvt_pk_bf16_f32 v2, v2, v3
	v_cvt_pk_bf16_f32 v3, v6, v7
	global_store_dwordx4 v25, v[0:3], s[70:71] offset:256
	v_lshl_add_u32 v50, v23, 11, v22
	v_mov_b32_e32 v41, v97
	v_ashrrev_i32_e32 v0, 12, v24
	v_mul_i32_i24_e32 v0, 0x1800, v0
	v_add_lshl_u32 v0, v0, v21, 1
	global_load_dwordx4 v[24:27], v40, s[70:71]
	global_load_dwordx4 v[28:31], v0, s[2:3]
	global_load_dwordx4 v[32:35], v40, s[70:71] offset:256
	global_load_dwordx4 v[36:39], v0, s[2:3] offset:256
	v_ashrrev_i32_e32 v0, 12, v23
	s_nop 0
	v_mul_i32_i24_e32 v0, 0x1800, v0
	v_add_lshl_u32 v0, v0, v21, 1
	global_load_dwordx4 v[8:11], v50, s[70:71]
	global_load_dwordx4 v[12:15], v0, s[2:3]
	global_load_dwordx4 v[4:7], v50, s[70:71] offset:256
	s_nop 0
	s_nop 0
	global_load_dwordx4 v[0:3], v0, s[2:3] offset:256
	v_add_u32_e64 v23, v17, v241
	v_cmp_lt_i32_e32 vcc, v23, v16
	v_lshlrev_b32_e32 v23, 11, v241
	v_add_u32_e32 v23, v18, v23
	v_cndmask_b32_e32 v40, v23, v40, vcc
	v_lshl_add_u64 v[40:41], s[70:71], 0, v[40:41]
	v_add_u32_e64 v23, v17, v242
	v_cmp_lt_i32_e32 vcc, v23, v16
	v_lshlrev_b32_e32 v23, 11, v242
	v_add_u32_e32 v23, v18, v23
	v_cndmask_b32_e32 v23, v23, v50, vcc
	s_waitcnt vmcnt(7)
	v_lshlrev_b32_e32 v42, 16, v24
	v_and_b32_e32 v43, 0xffff0000, v24
	v_lshlrev_b32_e32 v24, 16, v25
	s_nop 0
	v_and_b32_e32 v25, 0xffff0000, v25
	v_lshlrev_b32_e32 v44, 16, v26
	s_nop 0
	v_and_b32_e32 v45, 0xffff0000, v26
	v_lshlrev_b32_e32 v26, 16, v27
	s_nop 0
	v_and_b32_e32 v27, 0xffff0000, v27
	s_waitcnt vmcnt(6)
	v_lshlrev_b32_e32 v46, 16, v28
	v_and_b32_e32 v47, 0xffff0000, v28
	v_lshlrev_b32_e32 v28, 16, v29
	s_nop 0
	v_and_b32_e32 v29, 0xffff0000, v29
	v_lshlrev_b32_e32 v48, 16, v30
	s_nop 0
	v_and_b32_e32 v49, 0xffff0000, v30
	v_lshlrev_b32_e32 v30, 16, v31
	s_nop 0
	v_and_b32_e32 v31, 0xffff0000, v31
	v_pk_fma_f32 v[28:29], v[128:129], v[28:29], v[24:25]
	v_pk_fma_f32 v[24:25], v[126:127], v[46:47], v[42:43]
	v_pk_fma_f32 v[30:31], v[124:125], v[30:31], v[26:27]
	v_pk_fma_f32 v[26:27], v[122:123], v[48:49], v[44:45]
	v_cvt_pk_bf16_f32 v24, v24, v25
	v_cvt_pk_bf16_f32 v25, v28, v29
	s_waitcnt vmcnt(5)
	v_lshlrev_b32_e32 v28, 16, v34
	v_cvt_pk_bf16_f32 v26, v26, v27
	v_cvt_pk_bf16_f32 v27, v30, v31
	global_store_dwordx4 v[40:41], v[24:27], off
	v_and_b32_e32 v29, 0xffff0000, v34
	v_lshlrev_b32_e32 v30, 16, v35
	v_lshlrev_b32_e32 v24, 16, v32
	v_and_b32_e32 v25, 0xffff0000, v32
	v_lshlrev_b32_e32 v26, 16, v33
	s_nop 0
	v_and_b32_e32 v27, 0xffff0000, v33
	s_waitcnt vmcnt(5)
	v_lshlrev_b32_e32 v32, 16, v36
	v_and_b32_e32 v33, 0xffff0000, v36
	v_and_b32_e32 v31, 0xffff0000, v35
	v_lshlrev_b32_e32 v34, 16, v37
	s_nop 0
	v_and_b32_e32 v35, 0xffff0000, v37
	v_lshlrev_b32_e32 v36, 16, v38
	s_nop 0
	v_and_b32_e32 v37, 0xffff0000, v38
	v_pk_fma_f32 v[24:25], v[92:93], v[32:33], v[24:25]
	v_lshlrev_b32_e32 v38, 16, v39
	s_nop 0
	v_and_b32_e32 v39, 0xffff0000, v39
	v_pk_fma_f32 v[26:27], v[94:95], v[34:35], v[26:27]
	v_pk_fma_f32 v[28:29], v[88:89], v[36:37], v[28:29]
	v_cvt_pk_bf16_f32 v24, v24, v25
	v_cvt_pk_bf16_f32 v25, v26, v27
	v_pk_fma_f32 v[30:31], v[90:91], v[38:39], v[30:31]
	v_cvt_pk_bf16_f32 v26, v28, v29
	s_waitcnt vmcnt(3)
	v_lshlrev_b32_e32 v28, 16, v12
	v_cvt_pk_bf16_f32 v27, v30, v31
	global_store_dwordx4 v[40:41], v[24:27], off offset:256
	v_and_b32_e32 v29, 0xffff0000, v12
	v_lshlrev_b32_e32 v12, 16, v13
	v_lshlrev_b32_e32 v24, 16, v8
	v_and_b32_e32 v25, 0xffff0000, v8
	v_lshlrev_b32_e32 v8, 16, v9
	s_nop 0
	v_and_b32_e32 v9, 0xffff0000, v9
	v_and_b32_e32 v13, 0xffff0000, v13
	v_lshlrev_b32_e32 v26, 16, v10
	s_nop 0
	v_and_b32_e32 v27, 0xffff0000, v10
	v_lshlrev_b32_e32 v10, 16, v11
	s_nop 0
	v_and_b32_e32 v11, 0xffff0000, v11
	v_lshlrev_b32_e32 v30, 16, v14
	s_nop 0
	v_and_b32_e32 v31, 0xffff0000, v14
	v_lshlrev_b32_e32 v14, 16, v15
	s_nop 0
	v_and_b32_e32 v15, 0xffff0000, v15
	v_pk_fma_f32 v[12:13], v[120:121], v[12:13], v[8:9]
	v_pk_fma_f32 v[8:9], v[118:119], v[28:29], v[24:25]
	v_pk_fma_f32 v[14:15], v[116:117], v[14:15], v[10:11]
	v_pk_fma_f32 v[10:11], v[114:115], v[30:31], v[26:27]
	v_cvt_pk_bf16_f32 v8, v8, v9
	v_cvt_pk_bf16_f32 v9, v12, v13
	s_waitcnt vmcnt(2)
	v_lshlrev_b32_e32 v12, 16, v0
	v_cvt_pk_bf16_f32 v10, v10, v11
	v_cvt_pk_bf16_f32 v11, v14, v15
	global_store_dwordx4 v23, v[8:11], s[70:71]
	v_and_b32_e32 v13, 0xffff0000, v0
	v_lshlrev_b32_e32 v0, 16, v1
	v_lshlrev_b32_e32 v8, 16, v4
	v_and_b32_e32 v9, 0xffff0000, v4
	v_lshlrev_b32_e32 v4, 16, v5
	s_nop 0
	v_and_b32_e32 v5, 0xffff0000, v5
	v_and_b32_e32 v1, 0xffff0000, v1
	v_lshlrev_b32_e32 v10, 16, v6
	s_nop 0
	v_and_b32_e32 v11, 0xffff0000, v6
	v_lshlrev_b32_e32 v6, 16, v7
	s_nop 0
	v_and_b32_e32 v7, 0xffff0000, v7
	v_lshlrev_b32_e32 v14, 16, v2
	s_nop 0
	v_and_b32_e32 v15, 0xffff0000, v2
	v_lshlrev_b32_e32 v2, 16, v3
	s_nop 0
	v_and_b32_e32 v3, 0xffff0000, v3
	v_pk_fma_f32 v[4:5], v[86:87], v[0:1], v[4:5]
	v_pk_fma_f32 v[0:1], v[84:85], v[12:13], v[8:9]
	v_pk_fma_f32 v[6:7], v[82:83], v[2:3], v[6:7]
	v_pk_fma_f32 v[2:3], v[80:81], v[14:15], v[10:11]
	v_cvt_pk_bf16_f32 v0, v0, v1
	v_cvt_pk_bf16_f32 v1, v4, v5
	v_lshl_add_u32 v36, v20, 11, v22
	v_cvt_pk_bf16_f32 v2, v2, v3
	v_cvt_pk_bf16_f32 v3, v6, v7
	global_store_dwordx4 v23, v[0:3], s[70:71] offset:256
	v_lshl_add_u32 v46, v19, 11, v22
	v_ashrrev_i32_e32 v19, 12, v19
	v_ashrrev_i32_e32 v0, 12, v20
	v_mul_i32_i24_e32 v0, 0x1800, v0
	v_add_lshl_u32 v12, v0, v21, 1
	global_load_dwordx4 v[0:3], v36, s[70:71]
	global_load_dwordx4 v[4:7], v12, s[2:3]
	global_load_dwordx4 v[8:11], v36, s[70:71] offset:256
	s_nop 0
	s_nop 0
	global_load_dwordx4 v[12:15], v12, s[2:3] offset:256
	v_mul_i32_i24_e32 v19, 0x1800, v19
	v_add_lshl_u32 v19, v19, v21, 1
	global_load_dwordx4 v[20:23], v46, s[70:71]
	global_load_dwordx4 v[24:27], v19, s[2:3]
	global_load_dwordx4 v[28:31], v46, s[70:71] offset:256
	global_load_dwordx4 v[32:35], v19, s[2:3] offset:256
	v_add_u32_e32 v19, v17, v243
	v_cmp_lt_i32_e32 vcc, v19, v16
	v_add_u32_e64 v19, v18, v244
	v_mov_b32_e32 v37, v97
	v_cndmask_b32_e32 v36, v19, v36, vcc
	v_lshl_add_u64 v[36:37], s[70:71], 0, v[36:37]
	s_waitcnt vmcnt(7)
	v_lshlrev_b32_e32 v38, 16, v0
	v_and_b32_e32 v39, 0xffff0000, v0
	v_lshlrev_b32_e32 v0, 16, v1
	s_nop 0
	v_and_b32_e32 v1, 0xffff0000, v1
	v_lshlrev_b32_e32 v40, 16, v2
	s_nop 0
	v_and_b32_e32 v41, 0xffff0000, v2
	v_lshlrev_b32_e32 v2, 16, v3
	s_nop 0
	v_and_b32_e32 v3, 0xffff0000, v3
	s_waitcnt vmcnt(6)
	v_lshlrev_b32_e32 v42, 16, v4
	v_and_b32_e32 v43, 0xffff0000, v4
	v_lshlrev_b32_e32 v4, 16, v5
	s_nop 0
	v_and_b32_e32 v5, 0xffff0000, v5
	v_lshlrev_b32_e32 v44, 16, v6
	s_nop 0
	v_and_b32_e32 v45, 0xffff0000, v6
	v_lshlrev_b32_e32 v6, 16, v7
	s_nop 0
	v_and_b32_e32 v7, 0xffff0000, v7
	v_pk_fma_f32 v[4:5], v[112:113], v[4:5], v[0:1]
	v_pk_fma_f32 v[0:1], v[110:111], v[42:43], v[38:39]
	v_pk_fma_f32 v[6:7], v[108:109], v[6:7], v[2:3]
	v_pk_fma_f32 v[2:3], v[106:107], v[44:45], v[40:41]
	v_cvt_pk_bf16_f32 v0, v0, v1
	v_cvt_pk_bf16_f32 v1, v4, v5
	s_waitcnt vmcnt(5)
	v_lshlrev_b32_e32 v4, 16, v10
	v_cvt_pk_bf16_f32 v2, v2, v3
	v_cvt_pk_bf16_f32 v3, v6, v7
	global_store_dwordx4 v[36:37], v[0:3], off
	v_and_b32_e32 v5, 0xffff0000, v10
	v_lshlrev_b32_e32 v6, 16, v11
	v_lshlrev_b32_e32 v0, 16, v8
	v_and_b32_e32 v1, 0xffff0000, v8
	v_lshlrev_b32_e32 v2, 16, v9
	s_nop 0
	v_and_b32_e32 v3, 0xffff0000, v9
	s_waitcnt vmcnt(5)
	v_lshlrev_b32_e32 v8, 16, v12
	v_and_b32_e32 v9, 0xffff0000, v12
	v_and_b32_e32 v7, 0xffff0000, v11
	v_lshlrev_b32_e32 v10, 16, v13
	s_nop 0
	v_and_b32_e32 v11, 0xffff0000, v13
	v_pk_fma_f32 v[0:1], v[76:77], v[8:9], v[0:1]
	v_lshlrev_b32_e32 v12, 16, v14
	s_nop 0
	v_and_b32_e32 v13, 0xffff0000, v14
	v_lshlrev_b32_e32 v14, 16, v15
	s_nop 0
	v_and_b32_e32 v15, 0xffff0000, v15
	v_pk_fma_f32 v[2:3], v[78:79], v[10:11], v[2:3]
	v_cvt_pk_bf16_f32 v0, v0, v1
	v_pk_fma_f32 v[6:7], v[74:75], v[14:15], v[6:7]
	v_pk_fma_f32 v[4:5], v[72:73], v[12:13], v[4:5]
	v_cvt_pk_bf16_f32 v1, v2, v3
	s_waitcnt vmcnt(3)
	v_lshlrev_b32_e32 v8, 16, v24
	v_cvt_pk_bf16_f32 v2, v4, v5
	v_cvt_pk_bf16_f32 v3, v6, v7
	global_store_dwordx4 v[36:37], v[0:3], off offset:256
	v_and_b32_e32 v9, 0xffff0000, v24
	v_lshlrev_b32_e32 v10, 16, v25
	v_add_u32_e32 v0, v17, v245
	v_cmp_lt_i32_e32 vcc, v0, v16
	v_add_u32_e32 v0, v18, v246
	v_and_b32_e32 v1, 0xffff0000, v20
	v_cndmask_b32_e32 v16, v0, v46, vcc
	v_lshlrev_b32_e32 v0, 16, v20
	v_lshlrev_b32_e32 v2, 16, v21
	s_nop 0
	v_and_b32_e32 v3, 0xffff0000, v21
	v_and_b32_e32 v11, 0xffff0000, v25
	v_lshlrev_b32_e32 v4, 16, v22
	s_nop 0
	v_and_b32_e32 v5, 0xffff0000, v22
	v_lshlrev_b32_e32 v6, 16, v23
	s_nop 0
	v_and_b32_e32 v7, 0xffff0000, v23
	v_lshlrev_b32_e32 v12, 16, v26
	s_nop 0
	v_and_b32_e32 v13, 0xffff0000, v26
	v_lshlrev_b32_e32 v14, 16, v27
	s_nop 0
	v_and_b32_e32 v15, 0xffff0000, v27
	v_pk_fma_f32 v[2:3], v[104:105], v[10:11], v[2:3]
	v_pk_fma_f32 v[0:1], v[102:103], v[8:9], v[0:1]
	v_pk_fma_f32 v[6:7], v[100:101], v[14:15], v[6:7]
	v_pk_fma_f32 v[4:5], v[98:99], v[12:13], v[4:5]
	v_cvt_pk_bf16_f32 v0, v0, v1
	v_cvt_pk_bf16_f32 v1, v2, v3
	s_waitcnt vmcnt(2)
	v_lshlrev_b32_e32 v8, 16, v32
	v_cvt_pk_bf16_f32 v2, v4, v5
	v_cvt_pk_bf16_f32 v3, v6, v7
	global_store_dwordx4 v16, v[0:3], s[70:71]
	v_and_b32_e32 v9, 0xffff0000, v32
	v_lshlrev_b32_e32 v10, 16, v33
	v_lshlrev_b32_e32 v0, 16, v28
	v_and_b32_e32 v1, 0xffff0000, v28
	v_lshlrev_b32_e32 v2, 16, v29
	s_nop 0
	v_and_b32_e32 v3, 0xffff0000, v29
	v_and_b32_e32 v11, 0xffff0000, v33
	v_lshlrev_b32_e32 v4, 16, v30
	s_nop 0
	v_and_b32_e32 v5, 0xffff0000, v30
	v_lshlrev_b32_e32 v6, 16, v31
	s_nop 0
	v_and_b32_e32 v7, 0xffff0000, v31
	v_lshlrev_b32_e32 v12, 16, v34
	s_nop 0
	v_and_b32_e32 v13, 0xffff0000, v34
	v_lshlrev_b32_e32 v14, 16, v35
	s_nop 0
	v_and_b32_e32 v15, 0xffff0000, v35
	v_pk_fma_f32 v[2:3], v[70:71], v[10:11], v[2:3]
	v_pk_fma_f32 v[0:1], v[68:69], v[8:9], v[0:1]
	s_andn2_b64 vcc, exec, s[24:25]
	s_nop 0
	v_pk_fma_f32 v[6:7], v[66:67], v[14:15], v[6:7]
	v_pk_fma_f32 v[4:5], v[64:65], v[12:13], v[4:5]
	v_cvt_pk_bf16_f32 v0, v0, v1
	v_cvt_pk_bf16_f32 v1, v2, v3
	s_nop 0
	s_nop 0
	v_cvt_pk_bf16_f32 v2, v4, v5
	v_cvt_pk_bf16_f32 v3, v6, v7
	global_store_dwordx4 v16, v[0:3], s[70:71] offset:256
	s_cbranch_vccnz .LBB0_1441
	s_nop 0
	v_readlane_b32 s12, v254, 26
	v_readlane_b32 s13, v254, 27
	s_andn2_b64 vcc, exec, s[12:13]
	s_cbranch_vccnz .LBB0_1440
	s_barrier
	s_branch .LBB0_1440
.LBB0_1512:
	s_waitcnt vmcnt(0)
	s_nop 0
	v_readlane_b32 s36, v254, 5
	v_readlane_b32 s61, v254, 3
	v_readlane_b32 s64, v254, 4
	v_readlane_b32 s65, v255, 47
	v_readlane_b32 s92, v255, 51
	v_readlane_b32 s37, v254, 6
	v_readlane_b32 s30, v254, 17
	v_readlane_b32 s31, v254, 12
	v_readlane_b32 s93, v254, 7
	v_readlane_b32 s38, v253, 9
	v_readlane_b32 s39, v255, 49
	s_barrier
.LBB0_1513:
	s_mov_b32 s10, s97
	s_nop 0
	s_nop 0
	v_mbcnt_lo_u32_b32 v0, -1, s10
	v_mbcnt_hi_u32_b32 v0, -1, v0
	v_readlane_b32 s10, v254, 40
	v_add_u32_e64 v8, s64, v0
	v_readlane_b32 s11, v254, 41
	s_and_b64 vcc, exec, s[10:11]
	v_readfirstlane_b32 s13, v8
	s_cbranch_vccz .LBB0_1526
	s_abs_i32 s11, s6
	v_readlane_b32 s12, v255, 6
	s_mul_hi_u32 s12, s11, s12
	s_nop 0
	v_readlane_b32 s16, v255, 7
	s_mul_i32 s14, s12, s16
	s_nop 0
	v_readlane_b32 s10, v254, 38
	s_sub_i32 s11, s11, s14
	s_xor_b32 s10, s7, s10
	s_add_i32 s14, s12, 1
	s_sub_i32 s15, s11, s16
	s_cmp_ge_u32 s11, s16
	s_cselect_b32 s12, s14, s12
	s_cselect_b32 s11, s15, s11
	s_add_i32 s14, s12, 1
	s_cmp_ge_u32 s11, s16
	s_cselect_b32 s11, s14, s12
	s_xor_b32 s11, s11, s10
	s_sub_i32 s12, s11, s10
	s_mul_i32 s10, s12, s61
	s_sub_i32 s10, s6, s10
	s_lshl_b32 s14, s10, 1
	s_cmp_le_i32 s14, s61
	v_readlane_b32 s15, v254, 56
	s_cselect_b64 s[10:11], -1, 0
	s_cmp_lt_i32 s15, s14
	s_cselect_b64 s[14:15], -1, 0
	s_and_b64 s[10:11], s[10:11], s[14:15]
	s_mov_b64 s[14:15], 0
	s_and_b64 vcc, exec, s[10:11]
	s_mov_b64 s[16:17], 0
	s_cbranch_vccz .LBB0_1521
	s_mul_hi_i32 s10, s12, s61
	s_mul_i32 s12, s12, s61
	v_readlane_b32 s11, v254, 57
	s_add_u32 s18, s12, s11
	s_nop 0
	v_readlane_b32 s11, v254, 58
	s_addc_u32 s19, s10, s11
	v_mov_b64_e32 v[0:1], s[6:7]
	v_cmp_lt_i64_e32 vcc, s[18:19], v[0:1]
	s_cbranch_vccz .LBB0_1521
	s_ashr_i32 s6, s18, 31
	s_lshr_b32 s6, s6, 29
	s_add_i32 s10, s18, s6
	s_and_b32 s6, s10, -8
	s_sub_i32 s11, s18, s6
	s_cmp_ge_i32 s11, s46
	s_mov_b64 s[6:7], -1
	s_cbranch_scc0 .LBB0_1518
	s_sub_i32 s6, s11, s46
	s_mul_i32 s6, s6, s31
	v_readlane_b32 s7, v254, 16
	s_add_i32 s12, s6, s7
	s_mov_b64 s[6:7], 0

.LBB0_1520:
	s_ashr_i32 s6, s10, 3
	s_add_i32 s6, s12, s6
	s_ashr_i32 s7, s6, 31
	s_lshr_b32 s7, s7, 27
	s_add_i32 s7, s6, s7
	s_ashr_i32 s10, s7, 5
	s_lshl_b32 s11, s10, 3
	s_sub_i32 s10, s58, s11
	s_min_i32 s12, s10, 8
	s_abs_i32 s10, s12
	v_cvt_f32_u32_e32 v0, s10
	s_sub_i32 s17, 0, s10
	s_andn2_b32 s7, s7, 31
	s_sub_i32 s6, s6, s7
	v_rcp_iflag_f32_e32 v0, v0
	s_abs_i32 s7, s6
	s_xor_b32 s16, s6, s12
	s_ashr_i32 s16, s16, 31
	s_nop 0
	v_mul_f32_e32 v0, 0x4f7ffffe, v0
	v_cvt_u32_f32_e32 v0, v0
	s_nop 0
	v_readfirstlane_b32 s18, v0
	s_mul_i32 s17, s17, s18
	s_mul_hi_u32 s17, s18, s17
	s_add_i32 s18, s18, s17
	s_mul_hi_u32 s17, s7, s18
	s_mul_i32 s18, s17, s10
	s_sub_i32 s7, s7, s18
	s_add_i32 s19, s17, 1
	s_sub_i32 s18, s7, s10
	s_cmp_ge_u32 s7, s10
	s_cselect_b32 s17, s19, s17
	s_cselect_b32 s7, s18, s7
	s_add_i32 s18, s17, 1
	s_cmp_ge_u32 s7, s10
	s_cselect_b32 s7, s18, s17
	s_xor_b32 s7, s7, s16
	s_sub_i32 s10, s7, s16
	s_mul_i32 s7, s10, s12
	s_sub_i32 s6, s6, s7
	s_add_i32 s11, s11, s6
	s_mov_b64 s[16:17], -1

.LBB0_1522:
	s_nop 0
	v_readlane_b32 s6, v254, 36
	v_readlane_b32 s7, v254, 37
	s_and_b64 vcc, exec, s[6:7]
	s_cbranch_vccz .LBB0_1542
	s_ashr_i32 s6, s38, 31
	s_lshr_b32 s6, s6, 27
	s_add_i32 s6, s38, s6
	s_andn2_b32 s6, s6, 31
	s_sub_i32 s6, s6, s38
	s_nop 0
	v_readlane_b32 s7, v254, 19
	s_add_i32 s6, s7, s6
	s_lshr_b32 s7, s6, 26
	s_and_b32 s7, s7, 32
	s_add_i32 s6, s7, s6
	s_cmp_lt_i32 s6, s39
	s_cbranch_scc0 .LBB0_1542
	v_readlane_b32 s7, v254, 24
	s_lshl_b32 s7, s7, 5
	s_ashr_i32 s6, s6, 1
	s_add_i32 s6, s6, s7
	s_cmp_lt_i32 s6, s44
	s_cbranch_scc0 .LBB0_1543
	s_ashr_i32 s7, s6, 31
	s_lshr_b32 s7, s7, 27
	s_add_i32 s7, s6, s7
	s_ashr_i32 s10, s7, 5
	s_lshl_b32 s10, s10, 3
	s_sub_i32 s11, s89, s10
	s_min_i32 s11, s11, 8
	s_abs_i32 s12, s11
	v_cvt_f32_u32_e32 v0, s12
	s_sub_i32 s15, 0, s12
	s_andn2_b32 s7, s7, 31
	s_sub_i32 s6, s6, s7
	v_rcp_iflag_f32_e32 v0, v0
	s_add_i32 s7, s10, s47
	s_abs_i32 s10, s6
	s_xor_b32 s14, s6, s11
	s_nop 0
	v_mul_f32_e32 v0, 0x4f7ffffe, v0
	v_cvt_u32_f32_e32 v0, v0
	s_ashr_i32 s14, s14, 31
	v_readfirstlane_b32 s16, v0
	s_mul_i32 s15, s15, s16
	s_mul_hi_u32 s15, s16, s15
	s_add_i32 s16, s16, s15
	s_mul_hi_u32 s15, s10, s16
	s_mul_i32 s16, s15, s12
	s_sub_i32 s10, s10, s16
	s_add_i32 s17, s15, 1
	s_sub_i32 s16, s10, s12
	s_cmp_ge_u32 s10, s12
	s_cselect_b32 s15, s17, s15
	s_cselect_b32 s10, s16, s10
	s_add_i32 s16, s15, 1
	s_cmp_ge_u32 s10, s12
	s_cselect_b32 s10, s16, s15
	s_xor_b32 s10, s10, s14
	s_sub_i32 s10, s10, s14
	s_mul_i32 s11, s10, s11
	s_sub_i32 s6, s6, s11
	s_add_i32 s11, s7, s6
	s_mov_b64 s[16:17], -1
	s_branch .LBB0_1543

.LBB0_1530:
	s_mov_b32 s0, s97
	s_waitcnt vmcnt(0)
	s_barrier
	s_nop 0
	v_mbcnt_lo_u32_b32 v0, -1, s0
	v_mbcnt_hi_u32_b32 v0, -1, v0
	v_cmp_eq_u32_e32 vcc, s65, v0
	s_and_saveexec_b64 s[22:23], vcc
	s_cbranch_execz .LBB0_1610
	s_nop 0
	v_readlane_b32 s34, v253, 12
	v_readlane_b32 s0, v253, 14
	v_readlane_b32 s35, v253, 13
	v_readlane_b32 s38, v253, 17
	v_mov_b32_e32 v0, s0
	s_waitcnt vmcnt(0) expcnt(0) lgkmcnt(0)
	ds_read_b32 v2, v0
	ds_read_b32 v0, v0 offset:4
	s_waitcnt lgkmcnt(1)
	v_cmp_ne_u32_e32 vcc, 0, v2
	s_cbranch_vccnz .LBB0_1559
	s_nop 0
	v_readlane_b32 s0, v253, 6
	v_readlane_b32 s1, v253, 7
	s_load_dwordx2 s[4:5], s[0:1], 0x4
	s_add_u32 s0, s34, 0x1000
	s_addc_u32 s1, s35, 0
	s_nop 0
	s_add_u32 s2, s34, 0x1100
	s_addc_u32 s3, s35, 0
	s_waitcnt lgkmcnt(0)
	s_mul_i32 s28, s4, s61
	s_nop 0
	s_add_u32 s4, s34, 0x1200
	s_mul_i32 s28, s28, s5
	s_addc_u32 s5, s35, 0
	s_add_u32 s6, s34, 0x1300
	s_addc_u32 s7, s35, 0
	s_mov_b32 s29, 1
	s_mov_b64 s[8:9], 0
	s_branch .LBB0_1535

.LBB0_1535:
	v_mov_b64_e32 v[12:13], s[34:35]
	flat_load_dword v1, v[12:13] offset:1024 sc1
	flat_load_dword v0, v[12:13] offset:1280 sc1
	flat_load_dword v2, v[12:13] offset:1536 sc1
	s_or_b64 s[14:15], s[14:15], exec
	s_or_b64 s[12:13], s[12:13], exec
	s_waitcnt vmcnt(0) lgkmcnt(0)
	v_add_u32_e32 v3, v0, v1
	v_add_u32_e64 v4, v3, v2
	flat_load_dword v3, v[12:13] offset:1792 sc1
	s_waitcnt vmcnt(0) lgkmcnt(0)
	v_add_u32_e32 v5, v4, v3
	flat_load_dword v4, v[12:13] offset:2048 sc1
	s_waitcnt vmcnt(0) lgkmcnt(0)
	v_add_u32_e32 v6, v5, v4
	flat_load_dword v5, v[12:13] offset:2304 sc1
	s_waitcnt vmcnt(0) lgkmcnt(0)
	v_add_u32_e32 v7, v6, v5
	flat_load_dword v6, v[12:13] offset:2560 sc1
	s_waitcnt vmcnt(0) lgkmcnt(0)
	v_add_u32_e32 v8, v7, v6
	flat_load_dword v7, v[12:13] offset:2816 sc1
	s_waitcnt vmcnt(0) lgkmcnt(0)
	v_add_u32_e32 v9, v8, v7
	flat_load_dword v8, v[12:13] offset:3072 sc1
	s_waitcnt vmcnt(0) lgkmcnt(0)
	v_add_u32_e32 v10, v9, v8
	flat_load_dword v9, v[12:13] offset:3328 sc1
	s_waitcnt vmcnt(0) lgkmcnt(0)
	v_add_u32_e32 v11, v10, v9
	flat_load_dword v10, v[12:13] offset:3584 sc1
	s_waitcnt vmcnt(0) lgkmcnt(0)
	v_add_u32_e32 v14, v11, v10
	flat_load_dword v11, v[12:13] offset:3840 sc1
	v_mov_b64_e32 v[12:13], s[0:1]
	s_nop 0
	flat_load_dword v12, v[12:13] sc1
	s_waitcnt vmcnt(0) lgkmcnt(0)
	v_add_u32_e32 v14, v14, v11
	v_add_u32_e32 v16, v14, v12
	v_mov_b64_e32 v[14:15], s[2:3]
	flat_load_dword v13, v[14:15] sc1
	v_mov_b64_e32 v[14:15], s[4:5]
	s_nop 0
	flat_load_dword v14, v[14:15] sc1
	s_waitcnt vmcnt(0) lgkmcnt(0)
	v_add_u32_e32 v16, v16, v13
	v_add_u32_e32 v18, v16, v14
	v_mov_b64_e32 v[16:17], s[6:7]
	flat_load_dword v15, v[16:17] sc1
	s_waitcnt vmcnt(0) lgkmcnt(0)
	v_add_u32_e32 v16, v18, v15
	v_cmp_ne_u32_e32 vcc, s28, v16
	s_and_saveexec_b64 s[16:17], vcc
	s_cbranch_execz .LBB0_1534
	s_nop 0
	s_and_b32 s20, s29, 0xff
	s_mov_b64 s[18:19], -1
	s_cmp_eq_u32 s20, 0
	s_mov_b64 s[24:25], -1
	s_mov_b64 s[20:21], -1
	s_sleep 1
	s_cbranch_scc1 .LBB0_1538
	s_and_saveexec_b64 s[26:27], s[24:25]
	s_cbranch_execz .LBB0_1533
	s_branch .LBB0_1541

.LBB0_1542:
.LBB0_1543:
	s_nop 0
	v_readlane_b32 s6, v254, 19
	s_and_b64 vcc, exec, s[16:17]
	s_cbranch_vccz .LBB0_1528
.LBB0_1544:
	s_lshl_b32 s7, s11, 2
	s_nop 0
	v_readlane_b32 s14, v254, 30
	s_add_i32 s7, s14, s7
	v_mov_b32_e32 v0, s7
	ds_read_b32 v0, v0 offset:256
	s_lshl_b32 s6, s6, 7
	s_nop 0
	s_and_b32 s6, s6, 0x80
	s_waitcnt lgkmcnt(0)
	v_readfirstlane_b32 s12, v0
	v_lshlrev_b32_e32 v0, 2, v0
	v_add_u32_e32 v0, s14, v0
	ds_read_b32 v0, v0
	s_waitcnt lgkmcnt(0)
	v_sub_u32_e32 v0, s11, v0
	v_lshlrev_b32_e32 v78, 8, v0
.LBB0_1545:
	s_and_b64 vcc, exec, s[0:1]
	s_cbranch_vccnz .LBB0_1583
	v_mov_b32_e32 v0, s51
	ds_read_b32 v0, v0
	s_waitcnt lgkmcnt(0)
	v_cmp_ne_u32_e32 vcc, 0, v0
	s_cbranch_vccnz .LBB0_1583
	s_nop 0
	s_memrealtime s[0:1]
	s_lshl_b32 s14, s11, 6
	s_ashr_i32 s15, s14, 31
	s_lshl_b64 s[14:15], s[14:15], 2
	s_add_u32 s14, s4, s14
	s_addc_u32 s15, s5, s15
	s_mov_b32 s7, 1
	s_branch .LBB0_1550

.LBB0_1553:
	s_nop 0
	global_load_dword v0, v97, s[8:9] sc1
	s_waitcnt vmcnt(0)
	v_readfirstlane_b32 s16, v0
	s_cmp_eq_u32 s16, 0
	s_cselect_b64 s[18:19], -1, 0
	s_mov_b64 s[16:17], -1
	s_andn2_b64 vcc, exec, s[18:19]
	s_mov_b64 s[18:19], -1
	s_cbranch_vccnz .LBB0_1549

.LBB0_1558:
	s_or_b64 exec, exec, s[0:1]
	s_cmp_eq_u32 s38, 15
	s_cselect_b64 vcc, -1, 0
	s_cmp_eq_u32 s38, 14
	s_cselect_b64 s[0:1], -1, 0
	s_cmp_eq_u32 s38, 13
	s_cselect_b64 s[2:3], -1, 0
	s_cmp_eq_u32 s38, 12
	s_cselect_b64 s[4:5], -1, 0
	s_cmp_eq_u32 s38, 11
	s_cselect_b64 s[6:7], -1, 0
	s_cmp_eq_u32 s38, 10
	s_cselect_b64 s[8:9], -1, 0
	s_cmp_eq_u32 s38, 9
	s_cselect_b64 s[10:11], -1, 0
	s_cmp_eq_u32 s38, 8
	s_cselect_b64 s[12:13], -1, 0
	s_cmp_eq_u32 s38, 7
	s_cselect_b64 s[14:15], -1, 0
	s_cmp_eq_u32 s38, 6
	s_cselect_b64 s[16:17], -1, 0
	s_cmp_eq_u32 s38, 5
	s_cselect_b64 s[18:19], -1, 0
	s_cmp_eq_u32 s38, 4
	s_cselect_b64 s[20:21], -1, 0
	s_cmp_eq_u32 s38, 3
	s_cselect_b64 s[24:25], -1, 0
	s_cmp_eq_u32 s38, 2
	s_cselect_b64 s[26:27], -1, 0
	s_cmp_eq_u32 s38, 1
	s_cselect_b64 s[28:29], -1, 0
	s_cmp_eq_u32 s38, 0
	s_cselect_b64 s[30:31], -1, 0
	s_nop 0
	v_cndmask_b32_e64 v16, 0, v1, s[30:31]
	v_cndmask_b32_e64 v16, v16, v0, s[28:29]
	v_cndmask_b32_e64 v16, v16, v2, s[26:27]
	v_cndmask_b32_e64 v16, v16, v3, s[24:25]
	v_cndmask_b32_e64 v16, v16, v4, s[20:21]
	v_cndmask_b32_e64 v16, v16, v5, s[18:19]
	v_cndmask_b32_e64 v16, v16, v6, s[16:17]
	v_cndmask_b32_e64 v16, v16, v7, s[14:15]
	v_cndmask_b32_e64 v16, v16, v8, s[12:13]
	v_cndmask_b32_e64 v16, v16, v9, s[10:11]
	v_cndmask_b32_e64 v16, v16, v10, s[8:9]
	v_cndmask_b32_e64 v16, v16, v11, s[6:7]
	v_cndmask_b32_e64 v16, v16, v12, s[4:5]
	v_cndmask_b32_e64 v16, v16, v13, s[2:3]
	v_cndmask_b32_e64 v16, v16, v14, s[0:1]
	v_cndmask_b32_e32 v16, v16, v15, vcc
	v_cmp_ne_u32_e32 vcc, 0, v1
	v_readlane_b32 s0, v253, 14
	s_nop 0
	s_nop 0
	v_cndmask_b32_e64 v1, 0, 1, vcc
	v_cmp_ne_u32_e32 vcc, 0, v0
	s_nop 1
	v_addc_co_u32_e32 v0, vcc, 0, v1, vcc
	v_cmp_ne_u32_e32 vcc, 0, v2
	v_max_u32_e32 v2, 1, v16
	s_nop 0
	v_cndmask_b32_e64 v1, 0, 1, vcc
	v_cmp_ne_u32_e32 vcc, 0, v3
	s_nop 1
	v_addc_co_u32_e32 v0, vcc, v0, v1, vcc
	v_cmp_ne_u32_e32 vcc, 0, v4
	s_nop 1
	s_nop 0
	v_cndmask_b32_e64 v1, 0, 1, vcc
	v_cmp_ne_u32_e32 vcc, 0, v5
	s_nop 1
	v_addc_co_u32_e32 v0, vcc, v0, v1, vcc
	v_cmp_ne_u32_e32 vcc, 0, v6
	s_nop 1
	s_nop 0
	v_cndmask_b32_e64 v1, 0, 1, vcc
	v_cmp_ne_u32_e32 vcc, 0, v7
	s_nop 1
	v_addc_co_u32_e32 v0, vcc, v0, v1, vcc
	v_cmp_ne_u32_e32 vcc, 0, v8
	s_nop 1
	s_nop 0
	v_cndmask_b32_e64 v1, 0, 1, vcc
	v_cmp_ne_u32_e32 vcc, 0, v9
	s_nop 1
	v_addc_co_u32_e32 v0, vcc, v0, v1, vcc
	v_cmp_ne_u32_e32 vcc, 0, v10
	s_nop 1
	s_nop 0
	v_cndmask_b32_e64 v1, 0, 1, vcc
	v_cmp_ne_u32_e32 vcc, 0, v11
	s_nop 1
	v_addc_co_u32_e32 v0, vcc, v0, v1, vcc
	v_cmp_ne_u32_e32 vcc, 0, v12
	s_nop 1
	s_nop 0
	v_cndmask_b32_e64 v1, 0, 1, vcc
	v_cmp_ne_u32_e32 vcc, 0, v13
	s_nop 1
	v_addc_co_u32_e32 v0, vcc, v0, v1, vcc
	v_cmp_ne_u32_e32 vcc, 0, v14
	s_nop 1
	s_nop 0
	v_cndmask_b32_e64 v1, 0, 1, vcc
	v_cmp_ne_u32_e32 vcc, 0, v15
	s_nop 1
	v_addc_co_u32_e32 v0, vcc, v0, v1, vcc
	v_max_u32_e32 v0, 1, v0
	v_mov_b32_e64 v1, s0
	ds_write_b32 v1, v2
	ds_write_b32 v1, v0 offset:4
.LBB0_1559:
	s_lshl_b32 s20, s38, 6
	s_nop 0
	s_add_i32 s96, s20, 0x500
	s_lshl_b64 s[0:1], s[96:97], 2
	s_add_u32 s0, s34, s0
	s_addc_u32 s1, s35, s1
	v_mov_b64_e32 v[4:5], s[0:1]
	v_mov_b32_e64 v1, 1
	flat_atomic_add v3, v[4:5], v1 sc0
	v_cvt_f32_u32_e32 v1, v2
	v_sub_u32_e32 v4, 0, v2
	v_rcp_iflag_f32_e32 v1, v1
	s_nop 0
	v_mul_f32_e32 v1, 0x4f7ffffe, v1
	v_cvt_u32_f32_e32 v1, v1
	s_nop 0
	v_mul_lo_u32 v4, v4, v1
	v_mul_hi_u32 v4, v1, v4
	v_add_u32_e32 v1, v1, v4
	s_waitcnt vmcnt(0) lgkmcnt(0)
	v_mul_hi_u32 v1, v3, v1
	v_mul_lo_u32 v4, v1, v2
	v_sub_u32_e32 v4, v3, v4
	v_cmp_ge_u32_e32 vcc, v4, v2
	v_add_u32_e32 v5, 1, v1
	s_nop 0
	v_cndmask_b32_e32 v1, v1, v5, vcc
	v_sub_u32_e32 v5, v4, v2
	v_cndmask_b32_e32 v4, v4, v5, vcc
	v_cmp_ge_u32_e32 vcc, v4, v2
	v_add_u32_e32 v4, 1, v1
	s_nop 0
	v_cndmask_b32_e32 v1, v1, v4, vcc
	v_add_u32_e32 v4, 1, v3
	v_mad_u64_u32 v[2:3], s[0:1], v2, v1, v[2:3]
	v_cmp_ne_u32_e32 vcc, v4, v2
	s_and_saveexec_b64 s[0:1], vcc
	s_xor_b64 s[0:1], exec, s[0:1]
	s_cbranch_execz .LBB0_1594
	s_add_i32 s96, s20, 0x900
	s_lshl_b64 s[2:3], s[96:97], 2
	s_add_u32 s4, s34, s2
	s_addc_u32 s5, s35, s3
	v_mov_b64_e32 v[2:3], s[4:5]
	flat_load_dword v0, v[2:3] sc1
	s_waitcnt vmcnt(0) lgkmcnt(0)
	v_cmp_eq_u32_e32 vcc, v0, v1
	s_and_saveexec_b64 s[2:3], vcc
	s_cbranch_execz .LBB0_1593
	s_mov_b32 s21, 1
	s_mov_b64 s[6:7], 0
	s_branch .LBB0_1563

.LBB0_1569:
	s_andn2_b64 vcc, exec, s[16:17]
	s_cbranch_vccz .LBB0_1571
	v_mov_b32_e64 v0, 1
	global_store_dword v97, v0, s[8:9] sc1
.LBB0_1571:
	v_cmp_gt_i32_e32 vcc, s58, v227
	s_waitcnt lgkmcnt(0)
	s_mov_b64 s[0:1], -1
	s_mov_b64 s[8:9], -1
	s_and_saveexec_b64 s[14:15], vcc
	s_cbranch_execz .LBB0_1573
	v_lshlrev_b32_e32 v0, 8, v227
	s_nop 0
	global_load_dword v0, v0, s[4:5] sc1
	s_waitcnt vmcnt(0)
	v_cmp_le_u32_e32 vcc, s69, v0
	s_orn2_b64 s[8:9], vcc, exec
.LBB0_1573:
	s_or_b64 exec, exec, s[14:15]
	v_add_u32_e64 v0, 64, v227
	v_cmp_gt_i32_e32 vcc, s58, v0
	s_and_saveexec_b64 s[14:15], vcc
	s_cbranch_execz .LBB0_1575
	v_lshlrev_b32_e32 v0, 8, v0
	global_load_dword v0, v0, s[4:5] sc1
	s_waitcnt vmcnt(0)
	v_cmp_le_u32_e32 vcc, s69, v0
	s_orn2_b64 s[0:1], vcc, exec

.LBB0_1579:
	s_or_b64 exec, exec, s[18:19]
	v_or_b32_e32 v0, 0x100, v227
	v_cmp_gt_i32_e32 vcc, s58, v0
	s_mov_b64 s[18:19], -1
	s_and_saveexec_b64 s[20:21], vcc
	s_cbranch_execz .LBB0_1581
	v_lshlrev_b32_e32 v0, 8, v0
	s_nop 0
	global_load_dword v0, v0, s[4:5] sc1
	s_waitcnt vmcnt(0)
	v_cmp_le_u32_e32 vcc, s69, v0
	s_orn2_b64 s[18:19], vcc, exec
.LBB0_1581:
	s_or_b64 exec, exec, s[20:21]
	s_and_b64 s[0:1], s[8:9], s[0:1]
	s_and_b64 s[0:1], s[0:1], s[16:17]
	s_and_b64 s[0:1], s[0:1], s[14:15]
	s_and_b64 s[0:1], s[0:1], s[18:19]
	s_xor_b64 s[0:1], s[0:1], -1
	s_waitcnt vmcnt(0)
	buffer_inv sc1
	s_waitcnt vmcnt(0)
	s_nop 0
	v_cndmask_b32_e64 v0, 0, 1, s[0:1]
	v_cmp_ne_u32_e32 vcc, 0, v0
	s_cbranch_vccnz .LBB0_1583
	v_mov_b32_e32 v0, s51
	v_mov_b32_e32 v1, 1
	ds_write_b32 v0, v1
.LBB0_1583:
	v_ashrrev_i32_e32 v1, 31, v8
	v_lshrrev_b32_e32 v1, 26, v1
	v_add_u32_e32 v1, v8, v1
	v_ashrrev_i32_e32 v9, 6, v1
	v_bfe_i32 v1, v8, 27, 1
	v_lshlrev_b32_e32 v0, 4, v8
	v_lshrrev_b32_e32 v1, 22, v1
	v_add_u32_e64 v1, v0, v1
	v_and_b32_e32 v1, 0xfffffc00, v1
	v_sub_u32_e32 v0, v0, v1
	v_lshrrev_b32_e32 v1, 4, v0
	v_bitop3_b32 v0, v1, v0, 32 bitop3:0x6c
	v_ashrrev_i32_e32 v2, 31, v0
	v_lshrrev_b32_e32 v2, 26, v2
	v_add_u32_e32 v2, v0, v2
	v_ashrrev_i32_e32 v10, 6, v2
	v_and_b32_e32 v2, 0xc0, v2
	v_sub_u32_e32 v0, v0, v2
	v_mov_b32_e32 v2, 1
	v_lshlrev_b32_e32 v1, 3, v9
	v_lshlrev_b32_e32 v3, 5, v9
	v_ashrrev_i16_sdwa v0, v2, sext(v0) dst_sel:DWORD dst_unused:UNUSED_PAD src0_sel:DWORD src1_sel:BYTE_0
	v_and_b32_e32 v1, -16, v1
	v_and_b32_e32 v3, 32, v3
	v_bfe_i32 v11, v0, 0, 16
	v_add_u32_e64 v1, v10, v1
	v_add_lshl_u32 v0, v3, v11, 1
	s_lshl_b32 s27, s11, 18
	s_nop 0
	v_lshl_add_u32 v2, v1, 10, s27
	v_add_u32_e32 v3, 0x10000, v0
	v_add_u32_e32 v64, v2, v0
	v_add_u32_e32 v66, v3, v2
	v_add_u32_e32 v2, 0x20000, v2
	v_and_b32_e32 v4, 3, v10
	s_nop 0
	s_mov_b32 s0, 0x7fffe0
	v_add_u32_e32 v68, v2, v0
	v_add_u32_e32 v70, v3, v2
	v_lshlrev_b32_e32 v2, 1, v1
	v_lshrrev_b32_e32 v3, 2, v1
	v_and_or_b32 v1, v1, s0, v4
	s_mul_hi_i32 s0, s12, 0x2aaaaaab
	s_lshr_b32 s1, s0, 31
	s_add_i32 s0, s0, s1
	s_ashr_i32 s19, s13, 6
	s_mul_i32 s1, s0, 6
	s_ashr_i32 s20, s13, 8
	s_lshl_b32 s14, s19, 10
	s_sub_i32 s22, s12, s1
	s_cmp_lt_u32 s22, 5
	s_cselect_b32 s1, 1, 2
	s_cmp_gt_i32 s22, 2
	s_cselect_b32 s1, s1, 0
	s_lshl_b32 s24, s0, 2
	s_or_b32 s0, s1, s24
	s_ashr_i32 s1, s0, 31
	s_ashr_i32 s11, s10, 31
	s_ashr_i32 s7, s6, 31
	s_lshl_b64 s[8:9], s[0:1], 19
	s_lshl_b64 s[4:5], s[10:11], 17
	s_lshl_b64 s[0:1], s[6:7], 9
	s_add_u32 s7, s59, s8
	s_addc_u32 s8, s60, s9
	s_add_u32 s7, s7, s4
	s_addc_u32 s9, s8, s5
	v_and_b32_e32 v2, 24, v2
	v_and_b32_e32 v3, 4, v3
	s_add_u32 s8, s7, s0
	v_or3_b32 v1, v1, v3, v2
	s_addc_u32 s9, s9, s1
	s_add_i32 s7, s14, 0
	v_lshl_add_u32 v96, v1, 9, v0
	s_barrier
	s_nop 0
	s_add_i32 m0, s7, 0x10000
	v_add_u32_e32 v72, 0x8000, v96
	global_load_lds_dwordx4 v96, s[8:9]
	s_add_i32 m0, s7, 0x12000
	s_add_u32 s16, s8, 0x10000
	s_addc_u32 s17, s9, 0
	s_nop 0
	s_add_i32 s11, s7, 0x14000
	global_load_lds_dwordx4 v72, s[8:9]
	s_mov_b32 m0, s11
	s_nop 0
	s_add_i32 s15, s7, 0x16000
	global_load_lds_dwordx4 v96, s[16:17]
	s_mov_b32 m0, s15
	s_nop 0
	s_add_i32 s18, s7, 0x6000
	global_load_lds_dwordx4 v72, s[16:17]
	s_mov_b32 m0, s7
	s_nop 0
	s_add_i32 s16, s7, 0x2000
	global_load_lds_dwordx4 v64, s[34:35]
	s_mov_b32 m0, s16
	s_nop 0
	s_add_i32 s17, s7, 0x4000
	global_load_lds_dwordx4 v66, s[34:35]
	s_mov_b32 m0, s17
	v_mov_b32_e32 v73, v97
	global_load_lds_dwordx4 v68, s[34:35]
	s_mov_b32 m0, s18
	v_mov_b32_e32 v65, v97
	global_load_lds_dwordx4 v70, s[34:35]
	v_mov_b32_e64 v67, v97
	v_lshl_add_u64 v[6:7], s[8:9], 0, v[96:97]
	v_lshl_add_u64 v[4:5], s[8:9], 0, v[72:73]
	v_lshl_add_u64 v[2:3], s[34:35], 0, v[64:65]
	s_cmp_lg_u32 s20, 1
	s_nop 0
	v_lshl_add_u64 v[0:1], s[34:35], 0, v[66:67]
	s_cbranch_scc1 .LBB0_1585
	s_barrier
.LBB0_1585:
	v_and_b32_e32 v12, 15, v8
	v_lshrrev_b32_e32 v13, 4, v8
	s_lshl_b32 s19, s19, 5
	s_nop 0
	v_lshl_or_b32 v86, s20, 6, v12
	v_bfe_u32 v13, v13, 1, 1
	s_lshl_b32 s20, s20, 13
	s_nop 0
	s_and_b32 s19, s19, 0x60
	s_mov_b64 s[28:29], 0x80
	v_lshl_or_b32 v16, v13, 10, s20
	s_lshr_b32 s20, s19, 3
	s_nop 0
	s_add_i32 m0, s7, 0x18000
	v_lshl_add_u64 v[6:7], v[6:7], 0, s[28:29]
	v_or_b32_e32 v13, s20, v13
	s_waitcnt vmcnt(2)
	s_barrier
	s_nop 0
	global_load_lds_dwordx4 v[6:7], off
	v_lshl_add_u64 v[4:5], v[4:5], 0, s[28:29]
	s_add_i32 m0, s7, 0x1a000
	s_add_i32 s20, s7, 0x8000
	s_add_i32 s21, s7, 0xa000
	global_load_lds_dwordx4 v[4:5], off
	v_lshl_add_u64 v[2:3], v[2:3], 0, s[28:29]
	s_mov_b32 m0, s20
	s_nop 0
	v_lshl_add_u64 v[0:1], v[0:1], 0, s[28:29]
	s_add_u32 s28, s8, 0x10080
	global_load_lds_dwordx4 v[2:3], off
	s_mov_b32 m0, s21
	s_addc_u32 s29, s9, 0
	s_add_i32 s8, s7, 0x1c000
	global_load_lds_dwordx4 v[0:1], off
	v_lshl_add_u64 v[0:1], s[28:29], 0, v[96:97]
	s_mov_b32 m0, s8
	s_nop 0
	s_add_i32 s9, s7, 0x1e000
	global_load_lds_dwordx4 v[0:1], off
	v_lshl_add_u64 v[0:1], s[28:29], 0, v[72:73]
	s_mov_b32 m0, s9
	s_cmp_lt_u32 s22, 5
	global_load_lds_dwordx4 v[0:1], off
	s_cselect_b32 s23, 1, 2
	s_min_u32 s26, s22, 4
	s_add_i32 s25, s22, 1
	s_add_i32 s26, s26, -1
	s_cmp_lt_i32 s22, 3
	s_cselect_b32 s23, 0, s23
	s_cselect_b32 s25, s25, s26
	s_or_b32 s23, s23, s24
	s_add_i32 s24, s25, s24
	s_add_u32 s4, s59, s4
	s_addc_u32 s5, s60, s5
	s_add_u32 s25, s4, s0
	s_addc_u32 s26, s5, s1
	s_nop 0
	s_add_u32 s0, s70, 0x2ee00080
	v_lshlrev_b32_e32 v0, 13, v9
	s_addc_u32 s1, s71, 0
	s_add_i32 s4, s27, 0x30000
	v_and_b32_e32 v2, 0xffffc000, v0
	v_lshlrev_b32_e32 v3, 10, v10
	v_and_b32_e32 v1, 1, v9
	v_lshlrev_b32_e32 v14, 1, v8
	s_nop 0
	v_add3_u32 v0, s4, v2, v3
	v_lshlrev_b32_e32 v4, 6, v1
	v_lshlrev_b32_e32 v5, 1, v11
	v_bfe_u32 v79, v8, 4, 2
	v_and_b32_e32 v14, 32, v14
	v_lshlrev_b32_e32 v12, 6, v12
	v_lshlrev_b32_e32 v8, 2, v8
	s_nop 0
	v_add3_u32 v0, v0, v4, v5
	v_mov_b32_e64 v1, v97
	s_add_i32 s27, s27, 0x20000
	v_or_b32_e32 v15, v12, v14
	v_and_b32_e32 v8, 32, v8
	v_lshlrev_b32_e32 v13, 10, v13
	s_nop 0
	v_lshl_add_u64 v[74:75], s[0:1], 0, v[0:1]
	v_add3_u32 v0, s27, v2, v3
	v_bitop3_b32 v12, v12, v8, v14 bitop3:0x36
	v_bitop3_b32 v80, v13, v15, v8 bitop3:0xf6
	v_or_b32_e32 v14, 16, v15
	s_nop 0
	v_bitop3_b32 v15, v15, v8, 16 bitop3:0x36
	s_waitcnt vmcnt(6)
	s_nop 0
	v_add3_u32 v0, v0, v4, v5
	v_or_b32_e32 v12, v12, v16
	v_or_b32_e32 v15, v15, v16
	v_lshl_add_u64 v[76:77], s[0:1], 0, v[0:1]
	v_mov_b32_e32 v0, 0
	v_mov_b32_e32 v69, v97
	v_mov_b32_e64 v71, v97
	v_bitop3_b32 v81, v14, v13, v8 bitop3:0xde
	s_mov_b32 s22, 0
	s_mov_b64 s[0:1], 0
	v_add_u32_e32 v82, 0, v12
	v_add_u32_e32 v83, 0, v15
	v_mbcnt_lo_u32_b32 v84, -1, 0
	v_mbcnt_hi_u32_b32 v84, -1, v84
	v_and_b32_e32 v84, 16, v84
	v_xor_b32_e32 v82, v82, v84
	v_xor_b32_e32 v83, v83, v84
	v_xor_b32_e32 v80, v80, v84
	v_xor_b32_e32 v81, v81, v84
	v_mov_b32_e32 v1, v0
	v_mov_b32_e32 v2, v0
	v_mov_b32_e32 v3, v0
	v_mov_b32_e32 v4, v0
	v_mov_b32_e32 v5, v0
	v_mov_b32_e32 v6, v0
	v_mov_b32_e32 v7, v0
	v_mov_b32_e32 v8, v0
	v_mov_b32_e32 v9, v0
	v_mov_b32_e32 v10, v0
	v_mov_b32_e32 v11, v0
	v_mov_b32_e32 v12, v0
	v_mov_b32_e32 v13, v0
	v_mov_b32_e32 v14, v0
	v_mov_b32_e32 v15, v0
	v_mov_b32_e32 v16, v0
	v_mov_b32_e32 v17, v0
	v_mov_b32_e32 v18, v0
	v_mov_b32_e32 v19, v0
	v_mov_b32_e32 v20, v0
	v_mov_b32_e32 v21, v0
	v_mov_b32_e32 v22, v0
	v_mov_b32_e32 v23, v0
	v_mov_b32_e32 v24, v0
	v_mov_b32_e32 v25, v0
	v_mov_b32_e32 v26, v0
	v_mov_b32_e32 v27, v0
	v_mov_b32_e32 v28, v0
	v_mov_b32_e32 v29, v0
	v_mov_b32_e32 v30, v0
	v_mov_b32_e32 v31, v0
	v_mov_b32_e32 v32, v0
	v_mov_b32_e32 v33, v0
	v_mov_b32_e32 v34, v0
	v_mov_b32_e32 v35, v0
	v_mov_b32_e32 v36, v0
	v_mov_b32_e32 v37, v0
	v_mov_b32_e32 v38, v0
	v_mov_b32_e32 v39, v0
	v_mov_b32_e32 v40, v0
	v_mov_b32_e32 v41, v0
	v_mov_b32_e32 v42, v0
	v_mov_b32_e32 v43, v0
	v_mov_b32_e32 v44, v0
	v_mov_b32_e32 v45, v0
	v_mov_b32_e32 v46, v0
	v_mov_b32_e32 v47, v0
	v_mov_b32_e32 v48, v0
	v_mov_b32_e32 v49, v0
	v_mov_b32_e32 v50, v0
	v_mov_b32_e32 v51, v0
	v_mov_b32_e32 v52, v0
	v_mov_b32_e32 v53, v0
	v_mov_b32_e32 v54, v0
	v_mov_b32_e32 v55, v0
	v_mov_b32_e32 v56, v0
	v_mov_b32_e32 v57, v0
	v_mov_b32_e32 v58, v0
	v_mov_b32_e32 v59, v0
	v_mov_b32_e32 v60, v0
	v_mov_b32_e32 v61, v0
	v_mov_b32_e64 v62, v0
	v_mov_b32_e32 v63, v0
	s_barrier

.LBB0_1589:
	s_lshl_b32 s0, s12, 2
	s_add_i32 s0, s0, 0
	s_nop 0
	s_add_i32 s0, s0, 0x20240
	v_mov_b32_e64 v64, s0
	ds_read_b32 v73, v64
	s_ashr_i32 s13, s12, 31
	v_add_u32_e32 v91, v78, v86
	s_lshl_b64 s[0:1], s[12:13], 18
	s_add_u32 s0, s90, s0
	s_waitcnt lgkmcnt(0)
	v_add_u32_e32 v92, -1, v73
	v_min_i32_e32 v64, v91, v92
	s_addc_u32 s1, s91, s1
	v_ashrrev_i32_e32 v65, 31, v64
	s_nop 0
	v_lshl_add_u64 v[64:65], v[64:65], 2, s[0:1]
	global_load_dword v67, v[64:65], off
	v_or_b32_e32 v64, 32, v91
	v_min_i32_e32 v64, v64, v92
	v_ashrrev_i32_e32 v65, 31, v64
	s_nop 0
	v_lshl_add_u64 v[64:65], v[64:65], 2, s[0:1]
	global_load_dword v89, v[64:65], off
	v_or_b32_e32 v64, 48, v91
	v_min_i32_e32 v64, v64, v92
	v_ashrrev_i32_e32 v65, 31, v64
	s_nop 0
	v_lshl_add_u64 v[64:65], v[64:65], 2, s[0:1]
	global_load_dword v88, v[64:65], off
	v_add_u32_e32 v64, 0x80, v91
	v_min_i32_e32 v64, v64, v92
	v_ashrrev_i32_e32 v65, 31, v64
	v_lshl_add_u64 v[64:65], v[64:65], 2, s[0:1]
	global_load_dword v84, v[64:65], off
	v_add_u32_e32 v64, 0x90, v91
	v_min_i32_e32 v64, v64, v92
	v_ashrrev_i32_e32 v65, 31, v64
	v_lshl_add_u64 v[64:65], v[64:65], 2, s[0:1]
	global_load_dword v83, v[64:65], off
	v_add_u32_e32 v64, 0xa0, v91
	v_min_i32_e32 v64, v64, v92
	v_ashrrev_i32_e32 v65, 31, v64
	v_lshl_add_u64 v[64:65], v[64:65], 2, s[0:1]
	global_load_dword v80, v[64:65], off
	v_add_u32_e32 v64, 0xb0, v91
	v_min_i32_e32 v64, v64, v92
	s_lshl_b32 s4, s10, 8
	v_lshl_or_b32 v66, v79, 3, s19
	v_ashrrev_i32_e32 v65, 31, v64
	s_add_i32 s4, s4, s6
	v_lshl_add_u64 v[64:65], v[64:65], 2, s[0:1]
	v_add_u32_e64 v77, s4, v66
	global_load_dword v76, v[64:65], off
	v_lshlrev_b32_e32 v64, 1, v77
	v_or_b32_e32 v93, 16, v91
	v_add_u32_e32 v74, 0x2000000, v64
	v_add_u32_e32 v79, 0x37a00000, v64
	v_min_i32_e32 v92, v93, v92
	v_ashrrev_i32_e32 v93, 31, v92
	v_lshl_add_u64 v[92:93], v[92:93], 2, s[0:1]
	v_or_b32_e32 v90, 16, v86
	v_or_b32_e32 v87, 32, v86
	v_or_b32_e32 v85, 48, v86
	s_nop 0
	v_add_u32_e32 v82, 0x80, v86
	v_add_u32_e32 v81, 0x90, v86
	v_add_u32_e32 v75, 0xa0, v86
	v_add_u32_e32 v72, 0xb0, v86
	v_cmp_lt_i32_e32 vcc, v91, v73
	s_nop 0
	v_lshl_add_u32 v86, v86, 11, v74
	s_waitcnt vmcnt(0)
	v_ashrrev_i32_e32 v64, 12, v67
	v_mul_i32_i24_e32 v64, 0x1800, v64
	v_lshl_add_u32 v96, v67, 11, v79
	v_add_lshl_u32 v64, v64, v77, 1
	global_load_dwordx4 v[68:71], v96, s[70:71]
	s_nop 0
	s_nop 0
	global_load_dwordx4 v[64:67], v64, s[2:3]
	v_cndmask_b32_e32 v96, v86, v96, vcc
	s_nop 0
	global_load_dword v92, v[92:93], off
	v_lshl_add_u64 v[102:103], s[70:71], 0, v[96:97]
	s_waitcnt vmcnt(2)
	v_lshlrev_b32_e32 v104, 16, v68
	v_and_b32_e32 v105, 0xffff0000, v68
	v_lshlrev_b32_e32 v68, 16, v69
	s_waitcnt vmcnt(0)
	v_lshl_add_u32 v112, v92, 11, v79
	v_ashrrev_i32_e32 v92, 12, v92
	s_nop 0
	v_mul_i32_i24_e32 v92, 0x1800, v92
	v_add_lshl_u32 v98, v92, v77, 1
	global_load_dwordx4 v[92:95], v112, s[70:71]
	s_nop 0
	s_nop 0
	global_load_dwordx4 v[98:101], v98, s[2:3]
	v_and_b32_e32 v69, 0xffff0000, v69
	v_lshlrev_b32_e32 v106, 16, v70
	s_nop 0
	v_and_b32_e32 v107, 0xffff0000, v70
	v_lshlrev_b32_e32 v70, 16, v71
	s_nop 0
	v_and_b32_e32 v71, 0xffff0000, v71
	v_lshlrev_b32_e32 v108, 16, v64
	s_nop 0
	v_and_b32_e32 v109, 0xffff0000, v64
	v_lshlrev_b32_e32 v64, 16, v65
	s_nop 0
	v_and_b32_e32 v65, 0xffff0000, v65
	v_lshlrev_b32_e32 v110, 16, v66
	s_nop 0
	v_and_b32_e32 v111, 0xffff0000, v66
	v_lshlrev_b32_e32 v66, 16, v67
	s_nop 0
	v_and_b32_e32 v67, 0xffff0000, v67
	v_pk_fma_f32 v[62:63], v[62:63], v[64:65], v[68:69]
	v_pk_fma_f32 v[60:61], v[60:61], v[108:109], v[104:105]
	v_pk_fma_f32 v[64:65], v[58:59], v[66:67], v[70:71]
	v_pk_fma_f32 v[58:59], v[56:57], v[110:111], v[106:107]
	v_cvt_pk_bf16_f32 v56, v60, v61
	v_cvt_pk_bf16_f32 v57, v62, v63
	s_waitcnt vmcnt(1)
	v_lshlrev_b32_e32 v60, 16, v94
	v_cvt_pk_bf16_f32 v58, v58, v59
	v_cvt_pk_bf16_f32 v59, v64, v65
	global_store_dwordx4 v[102:103], v[56:59], off
	v_and_b32_e32 v61, 0xffff0000, v94
	v_lshlrev_b32_e32 v62, 16, v95
	v_add_u32_e32 v56, v78, v90
	v_cmp_lt_i32_e32 vcc, v56, v73
	s_nop 0
	v_lshl_add_u32 v56, v90, 11, v74
	v_and_b32_e32 v57, 0xffff0000, v92
	v_cndmask_b32_e32 v86, v56, v112, vcc
	v_lshlrev_b32_e32 v56, 16, v92
	v_and_b32_e32 v63, 0xffff0000, v95
	s_waitcnt vmcnt(1)
	v_lshlrev_b32_e32 v64, 16, v98
	v_and_b32_e32 v65, 0xffff0000, v98
	v_lshlrev_b32_e32 v68, 16, v100
	s_nop 0
	v_and_b32_e32 v69, 0xffff0000, v100
	v_lshlrev_b32_e32 v70, 16, v101
	s_nop 0
	v_and_b32_e32 v71, 0xffff0000, v101
	v_lshlrev_b32_e32 v58, 16, v93
	s_nop 0
	v_and_b32_e32 v59, 0xffff0000, v93
	v_lshlrev_b32_e32 v66, 16, v99
	s_nop 0
	v_and_b32_e32 v67, 0xffff0000, v99
	v_pk_fma_f32 v[52:53], v[52:53], v[64:65], v[56:57]
	v_pk_fma_f32 v[56:57], v[50:51], v[70:71], v[62:63]
	v_pk_fma_f32 v[50:51], v[48:49], v[68:69], v[60:61]
	v_cvt_pk_bf16_f32 v48, v52, v53
	v_pk_fma_f32 v[54:55], v[54:55], v[66:67], v[58:59]
	v_lshl_add_u32 v64, v89, 11, v79
	v_cvt_pk_bf16_f32 v49, v54, v55
	v_cvt_pk_bf16_f32 v50, v50, v51
	v_cvt_pk_bf16_f32 v51, v56, v57
	global_store_dwordx4 v86, v[48:51], s[70:71]
	v_ashrrev_i32_e32 v56, 12, v88
	s_nop 0
	v_mul_i32_i24_e32 v56, 0x1800, v56
	v_ashrrev_i32_e32 v48, 12, v89
	s_nop 0
	v_mul_i32_i24_e32 v48, 0x1800, v48
	v_add_lshl_u32 v52, v48, v77, 1
	global_load_dwordx4 v[48:51], v64, s[70:71]
	s_nop 0
	s_nop 0
	global_load_dwordx4 v[52:55], v52, s[2:3]
	v_lshl_add_u32 v89, v88, 11, v79
	v_add_lshl_u32 v60, v56, v77, 1
	global_load_dwordx4 v[56:59], v89, s[70:71]
	s_nop 0
	s_nop 0
	global_load_dwordx4 v[60:63], v60, s[2:3]
	v_add_u32_e32 v65, v78, v87
	v_cmp_lt_i32_e32 vcc, v65, v73
	v_lshl_add_u32 v65, v87, 11, v74
	s_waitcnt vmcnt(3)
	v_lshlrev_b32_e32 v66, 16, v48
	v_cndmask_b32_e32 v96, v65, v64, vcc
	s_nop 0
	v_and_b32_e32 v67, 0xffff0000, v48
	v_lshlrev_b32_e32 v48, 16, v49
	s_nop 0
	v_and_b32_e32 v49, 0xffff0000, v49
	v_lshlrev_b32_e32 v68, 16, v50
	s_nop 0
	v_and_b32_e32 v69, 0xffff0000, v50
	v_lshlrev_b32_e32 v50, 16, v51
	s_nop 0
	v_and_b32_e32 v51, 0xffff0000, v51
	s_waitcnt vmcnt(2)
	v_lshlrev_b32_e32 v70, 16, v52
	v_and_b32_e32 v71, 0xffff0000, v52
	v_lshlrev_b32_e32 v52, 16, v53
	s_nop 0
	v_and_b32_e32 v53, 0xffff0000, v53
	v_lshlrev_b32_e32 v86, 16, v54
	s_nop 0
	v_and_b32_e32 v87, 0xffff0000, v54
	v_lshlrev_b32_e32 v54, 16, v55
	s_nop 0
	v_and_b32_e32 v55, 0xffff0000, v55
	v_lshl_add_u64 v[64:65], s[70:71], 0, v[96:97]
	v_pk_fma_f32 v[46:47], v[46:47], v[52:53], v[48:49]
	v_pk_fma_f32 v[44:45], v[44:45], v[70:71], v[66:67]
	v_pk_fma_f32 v[48:49], v[42:43], v[54:55], v[50:51]
	v_pk_fma_f32 v[42:43], v[40:41], v[86:87], v[68:69]
	v_cvt_pk_bf16_f32 v40, v44, v45
	v_cvt_pk_bf16_f32 v41, v46, v47
	s_waitcnt vmcnt(1)
	v_lshlrev_b32_e32 v44, 16, v58
	v_cvt_pk_bf16_f32 v42, v42, v43
	v_cvt_pk_bf16_f32 v43, v48, v49
	global_store_dwordx4 v[64:65], v[40:43], off
	v_and_b32_e32 v45, 0xffff0000, v58
	v_lshlrev_b32_e32 v46, 16, v59
	v_add_u32_e32 v40, v78, v85
	v_cmp_lt_i32_e32 vcc, v40, v73
	s_nop 0
	v_lshl_add_u32 v40, v85, 11, v74
	v_and_b32_e32 v41, 0xffff0000, v56
	v_cndmask_b32_e32 v64, v40, v89, vcc
	v_lshlrev_b32_e32 v40, 16, v56
	v_and_b32_e32 v47, 0xffff0000, v59
	s_waitcnt vmcnt(1)
	v_lshlrev_b32_e32 v48, 16, v60
	v_and_b32_e32 v49, 0xffff0000, v60
	v_lshlrev_b32_e32 v52, 16, v62
	s_nop 0
	v_and_b32_e32 v53, 0xffff0000, v62
	v_lshlrev_b32_e32 v54, 16, v63
	s_nop 0
	v_and_b32_e32 v55, 0xffff0000, v63
	v_lshlrev_b32_e32 v42, 16, v57
	s_nop 0
	v_and_b32_e32 v43, 0xffff0000, v57
	v_lshlrev_b32_e32 v50, 16, v61
	s_nop 0
	v_and_b32_e32 v51, 0xffff0000, v61
	v_pk_fma_f32 v[36:37], v[36:37], v[48:49], v[40:41]
	v_pk_fma_f32 v[40:41], v[34:35], v[54:55], v[46:47]
	v_pk_fma_f32 v[34:35], v[32:33], v[52:53], v[44:45]
	v_cvt_pk_bf16_f32 v32, v36, v37
	v_pk_fma_f32 v[38:39], v[38:39], v[50:51], v[42:43]
	v_lshl_add_u32 v48, v84, 11, v79
	v_cvt_pk_bf16_f32 v33, v38, v39
	v_cvt_pk_bf16_f32 v34, v34, v35
	v_cvt_pk_bf16_f32 v35, v40, v41
	global_store_dwordx4 v64, v[32:35], s[70:71]
	v_ashrrev_i32_e32 v40, 12, v83
	s_nop 0
	v_mul_i32_i24_e32 v40, 0x1800, v40
	v_ashrrev_i32_e32 v32, 12, v84
	s_nop 0
	v_mul_i32_i24_e32 v32, 0x1800, v32
	v_add_lshl_u32 v36, v32, v77, 1
	global_load_dwordx4 v[32:35], v48, s[70:71]
	s_nop 0
	s_nop 0
	global_load_dwordx4 v[36:39], v36, s[2:3]
	v_lshl_add_u32 v58, v83, 11, v79
	v_add_lshl_u32 v44, v40, v77, 1
	global_load_dwordx4 v[40:43], v58, s[70:71]
	s_nop 0
	s_nop 0
	global_load_dwordx4 v[44:47], v44, s[2:3]
	v_add_u32_e32 v49, v78, v82
	v_cmp_lt_i32_e32 vcc, v49, v73
	v_lshl_add_u32 v49, v82, 11, v74
	s_waitcnt vmcnt(3)
	v_lshlrev_b32_e32 v50, 16, v32
	v_cndmask_b32_e32 v96, v49, v48, vcc
	s_nop 0
	v_and_b32_e32 v51, 0xffff0000, v32
	v_lshlrev_b32_e32 v32, 16, v33
	s_nop 0
	v_and_b32_e32 v33, 0xffff0000, v33
	v_lshlrev_b32_e32 v52, 16, v34
	s_nop 0
	v_and_b32_e32 v53, 0xffff0000, v34
	v_lshlrev_b32_e32 v34, 16, v35
	s_nop 0
	v_and_b32_e32 v35, 0xffff0000, v35
	s_waitcnt vmcnt(2)
	v_lshlrev_b32_e32 v54, 16, v36
	v_and_b32_e32 v55, 0xffff0000, v36
	v_lshlrev_b32_e32 v36, 16, v37
	s_nop 0
	v_and_b32_e32 v37, 0xffff0000, v37
	v_lshlrev_b32_e32 v56, 16, v38
	s_nop 0
	v_and_b32_e32 v57, 0xffff0000, v38
	v_lshlrev_b32_e32 v38, 16, v39
	s_nop 0
	v_and_b32_e32 v39, 0xffff0000, v39
	v_lshl_add_u64 v[48:49], s[70:71], 0, v[96:97]
	v_pk_fma_f32 v[30:31], v[30:31], v[36:37], v[32:33]
	v_pk_fma_f32 v[28:29], v[28:29], v[54:55], v[50:51]
	v_pk_fma_f32 v[32:33], v[26:27], v[38:39], v[34:35]
	v_pk_fma_f32 v[26:27], v[24:25], v[56:57], v[52:53]
	v_cvt_pk_bf16_f32 v24, v28, v29
	v_cvt_pk_bf16_f32 v25, v30, v31
	s_waitcnt vmcnt(1)
	v_lshlrev_b32_e32 v28, 16, v42
	v_cvt_pk_bf16_f32 v26, v26, v27
	v_cvt_pk_bf16_f32 v27, v32, v33
	global_store_dwordx4 v[48:49], v[24:27], off
	v_and_b32_e32 v29, 0xffff0000, v42
	v_lshlrev_b32_e32 v30, 16, v43
	v_add_u32_e32 v24, v78, v81
	v_cmp_lt_i32_e32 vcc, v24, v73
	s_nop 0
	v_lshl_add_u32 v24, v81, 11, v74
	v_and_b32_e32 v25, 0xffff0000, v40
	v_cndmask_b32_e32 v48, v24, v58, vcc
	v_lshlrev_b32_e32 v24, 16, v40
	v_and_b32_e32 v31, 0xffff0000, v43
	s_waitcnt vmcnt(1)
	v_lshlrev_b32_e32 v32, 16, v44
	v_and_b32_e32 v33, 0xffff0000, v44
	v_lshlrev_b32_e32 v36, 16, v46
	s_nop 0
	v_and_b32_e32 v37, 0xffff0000, v46
	v_lshlrev_b32_e32 v38, 16, v47
	s_nop 0
	v_and_b32_e32 v39, 0xffff0000, v47
	v_lshlrev_b32_e32 v26, 16, v41
	s_nop 0
	v_and_b32_e32 v27, 0xffff0000, v41
	v_lshlrev_b32_e32 v34, 16, v45
	s_nop 0
	v_and_b32_e32 v35, 0xffff0000, v45
	v_pk_fma_f32 v[20:21], v[20:21], v[32:33], v[24:25]
	v_pk_fma_f32 v[24:25], v[18:19], v[38:39], v[30:31]
	v_pk_fma_f32 v[18:19], v[16:17], v[36:37], v[28:29]
	v_cvt_pk_bf16_f32 v16, v20, v21
	v_pk_fma_f32 v[22:23], v[22:23], v[34:35], v[26:27]
	v_lshl_add_u32 v32, v80, 11, v79
	v_cvt_pk_bf16_f32 v17, v22, v23
	v_cvt_pk_bf16_f32 v18, v18, v19
	v_cvt_pk_bf16_f32 v19, v24, v25
	global_store_dwordx4 v48, v[16:19], s[70:71]
	v_lshl_add_u32 v42, v76, 11, v79
	v_add_u32_e32 v33, v78, v75
	v_ashrrev_i32_e32 v16, 12, v80
	v_mul_i32_i24_e32 v16, 0x1800, v16
	v_add_lshl_u32 v16, v16, v77, 1
	global_load_dwordx4 v[24:27], v32, s[70:71]
	global_load_dwordx4 v[28:31], v16, s[2:3]
	v_ashrrev_i32_e32 v16, 12, v76
	s_nop 0
	v_mul_i32_i24_e32 v16, 0x1800, v16
	v_add_lshl_u32 v20, v16, v77, 1
	global_load_dwordx4 v[16:19], v42, s[70:71]
	s_nop 0
	s_nop 0
	global_load_dwordx4 v[20:23], v20, s[2:3]
	v_cmp_lt_i32_e32 vcc, v33, v73
	s_nop 0
	v_lshl_add_u32 v33, v75, 11, v74
	s_waitcnt vmcnt(3)
	v_lshlrev_b32_e32 v34, 16, v24
	v_cndmask_b32_e32 v96, v33, v32, vcc
	s_nop 0
	v_and_b32_e32 v35, 0xffff0000, v24
	v_lshlrev_b32_e32 v24, 16, v25
	s_nop 0
	v_and_b32_e32 v25, 0xffff0000, v25
	v_lshlrev_b32_e32 v36, 16, v26
	s_nop 0
	v_and_b32_e32 v37, 0xffff0000, v26
	v_lshlrev_b32_e32 v26, 16, v27
	s_nop 0
	v_and_b32_e32 v27, 0xffff0000, v27
	s_waitcnt vmcnt(2)
	v_lshlrev_b32_e32 v38, 16, v28
	v_and_b32_e32 v39, 0xffff0000, v28
	v_lshlrev_b32_e32 v28, 16, v29
	s_nop 0
	v_and_b32_e32 v29, 0xffff0000, v29
	v_lshlrev_b32_e32 v40, 16, v30
	s_nop 0
	v_and_b32_e32 v41, 0xffff0000, v30
	v_lshlrev_b32_e32 v30, 16, v31
	s_nop 0
	v_and_b32_e32 v31, 0xffff0000, v31
	v_lshl_add_u64 v[32:33], s[70:71], 0, v[96:97]
	v_pk_fma_f32 v[14:15], v[14:15], v[28:29], v[24:25]
	v_pk_fma_f32 v[12:13], v[12:13], v[38:39], v[34:35]
	v_pk_fma_f32 v[24:25], v[10:11], v[30:31], v[26:27]
	v_pk_fma_f32 v[10:11], v[8:9], v[40:41], v[36:37]
	v_cvt_pk_bf16_f32 v8, v12, v13
	v_cvt_pk_bf16_f32 v9, v14, v15
	s_waitcnt vmcnt(1)
	v_lshlrev_b32_e32 v12, 16, v18
	v_cvt_pk_bf16_f32 v10, v10, v11
	v_cvt_pk_bf16_f32 v11, v24, v25
	global_store_dwordx4 v[32:33], v[8:11], off
	v_and_b32_e32 v13, 0xffff0000, v18
	v_lshlrev_b32_e32 v14, 16, v19
	v_add_u32_e32 v8, v78, v72
	v_cmp_lt_i32_e32 vcc, v8, v73
	s_nop 0
	v_lshl_add_u32 v8, v72, 11, v74
	v_and_b32_e32 v9, 0xffff0000, v16
	v_cndmask_b32_e32 v24, v8, v42, vcc
	v_lshlrev_b32_e32 v8, 16, v16
	v_lshlrev_b32_e32 v10, 16, v17
	s_nop 0
	v_and_b32_e32 v11, 0xffff0000, v17
	v_and_b32_e32 v15, 0xffff0000, v19
	s_waitcnt vmcnt(1)
	v_lshlrev_b32_e32 v16, 16, v20
	v_and_b32_e32 v17, 0xffff0000, v20
	v_lshlrev_b32_e32 v18, 16, v21
	s_nop 0
	v_and_b32_e32 v19, 0xffff0000, v21
	v_lshlrev_b32_e32 v20, 16, v22
	s_nop 0
	v_and_b32_e32 v21, 0xffff0000, v22
	v_lshlrev_b32_e32 v22, 16, v23
	s_nop 0
	v_and_b32_e32 v23, 0xffff0000, v23
	v_pk_fma_f32 v[4:5], v[4:5], v[16:17], v[8:9]
	v_pk_fma_f32 v[8:9], v[2:3], v[22:23], v[14:15]
	v_pk_fma_f32 v[2:3], v[0:1], v[20:21], v[12:13]
	v_pk_fma_f32 v[6:7], v[6:7], v[18:19], v[10:11]
	v_cvt_pk_bf16_f32 v0, v4, v5
	s_nop 0
	s_nop 0
	v_cvt_pk_bf16_f32 v1, v6, v7
	v_cvt_pk_bf16_f32 v2, v2, v3
	v_cvt_pk_bf16_f32 v3, v8, v9
	global_store_dwordx4 v24, v[0:3], s[70:71]
	s_waitcnt vmcnt(0)
	s_barrier
	s_cmp_ge_i32 s92, s37
	s_cbranch_scc0 .LBB0_1530
.LBB0_1590:
	v_readlane_b32 s4, v254, 22
	v_readlane_b32 s5, v254, 23
	s_nop 0
	s_getpc_b64 s[98:99]

.LBB0_1594:
	s_andn2_saveexec_b64 s[0:1], s[0:1]
	s_cbranch_execz .LBB0_1610
	v_mov_b32_e32 v1, s34
	v_add_co_u32_e32 v2, vcc, 0x3000, v1
	v_mov_b32_e64 v1, s35
	buffer_wbl2 sc1
	s_waitcnt vmcnt(0)
	v_addc_co_u32_e32 v3, vcc, 0, v1, vcc
	v_mov_b32_e64 v1, 1
	flat_atomic_add v1, v[2:3], v1 offset:1024 sc0
	v_cvt_f32_u32_e32 v2, v0
	v_sub_u32_e32 v3, 0, v0
	s_mov_b64 s[4:5], -1
	v_rcp_iflag_f32_e32 v2, v2
	s_nop 0
	s_nop 0
	v_mul_f32_e32 v2, 0x4f7ffffe, v2
	v_cvt_u32_f32_e32 v2, v2
	s_nop 0
	v_mul_lo_u32 v3, v3, v2
	v_mul_hi_u32 v3, v2, v3
	v_add_u32_e32 v2, v2, v3
	s_waitcnt vmcnt(0) lgkmcnt(0)
	v_mul_hi_u32 v2, v1, v2
	v_mul_lo_u32 v3, v2, v0
	v_sub_u32_e32 v3, v1, v3
	v_cmp_ge_u32_e32 vcc, v3, v0
	v_add_u32_e32 v4, 1, v2
	s_nop 0
	v_cndmask_b32_e32 v2, v2, v4, vcc
	v_sub_u32_e32 v4, v3, v0
	v_cndmask_b32_e32 v3, v3, v4, vcc
	v_cmp_ge_u32_e32 vcc, v3, v0
	v_add_u32_e32 v3, 1, v2
	s_nop 0
	v_cndmask_b32_e32 v2, v2, v3, vcc
	v_add_u32_e32 v3, 1, v1
	v_mad_u64_u32 v[0:1], s[0:1], v0, v2, v[0:1]
	s_add_u32 s0, s34, 0x3500
	s_addc_u32 s1, s35, 0
	v_cmp_ne_u32_e32 vcc, v3, v0
	v_mov_b64_e32 v[0:1], s[0:1]
	s_and_saveexec_b64 s[2:3], vcc
	s_cbranch_execz .LBB0_1607
	v_mov_b64_e32 v[0:1], s[0:1]
	flat_load_dword v0, v[0:1] sc1
	s_mov_b64 s[8:9], 0
	s_waitcnt vmcnt(0) lgkmcnt(0)
	v_cmp_eq_u32_e32 vcc, v0, v2
	s_and_saveexec_b64 s[6:7], vcc
	s_cbranch_execz .LBB0_1606
	s_nop 0
	s_add_u32 s4, s34, 0x200
	s_addc_u32 s5, s35, 0
	s_mov_b32 s21, 1
	s_branch .LBB0_1599

.LBB0_1609:
	s_or_b64 exec, exec, s[0:1]
	s_nop 0
	s_add_i32 s96, s20, 0x900
	s_lshl_b64 s[0:1], s[96:97], 2
	s_add_u32 s0, s34, s0
	s_addc_u32 s1, s35, s1
	v_mov_b64_e32 v[0:1], s[0:1]
	v_mov_b32_e32 v2, 1
	s_waitcnt vmcnt(0) lgkmcnt(0)
	buffer_inv sc1
	flat_atomic_add v[0:1], v2
	s_waitcnt vmcnt(0)
.LBB0_1610:
	s_or_b64 exec, exec, s[22:23]
	v_readlane_b32 s4, v254, 22
	v_readlane_b32 s5, v254, 23
	s_waitcnt lgkmcnt(0)
	s_barrier
	s_nop 0
	s_getpc_b64 s[98:99]

.LBB0_1636:
	s_cmp_le_i32 s36, s92
	s_cselect_b64 s[0:1], -1, 0
	s_cmp_lt_i32 s92, s37
	s_cselect_b64 s[2:3], -1, 0
	s_and_b64 s[0:1], s[0:1], s[2:3]
	s_and_b64 vcc, exec, s[0:1]
	s_nop 0
	v_readlane_b32 s9, v254, 2
	s_cbranch_vccz .LBB0_1644
	s_mov_b32 s0, 0
	s_waitcnt vmcnt(0)
	s_nop 0
	v_mbcnt_lo_u32_b32 v0, -1, s0
	v_mbcnt_hi_u32_b32 v0, -1, v0
	v_add_u32_e32 v0, s64, v0
	s_cmpk_gt_i32 s9, 0xff
	v_readfirstlane_b32 s0, v0
	s_cbranch_scc1 .LBB0_1644
	v_and_b32_e32 v2, 63, v0
	v_and_b32_e32 v0, 64, v227
	v_add_u32_e32 v0, 64, v0
	v_xor_b32_e32 v1, 1, v227
	v_cmp_lt_i32_e32 vcc, v1, v0
	s_ashr_i32 s4, s0, 1
	v_readlane_b32 s0, v254, 32
	v_cndmask_b32_e32 v1, v227, v1, vcc
	v_lshlrev_b32_e32 v58, 2, v1
	v_xor_b32_e32 v1, 2, v227
	v_cmp_lt_i32_e32 vcc, v1, v0
	v_readlane_b32 s1, v254, 33
	v_readlane_b32 s12, v253, 50
	v_cndmask_b32_e32 v1, v227, v1, vcc
	v_lshlrev_b32_e32 v59, 2, v1
	v_xor_b32_e32 v1, 4, v227
	v_cmp_lt_i32_e32 vcc, v1, v0
	v_readlane_b32 s24, v253, 62
	v_readlane_b32 s25, v253, 63
	v_cndmask_b32_e32 v1, v227, v1, vcc
	v_lshlrev_b32_e32 v60, 2, v1
	v_xor_b32_e32 v1, 8, v227
	v_cmp_lt_i32_e32 vcc, v1, v0
	s_andn2_b32 s4, s4, 31
	s_lshl_b32 s6, s61, 8
	v_cndmask_b32_e32 v1, v227, v1, vcc
	v_lshlrev_b32_e32 v61, 2, v1
	v_xor_b32_e32 v1, 16, v227
	v_cmp_lt_i32_e32 vcc, v1, v0
	v_mov_b32_e32 v64, 0x358637bd
	s_mov_b32 s7, 0xf800000
	v_cndmask_b32_e32 v1, v227, v1, vcc
	v_lshlrev_b32_e32 v62, 2, v1
	v_xor_b32_e32 v1, 32, v227
	v_cmp_lt_i32_e32 vcc, v1, v0
	v_mov_b32_e32 v65, 0x260
	v_readlane_b32 s13, v253, 51
	v_cndmask_b32_e32 v0, v227, v1, vcc
	v_mov_b32_e32 v1, 0
	v_lshlrev_b32_e32 v63, 2, v0
	v_lshlrev_b32_e32 v0, 4, v2
	v_lshlrev_b32_e32 v2, 3, v2
	v_mov_b32_e32 v3, v1
	v_lshl_add_u64 v[18:19], s[0:1], 0, v[2:3]
	v_readlane_b32 s0, v253, 2
	v_readlane_b32 s1, v253, 3
	v_readlane_b32 s0, v253, 0
	v_readlane_b32 s2, v253, 4
	v_readlane_b32 s3, v253, 5
	v_readlane_b32 s1, v253, 1
	v_lshl_add_u64 v[16:17], s[24:25], 0, v[0:1]
	v_lshl_add_u64 v[20:21], s[2:3], 0, v[0:1]
	v_lshl_add_u64 v[0:1], s[0:1], 0, v[0:1]
	s_mov_b64 s[0:1], 0x2a1000
	v_lshl_add_u64 v[22:23], v[0:1], 0, s[0:1]
	s_mov_b64 s[0:1], 0x2a0000
	v_lshl_add_u64 v[24:25], v[0:1], 0, s[0:1]
	s_lshl_b32 s0, s9, 8
	s_add_i32 s5, s0, s4
	v_readlane_b32 s14, v253, 52
	v_readlane_b32 s15, v253, 53
	v_readlane_b32 s16, v253, 54
	v_readlane_b32 s17, v253, 55
	v_readlane_b32 s18, v253, 56
	v_readlane_b32 s19, v253, 57
	v_readlane_b32 s20, v253, 58
	v_readlane_b32 s21, v253, 59
	v_readlane_b32 s22, v253, 60
	v_readlane_b32 s23, v253, 61
	v_readlane_b32 s26, v254, 0
	v_readlane_b32 s27, v254, 1
	s_branch .LBB0_1640

.LBB0_1640:
	s_ashr_i32 s0, s9, 4
	s_ashr_i32 s1, s0, 31
	s_lshl_b64 s[0:1], s[0:1], 13
	v_lshl_add_u64 v[26:27], v[22:23], 0, s[0:1]
	v_lshl_add_u64 v[48:49], v[24:25], 0, s[0:1]
	s_lshl_b32 s0, s9, 8
	s_add_i32 s0, s0, s4
	s_ashr_i32 s1, s0, 31
	s_lshl_b64 s[0:1], s[0:1], 11
	global_load_dwordx4 v[28:31], v[16:17], off
	global_load_dwordx4 v[32:35], v[16:17], off offset:1024
	global_load_dwordx4 v[36:39], v[26:27], off
	global_load_dwordx4 v[40:43], v[26:27], off offset:1024
	global_load_dwordx4 v[0:3], v[48:49], off
	global_load_dwordx4 v[4:7], v[48:49], off offset:1024
	global_load_dwordx4 v[44:47], v[26:27], off offset:2048
	global_load_dwordx4 v[66:69], v[16:17], off offset:2048
	global_load_dwordx4 v[70:73], v[16:17], off offset:3072
	global_load_dwordx4 v[74:77], v[26:27], off offset:3072
	global_load_dwordx4 v[8:11], v[48:49], off offset:2048
	global_load_dwordx4 v[12:15], v[48:49], off offset:3072
	v_lshl_add_u64 v[26:27], v[18:19], 0, s[0:1]
	global_load_dwordx2 v[56:57], v[26:27], off
	global_load_dwordx2 v[54:55], v[26:27], off offset:512
	global_load_dwordx2 v[52:53], v[26:27], off offset:1024
	global_load_dwordx2 v[50:51], v[26:27], off offset:1536
	s_mov_b32 s8, 0
	s_waitcnt vmcnt(13)
	v_pk_add_f32 v[26:27], v[38:39], 1.0 op_sel_hi:[1,0]
	v_pk_add_f32 v[36:37], v[36:37], 1.0 op_sel_hi:[1,0]
	s_waitcnt vmcnt(12)
	s_nop 0
	v_pk_add_f32 v[38:39], v[42:43], 1.0 op_sel_hi:[1,0]
	v_pk_add_f32 v[40:41], v[40:41], 1.0 op_sel_hi:[1,0]
	s_waitcnt vmcnt(9)
	s_nop 0
	v_pk_add_f32 v[42:43], v[46:47], 1.0 op_sel_hi:[1,0]
	v_pk_add_f32 v[44:45], v[44:45], 1.0 op_sel_hi:[1,0]
	v_pk_mul_f32 v[26:27], v[30:31], v[26:27]
	s_waitcnt vmcnt(6)
	s_nop 0
	v_pk_add_f32 v[46:47], v[76:77], 1.0 op_sel_hi:[1,0]
	v_pk_add_f32 v[48:49], v[74:75], 1.0 op_sel_hi:[1,0]
	v_pk_mul_f32 v[28:29], v[28:29], v[36:37]
	v_pk_mul_f32 v[30:31], v[34:35], v[38:39]
	v_pk_mul_f32 v[32:33], v[32:33], v[40:41]
	v_pk_mul_f32 v[34:35], v[68:69], v[42:43]
	v_pk_mul_f32 v[36:37], v[66:67], v[44:45]
	v_pk_mul_f32 v[38:39], v[72:73], v[46:47]
	v_pk_mul_f32 v[40:41], v[70:71], v[48:49]
	s_branch .LBB0_1642
.LBB0_1641:
	v_lshlrev_b32_e32 v67, 16, v57
	v_lshlrev_b32_e32 v66, 16, v56
	s_nop 0
	v_and_b32_e32 v57, 0xffff0000, v57
	v_and_b32_e32 v56, 0xffff0000, v56
	v_lshlrev_b32_e32 v71, 16, v55
	v_lshlrev_b32_e32 v70, 16, v54
	v_and_b32_e32 v55, 0xffff0000, v55
	v_and_b32_e32 v54, 0xffff0000, v54
	v_and_b32_e32 v75, 0xffff0000, v52
	v_lshlrev_b32_e32 v76, 16, v53
	s_nop 0
	v_pk_mul_f32 v[68:69], v[56:57], v[56:57]
	v_pk_mul_f32 v[72:73], v[54:55], v[54:55]
	v_lshlrev_b32_e32 v74, 16, v52
	s_nop 0
	v_and_b32_e32 v77, 0xffff0000, v53
	v_mul_f32_e64 v53, v75, v75
	v_mul_f32_e32 v52, v76, v76
	v_lshlrev_b32_e32 v78, 16, v50
	v_pk_fma_f32 v[68:69], v[66:67], v[66:67], v[68:69]
	v_pk_fma_f32 v[72:73], v[70:71], v[70:71], v[72:73]
	v_mul_f32_e64 v79, v74, v74
	v_pk_fma_f32 v[80:81], v[76:77], v[76:77], v[52:53] op_sel_hi:[1,1,0]
	v_mov_b32_e64 v52, v78
	v_pk_add_f32 v[68:69], v[68:69], v[68:69] op_sel_hi:[0,1]
	v_pk_add_f32 v[72:73], v[72:73], v[72:73] op_sel_hi:[0,1]
	v_and_b32_e32 v84, 0xffff0000, v50
	v_lshlrev_b32_e32 v82, 16, v51
	s_nop 0
	v_and_b32_e32 v83, 0xffff0000, v51
	v_pk_add_f32 v[52:53], v[78:79], v[52:53]
	v_mul_f32_e32 v80, v84, v84
	v_mul_f32_e32 v68, v82, v82
	v_mul_f32_e32 v72, v83, v83
	v_mul_f32_e32 v50, v78, v78
	v_mov_b32_e64 v51, v53
	v_pk_add_f32 v[50:51], v[50:51], v[80:81]
	v_pk_add_f32 v[52:53], v[68:69], v[72:73]
	s_ashr_i32 s3, s2, 31
	s_nop 0
	v_pk_add_f32 v[50:51], v[50:51], v[52:53]
	v_mov_b32_e32 v79, v84
	v_add_f32_e32 v50, v50, v51
	ds_bpermute_b32 v51, v58, v50
	s_add_i32 s8, s8, 1
	s_waitcnt lgkmcnt(0)
	v_add_f32_e64 v50, v50, v51
	ds_bpermute_b32 v51, v59, v50
	s_waitcnt lgkmcnt(0)
	v_add_f32_e32 v50, v50, v51
	ds_bpermute_b32 v51, v60, v50
	s_waitcnt lgkmcnt(0)
	v_add_f32_e32 v50, v50, v51
	ds_bpermute_b32 v51, v61, v50
	s_waitcnt lgkmcnt(0)
	v_add_f32_e32 v50, v50, v51
	ds_bpermute_b32 v51, v62, v50
	s_waitcnt lgkmcnt(0)
	v_add_f32_e32 v50, v50, v51
	ds_bpermute_b32 v51, v63, v50
	s_waitcnt lgkmcnt(0)
	v_add_f32_e32 v50, v50, v51
	v_fmamk_f32 v50, v50, 0x3a800000, v64
	v_mul_f32_e32 v51, 0x4f800000, v50
	v_cmp_gt_f32_e32 vcc, s7, v50
	s_nop 1
	v_cndmask_b32_e32 v50, v50, v51, vcc
	v_sqrt_f32_e32 v51, v50
	s_nop 0
	v_add_u32_e32 v52, -1, v51
	v_fma_f32 v53, -v52, v51, v50
	v_cmp_ge_f32_e64 s[0:1], 0, v53
	v_add_u32_e32 v53, 1, v51
	s_nop 0
	v_cndmask_b32_e64 v52, v51, v52, s[0:1]
	v_fma_f32 v51, -v53, v51, v50
	v_cmp_lt_f32_e64 s[0:1], 0, v51
	s_nop 1
	s_nop 0
	v_cndmask_b32_e64 v51, v52, v53, s[0:1]
	v_mul_f32_e32 v52, 0x37800000, v51
	v_cndmask_b32_e32 v51, v51, v52, vcc
	v_cmp_class_f32_e32 vcc, v50, v65
	s_nop 1
	v_cndmask_b32_e32 v50, v51, v50, vcc
	v_div_scale_f32 v51, s[0:1], v50, v50, 1.0
	v_rcp_f32_e32 v52, v51
	s_lshl_b64 s[0:1], s[2:3], 12
	v_lshl_add_u64 v[68:69], v[20:21], 0, s[0:1]
	s_cmp_eq_u32 s8, 32
	s_nop 0
	v_fma_f32 v53, -v51, v52, 1.0
	v_fmac_f32_e32 v52, v53, v52
	s_nop 0
	v_div_scale_f32 v53, vcc, 1.0, v50, 1.0
	v_mul_f32_e64 v72, v53, v52
	v_fma_f32 v73, -v51, v72, v53
	v_fmac_f32_e32 v72, v73, v52
	s_nop 0
	v_fma_f32 v51, -v51, v72, v53
	v_div_fmas_f32 v51, v51, v52, v72
	v_div_fixup_f32 v72, v51, v50, 1.0
	v_mov_b32_e32 v50, v66
	v_mov_b32_e32 v51, v56
	v_mov_b32_e64 v56, v67
	v_pk_mul_f32 v[50:51], v[72:73], v[50:51] op_sel_hi:[0,1]
	v_pk_mul_f32 v[52:53], v[72:73], v[56:57] op_sel_hi:[0,1]
	v_pk_fma_f32 v[52:53], v[26:27], v[52:53], v[2:3]
	v_pk_fma_f32 v[50:51], v[28:29], v[50:51], v[0:1]
	global_store_dwordx4 v[68:69], v[50:53], off
	s_waitcnt vmcnt(4)
	v_mov_b32_e32 v56, v42
	v_mov_b32_e32 v57, v43
	v_mov_b32_e32 v50, v70
	v_mov_b32_e32 v51, v54
	v_mov_b32_e32 v54, v71
	v_pk_mul_f32 v[50:51], v[72:73], v[50:51] op_sel_hi:[0,1]
	v_pk_mul_f32 v[52:53], v[72:73], v[54:55] op_sel_hi:[0,1]
	v_pk_fma_f32 v[52:53], v[30:31], v[52:53], v[6:7]
	v_pk_fma_f32 v[50:51], v[32:33], v[50:51], v[4:5]
	global_store_dwordx4 v[68:69], v[50:53], off offset:1024
	s_waitcnt vmcnt(4)
	v_mov_b32_e32 v54, v44
	v_mov_b32_e64 v55, v45
	v_pk_mul_f32 v[50:51], v[74:75], v[72:73] op_sel_hi:[1,0]
	v_pk_mul_f32 v[52:53], v[76:77], v[72:73] op_sel_hi:[1,0]
	v_pk_fma_f32 v[50:51], v[36:37], v[50:51], v[8:9]
	v_pk_fma_f32 v[52:53], v[34:35], v[52:53], v[10:11]
	global_store_dwordx4 v[68:69], v[50:53], off offset:2048
	s_nop 1
	s_nop 0
	v_pk_mul_f32 v[50:51], v[78:79], v[72:73] op_sel_hi:[1,0]
	v_pk_mul_f32 v[52:53], v[82:83], v[72:73] op_sel_hi:[1,0]
	v_pk_fma_f32 v[50:51], v[40:41], v[50:51], v[12:13]
	v_pk_fma_f32 v[52:53], v[38:39], v[52:53], v[14:15]
	global_store_dwordx4 v[68:69], v[50:53], off offset:3072
	s_waitcnt vmcnt(5)
	s_nop 0
	v_mov_b32_e32 v52, v46
	v_mov_b32_e32 v53, v47
	s_waitcnt vmcnt(4)
	v_mov_b32_e32 v50, v48
	v_mov_b32_e32 v51, v49
	s_cbranch_scc1 .LBB0_1639
